# half of the layer-1 w_down transposition moved out of the prologue into the idle slot of the 96 workgroups without a last-round tile in the layer-1 in-projection
# speedup vs baseline: 1.0059x; 1.0037x over previous
; #define LAS __attribute__((address_space(3)))
; #define PHASE_IDS() int tid_l_ = threadIdx.x; asm volatile("" : "+v"(tid_l_)); const int tid = tid_l_, lane = tid & 63, wave = __builtin_amdgcn_readfirstlane(tid >> 6); \
;     const int gw = F.vcu * NWAVES + wave, NGW = F.G * NWAVES, gt = F.vcu * (NWAVES * 64) + tid, NGT = F.G * NWAVES * 64; (void)gw; (void)NGW; (void)gt; (void)NGT; (void)lane
; __global__ void __launch_bounds__(NWAVES * 64, 2) hybrid_fwd(Args args) {
;     ...
;     {
;         PHASE_IDS();
;         LAS float* scr = (LAS float*)(F.lds + RING_OFF + wave * 16384);
;         constexpr int I_IN = (DM / 64) * (NPROJ / 32), I_O = (DM / 64) * (DM / 32), I_UP = (DM / 64) * (FF / 32), I_DN = (FF / 64) * (DM / 32);
;         constexpr int I_L = I_IN + I_O + I_UP + I_DN;
;         for (int rep = 0; rep < REP_PRO; ++rep)
;         for (int it = gw; it < DEPTH * I_L; it += NGW) {
;             const int l = it / I_L; int r = it % I_L;
;             if (r < I_IN) { if (l >= PROJ_F8_FROM) p0_transpose_item_f8<true, 1>(args.in[2] + (size_t)l * DM * NSRC, DM, NSRC, NPROJ / 32, (unsigned char*)(ws + WS_WIN + l * SZ_WIN), WUP8_SCALE, args.in[1] + l * DM, args.in[1] + l * DM, DM, scr, r, lane);
;                 else p0_transpose_item<1, true>(args.in[2] + (size_t)l * DM * NSRC, DM, NSRC, NPROJ / 32, (bf16*)(ws + WS_WIN + l * SZ_WIN), args.in[1] + l * DM, args.in[1] + l * DM, DM, scr, r, lane); continue; } r -= I_IN;
;             if (r < I_O) { if (l >= WO_F8_FROM) p0_transpose_item_f8<true>(args.in[13] + (size_t)l * DM * DM, DM, DM, DM / 32, (unsigned char*)(ws + WS_WO + l * SZ_WO), 64.f, args.in[6] + l * 2048, args.in[12] + l * 2048, 2048, scr, r, lane);
;                 else p0_transpose_item<0, true>(args.in[13] + (size_t)l * DM * DM, DM, DM, DM / 32, (bf16*)(ws + WS_WO + l * SZ_WO), args.in[6] + l * 2048, args.in[12] + l * 2048, 2048, scr, r, lane); continue; } r -= I_O;
;             if (r < I_UP) { p0_transpose_item_f8<true>(args.in[15] + (size_t)l * DM * FF, DM, FF, FF / 32, (unsigned char*)(ws + WS_WUP + l * SZ_WUP), WUP8_SCALE, args.in[14] + l * DM, args.in[14] + l * DM, DM, scr, r, lane); continue; } r -= I_UP;
;             p0_transpose_item_f8<false>(args.in[16] + (size_t)l * FF * DM, FF, DM, DM / 32, (unsigned char*)(ws + WS_WDN + l * SZ_WDN), 128.f, args.in[16], args.in[16], 0, scr, r, lane);
.LBB0_11:
	s_or_b64 exec, exec, s[0:1]
	v_mov_b32_e32 v1, v0
	v_readlane_b32 s1, v253, 2
	v_readfirstlane_b32 s0, v1
	s_ashr_i32 s0, s0, 6
	s_lshl_b32 s1, s1, 3
	s_add_i32 s80, s0, s1
	s_lshl_b32 s0, s0, 14
	v_lshlrev_b32_e32 v2, 3, v1
	v_writelane_b32 v253, s1, 46
	s_add_i32 s1, s0, 0
	v_and_b32_e32 v18, 31, v1
	v_bfe_u32 v20, v1, 3, 3
	v_and_b32_e32 v8, 56, v2
	s_lshl_b32 s96, s83, 3
	s_lshl_b32 s76, s83, 9
	v_bfe_u32 v6, v1, 5, 1
	v_lshl_add_u32 v25, v18, 2, s1
	s_movk_i32 s0, 0x84
	v_mul_u32_u24_e32 v2, 0x84, v8
	v_lshlrev_b32_e32 v3, 2, v20
	s_cmp_gt_i32 s80, 0x2f3ff
	v_mad_u32_u24 v19, v6, s0, v25
	v_mov_b32_e32 v11, 0
	v_add3_u32 v21, s1, v2, v3
	v_or_b32_e32 v22, 8, v20
	v_or_b32_e32 v23, 16, v20
	v_or_b32_e32 v24, 24, v20
	s_cbranch_scc1 .Lco3_hop_192
	v_and_b32_e32 v249, 63, v0
	v_lshrrev_b32_e32 v250, 6, v0
	v_readlane_b32 s15, v253, 2
	s_lshr_b32 s22, s15, 3
	s_and_b32 s23, s15, 7
	v_lshrrev_b32_e32 v246, 5, v249
	v_lshl_add_u32 v247, v250, 4, v246
	v_and_b32_e32 v248, 31, v249
	v_xor_b32_e32 v248, v248, v250
	v_lshlrev_b32_e32 v248, 4, v248
	v_lshl_add_u32 v209, v247, 9, v248
	v_add_u32_e32 v210, 0x10000, v209
	v_lshlrev_b32_e32 v96, 2, v247
	v_and_b32_e32 v248, 31, v249
	v_lshlrev_b32_e32 v248, 4, v248
	s_mov_b32 s20, 0x10000
	v_mad_u32_u24 v74, v247, s20, v248
	s_mov_b32 s20, 0x4000
	v_mad_u32_u24 v75, v247, s20, v248
	s_mov_b32 s20, 0xb140
	v_mad_u32_u24 v76, v247, s20, v248
	v_and_b32_e32 v246, 7, v249
	v_lshrrev_b32_e32 v247, 5, v249
	v_lshl_add_u32 v247, v250, 2, v247
	v_xor_b32_e32 v247, v247, v246
	v_lshlrev_b32_e32 v247, 4, v247
	v_lshl_add_u32 v247, v246, 13, v247
	v_bfe_u32 v248, v249, 3, 2
	v_lshl_add_u32 v211, v248, 2, v247
	v_add_u32_e32 v212, 0x10000, v211
	v_and_b32_e32 v246, 7, v249
	v_lshrrev_b32_e32 v247, 5, v249
	v_lshl_add_u32 v247, v250, 2, v247
	v_add_u32_e32 v247, 2, v247
	v_xor_b32_e32 v247, v247, v246
	v_lshlrev_b32_e32 v247, 4, v247
	v_lshl_add_u32 v247, v246, 13, v247
	v_bfe_u32 v248, v249, 3, 2
	v_lshl_add_u32 v213, v248, 2, v247
	v_add_u32_e32 v214, 0x10000, v213
	v_and_b32_e32 v246, 15, v249
	v_lshrrev_b32_e32 v247, 1, v246
	v_lshlrev_b32_e32 v248, 2, v250
	v_xor_b32_e32 v248, v248, v247
	v_lshlrev_b32_e32 v248, 4, v248
	v_lshl_add_u32 v248, v246, 12, v248
	v_lshrrev_b32_e32 v247, 4, v249
	v_lshl_add_u32 v112, v247, 2, v248
	v_add_u32_e32 v113, 0x10000, v112
	v_and_b32_e32 v246, 15, v249
	v_lshrrev_b32_e32 v247, 1, v246
	v_lshlrev_b32_e32 v248, 2, v250
	v_add_u32_e32 v248, 1, v248
	v_xor_b32_e32 v248, v248, v247
	v_lshlrev_b32_e32 v248, 4, v248
	v_lshl_add_u32 v248, v246, 12, v248
	v_lshrrev_b32_e32 v247, 4, v249
	v_lshl_add_u32 v114, v247, 2, v248
	v_add_u32_e32 v115, 0x10000, v114
	v_and_b32_e32 v246, 15, v249
	v_lshrrev_b32_e32 v247, 1, v246
	v_lshlrev_b32_e32 v248, 2, v250
	v_add_u32_e32 v248, 2, v248
	v_xor_b32_e32 v248, v248, v247
	v_lshlrev_b32_e32 v248, 4, v248
	v_lshl_add_u32 v248, v246, 12, v248
	v_lshrrev_b32_e32 v247, 4, v249
	v_lshl_add_u32 v116, v247, 2, v248
	v_add_u32_e32 v117, 0x10000, v116
	v_and_b32_e32 v246, 15, v249
	v_lshrrev_b32_e32 v247, 1, v246
	v_lshlrev_b32_e32 v248, 2, v250
	v_add_u32_e32 v248, 3, v248
	v_xor_b32_e32 v248, v248, v247
	v_lshlrev_b32_e32 v248, 4, v248
	v_lshl_add_u32 v248, v246, 12, v248
	v_lshrrev_b32_e32 v247, 4, v249
	v_lshl_add_u32 v118, v247, 2, v248
	v_add_u32_e32 v119, 0x10000, v118
	v_lshrrev_b32_e32 v246, 3, v249
	v_lshl_add_u32 v246, v250, 4, v246
	v_and_b32_e32 v247, 7, v249
	v_lshlrev_b32_e32 v247, 4, v247
	v_lshl_add_u32 v77, v246, 12, v247
	v_lshl_add_u32 v79, v246, 14, v247
	v_and_b32_e32 v248, 63, v246
	v_lshlrev_b32_e32 v248, 1, v248
	v_lshrrev_b32_e32 v246, 6, v246
	v_or_b32_e32 v248, v248, v246
	v_lshl_add_u32 v81, v248, 12, v247
	v_lshrrev_b32_e32 v246, 3, v249
	v_lshl_add_u32 v246, v250, 4, v246
	v_add_u32_e32 v246, 8, v246
	v_and_b32_e32 v247, 7, v249
	v_lshlrev_b32_e32 v247, 4, v247
	v_lshl_add_u32 v78, v246, 12, v247
	v_lshl_add_u32 v80, v246, 14, v247
	v_and_b32_e32 v248, 63, v246
	v_lshlrev_b32_e32 v248, 1, v248
	v_lshrrev_b32_e32 v246, 6, v246
	v_or_b32_e32 v248, v248, v246
	v_lshl_add_u32 v82, v248, 12, v247
	v_lshrrev_b32_e32 v246, 4, v249
	v_lshl_add_u32 v246, v250, 4, v246
	v_and_b32_e32 v247, 15, v249
	v_lshlrev_b32_e32 v247, 4, v247
	v_lshl_add_u32 v83, v246, 13, v247
	v_and_b32_e32 v248, 63, v246
	v_lshlrev_b32_e32 v248, 1, v248
	v_lshrrev_b32_e32 v246, 6, v246
	v_or_b32_e32 v248, v248, v246
	v_lshl_add_u32 v87, v248, 13, v247
	v_lshrrev_b32_e32 v246, 4, v249
	v_lshl_add_u32 v246, v250, 4, v246
	v_add_u32_e32 v246, 4, v246
	v_and_b32_e32 v247, 15, v249
	v_lshlrev_b32_e32 v247, 4, v247
	v_lshl_add_u32 v84, v246, 13, v247
	v_and_b32_e32 v248, 63, v246
	v_lshlrev_b32_e32 v248, 1, v248
	v_lshrrev_b32_e32 v246, 6, v246
	v_or_b32_e32 v248, v248, v246
	v_lshl_add_u32 v88, v248, 13, v247
	v_lshrrev_b32_e32 v246, 4, v249
	v_lshl_add_u32 v246, v250, 4, v246
	v_add_u32_e32 v246, 8, v246
	v_and_b32_e32 v247, 15, v249
	v_lshlrev_b32_e32 v247, 4, v247
	v_lshl_add_u32 v85, v246, 13, v247
	v_and_b32_e32 v248, 63, v246
	v_lshlrev_b32_e32 v248, 1, v248
	v_lshrrev_b32_e32 v246, 6, v246
	v_or_b32_e32 v248, v248, v246
	v_lshl_add_u32 v89, v248, 13, v247
	v_lshrrev_b32_e32 v246, 4, v249
	v_lshl_add_u32 v246, v250, 4, v246
	v_add_u32_e32 v246, 12, v246
	v_and_b32_e32 v247, 15, v249
	v_lshlrev_b32_e32 v247, 4, v247
	v_lshl_add_u32 v86, v246, 13, v247
	v_and_b32_e32 v248, 63, v246
	v_lshlrev_b32_e32 v248, 1, v248
	v_lshrrev_b32_e32 v246, 6, v246
	v_or_b32_e32 v248, v248, v246
	v_lshl_add_u32 v90, v248, 13, v247
	v_mov_b32_e32 v95, 0x43e00000
	s_mov_b32 s62, 0xc3e00000
	s_mov_b32 s63, 0x7fff
	s_mov_b32 s64, 0x07060302
	v_readlane_b32 s10, v253, 5
; __device__ __forceinline__ int nat_dim(int p) { return (p >> 1) + 64 * (p & 1); }
; template <int MAP, bool KS, bool KPERM = false>
; __device__ __forceinline__ void p0_transpose_item(const float* W, int K, int Nsrc, int nblk, bf16* WT, const float* ksA, const float* ksB, int ksplit, LAS float* scr, int item, int lane) {
;     ...
;     for (int i = 0; i < 32; ++i) { const int k = k0 + 2 * i + (lane >> 5); const int ksrc = KPERM ? ((k & ~127) + nat_dim(k & 127)) : k;
;         v[i] = sc >= 0 ? W[(size_t)ksrc * Nsrc + sc] : 0.f; }
; #pragma unroll
;     for (int i = 0; i < 32; ++i) { const int kk = 2 * i + (lane >> 5); const int k = k0 + kk;
;         if (KS) v[i] *= (k < ksplit ? ksA[k] : ksB[k - ksplit]);
;         scr[kk * 33 + (lane & 31)] = v[i]; }
; __global__ void __launch_bounds__(NWAVES * 64, 2) hybrid_fwd(Args args) {
;     ...
;         for (int rep = 0; rep < REP_PRO; ++rep)
;         for (int it = gw; it < DEPTH * I_L; it += NGW) {
;             const int l = it / I_L; int r = it % I_L;
;             if (r < I_IN) { if (l >= PROJ_F8_FROM) p0_transpose_item_f8<true, 1>(args.in[2] + (size_t)l * DM * NSRC, DM, NSRC, NPROJ / 32, (unsigned char*)(ws + WS_WIN + l * SZ_WIN), WUP8_SCALE, args.in[1] + l * DM, args.in[1] + l * DM, DM, scr, r, lane);
;                 else p0_transpose_item<1, true>(args.in[2] + (size_t)l * DM * NSRC, DM, NSRC, NPROJ / 32, (bf16*)(ws + WS_WIN + l * SZ_WIN), args.in[1] + l * DM, args.in[1] + l * DM, DM, scr, r, lane); continue; } r -= I_IN;
;             if (r < I_O) { if (l >= WO_F8_FROM) p0_transpose_item_f8<true>(args.in[13] + (size_t)l * DM * DM, DM, DM, DM / 32, (unsigned char*)(ws + WS_WO + l * SZ_WO), 64.f, args.in[6] + l * 2048, args.in[12] + l * 2048, 2048, scr, r, lane);
;                 else p0_transpose_item<0, true>(args.in[13] + (size_t)l * DM * DM, DM, DM, DM / 32, (bf16*)(ws + WS_WO + l * SZ_WO), args.in[6] + l * 2048, args.in[12] + l * 2048, 2048, scr, r, lane); continue; } r -= I_O;
;             if (r < I_UP) { p0_transpose_item_f8<true>(args.in[15] + (size_t)l * DM * FF, DM, FF, FF / 32, (unsigned char*)(ws + WS_WUP + l * SZ_WUP), WUP8_SCALE, args.in[14] + l * DM, args.in[14] + l * DM, DM, scr, r, lane); continue; } r -= I_UP;
;             p0_transpose_item_f8<false>(args.in[16] + (size_t)l * FF * DM, FF, DM, DM / 32, (unsigned char*)(ws + WS_WDN + l * SZ_WDN), 128.f, args.in[16], args.in[16], 0, scr, r, lane);
	v_readlane_b32 s11, v253, 6
	s_lshl_b32 s20, s22, 9
	s_add_u32 s10, s10, s20
	s_addc_u32 s11, s11, 0
	global_load_dword v42, v96, s[10:11] offset:0
	global_load_dword v43, v96, s[10:11] offset:8
	global_load_dword v44, v96, s[10:11] offset:16
	global_load_dword v45, v96, s[10:11] offset:24
	global_load_dword v46, v96, s[10:11] offset:32
	global_load_dword v47, v96, s[10:11] offset:40
	global_load_dword v48, v96, s[10:11] offset:48
	global_load_dword v49, v96, s[10:11] offset:56
	v_readlane_b32 s10, v253, 5
	v_readlane_b32 s11, v253, 6
	s_lshl_b32 s20, s22, 9
	s_add_i32 s20, s20, 0x4000
	s_add_u32 s10, s10, s20
	s_addc_u32 s11, s11, 0
	global_load_dword v50, v96, s[10:11] offset:0
	global_load_dword v51, v96, s[10:11] offset:8
	global_load_dword v52, v96, s[10:11] offset:16
	global_load_dword v53, v96, s[10:11] offset:24
	global_load_dword v54, v96, s[10:11] offset:32
	global_load_dword v55, v96, s[10:11] offset:40
	global_load_dword v56, v96, s[10:11] offset:48
	global_load_dword v57, v96, s[10:11] offset:56
	v_readlane_b32 s10, v253, 15
	v_readlane_b32 s11, v253, 16
	v_readlane_b32 s20, v253, 27
	v_readlane_b32 s21, v253, 28
	s_sub_i32 s26, s22, 16
	s_cmp_lt_u32 s22, 16
	s_cselect_b32 s10, s10, s20
	s_cselect_b32 s11, s11, s21
	s_cselect_b32 s26, s22, s26
	s_lshl_b32 s20, s26, 9
	s_add_u32 s10, s10, s20
	s_addc_u32 s11, s11, 0
	global_load_dword v58, v96, s[10:11] offset:0
	global_load_dword v59, v96, s[10:11] offset:8
	global_load_dword v60, v96, s[10:11] offset:16
	global_load_dword v61, v96, s[10:11] offset:24
	global_load_dword v62, v96, s[10:11] offset:32
	global_load_dword v63, v96, s[10:11] offset:40
	global_load_dword v64, v96, s[10:11] offset:48
	global_load_dword v65, v96, s[10:11] offset:56
	v_readlane_b32 s10, v253, 15
	v_readlane_b32 s11, v253, 16
	v_readlane_b32 s20, v253, 27
	v_readlane_b32 s21, v253, 28
	s_sub_i32 s26, s22, 16
	s_cmp_lt_u32 s22, 16
	s_cselect_b32 s10, s10, s20
	s_cselect_b32 s11, s11, s21
	s_cselect_b32 s26, s22, s26
	s_lshl_b32 s20, s26, 9
	s_add_i32 s20, s20, 0x2000
	s_add_u32 s10, s10, s20
	s_addc_u32 s11, s11, 0
	global_load_dword v66, v96, s[10:11] offset:0
	global_load_dword v67, v96, s[10:11] offset:8
	global_load_dword v68, v96, s[10:11] offset:16
	global_load_dword v69, v96, s[10:11] offset:24
	global_load_dword v70, v96, s[10:11] offset:32
	global_load_dword v71, v96, s[10:11] offset:40
	global_load_dword v72, v96, s[10:11] offset:48
	global_load_dword v73, v96, s[10:11] offset:56
	v_readlane_b32 s10, v253, 31
	v_readlane_b32 s11, v253, 32
	s_lshl_b32 s20, s22, 9
	s_add_u32 s10, s10, s20
	s_addc_u32 s11, s11, 0
	global_load_dword v26, v96, s[10:11] offset:0
	global_load_dword v27, v96, s[10:11] offset:8
	global_load_dword v28, v96, s[10:11] offset:16
	global_load_dword v29, v96, s[10:11] offset:24
	global_load_dword v30, v96, s[10:11] offset:32
	global_load_dword v31, v96, s[10:11] offset:40
	global_load_dword v32, v96, s[10:11] offset:48
	global_load_dword v33, v96, s[10:11] offset:56
	v_readlane_b32 s10, v253, 31
	v_readlane_b32 s11, v253, 32
	s_lshl_b32 s20, s22, 9
	s_add_i32 s20, s20, 0x4000
	s_add_u32 s10, s10, s20
	s_addc_u32 s11, s11, 0
	global_load_dword v34, v96, s[10:11] offset:0
	global_load_dword v35, v96, s[10:11] offset:8
	global_load_dword v36, v96, s[10:11] offset:16
	global_load_dword v37, v96, s[10:11] offset:24
	global_load_dword v38, v96, s[10:11] offset:32
	global_load_dword v39, v96, s[10:11] offset:40
	global_load_dword v40, v96, s[10:11] offset:48
	global_load_dword v41, v96, s[10:11] offset:56
	s_waitcnt vmcnt(0)
	v_mul_f32_e32 v50, 0x42800000, v50
	v_mul_f32_e32 v51, 0x42800000, v51
	v_mul_f32_e32 v52, 0x42800000, v52
	v_mul_f32_e32 v53, 0x42800000, v53
	v_mul_f32_e32 v54, 0x42800000, v54
	v_mul_f32_e32 v55, 0x42800000, v55
	v_mul_f32_e32 v56, 0x42800000, v56
	v_mul_f32_e32 v57, 0x42800000, v57
	v_mul_f32_e32 v66, 0x42800000, v66
	v_mul_f32_e32 v67, 0x42800000, v67
	v_mul_f32_e32 v68, 0x42800000, v68
	v_mul_f32_e32 v69, 0x42800000, v69
	v_mul_f32_e32 v70, 0x42800000, v70
	v_mul_f32_e32 v71, 0x42800000, v71
	v_mul_f32_e32 v72, 0x42800000, v72
	v_mul_f32_e32 v73, 0x42800000, v73
	v_mul_f32_e32 v26, 0x42800000, v26
	v_mul_f32_e32 v27, 0x42800000, v27
	v_mul_f32_e32 v28, 0x42800000, v28
	v_mul_f32_e32 v29, 0x42800000, v29
	v_mul_f32_e32 v30, 0x42800000, v30
	v_mul_f32_e32 v31, 0x42800000, v31
	v_mul_f32_e32 v32, 0x42800000, v32
	v_mul_f32_e32 v33, 0x42800000, v33
	v_mul_f32_e32 v34, 0x42800000, v34
	v_mul_f32_e32 v35, 0x42800000, v35
	v_mul_f32_e32 v36, 0x42800000, v36
	v_mul_f32_e32 v37, 0x42800000, v37
	v_mul_f32_e32 v38, 0x42800000, v38
	v_mul_f32_e32 v39, 0x42800000, v39
	v_mul_f32_e32 v40, 0x42800000, v40
	v_mul_f32_e32 v41, 0x42800000, v41
	v_readlane_b32 s30, v253, 33
	v_readlane_b32 s31, v253, 34
	v_readlane_b32 s32, v253, 41
	v_readlane_b32 s33, v253, 42
	s_mul_i32 s20, s22, 0x800000
	s_lshl_b32 s21, s23, 9
	s_add_u32 s20, s20, s21
	s_add_u32 s30, s30, s20
	s_addc_u32 s31, s31, 0
	s_add_u32 s32, s32, 0xf600000
	s_addc_u32 s33, s33, 0
	s_lshl_b32 s20, s22, 7
	s_mul_i32 s21, s23, 0x80000
	s_add_u32 s20, s20, s21
	s_add_u32 s32, s32, s20
	s_addc_u32 s33, s33, 0
	v_readlane_b32 s34, v253, 33
	v_readlane_b32 s35, v253, 34
	v_readlane_b32 s36, v253, 41
	v_readlane_b32 s37, v253, 42
	s_add_u32 s34, s34, 0x10000000
	s_addc_u32 s35, s35, 0
	s_mul_i32 s20, s22, 0x800000
	s_lshl_b32 s21, s23, 9
	s_add_u32 s20, s20, s21
	s_add_u32 s34, s34, s20
	s_addc_u32 s35, s35, 0
	s_add_u32 s36, s36, 0x17600000
	s_addc_u32 s37, s37, 0
	s_lshl_b32 s20, s22, 7
	s_mul_i32 s21, s23, 0x80000
	s_add_u32 s20, s20, s21
	s_add_u32 s36, s36, s20
	s_addc_u32 s37, s37, 0
	v_readlane_b32 s38, v253, 35
;     const int pr = item >> 1, kb = 2 * (pr / nblk) + (item & 1), nb = pr % nblk, k0 = 64 * kb, n0 = 32 * nb;
;     const int nr = n0 + (lane & 31); const int sc = MAP == 1 ? src_col_in(nr) : nr;
;     float v[32];
; #pragma unroll
;     for (int i = 0; i < 32; ++i) v[i] = sc >= 0 ? W[(size_t)(k0 + 2 * i + (lane >> 5)) * Nsrc + sc] : 0.f;
; #pragma unroll
;     for (int i = 0; i < 32; ++i) { const int k = k0 + 2 * i + (lane >> 5); float x = v[i] * wscale; if (KS) x *= (k < ksplit ? ksA[k] : ksB[k - ksplit]); scr[(2 * i + (lane >> 5)) * 33 + (lane & 31)] = x; }
; __global__ void __launch_bounds__(NWAVES * 64, 2) hybrid_fwd(Args args) {
;     ...
;             if (r < I_IN) { if (l >= PROJ_F8_FROM) p0_transpose_item_f8<true, 1>(args.in[2] + (size_t)l * DM * NSRC, DM, NSRC, NPROJ / 32, (unsigned char*)(ws + WS_WIN + l * SZ_WIN), WUP8_SCALE, args.in[1] + l * DM, args.in[1] + l * DM, DM, scr, r, lane);
;                 else p0_transpose_item<1, true>(args.in[2] + (size_t)l * DM * NSRC, DM, NSRC, NPROJ / 32, (bf16*)(ws + WS_WIN + l * SZ_WIN), args.in[1] + l * DM, args.in[1] + l * DM, DM, scr, r, lane); continue; } r -= I_IN;
;             if (r < I_O) { if (l >= WO_F8_FROM) p0_transpose_item_f8<true>(args.in[13] + (size_t)l * DM * DM, DM, DM, DM / 32, (unsigned char*)(ws + WS_WO + l * SZ_WO), 64.f, args.in[6] + l * 2048, args.in[12] + l * 2048, 2048, scr, r, lane);
;                 else p0_transpose_item<0, true>(args.in[13] + (size_t)l * DM * DM, DM, DM, DM / 32, (bf16*)(ws + WS_WO + l * SZ_WO), args.in[6] + l * 2048, args.in[12] + l * 2048, 2048, scr, r, lane); continue; } r -= I_O;
;             if (r < I_UP) { p0_transpose_item_f8<true>(args.in[15] + (size_t)l * DM * FF, DM, FF, FF / 32, (unsigned char*)(ws + WS_WUP + l * SZ_WUP), WUP8_SCALE, args.in[14] + l * DM, args.in[14] + l * DM, DM, scr, r, lane); continue; } r -= I_UP;
;             p0_transpose_item_f8<false>(args.in[16] + (size_t)l * FF * DM, FF, DM, DM / 32, (unsigned char*)(ws + WS_WDN + l * SZ_WDN), 128.f, args.in[16], args.in[16], 0, scr, r, lane);
	v_readlane_b32 s39, v253, 36
	v_readlane_b32 s40, v253, 41
	v_readlane_b32 s41, v253, 42
	s_mul_i32 s20, s22, 0x200000
	s_lshl_b32 s21, s23, 9
	s_add_u32 s20, s20, s21
	s_add_u32 s38, s38, s20
	s_addc_u32 s39, s39, 0
	s_add_u32 s40, s40, 0x1f600000
	s_addc_u32 s41, s41, 0
	s_lshl_b32 s20, s22, 7
	s_mul_i32 s21, s23, 0x200000
	s_add_u32 s20, s20, s21
	s_add_u32 s40, s40, s20
	s_addc_u32 s41, s41, 0
	v_readlane_b32 s42, v253, 35
	v_readlane_b32 s43, v253, 36
	v_readlane_b32 s44, v253, 41
	v_readlane_b32 s45, v253, 42
	s_add_u32 s42, s42, 0x10000000
	s_addc_u32 s43, s43, 0
	s_mul_i32 s20, s22, 0x200000
	s_lshl_b32 s21, s23, 9
	s_add_u32 s20, s20, s21
	s_add_u32 s42, s42, s20
	s_addc_u32 s43, s43, 0
	s_add_u32 s44, s44, 0x27600000
	s_addc_u32 s45, s45, 0
	s_lshl_b32 s20, s22, 7
	s_mul_i32 s21, s23, 0x200000
	s_add_u32 s20, s20, s21
	s_add_u32 s44, s44, s20
	s_addc_u32 s45, s45, 0
	v_readlane_b32 s46, v253, 7
	v_readlane_b32 s47, v253, 8
	v_readlane_b32 s48, v253, 41
	v_readlane_b32 s49, v253, 42
	s_mul_i32 s20, s22, 0x58a000
	s_add_u32 s46, s46, s20
	s_addc_u32 s47, s47, 0
	s_add_u32 s48, s48, 0x200000
	s_addc_u32 s49, s49, 0
	s_lshl_b32 s20, s22, 8
	s_add_u32 s48, s48, s20
	s_addc_u32 s49, s49, 0
	v_readlane_b32 s50, v253, 7
	v_readlane_b32 s51, v253, 8
	v_readlane_b32 s52, v253, 41
	v_readlane_b32 s53, v253, 42
	s_add_u32 s50, s50, 0xb140000
	s_addc_u32 s51, s51, 0
	s_mul_i32 s20, s22, 0x58a000
	s_add_u32 s50, s50, s20
	s_addc_u32 s51, s51, 0
	s_add_u32 s52, s52, 0x5c00000
	s_addc_u32 s53, s53, 0
	s_lshl_b32 s20, s22, 7
	s_add_u32 s52, s52, s20
	s_addc_u32 s53, s53, 0
	v_readlane_b32 s54, v253, 29
	v_readlane_b32 s55, v253, 30
	v_readlane_b32 s56, v253, 41
	v_readlane_b32 s57, v253, 42
	s_mul_i32 s20, s22, 0x200000
	s_lshl_b32 s21, s23, 9
	s_add_u32 s20, s20, s21
	s_add_u32 s54, s54, s20
	s_addc_u32 s55, s55, 0
	s_add_u32 s56, s56, 0xb600000
	s_addc_u32 s57, s57, 0
	s_lshl_b32 s20, s22, 8
	s_mul_i32 s21, s23, 0x100000
	s_add_u32 s20, s20, s21
	s_add_u32 s56, s56, s20
	s_addc_u32 s57, s57, 0
	v_readlane_b32 s58, v253, 29
	v_readlane_b32 s59, v253, 30
	v_readlane_b32 s60, v253, 41
	v_readlane_b32 s61, v253, 42
	s_add_u32 s58, s58, 0x4000000
	s_addc_u32 s59, s59, 0
	s_mul_i32 s20, s22, 0x200000
	s_lshl_b32 s21, s23, 9
	s_add_u32 s20, s20, s21
	s_add_u32 s58, s58, s20
	s_addc_u32 s59, s59, 0
	s_add_u32 s60, s60, 0xd600000
	s_addc_u32 s61, s61, 0
	s_lshl_b32 s20, s22, 7
	s_mul_i32 s21, s23, 0x80000
	s_add_u32 s20, s20, s21
	s_add_u32 s60, s60, s20
	s_addc_u32 s61, s61, 0
	s_mov_b64 s[8:9], s[30:31]
	global_load_dwordx4 v[144:147], v74, s[8:9]
	s_add_u32 s8, s8, 0x20000
	s_addc_u32 s9, s9, 0
	global_load_dwordx4 v[148:151], v74, s[8:9]
	s_add_u32 s8, s8, 0x20000
	s_addc_u32 s9, s9, 0
	global_load_dwordx4 v[152:155], v74, s[8:9]
	s_add_u32 s8, s8, 0x20000
	s_addc_u32 s9, s9, 0
	global_load_dwordx4 v[156:159], v74, s[8:9]
	s_add_u32 s8, s8, 0x20000
	s_addc_u32 s9, s9, 0
	global_load_dwordx4 v[160:163], v74, s[8:9]
	s_add_u32 s8, s8, 0x20000
	s_addc_u32 s9, s9, 0
	global_load_dwordx4 v[164:167], v74, s[8:9]
	s_add_u32 s8, s8, 0x20000
	s_addc_u32 s9, s9, 0
	global_load_dwordx4 v[168:171], v74, s[8:9]
	s_add_u32 s8, s8, 0x20000
	s_addc_u32 s9, s9, 0
	global_load_dwordx4 v[172:175], v74, s[8:9]
	s_add_u32 s8, s30, 0x1000
	s_addc_u32 s9, s31, 0
	global_load_dwordx4 v[176:179], v74, s[8:9]
	s_add_u32 s8, s8, 0x20000
	s_addc_u32 s9, s9, 0
	global_load_dwordx4 v[180:183], v74, s[8:9]
	s_add_u32 s8, s8, 0x20000
	s_addc_u32 s9, s9, 0
	global_load_dwordx4 v[184:187], v74, s[8:9]
	s_add_u32 s8, s8, 0x20000
	s_addc_u32 s9, s9, 0
	global_load_dwordx4 v[188:191], v74, s[8:9]
	s_add_u32 s8, s8, 0x20000
	s_addc_u32 s9, s9, 0
	global_load_dwordx4 v[192:195], v74, s[8:9]
	s_add_u32 s8, s8, 0x20000
	s_addc_u32 s9, s9, 0
	global_load_dwordx4 v[196:199], v74, s[8:9]
	s_add_u32 s8, s8, 0x20000
	s_addc_u32 s9, s9, 0
	global_load_dwordx4 v[200:203], v74, s[8:9]
	s_add_u32 s8, s8, 0x20000
	s_addc_u32 s9, s9, 0
	global_load_dwordx4 v[204:207], v74, s[8:9]
	s_waitcnt vmcnt(8)
	v_mul_f32_e32 v144, v26, v144
	v_mul_f32_e32 v145, v26, v145
	v_mul_f32_e32 v146, v26, v146
	v_mul_f32_e32 v147, v26, v147
	ds_write_b128 v209, v[144:147]
	v_mul_f32_e32 v148, v27, v148
	v_mul_f32_e32 v149, v27, v149
	v_mul_f32_e32 v150, v27, v150
	v_mul_f32_e32 v151, v27, v151
	ds_write_b128 v209, v[148:151] offset:1024
	v_mul_f32_e32 v152, v28, v152
	v_mul_f32_e32 v153, v28, v153
	v_mul_f32_e32 v154, v28, v154
	v_mul_f32_e32 v155, v28, v155
	ds_write_b128 v209, v[152:155] offset:2048
	v_mul_f32_e32 v156, v29, v156
	v_mul_f32_e32 v157, v29, v157
	v_mul_f32_e32 v158, v29, v158
	v_mul_f32_e32 v159, v29, v159
	ds_write_b128 v209, v[156:159] offset:3072
	v_mul_f32_e32 v160, v30, v160
	v_mul_f32_e32 v161, v30, v161
	v_mul_f32_e32 v162, v30, v162
	v_mul_f32_e32 v163, v30, v163
	ds_write_b128 v209, v[160:163] offset:4096
	v_mul_f32_e32 v164, v31, v164
	v_mul_f32_e32 v165, v31, v165
	v_mul_f32_e32 v166, v31, v166
	v_mul_f32_e32 v167, v31, v167
	ds_write_b128 v209, v[164:167] offset:5120
	v_mul_f32_e32 v168, v32, v168
	v_mul_f32_e32 v169, v32, v169
	v_mul_f32_e32 v170, v32, v170
	v_mul_f32_e32 v171, v32, v171
	ds_write_b128 v209, v[168:171] offset:6144
	v_mul_f32_e32 v172, v33, v172
	v_mul_f32_e32 v173, v33, v173
	v_mul_f32_e32 v174, v33, v174
	v_mul_f32_e32 v175, v33, v175
	ds_write_b128 v209, v[172:175] offset:7168
	s_waitcnt lgkmcnt(0)
	s_barrier
; #define GAS __attribute__((address_space(1)))
; #define LAS __attribute__((address_space(3)))
; #define LDS_WAIT() asm volatile("s_waitcnt lgkmcnt(0)" ::: "memory")
; __device__ __forceinline__ unsigned pk4_fp8(float a, float b, float c, float d) {
;     a = fminf(fmaxf(a, -448.f), 448.f); b = fminf(fmaxf(b, -448.f), 448.f); c = fminf(fmaxf(c, -448.f), 448.f); d = fminf(fmaxf(d, -448.f), 448.f);
;     int w = __builtin_amdgcn_cvt_pk_fp8_f32(a, b, 0, false); w = __builtin_amdgcn_cvt_pk_fp8_f32(c, d, w, true); return (unsigned)w; }
;     const int pr = item >> 1, kb = 2 * (pr / nblk) + (item & 1), nb = pr % nblk, k0 = 64 * kb, n0 = 32 * nb;
;     const int nr = n0 + (lane & 31); const int sc = MAP == 1 ? src_col_in(nr) : nr;
;     float v[32];
; #pragma unroll
;     for (int i = 0; i < 32; ++i) v[i] = sc >= 0 ? W[(size_t)(k0 + 2 * i + (lane >> 5)) * Nsrc + sc] : 0.f;
; #pragma unroll
;     for (int i = 0; i < 32; ++i) { const int k = k0 + 2 * i + (lane >> 5); float x = v[i] * wscale; if (KS) x *= (k < ksplit ? ksA[k] : ksB[k - ksplit]); scr[(2 * i + (lane >> 5)) * 33 + (lane & 31)] = x; }
;     LDS_WAIT(); asm volatile("" ::: "memory");
;     const int c = lane & 7;
; #pragma unroll
;     for (int j = 0; j < 4; ++j) { const int n = (lane >> 3) + 8 * j; const LAS float* s = scr + (8 * c) * 33 + n;
;         const unsigned long long o = (unsigned long long)pg8::pk4_fp8(s[0 * 33], s[1 * 33], s[2 * 33], s[3 * 33]) | ((unsigned long long)pg8::pk4_fp8(s[4 * 33], s[5 * 33], s[6 * 33], s[7 * 33]) << 32);
;         *(GAS unsigned long long*)(WT + (size_t)(n0 + n) * K + k0 + 8 * c) = o; }
;     LDS_WAIT(); asm volatile("" ::: "memory");
; }
	s_add_u32 s8, s30, 0x2000
	s_addc_u32 s9, s31, 0
	global_load_dwordx4 v[144:147], v74, s[8:9]
	s_add_u32 s8, s8, 0x20000
	s_addc_u32 s9, s9, 0
	global_load_dwordx4 v[148:151], v74, s[8:9]
	s_add_u32 s8, s8, 0x20000
	s_addc_u32 s9, s9, 0
	global_load_dwordx4 v[152:155], v74, s[8:9]
	s_add_u32 s8, s8, 0x20000
	s_addc_u32 s9, s9, 0
	global_load_dwordx4 v[156:159], v74, s[8:9]
	s_add_u32 s8, s8, 0x20000
	s_addc_u32 s9, s9, 0
	global_load_dwordx4 v[160:163], v74, s[8:9]
	s_add_u32 s8, s8, 0x20000
	s_addc_u32 s9, s9, 0
	global_load_dwordx4 v[164:167], v74, s[8:9]
	s_add_u32 s8, s8, 0x20000
	s_addc_u32 s9, s9, 0
	global_load_dwordx4 v[168:171], v74, s[8:9]
	s_add_u32 s8, s8, 0x20000
	s_addc_u32 s9, s9, 0
	global_load_dwordx4 v[172:175], v74, s[8:9]
	s_mov_b64 s[6:7], s[32:33]
	ds_read_b32 v226, v211
	ds_read_b32 v227, v211 offset:512
	ds_read_b32 v228, v211 offset:1024
	ds_read_b32 v229, v211 offset:1536
	ds_read_b32 v230, v211 offset:2048
	ds_read_b32 v231, v211 offset:2560
	ds_read_b32 v232, v211 offset:3072
	ds_read_b32 v233, v211 offset:3584
	ds_read_b32 v234, v211 offset:4096
	ds_read_b32 v235, v211 offset:4608
	ds_read_b32 v236, v211 offset:5120
	ds_read_b32 v237, v211 offset:5632
	ds_read_b32 v238, v211 offset:6144
	ds_read_b32 v239, v211 offset:6656
	ds_read_b32 v240, v211 offset:7168
	ds_read_b32 v241, v211 offset:7680
	s_waitcnt lgkmcnt(0)
	v_max_f32_e32 v226, v226, v226
	v_max_f32_e32 v227, v227, v227
	v_max_f32_e32 v228, v228, v228
	v_max_f32_e32 v229, v229, v229
	v_max_f32_e32 v230, v230, v230
	v_max_f32_e32 v231, v231, v231
	v_max_f32_e32 v232, v232, v232
	v_max_f32_e32 v233, v233, v233
	v_max_f32_e32 v234, v234, v234
	v_max_f32_e32 v235, v235, v235
	v_max_f32_e32 v236, v236, v236
	v_max_f32_e32 v237, v237, v237
	v_max_f32_e32 v238, v238, v238
	v_max_f32_e32 v239, v239, v239
	v_max_f32_e32 v240, v240, v240
	v_max_f32_e32 v241, v241, v241
	v_med3_f32 v226, v226, s62, v95
	v_med3_f32 v227, v227, s62, v95
	v_med3_f32 v228, v228, s62, v95
	v_med3_f32 v229, v229, s62, v95
	v_med3_f32 v230, v230, s62, v95
	v_med3_f32 v231, v231, s62, v95
	v_med3_f32 v232, v232, s62, v95
	v_med3_f32 v233, v233, s62, v95
	v_med3_f32 v234, v234, s62, v95
	v_med3_f32 v235, v235, s62, v95
	v_med3_f32 v236, v236, s62, v95
	v_med3_f32 v237, v237, s62, v95
	v_med3_f32 v238, v238, s62, v95
	v_med3_f32 v239, v239, s62, v95
	v_med3_f32 v240, v240, s62, v95
	v_med3_f32 v241, v241, s62, v95
	v_mov_b32_e32 v242, 0
	v_mov_b32_e32 v243, 0
	v_mov_b32_e32 v244, 0
	v_mov_b32_e32 v245, 0
	v_cvt_pk_fp8_f32 v242, v226, v227
	v_cvt_pk_fp8_f32 v243, v230, v231
	v_cvt_pk_fp8_f32 v244, v234, v235
	v_cvt_pk_fp8_f32 v245, v238, v239
	v_cvt_pk_fp8_f32 v242, v228, v229 op_sel:[0,0,1]
	v_cvt_pk_fp8_f32 v243, v232, v233 op_sel:[0,0,1]
	v_cvt_pk_fp8_f32 v244, v236, v237 op_sel:[0,0,1]
	v_cvt_pk_fp8_f32 v245, v240, v241 op_sel:[0,0,1]
	s_nop 0
	global_store_dwordx4 v77, v[242:245], s[6:7]
	ds_read_b32 v226, v213
	ds_read_b32 v227, v213 offset:512
	ds_read_b32 v228, v213 offset:1024
	ds_read_b32 v229, v213 offset:1536
	ds_read_b32 v230, v213 offset:2048
	ds_read_b32 v231, v213 offset:2560
	ds_read_b32 v232, v213 offset:3072
	ds_read_b32 v233, v213 offset:3584
	ds_read_b32 v234, v213 offset:4096
	ds_read_b32 v235, v213 offset:4608
	ds_read_b32 v236, v213 offset:5120
	ds_read_b32 v237, v213 offset:5632
	ds_read_b32 v238, v213 offset:6144
	ds_read_b32 v239, v213 offset:6656
	ds_read_b32 v240, v213 offset:7168
	ds_read_b32 v241, v213 offset:7680
	s_waitcnt lgkmcnt(0)
	v_max_f32_e32 v226, v226, v226
	v_max_f32_e32 v227, v227, v227
	v_max_f32_e32 v228, v228, v228
	v_max_f32_e32 v229, v229, v229
	v_max_f32_e32 v230, v230, v230
	v_max_f32_e32 v231, v231, v231
	v_max_f32_e32 v232, v232, v232
	v_max_f32_e32 v233, v233, v233
	v_max_f32_e32 v234, v234, v234
	v_max_f32_e32 v235, v235, v235
	v_max_f32_e32 v236, v236, v236
	v_max_f32_e32 v237, v237, v237
	v_max_f32_e32 v238, v238, v238
	v_max_f32_e32 v239, v239, v239
	v_max_f32_e32 v240, v240, v240
	v_max_f32_e32 v241, v241, v241
	v_med3_f32 v226, v226, s62, v95
	v_med3_f32 v227, v227, s62, v95
	v_med3_f32 v228, v228, s62, v95
	v_med3_f32 v229, v229, s62, v95
	v_med3_f32 v230, v230, s62, v95
	v_med3_f32 v231, v231, s62, v95
	v_med3_f32 v232, v232, s62, v95
	v_med3_f32 v233, v233, s62, v95
	v_med3_f32 v234, v234, s62, v95
	v_med3_f32 v235, v235, s62, v95
	v_med3_f32 v236, v236, s62, v95
	v_med3_f32 v237, v237, s62, v95
	v_med3_f32 v238, v238, s62, v95
	v_med3_f32 v239, v239, s62, v95
	v_med3_f32 v240, v240, s62, v95
	v_med3_f32 v241, v241, s62, v95
	v_mov_b32_e32 v242, 0
	v_mov_b32_e32 v243, 0
	v_mov_b32_e32 v244, 0
	v_mov_b32_e32 v245, 0
	v_cvt_pk_fp8_f32 v242, v226, v227
	v_cvt_pk_fp8_f32 v243, v230, v231
	v_cvt_pk_fp8_f32 v244, v234, v235
	v_cvt_pk_fp8_f32 v245, v238, v239
	v_cvt_pk_fp8_f32 v242, v228, v229 op_sel:[0,0,1]
	v_cvt_pk_fp8_f32 v243, v232, v233 op_sel:[0,0,1]
	v_cvt_pk_fp8_f32 v244, v236, v237 op_sel:[0,0,1]
	v_cvt_pk_fp8_f32 v245, v240, v241 op_sel:[0,0,1]
	s_nop 0
	global_store_dwordx4 v78, v[242:245], s[6:7]
	s_waitcnt vmcnt(10)
	v_mul_f32_e32 v176, v26, v176
	v_mul_f32_e32 v177, v26, v177
	v_mul_f32_e32 v178, v26, v178
	v_mul_f32_e32 v179, v26, v179
	ds_write_b128 v210, v[176:179]
	v_mul_f32_e32 v180, v27, v180
	v_mul_f32_e32 v181, v27, v181
	v_mul_f32_e32 v182, v27, v182
	v_mul_f32_e32 v183, v27, v183
	ds_write_b128 v210, v[180:183] offset:1024
	v_mul_f32_e32 v184, v28, v184
	v_mul_f32_e32 v185, v28, v185
	v_mul_f32_e32 v186, v28, v186
	v_mul_f32_e32 v187, v28, v187
	ds_write_b128 v210, v[184:187] offset:2048
	v_mul_f32_e32 v188, v29, v188
	v_mul_f32_e32 v189, v29, v189
	v_mul_f32_e32 v190, v29, v190
	v_mul_f32_e32 v191, v29, v191
	ds_write_b128 v210, v[188:191] offset:3072
	v_mul_f32_e32 v192, v30, v192
	v_mul_f32_e32 v193, v30, v193
	v_mul_f32_e32 v194, v30, v194
	v_mul_f32_e32 v195, v30, v195
	ds_write_b128 v210, v[192:195] offset:4096
	v_mul_f32_e32 v196, v31, v196
	v_mul_f32_e32 v197, v31, v197
	v_mul_f32_e32 v198, v31, v198
	v_mul_f32_e32 v199, v31, v199
	ds_write_b128 v210, v[196:199] offset:5120
	v_mul_f32_e32 v200, v32, v200
	v_mul_f32_e32 v201, v32, v201
	v_mul_f32_e32 v202, v32, v202
	v_mul_f32_e32 v203, v32, v203
	ds_write_b128 v210, v[200:203] offset:6144
	v_mul_f32_e32 v204, v33, v204
	v_mul_f32_e32 v205, v33, v205
	v_mul_f32_e32 v206, v33, v206
	v_mul_f32_e32 v207, v33, v207
	ds_write_b128 v210, v[204:207] offset:7168
	s_waitcnt lgkmcnt(0)
	s_barrier
; #define GAS __attribute__((address_space(1)))
; #define LAS __attribute__((address_space(3)))
; #define LDS_WAIT() asm volatile("s_waitcnt lgkmcnt(0)" ::: "memory")
; __device__ __forceinline__ unsigned pk4_fp8(float a, float b, float c, float d) {
;     a = fminf(fmaxf(a, -448.f), 448.f); b = fminf(fmaxf(b, -448.f), 448.f); c = fminf(fmaxf(c, -448.f), 448.f); d = fminf(fmaxf(d, -448.f), 448.f);
;     int w = __builtin_amdgcn_cvt_pk_fp8_f32(a, b, 0, false); w = __builtin_amdgcn_cvt_pk_fp8_f32(c, d, w, true); return (unsigned)w; }
;     const int pr = item >> 1, kb = 2 * (pr / nblk) + (item & 1), nb = pr % nblk, k0 = 64 * kb, n0 = 32 * nb;
;     const int nr = n0 + (lane & 31); const int sc = MAP == 1 ? src_col_in(nr) : nr;
;     float v[32];
; #pragma unroll
;     for (int i = 0; i < 32; ++i) v[i] = sc >= 0 ? W[(size_t)(k0 + 2 * i + (lane >> 5)) * Nsrc + sc] : 0.f;
; #pragma unroll
;     for (int i = 0; i < 32; ++i) { const int k = k0 + 2 * i + (lane >> 5); float x = v[i] * wscale; if (KS) x *= (k < ksplit ? ksA[k] : ksB[k - ksplit]); scr[(2 * i + (lane >> 5)) * 33 + (lane & 31)] = x; }
;     LDS_WAIT(); asm volatile("" ::: "memory");
;     const int c = lane & 7;
; #pragma unroll
;     for (int j = 0; j < 4; ++j) { const int n = (lane >> 3) + 8 * j; const LAS float* s = scr + (8 * c) * 33 + n;
;         const unsigned long long o = (unsigned long long)pg8::pk4_fp8(s[0 * 33], s[1 * 33], s[2 * 33], s[3 * 33]) | ((unsigned long long)pg8::pk4_fp8(s[4 * 33], s[5 * 33], s[6 * 33], s[7 * 33]) << 32);
;         *(GAS unsigned long long*)(WT + (size_t)(n0 + n) * K + k0 + 8 * c) = o; }
;     LDS_WAIT(); asm volatile("" ::: "memory");
; }
	s_add_u32 s8, s30, 0x3000
	s_addc_u32 s9, s31, 0
	global_load_dwordx4 v[176:179], v74, s[8:9]
	s_add_u32 s8, s8, 0x20000
	s_addc_u32 s9, s9, 0
	global_load_dwordx4 v[180:183], v74, s[8:9]
	s_add_u32 s8, s8, 0x20000
	s_addc_u32 s9, s9, 0
	global_load_dwordx4 v[184:187], v74, s[8:9]
	s_add_u32 s8, s8, 0x20000
	s_addc_u32 s9, s9, 0
	global_load_dwordx4 v[188:191], v74, s[8:9]
	s_add_u32 s8, s8, 0x20000
	s_addc_u32 s9, s9, 0
	global_load_dwordx4 v[192:195], v74, s[8:9]
	s_add_u32 s8, s8, 0x20000
	s_addc_u32 s9, s9, 0
	global_load_dwordx4 v[196:199], v74, s[8:9]
	s_add_u32 s8, s8, 0x20000
	s_addc_u32 s9, s9, 0
	global_load_dwordx4 v[200:203], v74, s[8:9]
	s_add_u32 s8, s8, 0x20000
	s_addc_u32 s9, s9, 0
	global_load_dwordx4 v[204:207], v74, s[8:9]
	s_add_u32 s6, s32, 0x400000
	s_addc_u32 s7, s33, 0
	ds_read_b32 v226, v212
	ds_read_b32 v227, v212 offset:512
	ds_read_b32 v228, v212 offset:1024
	ds_read_b32 v229, v212 offset:1536
	ds_read_b32 v230, v212 offset:2048
	ds_read_b32 v231, v212 offset:2560
	ds_read_b32 v232, v212 offset:3072
	ds_read_b32 v233, v212 offset:3584
	ds_read_b32 v234, v212 offset:4096
	ds_read_b32 v235, v212 offset:4608
	ds_read_b32 v236, v212 offset:5120
	ds_read_b32 v237, v212 offset:5632
	ds_read_b32 v238, v212 offset:6144
	ds_read_b32 v239, v212 offset:6656
	ds_read_b32 v240, v212 offset:7168
	ds_read_b32 v241, v212 offset:7680
	s_waitcnt lgkmcnt(0)
	v_max_f32_e32 v226, v226, v226
	v_max_f32_e32 v227, v227, v227
	v_max_f32_e32 v228, v228, v228
	v_max_f32_e32 v229, v229, v229
	v_max_f32_e32 v230, v230, v230
	v_max_f32_e32 v231, v231, v231
	v_max_f32_e32 v232, v232, v232
	v_max_f32_e32 v233, v233, v233
	v_max_f32_e32 v234, v234, v234
	v_max_f32_e32 v235, v235, v235
	v_max_f32_e32 v236, v236, v236
	v_max_f32_e32 v237, v237, v237
	v_max_f32_e32 v238, v238, v238
	v_max_f32_e32 v239, v239, v239
	v_max_f32_e32 v240, v240, v240
	v_max_f32_e32 v241, v241, v241
	v_med3_f32 v226, v226, s62, v95
	v_med3_f32 v227, v227, s62, v95
	v_med3_f32 v228, v228, s62, v95
	v_med3_f32 v229, v229, s62, v95
	v_med3_f32 v230, v230, s62, v95
	v_med3_f32 v231, v231, s62, v95
	v_med3_f32 v232, v232, s62, v95
	v_med3_f32 v233, v233, s62, v95
	v_med3_f32 v234, v234, s62, v95
	v_med3_f32 v235, v235, s62, v95
	v_med3_f32 v236, v236, s62, v95
	v_med3_f32 v237, v237, s62, v95
	v_med3_f32 v238, v238, s62, v95
	v_med3_f32 v239, v239, s62, v95
	v_med3_f32 v240, v240, s62, v95
	v_med3_f32 v241, v241, s62, v95
	v_mov_b32_e32 v242, 0
	v_mov_b32_e32 v243, 0
	v_mov_b32_e32 v244, 0
	v_mov_b32_e32 v245, 0
	v_cvt_pk_fp8_f32 v242, v226, v227
	v_cvt_pk_fp8_f32 v243, v230, v231
	v_cvt_pk_fp8_f32 v244, v234, v235
	v_cvt_pk_fp8_f32 v245, v238, v239
	v_cvt_pk_fp8_f32 v242, v228, v229 op_sel:[0,0,1]
	v_cvt_pk_fp8_f32 v243, v232, v233 op_sel:[0,0,1]
	v_cvt_pk_fp8_f32 v244, v236, v237 op_sel:[0,0,1]
	v_cvt_pk_fp8_f32 v245, v240, v241 op_sel:[0,0,1]
	s_nop 0
	global_store_dwordx4 v77, v[242:245], s[6:7]
	ds_read_b32 v226, v214
	ds_read_b32 v227, v214 offset:512
	ds_read_b32 v228, v214 offset:1024
	ds_read_b32 v229, v214 offset:1536
	ds_read_b32 v230, v214 offset:2048
	ds_read_b32 v231, v214 offset:2560
	ds_read_b32 v232, v214 offset:3072
	ds_read_b32 v233, v214 offset:3584
	ds_read_b32 v234, v214 offset:4096
	ds_read_b32 v235, v214 offset:4608
	ds_read_b32 v236, v214 offset:5120
	ds_read_b32 v237, v214 offset:5632
	ds_read_b32 v238, v214 offset:6144
	ds_read_b32 v239, v214 offset:6656
	ds_read_b32 v240, v214 offset:7168
	ds_read_b32 v241, v214 offset:7680
	s_waitcnt lgkmcnt(0)
	v_max_f32_e32 v226, v226, v226
	v_max_f32_e32 v227, v227, v227
	v_max_f32_e32 v228, v228, v228
	v_max_f32_e32 v229, v229, v229
	v_max_f32_e32 v230, v230, v230
	v_max_f32_e32 v231, v231, v231
	v_max_f32_e32 v232, v232, v232
	v_max_f32_e32 v233, v233, v233
	v_max_f32_e32 v234, v234, v234
	v_max_f32_e32 v235, v235, v235
	v_max_f32_e32 v236, v236, v236
	v_max_f32_e32 v237, v237, v237
	v_max_f32_e32 v238, v238, v238
	v_max_f32_e32 v239, v239, v239
	v_max_f32_e32 v240, v240, v240
	v_max_f32_e32 v241, v241, v241
	v_med3_f32 v226, v226, s62, v95
	v_med3_f32 v227, v227, s62, v95
	v_med3_f32 v228, v228, s62, v95
	v_med3_f32 v229, v229, s62, v95
	v_med3_f32 v230, v230, s62, v95
	v_med3_f32 v231, v231, s62, v95
	v_med3_f32 v232, v232, s62, v95
	v_med3_f32 v233, v233, s62, v95
	v_med3_f32 v234, v234, s62, v95
	v_med3_f32 v235, v235, s62, v95
	v_med3_f32 v236, v236, s62, v95
	v_med3_f32 v237, v237, s62, v95
	v_med3_f32 v238, v238, s62, v95
	v_med3_f32 v239, v239, s62, v95
	v_med3_f32 v240, v240, s62, v95
	v_med3_f32 v241, v241, s62, v95
	v_mov_b32_e32 v242, 0
	v_mov_b32_e32 v243, 0
	v_mov_b32_e32 v244, 0
	v_mov_b32_e32 v245, 0
	v_cvt_pk_fp8_f32 v242, v226, v227
	v_cvt_pk_fp8_f32 v243, v230, v231
	v_cvt_pk_fp8_f32 v244, v234, v235
	v_cvt_pk_fp8_f32 v245, v238, v239
	v_cvt_pk_fp8_f32 v242, v228, v229 op_sel:[0,0,1]
	v_cvt_pk_fp8_f32 v243, v232, v233 op_sel:[0,0,1]
	v_cvt_pk_fp8_f32 v244, v236, v237 op_sel:[0,0,1]
	v_cvt_pk_fp8_f32 v245, v240, v241 op_sel:[0,0,1]
	s_nop 0
	global_store_dwordx4 v78, v[242:245], s[6:7]
	s_waitcnt vmcnt(12)
	v_mul_f32_e32 v144, v26, v144
	v_mul_f32_e32 v145, v26, v145
	v_mul_f32_e32 v146, v26, v146
	v_mul_f32_e32 v147, v26, v147
	ds_write_b128 v209, v[144:147]
	v_mul_f32_e32 v148, v27, v148
	v_mul_f32_e32 v149, v27, v149
	v_mul_f32_e32 v150, v27, v150
	v_mul_f32_e32 v151, v27, v151
	ds_write_b128 v209, v[148:151] offset:1024
	v_mul_f32_e32 v152, v28, v152
	v_mul_f32_e32 v153, v28, v153
	v_mul_f32_e32 v154, v28, v154
	v_mul_f32_e32 v155, v28, v155
	ds_write_b128 v209, v[152:155] offset:2048
	v_mul_f32_e32 v156, v29, v156
	v_mul_f32_e32 v157, v29, v157
	v_mul_f32_e32 v158, v29, v158
	v_mul_f32_e32 v159, v29, v159
	ds_write_b128 v209, v[156:159] offset:3072
	v_mul_f32_e32 v160, v30, v160
	v_mul_f32_e32 v161, v30, v161
	v_mul_f32_e32 v162, v30, v162
	v_mul_f32_e32 v163, v30, v163
	ds_write_b128 v209, v[160:163] offset:4096
	v_mul_f32_e32 v164, v31, v164
	v_mul_f32_e32 v165, v31, v165
	v_mul_f32_e32 v166, v31, v166
	v_mul_f32_e32 v167, v31, v167
	ds_write_b128 v209, v[164:167] offset:5120
	v_mul_f32_e32 v168, v32, v168
	v_mul_f32_e32 v169, v32, v169
	v_mul_f32_e32 v170, v32, v170
	v_mul_f32_e32 v171, v32, v171
	ds_write_b128 v209, v[168:171] offset:6144
	v_mul_f32_e32 v172, v33, v172
	v_mul_f32_e32 v173, v33, v173
	v_mul_f32_e32 v174, v33, v174
	v_mul_f32_e32 v175, v33, v175
	ds_write_b128 v209, v[172:175] offset:7168
	s_waitcnt lgkmcnt(0)
	s_barrier
; #define GAS __attribute__((address_space(1)))
; #define LAS __attribute__((address_space(3)))
; #define LDS_WAIT() asm volatile("s_waitcnt lgkmcnt(0)" ::: "memory")
; __device__ __forceinline__ unsigned pk4_fp8(float a, float b, float c, float d) {
;     a = fminf(fmaxf(a, -448.f), 448.f); b = fminf(fmaxf(b, -448.f), 448.f); c = fminf(fmaxf(c, -448.f), 448.f); d = fminf(fmaxf(d, -448.f), 448.f);
;     int w = __builtin_amdgcn_cvt_pk_fp8_f32(a, b, 0, false); w = __builtin_amdgcn_cvt_pk_fp8_f32(c, d, w, true); return (unsigned)w; }
;     const int pr = item >> 1, kb = 2 * (pr / nblk) + (item & 1), nb = pr % nblk, k0 = 64 * kb, n0 = 32 * nb;
;     const int nr = n0 + (lane & 31); const int sc = MAP == 1 ? src_col_in(nr) : nr;
;     float v[32];
; #pragma unroll
;     for (int i = 0; i < 32; ++i) v[i] = sc >= 0 ? W[(size_t)(k0 + 2 * i + (lane >> 5)) * Nsrc + sc] : 0.f;
; #pragma unroll
;     for (int i = 0; i < 32; ++i) { const int k = k0 + 2 * i + (lane >> 5); float x = v[i] * wscale; if (KS) x *= (k < ksplit ? ksA[k] : ksB[k - ksplit]); scr[(2 * i + (lane >> 5)) * 33 + (lane & 31)] = x; }
;     LDS_WAIT(); asm volatile("" ::: "memory");
;     const int c = lane & 7;
; #pragma unroll
;     for (int j = 0; j < 4; ++j) { const int n = (lane >> 3) + 8 * j; const LAS float* s = scr + (8 * c) * 33 + n;
;         const unsigned long long o = (unsigned long long)pg8::pk4_fp8(s[0 * 33], s[1 * 33], s[2 * 33], s[3 * 33]) | ((unsigned long long)pg8::pk4_fp8(s[4 * 33], s[5 * 33], s[6 * 33], s[7 * 33]) << 32);
;         *(GAS unsigned long long*)(WT + (size_t)(n0 + n) * K + k0 + 8 * c) = o; }
;     LDS_WAIT(); asm volatile("" ::: "memory");
; }
	s_add_u32 s8, s30, 0x4000
	s_addc_u32 s9, s31, 0
	global_load_dwordx4 v[144:147], v74, s[8:9]
	s_add_u32 s8, s8, 0x20000
	s_addc_u32 s9, s9, 0
	global_load_dwordx4 v[148:151], v74, s[8:9]
	s_add_u32 s8, s8, 0x20000
	s_addc_u32 s9, s9, 0
	global_load_dwordx4 v[152:155], v74, s[8:9]
	s_add_u32 s8, s8, 0x20000
	s_addc_u32 s9, s9, 0
	global_load_dwordx4 v[156:159], v74, s[8:9]
	s_add_u32 s8, s8, 0x20000
	s_addc_u32 s9, s9, 0
	global_load_dwordx4 v[160:163], v74, s[8:9]
	s_add_u32 s8, s8, 0x20000
	s_addc_u32 s9, s9, 0
	global_load_dwordx4 v[164:167], v74, s[8:9]
	s_add_u32 s8, s8, 0x20000
	s_addc_u32 s9, s9, 0
	global_load_dwordx4 v[168:171], v74, s[8:9]
	s_add_u32 s8, s8, 0x20000
	s_addc_u32 s9, s9, 0
	global_load_dwordx4 v[172:175], v74, s[8:9]
	s_add_u32 s6, s32, 0x800000
	s_addc_u32 s7, s33, 0
	ds_read_b32 v226, v211
	ds_read_b32 v227, v211 offset:512
	ds_read_b32 v228, v211 offset:1024
	ds_read_b32 v229, v211 offset:1536
	ds_read_b32 v230, v211 offset:2048
	ds_read_b32 v231, v211 offset:2560
	ds_read_b32 v232, v211 offset:3072
	ds_read_b32 v233, v211 offset:3584
	ds_read_b32 v234, v211 offset:4096
	ds_read_b32 v235, v211 offset:4608
	ds_read_b32 v236, v211 offset:5120
	ds_read_b32 v237, v211 offset:5632
	ds_read_b32 v238, v211 offset:6144
	ds_read_b32 v239, v211 offset:6656
	ds_read_b32 v240, v211 offset:7168
	ds_read_b32 v241, v211 offset:7680
	s_waitcnt lgkmcnt(0)
	v_max_f32_e32 v226, v226, v226
	v_max_f32_e32 v227, v227, v227
	v_max_f32_e32 v228, v228, v228
	v_max_f32_e32 v229, v229, v229
	v_max_f32_e32 v230, v230, v230
	v_max_f32_e32 v231, v231, v231
	v_max_f32_e32 v232, v232, v232
	v_max_f32_e32 v233, v233, v233
	v_max_f32_e32 v234, v234, v234
	v_max_f32_e32 v235, v235, v235
	v_max_f32_e32 v236, v236, v236
	v_max_f32_e32 v237, v237, v237
	v_max_f32_e32 v238, v238, v238
	v_max_f32_e32 v239, v239, v239
	v_max_f32_e32 v240, v240, v240
	v_max_f32_e32 v241, v241, v241
	v_med3_f32 v226, v226, s62, v95
	v_med3_f32 v227, v227, s62, v95
	v_med3_f32 v228, v228, s62, v95
	v_med3_f32 v229, v229, s62, v95
	v_med3_f32 v230, v230, s62, v95
	v_med3_f32 v231, v231, s62, v95
	v_med3_f32 v232, v232, s62, v95
	v_med3_f32 v233, v233, s62, v95
	v_med3_f32 v234, v234, s62, v95
	v_med3_f32 v235, v235, s62, v95
	v_med3_f32 v236, v236, s62, v95
	v_med3_f32 v237, v237, s62, v95
	v_med3_f32 v238, v238, s62, v95
	v_med3_f32 v239, v239, s62, v95
	v_med3_f32 v240, v240, s62, v95
	v_med3_f32 v241, v241, s62, v95
	v_mov_b32_e32 v242, 0
	v_mov_b32_e32 v243, 0
	v_mov_b32_e32 v244, 0
	v_mov_b32_e32 v245, 0
	v_cvt_pk_fp8_f32 v242, v226, v227
	v_cvt_pk_fp8_f32 v243, v230, v231
	v_cvt_pk_fp8_f32 v244, v234, v235
	v_cvt_pk_fp8_f32 v245, v238, v239
	v_cvt_pk_fp8_f32 v242, v228, v229 op_sel:[0,0,1]
	v_cvt_pk_fp8_f32 v243, v232, v233 op_sel:[0,0,1]
	v_cvt_pk_fp8_f32 v244, v236, v237 op_sel:[0,0,1]
	v_cvt_pk_fp8_f32 v245, v240, v241 op_sel:[0,0,1]
	s_nop 0
	global_store_dwordx4 v77, v[242:245], s[6:7]
	ds_read_b32 v226, v213
	ds_read_b32 v227, v213 offset:512
	ds_read_b32 v228, v213 offset:1024
	ds_read_b32 v229, v213 offset:1536
	ds_read_b32 v230, v213 offset:2048
	ds_read_b32 v231, v213 offset:2560
	ds_read_b32 v232, v213 offset:3072
	ds_read_b32 v233, v213 offset:3584
	ds_read_b32 v234, v213 offset:4096
	ds_read_b32 v235, v213 offset:4608
	ds_read_b32 v236, v213 offset:5120
	ds_read_b32 v237, v213 offset:5632
	ds_read_b32 v238, v213 offset:6144
	ds_read_b32 v239, v213 offset:6656
	ds_read_b32 v240, v213 offset:7168
	ds_read_b32 v241, v213 offset:7680
	s_waitcnt lgkmcnt(0)
	v_max_f32_e32 v226, v226, v226
	v_max_f32_e32 v227, v227, v227
	v_max_f32_e32 v228, v228, v228
	v_max_f32_e32 v229, v229, v229
	v_max_f32_e32 v230, v230, v230
	v_max_f32_e32 v231, v231, v231
	v_max_f32_e32 v232, v232, v232
	v_max_f32_e32 v233, v233, v233
	v_max_f32_e32 v234, v234, v234
	v_max_f32_e32 v235, v235, v235
	v_max_f32_e32 v236, v236, v236
	v_max_f32_e32 v237, v237, v237
	v_max_f32_e32 v238, v238, v238
	v_max_f32_e32 v239, v239, v239
	v_max_f32_e32 v240, v240, v240
	v_max_f32_e32 v241, v241, v241
	v_med3_f32 v226, v226, s62, v95
	v_med3_f32 v227, v227, s62, v95
	v_med3_f32 v228, v228, s62, v95
	v_med3_f32 v229, v229, s62, v95
	v_med3_f32 v230, v230, s62, v95
	v_med3_f32 v231, v231, s62, v95
	v_med3_f32 v232, v232, s62, v95
	v_med3_f32 v233, v233, s62, v95
	v_med3_f32 v234, v234, s62, v95
	v_med3_f32 v235, v235, s62, v95
	v_med3_f32 v236, v236, s62, v95
	v_med3_f32 v237, v237, s62, v95
	v_med3_f32 v238, v238, s62, v95
	v_med3_f32 v239, v239, s62, v95
	v_med3_f32 v240, v240, s62, v95
	v_med3_f32 v241, v241, s62, v95
	v_mov_b32_e32 v242, 0
	v_mov_b32_e32 v243, 0
	v_mov_b32_e32 v244, 0
	v_mov_b32_e32 v245, 0
	v_cvt_pk_fp8_f32 v242, v226, v227
	v_cvt_pk_fp8_f32 v243, v230, v231
	v_cvt_pk_fp8_f32 v244, v234, v235
	v_cvt_pk_fp8_f32 v245, v238, v239
	v_cvt_pk_fp8_f32 v242, v228, v229 op_sel:[0,0,1]
	v_cvt_pk_fp8_f32 v243, v232, v233 op_sel:[0,0,1]
	v_cvt_pk_fp8_f32 v244, v236, v237 op_sel:[0,0,1]
	v_cvt_pk_fp8_f32 v245, v240, v241 op_sel:[0,0,1]
	s_nop 0
	global_store_dwordx4 v78, v[242:245], s[6:7]
	s_waitcnt vmcnt(12)
	v_mul_f32_e32 v176, v26, v176
	v_mul_f32_e32 v177, v26, v177
	v_mul_f32_e32 v178, v26, v178
	v_mul_f32_e32 v179, v26, v179
	ds_write_b128 v210, v[176:179]
	v_mul_f32_e32 v180, v27, v180
	v_mul_f32_e32 v181, v27, v181
	v_mul_f32_e32 v182, v27, v182
	v_mul_f32_e32 v183, v27, v183
	ds_write_b128 v210, v[180:183] offset:1024
	v_mul_f32_e32 v184, v28, v184
	v_mul_f32_e32 v185, v28, v185
	v_mul_f32_e32 v186, v28, v186
	v_mul_f32_e32 v187, v28, v187
	ds_write_b128 v210, v[184:187] offset:2048
	v_mul_f32_e32 v188, v29, v188
	v_mul_f32_e32 v189, v29, v189
	v_mul_f32_e32 v190, v29, v190
	v_mul_f32_e32 v191, v29, v191
	ds_write_b128 v210, v[188:191] offset:3072
	v_mul_f32_e32 v192, v30, v192
	v_mul_f32_e32 v193, v30, v193
	v_mul_f32_e32 v194, v30, v194
	v_mul_f32_e32 v195, v30, v195
	ds_write_b128 v210, v[192:195] offset:4096
	v_mul_f32_e32 v196, v31, v196
	v_mul_f32_e32 v197, v31, v197
	v_mul_f32_e32 v198, v31, v198
	v_mul_f32_e32 v199, v31, v199
	ds_write_b128 v210, v[196:199] offset:5120
	v_mul_f32_e32 v200, v32, v200
	v_mul_f32_e32 v201, v32, v201
	v_mul_f32_e32 v202, v32, v202
	v_mul_f32_e32 v203, v32, v203
	ds_write_b128 v210, v[200:203] offset:6144
	v_mul_f32_e32 v204, v33, v204
	v_mul_f32_e32 v205, v33, v205
	v_mul_f32_e32 v206, v33, v206
	v_mul_f32_e32 v207, v33, v207
	ds_write_b128 v210, v[204:207] offset:7168
	s_waitcnt lgkmcnt(0)
	s_barrier
; #define GAS __attribute__((address_space(1)))
; #define LAS __attribute__((address_space(3)))
; #define LDS_WAIT() asm volatile("s_waitcnt lgkmcnt(0)" ::: "memory")
; __device__ __forceinline__ unsigned pk4_fp8(float a, float b, float c, float d) {
;     a = fminf(fmaxf(a, -448.f), 448.f); b = fminf(fmaxf(b, -448.f), 448.f); c = fminf(fmaxf(c, -448.f), 448.f); d = fminf(fmaxf(d, -448.f), 448.f);
;     int w = __builtin_amdgcn_cvt_pk_fp8_f32(a, b, 0, false); w = __builtin_amdgcn_cvt_pk_fp8_f32(c, d, w, true); return (unsigned)w; }
;     const int pr = item >> 1, kb = 2 * (pr / nblk) + (item & 1), nb = pr % nblk, k0 = 64 * kb, n0 = 32 * nb;
;     const int nr = n0 + (lane & 31); const int sc = MAP == 1 ? src_col_in(nr) : nr;
;     float v[32];
; #pragma unroll
;     for (int i = 0; i < 32; ++i) v[i] = sc >= 0 ? W[(size_t)(k0 + 2 * i + (lane >> 5)) * Nsrc + sc] : 0.f;
; #pragma unroll
;     for (int i = 0; i < 32; ++i) { const int k = k0 + 2 * i + (lane >> 5); float x = v[i] * wscale; if (KS) x *= (k < ksplit ? ksA[k] : ksB[k - ksplit]); scr[(2 * i + (lane >> 5)) * 33 + (lane & 31)] = x; }
;     LDS_WAIT(); asm volatile("" ::: "memory");
;     const int c = lane & 7;
; #pragma unroll
;     for (int j = 0; j < 4; ++j) { const int n = (lane >> 3) + 8 * j; const LAS float* s = scr + (8 * c) * 33 + n;
;         const unsigned long long o = (unsigned long long)pg8::pk4_fp8(s[0 * 33], s[1 * 33], s[2 * 33], s[3 * 33]) | ((unsigned long long)pg8::pk4_fp8(s[4 * 33], s[5 * 33], s[6 * 33], s[7 * 33]) << 32);
;         *(GAS unsigned long long*)(WT + (size_t)(n0 + n) * K + k0 + 8 * c) = o; }
;     LDS_WAIT(); asm volatile("" ::: "memory");
; }
	s_add_u32 s8, s30, 0x5000
	s_addc_u32 s9, s31, 0
	global_load_dwordx4 v[176:179], v74, s[8:9]
	s_add_u32 s8, s8, 0x20000
	s_addc_u32 s9, s9, 0
	global_load_dwordx4 v[180:183], v74, s[8:9]
	s_add_u32 s8, s8, 0x20000
	s_addc_u32 s9, s9, 0
	global_load_dwordx4 v[184:187], v74, s[8:9]
	s_add_u32 s8, s8, 0x20000
	s_addc_u32 s9, s9, 0
	global_load_dwordx4 v[188:191], v74, s[8:9]
	s_add_u32 s8, s8, 0x20000
	s_addc_u32 s9, s9, 0
	global_load_dwordx4 v[192:195], v74, s[8:9]
	s_add_u32 s8, s8, 0x20000
	s_addc_u32 s9, s9, 0
	global_load_dwordx4 v[196:199], v74, s[8:9]
	s_add_u32 s8, s8, 0x20000
	s_addc_u32 s9, s9, 0
	global_load_dwordx4 v[200:203], v74, s[8:9]
	s_add_u32 s8, s8, 0x20000
	s_addc_u32 s9, s9, 0
	global_load_dwordx4 v[204:207], v74, s[8:9]
	s_add_u32 s6, s32, 0xc00000
	s_addc_u32 s7, s33, 0
	ds_read_b32 v226, v212
	ds_read_b32 v227, v212 offset:512
	ds_read_b32 v228, v212 offset:1024
	ds_read_b32 v229, v212 offset:1536
	ds_read_b32 v230, v212 offset:2048
	ds_read_b32 v231, v212 offset:2560
	ds_read_b32 v232, v212 offset:3072
	ds_read_b32 v233, v212 offset:3584
	ds_read_b32 v234, v212 offset:4096
	ds_read_b32 v235, v212 offset:4608
	ds_read_b32 v236, v212 offset:5120
	ds_read_b32 v237, v212 offset:5632
	ds_read_b32 v238, v212 offset:6144
	ds_read_b32 v239, v212 offset:6656
	ds_read_b32 v240, v212 offset:7168
	ds_read_b32 v241, v212 offset:7680
	s_waitcnt lgkmcnt(0)
	v_max_f32_e32 v226, v226, v226
	v_max_f32_e32 v227, v227, v227
	v_max_f32_e32 v228, v228, v228
	v_max_f32_e32 v229, v229, v229
	v_max_f32_e32 v230, v230, v230
	v_max_f32_e32 v231, v231, v231
	v_max_f32_e32 v232, v232, v232
	v_max_f32_e32 v233, v233, v233
	v_max_f32_e32 v234, v234, v234
	v_max_f32_e32 v235, v235, v235
	v_max_f32_e32 v236, v236, v236
	v_max_f32_e32 v237, v237, v237
	v_max_f32_e32 v238, v238, v238
	v_max_f32_e32 v239, v239, v239
	v_max_f32_e32 v240, v240, v240
	v_max_f32_e32 v241, v241, v241
	v_med3_f32 v226, v226, s62, v95
	v_med3_f32 v227, v227, s62, v95
	v_med3_f32 v228, v228, s62, v95
	v_med3_f32 v229, v229, s62, v95
	v_med3_f32 v230, v230, s62, v95
	v_med3_f32 v231, v231, s62, v95
	v_med3_f32 v232, v232, s62, v95
	v_med3_f32 v233, v233, s62, v95
	v_med3_f32 v234, v234, s62, v95
	v_med3_f32 v235, v235, s62, v95
	v_med3_f32 v236, v236, s62, v95
	v_med3_f32 v237, v237, s62, v95
	v_med3_f32 v238, v238, s62, v95
	v_med3_f32 v239, v239, s62, v95
	v_med3_f32 v240, v240, s62, v95
	v_med3_f32 v241, v241, s62, v95
	v_mov_b32_e32 v242, 0
	v_mov_b32_e32 v243, 0
	v_mov_b32_e32 v244, 0
	v_mov_b32_e32 v245, 0
	v_cvt_pk_fp8_f32 v242, v226, v227
	v_cvt_pk_fp8_f32 v243, v230, v231
	v_cvt_pk_fp8_f32 v244, v234, v235
	v_cvt_pk_fp8_f32 v245, v238, v239
	v_cvt_pk_fp8_f32 v242, v228, v229 op_sel:[0,0,1]
	v_cvt_pk_fp8_f32 v243, v232, v233 op_sel:[0,0,1]
	v_cvt_pk_fp8_f32 v244, v236, v237 op_sel:[0,0,1]
	v_cvt_pk_fp8_f32 v245, v240, v241 op_sel:[0,0,1]
	s_nop 0
	global_store_dwordx4 v77, v[242:245], s[6:7]
	ds_read_b32 v226, v214
	ds_read_b32 v227, v214 offset:512
	ds_read_b32 v228, v214 offset:1024
	ds_read_b32 v229, v214 offset:1536
	ds_read_b32 v230, v214 offset:2048
	ds_read_b32 v231, v214 offset:2560
	ds_read_b32 v232, v214 offset:3072
	ds_read_b32 v233, v214 offset:3584
	ds_read_b32 v234, v214 offset:4096
	ds_read_b32 v235, v214 offset:4608
	ds_read_b32 v236, v214 offset:5120
	ds_read_b32 v237, v214 offset:5632
	ds_read_b32 v238, v214 offset:6144
	ds_read_b32 v239, v214 offset:6656
	ds_read_b32 v240, v214 offset:7168
	ds_read_b32 v241, v214 offset:7680
	s_waitcnt lgkmcnt(0)
	v_max_f32_e32 v226, v226, v226
	v_max_f32_e32 v227, v227, v227
	v_max_f32_e32 v228, v228, v228
	v_max_f32_e32 v229, v229, v229
	v_max_f32_e32 v230, v230, v230
	v_max_f32_e32 v231, v231, v231
	v_max_f32_e32 v232, v232, v232
	v_max_f32_e32 v233, v233, v233
	v_max_f32_e32 v234, v234, v234
	v_max_f32_e32 v235, v235, v235
	v_max_f32_e32 v236, v236, v236
	v_max_f32_e32 v237, v237, v237
	v_max_f32_e32 v238, v238, v238
	v_max_f32_e32 v239, v239, v239
	v_max_f32_e32 v240, v240, v240
	v_max_f32_e32 v241, v241, v241
	v_med3_f32 v226, v226, s62, v95
	v_med3_f32 v227, v227, s62, v95
	v_med3_f32 v228, v228, s62, v95
	v_med3_f32 v229, v229, s62, v95
	v_med3_f32 v230, v230, s62, v95
	v_med3_f32 v231, v231, s62, v95
	v_med3_f32 v232, v232, s62, v95
	v_med3_f32 v233, v233, s62, v95
	v_med3_f32 v234, v234, s62, v95
	v_med3_f32 v235, v235, s62, v95
	v_med3_f32 v236, v236, s62, v95
	v_med3_f32 v237, v237, s62, v95
	v_med3_f32 v238, v238, s62, v95
	v_med3_f32 v239, v239, s62, v95
	v_med3_f32 v240, v240, s62, v95
	v_med3_f32 v241, v241, s62, v95
	v_mov_b32_e32 v242, 0
	v_mov_b32_e32 v243, 0
	v_mov_b32_e32 v244, 0
	v_mov_b32_e32 v245, 0
	v_cvt_pk_fp8_f32 v242, v226, v227
	v_cvt_pk_fp8_f32 v243, v230, v231
	v_cvt_pk_fp8_f32 v244, v234, v235
	v_cvt_pk_fp8_f32 v245, v238, v239
	v_cvt_pk_fp8_f32 v242, v228, v229 op_sel:[0,0,1]
	v_cvt_pk_fp8_f32 v243, v232, v233 op_sel:[0,0,1]
	v_cvt_pk_fp8_f32 v244, v236, v237 op_sel:[0,0,1]
	v_cvt_pk_fp8_f32 v245, v240, v241 op_sel:[0,0,1]
	s_nop 0
	global_store_dwordx4 v78, v[242:245], s[6:7]
	s_waitcnt vmcnt(12)
	v_mul_f32_e32 v144, v26, v144
	v_mul_f32_e32 v145, v26, v145
	v_mul_f32_e32 v146, v26, v146
	v_mul_f32_e32 v147, v26, v147
	ds_write_b128 v209, v[144:147]
	v_mul_f32_e32 v148, v27, v148
	v_mul_f32_e32 v149, v27, v149
	v_mul_f32_e32 v150, v27, v150
	v_mul_f32_e32 v151, v27, v151
	ds_write_b128 v209, v[148:151] offset:1024
	v_mul_f32_e32 v152, v28, v152
	v_mul_f32_e32 v153, v28, v153
	v_mul_f32_e32 v154, v28, v154
	v_mul_f32_e32 v155, v28, v155
	ds_write_b128 v209, v[152:155] offset:2048
	v_mul_f32_e32 v156, v29, v156
	v_mul_f32_e32 v157, v29, v157
	v_mul_f32_e32 v158, v29, v158
	v_mul_f32_e32 v159, v29, v159
	ds_write_b128 v209, v[156:159] offset:3072
	v_mul_f32_e32 v160, v30, v160
	v_mul_f32_e32 v161, v30, v161
	v_mul_f32_e32 v162, v30, v162
	v_mul_f32_e32 v163, v30, v163
	ds_write_b128 v209, v[160:163] offset:4096
	v_mul_f32_e32 v164, v31, v164
	v_mul_f32_e32 v165, v31, v165
	v_mul_f32_e32 v166, v31, v166
	v_mul_f32_e32 v167, v31, v167
	ds_write_b128 v209, v[164:167] offset:5120
	v_mul_f32_e32 v168, v32, v168
	v_mul_f32_e32 v169, v32, v169
	v_mul_f32_e32 v170, v32, v170
	v_mul_f32_e32 v171, v32, v171
	ds_write_b128 v209, v[168:171] offset:6144
	v_mul_f32_e32 v172, v33, v172
	v_mul_f32_e32 v173, v33, v173
	v_mul_f32_e32 v174, v33, v174
	v_mul_f32_e32 v175, v33, v175
	ds_write_b128 v209, v[172:175] offset:7168
	s_waitcnt lgkmcnt(0)
	s_barrier
; #define GAS __attribute__((address_space(1)))
; #define LAS __attribute__((address_space(3)))
; #define LDS_WAIT() asm volatile("s_waitcnt lgkmcnt(0)" ::: "memory")
; __device__ __forceinline__ unsigned pk4_fp8(float a, float b, float c, float d) {
;     a = fminf(fmaxf(a, -448.f), 448.f); b = fminf(fmaxf(b, -448.f), 448.f); c = fminf(fmaxf(c, -448.f), 448.f); d = fminf(fmaxf(d, -448.f), 448.f);
;     int w = __builtin_amdgcn_cvt_pk_fp8_f32(a, b, 0, false); w = __builtin_amdgcn_cvt_pk_fp8_f32(c, d, w, true); return (unsigned)w; }
;     const int pr = item >> 1, kb = 2 * (pr / nblk) + (item & 1), nb = pr % nblk, k0 = 64 * kb, n0 = 32 * nb;
;     const int nr = n0 + (lane & 31); const int sc = MAP == 1 ? src_col_in(nr) : nr;
;     float v[32];
; #pragma unroll
;     for (int i = 0; i < 32; ++i) v[i] = sc >= 0 ? W[(size_t)(k0 + 2 * i + (lane >> 5)) * Nsrc + sc] : 0.f;
; #pragma unroll
;     for (int i = 0; i < 32; ++i) { const int k = k0 + 2 * i + (lane >> 5); float x = v[i] * wscale; if (KS) x *= (k < ksplit ? ksA[k] : ksB[k - ksplit]); scr[(2 * i + (lane >> 5)) * 33 + (lane & 31)] = x; }
;     LDS_WAIT(); asm volatile("" ::: "memory");
;     const int c = lane & 7;
; #pragma unroll
;     for (int j = 0; j < 4; ++j) { const int n = (lane >> 3) + 8 * j; const LAS float* s = scr + (8 * c) * 33 + n;
;         const unsigned long long o = (unsigned long long)pg8::pk4_fp8(s[0 * 33], s[1 * 33], s[2 * 33], s[3 * 33]) | ((unsigned long long)pg8::pk4_fp8(s[4 * 33], s[5 * 33], s[6 * 33], s[7 * 33]) << 32);
;         *(GAS unsigned long long*)(WT + (size_t)(n0 + n) * K + k0 + 8 * c) = o; }
;     LDS_WAIT(); asm volatile("" ::: "memory");
; }
	s_add_u32 s8, s30, 0x6000
	s_addc_u32 s9, s31, 0
	global_load_dwordx4 v[144:147], v74, s[8:9]
	s_add_u32 s8, s8, 0x20000
	s_addc_u32 s9, s9, 0
	global_load_dwordx4 v[148:151], v74, s[8:9]
	s_add_u32 s8, s8, 0x20000
	s_addc_u32 s9, s9, 0
	global_load_dwordx4 v[152:155], v74, s[8:9]
	s_add_u32 s8, s8, 0x20000
	s_addc_u32 s9, s9, 0
	global_load_dwordx4 v[156:159], v74, s[8:9]
	s_add_u32 s8, s8, 0x20000
	s_addc_u32 s9, s9, 0
	global_load_dwordx4 v[160:163], v74, s[8:9]
	s_add_u32 s8, s8, 0x20000
	s_addc_u32 s9, s9, 0
	global_load_dwordx4 v[164:167], v74, s[8:9]
	s_add_u32 s8, s8, 0x20000
	s_addc_u32 s9, s9, 0
	global_load_dwordx4 v[168:171], v74, s[8:9]
	s_add_u32 s8, s8, 0x20000
	s_addc_u32 s9, s9, 0
	global_load_dwordx4 v[172:175], v74, s[8:9]
	s_add_u32 s6, s32, 0x1000000
	s_addc_u32 s7, s33, 0
	ds_read_b32 v226, v211
	ds_read_b32 v227, v211 offset:512
	ds_read_b32 v228, v211 offset:1024
	ds_read_b32 v229, v211 offset:1536
	ds_read_b32 v230, v211 offset:2048
	ds_read_b32 v231, v211 offset:2560
	ds_read_b32 v232, v211 offset:3072
	ds_read_b32 v233, v211 offset:3584
	ds_read_b32 v234, v211 offset:4096
	ds_read_b32 v235, v211 offset:4608
	ds_read_b32 v236, v211 offset:5120
	ds_read_b32 v237, v211 offset:5632
	ds_read_b32 v238, v211 offset:6144
	ds_read_b32 v239, v211 offset:6656
	ds_read_b32 v240, v211 offset:7168
	ds_read_b32 v241, v211 offset:7680
	s_waitcnt lgkmcnt(0)
	v_max_f32_e32 v226, v226, v226
	v_max_f32_e32 v227, v227, v227
	v_max_f32_e32 v228, v228, v228
	v_max_f32_e32 v229, v229, v229
	v_max_f32_e32 v230, v230, v230
	v_max_f32_e32 v231, v231, v231
	v_max_f32_e32 v232, v232, v232
	v_max_f32_e32 v233, v233, v233
	v_max_f32_e32 v234, v234, v234
	v_max_f32_e32 v235, v235, v235
	v_max_f32_e32 v236, v236, v236
	v_max_f32_e32 v237, v237, v237
	v_max_f32_e32 v238, v238, v238
	v_max_f32_e32 v239, v239, v239
	v_max_f32_e32 v240, v240, v240
	v_max_f32_e32 v241, v241, v241
	v_med3_f32 v226, v226, s62, v95
	v_med3_f32 v227, v227, s62, v95
	v_med3_f32 v228, v228, s62, v95
	v_med3_f32 v229, v229, s62, v95
	v_med3_f32 v230, v230, s62, v95
	v_med3_f32 v231, v231, s62, v95
	v_med3_f32 v232, v232, s62, v95
	v_med3_f32 v233, v233, s62, v95
	v_med3_f32 v234, v234, s62, v95
	v_med3_f32 v235, v235, s62, v95
	v_med3_f32 v236, v236, s62, v95
	v_med3_f32 v237, v237, s62, v95
	v_med3_f32 v238, v238, s62, v95
	v_med3_f32 v239, v239, s62, v95
	v_med3_f32 v240, v240, s62, v95
	v_med3_f32 v241, v241, s62, v95
	v_mov_b32_e32 v242, 0
	v_mov_b32_e32 v243, 0
	v_mov_b32_e32 v244, 0
	v_mov_b32_e32 v245, 0
	v_cvt_pk_fp8_f32 v242, v226, v227
	v_cvt_pk_fp8_f32 v243, v230, v231
	v_cvt_pk_fp8_f32 v244, v234, v235
	v_cvt_pk_fp8_f32 v245, v238, v239
	v_cvt_pk_fp8_f32 v242, v228, v229 op_sel:[0,0,1]
	v_cvt_pk_fp8_f32 v243, v232, v233 op_sel:[0,0,1]
	v_cvt_pk_fp8_f32 v244, v236, v237 op_sel:[0,0,1]
	v_cvt_pk_fp8_f32 v245, v240, v241 op_sel:[0,0,1]
	s_nop 0
	global_store_dwordx4 v77, v[242:245], s[6:7]
	ds_read_b32 v226, v213
	ds_read_b32 v227, v213 offset:512
	ds_read_b32 v228, v213 offset:1024
	ds_read_b32 v229, v213 offset:1536
	ds_read_b32 v230, v213 offset:2048
	ds_read_b32 v231, v213 offset:2560
	ds_read_b32 v232, v213 offset:3072
	ds_read_b32 v233, v213 offset:3584
	ds_read_b32 v234, v213 offset:4096
	ds_read_b32 v235, v213 offset:4608
	ds_read_b32 v236, v213 offset:5120
	ds_read_b32 v237, v213 offset:5632
	ds_read_b32 v238, v213 offset:6144
	ds_read_b32 v239, v213 offset:6656
	ds_read_b32 v240, v213 offset:7168
	ds_read_b32 v241, v213 offset:7680
	s_waitcnt lgkmcnt(0)
	v_max_f32_e32 v226, v226, v226
	v_max_f32_e32 v227, v227, v227
	v_max_f32_e32 v228, v228, v228
	v_max_f32_e32 v229, v229, v229
	v_max_f32_e32 v230, v230, v230
	v_max_f32_e32 v231, v231, v231
	v_max_f32_e32 v232, v232, v232
	v_max_f32_e32 v233, v233, v233
	v_max_f32_e32 v234, v234, v234
	v_max_f32_e32 v235, v235, v235
	v_max_f32_e32 v236, v236, v236
	v_max_f32_e32 v237, v237, v237
	v_max_f32_e32 v238, v238, v238
	v_max_f32_e32 v239, v239, v239
	v_max_f32_e32 v240, v240, v240
	v_max_f32_e32 v241, v241, v241
	v_med3_f32 v226, v226, s62, v95
	v_med3_f32 v227, v227, s62, v95
	v_med3_f32 v228, v228, s62, v95
	v_med3_f32 v229, v229, s62, v95
	v_med3_f32 v230, v230, s62, v95
	v_med3_f32 v231, v231, s62, v95
	v_med3_f32 v232, v232, s62, v95
	v_med3_f32 v233, v233, s62, v95
	v_med3_f32 v234, v234, s62, v95
	v_med3_f32 v235, v235, s62, v95
	v_med3_f32 v236, v236, s62, v95
	v_med3_f32 v237, v237, s62, v95
	v_med3_f32 v238, v238, s62, v95
	v_med3_f32 v239, v239, s62, v95
	v_med3_f32 v240, v240, s62, v95
	v_med3_f32 v241, v241, s62, v95
	v_mov_b32_e32 v242, 0
	v_mov_b32_e32 v243, 0
	v_mov_b32_e32 v244, 0
	v_mov_b32_e32 v245, 0
	v_cvt_pk_fp8_f32 v242, v226, v227
	v_cvt_pk_fp8_f32 v243, v230, v231
	v_cvt_pk_fp8_f32 v244, v234, v235
	v_cvt_pk_fp8_f32 v245, v238, v239
	v_cvt_pk_fp8_f32 v242, v228, v229 op_sel:[0,0,1]
	v_cvt_pk_fp8_f32 v243, v232, v233 op_sel:[0,0,1]
	v_cvt_pk_fp8_f32 v244, v236, v237 op_sel:[0,0,1]
	v_cvt_pk_fp8_f32 v245, v240, v241 op_sel:[0,0,1]
	s_nop 0
	global_store_dwordx4 v78, v[242:245], s[6:7]
	s_waitcnt vmcnt(12)
	v_mul_f32_e32 v176, v26, v176
	v_mul_f32_e32 v177, v26, v177
	v_mul_f32_e32 v178, v26, v178
	v_mul_f32_e32 v179, v26, v179
	ds_write_b128 v210, v[176:179]
	v_mul_f32_e32 v180, v27, v180
	v_mul_f32_e32 v181, v27, v181
	v_mul_f32_e32 v182, v27, v182
	v_mul_f32_e32 v183, v27, v183
	ds_write_b128 v210, v[180:183] offset:1024
	v_mul_f32_e32 v184, v28, v184
	v_mul_f32_e32 v185, v28, v185
	v_mul_f32_e32 v186, v28, v186
	v_mul_f32_e32 v187, v28, v187
	ds_write_b128 v210, v[184:187] offset:2048
	v_mul_f32_e32 v188, v29, v188
	v_mul_f32_e32 v189, v29, v189
	v_mul_f32_e32 v190, v29, v190
	v_mul_f32_e32 v191, v29, v191
	ds_write_b128 v210, v[188:191] offset:3072
	v_mul_f32_e32 v192, v30, v192
	v_mul_f32_e32 v193, v30, v193
	v_mul_f32_e32 v194, v30, v194
	v_mul_f32_e32 v195, v30, v195
	ds_write_b128 v210, v[192:195] offset:4096
	v_mul_f32_e32 v196, v31, v196
	v_mul_f32_e32 v197, v31, v197
	v_mul_f32_e32 v198, v31, v198
	v_mul_f32_e32 v199, v31, v199
	ds_write_b128 v210, v[196:199] offset:5120
	v_mul_f32_e32 v200, v32, v200
	v_mul_f32_e32 v201, v32, v201
	v_mul_f32_e32 v202, v32, v202
	v_mul_f32_e32 v203, v32, v203
	ds_write_b128 v210, v[200:203] offset:6144
	v_mul_f32_e32 v204, v33, v204
	v_mul_f32_e32 v205, v33, v205
	v_mul_f32_e32 v206, v33, v206
	v_mul_f32_e32 v207, v33, v207
	ds_write_b128 v210, v[204:207] offset:7168
	s_waitcnt lgkmcnt(0)
	s_barrier
; #define GAS __attribute__((address_space(1)))
; #define LAS __attribute__((address_space(3)))
; #define LDS_WAIT() asm volatile("s_waitcnt lgkmcnt(0)" ::: "memory")
; __device__ __forceinline__ unsigned pk4_fp8(float a, float b, float c, float d) {
;     a = fminf(fmaxf(a, -448.f), 448.f); b = fminf(fmaxf(b, -448.f), 448.f); c = fminf(fmaxf(c, -448.f), 448.f); d = fminf(fmaxf(d, -448.f), 448.f);
;     int w = __builtin_amdgcn_cvt_pk_fp8_f32(a, b, 0, false); w = __builtin_amdgcn_cvt_pk_fp8_f32(c, d, w, true); return (unsigned)w; }
;     const int pr = item >> 1, kb = 2 * (pr / nblk) + (item & 1), nb = pr % nblk, k0 = 64 * kb, n0 = 32 * nb;
;     const int nr = n0 + (lane & 31); const int sc = MAP == 1 ? src_col_in(nr) : nr;
;     float v[32];
; #pragma unroll
;     for (int i = 0; i < 32; ++i) v[i] = sc >= 0 ? W[(size_t)(k0 + 2 * i + (lane >> 5)) * Nsrc + sc] : 0.f;
; #pragma unroll
;     for (int i = 0; i < 32; ++i) { const int k = k0 + 2 * i + (lane >> 5); float x = v[i] * wscale; if (KS) x *= (k < ksplit ? ksA[k] : ksB[k - ksplit]); scr[(2 * i + (lane >> 5)) * 33 + (lane & 31)] = x; }
;     LDS_WAIT(); asm volatile("" ::: "memory");
;     const int c = lane & 7;
; #pragma unroll
;     for (int j = 0; j < 4; ++j) { const int n = (lane >> 3) + 8 * j; const LAS float* s = scr + (8 * c) * 33 + n;
;         const unsigned long long o = (unsigned long long)pg8::pk4_fp8(s[0 * 33], s[1 * 33], s[2 * 33], s[3 * 33]) | ((unsigned long long)pg8::pk4_fp8(s[4 * 33], s[5 * 33], s[6 * 33], s[7 * 33]) << 32);
;         *(GAS unsigned long long*)(WT + (size_t)(n0 + n) * K + k0 + 8 * c) = o; }
;     LDS_WAIT(); asm volatile("" ::: "memory");
; }
	s_add_u32 s8, s30, 0x7000
	s_addc_u32 s9, s31, 0
	global_load_dwordx4 v[176:179], v74, s[8:9]
	s_add_u32 s8, s8, 0x20000
	s_addc_u32 s9, s9, 0
	global_load_dwordx4 v[180:183], v74, s[8:9]
	s_add_u32 s8, s8, 0x20000
	s_addc_u32 s9, s9, 0
	global_load_dwordx4 v[184:187], v74, s[8:9]
	s_add_u32 s8, s8, 0x20000
	s_addc_u32 s9, s9, 0
	global_load_dwordx4 v[188:191], v74, s[8:9]
	s_add_u32 s8, s8, 0x20000
	s_addc_u32 s9, s9, 0
	global_load_dwordx4 v[192:195], v74, s[8:9]
	s_add_u32 s8, s8, 0x20000
	s_addc_u32 s9, s9, 0
	global_load_dwordx4 v[196:199], v74, s[8:9]
	s_add_u32 s8, s8, 0x20000
	s_addc_u32 s9, s9, 0
	global_load_dwordx4 v[200:203], v74, s[8:9]
	s_add_u32 s8, s8, 0x20000
	s_addc_u32 s9, s9, 0
	global_load_dwordx4 v[204:207], v74, s[8:9]
	s_add_u32 s6, s32, 0x1400000
	s_addc_u32 s7, s33, 0
	ds_read_b32 v226, v212
	ds_read_b32 v227, v212 offset:512
	ds_read_b32 v228, v212 offset:1024
	ds_read_b32 v229, v212 offset:1536
	ds_read_b32 v230, v212 offset:2048
	ds_read_b32 v231, v212 offset:2560
	ds_read_b32 v232, v212 offset:3072
	ds_read_b32 v233, v212 offset:3584
	ds_read_b32 v234, v212 offset:4096
	ds_read_b32 v235, v212 offset:4608
	ds_read_b32 v236, v212 offset:5120
	ds_read_b32 v237, v212 offset:5632
	ds_read_b32 v238, v212 offset:6144
	ds_read_b32 v239, v212 offset:6656
	ds_read_b32 v240, v212 offset:7168
	ds_read_b32 v241, v212 offset:7680
	s_waitcnt lgkmcnt(0)
	v_max_f32_e32 v226, v226, v226
	v_max_f32_e32 v227, v227, v227
	v_max_f32_e32 v228, v228, v228
	v_max_f32_e32 v229, v229, v229
	v_max_f32_e32 v230, v230, v230
	v_max_f32_e32 v231, v231, v231
	v_max_f32_e32 v232, v232, v232
	v_max_f32_e32 v233, v233, v233
	v_max_f32_e32 v234, v234, v234
	v_max_f32_e32 v235, v235, v235
	v_max_f32_e32 v236, v236, v236
	v_max_f32_e32 v237, v237, v237
	v_max_f32_e32 v238, v238, v238
	v_max_f32_e32 v239, v239, v239
	v_max_f32_e32 v240, v240, v240
	v_max_f32_e32 v241, v241, v241
	v_med3_f32 v226, v226, s62, v95
	v_med3_f32 v227, v227, s62, v95
	v_med3_f32 v228, v228, s62, v95
	v_med3_f32 v229, v229, s62, v95
	v_med3_f32 v230, v230, s62, v95
	v_med3_f32 v231, v231, s62, v95
	v_med3_f32 v232, v232, s62, v95
	v_med3_f32 v233, v233, s62, v95
	v_med3_f32 v234, v234, s62, v95
	v_med3_f32 v235, v235, s62, v95
	v_med3_f32 v236, v236, s62, v95
	v_med3_f32 v237, v237, s62, v95
	v_med3_f32 v238, v238, s62, v95
	v_med3_f32 v239, v239, s62, v95
	v_med3_f32 v240, v240, s62, v95
	v_med3_f32 v241, v241, s62, v95
	v_mov_b32_e32 v242, 0
	v_mov_b32_e32 v243, 0
	v_mov_b32_e32 v244, 0
	v_mov_b32_e32 v245, 0
	v_cvt_pk_fp8_f32 v242, v226, v227
	v_cvt_pk_fp8_f32 v243, v230, v231
	v_cvt_pk_fp8_f32 v244, v234, v235
	v_cvt_pk_fp8_f32 v245, v238, v239
	v_cvt_pk_fp8_f32 v242, v228, v229 op_sel:[0,0,1]
	v_cvt_pk_fp8_f32 v243, v232, v233 op_sel:[0,0,1]
	v_cvt_pk_fp8_f32 v244, v236, v237 op_sel:[0,0,1]
	v_cvt_pk_fp8_f32 v245, v240, v241 op_sel:[0,0,1]
	s_nop 0
	global_store_dwordx4 v77, v[242:245], s[6:7]
	ds_read_b32 v226, v214
	ds_read_b32 v227, v214 offset:512
	ds_read_b32 v228, v214 offset:1024
	ds_read_b32 v229, v214 offset:1536
	ds_read_b32 v230, v214 offset:2048
	ds_read_b32 v231, v214 offset:2560
	ds_read_b32 v232, v214 offset:3072
	ds_read_b32 v233, v214 offset:3584
	ds_read_b32 v234, v214 offset:4096
	ds_read_b32 v235, v214 offset:4608
	ds_read_b32 v236, v214 offset:5120
	ds_read_b32 v237, v214 offset:5632
	ds_read_b32 v238, v214 offset:6144
	ds_read_b32 v239, v214 offset:6656
	ds_read_b32 v240, v214 offset:7168
	ds_read_b32 v241, v214 offset:7680
	s_waitcnt lgkmcnt(0)
	v_max_f32_e32 v226, v226, v226
	v_max_f32_e32 v227, v227, v227
	v_max_f32_e32 v228, v228, v228
	v_max_f32_e32 v229, v229, v229
	v_max_f32_e32 v230, v230, v230
	v_max_f32_e32 v231, v231, v231
	v_max_f32_e32 v232, v232, v232
	v_max_f32_e32 v233, v233, v233
	v_max_f32_e32 v234, v234, v234
	v_max_f32_e32 v235, v235, v235
	v_max_f32_e32 v236, v236, v236
	v_max_f32_e32 v237, v237, v237
	v_max_f32_e32 v238, v238, v238
	v_max_f32_e32 v239, v239, v239
	v_max_f32_e32 v240, v240, v240
	v_max_f32_e32 v241, v241, v241
	v_med3_f32 v226, v226, s62, v95
	v_med3_f32 v227, v227, s62, v95
	v_med3_f32 v228, v228, s62, v95
	v_med3_f32 v229, v229, s62, v95
	v_med3_f32 v230, v230, s62, v95
	v_med3_f32 v231, v231, s62, v95
	v_med3_f32 v232, v232, s62, v95
	v_med3_f32 v233, v233, s62, v95
	v_med3_f32 v234, v234, s62, v95
	v_med3_f32 v235, v235, s62, v95
	v_med3_f32 v236, v236, s62, v95
	v_med3_f32 v237, v237, s62, v95
	v_med3_f32 v238, v238, s62, v95
	v_med3_f32 v239, v239, s62, v95
	v_med3_f32 v240, v240, s62, v95
	v_med3_f32 v241, v241, s62, v95
	v_mov_b32_e32 v242, 0
	v_mov_b32_e32 v243, 0
	v_mov_b32_e32 v244, 0
	v_mov_b32_e32 v245, 0
	v_cvt_pk_fp8_f32 v242, v226, v227
	v_cvt_pk_fp8_f32 v243, v230, v231
	v_cvt_pk_fp8_f32 v244, v234, v235
	v_cvt_pk_fp8_f32 v245, v238, v239
	v_cvt_pk_fp8_f32 v242, v228, v229 op_sel:[0,0,1]
	v_cvt_pk_fp8_f32 v243, v232, v233 op_sel:[0,0,1]
	v_cvt_pk_fp8_f32 v244, v236, v237 op_sel:[0,0,1]
	v_cvt_pk_fp8_f32 v245, v240, v241 op_sel:[0,0,1]
	s_nop 0
	global_store_dwordx4 v78, v[242:245], s[6:7]
	s_waitcnt vmcnt(12)
	v_mul_f32_e32 v144, v26, v144
	v_mul_f32_e32 v145, v26, v145
	v_mul_f32_e32 v146, v26, v146
	v_mul_f32_e32 v147, v26, v147
	ds_write_b128 v209, v[144:147]
	v_mul_f32_e32 v148, v27, v148
	v_mul_f32_e32 v149, v27, v149
	v_mul_f32_e32 v150, v27, v150
	v_mul_f32_e32 v151, v27, v151
	ds_write_b128 v209, v[148:151] offset:1024
	v_mul_f32_e32 v152, v28, v152
	v_mul_f32_e32 v153, v28, v153
	v_mul_f32_e32 v154, v28, v154
	v_mul_f32_e32 v155, v28, v155
	ds_write_b128 v209, v[152:155] offset:2048
	v_mul_f32_e32 v156, v29, v156
	v_mul_f32_e32 v157, v29, v157
	v_mul_f32_e32 v158, v29, v158
	v_mul_f32_e32 v159, v29, v159
	ds_write_b128 v209, v[156:159] offset:3072
	v_mul_f32_e32 v160, v30, v160
	v_mul_f32_e32 v161, v30, v161
	v_mul_f32_e32 v162, v30, v162
	v_mul_f32_e32 v163, v30, v163
	ds_write_b128 v209, v[160:163] offset:4096
	v_mul_f32_e32 v164, v31, v164
	v_mul_f32_e32 v165, v31, v165
	v_mul_f32_e32 v166, v31, v166
	v_mul_f32_e32 v167, v31, v167
	ds_write_b128 v209, v[164:167] offset:5120
	v_mul_f32_e32 v168, v32, v168
	v_mul_f32_e32 v169, v32, v169
	v_mul_f32_e32 v170, v32, v170
	v_mul_f32_e32 v171, v32, v171
	ds_write_b128 v209, v[168:171] offset:6144
	v_mul_f32_e32 v172, v33, v172
	v_mul_f32_e32 v173, v33, v173
	v_mul_f32_e32 v174, v33, v174
	v_mul_f32_e32 v175, v33, v175
	ds_write_b128 v209, v[172:175] offset:7168
	s_waitcnt lgkmcnt(0)
	s_barrier
; #define GAS __attribute__((address_space(1)))
; #define LAS __attribute__((address_space(3)))
; #define LDS_WAIT() asm volatile("s_waitcnt lgkmcnt(0)" ::: "memory")
; __device__ __forceinline__ unsigned pk4_fp8(float a, float b, float c, float d) {
;     a = fminf(fmaxf(a, -448.f), 448.f); b = fminf(fmaxf(b, -448.f), 448.f); c = fminf(fmaxf(c, -448.f), 448.f); d = fminf(fmaxf(d, -448.f), 448.f);
;     int w = __builtin_amdgcn_cvt_pk_fp8_f32(a, b, 0, false); w = __builtin_amdgcn_cvt_pk_fp8_f32(c, d, w, true); return (unsigned)w; }
;     const int pr = item >> 1, kb = 2 * (pr / nblk) + (item & 1), nb = pr % nblk, k0 = 64 * kb, n0 = 32 * nb;
;     const int nr = n0 + (lane & 31); const int sc = MAP == 1 ? src_col_in(nr) : nr;
;     float v[32];
; #pragma unroll
;     for (int i = 0; i < 32; ++i) v[i] = sc >= 0 ? W[(size_t)(k0 + 2 * i + (lane >> 5)) * Nsrc + sc] : 0.f;
; #pragma unroll
;     for (int i = 0; i < 32; ++i) { const int k = k0 + 2 * i + (lane >> 5); float x = v[i] * wscale; if (KS) x *= (k < ksplit ? ksA[k] : ksB[k - ksplit]); scr[(2 * i + (lane >> 5)) * 33 + (lane & 31)] = x; }
;     LDS_WAIT(); asm volatile("" ::: "memory");
;     const int c = lane & 7;
; #pragma unroll
;     for (int j = 0; j < 4; ++j) { const int n = (lane >> 3) + 8 * j; const LAS float* s = scr + (8 * c) * 33 + n;
;         const unsigned long long o = (unsigned long long)pg8::pk4_fp8(s[0 * 33], s[1 * 33], s[2 * 33], s[3 * 33]) | ((unsigned long long)pg8::pk4_fp8(s[4 * 33], s[5 * 33], s[6 * 33], s[7 * 33]) << 32);
;         *(GAS unsigned long long*)(WT + (size_t)(n0 + n) * K + k0 + 8 * c) = o; }
;     LDS_WAIT(); asm volatile("" ::: "memory");
; }
	s_add_u32 s8, s30, 0x8000
	s_addc_u32 s9, s31, 0
	global_load_dwordx4 v[144:147], v74, s[8:9]
	s_add_u32 s8, s8, 0x20000
	s_addc_u32 s9, s9, 0
	global_load_dwordx4 v[148:151], v74, s[8:9]
	s_add_u32 s8, s8, 0x20000
	s_addc_u32 s9, s9, 0
	global_load_dwordx4 v[152:155], v74, s[8:9]
	s_add_u32 s8, s8, 0x20000
	s_addc_u32 s9, s9, 0
	global_load_dwordx4 v[156:159], v74, s[8:9]
	s_add_u32 s8, s8, 0x20000
	s_addc_u32 s9, s9, 0
	global_load_dwordx4 v[160:163], v74, s[8:9]
	s_add_u32 s8, s8, 0x20000
	s_addc_u32 s9, s9, 0
	global_load_dwordx4 v[164:167], v74, s[8:9]
	s_add_u32 s8, s8, 0x20000
	s_addc_u32 s9, s9, 0
	global_load_dwordx4 v[168:171], v74, s[8:9]
	s_add_u32 s8, s8, 0x20000
	s_addc_u32 s9, s9, 0
	global_load_dwordx4 v[172:175], v74, s[8:9]
	s_add_u32 s6, s32, 0x1800000
	s_addc_u32 s7, s33, 0
	ds_read_b32 v226, v211
	ds_read_b32 v227, v211 offset:512
	ds_read_b32 v228, v211 offset:1024
	ds_read_b32 v229, v211 offset:1536
	ds_read_b32 v230, v211 offset:2048
	ds_read_b32 v231, v211 offset:2560
	ds_read_b32 v232, v211 offset:3072
	ds_read_b32 v233, v211 offset:3584
	ds_read_b32 v234, v211 offset:4096
	ds_read_b32 v235, v211 offset:4608
	ds_read_b32 v236, v211 offset:5120
	ds_read_b32 v237, v211 offset:5632
	ds_read_b32 v238, v211 offset:6144
	ds_read_b32 v239, v211 offset:6656
	ds_read_b32 v240, v211 offset:7168
	ds_read_b32 v241, v211 offset:7680
	s_waitcnt lgkmcnt(0)
	v_max_f32_e32 v226, v226, v226
	v_max_f32_e32 v227, v227, v227
	v_max_f32_e32 v228, v228, v228
	v_max_f32_e32 v229, v229, v229
	v_max_f32_e32 v230, v230, v230
	v_max_f32_e32 v231, v231, v231
	v_max_f32_e32 v232, v232, v232
	v_max_f32_e32 v233, v233, v233
	v_max_f32_e32 v234, v234, v234
	v_max_f32_e32 v235, v235, v235
	v_max_f32_e32 v236, v236, v236
	v_max_f32_e32 v237, v237, v237
	v_max_f32_e32 v238, v238, v238
	v_max_f32_e32 v239, v239, v239
	v_max_f32_e32 v240, v240, v240
	v_max_f32_e32 v241, v241, v241
	v_med3_f32 v226, v226, s62, v95
	v_med3_f32 v227, v227, s62, v95
	v_med3_f32 v228, v228, s62, v95
	v_med3_f32 v229, v229, s62, v95
	v_med3_f32 v230, v230, s62, v95
	v_med3_f32 v231, v231, s62, v95
	v_med3_f32 v232, v232, s62, v95
	v_med3_f32 v233, v233, s62, v95
	v_med3_f32 v234, v234, s62, v95
	v_med3_f32 v235, v235, s62, v95
	v_med3_f32 v236, v236, s62, v95
	v_med3_f32 v237, v237, s62, v95
	v_med3_f32 v238, v238, s62, v95
	v_med3_f32 v239, v239, s62, v95
	v_med3_f32 v240, v240, s62, v95
	v_med3_f32 v241, v241, s62, v95
	v_mov_b32_e32 v242, 0
	v_mov_b32_e32 v243, 0
	v_mov_b32_e32 v244, 0
	v_mov_b32_e32 v245, 0
	v_cvt_pk_fp8_f32 v242, v226, v227
	v_cvt_pk_fp8_f32 v243, v230, v231
	v_cvt_pk_fp8_f32 v244, v234, v235
	v_cvt_pk_fp8_f32 v245, v238, v239
	v_cvt_pk_fp8_f32 v242, v228, v229 op_sel:[0,0,1]
	v_cvt_pk_fp8_f32 v243, v232, v233 op_sel:[0,0,1]
	v_cvt_pk_fp8_f32 v244, v236, v237 op_sel:[0,0,1]
	v_cvt_pk_fp8_f32 v245, v240, v241 op_sel:[0,0,1]
	s_nop 0
	global_store_dwordx4 v77, v[242:245], s[6:7]
	ds_read_b32 v226, v213
	ds_read_b32 v227, v213 offset:512
	ds_read_b32 v228, v213 offset:1024
	ds_read_b32 v229, v213 offset:1536
	ds_read_b32 v230, v213 offset:2048
	ds_read_b32 v231, v213 offset:2560
	ds_read_b32 v232, v213 offset:3072
	ds_read_b32 v233, v213 offset:3584
	ds_read_b32 v234, v213 offset:4096
	ds_read_b32 v235, v213 offset:4608
	ds_read_b32 v236, v213 offset:5120
	ds_read_b32 v237, v213 offset:5632
	ds_read_b32 v238, v213 offset:6144
	ds_read_b32 v239, v213 offset:6656
	ds_read_b32 v240, v213 offset:7168
	ds_read_b32 v241, v213 offset:7680
	s_waitcnt lgkmcnt(0)
	v_max_f32_e32 v226, v226, v226
	v_max_f32_e32 v227, v227, v227
	v_max_f32_e32 v228, v228, v228
	v_max_f32_e32 v229, v229, v229
	v_max_f32_e32 v230, v230, v230
	v_max_f32_e32 v231, v231, v231
	v_max_f32_e32 v232, v232, v232
	v_max_f32_e32 v233, v233, v233
	v_max_f32_e32 v234, v234, v234
	v_max_f32_e32 v235, v235, v235
	v_max_f32_e32 v236, v236, v236
	v_max_f32_e32 v237, v237, v237
	v_max_f32_e32 v238, v238, v238
	v_max_f32_e32 v239, v239, v239
	v_max_f32_e32 v240, v240, v240
	v_max_f32_e32 v241, v241, v241
	v_med3_f32 v226, v226, s62, v95
	v_med3_f32 v227, v227, s62, v95
	v_med3_f32 v228, v228, s62, v95
	v_med3_f32 v229, v229, s62, v95
	v_med3_f32 v230, v230, s62, v95
	v_med3_f32 v231, v231, s62, v95
	v_med3_f32 v232, v232, s62, v95
	v_med3_f32 v233, v233, s62, v95
	v_med3_f32 v234, v234, s62, v95
	v_med3_f32 v235, v235, s62, v95
	v_med3_f32 v236, v236, s62, v95
	v_med3_f32 v237, v237, s62, v95
	v_med3_f32 v238, v238, s62, v95
	v_med3_f32 v239, v239, s62, v95
	v_med3_f32 v240, v240, s62, v95
	v_med3_f32 v241, v241, s62, v95
	v_mov_b32_e32 v242, 0
	v_mov_b32_e32 v243, 0
	v_mov_b32_e32 v244, 0
	v_mov_b32_e32 v245, 0
	v_cvt_pk_fp8_f32 v242, v226, v227
	v_cvt_pk_fp8_f32 v243, v230, v231
	v_cvt_pk_fp8_f32 v244, v234, v235
	v_cvt_pk_fp8_f32 v245, v238, v239
	v_cvt_pk_fp8_f32 v242, v228, v229 op_sel:[0,0,1]
	v_cvt_pk_fp8_f32 v243, v232, v233 op_sel:[0,0,1]
	v_cvt_pk_fp8_f32 v244, v236, v237 op_sel:[0,0,1]
	v_cvt_pk_fp8_f32 v245, v240, v241 op_sel:[0,0,1]
	s_nop 0
	global_store_dwordx4 v78, v[242:245], s[6:7]
	s_waitcnt vmcnt(12)
	v_mul_f32_e32 v176, v26, v176
	v_mul_f32_e32 v177, v26, v177
	v_mul_f32_e32 v178, v26, v178
	v_mul_f32_e32 v179, v26, v179
	ds_write_b128 v210, v[176:179]
	v_mul_f32_e32 v180, v27, v180
	v_mul_f32_e32 v181, v27, v181
	v_mul_f32_e32 v182, v27, v182
	v_mul_f32_e32 v183, v27, v183
	ds_write_b128 v210, v[180:183] offset:1024
	v_mul_f32_e32 v184, v28, v184
	v_mul_f32_e32 v185, v28, v185
	v_mul_f32_e32 v186, v28, v186
	v_mul_f32_e32 v187, v28, v187
	ds_write_b128 v210, v[184:187] offset:2048
	v_mul_f32_e32 v188, v29, v188
	v_mul_f32_e32 v189, v29, v189
	v_mul_f32_e32 v190, v29, v190
	v_mul_f32_e32 v191, v29, v191
	ds_write_b128 v210, v[188:191] offset:3072
	v_mul_f32_e32 v192, v30, v192
	v_mul_f32_e32 v193, v30, v193
	v_mul_f32_e32 v194, v30, v194
	v_mul_f32_e32 v195, v30, v195
	ds_write_b128 v210, v[192:195] offset:4096
	v_mul_f32_e32 v196, v31, v196
	v_mul_f32_e32 v197, v31, v197
	v_mul_f32_e32 v198, v31, v198
	v_mul_f32_e32 v199, v31, v199
	ds_write_b128 v210, v[196:199] offset:5120
	v_mul_f32_e32 v200, v32, v200
	v_mul_f32_e32 v201, v32, v201
	v_mul_f32_e32 v202, v32, v202
	v_mul_f32_e32 v203, v32, v203
	ds_write_b128 v210, v[200:203] offset:6144
	v_mul_f32_e32 v204, v33, v204
	v_mul_f32_e32 v205, v33, v205
	v_mul_f32_e32 v206, v33, v206
	v_mul_f32_e32 v207, v33, v207
	ds_write_b128 v210, v[204:207] offset:7168
	s_waitcnt lgkmcnt(0)
	s_barrier
; #define GAS __attribute__((address_space(1)))
; #define LAS __attribute__((address_space(3)))
; #define LDS_WAIT() asm volatile("s_waitcnt lgkmcnt(0)" ::: "memory")
; __device__ __forceinline__ unsigned pk4_fp8(float a, float b, float c, float d) {
;     a = fminf(fmaxf(a, -448.f), 448.f); b = fminf(fmaxf(b, -448.f), 448.f); c = fminf(fmaxf(c, -448.f), 448.f); d = fminf(fmaxf(d, -448.f), 448.f);
;     int w = __builtin_amdgcn_cvt_pk_fp8_f32(a, b, 0, false); w = __builtin_amdgcn_cvt_pk_fp8_f32(c, d, w, true); return (unsigned)w; }
;     const int pr = item >> 1, kb = 2 * (pr / nblk) + (item & 1), nb = pr % nblk, k0 = 64 * kb, n0 = 32 * nb;
;     const int nr = n0 + (lane & 31); const int sc = MAP == 1 ? src_col_in(nr) : nr;
;     float v[32];
; #pragma unroll
;     for (int i = 0; i < 32; ++i) v[i] = sc >= 0 ? W[(size_t)(k0 + 2 * i + (lane >> 5)) * Nsrc + sc] : 0.f;
; #pragma unroll
;     for (int i = 0; i < 32; ++i) { const int k = k0 + 2 * i + (lane >> 5); float x = v[i] * wscale; if (KS) x *= (k < ksplit ? ksA[k] : ksB[k - ksplit]); scr[(2 * i + (lane >> 5)) * 33 + (lane & 31)] = x; }
;     LDS_WAIT(); asm volatile("" ::: "memory");
;     const int c = lane & 7;
; #pragma unroll
;     for (int j = 0; j < 4; ++j) { const int n = (lane >> 3) + 8 * j; const LAS float* s = scr + (8 * c) * 33 + n;
;         const unsigned long long o = (unsigned long long)pg8::pk4_fp8(s[0 * 33], s[1 * 33], s[2 * 33], s[3 * 33]) | ((unsigned long long)pg8::pk4_fp8(s[4 * 33], s[5 * 33], s[6 * 33], s[7 * 33]) << 32);
;         *(GAS unsigned long long*)(WT + (size_t)(n0 + n) * K + k0 + 8 * c) = o; }
;     LDS_WAIT(); asm volatile("" ::: "memory");
; }
	s_add_u32 s8, s30, 0x9000
	s_addc_u32 s9, s31, 0
	global_load_dwordx4 v[176:179], v74, s[8:9]
	s_add_u32 s8, s8, 0x20000
	s_addc_u32 s9, s9, 0
	global_load_dwordx4 v[180:183], v74, s[8:9]
	s_add_u32 s8, s8, 0x20000
	s_addc_u32 s9, s9, 0
	global_load_dwordx4 v[184:187], v74, s[8:9]
	s_add_u32 s8, s8, 0x20000
	s_addc_u32 s9, s9, 0
	global_load_dwordx4 v[188:191], v74, s[8:9]
	s_add_u32 s8, s8, 0x20000
	s_addc_u32 s9, s9, 0
	global_load_dwordx4 v[192:195], v74, s[8:9]
	s_add_u32 s8, s8, 0x20000
	s_addc_u32 s9, s9, 0
	global_load_dwordx4 v[196:199], v74, s[8:9]
	s_add_u32 s8, s8, 0x20000
	s_addc_u32 s9, s9, 0
	global_load_dwordx4 v[200:203], v74, s[8:9]
	s_add_u32 s8, s8, 0x20000
	s_addc_u32 s9, s9, 0
	global_load_dwordx4 v[204:207], v74, s[8:9]
	s_add_u32 s6, s32, 0x1c00000
	s_addc_u32 s7, s33, 0
	ds_read_b32 v226, v212
	ds_read_b32 v227, v212 offset:512
	ds_read_b32 v228, v212 offset:1024
	ds_read_b32 v229, v212 offset:1536
	ds_read_b32 v230, v212 offset:2048
	ds_read_b32 v231, v212 offset:2560
	ds_read_b32 v232, v212 offset:3072
	ds_read_b32 v233, v212 offset:3584
	ds_read_b32 v234, v212 offset:4096
	ds_read_b32 v235, v212 offset:4608
	ds_read_b32 v236, v212 offset:5120
	ds_read_b32 v237, v212 offset:5632
	ds_read_b32 v238, v212 offset:6144
	ds_read_b32 v239, v212 offset:6656
	ds_read_b32 v240, v212 offset:7168
	ds_read_b32 v241, v212 offset:7680
	s_waitcnt lgkmcnt(0)
	v_max_f32_e32 v226, v226, v226
	v_max_f32_e32 v227, v227, v227
	v_max_f32_e32 v228, v228, v228
	v_max_f32_e32 v229, v229, v229
	v_max_f32_e32 v230, v230, v230
	v_max_f32_e32 v231, v231, v231
	v_max_f32_e32 v232, v232, v232
	v_max_f32_e32 v233, v233, v233
	v_max_f32_e32 v234, v234, v234
	v_max_f32_e32 v235, v235, v235
	v_max_f32_e32 v236, v236, v236
	v_max_f32_e32 v237, v237, v237
	v_max_f32_e32 v238, v238, v238
	v_max_f32_e32 v239, v239, v239
	v_max_f32_e32 v240, v240, v240
	v_max_f32_e32 v241, v241, v241
	v_med3_f32 v226, v226, s62, v95
	v_med3_f32 v227, v227, s62, v95
	v_med3_f32 v228, v228, s62, v95
	v_med3_f32 v229, v229, s62, v95
	v_med3_f32 v230, v230, s62, v95
	v_med3_f32 v231, v231, s62, v95
	v_med3_f32 v232, v232, s62, v95
	v_med3_f32 v233, v233, s62, v95
	v_med3_f32 v234, v234, s62, v95
	v_med3_f32 v235, v235, s62, v95
	v_med3_f32 v236, v236, s62, v95
	v_med3_f32 v237, v237, s62, v95
	v_med3_f32 v238, v238, s62, v95
	v_med3_f32 v239, v239, s62, v95
	v_med3_f32 v240, v240, s62, v95
	v_med3_f32 v241, v241, s62, v95
	v_mov_b32_e32 v242, 0
	v_mov_b32_e32 v243, 0
	v_mov_b32_e32 v244, 0
	v_mov_b32_e32 v245, 0
	v_cvt_pk_fp8_f32 v242, v226, v227
	v_cvt_pk_fp8_f32 v243, v230, v231
	v_cvt_pk_fp8_f32 v244, v234, v235
	v_cvt_pk_fp8_f32 v245, v238, v239
	v_cvt_pk_fp8_f32 v242, v228, v229 op_sel:[0,0,1]
	v_cvt_pk_fp8_f32 v243, v232, v233 op_sel:[0,0,1]
	v_cvt_pk_fp8_f32 v244, v236, v237 op_sel:[0,0,1]
	v_cvt_pk_fp8_f32 v245, v240, v241 op_sel:[0,0,1]
	s_nop 0
	global_store_dwordx4 v77, v[242:245], s[6:7]
	ds_read_b32 v226, v214
	ds_read_b32 v227, v214 offset:512
	ds_read_b32 v228, v214 offset:1024
	ds_read_b32 v229, v214 offset:1536
	ds_read_b32 v230, v214 offset:2048
	ds_read_b32 v231, v214 offset:2560
	ds_read_b32 v232, v214 offset:3072
	ds_read_b32 v233, v214 offset:3584
	ds_read_b32 v234, v214 offset:4096
	ds_read_b32 v235, v214 offset:4608
	ds_read_b32 v236, v214 offset:5120
	ds_read_b32 v237, v214 offset:5632
	ds_read_b32 v238, v214 offset:6144
	ds_read_b32 v239, v214 offset:6656
	ds_read_b32 v240, v214 offset:7168
	ds_read_b32 v241, v214 offset:7680
	s_waitcnt lgkmcnt(0)
	v_max_f32_e32 v226, v226, v226
	v_max_f32_e32 v227, v227, v227
	v_max_f32_e32 v228, v228, v228
	v_max_f32_e32 v229, v229, v229
	v_max_f32_e32 v230, v230, v230
	v_max_f32_e32 v231, v231, v231
	v_max_f32_e32 v232, v232, v232
	v_max_f32_e32 v233, v233, v233
	v_max_f32_e32 v234, v234, v234
	v_max_f32_e32 v235, v235, v235
	v_max_f32_e32 v236, v236, v236
	v_max_f32_e32 v237, v237, v237
	v_max_f32_e32 v238, v238, v238
	v_max_f32_e32 v239, v239, v239
	v_max_f32_e32 v240, v240, v240
	v_max_f32_e32 v241, v241, v241
	v_med3_f32 v226, v226, s62, v95
	v_med3_f32 v227, v227, s62, v95
	v_med3_f32 v228, v228, s62, v95
	v_med3_f32 v229, v229, s62, v95
	v_med3_f32 v230, v230, s62, v95
	v_med3_f32 v231, v231, s62, v95
	v_med3_f32 v232, v232, s62, v95
	v_med3_f32 v233, v233, s62, v95
	v_med3_f32 v234, v234, s62, v95
	v_med3_f32 v235, v235, s62, v95
	v_med3_f32 v236, v236, s62, v95
	v_med3_f32 v237, v237, s62, v95
	v_med3_f32 v238, v238, s62, v95
	v_med3_f32 v239, v239, s62, v95
	v_med3_f32 v240, v240, s62, v95
	v_med3_f32 v241, v241, s62, v95
	v_mov_b32_e32 v242, 0
	v_mov_b32_e32 v243, 0
	v_mov_b32_e32 v244, 0
	v_mov_b32_e32 v245, 0
	v_cvt_pk_fp8_f32 v242, v226, v227
	v_cvt_pk_fp8_f32 v243, v230, v231
	v_cvt_pk_fp8_f32 v244, v234, v235
	v_cvt_pk_fp8_f32 v245, v238, v239
	v_cvt_pk_fp8_f32 v242, v228, v229 op_sel:[0,0,1]
	v_cvt_pk_fp8_f32 v243, v232, v233 op_sel:[0,0,1]
	v_cvt_pk_fp8_f32 v244, v236, v237 op_sel:[0,0,1]
	v_cvt_pk_fp8_f32 v245, v240, v241 op_sel:[0,0,1]
	s_nop 0
	global_store_dwordx4 v78, v[242:245], s[6:7]
	s_waitcnt vmcnt(12)
	v_mul_f32_e32 v144, v26, v144
	v_mul_f32_e32 v145, v26, v145
	v_mul_f32_e32 v146, v26, v146
	v_mul_f32_e32 v147, v26, v147
	ds_write_b128 v209, v[144:147]
	v_mul_f32_e32 v148, v27, v148
	v_mul_f32_e32 v149, v27, v149
	v_mul_f32_e32 v150, v27, v150
	v_mul_f32_e32 v151, v27, v151
	ds_write_b128 v209, v[148:151] offset:1024
	v_mul_f32_e32 v152, v28, v152
	v_mul_f32_e32 v153, v28, v153
	v_mul_f32_e32 v154, v28, v154
	v_mul_f32_e32 v155, v28, v155
	ds_write_b128 v209, v[152:155] offset:2048
	v_mul_f32_e32 v156, v29, v156
	v_mul_f32_e32 v157, v29, v157
	v_mul_f32_e32 v158, v29, v158
	v_mul_f32_e32 v159, v29, v159
	ds_write_b128 v209, v[156:159] offset:3072
	v_mul_f32_e32 v160, v30, v160
	v_mul_f32_e32 v161, v30, v161
	v_mul_f32_e32 v162, v30, v162
	v_mul_f32_e32 v163, v30, v163
	ds_write_b128 v209, v[160:163] offset:4096
	v_mul_f32_e32 v164, v31, v164
	v_mul_f32_e32 v165, v31, v165
	v_mul_f32_e32 v166, v31, v166
	v_mul_f32_e32 v167, v31, v167
	ds_write_b128 v209, v[164:167] offset:5120
	v_mul_f32_e32 v168, v32, v168
	v_mul_f32_e32 v169, v32, v169
	v_mul_f32_e32 v170, v32, v170
	v_mul_f32_e32 v171, v32, v171
	ds_write_b128 v209, v[168:171] offset:6144
	v_mul_f32_e32 v172, v33, v172
	v_mul_f32_e32 v173, v33, v173
	v_mul_f32_e32 v174, v33, v174
	v_mul_f32_e32 v175, v33, v175
	ds_write_b128 v209, v[172:175] offset:7168
	s_waitcnt lgkmcnt(0)
	s_barrier
; #define GAS __attribute__((address_space(1)))
; #define LAS __attribute__((address_space(3)))
; #define LDS_WAIT() asm volatile("s_waitcnt lgkmcnt(0)" ::: "memory")
; __device__ __forceinline__ unsigned pk4_fp8(float a, float b, float c, float d) {
;     a = fminf(fmaxf(a, -448.f), 448.f); b = fminf(fmaxf(b, -448.f), 448.f); c = fminf(fmaxf(c, -448.f), 448.f); d = fminf(fmaxf(d, -448.f), 448.f);
;     int w = __builtin_amdgcn_cvt_pk_fp8_f32(a, b, 0, false); w = __builtin_amdgcn_cvt_pk_fp8_f32(c, d, w, true); return (unsigned)w; }
;     ...
; #pragma unroll
;     for (int i = 0; i < 32; ++i) v[i] = sc >= 0 ? W[(size_t)(k0 + 2 * i + (lane >> 5)) * Nsrc + sc] : 0.f;
; #pragma unroll
;     for (int i = 0; i < 32; ++i) { const int k = k0 + 2 * i + (lane >> 5); float x = v[i] * wscale; if (KS) x *= (k < ksplit ? ksA[k] : ksB[k - ksplit]); scr[(2 * i + (lane >> 5)) * 33 + (lane & 31)] = x; }
;     LDS_WAIT(); asm volatile("" ::: "memory");
;     const int c = lane & 7;
; #pragma unroll
;     for (int j = 0; j < 4; ++j) { const int n = (lane >> 3) + 8 * j; const LAS float* s = scr + (8 * c) * 33 + n;
;         const unsigned long long o = (unsigned long long)pg8::pk4_fp8(s[0 * 33], s[1 * 33], s[2 * 33], s[3 * 33]) | ((unsigned long long)pg8::pk4_fp8(s[4 * 33], s[5 * 33], s[6 * 33], s[7 * 33]) << 32);
;         *(GAS unsigned long long*)(WT + (size_t)(n0 + n) * K + k0 + 8 * c) = o; }
	s_add_u32 s8, s30, 0xa000
	s_addc_u32 s9, s31, 0
	global_load_dwordx4 v[144:147], v74, s[8:9]
	s_add_u32 s8, s8, 0x20000
	s_addc_u32 s9, s9, 0
	global_load_dwordx4 v[148:151], v74, s[8:9]
	s_add_u32 s8, s8, 0x20000
	s_addc_u32 s9, s9, 0
	global_load_dwordx4 v[152:155], v74, s[8:9]
	s_add_u32 s8, s8, 0x20000
	s_addc_u32 s9, s9, 0
	global_load_dwordx4 v[156:159], v74, s[8:9]
	s_add_u32 s8, s8, 0x20000
	s_addc_u32 s9, s9, 0
	global_load_dwordx4 v[160:163], v74, s[8:9]
	s_add_u32 s8, s8, 0x20000
	s_addc_u32 s9, s9, 0
	global_load_dwordx4 v[164:167], v74, s[8:9]
	s_add_u32 s8, s8, 0x20000
	s_addc_u32 s9, s9, 0
	global_load_dwordx4 v[168:171], v74, s[8:9]
	s_add_u32 s8, s8, 0x20000
	s_addc_u32 s9, s9, 0
	global_load_dwordx4 v[172:175], v74, s[8:9]
	s_add_u32 s6, s32, 0x2000000
	s_addc_u32 s7, s33, 0
	ds_read_b32 v226, v211
	ds_read_b32 v227, v211 offset:512
	ds_read_b32 v228, v211 offset:1024
	ds_read_b32 v229, v211 offset:1536
	ds_read_b32 v230, v211 offset:2048
	ds_read_b32 v231, v211 offset:2560
	ds_read_b32 v232, v211 offset:3072
	ds_read_b32 v233, v211 offset:3584
	ds_read_b32 v234, v211 offset:4096
	ds_read_b32 v235, v211 offset:4608
	ds_read_b32 v236, v211 offset:5120
	ds_read_b32 v237, v211 offset:5632
	ds_read_b32 v238, v211 offset:6144
	ds_read_b32 v239, v211 offset:6656
	ds_read_b32 v240, v211 offset:7168
	ds_read_b32 v241, v211 offset:7680
	s_waitcnt lgkmcnt(0)
	v_max_f32_e32 v226, v226, v226
	v_max_f32_e32 v227, v227, v227
	v_max_f32_e32 v228, v228, v228
	v_max_f32_e32 v229, v229, v229
	v_max_f32_e32 v230, v230, v230
	v_max_f32_e32 v231, v231, v231
	v_max_f32_e32 v232, v232, v232
	v_max_f32_e32 v233, v233, v233
	v_max_f32_e32 v234, v234, v234
	v_max_f32_e32 v235, v235, v235
	v_max_f32_e32 v236, v236, v236
	v_max_f32_e32 v237, v237, v237
	v_max_f32_e32 v238, v238, v238
	v_max_f32_e32 v239, v239, v239
	v_max_f32_e32 v240, v240, v240
	v_max_f32_e32 v241, v241, v241
	v_med3_f32 v226, v226, s62, v95
	v_med3_f32 v227, v227, s62, v95
	v_med3_f32 v228, v228, s62, v95
	v_med3_f32 v229, v229, s62, v95
	v_med3_f32 v230, v230, s62, v95
	v_med3_f32 v231, v231, s62, v95
	v_med3_f32 v232, v232, s62, v95
	v_med3_f32 v233, v233, s62, v95
	v_med3_f32 v234, v234, s62, v95
	v_med3_f32 v235, v235, s62, v95
	v_med3_f32 v236, v236, s62, v95
	v_med3_f32 v237, v237, s62, v95
	v_med3_f32 v238, v238, s62, v95
	v_med3_f32 v239, v239, s62, v95
	v_med3_f32 v240, v240, s62, v95
	v_med3_f32 v241, v241, s62, v95
	v_mov_b32_e32 v242, 0
	v_mov_b32_e32 v243, 0
	v_mov_b32_e32 v244, 0
	v_mov_b32_e32 v245, 0
	v_cvt_pk_fp8_f32 v242, v226, v227
	v_cvt_pk_fp8_f32 v243, v230, v231
	v_cvt_pk_fp8_f32 v244, v234, v235
	v_cvt_pk_fp8_f32 v245, v238, v239
	v_cvt_pk_fp8_f32 v242, v228, v229 op_sel:[0,0,1]
	v_cvt_pk_fp8_f32 v243, v232, v233 op_sel:[0,0,1]
	v_cvt_pk_fp8_f32 v244, v236, v237 op_sel:[0,0,1]
	v_cvt_pk_fp8_f32 v245, v240, v241 op_sel:[0,0,1]
	s_nop 0
	global_store_dwordx4 v77, v[242:245], s[6:7]
	ds_read_b32 v226, v213
	ds_read_b32 v227, v213 offset:512
	ds_read_b32 v228, v213 offset:1024
	ds_read_b32 v229, v213 offset:1536
	ds_read_b32 v230, v213 offset:2048
	ds_read_b32 v231, v213 offset:2560
	ds_read_b32 v232, v213 offset:3072
	ds_read_b32 v233, v213 offset:3584
	ds_read_b32 v234, v213 offset:4096
	ds_read_b32 v235, v213 offset:4608
	ds_read_b32 v236, v213 offset:5120
	ds_read_b32 v237, v213 offset:5632
	ds_read_b32 v238, v213 offset:6144
	ds_read_b32 v239, v213 offset:6656
	ds_read_b32 v240, v213 offset:7168
	ds_read_b32 v241, v213 offset:7680
	s_waitcnt lgkmcnt(0)
	v_max_f32_e32 v226, v226, v226
	v_max_f32_e32 v227, v227, v227
	v_max_f32_e32 v228, v228, v228
	v_max_f32_e32 v229, v229, v229
	v_max_f32_e32 v230, v230, v230
	v_max_f32_e32 v231, v231, v231
	v_max_f32_e32 v232, v232, v232
	v_max_f32_e32 v233, v233, v233
	v_max_f32_e32 v234, v234, v234
	v_max_f32_e32 v235, v235, v235
	v_max_f32_e32 v236, v236, v236
	v_max_f32_e32 v237, v237, v237
	v_max_f32_e32 v238, v238, v238
	v_max_f32_e32 v239, v239, v239
	v_max_f32_e32 v240, v240, v240
	v_max_f32_e32 v241, v241, v241
	v_med3_f32 v226, v226, s62, v95
	v_med3_f32 v227, v227, s62, v95
	v_med3_f32 v228, v228, s62, v95
	v_med3_f32 v229, v229, s62, v95
	v_med3_f32 v230, v230, s62, v95
	v_med3_f32 v231, v231, s62, v95
	v_med3_f32 v232, v232, s62, v95
	v_med3_f32 v233, v233, s62, v95
	v_med3_f32 v234, v234, s62, v95
	v_med3_f32 v235, v235, s62, v95
	v_med3_f32 v236, v236, s62, v95
	v_med3_f32 v237, v237, s62, v95
	v_med3_f32 v238, v238, s62, v95
	v_med3_f32 v239, v239, s62, v95
	v_med3_f32 v240, v240, s62, v95
	v_med3_f32 v241, v241, s62, v95
	v_mov_b32_e32 v242, 0
	v_mov_b32_e32 v243, 0
	v_mov_b32_e32 v244, 0
	v_mov_b32_e32 v245, 0
	v_cvt_pk_fp8_f32 v242, v226, v227
	v_cvt_pk_fp8_f32 v243, v230, v231
	v_cvt_pk_fp8_f32 v244, v234, v235
	v_cvt_pk_fp8_f32 v245, v238, v239
	v_cvt_pk_fp8_f32 v242, v228, v229 op_sel:[0,0,1]
	v_cvt_pk_fp8_f32 v243, v232, v233 op_sel:[0,0,1]
	v_cvt_pk_fp8_f32 v244, v236, v237 op_sel:[0,0,1]
	v_cvt_pk_fp8_f32 v245, v240, v241 op_sel:[0,0,1]
	s_nop 0
	global_store_dwordx4 v78, v[242:245], s[6:7]
	s_waitcnt vmcnt(12)
	v_mul_f32_e32 v176, v26, v176
	v_mul_f32_e32 v177, v26, v177
	v_mul_f32_e32 v178, v26, v178
	v_mul_f32_e32 v179, v26, v179
	ds_write_b128 v210, v[176:179]
	v_mul_f32_e32 v180, v27, v180
	v_mul_f32_e32 v181, v27, v181
	v_mul_f32_e32 v182, v27, v182
	v_mul_f32_e32 v183, v27, v183
	ds_write_b128 v210, v[180:183] offset:1024
	v_mul_f32_e32 v184, v28, v184
	v_mul_f32_e32 v185, v28, v185
	v_mul_f32_e32 v186, v28, v186
	v_mul_f32_e32 v187, v28, v187
	ds_write_b128 v210, v[184:187] offset:2048
	v_mul_f32_e32 v188, v29, v188
	v_mul_f32_e32 v189, v29, v189
	v_mul_f32_e32 v190, v29, v190
	v_mul_f32_e32 v191, v29, v191
	ds_write_b128 v210, v[188:191] offset:3072
	v_mul_f32_e32 v192, v30, v192
	v_mul_f32_e32 v193, v30, v193
	v_mul_f32_e32 v194, v30, v194
	v_mul_f32_e32 v195, v30, v195
	ds_write_b128 v210, v[192:195] offset:4096
	v_mul_f32_e32 v196, v31, v196
	v_mul_f32_e32 v197, v31, v197
	v_mul_f32_e32 v198, v31, v198
	v_mul_f32_e32 v199, v31, v199
	ds_write_b128 v210, v[196:199] offset:5120
	v_mul_f32_e32 v200, v32, v200
	v_mul_f32_e32 v201, v32, v201
	v_mul_f32_e32 v202, v32, v202
	v_mul_f32_e32 v203, v32, v203
	ds_write_b128 v210, v[200:203] offset:6144
	v_mul_f32_e32 v204, v33, v204
	v_mul_f32_e32 v205, v33, v205
	v_mul_f32_e32 v206, v33, v206
	v_mul_f32_e32 v207, v33, v207
	ds_write_b128 v210, v[204:207] offset:7168
	s_waitcnt lgkmcnt(0)
	s_barrier
; #define GAS __attribute__((address_space(1)))
; #define LAS __attribute__((address_space(3)))
; #define LDS_WAIT() asm volatile("s_waitcnt lgkmcnt(0)" ::: "memory")
; __device__ __forceinline__ unsigned pk4_fp8(float a, float b, float c, float d) {
;     a = fminf(fmaxf(a, -448.f), 448.f); b = fminf(fmaxf(b, -448.f), 448.f); c = fminf(fmaxf(c, -448.f), 448.f); d = fminf(fmaxf(d, -448.f), 448.f);
;     int w = __builtin_amdgcn_cvt_pk_fp8_f32(a, b, 0, false); w = __builtin_amdgcn_cvt_pk_fp8_f32(c, d, w, true); return (unsigned)w; }
;     ...
; #pragma unroll
;     for (int i = 0; i < 32; ++i) v[i] = sc >= 0 ? W[(size_t)(k0 + 2 * i + (lane >> 5)) * Nsrc + sc] : 0.f;
; #pragma unroll
;     for (int i = 0; i < 32; ++i) { const int k = k0 + 2 * i + (lane >> 5); float x = v[i] * wscale; if (KS) x *= (k < ksplit ? ksA[k] : ksB[k - ksplit]); scr[(2 * i + (lane >> 5)) * 33 + (lane & 31)] = x; }
;     LDS_WAIT(); asm volatile("" ::: "memory");
;     const int c = lane & 7;
; #pragma unroll
;     for (int j = 0; j < 4; ++j) { const int n = (lane >> 3) + 8 * j; const LAS float* s = scr + (8 * c) * 33 + n;
;         const unsigned long long o = (unsigned long long)pg8::pk4_fp8(s[0 * 33], s[1 * 33], s[2 * 33], s[3 * 33]) | ((unsigned long long)pg8::pk4_fp8(s[4 * 33], s[5 * 33], s[6 * 33], s[7 * 33]) << 32);
;         *(GAS unsigned long long*)(WT + (size_t)(n0 + n) * K + k0 + 8 * c) = o; }
	s_add_u32 s8, s30, 0xb000
	s_addc_u32 s9, s31, 0
	global_load_dwordx4 v[176:179], v74, s[8:9]
	s_add_u32 s8, s8, 0x20000
	s_addc_u32 s9, s9, 0
	global_load_dwordx4 v[180:183], v74, s[8:9]
	s_add_u32 s8, s8, 0x20000
	s_addc_u32 s9, s9, 0
	global_load_dwordx4 v[184:187], v74, s[8:9]
	s_add_u32 s8, s8, 0x20000
	s_addc_u32 s9, s9, 0
	global_load_dwordx4 v[188:191], v74, s[8:9]
	s_add_u32 s8, s8, 0x20000
	s_addc_u32 s9, s9, 0
	global_load_dwordx4 v[192:195], v74, s[8:9]
	s_add_u32 s8, s8, 0x20000
	s_addc_u32 s9, s9, 0
	global_load_dwordx4 v[196:199], v74, s[8:9]
	s_add_u32 s8, s8, 0x20000
	s_addc_u32 s9, s9, 0
	global_load_dwordx4 v[200:203], v74, s[8:9]
	s_add_u32 s8, s8, 0x20000
	s_addc_u32 s9, s9, 0
	global_load_dwordx4 v[204:207], v74, s[8:9]
	s_add_u32 s6, s32, 0x2400000
	s_addc_u32 s7, s33, 0
	ds_read_b32 v226, v212
	ds_read_b32 v227, v212 offset:512
	ds_read_b32 v228, v212 offset:1024
	ds_read_b32 v229, v212 offset:1536
	ds_read_b32 v230, v212 offset:2048
	ds_read_b32 v231, v212 offset:2560
	ds_read_b32 v232, v212 offset:3072
	ds_read_b32 v233, v212 offset:3584
	ds_read_b32 v234, v212 offset:4096
	ds_read_b32 v235, v212 offset:4608
	ds_read_b32 v236, v212 offset:5120
	ds_read_b32 v237, v212 offset:5632
	ds_read_b32 v238, v212 offset:6144
	ds_read_b32 v239, v212 offset:6656
	ds_read_b32 v240, v212 offset:7168
	ds_read_b32 v241, v212 offset:7680
	s_waitcnt lgkmcnt(0)
	v_max_f32_e32 v226, v226, v226
	v_max_f32_e32 v227, v227, v227
	v_max_f32_e32 v228, v228, v228
	v_max_f32_e32 v229, v229, v229
	v_max_f32_e32 v230, v230, v230
	v_max_f32_e32 v231, v231, v231
	v_max_f32_e32 v232, v232, v232
	v_max_f32_e32 v233, v233, v233
	v_max_f32_e32 v234, v234, v234
	v_max_f32_e32 v235, v235, v235
	v_max_f32_e32 v236, v236, v236
	v_max_f32_e32 v237, v237, v237
	v_max_f32_e32 v238, v238, v238
	v_max_f32_e32 v239, v239, v239
	v_max_f32_e32 v240, v240, v240
	v_max_f32_e32 v241, v241, v241
	v_med3_f32 v226, v226, s62, v95
	v_med3_f32 v227, v227, s62, v95
	v_med3_f32 v228, v228, s62, v95
	v_med3_f32 v229, v229, s62, v95
	v_med3_f32 v230, v230, s62, v95
	v_med3_f32 v231, v231, s62, v95
	v_med3_f32 v232, v232, s62, v95
	v_med3_f32 v233, v233, s62, v95
	v_med3_f32 v234, v234, s62, v95
	v_med3_f32 v235, v235, s62, v95
	v_med3_f32 v236, v236, s62, v95
	v_med3_f32 v237, v237, s62, v95
	v_med3_f32 v238, v238, s62, v95
	v_med3_f32 v239, v239, s62, v95
	v_med3_f32 v240, v240, s62, v95
	v_med3_f32 v241, v241, s62, v95
	v_mov_b32_e32 v242, 0
	v_mov_b32_e32 v243, 0
	v_mov_b32_e32 v244, 0
	v_mov_b32_e32 v245, 0
	v_cvt_pk_fp8_f32 v242, v226, v227
	v_cvt_pk_fp8_f32 v243, v230, v231
	v_cvt_pk_fp8_f32 v244, v234, v235
	v_cvt_pk_fp8_f32 v245, v238, v239
	v_cvt_pk_fp8_f32 v242, v228, v229 op_sel:[0,0,1]
	v_cvt_pk_fp8_f32 v243, v232, v233 op_sel:[0,0,1]
	v_cvt_pk_fp8_f32 v244, v236, v237 op_sel:[0,0,1]
	v_cvt_pk_fp8_f32 v245, v240, v241 op_sel:[0,0,1]
	s_nop 0
	global_store_dwordx4 v77, v[242:245], s[6:7]
	ds_read_b32 v226, v214
	ds_read_b32 v227, v214 offset:512
	ds_read_b32 v228, v214 offset:1024
	ds_read_b32 v229, v214 offset:1536
	ds_read_b32 v230, v214 offset:2048
	ds_read_b32 v231, v214 offset:2560
	ds_read_b32 v232, v214 offset:3072
	ds_read_b32 v233, v214 offset:3584
	ds_read_b32 v234, v214 offset:4096
	ds_read_b32 v235, v214 offset:4608
	ds_read_b32 v236, v214 offset:5120
	ds_read_b32 v237, v214 offset:5632
	ds_read_b32 v238, v214 offset:6144
	ds_read_b32 v239, v214 offset:6656
	ds_read_b32 v240, v214 offset:7168
	ds_read_b32 v241, v214 offset:7680
	s_waitcnt lgkmcnt(0)
	v_max_f32_e32 v226, v226, v226
	v_max_f32_e32 v227, v227, v227
	v_max_f32_e32 v228, v228, v228
	v_max_f32_e32 v229, v229, v229
	v_max_f32_e32 v230, v230, v230
	v_max_f32_e32 v231, v231, v231
	v_max_f32_e32 v232, v232, v232
	v_max_f32_e32 v233, v233, v233
	v_max_f32_e32 v234, v234, v234
	v_max_f32_e32 v235, v235, v235
	v_max_f32_e32 v236, v236, v236
	v_max_f32_e32 v237, v237, v237
	v_max_f32_e32 v238, v238, v238
	v_max_f32_e32 v239, v239, v239
	v_max_f32_e32 v240, v240, v240
	v_max_f32_e32 v241, v241, v241
	v_med3_f32 v226, v226, s62, v95
	v_med3_f32 v227, v227, s62, v95
	v_med3_f32 v228, v228, s62, v95
	v_med3_f32 v229, v229, s62, v95
	v_med3_f32 v230, v230, s62, v95
	v_med3_f32 v231, v231, s62, v95
	v_med3_f32 v232, v232, s62, v95
	v_med3_f32 v233, v233, s62, v95
	v_med3_f32 v234, v234, s62, v95
	v_med3_f32 v235, v235, s62, v95
	v_med3_f32 v236, v236, s62, v95
	v_med3_f32 v237, v237, s62, v95
	v_med3_f32 v238, v238, s62, v95
	v_med3_f32 v239, v239, s62, v95
	v_med3_f32 v240, v240, s62, v95
	v_med3_f32 v241, v241, s62, v95
	v_mov_b32_e32 v242, 0
	v_mov_b32_e32 v243, 0
	v_mov_b32_e32 v244, 0
	v_mov_b32_e32 v245, 0
	v_cvt_pk_fp8_f32 v242, v226, v227
	v_cvt_pk_fp8_f32 v243, v230, v231
	v_cvt_pk_fp8_f32 v244, v234, v235
	v_cvt_pk_fp8_f32 v245, v238, v239
	v_cvt_pk_fp8_f32 v242, v228, v229 op_sel:[0,0,1]
	v_cvt_pk_fp8_f32 v243, v232, v233 op_sel:[0,0,1]
	v_cvt_pk_fp8_f32 v244, v236, v237 op_sel:[0,0,1]
	v_cvt_pk_fp8_f32 v245, v240, v241 op_sel:[0,0,1]
	s_nop 0
	global_store_dwordx4 v78, v[242:245], s[6:7]
	s_waitcnt vmcnt(12)
	v_mul_f32_e32 v144, v26, v144
	v_mul_f32_e32 v145, v26, v145
	v_mul_f32_e32 v146, v26, v146
	v_mul_f32_e32 v147, v26, v147
	ds_write_b128 v209, v[144:147]
	v_mul_f32_e32 v148, v27, v148
	v_mul_f32_e32 v149, v27, v149
	v_mul_f32_e32 v150, v27, v150
	v_mul_f32_e32 v151, v27, v151
	ds_write_b128 v209, v[148:151] offset:1024
	v_mul_f32_e32 v152, v28, v152
	v_mul_f32_e32 v153, v28, v153
	v_mul_f32_e32 v154, v28, v154
	v_mul_f32_e32 v155, v28, v155
	ds_write_b128 v209, v[152:155] offset:2048
	v_mul_f32_e32 v156, v29, v156
	v_mul_f32_e32 v157, v29, v157
	v_mul_f32_e32 v158, v29, v158
	v_mul_f32_e32 v159, v29, v159
	ds_write_b128 v209, v[156:159] offset:3072
	v_mul_f32_e32 v160, v30, v160
	v_mul_f32_e32 v161, v30, v161
	v_mul_f32_e32 v162, v30, v162
	v_mul_f32_e32 v163, v30, v163
	ds_write_b128 v209, v[160:163] offset:4096
	v_mul_f32_e32 v164, v31, v164
	v_mul_f32_e32 v165, v31, v165
	v_mul_f32_e32 v166, v31, v166
	v_mul_f32_e32 v167, v31, v167
	ds_write_b128 v209, v[164:167] offset:5120
	v_mul_f32_e32 v168, v32, v168
	v_mul_f32_e32 v169, v32, v169
	v_mul_f32_e32 v170, v32, v170
	v_mul_f32_e32 v171, v32, v171
	ds_write_b128 v209, v[168:171] offset:6144
	v_mul_f32_e32 v172, v33, v172
	v_mul_f32_e32 v173, v33, v173
	v_mul_f32_e32 v174, v33, v174
	v_mul_f32_e32 v175, v33, v175
	ds_write_b128 v209, v[172:175] offset:7168
	s_waitcnt lgkmcnt(0)
	s_barrier
; #define GAS __attribute__((address_space(1)))
; #define LAS __attribute__((address_space(3)))
; #define LDS_WAIT() asm volatile("s_waitcnt lgkmcnt(0)" ::: "memory")
; __device__ __forceinline__ unsigned pk4_fp8(float a, float b, float c, float d) {
;     a = fminf(fmaxf(a, -448.f), 448.f); b = fminf(fmaxf(b, -448.f), 448.f); c = fminf(fmaxf(c, -448.f), 448.f); d = fminf(fmaxf(d, -448.f), 448.f);
;     int w = __builtin_amdgcn_cvt_pk_fp8_f32(a, b, 0, false); w = __builtin_amdgcn_cvt_pk_fp8_f32(c, d, w, true); return (unsigned)w; }
;     ...
; #pragma unroll
;     for (int i = 0; i < 32; ++i) v[i] = sc >= 0 ? W[(size_t)(k0 + 2 * i + (lane >> 5)) * Nsrc + sc] : 0.f;
; #pragma unroll
;     for (int i = 0; i < 32; ++i) { const int k = k0 + 2 * i + (lane >> 5); float x = v[i] * wscale; if (KS) x *= (k < ksplit ? ksA[k] : ksB[k - ksplit]); scr[(2 * i + (lane >> 5)) * 33 + (lane & 31)] = x; }
;     LDS_WAIT(); asm volatile("" ::: "memory");
;     const int c = lane & 7;
; #pragma unroll
;     for (int j = 0; j < 4; ++j) { const int n = (lane >> 3) + 8 * j; const LAS float* s = scr + (8 * c) * 33 + n;
;         const unsigned long long o = (unsigned long long)pg8::pk4_fp8(s[0 * 33], s[1 * 33], s[2 * 33], s[3 * 33]) | ((unsigned long long)pg8::pk4_fp8(s[4 * 33], s[5 * 33], s[6 * 33], s[7 * 33]) << 32);
;         *(GAS unsigned long long*)(WT + (size_t)(n0 + n) * K + k0 + 8 * c) = o; }
	s_add_u32 s8, s30, 0xc000
	s_addc_u32 s9, s31, 0
	global_load_dwordx4 v[144:147], v74, s[8:9]
	s_add_u32 s8, s8, 0x20000
	s_addc_u32 s9, s9, 0
	global_load_dwordx4 v[148:151], v74, s[8:9]
	s_add_u32 s8, s8, 0x20000
	s_addc_u32 s9, s9, 0
	global_load_dwordx4 v[152:155], v74, s[8:9]
	s_add_u32 s8, s8, 0x20000
	s_addc_u32 s9, s9, 0
	global_load_dwordx4 v[156:159], v74, s[8:9]
	s_add_u32 s8, s8, 0x20000
	s_addc_u32 s9, s9, 0
	global_load_dwordx4 v[160:163], v74, s[8:9]
	s_add_u32 s8, s8, 0x20000
	s_addc_u32 s9, s9, 0
	global_load_dwordx4 v[164:167], v74, s[8:9]
	s_add_u32 s8, s8, 0x20000
	s_addc_u32 s9, s9, 0
	global_load_dwordx4 v[168:171], v74, s[8:9]
	s_add_u32 s8, s8, 0x20000
	s_addc_u32 s9, s9, 0
	global_load_dwordx4 v[172:175], v74, s[8:9]
	s_add_u32 s6, s32, 0x2800000
	s_addc_u32 s7, s33, 0
	ds_read_b32 v226, v211
	ds_read_b32 v227, v211 offset:512
	ds_read_b32 v228, v211 offset:1024
	ds_read_b32 v229, v211 offset:1536
	ds_read_b32 v230, v211 offset:2048
	ds_read_b32 v231, v211 offset:2560
	ds_read_b32 v232, v211 offset:3072
	ds_read_b32 v233, v211 offset:3584
	ds_read_b32 v234, v211 offset:4096
	ds_read_b32 v235, v211 offset:4608
	ds_read_b32 v236, v211 offset:5120
	ds_read_b32 v237, v211 offset:5632
	ds_read_b32 v238, v211 offset:6144
	ds_read_b32 v239, v211 offset:6656
	ds_read_b32 v240, v211 offset:7168
	ds_read_b32 v241, v211 offset:7680
	s_waitcnt lgkmcnt(0)
	v_max_f32_e32 v226, v226, v226
	v_max_f32_e32 v227, v227, v227
	v_max_f32_e32 v228, v228, v228
	v_max_f32_e32 v229, v229, v229
	v_max_f32_e32 v230, v230, v230
	v_max_f32_e32 v231, v231, v231
	v_max_f32_e32 v232, v232, v232
	v_max_f32_e32 v233, v233, v233
	v_max_f32_e32 v234, v234, v234
	v_max_f32_e32 v235, v235, v235
	v_max_f32_e32 v236, v236, v236
	v_max_f32_e32 v237, v237, v237
	v_max_f32_e32 v238, v238, v238
	v_max_f32_e32 v239, v239, v239
	v_max_f32_e32 v240, v240, v240
	v_max_f32_e32 v241, v241, v241
	v_med3_f32 v226, v226, s62, v95
	v_med3_f32 v227, v227, s62, v95
	v_med3_f32 v228, v228, s62, v95
	v_med3_f32 v229, v229, s62, v95
	v_med3_f32 v230, v230, s62, v95
	v_med3_f32 v231, v231, s62, v95
	v_med3_f32 v232, v232, s62, v95
	v_med3_f32 v233, v233, s62, v95
	v_med3_f32 v234, v234, s62, v95
	v_med3_f32 v235, v235, s62, v95
	v_med3_f32 v236, v236, s62, v95
	v_med3_f32 v237, v237, s62, v95
	v_med3_f32 v238, v238, s62, v95
	v_med3_f32 v239, v239, s62, v95
	v_med3_f32 v240, v240, s62, v95
	v_med3_f32 v241, v241, s62, v95
	v_mov_b32_e32 v242, 0
	v_mov_b32_e32 v243, 0
	v_mov_b32_e32 v244, 0
	v_mov_b32_e32 v245, 0
	v_cvt_pk_fp8_f32 v242, v226, v227
	v_cvt_pk_fp8_f32 v243, v230, v231
	v_cvt_pk_fp8_f32 v244, v234, v235
	v_cvt_pk_fp8_f32 v245, v238, v239
	v_cvt_pk_fp8_f32 v242, v228, v229 op_sel:[0,0,1]
	v_cvt_pk_fp8_f32 v243, v232, v233 op_sel:[0,0,1]
	v_cvt_pk_fp8_f32 v244, v236, v237 op_sel:[0,0,1]
	v_cvt_pk_fp8_f32 v245, v240, v241 op_sel:[0,0,1]
	s_nop 0
	global_store_dwordx4 v77, v[242:245], s[6:7]
	ds_read_b32 v226, v213
	ds_read_b32 v227, v213 offset:512
	ds_read_b32 v228, v213 offset:1024
	ds_read_b32 v229, v213 offset:1536
	ds_read_b32 v230, v213 offset:2048
	ds_read_b32 v231, v213 offset:2560
	ds_read_b32 v232, v213 offset:3072
	ds_read_b32 v233, v213 offset:3584
	ds_read_b32 v234, v213 offset:4096
	ds_read_b32 v235, v213 offset:4608
	ds_read_b32 v236, v213 offset:5120
	ds_read_b32 v237, v213 offset:5632
	ds_read_b32 v238, v213 offset:6144
	ds_read_b32 v239, v213 offset:6656
	ds_read_b32 v240, v213 offset:7168
	ds_read_b32 v241, v213 offset:7680
	s_waitcnt lgkmcnt(0)
	v_max_f32_e32 v226, v226, v226
	v_max_f32_e32 v227, v227, v227
	v_max_f32_e32 v228, v228, v228
	v_max_f32_e32 v229, v229, v229
	v_max_f32_e32 v230, v230, v230
	v_max_f32_e32 v231, v231, v231
	v_max_f32_e32 v232, v232, v232
	v_max_f32_e32 v233, v233, v233
	v_max_f32_e32 v234, v234, v234
	v_max_f32_e32 v235, v235, v235
	v_max_f32_e32 v236, v236, v236
	v_max_f32_e32 v237, v237, v237
	v_max_f32_e32 v238, v238, v238
	v_max_f32_e32 v239, v239, v239
	v_max_f32_e32 v240, v240, v240
	v_max_f32_e32 v241, v241, v241
	v_med3_f32 v226, v226, s62, v95
	v_med3_f32 v227, v227, s62, v95
	v_med3_f32 v228, v228, s62, v95
	v_med3_f32 v229, v229, s62, v95
	v_med3_f32 v230, v230, s62, v95
	v_med3_f32 v231, v231, s62, v95
	v_med3_f32 v232, v232, s62, v95
	v_med3_f32 v233, v233, s62, v95
	v_med3_f32 v234, v234, s62, v95
	v_med3_f32 v235, v235, s62, v95
	v_med3_f32 v236, v236, s62, v95
	v_med3_f32 v237, v237, s62, v95
	v_med3_f32 v238, v238, s62, v95
	v_med3_f32 v239, v239, s62, v95
	v_med3_f32 v240, v240, s62, v95
	v_med3_f32 v241, v241, s62, v95
	v_mov_b32_e32 v242, 0
	v_mov_b32_e32 v243, 0
	v_mov_b32_e32 v244, 0
	v_mov_b32_e32 v245, 0
	v_cvt_pk_fp8_f32 v242, v226, v227
	v_cvt_pk_fp8_f32 v243, v230, v231
	v_cvt_pk_fp8_f32 v244, v234, v235
	v_cvt_pk_fp8_f32 v245, v238, v239
	v_cvt_pk_fp8_f32 v242, v228, v229 op_sel:[0,0,1]
	v_cvt_pk_fp8_f32 v243, v232, v233 op_sel:[0,0,1]
	v_cvt_pk_fp8_f32 v244, v236, v237 op_sel:[0,0,1]
	v_cvt_pk_fp8_f32 v245, v240, v241 op_sel:[0,0,1]
	s_nop 0
	global_store_dwordx4 v78, v[242:245], s[6:7]
	s_waitcnt vmcnt(12)
	v_mul_f32_e32 v176, v26, v176
	v_mul_f32_e32 v177, v26, v177
	v_mul_f32_e32 v178, v26, v178
	v_mul_f32_e32 v179, v26, v179
	ds_write_b128 v210, v[176:179]
	v_mul_f32_e32 v180, v27, v180
	v_mul_f32_e32 v181, v27, v181
	v_mul_f32_e32 v182, v27, v182
	v_mul_f32_e32 v183, v27, v183
	ds_write_b128 v210, v[180:183] offset:1024
	v_mul_f32_e32 v184, v28, v184
	v_mul_f32_e32 v185, v28, v185
	v_mul_f32_e32 v186, v28, v186
	v_mul_f32_e32 v187, v28, v187
	ds_write_b128 v210, v[184:187] offset:2048
	v_mul_f32_e32 v188, v29, v188
	v_mul_f32_e32 v189, v29, v189
	v_mul_f32_e32 v190, v29, v190
	v_mul_f32_e32 v191, v29, v191
	ds_write_b128 v210, v[188:191] offset:3072
	v_mul_f32_e32 v192, v30, v192
	v_mul_f32_e32 v193, v30, v193
	v_mul_f32_e32 v194, v30, v194
	v_mul_f32_e32 v195, v30, v195
	ds_write_b128 v210, v[192:195] offset:4096
	v_mul_f32_e32 v196, v31, v196
	v_mul_f32_e32 v197, v31, v197
	v_mul_f32_e32 v198, v31, v198
	v_mul_f32_e32 v199, v31, v199
	ds_write_b128 v210, v[196:199] offset:5120
	v_mul_f32_e32 v200, v32, v200
	v_mul_f32_e32 v201, v32, v201
	v_mul_f32_e32 v202, v32, v202
	v_mul_f32_e32 v203, v32, v203
	ds_write_b128 v210, v[200:203] offset:6144
	v_mul_f32_e32 v204, v33, v204
	v_mul_f32_e32 v205, v33, v205
	v_mul_f32_e32 v206, v33, v206
	v_mul_f32_e32 v207, v33, v207
	ds_write_b128 v210, v[204:207] offset:7168
	s_waitcnt lgkmcnt(0)
	s_barrier
; #define GAS __attribute__((address_space(1)))
; #define LAS __attribute__((address_space(3)))
; #define LDS_WAIT() asm volatile("s_waitcnt lgkmcnt(0)" ::: "memory")
; __device__ __forceinline__ unsigned pk4_fp8(float a, float b, float c, float d) {
;     a = fminf(fmaxf(a, -448.f), 448.f); b = fminf(fmaxf(b, -448.f), 448.f); c = fminf(fmaxf(c, -448.f), 448.f); d = fminf(fmaxf(d, -448.f), 448.f);
;     int w = __builtin_amdgcn_cvt_pk_fp8_f32(a, b, 0, false); w = __builtin_amdgcn_cvt_pk_fp8_f32(c, d, w, true); return (unsigned)w; }
;     ...
; #pragma unroll
;     for (int i = 0; i < 32; ++i) v[i] = sc >= 0 ? W[(size_t)(k0 + 2 * i + (lane >> 5)) * Nsrc + sc] : 0.f;
; #pragma unroll
;     for (int i = 0; i < 32; ++i) { const int k = k0 + 2 * i + (lane >> 5); float x = v[i] * wscale; if (KS) x *= (k < ksplit ? ksA[k] : ksB[k - ksplit]); scr[(2 * i + (lane >> 5)) * 33 + (lane & 31)] = x; }
;     LDS_WAIT(); asm volatile("" ::: "memory");
;     const int c = lane & 7;
; #pragma unroll
;     for (int j = 0; j < 4; ++j) { const int n = (lane >> 3) + 8 * j; const LAS float* s = scr + (8 * c) * 33 + n;
;         const unsigned long long o = (unsigned long long)pg8::pk4_fp8(s[0 * 33], s[1 * 33], s[2 * 33], s[3 * 33]) | ((unsigned long long)pg8::pk4_fp8(s[4 * 33], s[5 * 33], s[6 * 33], s[7 * 33]) << 32);
;         *(GAS unsigned long long*)(WT + (size_t)(n0 + n) * K + k0 + 8 * c) = o; }
	s_add_u32 s8, s30, 0xd000
	s_addc_u32 s9, s31, 0
	global_load_dwordx4 v[176:179], v74, s[8:9]
	s_add_u32 s8, s8, 0x20000
	s_addc_u32 s9, s9, 0
	global_load_dwordx4 v[180:183], v74, s[8:9]
	s_add_u32 s8, s8, 0x20000
	s_addc_u32 s9, s9, 0
	global_load_dwordx4 v[184:187], v74, s[8:9]
	s_add_u32 s8, s8, 0x20000
	s_addc_u32 s9, s9, 0
	global_load_dwordx4 v[188:191], v74, s[8:9]
	s_add_u32 s8, s8, 0x20000
	s_addc_u32 s9, s9, 0
	global_load_dwordx4 v[192:195], v74, s[8:9]
	s_add_u32 s8, s8, 0x20000
	s_addc_u32 s9, s9, 0
	global_load_dwordx4 v[196:199], v74, s[8:9]
	s_add_u32 s8, s8, 0x20000
	s_addc_u32 s9, s9, 0
	global_load_dwordx4 v[200:203], v74, s[8:9]
	s_add_u32 s8, s8, 0x20000
	s_addc_u32 s9, s9, 0
	global_load_dwordx4 v[204:207], v74, s[8:9]
	s_add_u32 s6, s32, 0x2c00000
	s_addc_u32 s7, s33, 0
	ds_read_b32 v226, v212
	ds_read_b32 v227, v212 offset:512
	ds_read_b32 v228, v212 offset:1024
	ds_read_b32 v229, v212 offset:1536
	ds_read_b32 v230, v212 offset:2048
	ds_read_b32 v231, v212 offset:2560
	ds_read_b32 v232, v212 offset:3072
	ds_read_b32 v233, v212 offset:3584
	ds_read_b32 v234, v212 offset:4096
	ds_read_b32 v235, v212 offset:4608
	ds_read_b32 v236, v212 offset:5120
	ds_read_b32 v237, v212 offset:5632
	ds_read_b32 v238, v212 offset:6144
	ds_read_b32 v239, v212 offset:6656
	ds_read_b32 v240, v212 offset:7168
	ds_read_b32 v241, v212 offset:7680
	s_waitcnt lgkmcnt(0)
	v_max_f32_e32 v226, v226, v226
	v_max_f32_e32 v227, v227, v227
	v_max_f32_e32 v228, v228, v228
	v_max_f32_e32 v229, v229, v229
	v_max_f32_e32 v230, v230, v230
	v_max_f32_e32 v231, v231, v231
	v_max_f32_e32 v232, v232, v232
	v_max_f32_e32 v233, v233, v233
	v_max_f32_e32 v234, v234, v234
	v_max_f32_e32 v235, v235, v235
	v_max_f32_e32 v236, v236, v236
	v_max_f32_e32 v237, v237, v237
	v_max_f32_e32 v238, v238, v238
	v_max_f32_e32 v239, v239, v239
	v_max_f32_e32 v240, v240, v240
	v_max_f32_e32 v241, v241, v241
	v_med3_f32 v226, v226, s62, v95
	v_med3_f32 v227, v227, s62, v95
	v_med3_f32 v228, v228, s62, v95
	v_med3_f32 v229, v229, s62, v95
	v_med3_f32 v230, v230, s62, v95
	v_med3_f32 v231, v231, s62, v95
	v_med3_f32 v232, v232, s62, v95
	v_med3_f32 v233, v233, s62, v95
	v_med3_f32 v234, v234, s62, v95
	v_med3_f32 v235, v235, s62, v95
	v_med3_f32 v236, v236, s62, v95
	v_med3_f32 v237, v237, s62, v95
	v_med3_f32 v238, v238, s62, v95
	v_med3_f32 v239, v239, s62, v95
	v_med3_f32 v240, v240, s62, v95
	v_med3_f32 v241, v241, s62, v95
	v_mov_b32_e32 v242, 0
	v_mov_b32_e32 v243, 0
	v_mov_b32_e32 v244, 0
	v_mov_b32_e32 v245, 0
	v_cvt_pk_fp8_f32 v242, v226, v227
	v_cvt_pk_fp8_f32 v243, v230, v231
	v_cvt_pk_fp8_f32 v244, v234, v235
	v_cvt_pk_fp8_f32 v245, v238, v239
	v_cvt_pk_fp8_f32 v242, v228, v229 op_sel:[0,0,1]
	v_cvt_pk_fp8_f32 v243, v232, v233 op_sel:[0,0,1]
	v_cvt_pk_fp8_f32 v244, v236, v237 op_sel:[0,0,1]
	v_cvt_pk_fp8_f32 v245, v240, v241 op_sel:[0,0,1]
	s_nop 0
	global_store_dwordx4 v77, v[242:245], s[6:7]
	ds_read_b32 v226, v214
	ds_read_b32 v227, v214 offset:512
	ds_read_b32 v228, v214 offset:1024
	ds_read_b32 v229, v214 offset:1536
	ds_read_b32 v230, v214 offset:2048
	ds_read_b32 v231, v214 offset:2560
	ds_read_b32 v232, v214 offset:3072
	ds_read_b32 v233, v214 offset:3584
	ds_read_b32 v234, v214 offset:4096
	ds_read_b32 v235, v214 offset:4608
	ds_read_b32 v236, v214 offset:5120
	ds_read_b32 v237, v214 offset:5632
	ds_read_b32 v238, v214 offset:6144
	ds_read_b32 v239, v214 offset:6656
	ds_read_b32 v240, v214 offset:7168
	ds_read_b32 v241, v214 offset:7680
	s_waitcnt lgkmcnt(0)
	v_max_f32_e32 v226, v226, v226
	v_max_f32_e32 v227, v227, v227
	v_max_f32_e32 v228, v228, v228
	v_max_f32_e32 v229, v229, v229
	v_max_f32_e32 v230, v230, v230
	v_max_f32_e32 v231, v231, v231
	v_max_f32_e32 v232, v232, v232
	v_max_f32_e32 v233, v233, v233
	v_max_f32_e32 v234, v234, v234
	v_max_f32_e32 v235, v235, v235
	v_max_f32_e32 v236, v236, v236
	v_max_f32_e32 v237, v237, v237
	v_max_f32_e32 v238, v238, v238
	v_max_f32_e32 v239, v239, v239
	v_max_f32_e32 v240, v240, v240
	v_max_f32_e32 v241, v241, v241
	v_med3_f32 v226, v226, s62, v95
	v_med3_f32 v227, v227, s62, v95
	v_med3_f32 v228, v228, s62, v95
	v_med3_f32 v229, v229, s62, v95
	v_med3_f32 v230, v230, s62, v95
	v_med3_f32 v231, v231, s62, v95
	v_med3_f32 v232, v232, s62, v95
	v_med3_f32 v233, v233, s62, v95
	v_med3_f32 v234, v234, s62, v95
	v_med3_f32 v235, v235, s62, v95
	v_med3_f32 v236, v236, s62, v95
	v_med3_f32 v237, v237, s62, v95
	v_med3_f32 v238, v238, s62, v95
	v_med3_f32 v239, v239, s62, v95
	v_med3_f32 v240, v240, s62, v95
	v_med3_f32 v241, v241, s62, v95
	v_mov_b32_e32 v242, 0
	v_mov_b32_e32 v243, 0
	v_mov_b32_e32 v244, 0
	v_mov_b32_e32 v245, 0
	v_cvt_pk_fp8_f32 v242, v226, v227
	v_cvt_pk_fp8_f32 v243, v230, v231
	v_cvt_pk_fp8_f32 v244, v234, v235
	v_cvt_pk_fp8_f32 v245, v238, v239
	v_cvt_pk_fp8_f32 v242, v228, v229 op_sel:[0,0,1]
	v_cvt_pk_fp8_f32 v243, v232, v233 op_sel:[0,0,1]
	v_cvt_pk_fp8_f32 v244, v236, v237 op_sel:[0,0,1]
	v_cvt_pk_fp8_f32 v245, v240, v241 op_sel:[0,0,1]
	s_nop 0
	global_store_dwordx4 v78, v[242:245], s[6:7]
	s_waitcnt vmcnt(12)
	v_mul_f32_e32 v144, v26, v144
	v_mul_f32_e32 v145, v26, v145
	v_mul_f32_e32 v146, v26, v146
	v_mul_f32_e32 v147, v26, v147
	ds_write_b128 v209, v[144:147]
	v_mul_f32_e32 v148, v27, v148
	v_mul_f32_e32 v149, v27, v149
	v_mul_f32_e32 v150, v27, v150
	v_mul_f32_e32 v151, v27, v151
	ds_write_b128 v209, v[148:151] offset:1024
	v_mul_f32_e32 v152, v28, v152
	v_mul_f32_e32 v153, v28, v153
	v_mul_f32_e32 v154, v28, v154
	v_mul_f32_e32 v155, v28, v155
	ds_write_b128 v209, v[152:155] offset:2048
	v_mul_f32_e32 v156, v29, v156
	v_mul_f32_e32 v157, v29, v157
	v_mul_f32_e32 v158, v29, v158
	v_mul_f32_e32 v159, v29, v159
	ds_write_b128 v209, v[156:159] offset:3072
	v_mul_f32_e32 v160, v30, v160
	v_mul_f32_e32 v161, v30, v161
	v_mul_f32_e32 v162, v30, v162
	v_mul_f32_e32 v163, v30, v163
	ds_write_b128 v209, v[160:163] offset:4096
	v_mul_f32_e32 v164, v31, v164
	v_mul_f32_e32 v165, v31, v165
	v_mul_f32_e32 v166, v31, v166
	v_mul_f32_e32 v167, v31, v167
	ds_write_b128 v209, v[164:167] offset:5120
	v_mul_f32_e32 v168, v32, v168
	v_mul_f32_e32 v169, v32, v169
	v_mul_f32_e32 v170, v32, v170
	v_mul_f32_e32 v171, v32, v171
	ds_write_b128 v209, v[168:171] offset:6144
	v_mul_f32_e32 v172, v33, v172
	v_mul_f32_e32 v173, v33, v173
	v_mul_f32_e32 v174, v33, v174
	v_mul_f32_e32 v175, v33, v175
	ds_write_b128 v209, v[172:175] offset:7168
	s_waitcnt lgkmcnt(0)
	s_barrier
; #define GAS __attribute__((address_space(1)))
; #define LAS __attribute__((address_space(3)))
; #define LDS_WAIT() asm volatile("s_waitcnt lgkmcnt(0)" ::: "memory")
; __device__ __forceinline__ unsigned pk4_fp8(float a, float b, float c, float d) {
;     a = fminf(fmaxf(a, -448.f), 448.f); b = fminf(fmaxf(b, -448.f), 448.f); c = fminf(fmaxf(c, -448.f), 448.f); d = fminf(fmaxf(d, -448.f), 448.f);
;     int w = __builtin_amdgcn_cvt_pk_fp8_f32(a, b, 0, false); w = __builtin_amdgcn_cvt_pk_fp8_f32(c, d, w, true); return (unsigned)w; }
;     ...
; #pragma unroll
;     for (int i = 0; i < 32; ++i) v[i] = sc >= 0 ? W[(size_t)(k0 + 2 * i + (lane >> 5)) * Nsrc + sc] : 0.f;
; #pragma unroll
;     for (int i = 0; i < 32; ++i) { const int k = k0 + 2 * i + (lane >> 5); float x = v[i] * wscale; if (KS) x *= (k < ksplit ? ksA[k] : ksB[k - ksplit]); scr[(2 * i + (lane >> 5)) * 33 + (lane & 31)] = x; }
;     LDS_WAIT(); asm volatile("" ::: "memory");
;     const int c = lane & 7;
; #pragma unroll
;     for (int j = 0; j < 4; ++j) { const int n = (lane >> 3) + 8 * j; const LAS float* s = scr + (8 * c) * 33 + n;
;         const unsigned long long o = (unsigned long long)pg8::pk4_fp8(s[0 * 33], s[1 * 33], s[2 * 33], s[3 * 33]) | ((unsigned long long)pg8::pk4_fp8(s[4 * 33], s[5 * 33], s[6 * 33], s[7 * 33]) << 32);
;         *(GAS unsigned long long*)(WT + (size_t)(n0 + n) * K + k0 + 8 * c) = o; }
	s_add_u32 s8, s30, 0xe000
	s_addc_u32 s9, s31, 0
	global_load_dwordx4 v[144:147], v74, s[8:9]
	s_add_u32 s8, s8, 0x20000
	s_addc_u32 s9, s9, 0
	global_load_dwordx4 v[148:151], v74, s[8:9]
	s_add_u32 s8, s8, 0x20000
	s_addc_u32 s9, s9, 0
	global_load_dwordx4 v[152:155], v74, s[8:9]
	s_add_u32 s8, s8, 0x20000
	s_addc_u32 s9, s9, 0
	global_load_dwordx4 v[156:159], v74, s[8:9]
	s_add_u32 s8, s8, 0x20000
	s_addc_u32 s9, s9, 0
	global_load_dwordx4 v[160:163], v74, s[8:9]
	s_add_u32 s8, s8, 0x20000
	s_addc_u32 s9, s9, 0
	global_load_dwordx4 v[164:167], v74, s[8:9]
	s_add_u32 s8, s8, 0x20000
	s_addc_u32 s9, s9, 0
	global_load_dwordx4 v[168:171], v74, s[8:9]
	s_add_u32 s8, s8, 0x20000
	s_addc_u32 s9, s9, 0
	global_load_dwordx4 v[172:175], v74, s[8:9]
	s_add_u32 s6, s32, 0x3000000
	s_addc_u32 s7, s33, 0
	ds_read_b32 v226, v211
	ds_read_b32 v227, v211 offset:512
	ds_read_b32 v228, v211 offset:1024
	ds_read_b32 v229, v211 offset:1536
	ds_read_b32 v230, v211 offset:2048
	ds_read_b32 v231, v211 offset:2560
	ds_read_b32 v232, v211 offset:3072
	ds_read_b32 v233, v211 offset:3584
	ds_read_b32 v234, v211 offset:4096
	ds_read_b32 v235, v211 offset:4608
	ds_read_b32 v236, v211 offset:5120
	ds_read_b32 v237, v211 offset:5632
	ds_read_b32 v238, v211 offset:6144
	ds_read_b32 v239, v211 offset:6656
	ds_read_b32 v240, v211 offset:7168
	ds_read_b32 v241, v211 offset:7680
	s_waitcnt lgkmcnt(0)
	v_max_f32_e32 v226, v226, v226
	v_max_f32_e32 v227, v227, v227
	v_max_f32_e32 v228, v228, v228
	v_max_f32_e32 v229, v229, v229
	v_max_f32_e32 v230, v230, v230
	v_max_f32_e32 v231, v231, v231
	v_max_f32_e32 v232, v232, v232
	v_max_f32_e32 v233, v233, v233
	v_max_f32_e32 v234, v234, v234
	v_max_f32_e32 v235, v235, v235
	v_max_f32_e32 v236, v236, v236
	v_max_f32_e32 v237, v237, v237
	v_max_f32_e32 v238, v238, v238
	v_max_f32_e32 v239, v239, v239
	v_max_f32_e32 v240, v240, v240
	v_max_f32_e32 v241, v241, v241
	v_med3_f32 v226, v226, s62, v95
	v_med3_f32 v227, v227, s62, v95
	v_med3_f32 v228, v228, s62, v95
	v_med3_f32 v229, v229, s62, v95
	v_med3_f32 v230, v230, s62, v95
	v_med3_f32 v231, v231, s62, v95
	v_med3_f32 v232, v232, s62, v95
	v_med3_f32 v233, v233, s62, v95
	v_med3_f32 v234, v234, s62, v95
	v_med3_f32 v235, v235, s62, v95
	v_med3_f32 v236, v236, s62, v95
	v_med3_f32 v237, v237, s62, v95
	v_med3_f32 v238, v238, s62, v95
	v_med3_f32 v239, v239, s62, v95
	v_med3_f32 v240, v240, s62, v95
	v_med3_f32 v241, v241, s62, v95
	v_mov_b32_e32 v242, 0
	v_mov_b32_e32 v243, 0
	v_mov_b32_e32 v244, 0
	v_mov_b32_e32 v245, 0
	v_cvt_pk_fp8_f32 v242, v226, v227
	v_cvt_pk_fp8_f32 v243, v230, v231
	v_cvt_pk_fp8_f32 v244, v234, v235
	v_cvt_pk_fp8_f32 v245, v238, v239
	v_cvt_pk_fp8_f32 v242, v228, v229 op_sel:[0,0,1]
	v_cvt_pk_fp8_f32 v243, v232, v233 op_sel:[0,0,1]
	v_cvt_pk_fp8_f32 v244, v236, v237 op_sel:[0,0,1]
	v_cvt_pk_fp8_f32 v245, v240, v241 op_sel:[0,0,1]
	s_nop 0
	global_store_dwordx4 v77, v[242:245], s[6:7]
	ds_read_b32 v226, v213
	ds_read_b32 v227, v213 offset:512
	ds_read_b32 v228, v213 offset:1024
	ds_read_b32 v229, v213 offset:1536
	ds_read_b32 v230, v213 offset:2048
	ds_read_b32 v231, v213 offset:2560
	ds_read_b32 v232, v213 offset:3072
	ds_read_b32 v233, v213 offset:3584
	ds_read_b32 v234, v213 offset:4096
	ds_read_b32 v235, v213 offset:4608
	ds_read_b32 v236, v213 offset:5120
	ds_read_b32 v237, v213 offset:5632
	ds_read_b32 v238, v213 offset:6144
	ds_read_b32 v239, v213 offset:6656
	ds_read_b32 v240, v213 offset:7168
	ds_read_b32 v241, v213 offset:7680
	s_waitcnt lgkmcnt(0)
	v_max_f32_e32 v226, v226, v226
	v_max_f32_e32 v227, v227, v227
	v_max_f32_e32 v228, v228, v228
	v_max_f32_e32 v229, v229, v229
	v_max_f32_e32 v230, v230, v230
	v_max_f32_e32 v231, v231, v231
	v_max_f32_e32 v232, v232, v232
	v_max_f32_e32 v233, v233, v233
	v_max_f32_e32 v234, v234, v234
	v_max_f32_e32 v235, v235, v235
	v_max_f32_e32 v236, v236, v236
	v_max_f32_e32 v237, v237, v237
	v_max_f32_e32 v238, v238, v238
	v_max_f32_e32 v239, v239, v239
	v_max_f32_e32 v240, v240, v240
	v_max_f32_e32 v241, v241, v241
	v_med3_f32 v226, v226, s62, v95
	v_med3_f32 v227, v227, s62, v95
	v_med3_f32 v228, v228, s62, v95
	v_med3_f32 v229, v229, s62, v95
	v_med3_f32 v230, v230, s62, v95
	v_med3_f32 v231, v231, s62, v95
	v_med3_f32 v232, v232, s62, v95
	v_med3_f32 v233, v233, s62, v95
	v_med3_f32 v234, v234, s62, v95
	v_med3_f32 v235, v235, s62, v95
	v_med3_f32 v236, v236, s62, v95
	v_med3_f32 v237, v237, s62, v95
	v_med3_f32 v238, v238, s62, v95
	v_med3_f32 v239, v239, s62, v95
	v_med3_f32 v240, v240, s62, v95
	v_med3_f32 v241, v241, s62, v95
	v_mov_b32_e32 v242, 0
	v_mov_b32_e32 v243, 0
	v_mov_b32_e32 v244, 0
	v_mov_b32_e32 v245, 0
	v_cvt_pk_fp8_f32 v242, v226, v227
	v_cvt_pk_fp8_f32 v243, v230, v231
	v_cvt_pk_fp8_f32 v244, v234, v235
	v_cvt_pk_fp8_f32 v245, v238, v239
	v_cvt_pk_fp8_f32 v242, v228, v229 op_sel:[0,0,1]
	v_cvt_pk_fp8_f32 v243, v232, v233 op_sel:[0,0,1]
	v_cvt_pk_fp8_f32 v244, v236, v237 op_sel:[0,0,1]
	v_cvt_pk_fp8_f32 v245, v240, v241 op_sel:[0,0,1]
	s_nop 0
	global_store_dwordx4 v78, v[242:245], s[6:7]
	s_waitcnt vmcnt(12)
	v_mul_f32_e32 v176, v26, v176
	v_mul_f32_e32 v177, v26, v177
	v_mul_f32_e32 v178, v26, v178
	v_mul_f32_e32 v179, v26, v179
	ds_write_b128 v210, v[176:179]
	v_mul_f32_e32 v180, v27, v180
	v_mul_f32_e32 v181, v27, v181
	v_mul_f32_e32 v182, v27, v182
	v_mul_f32_e32 v183, v27, v183
	ds_write_b128 v210, v[180:183] offset:1024
	v_mul_f32_e32 v184, v28, v184
	v_mul_f32_e32 v185, v28, v185
	v_mul_f32_e32 v186, v28, v186
	v_mul_f32_e32 v187, v28, v187
	ds_write_b128 v210, v[184:187] offset:2048
	v_mul_f32_e32 v188, v29, v188
	v_mul_f32_e32 v189, v29, v189
	v_mul_f32_e32 v190, v29, v190
	v_mul_f32_e32 v191, v29, v191
	ds_write_b128 v210, v[188:191] offset:3072
	v_mul_f32_e32 v192, v30, v192
	v_mul_f32_e32 v193, v30, v193
	v_mul_f32_e32 v194, v30, v194
	v_mul_f32_e32 v195, v30, v195
	ds_write_b128 v210, v[192:195] offset:4096
	v_mul_f32_e32 v196, v31, v196
	v_mul_f32_e32 v197, v31, v197
	v_mul_f32_e32 v198, v31, v198
	v_mul_f32_e32 v199, v31, v199
	ds_write_b128 v210, v[196:199] offset:5120
	v_mul_f32_e32 v200, v32, v200
	v_mul_f32_e32 v201, v32, v201
	v_mul_f32_e32 v202, v32, v202
	v_mul_f32_e32 v203, v32, v203
	ds_write_b128 v210, v[200:203] offset:6144
	v_mul_f32_e32 v204, v33, v204
	v_mul_f32_e32 v205, v33, v205
	v_mul_f32_e32 v206, v33, v206
	v_mul_f32_e32 v207, v33, v207
	ds_write_b128 v210, v[204:207] offset:7168
	s_waitcnt lgkmcnt(0)
	s_barrier
; #define GAS __attribute__((address_space(1)))
; #define LAS __attribute__((address_space(3)))
; #define LDS_WAIT() asm volatile("s_waitcnt lgkmcnt(0)" ::: "memory")
; __device__ __forceinline__ unsigned pk4_fp8(float a, float b, float c, float d) {
;     a = fminf(fmaxf(a, -448.f), 448.f); b = fminf(fmaxf(b, -448.f), 448.f); c = fminf(fmaxf(c, -448.f), 448.f); d = fminf(fmaxf(d, -448.f), 448.f);
;     int w = __builtin_amdgcn_cvt_pk_fp8_f32(a, b, 0, false); w = __builtin_amdgcn_cvt_pk_fp8_f32(c, d, w, true); return (unsigned)w; }
;     ...
; #pragma unroll
;     for (int i = 0; i < 32; ++i) v[i] = sc >= 0 ? W[(size_t)(k0 + 2 * i + (lane >> 5)) * Nsrc + sc] : 0.f;
; #pragma unroll
;     for (int i = 0; i < 32; ++i) { const int k = k0 + 2 * i + (lane >> 5); float x = v[i] * wscale; if (KS) x *= (k < ksplit ? ksA[k] : ksB[k - ksplit]); scr[(2 * i + (lane >> 5)) * 33 + (lane & 31)] = x; }
;     LDS_WAIT(); asm volatile("" ::: "memory");
;     const int c = lane & 7;
; #pragma unroll
;     for (int j = 0; j < 4; ++j) { const int n = (lane >> 3) + 8 * j; const LAS float* s = scr + (8 * c) * 33 + n;
;         const unsigned long long o = (unsigned long long)pg8::pk4_fp8(s[0 * 33], s[1 * 33], s[2 * 33], s[3 * 33]) | ((unsigned long long)pg8::pk4_fp8(s[4 * 33], s[5 * 33], s[6 * 33], s[7 * 33]) << 32);
;         *(GAS unsigned long long*)(WT + (size_t)(n0 + n) * K + k0 + 8 * c) = o; }
	s_add_u32 s8, s30, 0xf000
	s_addc_u32 s9, s31, 0
	global_load_dwordx4 v[176:179], v74, s[8:9]
	s_add_u32 s8, s8, 0x20000
	s_addc_u32 s9, s9, 0
	global_load_dwordx4 v[180:183], v74, s[8:9]
	s_add_u32 s8, s8, 0x20000
	s_addc_u32 s9, s9, 0
	global_load_dwordx4 v[184:187], v74, s[8:9]
	s_add_u32 s8, s8, 0x20000
	s_addc_u32 s9, s9, 0
	global_load_dwordx4 v[188:191], v74, s[8:9]
	s_add_u32 s8, s8, 0x20000
	s_addc_u32 s9, s9, 0
	global_load_dwordx4 v[192:195], v74, s[8:9]
	s_add_u32 s8, s8, 0x20000
	s_addc_u32 s9, s9, 0
	global_load_dwordx4 v[196:199], v74, s[8:9]
	s_add_u32 s8, s8, 0x20000
	s_addc_u32 s9, s9, 0
	global_load_dwordx4 v[200:203], v74, s[8:9]
	s_add_u32 s8, s8, 0x20000
	s_addc_u32 s9, s9, 0
	global_load_dwordx4 v[204:207], v74, s[8:9]
	s_add_u32 s6, s32, 0x3400000
	s_addc_u32 s7, s33, 0
	ds_read_b32 v226, v212
	ds_read_b32 v227, v212 offset:512
	ds_read_b32 v228, v212 offset:1024
	ds_read_b32 v229, v212 offset:1536
	ds_read_b32 v230, v212 offset:2048
	ds_read_b32 v231, v212 offset:2560
	ds_read_b32 v232, v212 offset:3072
	ds_read_b32 v233, v212 offset:3584
	ds_read_b32 v234, v212 offset:4096
	ds_read_b32 v235, v212 offset:4608
	ds_read_b32 v236, v212 offset:5120
	ds_read_b32 v237, v212 offset:5632
	ds_read_b32 v238, v212 offset:6144
	ds_read_b32 v239, v212 offset:6656
	ds_read_b32 v240, v212 offset:7168
	ds_read_b32 v241, v212 offset:7680
	s_waitcnt lgkmcnt(0)
	v_max_f32_e32 v226, v226, v226
	v_max_f32_e32 v227, v227, v227
	v_max_f32_e32 v228, v228, v228
	v_max_f32_e32 v229, v229, v229
	v_max_f32_e32 v230, v230, v230
	v_max_f32_e32 v231, v231, v231
	v_max_f32_e32 v232, v232, v232
	v_max_f32_e32 v233, v233, v233
	v_max_f32_e32 v234, v234, v234
	v_max_f32_e32 v235, v235, v235
	v_max_f32_e32 v236, v236, v236
	v_max_f32_e32 v237, v237, v237
	v_max_f32_e32 v238, v238, v238
	v_max_f32_e32 v239, v239, v239
	v_max_f32_e32 v240, v240, v240
	v_max_f32_e32 v241, v241, v241
	v_med3_f32 v226, v226, s62, v95
	v_med3_f32 v227, v227, s62, v95
	v_med3_f32 v228, v228, s62, v95
	v_med3_f32 v229, v229, s62, v95
	v_med3_f32 v230, v230, s62, v95
	v_med3_f32 v231, v231, s62, v95
	v_med3_f32 v232, v232, s62, v95
	v_med3_f32 v233, v233, s62, v95
	v_med3_f32 v234, v234, s62, v95
	v_med3_f32 v235, v235, s62, v95
	v_med3_f32 v236, v236, s62, v95
	v_med3_f32 v237, v237, s62, v95
	v_med3_f32 v238, v238, s62, v95
	v_med3_f32 v239, v239, s62, v95
	v_med3_f32 v240, v240, s62, v95
	v_med3_f32 v241, v241, s62, v95
	v_mov_b32_e32 v242, 0
	v_mov_b32_e32 v243, 0
	v_mov_b32_e32 v244, 0
	v_mov_b32_e32 v245, 0
	v_cvt_pk_fp8_f32 v242, v226, v227
	v_cvt_pk_fp8_f32 v243, v230, v231
	v_cvt_pk_fp8_f32 v244, v234, v235
	v_cvt_pk_fp8_f32 v245, v238, v239
	v_cvt_pk_fp8_f32 v242, v228, v229 op_sel:[0,0,1]
	v_cvt_pk_fp8_f32 v243, v232, v233 op_sel:[0,0,1]
	v_cvt_pk_fp8_f32 v244, v236, v237 op_sel:[0,0,1]
	v_cvt_pk_fp8_f32 v245, v240, v241 op_sel:[0,0,1]
	s_nop 0
	global_store_dwordx4 v77, v[242:245], s[6:7]
	ds_read_b32 v226, v214
	ds_read_b32 v227, v214 offset:512
	ds_read_b32 v228, v214 offset:1024
	ds_read_b32 v229, v214 offset:1536
	ds_read_b32 v230, v214 offset:2048
	ds_read_b32 v231, v214 offset:2560
	ds_read_b32 v232, v214 offset:3072
	ds_read_b32 v233, v214 offset:3584
	ds_read_b32 v234, v214 offset:4096
	ds_read_b32 v235, v214 offset:4608
	ds_read_b32 v236, v214 offset:5120
	ds_read_b32 v237, v214 offset:5632
	ds_read_b32 v238, v214 offset:6144
	ds_read_b32 v239, v214 offset:6656
	ds_read_b32 v240, v214 offset:7168
	ds_read_b32 v241, v214 offset:7680
	s_waitcnt lgkmcnt(0)
	v_max_f32_e32 v226, v226, v226
	v_max_f32_e32 v227, v227, v227
	v_max_f32_e32 v228, v228, v228
	v_max_f32_e32 v229, v229, v229
	v_max_f32_e32 v230, v230, v230
	v_max_f32_e32 v231, v231, v231
	v_max_f32_e32 v232, v232, v232
	v_max_f32_e32 v233, v233, v233
	v_max_f32_e32 v234, v234, v234
	v_max_f32_e32 v235, v235, v235
	v_max_f32_e32 v236, v236, v236
	v_max_f32_e32 v237, v237, v237
	v_max_f32_e32 v238, v238, v238
	v_max_f32_e32 v239, v239, v239
	v_max_f32_e32 v240, v240, v240
	v_max_f32_e32 v241, v241, v241
	v_med3_f32 v226, v226, s62, v95
	v_med3_f32 v227, v227, s62, v95
	v_med3_f32 v228, v228, s62, v95
	v_med3_f32 v229, v229, s62, v95
	v_med3_f32 v230, v230, s62, v95
	v_med3_f32 v231, v231, s62, v95
	v_med3_f32 v232, v232, s62, v95
	v_med3_f32 v233, v233, s62, v95
	v_med3_f32 v234, v234, s62, v95
	v_med3_f32 v235, v235, s62, v95
	v_med3_f32 v236, v236, s62, v95
	v_med3_f32 v237, v237, s62, v95
	v_med3_f32 v238, v238, s62, v95
	v_med3_f32 v239, v239, s62, v95
	v_med3_f32 v240, v240, s62, v95
	v_med3_f32 v241, v241, s62, v95
	v_mov_b32_e32 v242, 0
	v_mov_b32_e32 v243, 0
	v_mov_b32_e32 v244, 0
	v_mov_b32_e32 v245, 0
	v_cvt_pk_fp8_f32 v242, v226, v227
	v_cvt_pk_fp8_f32 v243, v230, v231
	v_cvt_pk_fp8_f32 v244, v234, v235
	v_cvt_pk_fp8_f32 v245, v238, v239
	v_cvt_pk_fp8_f32 v242, v228, v229 op_sel:[0,0,1]
	v_cvt_pk_fp8_f32 v243, v232, v233 op_sel:[0,0,1]
	v_cvt_pk_fp8_f32 v244, v236, v237 op_sel:[0,0,1]
	v_cvt_pk_fp8_f32 v245, v240, v241 op_sel:[0,0,1]
	s_nop 0
	global_store_dwordx4 v78, v[242:245], s[6:7]
	s_waitcnt vmcnt(12)
	v_mul_f32_e32 v144, v26, v144
	v_mul_f32_e32 v145, v26, v145
	v_mul_f32_e32 v146, v26, v146
	v_mul_f32_e32 v147, v26, v147
	ds_write_b128 v209, v[144:147]
	v_mul_f32_e32 v148, v27, v148
	v_mul_f32_e32 v149, v27, v149
	v_mul_f32_e32 v150, v27, v150
	v_mul_f32_e32 v151, v27, v151
	ds_write_b128 v209, v[148:151] offset:1024
	v_mul_f32_e32 v152, v28, v152
	v_mul_f32_e32 v153, v28, v153
	v_mul_f32_e32 v154, v28, v154
	v_mul_f32_e32 v155, v28, v155
	ds_write_b128 v209, v[152:155] offset:2048
	v_mul_f32_e32 v156, v29, v156
	v_mul_f32_e32 v157, v29, v157
	v_mul_f32_e32 v158, v29, v158
	v_mul_f32_e32 v159, v29, v159
	ds_write_b128 v209, v[156:159] offset:3072
	v_mul_f32_e32 v160, v30, v160
	v_mul_f32_e32 v161, v30, v161
	v_mul_f32_e32 v162, v30, v162
	v_mul_f32_e32 v163, v30, v163
	ds_write_b128 v209, v[160:163] offset:4096
	v_mul_f32_e32 v164, v31, v164
	v_mul_f32_e32 v165, v31, v165
	v_mul_f32_e32 v166, v31, v166
	v_mul_f32_e32 v167, v31, v167
	ds_write_b128 v209, v[164:167] offset:5120
	v_mul_f32_e32 v168, v32, v168
	v_mul_f32_e32 v169, v32, v169
	v_mul_f32_e32 v170, v32, v170
	v_mul_f32_e32 v171, v32, v171
	ds_write_b128 v209, v[168:171] offset:6144
	v_mul_f32_e32 v172, v33, v172
	v_mul_f32_e32 v173, v33, v173
	v_mul_f32_e32 v174, v33, v174
	v_mul_f32_e32 v175, v33, v175
	ds_write_b128 v209, v[172:175] offset:7168
	s_waitcnt lgkmcnt(0)
	s_barrier
; #define GAS __attribute__((address_space(1)))
; #define LAS __attribute__((address_space(3)))
; #define LDS_WAIT() asm volatile("s_waitcnt lgkmcnt(0)" ::: "memory")
; __device__ __forceinline__ unsigned pk4_fp8(float a, float b, float c, float d) {
;     a = fminf(fmaxf(a, -448.f), 448.f); b = fminf(fmaxf(b, -448.f), 448.f); c = fminf(fmaxf(c, -448.f), 448.f); d = fminf(fmaxf(d, -448.f), 448.f);
;     int w = __builtin_amdgcn_cvt_pk_fp8_f32(a, b, 0, false); w = __builtin_amdgcn_cvt_pk_fp8_f32(c, d, w, true); return (unsigned)w; }
;     ...
; #pragma unroll
;     for (int i = 0; i < 32; ++i) v[i] = sc >= 0 ? W[(size_t)(k0 + 2 * i + (lane >> 5)) * Nsrc + sc] : 0.f;
; #pragma unroll
;     for (int i = 0; i < 32; ++i) { const int k = k0 + 2 * i + (lane >> 5); float x = v[i] * wscale; if (KS) x *= (k < ksplit ? ksA[k] : ksB[k - ksplit]); scr[(2 * i + (lane >> 5)) * 33 + (lane & 31)] = x; }
;     LDS_WAIT(); asm volatile("" ::: "memory");
;     const int c = lane & 7;
; #pragma unroll
;     for (int j = 0; j < 4; ++j) { const int n = (lane >> 3) + 8 * j; const LAS float* s = scr + (8 * c) * 33 + n;
;         const unsigned long long o = (unsigned long long)pg8::pk4_fp8(s[0 * 33], s[1 * 33], s[2 * 33], s[3 * 33]) | ((unsigned long long)pg8::pk4_fp8(s[4 * 33], s[5 * 33], s[6 * 33], s[7 * 33]) << 32);
;         *(GAS unsigned long long*)(WT + (size_t)(n0 + n) * K + k0 + 8 * c) = o; }
	s_mov_b64 s[8:9], s[34:35]
	global_load_dwordx4 v[144:147], v74, s[8:9]
	s_add_u32 s8, s8, 0x20000
	s_addc_u32 s9, s9, 0
	global_load_dwordx4 v[148:151], v74, s[8:9]
	s_add_u32 s8, s8, 0x20000
	s_addc_u32 s9, s9, 0
	global_load_dwordx4 v[152:155], v74, s[8:9]
	s_add_u32 s8, s8, 0x20000
	s_addc_u32 s9, s9, 0
	global_load_dwordx4 v[156:159], v74, s[8:9]
	s_add_u32 s8, s8, 0x20000
	s_addc_u32 s9, s9, 0
	global_load_dwordx4 v[160:163], v74, s[8:9]
	s_add_u32 s8, s8, 0x20000
	s_addc_u32 s9, s9, 0
	global_load_dwordx4 v[164:167], v74, s[8:9]
	s_add_u32 s8, s8, 0x20000
	s_addc_u32 s9, s9, 0
	global_load_dwordx4 v[168:171], v74, s[8:9]
	s_add_u32 s8, s8, 0x20000
	s_addc_u32 s9, s9, 0
	global_load_dwordx4 v[172:175], v74, s[8:9]
	s_add_u32 s6, s32, 0x3800000
	s_addc_u32 s7, s33, 0
	ds_read_b32 v226, v211
	ds_read_b32 v227, v211 offset:512
	ds_read_b32 v228, v211 offset:1024
	ds_read_b32 v229, v211 offset:1536
	ds_read_b32 v230, v211 offset:2048
	ds_read_b32 v231, v211 offset:2560
	ds_read_b32 v232, v211 offset:3072
	ds_read_b32 v233, v211 offset:3584
	ds_read_b32 v234, v211 offset:4096
	ds_read_b32 v235, v211 offset:4608
	ds_read_b32 v236, v211 offset:5120
	ds_read_b32 v237, v211 offset:5632
	ds_read_b32 v238, v211 offset:6144
	ds_read_b32 v239, v211 offset:6656
	ds_read_b32 v240, v211 offset:7168
	ds_read_b32 v241, v211 offset:7680
	s_waitcnt lgkmcnt(0)
	v_max_f32_e32 v226, v226, v226
	v_max_f32_e32 v227, v227, v227
	v_max_f32_e32 v228, v228, v228
	v_max_f32_e32 v229, v229, v229
	v_max_f32_e32 v230, v230, v230
	v_max_f32_e32 v231, v231, v231
	v_max_f32_e32 v232, v232, v232
	v_max_f32_e32 v233, v233, v233
	v_max_f32_e32 v234, v234, v234
	v_max_f32_e32 v235, v235, v235
	v_max_f32_e32 v236, v236, v236
	v_max_f32_e32 v237, v237, v237
	v_max_f32_e32 v238, v238, v238
	v_max_f32_e32 v239, v239, v239
	v_max_f32_e32 v240, v240, v240
	v_max_f32_e32 v241, v241, v241
	v_med3_f32 v226, v226, s62, v95
	v_med3_f32 v227, v227, s62, v95
	v_med3_f32 v228, v228, s62, v95
	v_med3_f32 v229, v229, s62, v95
	v_med3_f32 v230, v230, s62, v95
	v_med3_f32 v231, v231, s62, v95
	v_med3_f32 v232, v232, s62, v95
	v_med3_f32 v233, v233, s62, v95
	v_med3_f32 v234, v234, s62, v95
	v_med3_f32 v235, v235, s62, v95
	v_med3_f32 v236, v236, s62, v95
	v_med3_f32 v237, v237, s62, v95
	v_med3_f32 v238, v238, s62, v95
	v_med3_f32 v239, v239, s62, v95
	v_med3_f32 v240, v240, s62, v95
	v_med3_f32 v241, v241, s62, v95
	v_mov_b32_e32 v242, 0
	v_mov_b32_e32 v243, 0
	v_mov_b32_e32 v244, 0
	v_mov_b32_e32 v245, 0
	v_cvt_pk_fp8_f32 v242, v226, v227
	v_cvt_pk_fp8_f32 v243, v230, v231
	v_cvt_pk_fp8_f32 v244, v234, v235
	v_cvt_pk_fp8_f32 v245, v238, v239
	v_cvt_pk_fp8_f32 v242, v228, v229 op_sel:[0,0,1]
	v_cvt_pk_fp8_f32 v243, v232, v233 op_sel:[0,0,1]
	v_cvt_pk_fp8_f32 v244, v236, v237 op_sel:[0,0,1]
	v_cvt_pk_fp8_f32 v245, v240, v241 op_sel:[0,0,1]
	s_nop 0
	global_store_dwordx4 v77, v[242:245], s[6:7]
	ds_read_b32 v226, v213
	ds_read_b32 v227, v213 offset:512
	ds_read_b32 v228, v213 offset:1024
	ds_read_b32 v229, v213 offset:1536
	ds_read_b32 v230, v213 offset:2048
	ds_read_b32 v231, v213 offset:2560
	ds_read_b32 v232, v213 offset:3072
	ds_read_b32 v233, v213 offset:3584
	ds_read_b32 v234, v213 offset:4096
	ds_read_b32 v235, v213 offset:4608
	ds_read_b32 v236, v213 offset:5120
	ds_read_b32 v237, v213 offset:5632
	ds_read_b32 v238, v213 offset:6144
	ds_read_b32 v239, v213 offset:6656
	ds_read_b32 v240, v213 offset:7168
	ds_read_b32 v241, v213 offset:7680
	s_waitcnt lgkmcnt(0)
	v_max_f32_e32 v226, v226, v226
	v_max_f32_e32 v227, v227, v227
	v_max_f32_e32 v228, v228, v228
	v_max_f32_e32 v229, v229, v229
	v_max_f32_e32 v230, v230, v230
	v_max_f32_e32 v231, v231, v231
	v_max_f32_e32 v232, v232, v232
	v_max_f32_e32 v233, v233, v233
	v_max_f32_e32 v234, v234, v234
	v_max_f32_e32 v235, v235, v235
	v_max_f32_e32 v236, v236, v236
	v_max_f32_e32 v237, v237, v237
	v_max_f32_e32 v238, v238, v238
	v_max_f32_e32 v239, v239, v239
	v_max_f32_e32 v240, v240, v240
	v_max_f32_e32 v241, v241, v241
	v_med3_f32 v226, v226, s62, v95
	v_med3_f32 v227, v227, s62, v95
	v_med3_f32 v228, v228, s62, v95
	v_med3_f32 v229, v229, s62, v95
	v_med3_f32 v230, v230, s62, v95
	v_med3_f32 v231, v231, s62, v95
	v_med3_f32 v232, v232, s62, v95
	v_med3_f32 v233, v233, s62, v95
	v_med3_f32 v234, v234, s62, v95
	v_med3_f32 v235, v235, s62, v95
	v_med3_f32 v236, v236, s62, v95
	v_med3_f32 v237, v237, s62, v95
	v_med3_f32 v238, v238, s62, v95
	v_med3_f32 v239, v239, s62, v95
	v_med3_f32 v240, v240, s62, v95
	v_med3_f32 v241, v241, s62, v95
	v_mov_b32_e32 v242, 0
	v_mov_b32_e32 v243, 0
	v_mov_b32_e32 v244, 0
	v_mov_b32_e32 v245, 0
	v_cvt_pk_fp8_f32 v242, v226, v227
	v_cvt_pk_fp8_f32 v243, v230, v231
	v_cvt_pk_fp8_f32 v244, v234, v235
	v_cvt_pk_fp8_f32 v245, v238, v239
	v_cvt_pk_fp8_f32 v242, v228, v229 op_sel:[0,0,1]
	v_cvt_pk_fp8_f32 v243, v232, v233 op_sel:[0,0,1]
	v_cvt_pk_fp8_f32 v244, v236, v237 op_sel:[0,0,1]
	v_cvt_pk_fp8_f32 v245, v240, v241 op_sel:[0,0,1]
	s_nop 0
	global_store_dwordx4 v78, v[242:245], s[6:7]
	s_waitcnt vmcnt(12)
	v_mul_f32_e32 v176, v26, v176
	v_mul_f32_e32 v177, v26, v177
	v_mul_f32_e32 v178, v26, v178
	v_mul_f32_e32 v179, v26, v179
	ds_write_b128 v210, v[176:179]
	v_mul_f32_e32 v180, v27, v180
	v_mul_f32_e32 v181, v27, v181
	v_mul_f32_e32 v182, v27, v182
	v_mul_f32_e32 v183, v27, v183
	ds_write_b128 v210, v[180:183] offset:1024
	v_mul_f32_e32 v184, v28, v184
	v_mul_f32_e32 v185, v28, v185
	v_mul_f32_e32 v186, v28, v186
	v_mul_f32_e32 v187, v28, v187
	ds_write_b128 v210, v[184:187] offset:2048
	v_mul_f32_e32 v188, v29, v188
	v_mul_f32_e32 v189, v29, v189
	v_mul_f32_e32 v190, v29, v190
	v_mul_f32_e32 v191, v29, v191
	ds_write_b128 v210, v[188:191] offset:3072
	v_mul_f32_e32 v192, v30, v192
	v_mul_f32_e32 v193, v30, v193
	v_mul_f32_e32 v194, v30, v194
	v_mul_f32_e32 v195, v30, v195
	ds_write_b128 v210, v[192:195] offset:4096
	v_mul_f32_e32 v196, v31, v196
	v_mul_f32_e32 v197, v31, v197
	v_mul_f32_e32 v198, v31, v198
	v_mul_f32_e32 v199, v31, v199
	ds_write_b128 v210, v[196:199] offset:5120
	v_mul_f32_e32 v200, v32, v200
	v_mul_f32_e32 v201, v32, v201
	v_mul_f32_e32 v202, v32, v202
	v_mul_f32_e32 v203, v32, v203
	ds_write_b128 v210, v[200:203] offset:6144
	v_mul_f32_e32 v204, v33, v204
	v_mul_f32_e32 v205, v33, v205
	v_mul_f32_e32 v206, v33, v206
	v_mul_f32_e32 v207, v33, v207
	ds_write_b128 v210, v[204:207] offset:7168
	s_waitcnt lgkmcnt(0)
	s_barrier
; #define GAS __attribute__((address_space(1)))
; #define LAS __attribute__((address_space(3)))
; #define LDS_WAIT() asm volatile("s_waitcnt lgkmcnt(0)" ::: "memory")
; __device__ __forceinline__ unsigned pk4_fp8(float a, float b, float c, float d) {
;     a = fminf(fmaxf(a, -448.f), 448.f); b = fminf(fmaxf(b, -448.f), 448.f); c = fminf(fmaxf(c, -448.f), 448.f); d = fminf(fmaxf(d, -448.f), 448.f);
;     int w = __builtin_amdgcn_cvt_pk_fp8_f32(a, b, 0, false); w = __builtin_amdgcn_cvt_pk_fp8_f32(c, d, w, true); return (unsigned)w; }
;     ...
; #pragma unroll
;     for (int i = 0; i < 32; ++i) v[i] = sc >= 0 ? W[(size_t)(k0 + 2 * i + (lane >> 5)) * Nsrc + sc] : 0.f;
; #pragma unroll
;     for (int i = 0; i < 32; ++i) { const int k = k0 + 2 * i + (lane >> 5); float x = v[i] * wscale; if (KS) x *= (k < ksplit ? ksA[k] : ksB[k - ksplit]); scr[(2 * i + (lane >> 5)) * 33 + (lane & 31)] = x; }
;     LDS_WAIT(); asm volatile("" ::: "memory");
;     const int c = lane & 7;
; #pragma unroll
;     for (int j = 0; j < 4; ++j) { const int n = (lane >> 3) + 8 * j; const LAS float* s = scr + (8 * c) * 33 + n;
;         const unsigned long long o = (unsigned long long)pg8::pk4_fp8(s[0 * 33], s[1 * 33], s[2 * 33], s[3 * 33]) | ((unsigned long long)pg8::pk4_fp8(s[4 * 33], s[5 * 33], s[6 * 33], s[7 * 33]) << 32);
;         *(GAS unsigned long long*)(WT + (size_t)(n0 + n) * K + k0 + 8 * c) = o; }
	s_add_u32 s8, s34, 0x1000
	s_addc_u32 s9, s35, 0
	global_load_dwordx4 v[176:179], v74, s[8:9]
	s_add_u32 s8, s8, 0x20000
	s_addc_u32 s9, s9, 0
	global_load_dwordx4 v[180:183], v74, s[8:9]
	s_add_u32 s8, s8, 0x20000
	s_addc_u32 s9, s9, 0
	global_load_dwordx4 v[184:187], v74, s[8:9]
	s_add_u32 s8, s8, 0x20000
	s_addc_u32 s9, s9, 0
	global_load_dwordx4 v[188:191], v74, s[8:9]
	s_add_u32 s8, s8, 0x20000
	s_addc_u32 s9, s9, 0
	global_load_dwordx4 v[192:195], v74, s[8:9]
	s_add_u32 s8, s8, 0x20000
	s_addc_u32 s9, s9, 0
	global_load_dwordx4 v[196:199], v74, s[8:9]
	s_add_u32 s8, s8, 0x20000
	s_addc_u32 s9, s9, 0
	global_load_dwordx4 v[200:203], v74, s[8:9]
	s_add_u32 s8, s8, 0x20000
	s_addc_u32 s9, s9, 0
	global_load_dwordx4 v[204:207], v74, s[8:9]
	s_add_u32 s6, s32, 0x3c00000
	s_addc_u32 s7, s33, 0
	ds_read_b32 v226, v212
	ds_read_b32 v227, v212 offset:512
	ds_read_b32 v228, v212 offset:1024
	ds_read_b32 v229, v212 offset:1536
	ds_read_b32 v230, v212 offset:2048
	ds_read_b32 v231, v212 offset:2560
	ds_read_b32 v232, v212 offset:3072
	ds_read_b32 v233, v212 offset:3584
	ds_read_b32 v234, v212 offset:4096
	ds_read_b32 v235, v212 offset:4608
	ds_read_b32 v236, v212 offset:5120
	ds_read_b32 v237, v212 offset:5632
	ds_read_b32 v238, v212 offset:6144
	ds_read_b32 v239, v212 offset:6656
	ds_read_b32 v240, v212 offset:7168
	ds_read_b32 v241, v212 offset:7680
	s_waitcnt lgkmcnt(0)
	v_max_f32_e32 v226, v226, v226
	v_max_f32_e32 v227, v227, v227
	v_max_f32_e32 v228, v228, v228
	v_max_f32_e32 v229, v229, v229
	v_max_f32_e32 v230, v230, v230
	v_max_f32_e32 v231, v231, v231
	v_max_f32_e32 v232, v232, v232
	v_max_f32_e32 v233, v233, v233
	v_max_f32_e32 v234, v234, v234
	v_max_f32_e32 v235, v235, v235
	v_max_f32_e32 v236, v236, v236
	v_max_f32_e32 v237, v237, v237
	v_max_f32_e32 v238, v238, v238
	v_max_f32_e32 v239, v239, v239
	v_max_f32_e32 v240, v240, v240
	v_max_f32_e32 v241, v241, v241
	v_med3_f32 v226, v226, s62, v95
	v_med3_f32 v227, v227, s62, v95
	v_med3_f32 v228, v228, s62, v95
	v_med3_f32 v229, v229, s62, v95
	v_med3_f32 v230, v230, s62, v95
	v_med3_f32 v231, v231, s62, v95
	v_med3_f32 v232, v232, s62, v95
	v_med3_f32 v233, v233, s62, v95
	v_med3_f32 v234, v234, s62, v95
	v_med3_f32 v235, v235, s62, v95
	v_med3_f32 v236, v236, s62, v95
	v_med3_f32 v237, v237, s62, v95
	v_med3_f32 v238, v238, s62, v95
	v_med3_f32 v239, v239, s62, v95
	v_med3_f32 v240, v240, s62, v95
	v_med3_f32 v241, v241, s62, v95
	v_mov_b32_e32 v242, 0
	v_mov_b32_e32 v243, 0
	v_mov_b32_e32 v244, 0
	v_mov_b32_e32 v245, 0
	v_cvt_pk_fp8_f32 v242, v226, v227
	v_cvt_pk_fp8_f32 v243, v230, v231
	v_cvt_pk_fp8_f32 v244, v234, v235
	v_cvt_pk_fp8_f32 v245, v238, v239
	v_cvt_pk_fp8_f32 v242, v228, v229 op_sel:[0,0,1]
	v_cvt_pk_fp8_f32 v243, v232, v233 op_sel:[0,0,1]
	v_cvt_pk_fp8_f32 v244, v236, v237 op_sel:[0,0,1]
	v_cvt_pk_fp8_f32 v245, v240, v241 op_sel:[0,0,1]
	s_nop 0
	global_store_dwordx4 v77, v[242:245], s[6:7]
	ds_read_b32 v226, v214
	ds_read_b32 v227, v214 offset:512
	ds_read_b32 v228, v214 offset:1024
	ds_read_b32 v229, v214 offset:1536
	ds_read_b32 v230, v214 offset:2048
	ds_read_b32 v231, v214 offset:2560
	ds_read_b32 v232, v214 offset:3072
	ds_read_b32 v233, v214 offset:3584
	ds_read_b32 v234, v214 offset:4096
	ds_read_b32 v235, v214 offset:4608
	ds_read_b32 v236, v214 offset:5120
	ds_read_b32 v237, v214 offset:5632
	ds_read_b32 v238, v214 offset:6144
	ds_read_b32 v239, v214 offset:6656
	ds_read_b32 v240, v214 offset:7168
	ds_read_b32 v241, v214 offset:7680
	s_waitcnt lgkmcnt(0)
	v_max_f32_e32 v226, v226, v226
	v_max_f32_e32 v227, v227, v227
	v_max_f32_e32 v228, v228, v228
	v_max_f32_e32 v229, v229, v229
	v_max_f32_e32 v230, v230, v230
	v_max_f32_e32 v231, v231, v231
	v_max_f32_e32 v232, v232, v232
	v_max_f32_e32 v233, v233, v233
	v_max_f32_e32 v234, v234, v234
	v_max_f32_e32 v235, v235, v235
	v_max_f32_e32 v236, v236, v236
	v_max_f32_e32 v237, v237, v237
	v_max_f32_e32 v238, v238, v238
	v_max_f32_e32 v239, v239, v239
	v_max_f32_e32 v240, v240, v240
	v_max_f32_e32 v241, v241, v241
	v_med3_f32 v226, v226, s62, v95
	v_med3_f32 v227, v227, s62, v95
	v_med3_f32 v228, v228, s62, v95
	v_med3_f32 v229, v229, s62, v95
	v_med3_f32 v230, v230, s62, v95
	v_med3_f32 v231, v231, s62, v95
	v_med3_f32 v232, v232, s62, v95
	v_med3_f32 v233, v233, s62, v95
	v_med3_f32 v234, v234, s62, v95
	v_med3_f32 v235, v235, s62, v95
	v_med3_f32 v236, v236, s62, v95
	v_med3_f32 v237, v237, s62, v95
	v_med3_f32 v238, v238, s62, v95
	v_med3_f32 v239, v239, s62, v95
	v_med3_f32 v240, v240, s62, v95
	v_med3_f32 v241, v241, s62, v95
	v_mov_b32_e32 v242, 0
	v_mov_b32_e32 v243, 0
	v_mov_b32_e32 v244, 0
	v_mov_b32_e32 v245, 0
	v_cvt_pk_fp8_f32 v242, v226, v227
	v_cvt_pk_fp8_f32 v243, v230, v231
	v_cvt_pk_fp8_f32 v244, v234, v235
	v_cvt_pk_fp8_f32 v245, v238, v239
	v_cvt_pk_fp8_f32 v242, v228, v229 op_sel:[0,0,1]
	v_cvt_pk_fp8_f32 v243, v232, v233 op_sel:[0,0,1]
	v_cvt_pk_fp8_f32 v244, v236, v237 op_sel:[0,0,1]
	v_cvt_pk_fp8_f32 v245, v240, v241 op_sel:[0,0,1]
	s_nop 0
	global_store_dwordx4 v78, v[242:245], s[6:7]
	s_waitcnt vmcnt(12)
	v_mul_f32_e32 v144, v34, v144
	v_mul_f32_e32 v145, v34, v145
	v_mul_f32_e32 v146, v34, v146
	v_mul_f32_e32 v147, v34, v147
	ds_write_b128 v209, v[144:147]
	v_mul_f32_e32 v148, v35, v148
	v_mul_f32_e32 v149, v35, v149
	v_mul_f32_e32 v150, v35, v150
	v_mul_f32_e32 v151, v35, v151
	ds_write_b128 v209, v[148:151] offset:1024
	v_mul_f32_e32 v152, v36, v152
	v_mul_f32_e32 v153, v36, v153
	v_mul_f32_e32 v154, v36, v154
	v_mul_f32_e32 v155, v36, v155
	ds_write_b128 v209, v[152:155] offset:2048
	v_mul_f32_e32 v156, v37, v156
	v_mul_f32_e32 v157, v37, v157
	v_mul_f32_e32 v158, v37, v158
	v_mul_f32_e32 v159, v37, v159
	ds_write_b128 v209, v[156:159] offset:3072
	v_mul_f32_e32 v160, v38, v160
	v_mul_f32_e32 v161, v38, v161
	v_mul_f32_e32 v162, v38, v162
	v_mul_f32_e32 v163, v38, v163
	ds_write_b128 v209, v[160:163] offset:4096
	v_mul_f32_e32 v164, v39, v164
	v_mul_f32_e32 v165, v39, v165
	v_mul_f32_e32 v166, v39, v166
	v_mul_f32_e32 v167, v39, v167
	ds_write_b128 v209, v[164:167] offset:5120
	v_mul_f32_e32 v168, v40, v168
	v_mul_f32_e32 v169, v40, v169
	v_mul_f32_e32 v170, v40, v170
	v_mul_f32_e32 v171, v40, v171
	ds_write_b128 v209, v[168:171] offset:6144
	v_mul_f32_e32 v172, v41, v172
	v_mul_f32_e32 v173, v41, v173
	v_mul_f32_e32 v174, v41, v174
	v_mul_f32_e32 v175, v41, v175
	ds_write_b128 v209, v[172:175] offset:7168
	s_waitcnt lgkmcnt(0)
	s_barrier
; #define GAS __attribute__((address_space(1)))
; #define LAS __attribute__((address_space(3)))
; #define LDS_WAIT() asm volatile("s_waitcnt lgkmcnt(0)" ::: "memory")
; __device__ __forceinline__ unsigned pk4_fp8(float a, float b, float c, float d) {
;     a = fminf(fmaxf(a, -448.f), 448.f); b = fminf(fmaxf(b, -448.f), 448.f); c = fminf(fmaxf(c, -448.f), 448.f); d = fminf(fmaxf(d, -448.f), 448.f);
;     int w = __builtin_amdgcn_cvt_pk_fp8_f32(a, b, 0, false); w = __builtin_amdgcn_cvt_pk_fp8_f32(c, d, w, true); return (unsigned)w; }
;     ...
; #pragma unroll
;     for (int i = 0; i < 32; ++i) v[i] = sc >= 0 ? W[(size_t)(k0 + 2 * i + (lane >> 5)) * Nsrc + sc] : 0.f;
; #pragma unroll
;     for (int i = 0; i < 32; ++i) { const int k = k0 + 2 * i + (lane >> 5); float x = v[i] * wscale; if (KS) x *= (k < ksplit ? ksA[k] : ksB[k - ksplit]); scr[(2 * i + (lane >> 5)) * 33 + (lane & 31)] = x; }
;     LDS_WAIT(); asm volatile("" ::: "memory");
;     const int c = lane & 7;
; #pragma unroll
;     for (int j = 0; j < 4; ++j) { const int n = (lane >> 3) + 8 * j; const LAS float* s = scr + (8 * c) * 33 + n;
;         const unsigned long long o = (unsigned long long)pg8::pk4_fp8(s[0 * 33], s[1 * 33], s[2 * 33], s[3 * 33]) | ((unsigned long long)pg8::pk4_fp8(s[4 * 33], s[5 * 33], s[6 * 33], s[7 * 33]) << 32);
;         *(GAS unsigned long long*)(WT + (size_t)(n0 + n) * K + k0 + 8 * c) = o; }
	s_add_u32 s8, s34, 0x2000
	s_addc_u32 s9, s35, 0
	global_load_dwordx4 v[144:147], v74, s[8:9]
	s_add_u32 s8, s8, 0x20000
	s_addc_u32 s9, s9, 0
	global_load_dwordx4 v[148:151], v74, s[8:9]
	s_add_u32 s8, s8, 0x20000
	s_addc_u32 s9, s9, 0
	global_load_dwordx4 v[152:155], v74, s[8:9]
	s_add_u32 s8, s8, 0x20000
	s_addc_u32 s9, s9, 0
	global_load_dwordx4 v[156:159], v74, s[8:9]
	s_add_u32 s8, s8, 0x20000
	s_addc_u32 s9, s9, 0
	global_load_dwordx4 v[160:163], v74, s[8:9]
	s_add_u32 s8, s8, 0x20000
	s_addc_u32 s9, s9, 0
	global_load_dwordx4 v[164:167], v74, s[8:9]
	s_add_u32 s8, s8, 0x20000
	s_addc_u32 s9, s9, 0
	global_load_dwordx4 v[168:171], v74, s[8:9]
	s_add_u32 s8, s8, 0x20000
	s_addc_u32 s9, s9, 0
	global_load_dwordx4 v[172:175], v74, s[8:9]
	s_mov_b64 s[6:7], s[36:37]
	ds_read_b32 v226, v211
	ds_read_b32 v227, v211 offset:512
	ds_read_b32 v228, v211 offset:1024
	ds_read_b32 v229, v211 offset:1536
	ds_read_b32 v230, v211 offset:2048
	ds_read_b32 v231, v211 offset:2560
	ds_read_b32 v232, v211 offset:3072
	ds_read_b32 v233, v211 offset:3584
	ds_read_b32 v234, v211 offset:4096
	ds_read_b32 v235, v211 offset:4608
	ds_read_b32 v236, v211 offset:5120
	ds_read_b32 v237, v211 offset:5632
	ds_read_b32 v238, v211 offset:6144
	ds_read_b32 v239, v211 offset:6656
	ds_read_b32 v240, v211 offset:7168
	ds_read_b32 v241, v211 offset:7680
	s_waitcnt lgkmcnt(0)
	v_max_f32_e32 v226, v226, v226
	v_max_f32_e32 v227, v227, v227
	v_max_f32_e32 v228, v228, v228
	v_max_f32_e32 v229, v229, v229
	v_max_f32_e32 v230, v230, v230
	v_max_f32_e32 v231, v231, v231
	v_max_f32_e32 v232, v232, v232
	v_max_f32_e32 v233, v233, v233
	v_max_f32_e32 v234, v234, v234
	v_max_f32_e32 v235, v235, v235
	v_max_f32_e32 v236, v236, v236
	v_max_f32_e32 v237, v237, v237
	v_max_f32_e32 v238, v238, v238
	v_max_f32_e32 v239, v239, v239
	v_max_f32_e32 v240, v240, v240
	v_max_f32_e32 v241, v241, v241
	v_med3_f32 v226, v226, s62, v95
	v_med3_f32 v227, v227, s62, v95
	v_med3_f32 v228, v228, s62, v95
	v_med3_f32 v229, v229, s62, v95
	v_med3_f32 v230, v230, s62, v95
	v_med3_f32 v231, v231, s62, v95
	v_med3_f32 v232, v232, s62, v95
	v_med3_f32 v233, v233, s62, v95
	v_med3_f32 v234, v234, s62, v95
	v_med3_f32 v235, v235, s62, v95
	v_med3_f32 v236, v236, s62, v95
	v_med3_f32 v237, v237, s62, v95
	v_med3_f32 v238, v238, s62, v95
	v_med3_f32 v239, v239, s62, v95
	v_med3_f32 v240, v240, s62, v95
	v_med3_f32 v241, v241, s62, v95
	v_mov_b32_e32 v242, 0
	v_mov_b32_e32 v243, 0
	v_mov_b32_e32 v244, 0
	v_mov_b32_e32 v245, 0
	v_cvt_pk_fp8_f32 v242, v226, v227
	v_cvt_pk_fp8_f32 v243, v230, v231
	v_cvt_pk_fp8_f32 v244, v234, v235
	v_cvt_pk_fp8_f32 v245, v238, v239
	v_cvt_pk_fp8_f32 v242, v228, v229 op_sel:[0,0,1]
	v_cvt_pk_fp8_f32 v243, v232, v233 op_sel:[0,0,1]
	v_cvt_pk_fp8_f32 v244, v236, v237 op_sel:[0,0,1]
	v_cvt_pk_fp8_f32 v245, v240, v241 op_sel:[0,0,1]
	s_nop 0
	global_store_dwordx4 v77, v[242:245], s[6:7]
	ds_read_b32 v226, v213
	ds_read_b32 v227, v213 offset:512
	ds_read_b32 v228, v213 offset:1024
	ds_read_b32 v229, v213 offset:1536
	ds_read_b32 v230, v213 offset:2048
	ds_read_b32 v231, v213 offset:2560
	ds_read_b32 v232, v213 offset:3072
	ds_read_b32 v233, v213 offset:3584
	ds_read_b32 v234, v213 offset:4096
	ds_read_b32 v235, v213 offset:4608
	ds_read_b32 v236, v213 offset:5120
	ds_read_b32 v237, v213 offset:5632
	ds_read_b32 v238, v213 offset:6144
	ds_read_b32 v239, v213 offset:6656
	ds_read_b32 v240, v213 offset:7168
	ds_read_b32 v241, v213 offset:7680
	s_waitcnt lgkmcnt(0)
	v_max_f32_e32 v226, v226, v226
	v_max_f32_e32 v227, v227, v227
	v_max_f32_e32 v228, v228, v228
	v_max_f32_e32 v229, v229, v229
	v_max_f32_e32 v230, v230, v230
	v_max_f32_e32 v231, v231, v231
	v_max_f32_e32 v232, v232, v232
	v_max_f32_e32 v233, v233, v233
	v_max_f32_e32 v234, v234, v234
	v_max_f32_e32 v235, v235, v235
	v_max_f32_e32 v236, v236, v236
	v_max_f32_e32 v237, v237, v237
	v_max_f32_e32 v238, v238, v238
	v_max_f32_e32 v239, v239, v239
	v_max_f32_e32 v240, v240, v240
	v_max_f32_e32 v241, v241, v241
	v_med3_f32 v226, v226, s62, v95
	v_med3_f32 v227, v227, s62, v95
	v_med3_f32 v228, v228, s62, v95
	v_med3_f32 v229, v229, s62, v95
	v_med3_f32 v230, v230, s62, v95
	v_med3_f32 v231, v231, s62, v95
	v_med3_f32 v232, v232, s62, v95
	v_med3_f32 v233, v233, s62, v95
	v_med3_f32 v234, v234, s62, v95
	v_med3_f32 v235, v235, s62, v95
	v_med3_f32 v236, v236, s62, v95
	v_med3_f32 v237, v237, s62, v95
	v_med3_f32 v238, v238, s62, v95
	v_med3_f32 v239, v239, s62, v95
	v_med3_f32 v240, v240, s62, v95
	v_med3_f32 v241, v241, s62, v95
	v_mov_b32_e32 v242, 0
	v_mov_b32_e32 v243, 0
	v_mov_b32_e32 v244, 0
	v_mov_b32_e32 v245, 0
	v_cvt_pk_fp8_f32 v242, v226, v227
	v_cvt_pk_fp8_f32 v243, v230, v231
	v_cvt_pk_fp8_f32 v244, v234, v235
	v_cvt_pk_fp8_f32 v245, v238, v239
	v_cvt_pk_fp8_f32 v242, v228, v229 op_sel:[0,0,1]
	v_cvt_pk_fp8_f32 v243, v232, v233 op_sel:[0,0,1]
	v_cvt_pk_fp8_f32 v244, v236, v237 op_sel:[0,0,1]
	v_cvt_pk_fp8_f32 v245, v240, v241 op_sel:[0,0,1]
	s_nop 0
	global_store_dwordx4 v78, v[242:245], s[6:7]
	s_waitcnt vmcnt(12)
	v_mul_f32_e32 v176, v34, v176
	v_mul_f32_e32 v177, v34, v177
	v_mul_f32_e32 v178, v34, v178
	v_mul_f32_e32 v179, v34, v179
	ds_write_b128 v210, v[176:179]
	v_mul_f32_e32 v180, v35, v180
	v_mul_f32_e32 v181, v35, v181
	v_mul_f32_e32 v182, v35, v182
	v_mul_f32_e32 v183, v35, v183
	ds_write_b128 v210, v[180:183] offset:1024
	v_mul_f32_e32 v184, v36, v184
	v_mul_f32_e32 v185, v36, v185
	v_mul_f32_e32 v186, v36, v186
	v_mul_f32_e32 v187, v36, v187
	ds_write_b128 v210, v[184:187] offset:2048
	v_mul_f32_e32 v188, v37, v188
	v_mul_f32_e32 v189, v37, v189
	v_mul_f32_e32 v190, v37, v190
	v_mul_f32_e32 v191, v37, v191
	ds_write_b128 v210, v[188:191] offset:3072
	v_mul_f32_e32 v192, v38, v192
	v_mul_f32_e32 v193, v38, v193
	v_mul_f32_e32 v194, v38, v194
	v_mul_f32_e32 v195, v38, v195
	ds_write_b128 v210, v[192:195] offset:4096
	v_mul_f32_e32 v196, v39, v196
	v_mul_f32_e32 v197, v39, v197
	v_mul_f32_e32 v198, v39, v198
	v_mul_f32_e32 v199, v39, v199
	ds_write_b128 v210, v[196:199] offset:5120
	v_mul_f32_e32 v200, v40, v200
	v_mul_f32_e32 v201, v40, v201
	v_mul_f32_e32 v202, v40, v202
	v_mul_f32_e32 v203, v40, v203
	ds_write_b128 v210, v[200:203] offset:6144
	v_mul_f32_e32 v204, v41, v204
	v_mul_f32_e32 v205, v41, v205
	v_mul_f32_e32 v206, v41, v206
	v_mul_f32_e32 v207, v41, v207
	ds_write_b128 v210, v[204:207] offset:7168
	s_waitcnt lgkmcnt(0)
	s_barrier
; #define GAS __attribute__((address_space(1)))
; #define LAS __attribute__((address_space(3)))
; #define LDS_WAIT() asm volatile("s_waitcnt lgkmcnt(0)" ::: "memory")
; __device__ __forceinline__ unsigned pk4_fp8(float a, float b, float c, float d) {
;     a = fminf(fmaxf(a, -448.f), 448.f); b = fminf(fmaxf(b, -448.f), 448.f); c = fminf(fmaxf(c, -448.f), 448.f); d = fminf(fmaxf(d, -448.f), 448.f);
;     int w = __builtin_amdgcn_cvt_pk_fp8_f32(a, b, 0, false); w = __builtin_amdgcn_cvt_pk_fp8_f32(c, d, w, true); return (unsigned)w; }
;     ...
; #pragma unroll
;     for (int i = 0; i < 32; ++i) v[i] = sc >= 0 ? W[(size_t)(k0 + 2 * i + (lane >> 5)) * Nsrc + sc] : 0.f;
; #pragma unroll
;     for (int i = 0; i < 32; ++i) { const int k = k0 + 2 * i + (lane >> 5); float x = v[i] * wscale; if (KS) x *= (k < ksplit ? ksA[k] : ksB[k - ksplit]); scr[(2 * i + (lane >> 5)) * 33 + (lane & 31)] = x; }
;     LDS_WAIT(); asm volatile("" ::: "memory");
;     const int c = lane & 7;
; #pragma unroll
;     for (int j = 0; j < 4; ++j) { const int n = (lane >> 3) + 8 * j; const LAS float* s = scr + (8 * c) * 33 + n;
;         const unsigned long long o = (unsigned long long)pg8::pk4_fp8(s[0 * 33], s[1 * 33], s[2 * 33], s[3 * 33]) | ((unsigned long long)pg8::pk4_fp8(s[4 * 33], s[5 * 33], s[6 * 33], s[7 * 33]) << 32);
;         *(GAS unsigned long long*)(WT + (size_t)(n0 + n) * K + k0 + 8 * c) = o; }
	s_add_u32 s8, s34, 0x3000
	s_addc_u32 s9, s35, 0
	global_load_dwordx4 v[176:179], v74, s[8:9]
	s_add_u32 s8, s8, 0x20000
	s_addc_u32 s9, s9, 0
	global_load_dwordx4 v[180:183], v74, s[8:9]
	s_add_u32 s8, s8, 0x20000
	s_addc_u32 s9, s9, 0
	global_load_dwordx4 v[184:187], v74, s[8:9]
	s_add_u32 s8, s8, 0x20000
	s_addc_u32 s9, s9, 0
	global_load_dwordx4 v[188:191], v74, s[8:9]
	s_add_u32 s8, s8, 0x20000
	s_addc_u32 s9, s9, 0
	global_load_dwordx4 v[192:195], v74, s[8:9]
	s_add_u32 s8, s8, 0x20000
	s_addc_u32 s9, s9, 0
	global_load_dwordx4 v[196:199], v74, s[8:9]
	s_add_u32 s8, s8, 0x20000
	s_addc_u32 s9, s9, 0
	global_load_dwordx4 v[200:203], v74, s[8:9]
	s_add_u32 s8, s8, 0x20000
	s_addc_u32 s9, s9, 0
	global_load_dwordx4 v[204:207], v74, s[8:9]
	s_add_u32 s6, s36, 0x400000
	s_addc_u32 s7, s37, 0
	ds_read_b32 v226, v212
	ds_read_b32 v227, v212 offset:512
	ds_read_b32 v228, v212 offset:1024
	ds_read_b32 v229, v212 offset:1536
	ds_read_b32 v230, v212 offset:2048
	ds_read_b32 v231, v212 offset:2560
	ds_read_b32 v232, v212 offset:3072
	ds_read_b32 v233, v212 offset:3584
	ds_read_b32 v234, v212 offset:4096
	ds_read_b32 v235, v212 offset:4608
	ds_read_b32 v236, v212 offset:5120
	ds_read_b32 v237, v212 offset:5632
	ds_read_b32 v238, v212 offset:6144
	ds_read_b32 v239, v212 offset:6656
	ds_read_b32 v240, v212 offset:7168
	ds_read_b32 v241, v212 offset:7680
	s_waitcnt lgkmcnt(0)
	v_max_f32_e32 v226, v226, v226
	v_max_f32_e32 v227, v227, v227
	v_max_f32_e32 v228, v228, v228
	v_max_f32_e32 v229, v229, v229
	v_max_f32_e32 v230, v230, v230
	v_max_f32_e32 v231, v231, v231
	v_max_f32_e32 v232, v232, v232
	v_max_f32_e32 v233, v233, v233
	v_max_f32_e32 v234, v234, v234
	v_max_f32_e32 v235, v235, v235
	v_max_f32_e32 v236, v236, v236
	v_max_f32_e32 v237, v237, v237
	v_max_f32_e32 v238, v238, v238
	v_max_f32_e32 v239, v239, v239
	v_max_f32_e32 v240, v240, v240
	v_max_f32_e32 v241, v241, v241
	v_med3_f32 v226, v226, s62, v95
	v_med3_f32 v227, v227, s62, v95
	v_med3_f32 v228, v228, s62, v95
	v_med3_f32 v229, v229, s62, v95
	v_med3_f32 v230, v230, s62, v95
	v_med3_f32 v231, v231, s62, v95
	v_med3_f32 v232, v232, s62, v95
	v_med3_f32 v233, v233, s62, v95
	v_med3_f32 v234, v234, s62, v95
	v_med3_f32 v235, v235, s62, v95
	v_med3_f32 v236, v236, s62, v95
	v_med3_f32 v237, v237, s62, v95
	v_med3_f32 v238, v238, s62, v95
	v_med3_f32 v239, v239, s62, v95
	v_med3_f32 v240, v240, s62, v95
	v_med3_f32 v241, v241, s62, v95
	v_mov_b32_e32 v242, 0
	v_mov_b32_e32 v243, 0
	v_mov_b32_e32 v244, 0
	v_mov_b32_e32 v245, 0
	v_cvt_pk_fp8_f32 v242, v226, v227
	v_cvt_pk_fp8_f32 v243, v230, v231
	v_cvt_pk_fp8_f32 v244, v234, v235
	v_cvt_pk_fp8_f32 v245, v238, v239
	v_cvt_pk_fp8_f32 v242, v228, v229 op_sel:[0,0,1]
	v_cvt_pk_fp8_f32 v243, v232, v233 op_sel:[0,0,1]
	v_cvt_pk_fp8_f32 v244, v236, v237 op_sel:[0,0,1]
	v_cvt_pk_fp8_f32 v245, v240, v241 op_sel:[0,0,1]
	s_nop 0
	global_store_dwordx4 v77, v[242:245], s[6:7]
	ds_read_b32 v226, v214
	ds_read_b32 v227, v214 offset:512
	ds_read_b32 v228, v214 offset:1024
	ds_read_b32 v229, v214 offset:1536
	ds_read_b32 v230, v214 offset:2048
	ds_read_b32 v231, v214 offset:2560
	ds_read_b32 v232, v214 offset:3072
	ds_read_b32 v233, v214 offset:3584
	ds_read_b32 v234, v214 offset:4096
	ds_read_b32 v235, v214 offset:4608
	ds_read_b32 v236, v214 offset:5120
	ds_read_b32 v237, v214 offset:5632
	ds_read_b32 v238, v214 offset:6144
	ds_read_b32 v239, v214 offset:6656
	ds_read_b32 v240, v214 offset:7168
	ds_read_b32 v241, v214 offset:7680
	s_waitcnt lgkmcnt(0)
	v_max_f32_e32 v226, v226, v226
	v_max_f32_e32 v227, v227, v227
	v_max_f32_e32 v228, v228, v228
	v_max_f32_e32 v229, v229, v229
	v_max_f32_e32 v230, v230, v230
	v_max_f32_e32 v231, v231, v231
	v_max_f32_e32 v232, v232, v232
	v_max_f32_e32 v233, v233, v233
	v_max_f32_e32 v234, v234, v234
	v_max_f32_e32 v235, v235, v235
	v_max_f32_e32 v236, v236, v236
	v_max_f32_e32 v237, v237, v237
	v_max_f32_e32 v238, v238, v238
	v_max_f32_e32 v239, v239, v239
	v_max_f32_e32 v240, v240, v240
	v_max_f32_e32 v241, v241, v241
	v_med3_f32 v226, v226, s62, v95
	v_med3_f32 v227, v227, s62, v95
	v_med3_f32 v228, v228, s62, v95
	v_med3_f32 v229, v229, s62, v95
	v_med3_f32 v230, v230, s62, v95
	v_med3_f32 v231, v231, s62, v95
	v_med3_f32 v232, v232, s62, v95
	v_med3_f32 v233, v233, s62, v95
	v_med3_f32 v234, v234, s62, v95
	v_med3_f32 v235, v235, s62, v95
	v_med3_f32 v236, v236, s62, v95
	v_med3_f32 v237, v237, s62, v95
	v_med3_f32 v238, v238, s62, v95
	v_med3_f32 v239, v239, s62, v95
	v_med3_f32 v240, v240, s62, v95
	v_med3_f32 v241, v241, s62, v95
	v_mov_b32_e32 v242, 0
	v_mov_b32_e32 v243, 0
	v_mov_b32_e32 v244, 0
	v_mov_b32_e32 v245, 0
	v_cvt_pk_fp8_f32 v242, v226, v227
	v_cvt_pk_fp8_f32 v243, v230, v231
	v_cvt_pk_fp8_f32 v244, v234, v235
	v_cvt_pk_fp8_f32 v245, v238, v239
	v_cvt_pk_fp8_f32 v242, v228, v229 op_sel:[0,0,1]
	v_cvt_pk_fp8_f32 v243, v232, v233 op_sel:[0,0,1]
	v_cvt_pk_fp8_f32 v244, v236, v237 op_sel:[0,0,1]
	v_cvt_pk_fp8_f32 v245, v240, v241 op_sel:[0,0,1]
	s_nop 0
	global_store_dwordx4 v78, v[242:245], s[6:7]
	s_waitcnt vmcnt(12)
	v_mul_f32_e32 v144, v34, v144
	v_mul_f32_e32 v145, v34, v145
	v_mul_f32_e32 v146, v34, v146
	v_mul_f32_e32 v147, v34, v147
	ds_write_b128 v209, v[144:147]
	v_mul_f32_e32 v148, v35, v148
	v_mul_f32_e32 v149, v35, v149
	v_mul_f32_e32 v150, v35, v150
	v_mul_f32_e32 v151, v35, v151
	ds_write_b128 v209, v[148:151] offset:1024
	v_mul_f32_e32 v152, v36, v152
	v_mul_f32_e32 v153, v36, v153
	v_mul_f32_e32 v154, v36, v154
	v_mul_f32_e32 v155, v36, v155
	ds_write_b128 v209, v[152:155] offset:2048
	v_mul_f32_e32 v156, v37, v156
	v_mul_f32_e32 v157, v37, v157
	v_mul_f32_e32 v158, v37, v158
	v_mul_f32_e32 v159, v37, v159
	ds_write_b128 v209, v[156:159] offset:3072
	v_mul_f32_e32 v160, v38, v160
	v_mul_f32_e32 v161, v38, v161
	v_mul_f32_e32 v162, v38, v162
	v_mul_f32_e32 v163, v38, v163
	ds_write_b128 v209, v[160:163] offset:4096
	v_mul_f32_e32 v164, v39, v164
	v_mul_f32_e32 v165, v39, v165
	v_mul_f32_e32 v166, v39, v166
	v_mul_f32_e32 v167, v39, v167
	ds_write_b128 v209, v[164:167] offset:5120
	v_mul_f32_e32 v168, v40, v168
	v_mul_f32_e32 v169, v40, v169
	v_mul_f32_e32 v170, v40, v170
	v_mul_f32_e32 v171, v40, v171
	ds_write_b128 v209, v[168:171] offset:6144
	v_mul_f32_e32 v172, v41, v172
	v_mul_f32_e32 v173, v41, v173
	v_mul_f32_e32 v174, v41, v174
	v_mul_f32_e32 v175, v41, v175
	ds_write_b128 v209, v[172:175] offset:7168
	s_waitcnt lgkmcnt(0)
	s_barrier
; #define GAS __attribute__((address_space(1)))
; #define LAS __attribute__((address_space(3)))
; #define LDS_WAIT() asm volatile("s_waitcnt lgkmcnt(0)" ::: "memory")
; __device__ __forceinline__ unsigned pk4_fp8(float a, float b, float c, float d) {
;     a = fminf(fmaxf(a, -448.f), 448.f); b = fminf(fmaxf(b, -448.f), 448.f); c = fminf(fmaxf(c, -448.f), 448.f); d = fminf(fmaxf(d, -448.f), 448.f);
;     int w = __builtin_amdgcn_cvt_pk_fp8_f32(a, b, 0, false); w = __builtin_amdgcn_cvt_pk_fp8_f32(c, d, w, true); return (unsigned)w; }
;     ...
; #pragma unroll
;     for (int i = 0; i < 32; ++i) v[i] = sc >= 0 ? W[(size_t)(k0 + 2 * i + (lane >> 5)) * Nsrc + sc] : 0.f;
; #pragma unroll
;     for (int i = 0; i < 32; ++i) { const int k = k0 + 2 * i + (lane >> 5); float x = v[i] * wscale; if (KS) x *= (k < ksplit ? ksA[k] : ksB[k - ksplit]); scr[(2 * i + (lane >> 5)) * 33 + (lane & 31)] = x; }
;     LDS_WAIT(); asm volatile("" ::: "memory");
;     const int c = lane & 7;
; #pragma unroll
;     for (int j = 0; j < 4; ++j) { const int n = (lane >> 3) + 8 * j; const LAS float* s = scr + (8 * c) * 33 + n;
;         const unsigned long long o = (unsigned long long)pg8::pk4_fp8(s[0 * 33], s[1 * 33], s[2 * 33], s[3 * 33]) | ((unsigned long long)pg8::pk4_fp8(s[4 * 33], s[5 * 33], s[6 * 33], s[7 * 33]) << 32);
;         *(GAS unsigned long long*)(WT + (size_t)(n0 + n) * K + k0 + 8 * c) = o; }
	s_add_u32 s8, s34, 0x4000
	s_addc_u32 s9, s35, 0
	global_load_dwordx4 v[144:147], v74, s[8:9]
	s_add_u32 s8, s8, 0x20000
	s_addc_u32 s9, s9, 0
	global_load_dwordx4 v[148:151], v74, s[8:9]
	s_add_u32 s8, s8, 0x20000
	s_addc_u32 s9, s9, 0
	global_load_dwordx4 v[152:155], v74, s[8:9]
	s_add_u32 s8, s8, 0x20000
	s_addc_u32 s9, s9, 0
	global_load_dwordx4 v[156:159], v74, s[8:9]
	s_add_u32 s8, s8, 0x20000
	s_addc_u32 s9, s9, 0
	global_load_dwordx4 v[160:163], v74, s[8:9]
	s_add_u32 s8, s8, 0x20000
	s_addc_u32 s9, s9, 0
	global_load_dwordx4 v[164:167], v74, s[8:9]
	s_add_u32 s8, s8, 0x20000
	s_addc_u32 s9, s9, 0
	global_load_dwordx4 v[168:171], v74, s[8:9]
	s_add_u32 s8, s8, 0x20000
	s_addc_u32 s9, s9, 0
	global_load_dwordx4 v[172:175], v74, s[8:9]
	s_add_u32 s6, s36, 0x800000
	s_addc_u32 s7, s37, 0
	ds_read_b32 v226, v211
	ds_read_b32 v227, v211 offset:512
	ds_read_b32 v228, v211 offset:1024
	ds_read_b32 v229, v211 offset:1536
	ds_read_b32 v230, v211 offset:2048
	ds_read_b32 v231, v211 offset:2560
	ds_read_b32 v232, v211 offset:3072
	ds_read_b32 v233, v211 offset:3584
	ds_read_b32 v234, v211 offset:4096
	ds_read_b32 v235, v211 offset:4608
	ds_read_b32 v236, v211 offset:5120
	ds_read_b32 v237, v211 offset:5632
	ds_read_b32 v238, v211 offset:6144
	ds_read_b32 v239, v211 offset:6656
	ds_read_b32 v240, v211 offset:7168
	ds_read_b32 v241, v211 offset:7680
	s_waitcnt lgkmcnt(0)
	v_max_f32_e32 v226, v226, v226
	v_max_f32_e32 v227, v227, v227
	v_max_f32_e32 v228, v228, v228
	v_max_f32_e32 v229, v229, v229
	v_max_f32_e32 v230, v230, v230
	v_max_f32_e32 v231, v231, v231
	v_max_f32_e32 v232, v232, v232
	v_max_f32_e32 v233, v233, v233
	v_max_f32_e32 v234, v234, v234
	v_max_f32_e32 v235, v235, v235
	v_max_f32_e32 v236, v236, v236
	v_max_f32_e32 v237, v237, v237
	v_max_f32_e32 v238, v238, v238
	v_max_f32_e32 v239, v239, v239
	v_max_f32_e32 v240, v240, v240
	v_max_f32_e32 v241, v241, v241
	v_med3_f32 v226, v226, s62, v95
	v_med3_f32 v227, v227, s62, v95
	v_med3_f32 v228, v228, s62, v95
	v_med3_f32 v229, v229, s62, v95
	v_med3_f32 v230, v230, s62, v95
	v_med3_f32 v231, v231, s62, v95
	v_med3_f32 v232, v232, s62, v95
	v_med3_f32 v233, v233, s62, v95
	v_med3_f32 v234, v234, s62, v95
	v_med3_f32 v235, v235, s62, v95
	v_med3_f32 v236, v236, s62, v95
	v_med3_f32 v237, v237, s62, v95
	v_med3_f32 v238, v238, s62, v95
	v_med3_f32 v239, v239, s62, v95
	v_med3_f32 v240, v240, s62, v95
	v_med3_f32 v241, v241, s62, v95
	v_mov_b32_e32 v242, 0
	v_mov_b32_e32 v243, 0
	v_mov_b32_e32 v244, 0
	v_mov_b32_e32 v245, 0
	v_cvt_pk_fp8_f32 v242, v226, v227
	v_cvt_pk_fp8_f32 v243, v230, v231
	v_cvt_pk_fp8_f32 v244, v234, v235
	v_cvt_pk_fp8_f32 v245, v238, v239
	v_cvt_pk_fp8_f32 v242, v228, v229 op_sel:[0,0,1]
	v_cvt_pk_fp8_f32 v243, v232, v233 op_sel:[0,0,1]
	v_cvt_pk_fp8_f32 v244, v236, v237 op_sel:[0,0,1]
	v_cvt_pk_fp8_f32 v245, v240, v241 op_sel:[0,0,1]
	s_nop 0
	global_store_dwordx4 v77, v[242:245], s[6:7]
	ds_read_b32 v226, v213
	ds_read_b32 v227, v213 offset:512
	ds_read_b32 v228, v213 offset:1024
	ds_read_b32 v229, v213 offset:1536
	ds_read_b32 v230, v213 offset:2048
	ds_read_b32 v231, v213 offset:2560
	ds_read_b32 v232, v213 offset:3072
	ds_read_b32 v233, v213 offset:3584
	ds_read_b32 v234, v213 offset:4096
	ds_read_b32 v235, v213 offset:4608
	ds_read_b32 v236, v213 offset:5120
	ds_read_b32 v237, v213 offset:5632
	ds_read_b32 v238, v213 offset:6144
	ds_read_b32 v239, v213 offset:6656
	ds_read_b32 v240, v213 offset:7168
	ds_read_b32 v241, v213 offset:7680
	s_waitcnt lgkmcnt(0)
	v_max_f32_e32 v226, v226, v226
	v_max_f32_e32 v227, v227, v227
	v_max_f32_e32 v228, v228, v228
	v_max_f32_e32 v229, v229, v229
	v_max_f32_e32 v230, v230, v230
	v_max_f32_e32 v231, v231, v231
	v_max_f32_e32 v232, v232, v232
	v_max_f32_e32 v233, v233, v233
	v_max_f32_e32 v234, v234, v234
	v_max_f32_e32 v235, v235, v235
	v_max_f32_e32 v236, v236, v236
	v_max_f32_e32 v237, v237, v237
	v_max_f32_e32 v238, v238, v238
	v_max_f32_e32 v239, v239, v239
	v_max_f32_e32 v240, v240, v240
	v_max_f32_e32 v241, v241, v241
	v_med3_f32 v226, v226, s62, v95
	v_med3_f32 v227, v227, s62, v95
	v_med3_f32 v228, v228, s62, v95
	v_med3_f32 v229, v229, s62, v95
	v_med3_f32 v230, v230, s62, v95
	v_med3_f32 v231, v231, s62, v95
	v_med3_f32 v232, v232, s62, v95
	v_med3_f32 v233, v233, s62, v95
	v_med3_f32 v234, v234, s62, v95
	v_med3_f32 v235, v235, s62, v95
	v_med3_f32 v236, v236, s62, v95
	v_med3_f32 v237, v237, s62, v95
	v_med3_f32 v238, v238, s62, v95
	v_med3_f32 v239, v239, s62, v95
	v_med3_f32 v240, v240, s62, v95
	v_med3_f32 v241, v241, s62, v95
	v_mov_b32_e32 v242, 0
	v_mov_b32_e32 v243, 0
	v_mov_b32_e32 v244, 0
	v_mov_b32_e32 v245, 0
	v_cvt_pk_fp8_f32 v242, v226, v227
	v_cvt_pk_fp8_f32 v243, v230, v231
	v_cvt_pk_fp8_f32 v244, v234, v235
	v_cvt_pk_fp8_f32 v245, v238, v239
	v_cvt_pk_fp8_f32 v242, v228, v229 op_sel:[0,0,1]
	v_cvt_pk_fp8_f32 v243, v232, v233 op_sel:[0,0,1]
	v_cvt_pk_fp8_f32 v244, v236, v237 op_sel:[0,0,1]
	v_cvt_pk_fp8_f32 v245, v240, v241 op_sel:[0,0,1]
	s_nop 0
	global_store_dwordx4 v78, v[242:245], s[6:7]
	s_waitcnt vmcnt(12)
	v_mul_f32_e32 v176, v34, v176
	v_mul_f32_e32 v177, v34, v177
	v_mul_f32_e32 v178, v34, v178
	v_mul_f32_e32 v179, v34, v179
	ds_write_b128 v210, v[176:179]
	v_mul_f32_e32 v180, v35, v180
	v_mul_f32_e32 v181, v35, v181
	v_mul_f32_e32 v182, v35, v182
	v_mul_f32_e32 v183, v35, v183
	ds_write_b128 v210, v[180:183] offset:1024
	v_mul_f32_e32 v184, v36, v184
	v_mul_f32_e32 v185, v36, v185
	v_mul_f32_e32 v186, v36, v186
	v_mul_f32_e32 v187, v36, v187
	ds_write_b128 v210, v[184:187] offset:2048
	v_mul_f32_e32 v188, v37, v188
	v_mul_f32_e32 v189, v37, v189
	v_mul_f32_e32 v190, v37, v190
	v_mul_f32_e32 v191, v37, v191
	ds_write_b128 v210, v[188:191] offset:3072
	v_mul_f32_e32 v192, v38, v192
	v_mul_f32_e32 v193, v38, v193
	v_mul_f32_e32 v194, v38, v194
	v_mul_f32_e32 v195, v38, v195
	ds_write_b128 v210, v[192:195] offset:4096
	v_mul_f32_e32 v196, v39, v196
	v_mul_f32_e32 v197, v39, v197
	v_mul_f32_e32 v198, v39, v198
	v_mul_f32_e32 v199, v39, v199
	ds_write_b128 v210, v[196:199] offset:5120
	v_mul_f32_e32 v200, v40, v200
	v_mul_f32_e32 v201, v40, v201
	v_mul_f32_e32 v202, v40, v202
	v_mul_f32_e32 v203, v40, v203
	ds_write_b128 v210, v[200:203] offset:6144
	v_mul_f32_e32 v204, v41, v204
	v_mul_f32_e32 v205, v41, v205
	v_mul_f32_e32 v206, v41, v206
	v_mul_f32_e32 v207, v41, v207
	ds_write_b128 v210, v[204:207] offset:7168
	s_waitcnt lgkmcnt(0)
	s_barrier
; #define GAS __attribute__((address_space(1)))
; #define LAS __attribute__((address_space(3)))
; #define LDS_WAIT() asm volatile("s_waitcnt lgkmcnt(0)" ::: "memory")
; __device__ __forceinline__ unsigned pk4_fp8(float a, float b, float c, float d) {
;     a = fminf(fmaxf(a, -448.f), 448.f); b = fminf(fmaxf(b, -448.f), 448.f); c = fminf(fmaxf(c, -448.f), 448.f); d = fminf(fmaxf(d, -448.f), 448.f);
;     int w = __builtin_amdgcn_cvt_pk_fp8_f32(a, b, 0, false); w = __builtin_amdgcn_cvt_pk_fp8_f32(c, d, w, true); return (unsigned)w; }
;     ...
; #pragma unroll
;     for (int i = 0; i < 32; ++i) v[i] = sc >= 0 ? W[(size_t)(k0 + 2 * i + (lane >> 5)) * Nsrc + sc] : 0.f;
; #pragma unroll
;     for (int i = 0; i < 32; ++i) { const int k = k0 + 2 * i + (lane >> 5); float x = v[i] * wscale; if (KS) x *= (k < ksplit ? ksA[k] : ksB[k - ksplit]); scr[(2 * i + (lane >> 5)) * 33 + (lane & 31)] = x; }
;     LDS_WAIT(); asm volatile("" ::: "memory");
;     const int c = lane & 7;
; #pragma unroll
;     for (int j = 0; j < 4; ++j) { const int n = (lane >> 3) + 8 * j; const LAS float* s = scr + (8 * c) * 33 + n;
;         const unsigned long long o = (unsigned long long)pg8::pk4_fp8(s[0 * 33], s[1 * 33], s[2 * 33], s[3 * 33]) | ((unsigned long long)pg8::pk4_fp8(s[4 * 33], s[5 * 33], s[6 * 33], s[7 * 33]) << 32);
;         *(GAS unsigned long long*)(WT + (size_t)(n0 + n) * K + k0 + 8 * c) = o; }
	s_add_u32 s8, s34, 0x5000
	s_addc_u32 s9, s35, 0
	global_load_dwordx4 v[176:179], v74, s[8:9]
	s_add_u32 s8, s8, 0x20000
	s_addc_u32 s9, s9, 0
	global_load_dwordx4 v[180:183], v74, s[8:9]
	s_add_u32 s8, s8, 0x20000
	s_addc_u32 s9, s9, 0
	global_load_dwordx4 v[184:187], v74, s[8:9]
	s_add_u32 s8, s8, 0x20000
	s_addc_u32 s9, s9, 0
	global_load_dwordx4 v[188:191], v74, s[8:9]
	s_add_u32 s8, s8, 0x20000
	s_addc_u32 s9, s9, 0
	global_load_dwordx4 v[192:195], v74, s[8:9]
	s_add_u32 s8, s8, 0x20000
	s_addc_u32 s9, s9, 0
	global_load_dwordx4 v[196:199], v74, s[8:9]
	s_add_u32 s8, s8, 0x20000
	s_addc_u32 s9, s9, 0
	global_load_dwordx4 v[200:203], v74, s[8:9]
	s_add_u32 s8, s8, 0x20000
	s_addc_u32 s9, s9, 0
	global_load_dwordx4 v[204:207], v74, s[8:9]
	s_add_u32 s6, s36, 0xc00000
	s_addc_u32 s7, s37, 0
	ds_read_b32 v226, v212
	ds_read_b32 v227, v212 offset:512
	ds_read_b32 v228, v212 offset:1024
	ds_read_b32 v229, v212 offset:1536
	ds_read_b32 v230, v212 offset:2048
	ds_read_b32 v231, v212 offset:2560
	ds_read_b32 v232, v212 offset:3072
	ds_read_b32 v233, v212 offset:3584
	ds_read_b32 v234, v212 offset:4096
	ds_read_b32 v235, v212 offset:4608
	ds_read_b32 v236, v212 offset:5120
	ds_read_b32 v237, v212 offset:5632
	ds_read_b32 v238, v212 offset:6144
	ds_read_b32 v239, v212 offset:6656
	ds_read_b32 v240, v212 offset:7168
	ds_read_b32 v241, v212 offset:7680
	s_waitcnt lgkmcnt(0)
	v_max_f32_e32 v226, v226, v226
	v_max_f32_e32 v227, v227, v227
	v_max_f32_e32 v228, v228, v228
	v_max_f32_e32 v229, v229, v229
	v_max_f32_e32 v230, v230, v230
	v_max_f32_e32 v231, v231, v231
	v_max_f32_e32 v232, v232, v232
	v_max_f32_e32 v233, v233, v233
	v_max_f32_e32 v234, v234, v234
	v_max_f32_e32 v235, v235, v235
	v_max_f32_e32 v236, v236, v236
	v_max_f32_e32 v237, v237, v237
	v_max_f32_e32 v238, v238, v238
	v_max_f32_e32 v239, v239, v239
	v_max_f32_e32 v240, v240, v240
	v_max_f32_e32 v241, v241, v241
	v_med3_f32 v226, v226, s62, v95
	v_med3_f32 v227, v227, s62, v95
	v_med3_f32 v228, v228, s62, v95
	v_med3_f32 v229, v229, s62, v95
	v_med3_f32 v230, v230, s62, v95
	v_med3_f32 v231, v231, s62, v95
	v_med3_f32 v232, v232, s62, v95
	v_med3_f32 v233, v233, s62, v95
	v_med3_f32 v234, v234, s62, v95
	v_med3_f32 v235, v235, s62, v95
	v_med3_f32 v236, v236, s62, v95
	v_med3_f32 v237, v237, s62, v95
	v_med3_f32 v238, v238, s62, v95
	v_med3_f32 v239, v239, s62, v95
	v_med3_f32 v240, v240, s62, v95
	v_med3_f32 v241, v241, s62, v95
	v_mov_b32_e32 v242, 0
	v_mov_b32_e32 v243, 0
	v_mov_b32_e32 v244, 0
	v_mov_b32_e32 v245, 0
	v_cvt_pk_fp8_f32 v242, v226, v227
	v_cvt_pk_fp8_f32 v243, v230, v231
	v_cvt_pk_fp8_f32 v244, v234, v235
	v_cvt_pk_fp8_f32 v245, v238, v239
	v_cvt_pk_fp8_f32 v242, v228, v229 op_sel:[0,0,1]
	v_cvt_pk_fp8_f32 v243, v232, v233 op_sel:[0,0,1]
	v_cvt_pk_fp8_f32 v244, v236, v237 op_sel:[0,0,1]
	v_cvt_pk_fp8_f32 v245, v240, v241 op_sel:[0,0,1]
	s_nop 0
	global_store_dwordx4 v77, v[242:245], s[6:7]
	ds_read_b32 v226, v214
	ds_read_b32 v227, v214 offset:512
	ds_read_b32 v228, v214 offset:1024
	ds_read_b32 v229, v214 offset:1536
	ds_read_b32 v230, v214 offset:2048
	ds_read_b32 v231, v214 offset:2560
	ds_read_b32 v232, v214 offset:3072
	ds_read_b32 v233, v214 offset:3584
	ds_read_b32 v234, v214 offset:4096
	ds_read_b32 v235, v214 offset:4608
	ds_read_b32 v236, v214 offset:5120
	ds_read_b32 v237, v214 offset:5632
	ds_read_b32 v238, v214 offset:6144
	ds_read_b32 v239, v214 offset:6656
	ds_read_b32 v240, v214 offset:7168
	ds_read_b32 v241, v214 offset:7680
	s_waitcnt lgkmcnt(0)
	v_max_f32_e32 v226, v226, v226
	v_max_f32_e32 v227, v227, v227
	v_max_f32_e32 v228, v228, v228
	v_max_f32_e32 v229, v229, v229
	v_max_f32_e32 v230, v230, v230
	v_max_f32_e32 v231, v231, v231
	v_max_f32_e32 v232, v232, v232
	v_max_f32_e32 v233, v233, v233
	v_max_f32_e32 v234, v234, v234
	v_max_f32_e32 v235, v235, v235
	v_max_f32_e32 v236, v236, v236
	v_max_f32_e32 v237, v237, v237
	v_max_f32_e32 v238, v238, v238
	v_max_f32_e32 v239, v239, v239
	v_max_f32_e32 v240, v240, v240
	v_max_f32_e32 v241, v241, v241
	v_med3_f32 v226, v226, s62, v95
	v_med3_f32 v227, v227, s62, v95
	v_med3_f32 v228, v228, s62, v95
	v_med3_f32 v229, v229, s62, v95
	v_med3_f32 v230, v230, s62, v95
	v_med3_f32 v231, v231, s62, v95
	v_med3_f32 v232, v232, s62, v95
	v_med3_f32 v233, v233, s62, v95
	v_med3_f32 v234, v234, s62, v95
	v_med3_f32 v235, v235, s62, v95
	v_med3_f32 v236, v236, s62, v95
	v_med3_f32 v237, v237, s62, v95
	v_med3_f32 v238, v238, s62, v95
	v_med3_f32 v239, v239, s62, v95
	v_med3_f32 v240, v240, s62, v95
	v_med3_f32 v241, v241, s62, v95
	v_mov_b32_e32 v242, 0
	v_mov_b32_e32 v243, 0
	v_mov_b32_e32 v244, 0
	v_mov_b32_e32 v245, 0
	v_cvt_pk_fp8_f32 v242, v226, v227
	v_cvt_pk_fp8_f32 v243, v230, v231
	v_cvt_pk_fp8_f32 v244, v234, v235
	v_cvt_pk_fp8_f32 v245, v238, v239
	v_cvt_pk_fp8_f32 v242, v228, v229 op_sel:[0,0,1]
	v_cvt_pk_fp8_f32 v243, v232, v233 op_sel:[0,0,1]
	v_cvt_pk_fp8_f32 v244, v236, v237 op_sel:[0,0,1]
	v_cvt_pk_fp8_f32 v245, v240, v241 op_sel:[0,0,1]
	s_nop 0
	global_store_dwordx4 v78, v[242:245], s[6:7]
	s_waitcnt vmcnt(12)
	v_mul_f32_e32 v144, v34, v144
	v_mul_f32_e32 v145, v34, v145
	v_mul_f32_e32 v146, v34, v146
	v_mul_f32_e32 v147, v34, v147
	ds_write_b128 v209, v[144:147]
	v_mul_f32_e32 v148, v35, v148
	v_mul_f32_e32 v149, v35, v149
	v_mul_f32_e32 v150, v35, v150
	v_mul_f32_e32 v151, v35, v151
	ds_write_b128 v209, v[148:151] offset:1024
	v_mul_f32_e32 v152, v36, v152
	v_mul_f32_e32 v153, v36, v153
	v_mul_f32_e32 v154, v36, v154
	v_mul_f32_e32 v155, v36, v155
	ds_write_b128 v209, v[152:155] offset:2048
	v_mul_f32_e32 v156, v37, v156
	v_mul_f32_e32 v157, v37, v157
	v_mul_f32_e32 v158, v37, v158
	v_mul_f32_e32 v159, v37, v159
	ds_write_b128 v209, v[156:159] offset:3072
	v_mul_f32_e32 v160, v38, v160
	v_mul_f32_e32 v161, v38, v161
	v_mul_f32_e32 v162, v38, v162
	v_mul_f32_e32 v163, v38, v163
	ds_write_b128 v209, v[160:163] offset:4096
	v_mul_f32_e32 v164, v39, v164
	v_mul_f32_e32 v165, v39, v165
	v_mul_f32_e32 v166, v39, v166
	v_mul_f32_e32 v167, v39, v167
	ds_write_b128 v209, v[164:167] offset:5120
	v_mul_f32_e32 v168, v40, v168
	v_mul_f32_e32 v169, v40, v169
	v_mul_f32_e32 v170, v40, v170
	v_mul_f32_e32 v171, v40, v171
	ds_write_b128 v209, v[168:171] offset:6144
	v_mul_f32_e32 v172, v41, v172
	v_mul_f32_e32 v173, v41, v173
	v_mul_f32_e32 v174, v41, v174
	v_mul_f32_e32 v175, v41, v175
	ds_write_b128 v209, v[172:175] offset:7168
	s_waitcnt lgkmcnt(0)
	s_barrier
; #define GAS __attribute__((address_space(1)))
; #define LAS __attribute__((address_space(3)))
; #define LDS_WAIT() asm volatile("s_waitcnt lgkmcnt(0)" ::: "memory")
; __device__ __forceinline__ unsigned pk4_fp8(float a, float b, float c, float d) {
;     a = fminf(fmaxf(a, -448.f), 448.f); b = fminf(fmaxf(b, -448.f), 448.f); c = fminf(fmaxf(c, -448.f), 448.f); d = fminf(fmaxf(d, -448.f), 448.f);
;     int w = __builtin_amdgcn_cvt_pk_fp8_f32(a, b, 0, false); w = __builtin_amdgcn_cvt_pk_fp8_f32(c, d, w, true); return (unsigned)w; }
;     ...
; #pragma unroll
;     for (int i = 0; i < 32; ++i) v[i] = sc >= 0 ? W[(size_t)(k0 + 2 * i + (lane >> 5)) * Nsrc + sc] : 0.f;
; #pragma unroll
;     for (int i = 0; i < 32; ++i) { const int k = k0 + 2 * i + (lane >> 5); float x = v[i] * wscale; if (KS) x *= (k < ksplit ? ksA[k] : ksB[k - ksplit]); scr[(2 * i + (lane >> 5)) * 33 + (lane & 31)] = x; }
;     LDS_WAIT(); asm volatile("" ::: "memory");
;     const int c = lane & 7;
; #pragma unroll
;     for (int j = 0; j < 4; ++j) { const int n = (lane >> 3) + 8 * j; const LAS float* s = scr + (8 * c) * 33 + n;
;         const unsigned long long o = (unsigned long long)pg8::pk4_fp8(s[0 * 33], s[1 * 33], s[2 * 33], s[3 * 33]) | ((unsigned long long)pg8::pk4_fp8(s[4 * 33], s[5 * 33], s[6 * 33], s[7 * 33]) << 32);
;         *(GAS unsigned long long*)(WT + (size_t)(n0 + n) * K + k0 + 8 * c) = o; }
	s_add_u32 s8, s34, 0x6000
	s_addc_u32 s9, s35, 0
	global_load_dwordx4 v[144:147], v74, s[8:9]
	s_add_u32 s8, s8, 0x20000
	s_addc_u32 s9, s9, 0
	global_load_dwordx4 v[148:151], v74, s[8:9]
	s_add_u32 s8, s8, 0x20000
	s_addc_u32 s9, s9, 0
	global_load_dwordx4 v[152:155], v74, s[8:9]
	s_add_u32 s8, s8, 0x20000
	s_addc_u32 s9, s9, 0
	global_load_dwordx4 v[156:159], v74, s[8:9]
	s_add_u32 s8, s8, 0x20000
	s_addc_u32 s9, s9, 0
	global_load_dwordx4 v[160:163], v74, s[8:9]
	s_add_u32 s8, s8, 0x20000
	s_addc_u32 s9, s9, 0
	global_load_dwordx4 v[164:167], v74, s[8:9]
	s_add_u32 s8, s8, 0x20000
	s_addc_u32 s9, s9, 0
	global_load_dwordx4 v[168:171], v74, s[8:9]
	s_add_u32 s8, s8, 0x20000
	s_addc_u32 s9, s9, 0
	global_load_dwordx4 v[172:175], v74, s[8:9]
	s_add_u32 s6, s36, 0x1000000
	s_addc_u32 s7, s37, 0
	ds_read_b32 v226, v211
	ds_read_b32 v227, v211 offset:512
	ds_read_b32 v228, v211 offset:1024
	ds_read_b32 v229, v211 offset:1536
	ds_read_b32 v230, v211 offset:2048
	ds_read_b32 v231, v211 offset:2560
	ds_read_b32 v232, v211 offset:3072
	ds_read_b32 v233, v211 offset:3584
	ds_read_b32 v234, v211 offset:4096
	ds_read_b32 v235, v211 offset:4608
	ds_read_b32 v236, v211 offset:5120
	ds_read_b32 v237, v211 offset:5632
	ds_read_b32 v238, v211 offset:6144
	ds_read_b32 v239, v211 offset:6656
	ds_read_b32 v240, v211 offset:7168
	ds_read_b32 v241, v211 offset:7680
	s_waitcnt lgkmcnt(0)
	v_max_f32_e32 v226, v226, v226
	v_max_f32_e32 v227, v227, v227
	v_max_f32_e32 v228, v228, v228
	v_max_f32_e32 v229, v229, v229
	v_max_f32_e32 v230, v230, v230
	v_max_f32_e32 v231, v231, v231
	v_max_f32_e32 v232, v232, v232
	v_max_f32_e32 v233, v233, v233
	v_max_f32_e32 v234, v234, v234
	v_max_f32_e32 v235, v235, v235
	v_max_f32_e32 v236, v236, v236
	v_max_f32_e32 v237, v237, v237
	v_max_f32_e32 v238, v238, v238
	v_max_f32_e32 v239, v239, v239
	v_max_f32_e32 v240, v240, v240
	v_max_f32_e32 v241, v241, v241
	v_med3_f32 v226, v226, s62, v95
	v_med3_f32 v227, v227, s62, v95
	v_med3_f32 v228, v228, s62, v95
	v_med3_f32 v229, v229, s62, v95
	v_med3_f32 v230, v230, s62, v95
	v_med3_f32 v231, v231, s62, v95
	v_med3_f32 v232, v232, s62, v95
	v_med3_f32 v233, v233, s62, v95
	v_med3_f32 v234, v234, s62, v95
	v_med3_f32 v235, v235, s62, v95
	v_med3_f32 v236, v236, s62, v95
	v_med3_f32 v237, v237, s62, v95
	v_med3_f32 v238, v238, s62, v95
	v_med3_f32 v239, v239, s62, v95
	v_med3_f32 v240, v240, s62, v95
	v_med3_f32 v241, v241, s62, v95
	v_mov_b32_e32 v242, 0
	v_mov_b32_e32 v243, 0
	v_mov_b32_e32 v244, 0
	v_mov_b32_e32 v245, 0
	v_cvt_pk_fp8_f32 v242, v226, v227
	v_cvt_pk_fp8_f32 v243, v230, v231
	v_cvt_pk_fp8_f32 v244, v234, v235
	v_cvt_pk_fp8_f32 v245, v238, v239
	v_cvt_pk_fp8_f32 v242, v228, v229 op_sel:[0,0,1]
	v_cvt_pk_fp8_f32 v243, v232, v233 op_sel:[0,0,1]
	v_cvt_pk_fp8_f32 v244, v236, v237 op_sel:[0,0,1]
	v_cvt_pk_fp8_f32 v245, v240, v241 op_sel:[0,0,1]
	s_nop 0
	global_store_dwordx4 v77, v[242:245], s[6:7]
	ds_read_b32 v226, v213
	ds_read_b32 v227, v213 offset:512
	ds_read_b32 v228, v213 offset:1024
	ds_read_b32 v229, v213 offset:1536
	ds_read_b32 v230, v213 offset:2048
	ds_read_b32 v231, v213 offset:2560
	ds_read_b32 v232, v213 offset:3072
	ds_read_b32 v233, v213 offset:3584
	ds_read_b32 v234, v213 offset:4096
	ds_read_b32 v235, v213 offset:4608
	ds_read_b32 v236, v213 offset:5120
	ds_read_b32 v237, v213 offset:5632
	ds_read_b32 v238, v213 offset:6144
	ds_read_b32 v239, v213 offset:6656
	ds_read_b32 v240, v213 offset:7168
	ds_read_b32 v241, v213 offset:7680
	s_waitcnt lgkmcnt(0)
	v_max_f32_e32 v226, v226, v226
	v_max_f32_e32 v227, v227, v227
	v_max_f32_e32 v228, v228, v228
	v_max_f32_e32 v229, v229, v229
	v_max_f32_e32 v230, v230, v230
	v_max_f32_e32 v231, v231, v231
	v_max_f32_e32 v232, v232, v232
	v_max_f32_e32 v233, v233, v233
	v_max_f32_e32 v234, v234, v234
	v_max_f32_e32 v235, v235, v235
	v_max_f32_e32 v236, v236, v236
	v_max_f32_e32 v237, v237, v237
	v_max_f32_e32 v238, v238, v238
	v_max_f32_e32 v239, v239, v239
	v_max_f32_e32 v240, v240, v240
	v_max_f32_e32 v241, v241, v241
	v_med3_f32 v226, v226, s62, v95
	v_med3_f32 v227, v227, s62, v95
	v_med3_f32 v228, v228, s62, v95
	v_med3_f32 v229, v229, s62, v95
	v_med3_f32 v230, v230, s62, v95
	v_med3_f32 v231, v231, s62, v95
	v_med3_f32 v232, v232, s62, v95
	v_med3_f32 v233, v233, s62, v95
	v_med3_f32 v234, v234, s62, v95
	v_med3_f32 v235, v235, s62, v95
	v_med3_f32 v236, v236, s62, v95
	v_med3_f32 v237, v237, s62, v95
	v_med3_f32 v238, v238, s62, v95
	v_med3_f32 v239, v239, s62, v95
	v_med3_f32 v240, v240, s62, v95
	v_med3_f32 v241, v241, s62, v95
	v_mov_b32_e32 v242, 0
	v_mov_b32_e32 v243, 0
	v_mov_b32_e32 v244, 0
	v_mov_b32_e32 v245, 0
	v_cvt_pk_fp8_f32 v242, v226, v227
	v_cvt_pk_fp8_f32 v243, v230, v231
	v_cvt_pk_fp8_f32 v244, v234, v235
	v_cvt_pk_fp8_f32 v245, v238, v239
	v_cvt_pk_fp8_f32 v242, v228, v229 op_sel:[0,0,1]
	v_cvt_pk_fp8_f32 v243, v232, v233 op_sel:[0,0,1]
	v_cvt_pk_fp8_f32 v244, v236, v237 op_sel:[0,0,1]
	v_cvt_pk_fp8_f32 v245, v240, v241 op_sel:[0,0,1]
	s_nop 0
	global_store_dwordx4 v78, v[242:245], s[6:7]
	s_waitcnt vmcnt(12)
	v_mul_f32_e32 v176, v34, v176
	v_mul_f32_e32 v177, v34, v177
	v_mul_f32_e32 v178, v34, v178
	v_mul_f32_e32 v179, v34, v179
	ds_write_b128 v210, v[176:179]
	v_mul_f32_e32 v180, v35, v180
	v_mul_f32_e32 v181, v35, v181
	v_mul_f32_e32 v182, v35, v182
	v_mul_f32_e32 v183, v35, v183
	ds_write_b128 v210, v[180:183] offset:1024
	v_mul_f32_e32 v184, v36, v184
	v_mul_f32_e32 v185, v36, v185
	v_mul_f32_e32 v186, v36, v186
	v_mul_f32_e32 v187, v36, v187
	ds_write_b128 v210, v[184:187] offset:2048
	v_mul_f32_e32 v188, v37, v188
	v_mul_f32_e32 v189, v37, v189
	v_mul_f32_e32 v190, v37, v190
	v_mul_f32_e32 v191, v37, v191
	ds_write_b128 v210, v[188:191] offset:3072
	v_mul_f32_e32 v192, v38, v192
	v_mul_f32_e32 v193, v38, v193
	v_mul_f32_e32 v194, v38, v194
	v_mul_f32_e32 v195, v38, v195
	ds_write_b128 v210, v[192:195] offset:4096
	v_mul_f32_e32 v196, v39, v196
	v_mul_f32_e32 v197, v39, v197
	v_mul_f32_e32 v198, v39, v198
	v_mul_f32_e32 v199, v39, v199
	ds_write_b128 v210, v[196:199] offset:5120
	v_mul_f32_e32 v200, v40, v200
	v_mul_f32_e32 v201, v40, v201
	v_mul_f32_e32 v202, v40, v202
	v_mul_f32_e32 v203, v40, v203
	ds_write_b128 v210, v[200:203] offset:6144
	v_mul_f32_e32 v204, v41, v204
	v_mul_f32_e32 v205, v41, v205
	v_mul_f32_e32 v206, v41, v206
	v_mul_f32_e32 v207, v41, v207
	ds_write_b128 v210, v[204:207] offset:7168
	s_waitcnt lgkmcnt(0)
	s_barrier
; #define GAS __attribute__((address_space(1)))
; #define LAS __attribute__((address_space(3)))
; #define LDS_WAIT() asm volatile("s_waitcnt lgkmcnt(0)" ::: "memory")
; __device__ __forceinline__ unsigned pk4_fp8(float a, float b, float c, float d) {
;     a = fminf(fmaxf(a, -448.f), 448.f); b = fminf(fmaxf(b, -448.f), 448.f); c = fminf(fmaxf(c, -448.f), 448.f); d = fminf(fmaxf(d, -448.f), 448.f);
;     int w = __builtin_amdgcn_cvt_pk_fp8_f32(a, b, 0, false); w = __builtin_amdgcn_cvt_pk_fp8_f32(c, d, w, true); return (unsigned)w; }
;     ...
; #pragma unroll
;     for (int i = 0; i < 32; ++i) v[i] = sc >= 0 ? W[(size_t)(k0 + 2 * i + (lane >> 5)) * Nsrc + sc] : 0.f;
; #pragma unroll
;     for (int i = 0; i < 32; ++i) { const int k = k0 + 2 * i + (lane >> 5); float x = v[i] * wscale; if (KS) x *= (k < ksplit ? ksA[k] : ksB[k - ksplit]); scr[(2 * i + (lane >> 5)) * 33 + (lane & 31)] = x; }
;     LDS_WAIT(); asm volatile("" ::: "memory");
;     const int c = lane & 7;
; #pragma unroll
;     for (int j = 0; j < 4; ++j) { const int n = (lane >> 3) + 8 * j; const LAS float* s = scr + (8 * c) * 33 + n;
;         const unsigned long long o = (unsigned long long)pg8::pk4_fp8(s[0 * 33], s[1 * 33], s[2 * 33], s[3 * 33]) | ((unsigned long long)pg8::pk4_fp8(s[4 * 33], s[5 * 33], s[6 * 33], s[7 * 33]) << 32);
;         *(GAS unsigned long long*)(WT + (size_t)(n0 + n) * K + k0 + 8 * c) = o; }
	s_add_u32 s8, s34, 0x7000
	s_addc_u32 s9, s35, 0
	global_load_dwordx4 v[176:179], v74, s[8:9]
	s_add_u32 s8, s8, 0x20000
	s_addc_u32 s9, s9, 0
	global_load_dwordx4 v[180:183], v74, s[8:9]
	s_add_u32 s8, s8, 0x20000
	s_addc_u32 s9, s9, 0
	global_load_dwordx4 v[184:187], v74, s[8:9]
	s_add_u32 s8, s8, 0x20000
	s_addc_u32 s9, s9, 0
	global_load_dwordx4 v[188:191], v74, s[8:9]
	s_add_u32 s8, s8, 0x20000
	s_addc_u32 s9, s9, 0
	global_load_dwordx4 v[192:195], v74, s[8:9]
	s_add_u32 s8, s8, 0x20000
	s_addc_u32 s9, s9, 0
	global_load_dwordx4 v[196:199], v74, s[8:9]
	s_add_u32 s8, s8, 0x20000
	s_addc_u32 s9, s9, 0
	global_load_dwordx4 v[200:203], v74, s[8:9]
	s_add_u32 s8, s8, 0x20000
	s_addc_u32 s9, s9, 0
	global_load_dwordx4 v[204:207], v74, s[8:9]
	s_add_u32 s6, s36, 0x1400000
	s_addc_u32 s7, s37, 0
	ds_read_b32 v226, v212
	ds_read_b32 v227, v212 offset:512
	ds_read_b32 v228, v212 offset:1024
	ds_read_b32 v229, v212 offset:1536
	ds_read_b32 v230, v212 offset:2048
	ds_read_b32 v231, v212 offset:2560
	ds_read_b32 v232, v212 offset:3072
	ds_read_b32 v233, v212 offset:3584
	ds_read_b32 v234, v212 offset:4096
	ds_read_b32 v235, v212 offset:4608
	ds_read_b32 v236, v212 offset:5120
	ds_read_b32 v237, v212 offset:5632
	ds_read_b32 v238, v212 offset:6144
	ds_read_b32 v239, v212 offset:6656
	ds_read_b32 v240, v212 offset:7168
	ds_read_b32 v241, v212 offset:7680
	s_waitcnt lgkmcnt(0)
	v_max_f32_e32 v226, v226, v226
	v_max_f32_e32 v227, v227, v227
	v_max_f32_e32 v228, v228, v228
	v_max_f32_e32 v229, v229, v229
	v_max_f32_e32 v230, v230, v230
	v_max_f32_e32 v231, v231, v231
	v_max_f32_e32 v232, v232, v232
	v_max_f32_e32 v233, v233, v233
	v_max_f32_e32 v234, v234, v234
	v_max_f32_e32 v235, v235, v235
	v_max_f32_e32 v236, v236, v236
	v_max_f32_e32 v237, v237, v237
	v_max_f32_e32 v238, v238, v238
	v_max_f32_e32 v239, v239, v239
	v_max_f32_e32 v240, v240, v240
	v_max_f32_e32 v241, v241, v241
	v_med3_f32 v226, v226, s62, v95
	v_med3_f32 v227, v227, s62, v95
	v_med3_f32 v228, v228, s62, v95
	v_med3_f32 v229, v229, s62, v95
	v_med3_f32 v230, v230, s62, v95
	v_med3_f32 v231, v231, s62, v95
	v_med3_f32 v232, v232, s62, v95
	v_med3_f32 v233, v233, s62, v95
	v_med3_f32 v234, v234, s62, v95
	v_med3_f32 v235, v235, s62, v95
	v_med3_f32 v236, v236, s62, v95
	v_med3_f32 v237, v237, s62, v95
	v_med3_f32 v238, v238, s62, v95
	v_med3_f32 v239, v239, s62, v95
	v_med3_f32 v240, v240, s62, v95
	v_med3_f32 v241, v241, s62, v95
	v_mov_b32_e32 v242, 0
	v_mov_b32_e32 v243, 0
	v_mov_b32_e32 v244, 0
	v_mov_b32_e32 v245, 0
	v_cvt_pk_fp8_f32 v242, v226, v227
	v_cvt_pk_fp8_f32 v243, v230, v231
	v_cvt_pk_fp8_f32 v244, v234, v235
	v_cvt_pk_fp8_f32 v245, v238, v239
	v_cvt_pk_fp8_f32 v242, v228, v229 op_sel:[0,0,1]
	v_cvt_pk_fp8_f32 v243, v232, v233 op_sel:[0,0,1]
	v_cvt_pk_fp8_f32 v244, v236, v237 op_sel:[0,0,1]
	v_cvt_pk_fp8_f32 v245, v240, v241 op_sel:[0,0,1]
	s_nop 0
	global_store_dwordx4 v77, v[242:245], s[6:7]
	ds_read_b32 v226, v214
	ds_read_b32 v227, v214 offset:512
	ds_read_b32 v228, v214 offset:1024
	ds_read_b32 v229, v214 offset:1536
	ds_read_b32 v230, v214 offset:2048
	ds_read_b32 v231, v214 offset:2560
	ds_read_b32 v232, v214 offset:3072
	ds_read_b32 v233, v214 offset:3584
	ds_read_b32 v234, v214 offset:4096
	ds_read_b32 v235, v214 offset:4608
	ds_read_b32 v236, v214 offset:5120
	ds_read_b32 v237, v214 offset:5632
	ds_read_b32 v238, v214 offset:6144
	ds_read_b32 v239, v214 offset:6656
	ds_read_b32 v240, v214 offset:7168
	ds_read_b32 v241, v214 offset:7680
	s_waitcnt lgkmcnt(0)
	v_max_f32_e32 v226, v226, v226
	v_max_f32_e32 v227, v227, v227
	v_max_f32_e32 v228, v228, v228
	v_max_f32_e32 v229, v229, v229
	v_max_f32_e32 v230, v230, v230
	v_max_f32_e32 v231, v231, v231
	v_max_f32_e32 v232, v232, v232
	v_max_f32_e32 v233, v233, v233
	v_max_f32_e32 v234, v234, v234
	v_max_f32_e32 v235, v235, v235
	v_max_f32_e32 v236, v236, v236
	v_max_f32_e32 v237, v237, v237
	v_max_f32_e32 v238, v238, v238
	v_max_f32_e32 v239, v239, v239
	v_max_f32_e32 v240, v240, v240
	v_max_f32_e32 v241, v241, v241
	v_med3_f32 v226, v226, s62, v95
	v_med3_f32 v227, v227, s62, v95
	v_med3_f32 v228, v228, s62, v95
	v_med3_f32 v229, v229, s62, v95
	v_med3_f32 v230, v230, s62, v95
	v_med3_f32 v231, v231, s62, v95
	v_med3_f32 v232, v232, s62, v95
	v_med3_f32 v233, v233, s62, v95
	v_med3_f32 v234, v234, s62, v95
	v_med3_f32 v235, v235, s62, v95
	v_med3_f32 v236, v236, s62, v95
	v_med3_f32 v237, v237, s62, v95
	v_med3_f32 v238, v238, s62, v95
	v_med3_f32 v239, v239, s62, v95
	v_med3_f32 v240, v240, s62, v95
	v_med3_f32 v241, v241, s62, v95
	v_mov_b32_e32 v242, 0
	v_mov_b32_e32 v243, 0
	v_mov_b32_e32 v244, 0
	v_mov_b32_e32 v245, 0
	v_cvt_pk_fp8_f32 v242, v226, v227
	v_cvt_pk_fp8_f32 v243, v230, v231
	v_cvt_pk_fp8_f32 v244, v234, v235
	v_cvt_pk_fp8_f32 v245, v238, v239
	v_cvt_pk_fp8_f32 v242, v228, v229 op_sel:[0,0,1]
	v_cvt_pk_fp8_f32 v243, v232, v233 op_sel:[0,0,1]
	v_cvt_pk_fp8_f32 v244, v236, v237 op_sel:[0,0,1]
	v_cvt_pk_fp8_f32 v245, v240, v241 op_sel:[0,0,1]
	s_nop 0
	global_store_dwordx4 v78, v[242:245], s[6:7]
	s_waitcnt vmcnt(12)
	v_mul_f32_e32 v144, v34, v144
	v_mul_f32_e32 v145, v34, v145
	v_mul_f32_e32 v146, v34, v146
	v_mul_f32_e32 v147, v34, v147
	ds_write_b128 v209, v[144:147]
	v_mul_f32_e32 v148, v35, v148
	v_mul_f32_e32 v149, v35, v149
	v_mul_f32_e32 v150, v35, v150
	v_mul_f32_e32 v151, v35, v151
	ds_write_b128 v209, v[148:151] offset:1024
	v_mul_f32_e32 v152, v36, v152
	v_mul_f32_e32 v153, v36, v153
	v_mul_f32_e32 v154, v36, v154
	v_mul_f32_e32 v155, v36, v155
	ds_write_b128 v209, v[152:155] offset:2048
	v_mul_f32_e32 v156, v37, v156
	v_mul_f32_e32 v157, v37, v157
	v_mul_f32_e32 v158, v37, v158
	v_mul_f32_e32 v159, v37, v159
	ds_write_b128 v209, v[156:159] offset:3072
	v_mul_f32_e32 v160, v38, v160
	v_mul_f32_e32 v161, v38, v161
	v_mul_f32_e32 v162, v38, v162
	v_mul_f32_e32 v163, v38, v163
	ds_write_b128 v209, v[160:163] offset:4096
	v_mul_f32_e32 v164, v39, v164
	v_mul_f32_e32 v165, v39, v165
	v_mul_f32_e32 v166, v39, v166
	v_mul_f32_e32 v167, v39, v167
	ds_write_b128 v209, v[164:167] offset:5120
	v_mul_f32_e32 v168, v40, v168
	v_mul_f32_e32 v169, v40, v169
	v_mul_f32_e32 v170, v40, v170
	v_mul_f32_e32 v171, v40, v171
	ds_write_b128 v209, v[168:171] offset:6144
	v_mul_f32_e32 v172, v41, v172
	v_mul_f32_e32 v173, v41, v173
	v_mul_f32_e32 v174, v41, v174
	v_mul_f32_e32 v175, v41, v175
	ds_write_b128 v209, v[172:175] offset:7168
	s_waitcnt lgkmcnt(0)
	s_barrier
; #define GAS __attribute__((address_space(1)))
; #define LAS __attribute__((address_space(3)))
; #define LDS_WAIT() asm volatile("s_waitcnt lgkmcnt(0)" ::: "memory")
; __device__ __forceinline__ unsigned pk4_fp8(float a, float b, float c, float d) {
;     a = fminf(fmaxf(a, -448.f), 448.f); b = fminf(fmaxf(b, -448.f), 448.f); c = fminf(fmaxf(c, -448.f), 448.f); d = fminf(fmaxf(d, -448.f), 448.f);
;     int w = __builtin_amdgcn_cvt_pk_fp8_f32(a, b, 0, false); w = __builtin_amdgcn_cvt_pk_fp8_f32(c, d, w, true); return (unsigned)w; }
;     ...
; #pragma unroll
;     for (int i = 0; i < 32; ++i) v[i] = sc >= 0 ? W[(size_t)(k0 + 2 * i + (lane >> 5)) * Nsrc + sc] : 0.f;
; #pragma unroll
;     for (int i = 0; i < 32; ++i) { const int k = k0 + 2 * i + (lane >> 5); float x = v[i] * wscale; if (KS) x *= (k < ksplit ? ksA[k] : ksB[k - ksplit]); scr[(2 * i + (lane >> 5)) * 33 + (lane & 31)] = x; }
;     LDS_WAIT(); asm volatile("" ::: "memory");
;     const int c = lane & 7;
; #pragma unroll
;     for (int j = 0; j < 4; ++j) { const int n = (lane >> 3) + 8 * j; const LAS float* s = scr + (8 * c) * 33 + n;
;         const unsigned long long o = (unsigned long long)pg8::pk4_fp8(s[0 * 33], s[1 * 33], s[2 * 33], s[3 * 33]) | ((unsigned long long)pg8::pk4_fp8(s[4 * 33], s[5 * 33], s[6 * 33], s[7 * 33]) << 32);
;         *(GAS unsigned long long*)(WT + (size_t)(n0 + n) * K + k0 + 8 * c) = o; }
	s_add_u32 s8, s34, 0x8000
	s_addc_u32 s9, s35, 0
	global_load_dwordx4 v[144:147], v74, s[8:9]
	s_add_u32 s8, s8, 0x20000
	s_addc_u32 s9, s9, 0
	global_load_dwordx4 v[148:151], v74, s[8:9]
	s_add_u32 s8, s8, 0x20000
	s_addc_u32 s9, s9, 0
	global_load_dwordx4 v[152:155], v74, s[8:9]
	s_add_u32 s8, s8, 0x20000
	s_addc_u32 s9, s9, 0
	global_load_dwordx4 v[156:159], v74, s[8:9]
	s_add_u32 s8, s8, 0x20000
	s_addc_u32 s9, s9, 0
	global_load_dwordx4 v[160:163], v74, s[8:9]
	s_add_u32 s8, s8, 0x20000
	s_addc_u32 s9, s9, 0
	global_load_dwordx4 v[164:167], v74, s[8:9]
	s_add_u32 s8, s8, 0x20000
	s_addc_u32 s9, s9, 0
	global_load_dwordx4 v[168:171], v74, s[8:9]
	s_add_u32 s8, s8, 0x20000
	s_addc_u32 s9, s9, 0
	global_load_dwordx4 v[172:175], v74, s[8:9]
	s_add_u32 s6, s36, 0x1800000
	s_addc_u32 s7, s37, 0
	ds_read_b32 v226, v211
	ds_read_b32 v227, v211 offset:512
	ds_read_b32 v228, v211 offset:1024
	ds_read_b32 v229, v211 offset:1536
	ds_read_b32 v230, v211 offset:2048
	ds_read_b32 v231, v211 offset:2560
	ds_read_b32 v232, v211 offset:3072
	ds_read_b32 v233, v211 offset:3584
	ds_read_b32 v234, v211 offset:4096
	ds_read_b32 v235, v211 offset:4608
	ds_read_b32 v236, v211 offset:5120
	ds_read_b32 v237, v211 offset:5632
	ds_read_b32 v238, v211 offset:6144
	ds_read_b32 v239, v211 offset:6656
	ds_read_b32 v240, v211 offset:7168
	ds_read_b32 v241, v211 offset:7680
	s_waitcnt lgkmcnt(0)
	v_max_f32_e32 v226, v226, v226
	v_max_f32_e32 v227, v227, v227
	v_max_f32_e32 v228, v228, v228
	v_max_f32_e32 v229, v229, v229
	v_max_f32_e32 v230, v230, v230
	v_max_f32_e32 v231, v231, v231
	v_max_f32_e32 v232, v232, v232
	v_max_f32_e32 v233, v233, v233
	v_max_f32_e32 v234, v234, v234
	v_max_f32_e32 v235, v235, v235
	v_max_f32_e32 v236, v236, v236
	v_max_f32_e32 v237, v237, v237
	v_max_f32_e32 v238, v238, v238
	v_max_f32_e32 v239, v239, v239
	v_max_f32_e32 v240, v240, v240
	v_max_f32_e32 v241, v241, v241
	v_med3_f32 v226, v226, s62, v95
	v_med3_f32 v227, v227, s62, v95
	v_med3_f32 v228, v228, s62, v95
	v_med3_f32 v229, v229, s62, v95
	v_med3_f32 v230, v230, s62, v95
	v_med3_f32 v231, v231, s62, v95
	v_med3_f32 v232, v232, s62, v95
	v_med3_f32 v233, v233, s62, v95
	v_med3_f32 v234, v234, s62, v95
	v_med3_f32 v235, v235, s62, v95
	v_med3_f32 v236, v236, s62, v95
	v_med3_f32 v237, v237, s62, v95
	v_med3_f32 v238, v238, s62, v95
	v_med3_f32 v239, v239, s62, v95
	v_med3_f32 v240, v240, s62, v95
	v_med3_f32 v241, v241, s62, v95
	v_mov_b32_e32 v242, 0
	v_mov_b32_e32 v243, 0
	v_mov_b32_e32 v244, 0
	v_mov_b32_e32 v245, 0
	v_cvt_pk_fp8_f32 v242, v226, v227
	v_cvt_pk_fp8_f32 v243, v230, v231
	v_cvt_pk_fp8_f32 v244, v234, v235
	v_cvt_pk_fp8_f32 v245, v238, v239
	v_cvt_pk_fp8_f32 v242, v228, v229 op_sel:[0,0,1]
	v_cvt_pk_fp8_f32 v243, v232, v233 op_sel:[0,0,1]
	v_cvt_pk_fp8_f32 v244, v236, v237 op_sel:[0,0,1]
	v_cvt_pk_fp8_f32 v245, v240, v241 op_sel:[0,0,1]
	s_nop 0
	global_store_dwordx4 v77, v[242:245], s[6:7]
	ds_read_b32 v226, v213
	ds_read_b32 v227, v213 offset:512
	ds_read_b32 v228, v213 offset:1024
	ds_read_b32 v229, v213 offset:1536
	ds_read_b32 v230, v213 offset:2048
	ds_read_b32 v231, v213 offset:2560
	ds_read_b32 v232, v213 offset:3072
	ds_read_b32 v233, v213 offset:3584
	ds_read_b32 v234, v213 offset:4096
	ds_read_b32 v235, v213 offset:4608
	ds_read_b32 v236, v213 offset:5120
	ds_read_b32 v237, v213 offset:5632
	ds_read_b32 v238, v213 offset:6144
	ds_read_b32 v239, v213 offset:6656
	ds_read_b32 v240, v213 offset:7168
	ds_read_b32 v241, v213 offset:7680
	s_waitcnt lgkmcnt(0)
	v_max_f32_e32 v226, v226, v226
	v_max_f32_e32 v227, v227, v227
	v_max_f32_e32 v228, v228, v228
	v_max_f32_e32 v229, v229, v229
	v_max_f32_e32 v230, v230, v230
	v_max_f32_e32 v231, v231, v231
	v_max_f32_e32 v232, v232, v232
	v_max_f32_e32 v233, v233, v233
	v_max_f32_e32 v234, v234, v234
	v_max_f32_e32 v235, v235, v235
	v_max_f32_e32 v236, v236, v236
	v_max_f32_e32 v237, v237, v237
	v_max_f32_e32 v238, v238, v238
	v_max_f32_e32 v239, v239, v239
	v_max_f32_e32 v240, v240, v240
	v_max_f32_e32 v241, v241, v241
	v_med3_f32 v226, v226, s62, v95
	v_med3_f32 v227, v227, s62, v95
	v_med3_f32 v228, v228, s62, v95
	v_med3_f32 v229, v229, s62, v95
	v_med3_f32 v230, v230, s62, v95
	v_med3_f32 v231, v231, s62, v95
	v_med3_f32 v232, v232, s62, v95
	v_med3_f32 v233, v233, s62, v95
	v_med3_f32 v234, v234, s62, v95
	v_med3_f32 v235, v235, s62, v95
	v_med3_f32 v236, v236, s62, v95
	v_med3_f32 v237, v237, s62, v95
	v_med3_f32 v238, v238, s62, v95
	v_med3_f32 v239, v239, s62, v95
	v_med3_f32 v240, v240, s62, v95
	v_med3_f32 v241, v241, s62, v95
	v_mov_b32_e32 v242, 0
	v_mov_b32_e32 v243, 0
	v_mov_b32_e32 v244, 0
	v_mov_b32_e32 v245, 0
	v_cvt_pk_fp8_f32 v242, v226, v227
	v_cvt_pk_fp8_f32 v243, v230, v231
	v_cvt_pk_fp8_f32 v244, v234, v235
	v_cvt_pk_fp8_f32 v245, v238, v239
	v_cvt_pk_fp8_f32 v242, v228, v229 op_sel:[0,0,1]
	v_cvt_pk_fp8_f32 v243, v232, v233 op_sel:[0,0,1]
	v_cvt_pk_fp8_f32 v244, v236, v237 op_sel:[0,0,1]
	v_cvt_pk_fp8_f32 v245, v240, v241 op_sel:[0,0,1]
	s_nop 0
	global_store_dwordx4 v78, v[242:245], s[6:7]
	s_waitcnt vmcnt(12)
	v_mul_f32_e32 v176, v34, v176
	v_mul_f32_e32 v177, v34, v177
	v_mul_f32_e32 v178, v34, v178
	v_mul_f32_e32 v179, v34, v179
	ds_write_b128 v210, v[176:179]
	v_mul_f32_e32 v180, v35, v180
	v_mul_f32_e32 v181, v35, v181
	v_mul_f32_e32 v182, v35, v182
	v_mul_f32_e32 v183, v35, v183
	ds_write_b128 v210, v[180:183] offset:1024
	v_mul_f32_e32 v184, v36, v184
	v_mul_f32_e32 v185, v36, v185
	v_mul_f32_e32 v186, v36, v186
	v_mul_f32_e32 v187, v36, v187
	ds_write_b128 v210, v[184:187] offset:2048
	v_mul_f32_e32 v188, v37, v188
	v_mul_f32_e32 v189, v37, v189
	v_mul_f32_e32 v190, v37, v190
	v_mul_f32_e32 v191, v37, v191
	ds_write_b128 v210, v[188:191] offset:3072
	v_mul_f32_e32 v192, v38, v192
	v_mul_f32_e32 v193, v38, v193
	v_mul_f32_e32 v194, v38, v194
	v_mul_f32_e32 v195, v38, v195
	ds_write_b128 v210, v[192:195] offset:4096
	v_mul_f32_e32 v196, v39, v196
	v_mul_f32_e32 v197, v39, v197
	v_mul_f32_e32 v198, v39, v198
	v_mul_f32_e32 v199, v39, v199
	ds_write_b128 v210, v[196:199] offset:5120
	v_mul_f32_e32 v200, v40, v200
	v_mul_f32_e32 v201, v40, v201
	v_mul_f32_e32 v202, v40, v202
	v_mul_f32_e32 v203, v40, v203
	ds_write_b128 v210, v[200:203] offset:6144
	v_mul_f32_e32 v204, v41, v204
	v_mul_f32_e32 v205, v41, v205
	v_mul_f32_e32 v206, v41, v206
	v_mul_f32_e32 v207, v41, v207
	ds_write_b128 v210, v[204:207] offset:7168
	s_waitcnt lgkmcnt(0)
	s_barrier
; #define GAS __attribute__((address_space(1)))
; #define LAS __attribute__((address_space(3)))
; #define LDS_WAIT() asm volatile("s_waitcnt lgkmcnt(0)" ::: "memory")
; __device__ __forceinline__ unsigned pk4_fp8(float a, float b, float c, float d) {
;     a = fminf(fmaxf(a, -448.f), 448.f); b = fminf(fmaxf(b, -448.f), 448.f); c = fminf(fmaxf(c, -448.f), 448.f); d = fminf(fmaxf(d, -448.f), 448.f);
;     int w = __builtin_amdgcn_cvt_pk_fp8_f32(a, b, 0, false); w = __builtin_amdgcn_cvt_pk_fp8_f32(c, d, w, true); return (unsigned)w; }
;     ...
; #pragma unroll
;     for (int i = 0; i < 32; ++i) v[i] = sc >= 0 ? W[(size_t)(k0 + 2 * i + (lane >> 5)) * Nsrc + sc] : 0.f;
; #pragma unroll
;     for (int i = 0; i < 32; ++i) { const int k = k0 + 2 * i + (lane >> 5); float x = v[i] * wscale; if (KS) x *= (k < ksplit ? ksA[k] : ksB[k - ksplit]); scr[(2 * i + (lane >> 5)) * 33 + (lane & 31)] = x; }
;     LDS_WAIT(); asm volatile("" ::: "memory");
;     const int c = lane & 7;
; #pragma unroll
;     for (int j = 0; j < 4; ++j) { const int n = (lane >> 3) + 8 * j; const LAS float* s = scr + (8 * c) * 33 + n;
;         const unsigned long long o = (unsigned long long)pg8::pk4_fp8(s[0 * 33], s[1 * 33], s[2 * 33], s[3 * 33]) | ((unsigned long long)pg8::pk4_fp8(s[4 * 33], s[5 * 33], s[6 * 33], s[7 * 33]) << 32);
;         *(GAS unsigned long long*)(WT + (size_t)(n0 + n) * K + k0 + 8 * c) = o; }
	s_add_u32 s8, s34, 0x9000
	s_addc_u32 s9, s35, 0
	global_load_dwordx4 v[176:179], v74, s[8:9]
	s_add_u32 s8, s8, 0x20000
	s_addc_u32 s9, s9, 0
	global_load_dwordx4 v[180:183], v74, s[8:9]
	s_add_u32 s8, s8, 0x20000
	s_addc_u32 s9, s9, 0
	global_load_dwordx4 v[184:187], v74, s[8:9]
	s_add_u32 s8, s8, 0x20000
	s_addc_u32 s9, s9, 0
	global_load_dwordx4 v[188:191], v74, s[8:9]
	s_add_u32 s8, s8, 0x20000
	s_addc_u32 s9, s9, 0
	global_load_dwordx4 v[192:195], v74, s[8:9]
	s_add_u32 s8, s8, 0x20000
	s_addc_u32 s9, s9, 0
	global_load_dwordx4 v[196:199], v74, s[8:9]
	s_add_u32 s8, s8, 0x20000
	s_addc_u32 s9, s9, 0
	global_load_dwordx4 v[200:203], v74, s[8:9]
	s_add_u32 s8, s8, 0x20000
	s_addc_u32 s9, s9, 0
	global_load_dwordx4 v[204:207], v74, s[8:9]
	s_add_u32 s6, s36, 0x1c00000
	s_addc_u32 s7, s37, 0
	ds_read_b32 v226, v212
	ds_read_b32 v227, v212 offset:512
	ds_read_b32 v228, v212 offset:1024
	ds_read_b32 v229, v212 offset:1536
	ds_read_b32 v230, v212 offset:2048
	ds_read_b32 v231, v212 offset:2560
	ds_read_b32 v232, v212 offset:3072
	ds_read_b32 v233, v212 offset:3584
	ds_read_b32 v234, v212 offset:4096
	ds_read_b32 v235, v212 offset:4608
	ds_read_b32 v236, v212 offset:5120
	ds_read_b32 v237, v212 offset:5632
	ds_read_b32 v238, v212 offset:6144
	ds_read_b32 v239, v212 offset:6656
	ds_read_b32 v240, v212 offset:7168
	ds_read_b32 v241, v212 offset:7680
	s_waitcnt lgkmcnt(0)
	v_max_f32_e32 v226, v226, v226
	v_max_f32_e32 v227, v227, v227
	v_max_f32_e32 v228, v228, v228
	v_max_f32_e32 v229, v229, v229
	v_max_f32_e32 v230, v230, v230
	v_max_f32_e32 v231, v231, v231
	v_max_f32_e32 v232, v232, v232
	v_max_f32_e32 v233, v233, v233
	v_max_f32_e32 v234, v234, v234
	v_max_f32_e32 v235, v235, v235
	v_max_f32_e32 v236, v236, v236
	v_max_f32_e32 v237, v237, v237
	v_max_f32_e32 v238, v238, v238
	v_max_f32_e32 v239, v239, v239
	v_max_f32_e32 v240, v240, v240
	v_max_f32_e32 v241, v241, v241
	v_med3_f32 v226, v226, s62, v95
	v_med3_f32 v227, v227, s62, v95
	v_med3_f32 v228, v228, s62, v95
	v_med3_f32 v229, v229, s62, v95
	v_med3_f32 v230, v230, s62, v95
	v_med3_f32 v231, v231, s62, v95
	v_med3_f32 v232, v232, s62, v95
	v_med3_f32 v233, v233, s62, v95
	v_med3_f32 v234, v234, s62, v95
	v_med3_f32 v235, v235, s62, v95
	v_med3_f32 v236, v236, s62, v95
	v_med3_f32 v237, v237, s62, v95
	v_med3_f32 v238, v238, s62, v95
	v_med3_f32 v239, v239, s62, v95
	v_med3_f32 v240, v240, s62, v95
	v_med3_f32 v241, v241, s62, v95
	v_mov_b32_e32 v242, 0
	v_mov_b32_e32 v243, 0
	v_mov_b32_e32 v244, 0
	v_mov_b32_e32 v245, 0
	v_cvt_pk_fp8_f32 v242, v226, v227
	v_cvt_pk_fp8_f32 v243, v230, v231
	v_cvt_pk_fp8_f32 v244, v234, v235
	v_cvt_pk_fp8_f32 v245, v238, v239
	v_cvt_pk_fp8_f32 v242, v228, v229 op_sel:[0,0,1]
	v_cvt_pk_fp8_f32 v243, v232, v233 op_sel:[0,0,1]
	v_cvt_pk_fp8_f32 v244, v236, v237 op_sel:[0,0,1]
	v_cvt_pk_fp8_f32 v245, v240, v241 op_sel:[0,0,1]
	s_nop 0
	global_store_dwordx4 v77, v[242:245], s[6:7]
	ds_read_b32 v226, v214
	ds_read_b32 v227, v214 offset:512
	ds_read_b32 v228, v214 offset:1024
	ds_read_b32 v229, v214 offset:1536
	ds_read_b32 v230, v214 offset:2048
	ds_read_b32 v231, v214 offset:2560
	ds_read_b32 v232, v214 offset:3072
	ds_read_b32 v233, v214 offset:3584
	ds_read_b32 v234, v214 offset:4096
	ds_read_b32 v235, v214 offset:4608
	ds_read_b32 v236, v214 offset:5120
	ds_read_b32 v237, v214 offset:5632
	ds_read_b32 v238, v214 offset:6144
	ds_read_b32 v239, v214 offset:6656
	ds_read_b32 v240, v214 offset:7168
	ds_read_b32 v241, v214 offset:7680
	s_waitcnt lgkmcnt(0)
	v_max_f32_e32 v226, v226, v226
	v_max_f32_e32 v227, v227, v227
	v_max_f32_e32 v228, v228, v228
	v_max_f32_e32 v229, v229, v229
	v_max_f32_e32 v230, v230, v230
	v_max_f32_e32 v231, v231, v231
	v_max_f32_e32 v232, v232, v232
	v_max_f32_e32 v233, v233, v233
	v_max_f32_e32 v234, v234, v234
	v_max_f32_e32 v235, v235, v235
	v_max_f32_e32 v236, v236, v236
	v_max_f32_e32 v237, v237, v237
	v_max_f32_e32 v238, v238, v238
	v_max_f32_e32 v239, v239, v239
	v_max_f32_e32 v240, v240, v240
	v_max_f32_e32 v241, v241, v241
	v_med3_f32 v226, v226, s62, v95
	v_med3_f32 v227, v227, s62, v95
	v_med3_f32 v228, v228, s62, v95
	v_med3_f32 v229, v229, s62, v95
	v_med3_f32 v230, v230, s62, v95
	v_med3_f32 v231, v231, s62, v95
	v_med3_f32 v232, v232, s62, v95
	v_med3_f32 v233, v233, s62, v95
	v_med3_f32 v234, v234, s62, v95
	v_med3_f32 v235, v235, s62, v95
	v_med3_f32 v236, v236, s62, v95
	v_med3_f32 v237, v237, s62, v95
	v_med3_f32 v238, v238, s62, v95
	v_med3_f32 v239, v239, s62, v95
	v_med3_f32 v240, v240, s62, v95
	v_med3_f32 v241, v241, s62, v95
	v_mov_b32_e32 v242, 0
	v_mov_b32_e32 v243, 0
	v_mov_b32_e32 v244, 0
	v_mov_b32_e32 v245, 0
	v_cvt_pk_fp8_f32 v242, v226, v227
	v_cvt_pk_fp8_f32 v243, v230, v231
	v_cvt_pk_fp8_f32 v244, v234, v235
	v_cvt_pk_fp8_f32 v245, v238, v239
	v_cvt_pk_fp8_f32 v242, v228, v229 op_sel:[0,0,1]
	v_cvt_pk_fp8_f32 v243, v232, v233 op_sel:[0,0,1]
	v_cvt_pk_fp8_f32 v244, v236, v237 op_sel:[0,0,1]
	v_cvt_pk_fp8_f32 v245, v240, v241 op_sel:[0,0,1]
	s_nop 0
	global_store_dwordx4 v78, v[242:245], s[6:7]
	s_waitcnt vmcnt(12)
	v_mul_f32_e32 v144, v34, v144
	v_mul_f32_e32 v145, v34, v145
	v_mul_f32_e32 v146, v34, v146
	v_mul_f32_e32 v147, v34, v147
	ds_write_b128 v209, v[144:147]
	v_mul_f32_e32 v148, v35, v148
	v_mul_f32_e32 v149, v35, v149
	v_mul_f32_e32 v150, v35, v150
	v_mul_f32_e32 v151, v35, v151
	ds_write_b128 v209, v[148:151] offset:1024
	v_mul_f32_e32 v152, v36, v152
	v_mul_f32_e32 v153, v36, v153
	v_mul_f32_e32 v154, v36, v154
	v_mul_f32_e32 v155, v36, v155
	ds_write_b128 v209, v[152:155] offset:2048
	v_mul_f32_e32 v156, v37, v156
	v_mul_f32_e32 v157, v37, v157
	v_mul_f32_e32 v158, v37, v158
	v_mul_f32_e32 v159, v37, v159
	ds_write_b128 v209, v[156:159] offset:3072
	v_mul_f32_e32 v160, v38, v160
	v_mul_f32_e32 v161, v38, v161
	v_mul_f32_e32 v162, v38, v162
	v_mul_f32_e32 v163, v38, v163
	ds_write_b128 v209, v[160:163] offset:4096
	v_mul_f32_e32 v164, v39, v164
	v_mul_f32_e32 v165, v39, v165
	v_mul_f32_e32 v166, v39, v166
	v_mul_f32_e32 v167, v39, v167
	ds_write_b128 v209, v[164:167] offset:5120
	v_mul_f32_e32 v168, v40, v168
	v_mul_f32_e32 v169, v40, v169
	v_mul_f32_e32 v170, v40, v170
	v_mul_f32_e32 v171, v40, v171
	ds_write_b128 v209, v[168:171] offset:6144
	v_mul_f32_e32 v172, v41, v172
	v_mul_f32_e32 v173, v41, v173
	v_mul_f32_e32 v174, v41, v174
	v_mul_f32_e32 v175, v41, v175
	ds_write_b128 v209, v[172:175] offset:7168
	s_waitcnt lgkmcnt(0)
	s_barrier
; #define GAS __attribute__((address_space(1)))
; #define LAS __attribute__((address_space(3)))
; #define LDS_WAIT() asm volatile("s_waitcnt lgkmcnt(0)" ::: "memory")
; __device__ __forceinline__ unsigned pk4_fp8(float a, float b, float c, float d) {
;     a = fminf(fmaxf(a, -448.f), 448.f); b = fminf(fmaxf(b, -448.f), 448.f); c = fminf(fmaxf(c, -448.f), 448.f); d = fminf(fmaxf(d, -448.f), 448.f);
;     int w = __builtin_amdgcn_cvt_pk_fp8_f32(a, b, 0, false); w = __builtin_amdgcn_cvt_pk_fp8_f32(c, d, w, true); return (unsigned)w; }
;     ...
; #pragma unroll
;     for (int i = 0; i < 32; ++i) v[i] = sc >= 0 ? W[(size_t)(k0 + 2 * i + (lane >> 5)) * Nsrc + sc] : 0.f;
; #pragma unroll
;     for (int i = 0; i < 32; ++i) { const int k = k0 + 2 * i + (lane >> 5); float x = v[i] * wscale; if (KS) x *= (k < ksplit ? ksA[k] : ksB[k - ksplit]); scr[(2 * i + (lane >> 5)) * 33 + (lane & 31)] = x; }
;     LDS_WAIT(); asm volatile("" ::: "memory");
;     const int c = lane & 7;
; #pragma unroll
;     for (int j = 0; j < 4; ++j) { const int n = (lane >> 3) + 8 * j; const LAS float* s = scr + (8 * c) * 33 + n;
;         const unsigned long long o = (unsigned long long)pg8::pk4_fp8(s[0 * 33], s[1 * 33], s[2 * 33], s[3 * 33]) | ((unsigned long long)pg8::pk4_fp8(s[4 * 33], s[5 * 33], s[6 * 33], s[7 * 33]) << 32);
;         *(GAS unsigned long long*)(WT + (size_t)(n0 + n) * K + k0 + 8 * c) = o; }
	s_add_u32 s8, s34, 0xa000
	s_addc_u32 s9, s35, 0
	global_load_dwordx4 v[144:147], v74, s[8:9]
	s_add_u32 s8, s8, 0x20000
	s_addc_u32 s9, s9, 0
	global_load_dwordx4 v[148:151], v74, s[8:9]
	s_add_u32 s8, s8, 0x20000
	s_addc_u32 s9, s9, 0
	global_load_dwordx4 v[152:155], v74, s[8:9]
	s_add_u32 s8, s8, 0x20000
	s_addc_u32 s9, s9, 0
	global_load_dwordx4 v[156:159], v74, s[8:9]
	s_add_u32 s8, s8, 0x20000
	s_addc_u32 s9, s9, 0
	global_load_dwordx4 v[160:163], v74, s[8:9]
	s_add_u32 s8, s8, 0x20000
	s_addc_u32 s9, s9, 0
	global_load_dwordx4 v[164:167], v74, s[8:9]
	s_add_u32 s8, s8, 0x20000
	s_addc_u32 s9, s9, 0
	global_load_dwordx4 v[168:171], v74, s[8:9]
	s_add_u32 s8, s8, 0x20000
	s_addc_u32 s9, s9, 0
	global_load_dwordx4 v[172:175], v74, s[8:9]
	s_add_u32 s6, s36, 0x2000000
	s_addc_u32 s7, s37, 0
	ds_read_b32 v226, v211
	ds_read_b32 v227, v211 offset:512
	ds_read_b32 v228, v211 offset:1024
	ds_read_b32 v229, v211 offset:1536
	ds_read_b32 v230, v211 offset:2048
	ds_read_b32 v231, v211 offset:2560
	ds_read_b32 v232, v211 offset:3072
	ds_read_b32 v233, v211 offset:3584
	ds_read_b32 v234, v211 offset:4096
	ds_read_b32 v235, v211 offset:4608
	ds_read_b32 v236, v211 offset:5120
	ds_read_b32 v237, v211 offset:5632
	ds_read_b32 v238, v211 offset:6144
	ds_read_b32 v239, v211 offset:6656
	ds_read_b32 v240, v211 offset:7168
	ds_read_b32 v241, v211 offset:7680
	s_waitcnt lgkmcnt(0)
	v_max_f32_e32 v226, v226, v226
	v_max_f32_e32 v227, v227, v227
	v_max_f32_e32 v228, v228, v228
	v_max_f32_e32 v229, v229, v229
	v_max_f32_e32 v230, v230, v230
	v_max_f32_e32 v231, v231, v231
	v_max_f32_e32 v232, v232, v232
	v_max_f32_e32 v233, v233, v233
	v_max_f32_e32 v234, v234, v234
	v_max_f32_e32 v235, v235, v235
	v_max_f32_e32 v236, v236, v236
	v_max_f32_e32 v237, v237, v237
	v_max_f32_e32 v238, v238, v238
	v_max_f32_e32 v239, v239, v239
	v_max_f32_e32 v240, v240, v240
	v_max_f32_e32 v241, v241, v241
	v_med3_f32 v226, v226, s62, v95
	v_med3_f32 v227, v227, s62, v95
	v_med3_f32 v228, v228, s62, v95
	v_med3_f32 v229, v229, s62, v95
	v_med3_f32 v230, v230, s62, v95
	v_med3_f32 v231, v231, s62, v95
	v_med3_f32 v232, v232, s62, v95
	v_med3_f32 v233, v233, s62, v95
	v_med3_f32 v234, v234, s62, v95
	v_med3_f32 v235, v235, s62, v95
	v_med3_f32 v236, v236, s62, v95
	v_med3_f32 v237, v237, s62, v95
	v_med3_f32 v238, v238, s62, v95
	v_med3_f32 v239, v239, s62, v95
	v_med3_f32 v240, v240, s62, v95
	v_med3_f32 v241, v241, s62, v95
	v_mov_b32_e32 v242, 0
	v_mov_b32_e32 v243, 0
	v_mov_b32_e32 v244, 0
	v_mov_b32_e32 v245, 0
	v_cvt_pk_fp8_f32 v242, v226, v227
	v_cvt_pk_fp8_f32 v243, v230, v231
	v_cvt_pk_fp8_f32 v244, v234, v235
	v_cvt_pk_fp8_f32 v245, v238, v239
	v_cvt_pk_fp8_f32 v242, v228, v229 op_sel:[0,0,1]
	v_cvt_pk_fp8_f32 v243, v232, v233 op_sel:[0,0,1]
	v_cvt_pk_fp8_f32 v244, v236, v237 op_sel:[0,0,1]
	v_cvt_pk_fp8_f32 v245, v240, v241 op_sel:[0,0,1]
	s_nop 0
	global_store_dwordx4 v77, v[242:245], s[6:7]
	ds_read_b32 v226, v213
	ds_read_b32 v227, v213 offset:512
	ds_read_b32 v228, v213 offset:1024
	ds_read_b32 v229, v213 offset:1536
	ds_read_b32 v230, v213 offset:2048
	ds_read_b32 v231, v213 offset:2560
	ds_read_b32 v232, v213 offset:3072
	ds_read_b32 v233, v213 offset:3584
	ds_read_b32 v234, v213 offset:4096
	ds_read_b32 v235, v213 offset:4608
	ds_read_b32 v236, v213 offset:5120
	ds_read_b32 v237, v213 offset:5632
	ds_read_b32 v238, v213 offset:6144
	ds_read_b32 v239, v213 offset:6656
	ds_read_b32 v240, v213 offset:7168
	ds_read_b32 v241, v213 offset:7680
	s_waitcnt lgkmcnt(0)
	v_max_f32_e32 v226, v226, v226
	v_max_f32_e32 v227, v227, v227
	v_max_f32_e32 v228, v228, v228
	v_max_f32_e32 v229, v229, v229
	v_max_f32_e32 v230, v230, v230
	v_max_f32_e32 v231, v231, v231
	v_max_f32_e32 v232, v232, v232
	v_max_f32_e32 v233, v233, v233
	v_max_f32_e32 v234, v234, v234
	v_max_f32_e32 v235, v235, v235
	v_max_f32_e32 v236, v236, v236
	v_max_f32_e32 v237, v237, v237
	v_max_f32_e32 v238, v238, v238
	v_max_f32_e32 v239, v239, v239
	v_max_f32_e32 v240, v240, v240
	v_max_f32_e32 v241, v241, v241
	v_med3_f32 v226, v226, s62, v95
	v_med3_f32 v227, v227, s62, v95
	v_med3_f32 v228, v228, s62, v95
	v_med3_f32 v229, v229, s62, v95
	v_med3_f32 v230, v230, s62, v95
	v_med3_f32 v231, v231, s62, v95
	v_med3_f32 v232, v232, s62, v95
	v_med3_f32 v233, v233, s62, v95
	v_med3_f32 v234, v234, s62, v95
	v_med3_f32 v235, v235, s62, v95
	v_med3_f32 v236, v236, s62, v95
	v_med3_f32 v237, v237, s62, v95
	v_med3_f32 v238, v238, s62, v95
	v_med3_f32 v239, v239, s62, v95
	v_med3_f32 v240, v240, s62, v95
	v_med3_f32 v241, v241, s62, v95
	v_mov_b32_e32 v242, 0
	v_mov_b32_e32 v243, 0
	v_mov_b32_e32 v244, 0
	v_mov_b32_e32 v245, 0
	v_cvt_pk_fp8_f32 v242, v226, v227
	v_cvt_pk_fp8_f32 v243, v230, v231
	v_cvt_pk_fp8_f32 v244, v234, v235
	v_cvt_pk_fp8_f32 v245, v238, v239
	v_cvt_pk_fp8_f32 v242, v228, v229 op_sel:[0,0,1]
	v_cvt_pk_fp8_f32 v243, v232, v233 op_sel:[0,0,1]
	v_cvt_pk_fp8_f32 v244, v236, v237 op_sel:[0,0,1]
	v_cvt_pk_fp8_f32 v245, v240, v241 op_sel:[0,0,1]
	s_nop 0
	global_store_dwordx4 v78, v[242:245], s[6:7]
	s_waitcnt vmcnt(12)
	v_mul_f32_e32 v176, v34, v176
	v_mul_f32_e32 v177, v34, v177
	v_mul_f32_e32 v178, v34, v178
	v_mul_f32_e32 v179, v34, v179
	ds_write_b128 v210, v[176:179]
	v_mul_f32_e32 v180, v35, v180
	v_mul_f32_e32 v181, v35, v181
	v_mul_f32_e32 v182, v35, v182
	v_mul_f32_e32 v183, v35, v183
	ds_write_b128 v210, v[180:183] offset:1024
	v_mul_f32_e32 v184, v36, v184
	v_mul_f32_e32 v185, v36, v185
	v_mul_f32_e32 v186, v36, v186
	v_mul_f32_e32 v187, v36, v187
	ds_write_b128 v210, v[184:187] offset:2048
	v_mul_f32_e32 v188, v37, v188
	v_mul_f32_e32 v189, v37, v189
	v_mul_f32_e32 v190, v37, v190
	v_mul_f32_e32 v191, v37, v191
	ds_write_b128 v210, v[188:191] offset:3072
	v_mul_f32_e32 v192, v38, v192
	v_mul_f32_e32 v193, v38, v193
	v_mul_f32_e32 v194, v38, v194
	v_mul_f32_e32 v195, v38, v195
	ds_write_b128 v210, v[192:195] offset:4096
	v_mul_f32_e32 v196, v39, v196
	v_mul_f32_e32 v197, v39, v197
	v_mul_f32_e32 v198, v39, v198
	v_mul_f32_e32 v199, v39, v199
	ds_write_b128 v210, v[196:199] offset:5120
	v_mul_f32_e32 v200, v40, v200
	v_mul_f32_e32 v201, v40, v201
	v_mul_f32_e32 v202, v40, v202
	v_mul_f32_e32 v203, v40, v203
	ds_write_b128 v210, v[200:203] offset:6144
	v_mul_f32_e32 v204, v41, v204
	v_mul_f32_e32 v205, v41, v205
	v_mul_f32_e32 v206, v41, v206
	v_mul_f32_e32 v207, v41, v207
	ds_write_b128 v210, v[204:207] offset:7168
	s_waitcnt lgkmcnt(0)
	s_barrier
; #define GAS __attribute__((address_space(1)))
; #define LAS __attribute__((address_space(3)))
; #define LDS_WAIT() asm volatile("s_waitcnt lgkmcnt(0)" ::: "memory")
; __device__ __forceinline__ unsigned pk4_fp8(float a, float b, float c, float d) {
;     a = fminf(fmaxf(a, -448.f), 448.f); b = fminf(fmaxf(b, -448.f), 448.f); c = fminf(fmaxf(c, -448.f), 448.f); d = fminf(fmaxf(d, -448.f), 448.f);
;     int w = __builtin_amdgcn_cvt_pk_fp8_f32(a, b, 0, false); w = __builtin_amdgcn_cvt_pk_fp8_f32(c, d, w, true); return (unsigned)w; }
;     ...
; #pragma unroll
;     for (int i = 0; i < 32; ++i) v[i] = sc >= 0 ? W[(size_t)(k0 + 2 * i + (lane >> 5)) * Nsrc + sc] : 0.f;
; #pragma unroll
;     for (int i = 0; i < 32; ++i) { const int k = k0 + 2 * i + (lane >> 5); float x = v[i] * wscale; if (KS) x *= (k < ksplit ? ksA[k] : ksB[k - ksplit]); scr[(2 * i + (lane >> 5)) * 33 + (lane & 31)] = x; }
;     LDS_WAIT(); asm volatile("" ::: "memory");
;     const int c = lane & 7;
; #pragma unroll
;     for (int j = 0; j < 4; ++j) { const int n = (lane >> 3) + 8 * j; const LAS float* s = scr + (8 * c) * 33 + n;
;         const unsigned long long o = (unsigned long long)pg8::pk4_fp8(s[0 * 33], s[1 * 33], s[2 * 33], s[3 * 33]) | ((unsigned long long)pg8::pk4_fp8(s[4 * 33], s[5 * 33], s[6 * 33], s[7 * 33]) << 32);
;         *(GAS unsigned long long*)(WT + (size_t)(n0 + n) * K + k0 + 8 * c) = o; }
	s_add_u32 s8, s34, 0xb000
	s_addc_u32 s9, s35, 0
	global_load_dwordx4 v[176:179], v74, s[8:9]
	s_add_u32 s8, s8, 0x20000
	s_addc_u32 s9, s9, 0
	global_load_dwordx4 v[180:183], v74, s[8:9]
	s_add_u32 s8, s8, 0x20000
	s_addc_u32 s9, s9, 0
	global_load_dwordx4 v[184:187], v74, s[8:9]
	s_add_u32 s8, s8, 0x20000
	s_addc_u32 s9, s9, 0
	global_load_dwordx4 v[188:191], v74, s[8:9]
	s_add_u32 s8, s8, 0x20000
	s_addc_u32 s9, s9, 0
	global_load_dwordx4 v[192:195], v74, s[8:9]
	s_add_u32 s8, s8, 0x20000
	s_addc_u32 s9, s9, 0
	global_load_dwordx4 v[196:199], v74, s[8:9]
	s_add_u32 s8, s8, 0x20000
	s_addc_u32 s9, s9, 0
	global_load_dwordx4 v[200:203], v74, s[8:9]
	s_add_u32 s8, s8, 0x20000
	s_addc_u32 s9, s9, 0
	global_load_dwordx4 v[204:207], v74, s[8:9]
	s_add_u32 s6, s36, 0x2400000
	s_addc_u32 s7, s37, 0
	ds_read_b32 v226, v212
	ds_read_b32 v227, v212 offset:512
	ds_read_b32 v228, v212 offset:1024
	ds_read_b32 v229, v212 offset:1536
	ds_read_b32 v230, v212 offset:2048
	ds_read_b32 v231, v212 offset:2560
	ds_read_b32 v232, v212 offset:3072
	ds_read_b32 v233, v212 offset:3584
	ds_read_b32 v234, v212 offset:4096
	ds_read_b32 v235, v212 offset:4608
	ds_read_b32 v236, v212 offset:5120
	ds_read_b32 v237, v212 offset:5632
	ds_read_b32 v238, v212 offset:6144
	ds_read_b32 v239, v212 offset:6656
	ds_read_b32 v240, v212 offset:7168
	ds_read_b32 v241, v212 offset:7680
	s_waitcnt lgkmcnt(0)
	v_max_f32_e32 v226, v226, v226
	v_max_f32_e32 v227, v227, v227
	v_max_f32_e32 v228, v228, v228
	v_max_f32_e32 v229, v229, v229
	v_max_f32_e32 v230, v230, v230
	v_max_f32_e32 v231, v231, v231
	v_max_f32_e32 v232, v232, v232
	v_max_f32_e32 v233, v233, v233
	v_max_f32_e32 v234, v234, v234
	v_max_f32_e32 v235, v235, v235
	v_max_f32_e32 v236, v236, v236
	v_max_f32_e32 v237, v237, v237
	v_max_f32_e32 v238, v238, v238
	v_max_f32_e32 v239, v239, v239
	v_max_f32_e32 v240, v240, v240
	v_max_f32_e32 v241, v241, v241
	v_med3_f32 v226, v226, s62, v95
	v_med3_f32 v227, v227, s62, v95
	v_med3_f32 v228, v228, s62, v95
	v_med3_f32 v229, v229, s62, v95
	v_med3_f32 v230, v230, s62, v95
	v_med3_f32 v231, v231, s62, v95
	v_med3_f32 v232, v232, s62, v95
	v_med3_f32 v233, v233, s62, v95
	v_med3_f32 v234, v234, s62, v95
	v_med3_f32 v235, v235, s62, v95
	v_med3_f32 v236, v236, s62, v95
	v_med3_f32 v237, v237, s62, v95
	v_med3_f32 v238, v238, s62, v95
	v_med3_f32 v239, v239, s62, v95
	v_med3_f32 v240, v240, s62, v95
	v_med3_f32 v241, v241, s62, v95
	v_mov_b32_e32 v242, 0
	v_mov_b32_e32 v243, 0
	v_mov_b32_e32 v244, 0
	v_mov_b32_e32 v245, 0
	v_cvt_pk_fp8_f32 v242, v226, v227
	v_cvt_pk_fp8_f32 v243, v230, v231
	v_cvt_pk_fp8_f32 v244, v234, v235
	v_cvt_pk_fp8_f32 v245, v238, v239
	v_cvt_pk_fp8_f32 v242, v228, v229 op_sel:[0,0,1]
	v_cvt_pk_fp8_f32 v243, v232, v233 op_sel:[0,0,1]
	v_cvt_pk_fp8_f32 v244, v236, v237 op_sel:[0,0,1]
	v_cvt_pk_fp8_f32 v245, v240, v241 op_sel:[0,0,1]
	s_nop 0
	global_store_dwordx4 v77, v[242:245], s[6:7]
	ds_read_b32 v226, v214
	ds_read_b32 v227, v214 offset:512
	ds_read_b32 v228, v214 offset:1024
	ds_read_b32 v229, v214 offset:1536
	ds_read_b32 v230, v214 offset:2048
	ds_read_b32 v231, v214 offset:2560
	ds_read_b32 v232, v214 offset:3072
	ds_read_b32 v233, v214 offset:3584
	ds_read_b32 v234, v214 offset:4096
	ds_read_b32 v235, v214 offset:4608
	ds_read_b32 v236, v214 offset:5120
	ds_read_b32 v237, v214 offset:5632
	ds_read_b32 v238, v214 offset:6144
	ds_read_b32 v239, v214 offset:6656
	ds_read_b32 v240, v214 offset:7168
	ds_read_b32 v241, v214 offset:7680
	s_waitcnt lgkmcnt(0)
	v_max_f32_e32 v226, v226, v226
	v_max_f32_e32 v227, v227, v227
	v_max_f32_e32 v228, v228, v228
	v_max_f32_e32 v229, v229, v229
	v_max_f32_e32 v230, v230, v230
	v_max_f32_e32 v231, v231, v231
	v_max_f32_e32 v232, v232, v232
	v_max_f32_e32 v233, v233, v233
	v_max_f32_e32 v234, v234, v234
	v_max_f32_e32 v235, v235, v235
	v_max_f32_e32 v236, v236, v236
	v_max_f32_e32 v237, v237, v237
	v_max_f32_e32 v238, v238, v238
	v_max_f32_e32 v239, v239, v239
	v_max_f32_e32 v240, v240, v240
	v_max_f32_e32 v241, v241, v241
	v_med3_f32 v226, v226, s62, v95
	v_med3_f32 v227, v227, s62, v95
	v_med3_f32 v228, v228, s62, v95
	v_med3_f32 v229, v229, s62, v95
	v_med3_f32 v230, v230, s62, v95
	v_med3_f32 v231, v231, s62, v95
	v_med3_f32 v232, v232, s62, v95
	v_med3_f32 v233, v233, s62, v95
	v_med3_f32 v234, v234, s62, v95
	v_med3_f32 v235, v235, s62, v95
	v_med3_f32 v236, v236, s62, v95
	v_med3_f32 v237, v237, s62, v95
	v_med3_f32 v238, v238, s62, v95
	v_med3_f32 v239, v239, s62, v95
	v_med3_f32 v240, v240, s62, v95
	v_med3_f32 v241, v241, s62, v95
	v_mov_b32_e32 v242, 0
	v_mov_b32_e32 v243, 0
	v_mov_b32_e32 v244, 0
	v_mov_b32_e32 v245, 0
	v_cvt_pk_fp8_f32 v242, v226, v227
	v_cvt_pk_fp8_f32 v243, v230, v231
	v_cvt_pk_fp8_f32 v244, v234, v235
	v_cvt_pk_fp8_f32 v245, v238, v239
	v_cvt_pk_fp8_f32 v242, v228, v229 op_sel:[0,0,1]
	v_cvt_pk_fp8_f32 v243, v232, v233 op_sel:[0,0,1]
	v_cvt_pk_fp8_f32 v244, v236, v237 op_sel:[0,0,1]
	v_cvt_pk_fp8_f32 v245, v240, v241 op_sel:[0,0,1]
	s_nop 0
	global_store_dwordx4 v78, v[242:245], s[6:7]
	s_waitcnt vmcnt(12)
	v_mul_f32_e32 v144, v34, v144
	v_mul_f32_e32 v145, v34, v145
	v_mul_f32_e32 v146, v34, v146
	v_mul_f32_e32 v147, v34, v147
	ds_write_b128 v209, v[144:147]
	v_mul_f32_e32 v148, v35, v148
	v_mul_f32_e32 v149, v35, v149
	v_mul_f32_e32 v150, v35, v150
	v_mul_f32_e32 v151, v35, v151
	ds_write_b128 v209, v[148:151] offset:1024
	v_mul_f32_e32 v152, v36, v152
	v_mul_f32_e32 v153, v36, v153
	v_mul_f32_e32 v154, v36, v154
	v_mul_f32_e32 v155, v36, v155
	ds_write_b128 v209, v[152:155] offset:2048
	v_mul_f32_e32 v156, v37, v156
	v_mul_f32_e32 v157, v37, v157
	v_mul_f32_e32 v158, v37, v158
	v_mul_f32_e32 v159, v37, v159
	ds_write_b128 v209, v[156:159] offset:3072
	v_mul_f32_e32 v160, v38, v160
	v_mul_f32_e32 v161, v38, v161
	v_mul_f32_e32 v162, v38, v162
	v_mul_f32_e32 v163, v38, v163
	ds_write_b128 v209, v[160:163] offset:4096
	v_mul_f32_e32 v164, v39, v164
	v_mul_f32_e32 v165, v39, v165
	v_mul_f32_e32 v166, v39, v166
	v_mul_f32_e32 v167, v39, v167
	ds_write_b128 v209, v[164:167] offset:5120
	v_mul_f32_e32 v168, v40, v168
	v_mul_f32_e32 v169, v40, v169
	v_mul_f32_e32 v170, v40, v170
	v_mul_f32_e32 v171, v40, v171
	ds_write_b128 v209, v[168:171] offset:6144
	v_mul_f32_e32 v172, v41, v172
	v_mul_f32_e32 v173, v41, v173
	v_mul_f32_e32 v174, v41, v174
	v_mul_f32_e32 v175, v41, v175
	ds_write_b128 v209, v[172:175] offset:7168
	s_waitcnt lgkmcnt(0)
	s_barrier
; #define GAS __attribute__((address_space(1)))
; #define LAS __attribute__((address_space(3)))
; #define LDS_WAIT() asm volatile("s_waitcnt lgkmcnt(0)" ::: "memory")
; __device__ __forceinline__ unsigned pk4_fp8(float a, float b, float c, float d) {
;     a = fminf(fmaxf(a, -448.f), 448.f); b = fminf(fmaxf(b, -448.f), 448.f); c = fminf(fmaxf(c, -448.f), 448.f); d = fminf(fmaxf(d, -448.f), 448.f);
;     int w = __builtin_amdgcn_cvt_pk_fp8_f32(a, b, 0, false); w = __builtin_amdgcn_cvt_pk_fp8_f32(c, d, w, true); return (unsigned)w; }
;     ...
; #pragma unroll
;     for (int i = 0; i < 32; ++i) v[i] = sc >= 0 ? W[(size_t)(k0 + 2 * i + (lane >> 5)) * Nsrc + sc] : 0.f;
; #pragma unroll
;     for (int i = 0; i < 32; ++i) { const int k = k0 + 2 * i + (lane >> 5); float x = v[i] * wscale; if (KS) x *= (k < ksplit ? ksA[k] : ksB[k - ksplit]); scr[(2 * i + (lane >> 5)) * 33 + (lane & 31)] = x; }
;     LDS_WAIT(); asm volatile("" ::: "memory");
;     const int c = lane & 7;
; #pragma unroll
;     for (int j = 0; j < 4; ++j) { const int n = (lane >> 3) + 8 * j; const LAS float* s = scr + (8 * c) * 33 + n;
;         const unsigned long long o = (unsigned long long)pg8::pk4_fp8(s[0 * 33], s[1 * 33], s[2 * 33], s[3 * 33]) | ((unsigned long long)pg8::pk4_fp8(s[4 * 33], s[5 * 33], s[6 * 33], s[7 * 33]) << 32);
;         *(GAS unsigned long long*)(WT + (size_t)(n0 + n) * K + k0 + 8 * c) = o; }
	s_add_u32 s8, s34, 0xc000
	s_addc_u32 s9, s35, 0
	global_load_dwordx4 v[144:147], v74, s[8:9]
	s_add_u32 s8, s8, 0x20000
	s_addc_u32 s9, s9, 0
	global_load_dwordx4 v[148:151], v74, s[8:9]
	s_add_u32 s8, s8, 0x20000
	s_addc_u32 s9, s9, 0
	global_load_dwordx4 v[152:155], v74, s[8:9]
	s_add_u32 s8, s8, 0x20000
	s_addc_u32 s9, s9, 0
	global_load_dwordx4 v[156:159], v74, s[8:9]
	s_add_u32 s8, s8, 0x20000
	s_addc_u32 s9, s9, 0
	global_load_dwordx4 v[160:163], v74, s[8:9]
	s_add_u32 s8, s8, 0x20000
	s_addc_u32 s9, s9, 0
	global_load_dwordx4 v[164:167], v74, s[8:9]
	s_add_u32 s8, s8, 0x20000
	s_addc_u32 s9, s9, 0
	global_load_dwordx4 v[168:171], v74, s[8:9]
	s_add_u32 s8, s8, 0x20000
	s_addc_u32 s9, s9, 0
	global_load_dwordx4 v[172:175], v74, s[8:9]
	s_add_u32 s6, s36, 0x2800000
	s_addc_u32 s7, s37, 0
	ds_read_b32 v226, v211
	ds_read_b32 v227, v211 offset:512
	ds_read_b32 v228, v211 offset:1024
	ds_read_b32 v229, v211 offset:1536
	ds_read_b32 v230, v211 offset:2048
	ds_read_b32 v231, v211 offset:2560
	ds_read_b32 v232, v211 offset:3072
	ds_read_b32 v233, v211 offset:3584
	ds_read_b32 v234, v211 offset:4096
	ds_read_b32 v235, v211 offset:4608
	ds_read_b32 v236, v211 offset:5120
	ds_read_b32 v237, v211 offset:5632
	ds_read_b32 v238, v211 offset:6144
	ds_read_b32 v239, v211 offset:6656
	ds_read_b32 v240, v211 offset:7168
	ds_read_b32 v241, v211 offset:7680
	s_waitcnt lgkmcnt(0)
	v_max_f32_e32 v226, v226, v226
	v_max_f32_e32 v227, v227, v227
	v_max_f32_e32 v228, v228, v228
	v_max_f32_e32 v229, v229, v229
	v_max_f32_e32 v230, v230, v230
	v_max_f32_e32 v231, v231, v231
	v_max_f32_e32 v232, v232, v232
	v_max_f32_e32 v233, v233, v233
	v_max_f32_e32 v234, v234, v234
	v_max_f32_e32 v235, v235, v235
	v_max_f32_e32 v236, v236, v236
	v_max_f32_e32 v237, v237, v237
	v_max_f32_e32 v238, v238, v238
	v_max_f32_e32 v239, v239, v239
	v_max_f32_e32 v240, v240, v240
	v_max_f32_e32 v241, v241, v241
	v_med3_f32 v226, v226, s62, v95
	v_med3_f32 v227, v227, s62, v95
	v_med3_f32 v228, v228, s62, v95
	v_med3_f32 v229, v229, s62, v95
	v_med3_f32 v230, v230, s62, v95
	v_med3_f32 v231, v231, s62, v95
	v_med3_f32 v232, v232, s62, v95
	v_med3_f32 v233, v233, s62, v95
	v_med3_f32 v234, v234, s62, v95
	v_med3_f32 v235, v235, s62, v95
	v_med3_f32 v236, v236, s62, v95
	v_med3_f32 v237, v237, s62, v95
	v_med3_f32 v238, v238, s62, v95
	v_med3_f32 v239, v239, s62, v95
	v_med3_f32 v240, v240, s62, v95
	v_med3_f32 v241, v241, s62, v95
	v_mov_b32_e32 v242, 0
	v_mov_b32_e32 v243, 0
	v_mov_b32_e32 v244, 0
	v_mov_b32_e32 v245, 0
	v_cvt_pk_fp8_f32 v242, v226, v227
	v_cvt_pk_fp8_f32 v243, v230, v231
	v_cvt_pk_fp8_f32 v244, v234, v235
	v_cvt_pk_fp8_f32 v245, v238, v239
	v_cvt_pk_fp8_f32 v242, v228, v229 op_sel:[0,0,1]
	v_cvt_pk_fp8_f32 v243, v232, v233 op_sel:[0,0,1]
	v_cvt_pk_fp8_f32 v244, v236, v237 op_sel:[0,0,1]
	v_cvt_pk_fp8_f32 v245, v240, v241 op_sel:[0,0,1]
	s_nop 0
	global_store_dwordx4 v77, v[242:245], s[6:7]
	ds_read_b32 v226, v213
	ds_read_b32 v227, v213 offset:512
	ds_read_b32 v228, v213 offset:1024
	ds_read_b32 v229, v213 offset:1536
	ds_read_b32 v230, v213 offset:2048
	ds_read_b32 v231, v213 offset:2560
	ds_read_b32 v232, v213 offset:3072
	ds_read_b32 v233, v213 offset:3584
	ds_read_b32 v234, v213 offset:4096
	ds_read_b32 v235, v213 offset:4608
	ds_read_b32 v236, v213 offset:5120
	ds_read_b32 v237, v213 offset:5632
	ds_read_b32 v238, v213 offset:6144
	ds_read_b32 v239, v213 offset:6656
	ds_read_b32 v240, v213 offset:7168
	ds_read_b32 v241, v213 offset:7680
	s_waitcnt lgkmcnt(0)
	v_max_f32_e32 v226, v226, v226
	v_max_f32_e32 v227, v227, v227
	v_max_f32_e32 v228, v228, v228
	v_max_f32_e32 v229, v229, v229
	v_max_f32_e32 v230, v230, v230
	v_max_f32_e32 v231, v231, v231
	v_max_f32_e32 v232, v232, v232
	v_max_f32_e32 v233, v233, v233
	v_max_f32_e32 v234, v234, v234
	v_max_f32_e32 v235, v235, v235
	v_max_f32_e32 v236, v236, v236
	v_max_f32_e32 v237, v237, v237
	v_max_f32_e32 v238, v238, v238
	v_max_f32_e32 v239, v239, v239
	v_max_f32_e32 v240, v240, v240
	v_max_f32_e32 v241, v241, v241
	v_med3_f32 v226, v226, s62, v95
	v_med3_f32 v227, v227, s62, v95
	v_med3_f32 v228, v228, s62, v95
	v_med3_f32 v229, v229, s62, v95
	v_med3_f32 v230, v230, s62, v95
	v_med3_f32 v231, v231, s62, v95
	v_med3_f32 v232, v232, s62, v95
	v_med3_f32 v233, v233, s62, v95
	v_med3_f32 v234, v234, s62, v95
	v_med3_f32 v235, v235, s62, v95
	v_med3_f32 v236, v236, s62, v95
	v_med3_f32 v237, v237, s62, v95
	v_med3_f32 v238, v238, s62, v95
	v_med3_f32 v239, v239, s62, v95
	v_med3_f32 v240, v240, s62, v95
	v_med3_f32 v241, v241, s62, v95
	v_mov_b32_e32 v242, 0
	v_mov_b32_e32 v243, 0
	v_mov_b32_e32 v244, 0
	v_mov_b32_e32 v245, 0
	v_cvt_pk_fp8_f32 v242, v226, v227
	v_cvt_pk_fp8_f32 v243, v230, v231
	v_cvt_pk_fp8_f32 v244, v234, v235
	v_cvt_pk_fp8_f32 v245, v238, v239
	v_cvt_pk_fp8_f32 v242, v228, v229 op_sel:[0,0,1]
	v_cvt_pk_fp8_f32 v243, v232, v233 op_sel:[0,0,1]
	v_cvt_pk_fp8_f32 v244, v236, v237 op_sel:[0,0,1]
	v_cvt_pk_fp8_f32 v245, v240, v241 op_sel:[0,0,1]
	s_nop 0
	global_store_dwordx4 v78, v[242:245], s[6:7]
	s_waitcnt vmcnt(12)
	v_mul_f32_e32 v176, v34, v176
	v_mul_f32_e32 v177, v34, v177
	v_mul_f32_e32 v178, v34, v178
	v_mul_f32_e32 v179, v34, v179
	ds_write_b128 v210, v[176:179]
	v_mul_f32_e32 v180, v35, v180
	v_mul_f32_e32 v181, v35, v181
	v_mul_f32_e32 v182, v35, v182
	v_mul_f32_e32 v183, v35, v183
	ds_write_b128 v210, v[180:183] offset:1024
	v_mul_f32_e32 v184, v36, v184
	v_mul_f32_e32 v185, v36, v185
	v_mul_f32_e32 v186, v36, v186
	v_mul_f32_e32 v187, v36, v187
	ds_write_b128 v210, v[184:187] offset:2048
	v_mul_f32_e32 v188, v37, v188
	v_mul_f32_e32 v189, v37, v189
	v_mul_f32_e32 v190, v37, v190
	v_mul_f32_e32 v191, v37, v191
	ds_write_b128 v210, v[188:191] offset:3072
	v_mul_f32_e32 v192, v38, v192
	v_mul_f32_e32 v193, v38, v193
	v_mul_f32_e32 v194, v38, v194
	v_mul_f32_e32 v195, v38, v195
	ds_write_b128 v210, v[192:195] offset:4096
	v_mul_f32_e32 v196, v39, v196
	v_mul_f32_e32 v197, v39, v197
	v_mul_f32_e32 v198, v39, v198
	v_mul_f32_e32 v199, v39, v199
	ds_write_b128 v210, v[196:199] offset:5120
	v_mul_f32_e32 v200, v40, v200
	v_mul_f32_e32 v201, v40, v201
	v_mul_f32_e32 v202, v40, v202
	v_mul_f32_e32 v203, v40, v203
	ds_write_b128 v210, v[200:203] offset:6144
	v_mul_f32_e32 v204, v41, v204
	v_mul_f32_e32 v205, v41, v205
	v_mul_f32_e32 v206, v41, v206
	v_mul_f32_e32 v207, v41, v207
	ds_write_b128 v210, v[204:207] offset:7168
	s_waitcnt lgkmcnt(0)
	s_barrier
; #define GAS __attribute__((address_space(1)))
; #define LAS __attribute__((address_space(3)))
; #define LDS_WAIT() asm volatile("s_waitcnt lgkmcnt(0)" ::: "memory")
; __device__ __forceinline__ unsigned pk4_fp8(float a, float b, float c, float d) {
;     a = fminf(fmaxf(a, -448.f), 448.f); b = fminf(fmaxf(b, -448.f), 448.f); c = fminf(fmaxf(c, -448.f), 448.f); d = fminf(fmaxf(d, -448.f), 448.f);
;     int w = __builtin_amdgcn_cvt_pk_fp8_f32(a, b, 0, false); w = __builtin_amdgcn_cvt_pk_fp8_f32(c, d, w, true); return (unsigned)w; }
;     ...
; #pragma unroll
;     for (int i = 0; i < 32; ++i) v[i] = sc >= 0 ? W[(size_t)(k0 + 2 * i + (lane >> 5)) * Nsrc + sc] : 0.f;
; #pragma unroll
;     for (int i = 0; i < 32; ++i) { const int k = k0 + 2 * i + (lane >> 5); float x = v[i] * wscale; if (KS) x *= (k < ksplit ? ksA[k] : ksB[k - ksplit]); scr[(2 * i + (lane >> 5)) * 33 + (lane & 31)] = x; }
;     LDS_WAIT(); asm volatile("" ::: "memory");
;     const int c = lane & 7;
; #pragma unroll
;     for (int j = 0; j < 4; ++j) { const int n = (lane >> 3) + 8 * j; const LAS float* s = scr + (8 * c) * 33 + n;
;         const unsigned long long o = (unsigned long long)pg8::pk4_fp8(s[0 * 33], s[1 * 33], s[2 * 33], s[3 * 33]) | ((unsigned long long)pg8::pk4_fp8(s[4 * 33], s[5 * 33], s[6 * 33], s[7 * 33]) << 32);
;         *(GAS unsigned long long*)(WT + (size_t)(n0 + n) * K + k0 + 8 * c) = o; }
	s_add_u32 s8, s34, 0xd000
	s_addc_u32 s9, s35, 0
	global_load_dwordx4 v[176:179], v74, s[8:9]
	s_add_u32 s8, s8, 0x20000
	s_addc_u32 s9, s9, 0
	global_load_dwordx4 v[180:183], v74, s[8:9]
	s_add_u32 s8, s8, 0x20000
	s_addc_u32 s9, s9, 0
	global_load_dwordx4 v[184:187], v74, s[8:9]
	s_add_u32 s8, s8, 0x20000
	s_addc_u32 s9, s9, 0
	global_load_dwordx4 v[188:191], v74, s[8:9]
	s_add_u32 s8, s8, 0x20000
	s_addc_u32 s9, s9, 0
	global_load_dwordx4 v[192:195], v74, s[8:9]
	s_add_u32 s8, s8, 0x20000
	s_addc_u32 s9, s9, 0
	global_load_dwordx4 v[196:199], v74, s[8:9]
	s_add_u32 s8, s8, 0x20000
	s_addc_u32 s9, s9, 0
	global_load_dwordx4 v[200:203], v74, s[8:9]
	s_add_u32 s8, s8, 0x20000
	s_addc_u32 s9, s9, 0
	global_load_dwordx4 v[204:207], v74, s[8:9]
	s_add_u32 s6, s36, 0x2c00000
	s_addc_u32 s7, s37, 0
	ds_read_b32 v226, v212
	ds_read_b32 v227, v212 offset:512
	ds_read_b32 v228, v212 offset:1024
	ds_read_b32 v229, v212 offset:1536
	ds_read_b32 v230, v212 offset:2048
	ds_read_b32 v231, v212 offset:2560
	ds_read_b32 v232, v212 offset:3072
	ds_read_b32 v233, v212 offset:3584
	ds_read_b32 v234, v212 offset:4096
	ds_read_b32 v235, v212 offset:4608
	ds_read_b32 v236, v212 offset:5120
	ds_read_b32 v237, v212 offset:5632
	ds_read_b32 v238, v212 offset:6144
	ds_read_b32 v239, v212 offset:6656
	ds_read_b32 v240, v212 offset:7168
	ds_read_b32 v241, v212 offset:7680
	s_waitcnt lgkmcnt(0)
	v_max_f32_e32 v226, v226, v226
	v_max_f32_e32 v227, v227, v227
	v_max_f32_e32 v228, v228, v228
	v_max_f32_e32 v229, v229, v229
	v_max_f32_e32 v230, v230, v230
	v_max_f32_e32 v231, v231, v231
	v_max_f32_e32 v232, v232, v232
	v_max_f32_e32 v233, v233, v233
	v_max_f32_e32 v234, v234, v234
	v_max_f32_e32 v235, v235, v235
	v_max_f32_e32 v236, v236, v236
	v_max_f32_e32 v237, v237, v237
	v_max_f32_e32 v238, v238, v238
	v_max_f32_e32 v239, v239, v239
	v_max_f32_e32 v240, v240, v240
	v_max_f32_e32 v241, v241, v241
	v_med3_f32 v226, v226, s62, v95
	v_med3_f32 v227, v227, s62, v95
	v_med3_f32 v228, v228, s62, v95
	v_med3_f32 v229, v229, s62, v95
	v_med3_f32 v230, v230, s62, v95
	v_med3_f32 v231, v231, s62, v95
	v_med3_f32 v232, v232, s62, v95
	v_med3_f32 v233, v233, s62, v95
	v_med3_f32 v234, v234, s62, v95
	v_med3_f32 v235, v235, s62, v95
	v_med3_f32 v236, v236, s62, v95
	v_med3_f32 v237, v237, s62, v95
	v_med3_f32 v238, v238, s62, v95
	v_med3_f32 v239, v239, s62, v95
	v_med3_f32 v240, v240, s62, v95
	v_med3_f32 v241, v241, s62, v95
	v_mov_b32_e32 v242, 0
	v_mov_b32_e32 v243, 0
	v_mov_b32_e32 v244, 0
	v_mov_b32_e32 v245, 0
	v_cvt_pk_fp8_f32 v242, v226, v227
	v_cvt_pk_fp8_f32 v243, v230, v231
	v_cvt_pk_fp8_f32 v244, v234, v235
	v_cvt_pk_fp8_f32 v245, v238, v239
	v_cvt_pk_fp8_f32 v242, v228, v229 op_sel:[0,0,1]
	v_cvt_pk_fp8_f32 v243, v232, v233 op_sel:[0,0,1]
	v_cvt_pk_fp8_f32 v244, v236, v237 op_sel:[0,0,1]
	v_cvt_pk_fp8_f32 v245, v240, v241 op_sel:[0,0,1]
	s_nop 0
	global_store_dwordx4 v77, v[242:245], s[6:7]
	ds_read_b32 v226, v214
	ds_read_b32 v227, v214 offset:512
	ds_read_b32 v228, v214 offset:1024
	ds_read_b32 v229, v214 offset:1536
	ds_read_b32 v230, v214 offset:2048
	ds_read_b32 v231, v214 offset:2560
	ds_read_b32 v232, v214 offset:3072
	ds_read_b32 v233, v214 offset:3584
	ds_read_b32 v234, v214 offset:4096
	ds_read_b32 v235, v214 offset:4608
	ds_read_b32 v236, v214 offset:5120
	ds_read_b32 v237, v214 offset:5632
	ds_read_b32 v238, v214 offset:6144
	ds_read_b32 v239, v214 offset:6656
	ds_read_b32 v240, v214 offset:7168
	ds_read_b32 v241, v214 offset:7680
	s_waitcnt lgkmcnt(0)
	v_max_f32_e32 v226, v226, v226
	v_max_f32_e32 v227, v227, v227
	v_max_f32_e32 v228, v228, v228
	v_max_f32_e32 v229, v229, v229
	v_max_f32_e32 v230, v230, v230
	v_max_f32_e32 v231, v231, v231
	v_max_f32_e32 v232, v232, v232
	v_max_f32_e32 v233, v233, v233
	v_max_f32_e32 v234, v234, v234
	v_max_f32_e32 v235, v235, v235
	v_max_f32_e32 v236, v236, v236
	v_max_f32_e32 v237, v237, v237
	v_max_f32_e32 v238, v238, v238
	v_max_f32_e32 v239, v239, v239
	v_max_f32_e32 v240, v240, v240
	v_max_f32_e32 v241, v241, v241
	v_med3_f32 v226, v226, s62, v95
	v_med3_f32 v227, v227, s62, v95
	v_med3_f32 v228, v228, s62, v95
	v_med3_f32 v229, v229, s62, v95
	v_med3_f32 v230, v230, s62, v95
	v_med3_f32 v231, v231, s62, v95
	v_med3_f32 v232, v232, s62, v95
	v_med3_f32 v233, v233, s62, v95
	v_med3_f32 v234, v234, s62, v95
	v_med3_f32 v235, v235, s62, v95
	v_med3_f32 v236, v236, s62, v95
	v_med3_f32 v237, v237, s62, v95
	v_med3_f32 v238, v238, s62, v95
	v_med3_f32 v239, v239, s62, v95
	v_med3_f32 v240, v240, s62, v95
	v_med3_f32 v241, v241, s62, v95
	v_mov_b32_e32 v242, 0
	v_mov_b32_e32 v243, 0
	v_mov_b32_e32 v244, 0
	v_mov_b32_e32 v245, 0
	v_cvt_pk_fp8_f32 v242, v226, v227
	v_cvt_pk_fp8_f32 v243, v230, v231
	v_cvt_pk_fp8_f32 v244, v234, v235
	v_cvt_pk_fp8_f32 v245, v238, v239
	v_cvt_pk_fp8_f32 v242, v228, v229 op_sel:[0,0,1]
	v_cvt_pk_fp8_f32 v243, v232, v233 op_sel:[0,0,1]
	v_cvt_pk_fp8_f32 v244, v236, v237 op_sel:[0,0,1]
	v_cvt_pk_fp8_f32 v245, v240, v241 op_sel:[0,0,1]
	s_nop 0
	global_store_dwordx4 v78, v[242:245], s[6:7]
	s_waitcnt vmcnt(12)
	v_mul_f32_e32 v144, v34, v144
	v_mul_f32_e32 v145, v34, v145
	v_mul_f32_e32 v146, v34, v146
	v_mul_f32_e32 v147, v34, v147
	ds_write_b128 v209, v[144:147]
	v_mul_f32_e32 v148, v35, v148
	v_mul_f32_e32 v149, v35, v149
	v_mul_f32_e32 v150, v35, v150
	v_mul_f32_e32 v151, v35, v151
	ds_write_b128 v209, v[148:151] offset:1024
	v_mul_f32_e32 v152, v36, v152
	v_mul_f32_e32 v153, v36, v153
	v_mul_f32_e32 v154, v36, v154
	v_mul_f32_e32 v155, v36, v155
	ds_write_b128 v209, v[152:155] offset:2048
	v_mul_f32_e32 v156, v37, v156
	v_mul_f32_e32 v157, v37, v157
	v_mul_f32_e32 v158, v37, v158
	v_mul_f32_e32 v159, v37, v159
	ds_write_b128 v209, v[156:159] offset:3072
	v_mul_f32_e32 v160, v38, v160
	v_mul_f32_e32 v161, v38, v161
	v_mul_f32_e32 v162, v38, v162
	v_mul_f32_e32 v163, v38, v163
	ds_write_b128 v209, v[160:163] offset:4096
	v_mul_f32_e32 v164, v39, v164
	v_mul_f32_e32 v165, v39, v165
	v_mul_f32_e32 v166, v39, v166
	v_mul_f32_e32 v167, v39, v167
	ds_write_b128 v209, v[164:167] offset:5120
	v_mul_f32_e32 v168, v40, v168
	v_mul_f32_e32 v169, v40, v169
	v_mul_f32_e32 v170, v40, v170
	v_mul_f32_e32 v171, v40, v171
	ds_write_b128 v209, v[168:171] offset:6144
	v_mul_f32_e32 v172, v41, v172
	v_mul_f32_e32 v173, v41, v173
	v_mul_f32_e32 v174, v41, v174
	v_mul_f32_e32 v175, v41, v175
	ds_write_b128 v209, v[172:175] offset:7168
	s_waitcnt lgkmcnt(0)
	s_barrier
; #define GAS __attribute__((address_space(1)))
; #define LAS __attribute__((address_space(3)))
; #define LDS_WAIT() asm volatile("s_waitcnt lgkmcnt(0)" ::: "memory")
; __device__ __forceinline__ unsigned pk4_fp8(float a, float b, float c, float d) {
;     a = fminf(fmaxf(a, -448.f), 448.f); b = fminf(fmaxf(b, -448.f), 448.f); c = fminf(fmaxf(c, -448.f), 448.f); d = fminf(fmaxf(d, -448.f), 448.f);
;     int w = __builtin_amdgcn_cvt_pk_fp8_f32(a, b, 0, false); w = __builtin_amdgcn_cvt_pk_fp8_f32(c, d, w, true); return (unsigned)w; }
;     ...
; #pragma unroll
;     for (int i = 0; i < 32; ++i) v[i] = sc >= 0 ? W[(size_t)(k0 + 2 * i + (lane >> 5)) * Nsrc + sc] : 0.f;
; #pragma unroll
;     for (int i = 0; i < 32; ++i) { const int k = k0 + 2 * i + (lane >> 5); float x = v[i] * wscale; if (KS) x *= (k < ksplit ? ksA[k] : ksB[k - ksplit]); scr[(2 * i + (lane >> 5)) * 33 + (lane & 31)] = x; }
;     LDS_WAIT(); asm volatile("" ::: "memory");
;     const int c = lane & 7;
; #pragma unroll
;     for (int j = 0; j < 4; ++j) { const int n = (lane >> 3) + 8 * j; const LAS float* s = scr + (8 * c) * 33 + n;
;         const unsigned long long o = (unsigned long long)pg8::pk4_fp8(s[0 * 33], s[1 * 33], s[2 * 33], s[3 * 33]) | ((unsigned long long)pg8::pk4_fp8(s[4 * 33], s[5 * 33], s[6 * 33], s[7 * 33]) << 32);
;         *(GAS unsigned long long*)(WT + (size_t)(n0 + n) * K + k0 + 8 * c) = o; }
	s_add_u32 s8, s34, 0xe000
	s_addc_u32 s9, s35, 0
	global_load_dwordx4 v[144:147], v74, s[8:9]
	s_add_u32 s8, s8, 0x20000
	s_addc_u32 s9, s9, 0
	global_load_dwordx4 v[148:151], v74, s[8:9]
	s_add_u32 s8, s8, 0x20000
	s_addc_u32 s9, s9, 0
	global_load_dwordx4 v[152:155], v74, s[8:9]
	s_add_u32 s8, s8, 0x20000
	s_addc_u32 s9, s9, 0
	global_load_dwordx4 v[156:159], v74, s[8:9]
	s_add_u32 s8, s8, 0x20000
	s_addc_u32 s9, s9, 0
	global_load_dwordx4 v[160:163], v74, s[8:9]
	s_add_u32 s8, s8, 0x20000
	s_addc_u32 s9, s9, 0
	global_load_dwordx4 v[164:167], v74, s[8:9]
	s_add_u32 s8, s8, 0x20000
	s_addc_u32 s9, s9, 0
	global_load_dwordx4 v[168:171], v74, s[8:9]
	s_add_u32 s8, s8, 0x20000
	s_addc_u32 s9, s9, 0
	global_load_dwordx4 v[172:175], v74, s[8:9]
	s_add_u32 s6, s36, 0x3000000
	s_addc_u32 s7, s37, 0
	ds_read_b32 v226, v211
	ds_read_b32 v227, v211 offset:512
	ds_read_b32 v228, v211 offset:1024
	ds_read_b32 v229, v211 offset:1536
	ds_read_b32 v230, v211 offset:2048
	ds_read_b32 v231, v211 offset:2560
	ds_read_b32 v232, v211 offset:3072
	ds_read_b32 v233, v211 offset:3584
	ds_read_b32 v234, v211 offset:4096
	ds_read_b32 v235, v211 offset:4608
	ds_read_b32 v236, v211 offset:5120
	ds_read_b32 v237, v211 offset:5632
	ds_read_b32 v238, v211 offset:6144
	ds_read_b32 v239, v211 offset:6656
	ds_read_b32 v240, v211 offset:7168
	ds_read_b32 v241, v211 offset:7680
	s_waitcnt lgkmcnt(0)
	v_max_f32_e32 v226, v226, v226
	v_max_f32_e32 v227, v227, v227
	v_max_f32_e32 v228, v228, v228
	v_max_f32_e32 v229, v229, v229
	v_max_f32_e32 v230, v230, v230
	v_max_f32_e32 v231, v231, v231
	v_max_f32_e32 v232, v232, v232
	v_max_f32_e32 v233, v233, v233
	v_max_f32_e32 v234, v234, v234
	v_max_f32_e32 v235, v235, v235
	v_max_f32_e32 v236, v236, v236
	v_max_f32_e32 v237, v237, v237
	v_max_f32_e32 v238, v238, v238
	v_max_f32_e32 v239, v239, v239
	v_max_f32_e32 v240, v240, v240
	v_max_f32_e32 v241, v241, v241
	v_med3_f32 v226, v226, s62, v95
	v_med3_f32 v227, v227, s62, v95
	v_med3_f32 v228, v228, s62, v95
	v_med3_f32 v229, v229, s62, v95
	v_med3_f32 v230, v230, s62, v95
	v_med3_f32 v231, v231, s62, v95
	v_med3_f32 v232, v232, s62, v95
	v_med3_f32 v233, v233, s62, v95
	v_med3_f32 v234, v234, s62, v95
	v_med3_f32 v235, v235, s62, v95
	v_med3_f32 v236, v236, s62, v95
	v_med3_f32 v237, v237, s62, v95
	v_med3_f32 v238, v238, s62, v95
	v_med3_f32 v239, v239, s62, v95
	v_med3_f32 v240, v240, s62, v95
	v_med3_f32 v241, v241, s62, v95
	v_mov_b32_e32 v242, 0
	v_mov_b32_e32 v243, 0
	v_mov_b32_e32 v244, 0
	v_mov_b32_e32 v245, 0
	v_cvt_pk_fp8_f32 v242, v226, v227
	v_cvt_pk_fp8_f32 v243, v230, v231
	v_cvt_pk_fp8_f32 v244, v234, v235
	v_cvt_pk_fp8_f32 v245, v238, v239
	v_cvt_pk_fp8_f32 v242, v228, v229 op_sel:[0,0,1]
	v_cvt_pk_fp8_f32 v243, v232, v233 op_sel:[0,0,1]
	v_cvt_pk_fp8_f32 v244, v236, v237 op_sel:[0,0,1]
	v_cvt_pk_fp8_f32 v245, v240, v241 op_sel:[0,0,1]
	s_nop 0
	global_store_dwordx4 v77, v[242:245], s[6:7]
	ds_read_b32 v226, v213
	ds_read_b32 v227, v213 offset:512
	ds_read_b32 v228, v213 offset:1024
	ds_read_b32 v229, v213 offset:1536
	ds_read_b32 v230, v213 offset:2048
	ds_read_b32 v231, v213 offset:2560
	ds_read_b32 v232, v213 offset:3072
	ds_read_b32 v233, v213 offset:3584
	ds_read_b32 v234, v213 offset:4096
	ds_read_b32 v235, v213 offset:4608
	ds_read_b32 v236, v213 offset:5120
	ds_read_b32 v237, v213 offset:5632
	ds_read_b32 v238, v213 offset:6144
	ds_read_b32 v239, v213 offset:6656
	ds_read_b32 v240, v213 offset:7168
	ds_read_b32 v241, v213 offset:7680
	s_waitcnt lgkmcnt(0)
	v_max_f32_e32 v226, v226, v226
	v_max_f32_e32 v227, v227, v227
	v_max_f32_e32 v228, v228, v228
	v_max_f32_e32 v229, v229, v229
	v_max_f32_e32 v230, v230, v230
	v_max_f32_e32 v231, v231, v231
	v_max_f32_e32 v232, v232, v232
	v_max_f32_e32 v233, v233, v233
	v_max_f32_e32 v234, v234, v234
	v_max_f32_e32 v235, v235, v235
	v_max_f32_e32 v236, v236, v236
	v_max_f32_e32 v237, v237, v237
	v_max_f32_e32 v238, v238, v238
	v_max_f32_e32 v239, v239, v239
	v_max_f32_e32 v240, v240, v240
	v_max_f32_e32 v241, v241, v241
	v_med3_f32 v226, v226, s62, v95
	v_med3_f32 v227, v227, s62, v95
	v_med3_f32 v228, v228, s62, v95
	v_med3_f32 v229, v229, s62, v95
	v_med3_f32 v230, v230, s62, v95
	v_med3_f32 v231, v231, s62, v95
	v_med3_f32 v232, v232, s62, v95
	v_med3_f32 v233, v233, s62, v95
	v_med3_f32 v234, v234, s62, v95
	v_med3_f32 v235, v235, s62, v95
	v_med3_f32 v236, v236, s62, v95
	v_med3_f32 v237, v237, s62, v95
	v_med3_f32 v238, v238, s62, v95
	v_med3_f32 v239, v239, s62, v95
	v_med3_f32 v240, v240, s62, v95
	v_med3_f32 v241, v241, s62, v95
	v_mov_b32_e32 v242, 0
	v_mov_b32_e32 v243, 0
	v_mov_b32_e32 v244, 0
	v_mov_b32_e32 v245, 0
	v_cvt_pk_fp8_f32 v242, v226, v227
	v_cvt_pk_fp8_f32 v243, v230, v231
	v_cvt_pk_fp8_f32 v244, v234, v235
	v_cvt_pk_fp8_f32 v245, v238, v239
	v_cvt_pk_fp8_f32 v242, v228, v229 op_sel:[0,0,1]
	v_cvt_pk_fp8_f32 v243, v232, v233 op_sel:[0,0,1]
	v_cvt_pk_fp8_f32 v244, v236, v237 op_sel:[0,0,1]
	v_cvt_pk_fp8_f32 v245, v240, v241 op_sel:[0,0,1]
	s_nop 0
	global_store_dwordx4 v78, v[242:245], s[6:7]
	s_waitcnt vmcnt(12)
	v_mul_f32_e32 v176, v34, v176
	v_mul_f32_e32 v177, v34, v177
	v_mul_f32_e32 v178, v34, v178
	v_mul_f32_e32 v179, v34, v179
	ds_write_b128 v210, v[176:179]
	v_mul_f32_e32 v180, v35, v180
	v_mul_f32_e32 v181, v35, v181
	v_mul_f32_e32 v182, v35, v182
	v_mul_f32_e32 v183, v35, v183
	ds_write_b128 v210, v[180:183] offset:1024
	v_mul_f32_e32 v184, v36, v184
	v_mul_f32_e32 v185, v36, v185
	v_mul_f32_e32 v186, v36, v186
	v_mul_f32_e32 v187, v36, v187
	ds_write_b128 v210, v[184:187] offset:2048
	v_mul_f32_e32 v188, v37, v188
	v_mul_f32_e32 v189, v37, v189
	v_mul_f32_e32 v190, v37, v190
	v_mul_f32_e32 v191, v37, v191
	ds_write_b128 v210, v[188:191] offset:3072
	v_mul_f32_e32 v192, v38, v192
	v_mul_f32_e32 v193, v38, v193
	v_mul_f32_e32 v194, v38, v194
	v_mul_f32_e32 v195, v38, v195
	ds_write_b128 v210, v[192:195] offset:4096
	v_mul_f32_e32 v196, v39, v196
	v_mul_f32_e32 v197, v39, v197
	v_mul_f32_e32 v198, v39, v198
	v_mul_f32_e32 v199, v39, v199
	ds_write_b128 v210, v[196:199] offset:5120
	v_mul_f32_e32 v200, v40, v200
	v_mul_f32_e32 v201, v40, v201
	v_mul_f32_e32 v202, v40, v202
	v_mul_f32_e32 v203, v40, v203
	ds_write_b128 v210, v[200:203] offset:6144
	v_mul_f32_e32 v204, v41, v204
	v_mul_f32_e32 v205, v41, v205
	v_mul_f32_e32 v206, v41, v206
	v_mul_f32_e32 v207, v41, v207
	ds_write_b128 v210, v[204:207] offset:7168
	s_waitcnt lgkmcnt(0)
	s_barrier
; #define GAS __attribute__((address_space(1)))
; #define LAS __attribute__((address_space(3)))
; #define LDS_WAIT() asm volatile("s_waitcnt lgkmcnt(0)" ::: "memory")
; __device__ __forceinline__ unsigned pk4_fp8(float a, float b, float c, float d) {
;     a = fminf(fmaxf(a, -448.f), 448.f); b = fminf(fmaxf(b, -448.f), 448.f); c = fminf(fmaxf(c, -448.f), 448.f); d = fminf(fmaxf(d, -448.f), 448.f);
;     int w = __builtin_amdgcn_cvt_pk_fp8_f32(a, b, 0, false); w = __builtin_amdgcn_cvt_pk_fp8_f32(c, d, w, true); return (unsigned)w; }
;     ...
; #pragma unroll
;     for (int i = 0; i < 32; ++i) v[i] = sc >= 0 ? W[(size_t)(k0 + 2 * i + (lane >> 5)) * Nsrc + sc] : 0.f;
; #pragma unroll
;     for (int i = 0; i < 32; ++i) { const int k = k0 + 2 * i + (lane >> 5); float x = v[i] * wscale; if (KS) x *= (k < ksplit ? ksA[k] : ksB[k - ksplit]); scr[(2 * i + (lane >> 5)) * 33 + (lane & 31)] = x; }
;     LDS_WAIT(); asm volatile("" ::: "memory");
;     const int c = lane & 7;
; #pragma unroll
;     for (int j = 0; j < 4; ++j) { const int n = (lane >> 3) + 8 * j; const LAS float* s = scr + (8 * c) * 33 + n;
;         const unsigned long long o = (unsigned long long)pg8::pk4_fp8(s[0 * 33], s[1 * 33], s[2 * 33], s[3 * 33]) | ((unsigned long long)pg8::pk4_fp8(s[4 * 33], s[5 * 33], s[6 * 33], s[7 * 33]) << 32);
;         *(GAS unsigned long long*)(WT + (size_t)(n0 + n) * K + k0 + 8 * c) = o; }
	s_add_u32 s8, s34, 0xf000
	s_addc_u32 s9, s35, 0
	global_load_dwordx4 v[176:179], v74, s[8:9]
	s_add_u32 s8, s8, 0x20000
	s_addc_u32 s9, s9, 0
	global_load_dwordx4 v[180:183], v74, s[8:9]
	s_add_u32 s8, s8, 0x20000
	s_addc_u32 s9, s9, 0
	global_load_dwordx4 v[184:187], v74, s[8:9]
	s_add_u32 s8, s8, 0x20000
	s_addc_u32 s9, s9, 0
	global_load_dwordx4 v[188:191], v74, s[8:9]
	s_add_u32 s8, s8, 0x20000
	s_addc_u32 s9, s9, 0
	global_load_dwordx4 v[192:195], v74, s[8:9]
	s_add_u32 s8, s8, 0x20000
	s_addc_u32 s9, s9, 0
	global_load_dwordx4 v[196:199], v74, s[8:9]
	s_add_u32 s8, s8, 0x20000
	s_addc_u32 s9, s9, 0
	global_load_dwordx4 v[200:203], v74, s[8:9]
	s_add_u32 s8, s8, 0x20000
	s_addc_u32 s9, s9, 0
	global_load_dwordx4 v[204:207], v74, s[8:9]
	s_add_u32 s6, s36, 0x3400000
	s_addc_u32 s7, s37, 0
	ds_read_b32 v226, v212
	ds_read_b32 v227, v212 offset:512
	ds_read_b32 v228, v212 offset:1024
	ds_read_b32 v229, v212 offset:1536
	ds_read_b32 v230, v212 offset:2048
	ds_read_b32 v231, v212 offset:2560
	ds_read_b32 v232, v212 offset:3072
	ds_read_b32 v233, v212 offset:3584
	ds_read_b32 v234, v212 offset:4096
	ds_read_b32 v235, v212 offset:4608
	ds_read_b32 v236, v212 offset:5120
	ds_read_b32 v237, v212 offset:5632
	ds_read_b32 v238, v212 offset:6144
	ds_read_b32 v239, v212 offset:6656
	ds_read_b32 v240, v212 offset:7168
	ds_read_b32 v241, v212 offset:7680
	s_waitcnt lgkmcnt(0)
	v_max_f32_e32 v226, v226, v226
	v_max_f32_e32 v227, v227, v227
	v_max_f32_e32 v228, v228, v228
	v_max_f32_e32 v229, v229, v229
	v_max_f32_e32 v230, v230, v230
	v_max_f32_e32 v231, v231, v231
	v_max_f32_e32 v232, v232, v232
	v_max_f32_e32 v233, v233, v233
	v_max_f32_e32 v234, v234, v234
	v_max_f32_e32 v235, v235, v235
	v_max_f32_e32 v236, v236, v236
	v_max_f32_e32 v237, v237, v237
	v_max_f32_e32 v238, v238, v238
	v_max_f32_e32 v239, v239, v239
	v_max_f32_e32 v240, v240, v240
	v_max_f32_e32 v241, v241, v241
	v_med3_f32 v226, v226, s62, v95
	v_med3_f32 v227, v227, s62, v95
	v_med3_f32 v228, v228, s62, v95
	v_med3_f32 v229, v229, s62, v95
	v_med3_f32 v230, v230, s62, v95
	v_med3_f32 v231, v231, s62, v95
	v_med3_f32 v232, v232, s62, v95
	v_med3_f32 v233, v233, s62, v95
	v_med3_f32 v234, v234, s62, v95
	v_med3_f32 v235, v235, s62, v95
	v_med3_f32 v236, v236, s62, v95
	v_med3_f32 v237, v237, s62, v95
	v_med3_f32 v238, v238, s62, v95
	v_med3_f32 v239, v239, s62, v95
	v_med3_f32 v240, v240, s62, v95
	v_med3_f32 v241, v241, s62, v95
	v_mov_b32_e32 v242, 0
	v_mov_b32_e32 v243, 0
	v_mov_b32_e32 v244, 0
	v_mov_b32_e32 v245, 0
	v_cvt_pk_fp8_f32 v242, v226, v227
	v_cvt_pk_fp8_f32 v243, v230, v231
	v_cvt_pk_fp8_f32 v244, v234, v235
	v_cvt_pk_fp8_f32 v245, v238, v239
	v_cvt_pk_fp8_f32 v242, v228, v229 op_sel:[0,0,1]
	v_cvt_pk_fp8_f32 v243, v232, v233 op_sel:[0,0,1]
	v_cvt_pk_fp8_f32 v244, v236, v237 op_sel:[0,0,1]
	v_cvt_pk_fp8_f32 v245, v240, v241 op_sel:[0,0,1]
	s_nop 0
	global_store_dwordx4 v77, v[242:245], s[6:7]
	ds_read_b32 v226, v214
	ds_read_b32 v227, v214 offset:512
	ds_read_b32 v228, v214 offset:1024
	ds_read_b32 v229, v214 offset:1536
	ds_read_b32 v230, v214 offset:2048
	ds_read_b32 v231, v214 offset:2560
	ds_read_b32 v232, v214 offset:3072
	ds_read_b32 v233, v214 offset:3584
	ds_read_b32 v234, v214 offset:4096
	ds_read_b32 v235, v214 offset:4608
	ds_read_b32 v236, v214 offset:5120
	ds_read_b32 v237, v214 offset:5632
	ds_read_b32 v238, v214 offset:6144
	ds_read_b32 v239, v214 offset:6656
	ds_read_b32 v240, v214 offset:7168
	ds_read_b32 v241, v214 offset:7680
	s_waitcnt lgkmcnt(0)
	v_max_f32_e32 v226, v226, v226
	v_max_f32_e32 v227, v227, v227
	v_max_f32_e32 v228, v228, v228
	v_max_f32_e32 v229, v229, v229
	v_max_f32_e32 v230, v230, v230
	v_max_f32_e32 v231, v231, v231
	v_max_f32_e32 v232, v232, v232
	v_max_f32_e32 v233, v233, v233
	v_max_f32_e32 v234, v234, v234
	v_max_f32_e32 v235, v235, v235
	v_max_f32_e32 v236, v236, v236
	v_max_f32_e32 v237, v237, v237
	v_max_f32_e32 v238, v238, v238
	v_max_f32_e32 v239, v239, v239
	v_max_f32_e32 v240, v240, v240
	v_max_f32_e32 v241, v241, v241
	v_med3_f32 v226, v226, s62, v95
	v_med3_f32 v227, v227, s62, v95
	v_med3_f32 v228, v228, s62, v95
	v_med3_f32 v229, v229, s62, v95
	v_med3_f32 v230, v230, s62, v95
	v_med3_f32 v231, v231, s62, v95
	v_med3_f32 v232, v232, s62, v95
	v_med3_f32 v233, v233, s62, v95
	v_med3_f32 v234, v234, s62, v95
	v_med3_f32 v235, v235, s62, v95
	v_med3_f32 v236, v236, s62, v95
	v_med3_f32 v237, v237, s62, v95
	v_med3_f32 v238, v238, s62, v95
	v_med3_f32 v239, v239, s62, v95
	v_med3_f32 v240, v240, s62, v95
	v_med3_f32 v241, v241, s62, v95
	v_mov_b32_e32 v242, 0
	v_mov_b32_e32 v243, 0
	v_mov_b32_e32 v244, 0
	v_mov_b32_e32 v245, 0
	v_cvt_pk_fp8_f32 v242, v226, v227
	v_cvt_pk_fp8_f32 v243, v230, v231
	v_cvt_pk_fp8_f32 v244, v234, v235
	v_cvt_pk_fp8_f32 v245, v238, v239
	v_cvt_pk_fp8_f32 v242, v228, v229 op_sel:[0,0,1]
	v_cvt_pk_fp8_f32 v243, v232, v233 op_sel:[0,0,1]
	v_cvt_pk_fp8_f32 v244, v236, v237 op_sel:[0,0,1]
	v_cvt_pk_fp8_f32 v245, v240, v241 op_sel:[0,0,1]
	s_nop 0
	global_store_dwordx4 v78, v[242:245], s[6:7]
	s_waitcnt vmcnt(12)
	v_mul_f32_e32 v144, v34, v144
	v_mul_f32_e32 v145, v34, v145
	v_mul_f32_e32 v146, v34, v146
	v_mul_f32_e32 v147, v34, v147
	ds_write_b128 v209, v[144:147]
	v_mul_f32_e32 v148, v35, v148
	v_mul_f32_e32 v149, v35, v149
	v_mul_f32_e32 v150, v35, v150
	v_mul_f32_e32 v151, v35, v151
	ds_write_b128 v209, v[148:151] offset:1024
	v_mul_f32_e32 v152, v36, v152
	v_mul_f32_e32 v153, v36, v153
	v_mul_f32_e32 v154, v36, v154
	v_mul_f32_e32 v155, v36, v155
	ds_write_b128 v209, v[152:155] offset:2048
	v_mul_f32_e32 v156, v37, v156
	v_mul_f32_e32 v157, v37, v157
	v_mul_f32_e32 v158, v37, v158
	v_mul_f32_e32 v159, v37, v159
	ds_write_b128 v209, v[156:159] offset:3072
	v_mul_f32_e32 v160, v38, v160
	v_mul_f32_e32 v161, v38, v161
	v_mul_f32_e32 v162, v38, v162
	v_mul_f32_e32 v163, v38, v163
	ds_write_b128 v209, v[160:163] offset:4096
	v_mul_f32_e32 v164, v39, v164
	v_mul_f32_e32 v165, v39, v165
	v_mul_f32_e32 v166, v39, v166
	v_mul_f32_e32 v167, v39, v167
	ds_write_b128 v209, v[164:167] offset:5120
	v_mul_f32_e32 v168, v40, v168
	v_mul_f32_e32 v169, v40, v169
	v_mul_f32_e32 v170, v40, v170
	v_mul_f32_e32 v171, v40, v171
	ds_write_b128 v209, v[168:171] offset:6144
	v_mul_f32_e32 v172, v41, v172
	v_mul_f32_e32 v173, v41, v173
	v_mul_f32_e32 v174, v41, v174
	v_mul_f32_e32 v175, v41, v175
	ds_write_b128 v209, v[172:175] offset:7168
	s_waitcnt lgkmcnt(0)
	s_barrier
; #define GAS __attribute__((address_space(1)))
; #define LAS __attribute__((address_space(3)))
; #define LDS_WAIT() asm volatile("s_waitcnt lgkmcnt(0)" ::: "memory")
;     ...
; #pragma unroll
;     for (int i = 0; i < 32; ++i) v[i] = sc >= 0 ? W[(size_t)(k0 + 2 * i + (lane >> 5)) * Nsrc + sc] : 0.f;
; #pragma unroll
;     for (int i = 0; i < 32; ++i) { const int k = k0 + 2 * i + (lane >> 5); float x = v[i] * wscale; if (KS) x *= (k < ksplit ? ksA[k] : ksB[k - ksplit]); scr[(2 * i + (lane >> 5)) * 33 + (lane & 31)] = x; }
;     LDS_WAIT(); asm volatile("" ::: "memory");
;     const int c = lane & 7;
; #pragma unroll
;     for (int j = 0; j < 4; ++j) { const int n = (lane >> 3) + 8 * j; const LAS float* s = scr + (8 * c) * 33 + n;
;         const unsigned long long o = (unsigned long long)pg8::pk4_fp8(s[0 * 33], s[1 * 33], s[2 * 33], s[3 * 33]) | ((unsigned long long)pg8::pk4_fp8(s[4 * 33], s[5 * 33], s[6 * 33], s[7 * 33]) << 32);
;         *(GAS unsigned long long*)(WT + (size_t)(n0 + n) * K + k0 + 8 * c) = o; }
; __global__ void __launch_bounds__(NWAVES * 64, 2) hybrid_fwd(Args args) {
;     ...
;             if (r < I_UP) { p0_transpose_item_f8<true>(args.in[15] + (size_t)l * DM * FF, DM, FF, FF / 32, (unsigned char*)(ws + WS_WUP + l * SZ_WUP), WUP8_SCALE, args.in[14] + l * DM, args.in[14] + l * DM, DM, scr, r, lane); continue; } r -= I_UP;
;             p0_transpose_item_f8<false>(args.in[16] + (size_t)l * FF * DM, FF, DM, DM / 32, (unsigned char*)(ws + WS_WDN + l * SZ_WDN), 128.f, args.in[16], args.in[16], 0, scr, r, lane);
	s_mov_b64 s[8:9], s[38:39]
	global_load_dwordx4 v[144:147], v75, s[8:9]
	s_add_u32 s8, s8, 0x8000
	s_addc_u32 s9, s9, 0
	global_load_dwordx4 v[148:151], v75, s[8:9]
	s_add_u32 s8, s8, 0x8000
	s_addc_u32 s9, s9, 0
	global_load_dwordx4 v[152:155], v75, s[8:9]
	s_add_u32 s8, s8, 0x8000
	s_addc_u32 s9, s9, 0
	global_load_dwordx4 v[156:159], v75, s[8:9]
	s_add_u32 s8, s8, 0x8000
	s_addc_u32 s9, s9, 0
	global_load_dwordx4 v[160:163], v75, s[8:9]
	s_add_u32 s8, s8, 0x8000
	s_addc_u32 s9, s9, 0
	global_load_dwordx4 v[164:167], v75, s[8:9]
	s_add_u32 s8, s8, 0x8000
	s_addc_u32 s9, s9, 0
	global_load_dwordx4 v[168:171], v75, s[8:9]
	s_add_u32 s8, s8, 0x8000
	s_addc_u32 s9, s9, 0
	global_load_dwordx4 v[172:175], v75, s[8:9]
	s_add_u32 s6, s36, 0x3800000
	s_addc_u32 s7, s37, 0
	ds_read_b32 v226, v211
	ds_read_b32 v227, v211 offset:512
	ds_read_b32 v228, v211 offset:1024
	ds_read_b32 v229, v211 offset:1536
	ds_read_b32 v230, v211 offset:2048
	ds_read_b32 v231, v211 offset:2560
	ds_read_b32 v232, v211 offset:3072
	ds_read_b32 v233, v211 offset:3584
	ds_read_b32 v234, v211 offset:4096
	ds_read_b32 v235, v211 offset:4608
	ds_read_b32 v236, v211 offset:5120
	ds_read_b32 v237, v211 offset:5632
	ds_read_b32 v238, v211 offset:6144
	ds_read_b32 v239, v211 offset:6656
	ds_read_b32 v240, v211 offset:7168
	ds_read_b32 v241, v211 offset:7680
	s_waitcnt lgkmcnt(0)
	v_max_f32_e32 v226, v226, v226
	v_max_f32_e32 v227, v227, v227
	v_max_f32_e32 v228, v228, v228
	v_max_f32_e32 v229, v229, v229
	v_max_f32_e32 v230, v230, v230
	v_max_f32_e32 v231, v231, v231
	v_max_f32_e32 v232, v232, v232
	v_max_f32_e32 v233, v233, v233
	v_max_f32_e32 v234, v234, v234
	v_max_f32_e32 v235, v235, v235
	v_max_f32_e32 v236, v236, v236
	v_max_f32_e32 v237, v237, v237
	v_max_f32_e32 v238, v238, v238
	v_max_f32_e32 v239, v239, v239
	v_max_f32_e32 v240, v240, v240
	v_max_f32_e32 v241, v241, v241
	v_med3_f32 v226, v226, s62, v95
	v_med3_f32 v227, v227, s62, v95
	v_med3_f32 v228, v228, s62, v95
	v_med3_f32 v229, v229, s62, v95
	v_med3_f32 v230, v230, s62, v95
	v_med3_f32 v231, v231, s62, v95
	v_med3_f32 v232, v232, s62, v95
	v_med3_f32 v233, v233, s62, v95
	v_med3_f32 v234, v234, s62, v95
	v_med3_f32 v235, v235, s62, v95
	v_med3_f32 v236, v236, s62, v95
	v_med3_f32 v237, v237, s62, v95
	v_med3_f32 v238, v238, s62, v95
	v_med3_f32 v239, v239, s62, v95
	v_med3_f32 v240, v240, s62, v95
	v_med3_f32 v241, v241, s62, v95
	v_mov_b32_e32 v242, 0
	v_mov_b32_e32 v243, 0
	v_mov_b32_e32 v244, 0
	v_mov_b32_e32 v245, 0
	v_cvt_pk_fp8_f32 v242, v226, v227
	v_cvt_pk_fp8_f32 v243, v230, v231
	v_cvt_pk_fp8_f32 v244, v234, v235
	v_cvt_pk_fp8_f32 v245, v238, v239
	v_cvt_pk_fp8_f32 v242, v228, v229 op_sel:[0,0,1]
	v_cvt_pk_fp8_f32 v243, v232, v233 op_sel:[0,0,1]
	v_cvt_pk_fp8_f32 v244, v236, v237 op_sel:[0,0,1]
	v_cvt_pk_fp8_f32 v245, v240, v241 op_sel:[0,0,1]
	s_nop 0
	global_store_dwordx4 v77, v[242:245], s[6:7]
	ds_read_b32 v226, v213
	ds_read_b32 v227, v213 offset:512
	ds_read_b32 v228, v213 offset:1024
	ds_read_b32 v229, v213 offset:1536
	ds_read_b32 v230, v213 offset:2048
	ds_read_b32 v231, v213 offset:2560
	ds_read_b32 v232, v213 offset:3072
	ds_read_b32 v233, v213 offset:3584
	ds_read_b32 v234, v213 offset:4096
	ds_read_b32 v235, v213 offset:4608
	ds_read_b32 v236, v213 offset:5120
	ds_read_b32 v237, v213 offset:5632
	ds_read_b32 v238, v213 offset:6144
	ds_read_b32 v239, v213 offset:6656
	ds_read_b32 v240, v213 offset:7168
	ds_read_b32 v241, v213 offset:7680
	s_waitcnt lgkmcnt(0)
	v_max_f32_e32 v226, v226, v226
	v_max_f32_e32 v227, v227, v227
	v_max_f32_e32 v228, v228, v228
	v_max_f32_e32 v229, v229, v229
	v_max_f32_e32 v230, v230, v230
	v_max_f32_e32 v231, v231, v231
	v_max_f32_e32 v232, v232, v232
	v_max_f32_e32 v233, v233, v233
	v_max_f32_e32 v234, v234, v234
	v_max_f32_e32 v235, v235, v235
	v_max_f32_e32 v236, v236, v236
	v_max_f32_e32 v237, v237, v237
	v_max_f32_e32 v238, v238, v238
	v_max_f32_e32 v239, v239, v239
	v_max_f32_e32 v240, v240, v240
	v_max_f32_e32 v241, v241, v241
	v_med3_f32 v226, v226, s62, v95
	v_med3_f32 v227, v227, s62, v95
	v_med3_f32 v228, v228, s62, v95
	v_med3_f32 v229, v229, s62, v95
	v_med3_f32 v230, v230, s62, v95
	v_med3_f32 v231, v231, s62, v95
	v_med3_f32 v232, v232, s62, v95
	v_med3_f32 v233, v233, s62, v95
	v_med3_f32 v234, v234, s62, v95
	v_med3_f32 v235, v235, s62, v95
	v_med3_f32 v236, v236, s62, v95
	v_med3_f32 v237, v237, s62, v95
	v_med3_f32 v238, v238, s62, v95
	v_med3_f32 v239, v239, s62, v95
	v_med3_f32 v240, v240, s62, v95
	v_med3_f32 v241, v241, s62, v95
	v_mov_b32_e32 v242, 0
	v_mov_b32_e32 v243, 0
	v_mov_b32_e32 v244, 0
	v_mov_b32_e32 v245, 0
	v_cvt_pk_fp8_f32 v242, v226, v227
	v_cvt_pk_fp8_f32 v243, v230, v231
	v_cvt_pk_fp8_f32 v244, v234, v235
	v_cvt_pk_fp8_f32 v245, v238, v239
	v_cvt_pk_fp8_f32 v242, v228, v229 op_sel:[0,0,1]
	v_cvt_pk_fp8_f32 v243, v232, v233 op_sel:[0,0,1]
	v_cvt_pk_fp8_f32 v244, v236, v237 op_sel:[0,0,1]
	v_cvt_pk_fp8_f32 v245, v240, v241 op_sel:[0,0,1]
	s_nop 0
	global_store_dwordx4 v78, v[242:245], s[6:7]
	s_waitcnt vmcnt(12)
	v_mul_f32_e32 v176, v34, v176
	v_mul_f32_e32 v177, v34, v177
	v_mul_f32_e32 v178, v34, v178
	v_mul_f32_e32 v179, v34, v179
	ds_write_b128 v210, v[176:179]
	v_mul_f32_e32 v180, v35, v180
	v_mul_f32_e32 v181, v35, v181
	v_mul_f32_e32 v182, v35, v182
	v_mul_f32_e32 v183, v35, v183
	ds_write_b128 v210, v[180:183] offset:1024
	v_mul_f32_e32 v184, v36, v184
	v_mul_f32_e32 v185, v36, v185
	v_mul_f32_e32 v186, v36, v186
	v_mul_f32_e32 v187, v36, v187
	ds_write_b128 v210, v[184:187] offset:2048
	v_mul_f32_e32 v188, v37, v188
	v_mul_f32_e32 v189, v37, v189
	v_mul_f32_e32 v190, v37, v190
	v_mul_f32_e32 v191, v37, v191
	ds_write_b128 v210, v[188:191] offset:3072
	v_mul_f32_e32 v192, v38, v192
	v_mul_f32_e32 v193, v38, v193
	v_mul_f32_e32 v194, v38, v194
	v_mul_f32_e32 v195, v38, v195
	ds_write_b128 v210, v[192:195] offset:4096
	v_mul_f32_e32 v196, v39, v196
	v_mul_f32_e32 v197, v39, v197
	v_mul_f32_e32 v198, v39, v198
	v_mul_f32_e32 v199, v39, v199
	ds_write_b128 v210, v[196:199] offset:5120
	v_mul_f32_e32 v200, v40, v200
	v_mul_f32_e32 v201, v40, v201
	v_mul_f32_e32 v202, v40, v202
	v_mul_f32_e32 v203, v40, v203
	ds_write_b128 v210, v[200:203] offset:6144
	v_mul_f32_e32 v204, v41, v204
	v_mul_f32_e32 v205, v41, v205
	v_mul_f32_e32 v206, v41, v206
	v_mul_f32_e32 v207, v41, v207
	ds_write_b128 v210, v[204:207] offset:7168
	s_waitcnt lgkmcnt(0)
	s_barrier
; #define GAS __attribute__((address_space(1)))
; #define LAS __attribute__((address_space(3)))
; #define LDS_WAIT() asm volatile("s_waitcnt lgkmcnt(0)" ::: "memory")
; __device__ __forceinline__ unsigned pk4_fp8(float a, float b, float c, float d) {
;     a = fminf(fmaxf(a, -448.f), 448.f); b = fminf(fmaxf(b, -448.f), 448.f); c = fminf(fmaxf(c, -448.f), 448.f); d = fminf(fmaxf(d, -448.f), 448.f);
;     int w = __builtin_amdgcn_cvt_pk_fp8_f32(a, b, 0, false); w = __builtin_amdgcn_cvt_pk_fp8_f32(c, d, w, true); return (unsigned)w; }
;     ...
; #pragma unroll
;     for (int i = 0; i < 32; ++i) v[i] = sc >= 0 ? W[(size_t)(k0 + 2 * i + (lane >> 5)) * Nsrc + sc] : 0.f;
; #pragma unroll
;     for (int i = 0; i < 32; ++i) { const int k = k0 + 2 * i + (lane >> 5); float x = v[i] * wscale; if (KS) x *= (k < ksplit ? ksA[k] : ksB[k - ksplit]); scr[(2 * i + (lane >> 5)) * 33 + (lane & 31)] = x; }
;     LDS_WAIT(); asm volatile("" ::: "memory");
;     const int c = lane & 7;
; #pragma unroll
;     for (int j = 0; j < 4; ++j) { const int n = (lane >> 3) + 8 * j; const LAS float* s = scr + (8 * c) * 33 + n;
;         const unsigned long long o = (unsigned long long)pg8::pk4_fp8(s[0 * 33], s[1 * 33], s[2 * 33], s[3 * 33]) | ((unsigned long long)pg8::pk4_fp8(s[4 * 33], s[5 * 33], s[6 * 33], s[7 * 33]) << 32);
;         *(GAS unsigned long long*)(WT + (size_t)(n0 + n) * K + k0 + 8 * c) = o; }
	s_add_u32 s8, s38, 0x1000
	s_addc_u32 s9, s39, 0
	global_load_dwordx4 v[176:179], v75, s[8:9]
	s_add_u32 s8, s8, 0x8000
	s_addc_u32 s9, s9, 0
	global_load_dwordx4 v[180:183], v75, s[8:9]
	s_add_u32 s8, s8, 0x8000
	s_addc_u32 s9, s9, 0
	global_load_dwordx4 v[184:187], v75, s[8:9]
	s_add_u32 s8, s8, 0x8000
	s_addc_u32 s9, s9, 0
	global_load_dwordx4 v[188:191], v75, s[8:9]
	s_add_u32 s8, s8, 0x8000
	s_addc_u32 s9, s9, 0
	global_load_dwordx4 v[192:195], v75, s[8:9]
	s_add_u32 s8, s8, 0x8000
	s_addc_u32 s9, s9, 0
	global_load_dwordx4 v[196:199], v75, s[8:9]
	s_add_u32 s8, s8, 0x8000
	s_addc_u32 s9, s9, 0
	global_load_dwordx4 v[200:203], v75, s[8:9]
	s_add_u32 s8, s8, 0x8000
	s_addc_u32 s9, s9, 0
	global_load_dwordx4 v[204:207], v75, s[8:9]
	s_add_u32 s6, s36, 0x3c00000
	s_addc_u32 s7, s37, 0
	ds_read_b32 v226, v212
	ds_read_b32 v227, v212 offset:512
	ds_read_b32 v228, v212 offset:1024
	ds_read_b32 v229, v212 offset:1536
	ds_read_b32 v230, v212 offset:2048
	ds_read_b32 v231, v212 offset:2560
	ds_read_b32 v232, v212 offset:3072
	ds_read_b32 v233, v212 offset:3584
	ds_read_b32 v234, v212 offset:4096
	ds_read_b32 v235, v212 offset:4608
	ds_read_b32 v236, v212 offset:5120
	ds_read_b32 v237, v212 offset:5632
	ds_read_b32 v238, v212 offset:6144
	ds_read_b32 v239, v212 offset:6656
	ds_read_b32 v240, v212 offset:7168
	ds_read_b32 v241, v212 offset:7680
	s_waitcnt lgkmcnt(0)
	v_max_f32_e32 v226, v226, v226
	v_max_f32_e32 v227, v227, v227
	v_max_f32_e32 v228, v228, v228
	v_max_f32_e32 v229, v229, v229
	v_max_f32_e32 v230, v230, v230
	v_max_f32_e32 v231, v231, v231
	v_max_f32_e32 v232, v232, v232
	v_max_f32_e32 v233, v233, v233
	v_max_f32_e32 v234, v234, v234
	v_max_f32_e32 v235, v235, v235
	v_max_f32_e32 v236, v236, v236
	v_max_f32_e32 v237, v237, v237
	v_max_f32_e32 v238, v238, v238
	v_max_f32_e32 v239, v239, v239
	v_max_f32_e32 v240, v240, v240
	v_max_f32_e32 v241, v241, v241
	v_med3_f32 v226, v226, s62, v95
	v_med3_f32 v227, v227, s62, v95
	v_med3_f32 v228, v228, s62, v95
	v_med3_f32 v229, v229, s62, v95
	v_med3_f32 v230, v230, s62, v95
	v_med3_f32 v231, v231, s62, v95
	v_med3_f32 v232, v232, s62, v95
	v_med3_f32 v233, v233, s62, v95
	v_med3_f32 v234, v234, s62, v95
	v_med3_f32 v235, v235, s62, v95
	v_med3_f32 v236, v236, s62, v95
	v_med3_f32 v237, v237, s62, v95
	v_med3_f32 v238, v238, s62, v95
	v_med3_f32 v239, v239, s62, v95
	v_med3_f32 v240, v240, s62, v95
	v_med3_f32 v241, v241, s62, v95
	v_mov_b32_e32 v242, 0
	v_mov_b32_e32 v243, 0
	v_mov_b32_e32 v244, 0
	v_mov_b32_e32 v245, 0
	v_cvt_pk_fp8_f32 v242, v226, v227
	v_cvt_pk_fp8_f32 v243, v230, v231
	v_cvt_pk_fp8_f32 v244, v234, v235
	v_cvt_pk_fp8_f32 v245, v238, v239
	v_cvt_pk_fp8_f32 v242, v228, v229 op_sel:[0,0,1]
	v_cvt_pk_fp8_f32 v243, v232, v233 op_sel:[0,0,1]
	v_cvt_pk_fp8_f32 v244, v236, v237 op_sel:[0,0,1]
	v_cvt_pk_fp8_f32 v245, v240, v241 op_sel:[0,0,1]
	s_nop 0
	global_store_dwordx4 v77, v[242:245], s[6:7]
	ds_read_b32 v226, v214
	ds_read_b32 v227, v214 offset:512
	ds_read_b32 v228, v214 offset:1024
	ds_read_b32 v229, v214 offset:1536
	ds_read_b32 v230, v214 offset:2048
	ds_read_b32 v231, v214 offset:2560
	ds_read_b32 v232, v214 offset:3072
	ds_read_b32 v233, v214 offset:3584
	ds_read_b32 v234, v214 offset:4096
	ds_read_b32 v235, v214 offset:4608
	ds_read_b32 v236, v214 offset:5120
	ds_read_b32 v237, v214 offset:5632
	ds_read_b32 v238, v214 offset:6144
	ds_read_b32 v239, v214 offset:6656
	ds_read_b32 v240, v214 offset:7168
	ds_read_b32 v241, v214 offset:7680
	s_waitcnt lgkmcnt(0)
	v_max_f32_e32 v226, v226, v226
	v_max_f32_e32 v227, v227, v227
	v_max_f32_e32 v228, v228, v228
	v_max_f32_e32 v229, v229, v229
	v_max_f32_e32 v230, v230, v230
	v_max_f32_e32 v231, v231, v231
	v_max_f32_e32 v232, v232, v232
	v_max_f32_e32 v233, v233, v233
	v_max_f32_e32 v234, v234, v234
	v_max_f32_e32 v235, v235, v235
	v_max_f32_e32 v236, v236, v236
	v_max_f32_e32 v237, v237, v237
	v_max_f32_e32 v238, v238, v238
	v_max_f32_e32 v239, v239, v239
	v_max_f32_e32 v240, v240, v240
	v_max_f32_e32 v241, v241, v241
	v_med3_f32 v226, v226, s62, v95
	v_med3_f32 v227, v227, s62, v95
	v_med3_f32 v228, v228, s62, v95
	v_med3_f32 v229, v229, s62, v95
	v_med3_f32 v230, v230, s62, v95
	v_med3_f32 v231, v231, s62, v95
	v_med3_f32 v232, v232, s62, v95
	v_med3_f32 v233, v233, s62, v95
	v_med3_f32 v234, v234, s62, v95
	v_med3_f32 v235, v235, s62, v95
	v_med3_f32 v236, v236, s62, v95
	v_med3_f32 v237, v237, s62, v95
	v_med3_f32 v238, v238, s62, v95
	v_med3_f32 v239, v239, s62, v95
	v_med3_f32 v240, v240, s62, v95
	v_med3_f32 v241, v241, s62, v95
	v_mov_b32_e32 v242, 0
	v_mov_b32_e32 v243, 0
	v_mov_b32_e32 v244, 0
	v_mov_b32_e32 v245, 0
	v_cvt_pk_fp8_f32 v242, v226, v227
	v_cvt_pk_fp8_f32 v243, v230, v231
	v_cvt_pk_fp8_f32 v244, v234, v235
	v_cvt_pk_fp8_f32 v245, v238, v239
	v_cvt_pk_fp8_f32 v242, v228, v229 op_sel:[0,0,1]
	v_cvt_pk_fp8_f32 v243, v232, v233 op_sel:[0,0,1]
	v_cvt_pk_fp8_f32 v244, v236, v237 op_sel:[0,0,1]
	v_cvt_pk_fp8_f32 v245, v240, v241 op_sel:[0,0,1]
	s_nop 0
	global_store_dwordx4 v78, v[242:245], s[6:7]
	s_waitcnt vmcnt(12)
	v_mul_f32_e32 v144, 0x43000000, v144
	v_mul_f32_e32 v145, 0x43000000, v145
	v_mul_f32_e32 v146, 0x43000000, v146
	v_mul_f32_e32 v147, 0x43000000, v147
	ds_write_b128 v209, v[144:147]
	v_mul_f32_e32 v148, 0x43000000, v148
	v_mul_f32_e32 v149, 0x43000000, v149
	v_mul_f32_e32 v150, 0x43000000, v150
	v_mul_f32_e32 v151, 0x43000000, v151
	ds_write_b128 v209, v[148:151] offset:1024
	v_mul_f32_e32 v152, 0x43000000, v152
	v_mul_f32_e32 v153, 0x43000000, v153
	v_mul_f32_e32 v154, 0x43000000, v154
	v_mul_f32_e32 v155, 0x43000000, v155
	ds_write_b128 v209, v[152:155] offset:2048
	v_mul_f32_e32 v156, 0x43000000, v156
	v_mul_f32_e32 v157, 0x43000000, v157
	v_mul_f32_e32 v158, 0x43000000, v158
	v_mul_f32_e32 v159, 0x43000000, v159
	ds_write_b128 v209, v[156:159] offset:3072
	v_mul_f32_e32 v160, 0x43000000, v160
	v_mul_f32_e32 v161, 0x43000000, v161
	v_mul_f32_e32 v162, 0x43000000, v162
	v_mul_f32_e32 v163, 0x43000000, v163
	ds_write_b128 v209, v[160:163] offset:4096
	v_mul_f32_e32 v164, 0x43000000, v164
	v_mul_f32_e32 v165, 0x43000000, v165
	v_mul_f32_e32 v166, 0x43000000, v166
	v_mul_f32_e32 v167, 0x43000000, v167
	ds_write_b128 v209, v[164:167] offset:5120
	v_mul_f32_e32 v168, 0x43000000, v168
	v_mul_f32_e32 v169, 0x43000000, v169
	v_mul_f32_e32 v170, 0x43000000, v170
	v_mul_f32_e32 v171, 0x43000000, v171
	ds_write_b128 v209, v[168:171] offset:6144
	v_mul_f32_e32 v172, 0x43000000, v172
	v_mul_f32_e32 v173, 0x43000000, v173
	v_mul_f32_e32 v174, 0x43000000, v174
	v_mul_f32_e32 v175, 0x43000000, v175
	ds_write_b128 v209, v[172:175] offset:7168
	s_waitcnt lgkmcnt(0)
	s_barrier
; #define GAS __attribute__((address_space(1)))
; #define LAS __attribute__((address_space(3)))
; #define LDS_WAIT() asm volatile("s_waitcnt lgkmcnt(0)" ::: "memory")
; __device__ __forceinline__ unsigned pk4_fp8(float a, float b, float c, float d) {
;     a = fminf(fmaxf(a, -448.f), 448.f); b = fminf(fmaxf(b, -448.f), 448.f); c = fminf(fmaxf(c, -448.f), 448.f); d = fminf(fmaxf(d, -448.f), 448.f);
;     int w = __builtin_amdgcn_cvt_pk_fp8_f32(a, b, 0, false); w = __builtin_amdgcn_cvt_pk_fp8_f32(c, d, w, true); return (unsigned)w; }
;     ...
; #pragma unroll
;     for (int i = 0; i < 32; ++i) v[i] = sc >= 0 ? W[(size_t)(k0 + 2 * i + (lane >> 5)) * Nsrc + sc] : 0.f;
; #pragma unroll
;     for (int i = 0; i < 32; ++i) { const int k = k0 + 2 * i + (lane >> 5); float x = v[i] * wscale; if (KS) x *= (k < ksplit ? ksA[k] : ksB[k - ksplit]); scr[(2 * i + (lane >> 5)) * 33 + (lane & 31)] = x; }
;     LDS_WAIT(); asm volatile("" ::: "memory");
;     const int c = lane & 7;
; #pragma unroll
;     for (int j = 0; j < 4; ++j) { const int n = (lane >> 3) + 8 * j; const LAS float* s = scr + (8 * c) * 33 + n;
;         const unsigned long long o = (unsigned long long)pg8::pk4_fp8(s[0 * 33], s[1 * 33], s[2 * 33], s[3 * 33]) | ((unsigned long long)pg8::pk4_fp8(s[4 * 33], s[5 * 33], s[6 * 33], s[7 * 33]) << 32);
;         *(GAS unsigned long long*)(WT + (size_t)(n0 + n) * K + k0 + 8 * c) = o; }
	s_add_u32 s8, s38, 0x2000
	s_addc_u32 s9, s39, 0
	global_load_dwordx4 v[144:147], v75, s[8:9]
	s_add_u32 s8, s8, 0x8000
	s_addc_u32 s9, s9, 0
	global_load_dwordx4 v[148:151], v75, s[8:9]
	s_add_u32 s8, s8, 0x8000
	s_addc_u32 s9, s9, 0
	global_load_dwordx4 v[152:155], v75, s[8:9]
	s_add_u32 s8, s8, 0x8000
	s_addc_u32 s9, s9, 0
	global_load_dwordx4 v[156:159], v75, s[8:9]
	s_add_u32 s8, s8, 0x8000
	s_addc_u32 s9, s9, 0
	global_load_dwordx4 v[160:163], v75, s[8:9]
	s_add_u32 s8, s8, 0x8000
	s_addc_u32 s9, s9, 0
	global_load_dwordx4 v[164:167], v75, s[8:9]
	s_add_u32 s8, s8, 0x8000
	s_addc_u32 s9, s9, 0
	global_load_dwordx4 v[168:171], v75, s[8:9]
	s_add_u32 s8, s8, 0x8000
	s_addc_u32 s9, s9, 0
	global_load_dwordx4 v[172:175], v75, s[8:9]
	s_mov_b64 s[6:7], s[40:41]
	ds_read_b32 v226, v211
	ds_read_b32 v227, v211 offset:512
	ds_read_b32 v228, v211 offset:1024
	ds_read_b32 v229, v211 offset:1536
	ds_read_b32 v230, v211 offset:2048
	ds_read_b32 v231, v211 offset:2560
	ds_read_b32 v232, v211 offset:3072
	ds_read_b32 v233, v211 offset:3584
	ds_read_b32 v234, v211 offset:4096
	ds_read_b32 v235, v211 offset:4608
	ds_read_b32 v236, v211 offset:5120
	ds_read_b32 v237, v211 offset:5632
	ds_read_b32 v238, v211 offset:6144
	ds_read_b32 v239, v211 offset:6656
	ds_read_b32 v240, v211 offset:7168
	ds_read_b32 v241, v211 offset:7680
	s_waitcnt lgkmcnt(0)
	v_max_f32_e32 v226, v226, v226
	v_max_f32_e32 v227, v227, v227
	v_max_f32_e32 v228, v228, v228
	v_max_f32_e32 v229, v229, v229
	v_max_f32_e32 v230, v230, v230
	v_max_f32_e32 v231, v231, v231
	v_max_f32_e32 v232, v232, v232
	v_max_f32_e32 v233, v233, v233
	v_max_f32_e32 v234, v234, v234
	v_max_f32_e32 v235, v235, v235
	v_max_f32_e32 v236, v236, v236
	v_max_f32_e32 v237, v237, v237
	v_max_f32_e32 v238, v238, v238
	v_max_f32_e32 v239, v239, v239
	v_max_f32_e32 v240, v240, v240
	v_max_f32_e32 v241, v241, v241
	v_med3_f32 v226, v226, s62, v95
	v_med3_f32 v227, v227, s62, v95
	v_med3_f32 v228, v228, s62, v95
	v_med3_f32 v229, v229, s62, v95
	v_med3_f32 v230, v230, s62, v95
	v_med3_f32 v231, v231, s62, v95
	v_med3_f32 v232, v232, s62, v95
	v_med3_f32 v233, v233, s62, v95
	v_med3_f32 v234, v234, s62, v95
	v_med3_f32 v235, v235, s62, v95
	v_med3_f32 v236, v236, s62, v95
	v_med3_f32 v237, v237, s62, v95
	v_med3_f32 v238, v238, s62, v95
	v_med3_f32 v239, v239, s62, v95
	v_med3_f32 v240, v240, s62, v95
	v_med3_f32 v241, v241, s62, v95
	v_mov_b32_e32 v242, 0
	v_mov_b32_e32 v243, 0
	v_mov_b32_e32 v244, 0
	v_mov_b32_e32 v245, 0
	v_cvt_pk_fp8_f32 v242, v226, v227
	v_cvt_pk_fp8_f32 v243, v230, v231
	v_cvt_pk_fp8_f32 v244, v234, v235
	v_cvt_pk_fp8_f32 v245, v238, v239
	v_cvt_pk_fp8_f32 v242, v228, v229 op_sel:[0,0,1]
	v_cvt_pk_fp8_f32 v243, v232, v233 op_sel:[0,0,1]
	v_cvt_pk_fp8_f32 v244, v236, v237 op_sel:[0,0,1]
	v_cvt_pk_fp8_f32 v245, v240, v241 op_sel:[0,0,1]
	s_nop 0
	global_store_dwordx4 v79, v[242:245], s[6:7]
	ds_read_b32 v226, v213
	ds_read_b32 v227, v213 offset:512
	ds_read_b32 v228, v213 offset:1024
	ds_read_b32 v229, v213 offset:1536
	ds_read_b32 v230, v213 offset:2048
	ds_read_b32 v231, v213 offset:2560
	ds_read_b32 v232, v213 offset:3072
	ds_read_b32 v233, v213 offset:3584
	ds_read_b32 v234, v213 offset:4096
	ds_read_b32 v235, v213 offset:4608
	ds_read_b32 v236, v213 offset:5120
	ds_read_b32 v237, v213 offset:5632
	ds_read_b32 v238, v213 offset:6144
	ds_read_b32 v239, v213 offset:6656
	ds_read_b32 v240, v213 offset:7168
	ds_read_b32 v241, v213 offset:7680
	s_waitcnt lgkmcnt(0)
	v_max_f32_e32 v226, v226, v226
	v_max_f32_e32 v227, v227, v227
	v_max_f32_e32 v228, v228, v228
	v_max_f32_e32 v229, v229, v229
	v_max_f32_e32 v230, v230, v230
	v_max_f32_e32 v231, v231, v231
	v_max_f32_e32 v232, v232, v232
	v_max_f32_e32 v233, v233, v233
	v_max_f32_e32 v234, v234, v234
	v_max_f32_e32 v235, v235, v235
	v_max_f32_e32 v236, v236, v236
	v_max_f32_e32 v237, v237, v237
	v_max_f32_e32 v238, v238, v238
	v_max_f32_e32 v239, v239, v239
	v_max_f32_e32 v240, v240, v240
	v_max_f32_e32 v241, v241, v241
	v_med3_f32 v226, v226, s62, v95
	v_med3_f32 v227, v227, s62, v95
	v_med3_f32 v228, v228, s62, v95
	v_med3_f32 v229, v229, s62, v95
	v_med3_f32 v230, v230, s62, v95
	v_med3_f32 v231, v231, s62, v95
	v_med3_f32 v232, v232, s62, v95
	v_med3_f32 v233, v233, s62, v95
	v_med3_f32 v234, v234, s62, v95
	v_med3_f32 v235, v235, s62, v95
	v_med3_f32 v236, v236, s62, v95
	v_med3_f32 v237, v237, s62, v95
	v_med3_f32 v238, v238, s62, v95
	v_med3_f32 v239, v239, s62, v95
	v_med3_f32 v240, v240, s62, v95
	v_med3_f32 v241, v241, s62, v95
	v_mov_b32_e32 v242, 0
	v_mov_b32_e32 v243, 0
	v_mov_b32_e32 v244, 0
	v_mov_b32_e32 v245, 0
	v_cvt_pk_fp8_f32 v242, v226, v227
	v_cvt_pk_fp8_f32 v243, v230, v231
	v_cvt_pk_fp8_f32 v244, v234, v235
	v_cvt_pk_fp8_f32 v245, v238, v239
	v_cvt_pk_fp8_f32 v242, v228, v229 op_sel:[0,0,1]
	v_cvt_pk_fp8_f32 v243, v232, v233 op_sel:[0,0,1]
	v_cvt_pk_fp8_f32 v244, v236, v237 op_sel:[0,0,1]
	v_cvt_pk_fp8_f32 v245, v240, v241 op_sel:[0,0,1]
	s_nop 0
	global_store_dwordx4 v80, v[242:245], s[6:7]
	s_waitcnt vmcnt(12)
	v_mul_f32_e32 v176, 0x43000000, v176
	v_mul_f32_e32 v177, 0x43000000, v177
	v_mul_f32_e32 v178, 0x43000000, v178
	v_mul_f32_e32 v179, 0x43000000, v179
	ds_write_b128 v210, v[176:179]
	v_mul_f32_e32 v180, 0x43000000, v180
	v_mul_f32_e32 v181, 0x43000000, v181
	v_mul_f32_e32 v182, 0x43000000, v182
	v_mul_f32_e32 v183, 0x43000000, v183
	ds_write_b128 v210, v[180:183] offset:1024
	v_mul_f32_e32 v184, 0x43000000, v184
	v_mul_f32_e32 v185, 0x43000000, v185
	v_mul_f32_e32 v186, 0x43000000, v186
	v_mul_f32_e32 v187, 0x43000000, v187
	ds_write_b128 v210, v[184:187] offset:2048
	v_mul_f32_e32 v188, 0x43000000, v188
	v_mul_f32_e32 v189, 0x43000000, v189
	v_mul_f32_e32 v190, 0x43000000, v190
	v_mul_f32_e32 v191, 0x43000000, v191
	ds_write_b128 v210, v[188:191] offset:3072
	v_mul_f32_e32 v192, 0x43000000, v192
	v_mul_f32_e32 v193, 0x43000000, v193
	v_mul_f32_e32 v194, 0x43000000, v194
	v_mul_f32_e32 v195, 0x43000000, v195
	ds_write_b128 v210, v[192:195] offset:4096
	v_mul_f32_e32 v196, 0x43000000, v196
	v_mul_f32_e32 v197, 0x43000000, v197
	v_mul_f32_e32 v198, 0x43000000, v198
	v_mul_f32_e32 v199, 0x43000000, v199
	ds_write_b128 v210, v[196:199] offset:5120
	v_mul_f32_e32 v200, 0x43000000, v200
	v_mul_f32_e32 v201, 0x43000000, v201
	v_mul_f32_e32 v202, 0x43000000, v202
	v_mul_f32_e32 v203, 0x43000000, v203
	ds_write_b128 v210, v[200:203] offset:6144
	v_mul_f32_e32 v204, 0x43000000, v204
	v_mul_f32_e32 v205, 0x43000000, v205
	v_mul_f32_e32 v206, 0x43000000, v206
	v_mul_f32_e32 v207, 0x43000000, v207
	ds_write_b128 v210, v[204:207] offset:7168
	s_waitcnt lgkmcnt(0)
	s_barrier
; #define GAS __attribute__((address_space(1)))
; #define LAS __attribute__((address_space(3)))
; #define LDS_WAIT() asm volatile("s_waitcnt lgkmcnt(0)" ::: "memory")
; __device__ __forceinline__ unsigned pk4_fp8(float a, float b, float c, float d) {
;     a = fminf(fmaxf(a, -448.f), 448.f); b = fminf(fmaxf(b, -448.f), 448.f); c = fminf(fmaxf(c, -448.f), 448.f); d = fminf(fmaxf(d, -448.f), 448.f);
;     int w = __builtin_amdgcn_cvt_pk_fp8_f32(a, b, 0, false); w = __builtin_amdgcn_cvt_pk_fp8_f32(c, d, w, true); return (unsigned)w; }
;     ...
; #pragma unroll
;     for (int i = 0; i < 32; ++i) v[i] = sc >= 0 ? W[(size_t)(k0 + 2 * i + (lane >> 5)) * Nsrc + sc] : 0.f;
; #pragma unroll
;     for (int i = 0; i < 32; ++i) { const int k = k0 + 2 * i + (lane >> 5); float x = v[i] * wscale; if (KS) x *= (k < ksplit ? ksA[k] : ksB[k - ksplit]); scr[(2 * i + (lane >> 5)) * 33 + (lane & 31)] = x; }
;     LDS_WAIT(); asm volatile("" ::: "memory");
;     const int c = lane & 7;
; #pragma unroll
;     for (int j = 0; j < 4; ++j) { const int n = (lane >> 3) + 8 * j; const LAS float* s = scr + (8 * c) * 33 + n;
;         const unsigned long long o = (unsigned long long)pg8::pk4_fp8(s[0 * 33], s[1 * 33], s[2 * 33], s[3 * 33]) | ((unsigned long long)pg8::pk4_fp8(s[4 * 33], s[5 * 33], s[6 * 33], s[7 * 33]) << 32);
;         *(GAS unsigned long long*)(WT + (size_t)(n0 + n) * K + k0 + 8 * c) = o; }
	s_add_u32 s8, s38, 0x3000
	s_addc_u32 s9, s39, 0
	global_load_dwordx4 v[176:179], v75, s[8:9]
	s_add_u32 s8, s8, 0x8000
	s_addc_u32 s9, s9, 0
	global_load_dwordx4 v[180:183], v75, s[8:9]
	s_add_u32 s8, s8, 0x8000
	s_addc_u32 s9, s9, 0
	global_load_dwordx4 v[184:187], v75, s[8:9]
	s_add_u32 s8, s8, 0x8000
	s_addc_u32 s9, s9, 0
	global_load_dwordx4 v[188:191], v75, s[8:9]
	s_add_u32 s8, s8, 0x8000
	s_addc_u32 s9, s9, 0
	global_load_dwordx4 v[192:195], v75, s[8:9]
	s_add_u32 s8, s8, 0x8000
	s_addc_u32 s9, s9, 0
	global_load_dwordx4 v[196:199], v75, s[8:9]
	s_add_u32 s8, s8, 0x8000
	s_addc_u32 s9, s9, 0
	global_load_dwordx4 v[200:203], v75, s[8:9]
	s_add_u32 s8, s8, 0x8000
	s_addc_u32 s9, s9, 0
	global_load_dwordx4 v[204:207], v75, s[8:9]
	s_add_u32 s6, s40, 0x1000000
	s_addc_u32 s7, s41, 0
	ds_read_b32 v226, v212
	ds_read_b32 v227, v212 offset:512
	ds_read_b32 v228, v212 offset:1024
	ds_read_b32 v229, v212 offset:1536
	ds_read_b32 v230, v212 offset:2048
	ds_read_b32 v231, v212 offset:2560
	ds_read_b32 v232, v212 offset:3072
	ds_read_b32 v233, v212 offset:3584
	ds_read_b32 v234, v212 offset:4096
	ds_read_b32 v235, v212 offset:4608
	ds_read_b32 v236, v212 offset:5120
	ds_read_b32 v237, v212 offset:5632
	ds_read_b32 v238, v212 offset:6144
	ds_read_b32 v239, v212 offset:6656
	ds_read_b32 v240, v212 offset:7168
	ds_read_b32 v241, v212 offset:7680
	s_waitcnt lgkmcnt(0)
	v_max_f32_e32 v226, v226, v226
	v_max_f32_e32 v227, v227, v227
	v_max_f32_e32 v228, v228, v228
	v_max_f32_e32 v229, v229, v229
	v_max_f32_e32 v230, v230, v230
	v_max_f32_e32 v231, v231, v231
	v_max_f32_e32 v232, v232, v232
	v_max_f32_e32 v233, v233, v233
	v_max_f32_e32 v234, v234, v234
	v_max_f32_e32 v235, v235, v235
	v_max_f32_e32 v236, v236, v236
	v_max_f32_e32 v237, v237, v237
	v_max_f32_e32 v238, v238, v238
	v_max_f32_e32 v239, v239, v239
	v_max_f32_e32 v240, v240, v240
	v_max_f32_e32 v241, v241, v241
	v_med3_f32 v226, v226, s62, v95
	v_med3_f32 v227, v227, s62, v95
	v_med3_f32 v228, v228, s62, v95
	v_med3_f32 v229, v229, s62, v95
	v_med3_f32 v230, v230, s62, v95
	v_med3_f32 v231, v231, s62, v95
	v_med3_f32 v232, v232, s62, v95
	v_med3_f32 v233, v233, s62, v95
	v_med3_f32 v234, v234, s62, v95
	v_med3_f32 v235, v235, s62, v95
	v_med3_f32 v236, v236, s62, v95
	v_med3_f32 v237, v237, s62, v95
	v_med3_f32 v238, v238, s62, v95
	v_med3_f32 v239, v239, s62, v95
	v_med3_f32 v240, v240, s62, v95
	v_med3_f32 v241, v241, s62, v95
	v_mov_b32_e32 v242, 0
	v_mov_b32_e32 v243, 0
	v_mov_b32_e32 v244, 0
	v_mov_b32_e32 v245, 0
	v_cvt_pk_fp8_f32 v242, v226, v227
	v_cvt_pk_fp8_f32 v243, v230, v231
	v_cvt_pk_fp8_f32 v244, v234, v235
	v_cvt_pk_fp8_f32 v245, v238, v239
	v_cvt_pk_fp8_f32 v242, v228, v229 op_sel:[0,0,1]
	v_cvt_pk_fp8_f32 v243, v232, v233 op_sel:[0,0,1]
	v_cvt_pk_fp8_f32 v244, v236, v237 op_sel:[0,0,1]
	v_cvt_pk_fp8_f32 v245, v240, v241 op_sel:[0,0,1]
	s_nop 0
	global_store_dwordx4 v79, v[242:245], s[6:7]
	ds_read_b32 v226, v214
	ds_read_b32 v227, v214 offset:512
	ds_read_b32 v228, v214 offset:1024
	ds_read_b32 v229, v214 offset:1536
	ds_read_b32 v230, v214 offset:2048
	ds_read_b32 v231, v214 offset:2560
	ds_read_b32 v232, v214 offset:3072
	ds_read_b32 v233, v214 offset:3584
	ds_read_b32 v234, v214 offset:4096
	ds_read_b32 v235, v214 offset:4608
	ds_read_b32 v236, v214 offset:5120
	ds_read_b32 v237, v214 offset:5632
	ds_read_b32 v238, v214 offset:6144
	ds_read_b32 v239, v214 offset:6656
	ds_read_b32 v240, v214 offset:7168
	ds_read_b32 v241, v214 offset:7680
	s_waitcnt lgkmcnt(0)
	v_max_f32_e32 v226, v226, v226
	v_max_f32_e32 v227, v227, v227
	v_max_f32_e32 v228, v228, v228
	v_max_f32_e32 v229, v229, v229
	v_max_f32_e32 v230, v230, v230
	v_max_f32_e32 v231, v231, v231
	v_max_f32_e32 v232, v232, v232
	v_max_f32_e32 v233, v233, v233
	v_max_f32_e32 v234, v234, v234
	v_max_f32_e32 v235, v235, v235
	v_max_f32_e32 v236, v236, v236
	v_max_f32_e32 v237, v237, v237
	v_max_f32_e32 v238, v238, v238
	v_max_f32_e32 v239, v239, v239
	v_max_f32_e32 v240, v240, v240
	v_max_f32_e32 v241, v241, v241
	v_med3_f32 v226, v226, s62, v95
	v_med3_f32 v227, v227, s62, v95
	v_med3_f32 v228, v228, s62, v95
	v_med3_f32 v229, v229, s62, v95
	v_med3_f32 v230, v230, s62, v95
	v_med3_f32 v231, v231, s62, v95
	v_med3_f32 v232, v232, s62, v95
	v_med3_f32 v233, v233, s62, v95
	v_med3_f32 v234, v234, s62, v95
	v_med3_f32 v235, v235, s62, v95
	v_med3_f32 v236, v236, s62, v95
	v_med3_f32 v237, v237, s62, v95
	v_med3_f32 v238, v238, s62, v95
	v_med3_f32 v239, v239, s62, v95
	v_med3_f32 v240, v240, s62, v95
	v_med3_f32 v241, v241, s62, v95
	v_mov_b32_e32 v242, 0
	v_mov_b32_e32 v243, 0
	v_mov_b32_e32 v244, 0
	v_mov_b32_e32 v245, 0
	v_cvt_pk_fp8_f32 v242, v226, v227
	v_cvt_pk_fp8_f32 v243, v230, v231
	v_cvt_pk_fp8_f32 v244, v234, v235
	v_cvt_pk_fp8_f32 v245, v238, v239
	v_cvt_pk_fp8_f32 v242, v228, v229 op_sel:[0,0,1]
	v_cvt_pk_fp8_f32 v243, v232, v233 op_sel:[0,0,1]
	v_cvt_pk_fp8_f32 v244, v236, v237 op_sel:[0,0,1]
	v_cvt_pk_fp8_f32 v245, v240, v241 op_sel:[0,0,1]
	s_nop 0
	global_store_dwordx4 v80, v[242:245], s[6:7]
	s_waitcnt vmcnt(12)
	v_mul_f32_e32 v144, 0x43000000, v144
	v_mul_f32_e32 v145, 0x43000000, v145
	v_mul_f32_e32 v146, 0x43000000, v146
	v_mul_f32_e32 v147, 0x43000000, v147
	ds_write_b128 v209, v[144:147]
	v_mul_f32_e32 v148, 0x43000000, v148
	v_mul_f32_e32 v149, 0x43000000, v149
	v_mul_f32_e32 v150, 0x43000000, v150
	v_mul_f32_e32 v151, 0x43000000, v151
	ds_write_b128 v209, v[148:151] offset:1024
	v_mul_f32_e32 v152, 0x43000000, v152
	v_mul_f32_e32 v153, 0x43000000, v153
	v_mul_f32_e32 v154, 0x43000000, v154
	v_mul_f32_e32 v155, 0x43000000, v155
	ds_write_b128 v209, v[152:155] offset:2048
	v_mul_f32_e32 v156, 0x43000000, v156
	v_mul_f32_e32 v157, 0x43000000, v157
	v_mul_f32_e32 v158, 0x43000000, v158
	v_mul_f32_e32 v159, 0x43000000, v159
	ds_write_b128 v209, v[156:159] offset:3072
	v_mul_f32_e32 v160, 0x43000000, v160
	v_mul_f32_e32 v161, 0x43000000, v161
	v_mul_f32_e32 v162, 0x43000000, v162
	v_mul_f32_e32 v163, 0x43000000, v163
	ds_write_b128 v209, v[160:163] offset:4096
	v_mul_f32_e32 v164, 0x43000000, v164
	v_mul_f32_e32 v165, 0x43000000, v165
	v_mul_f32_e32 v166, 0x43000000, v166
	v_mul_f32_e32 v167, 0x43000000, v167
	ds_write_b128 v209, v[164:167] offset:5120
	v_mul_f32_e32 v168, 0x43000000, v168
	v_mul_f32_e32 v169, 0x43000000, v169
	v_mul_f32_e32 v170, 0x43000000, v170
	v_mul_f32_e32 v171, 0x43000000, v171
	ds_write_b128 v209, v[168:171] offset:6144
	v_mul_f32_e32 v172, 0x43000000, v172
	v_mul_f32_e32 v173, 0x43000000, v173
	v_mul_f32_e32 v174, 0x43000000, v174
	v_mul_f32_e32 v175, 0x43000000, v175
	ds_write_b128 v209, v[172:175] offset:7168
	s_waitcnt lgkmcnt(0)
	s_barrier
; #define GAS __attribute__((address_space(1)))
; #define LAS __attribute__((address_space(3)))
; #define LDS_WAIT() asm volatile("s_waitcnt lgkmcnt(0)" ::: "memory")
; __device__ __forceinline__ unsigned pk4_fp8(float a, float b, float c, float d) {
;     a = fminf(fmaxf(a, -448.f), 448.f); b = fminf(fmaxf(b, -448.f), 448.f); c = fminf(fmaxf(c, -448.f), 448.f); d = fminf(fmaxf(d, -448.f), 448.f);
;     int w = __builtin_amdgcn_cvt_pk_fp8_f32(a, b, 0, false); w = __builtin_amdgcn_cvt_pk_fp8_f32(c, d, w, true); return (unsigned)w; }
;     ...
; #pragma unroll
;     for (int i = 0; i < 32; ++i) v[i] = sc >= 0 ? W[(size_t)(k0 + 2 * i + (lane >> 5)) * Nsrc + sc] : 0.f;
; #pragma unroll
;     for (int i = 0; i < 32; ++i) { const int k = k0 + 2 * i + (lane >> 5); float x = v[i] * wscale; if (KS) x *= (k < ksplit ? ksA[k] : ksB[k - ksplit]); scr[(2 * i + (lane >> 5)) * 33 + (lane & 31)] = x; }
;     LDS_WAIT(); asm volatile("" ::: "memory");
;     const int c = lane & 7;
; #pragma unroll
;     for (int j = 0; j < 4; ++j) { const int n = (lane >> 3) + 8 * j; const LAS float* s = scr + (8 * c) * 33 + n;
;         const unsigned long long o = (unsigned long long)pg8::pk4_fp8(s[0 * 33], s[1 * 33], s[2 * 33], s[3 * 33]) | ((unsigned long long)pg8::pk4_fp8(s[4 * 33], s[5 * 33], s[6 * 33], s[7 * 33]) << 32);
;         *(GAS unsigned long long*)(WT + (size_t)(n0 + n) * K + k0 + 8 * c) = o; }
	s_add_u32 s8, s38, 0x4000000
	s_addc_u32 s9, s39, 0
	global_load_dwordx4 v[144:147], v75, s[8:9]
	s_add_u32 s8, s8, 0x8000
	s_addc_u32 s9, s9, 0
	global_load_dwordx4 v[148:151], v75, s[8:9]
	s_add_u32 s8, s8, 0x8000
	s_addc_u32 s9, s9, 0
	global_load_dwordx4 v[152:155], v75, s[8:9]
	s_add_u32 s8, s8, 0x8000
	s_addc_u32 s9, s9, 0
	global_load_dwordx4 v[156:159], v75, s[8:9]
	s_add_u32 s8, s8, 0x8000
	s_addc_u32 s9, s9, 0
	global_load_dwordx4 v[160:163], v75, s[8:9]
	s_add_u32 s8, s8, 0x8000
	s_addc_u32 s9, s9, 0
	global_load_dwordx4 v[164:167], v75, s[8:9]
	s_add_u32 s8, s8, 0x8000
	s_addc_u32 s9, s9, 0
	global_load_dwordx4 v[168:171], v75, s[8:9]
	s_add_u32 s8, s8, 0x8000
	s_addc_u32 s9, s9, 0
	global_load_dwordx4 v[172:175], v75, s[8:9]
	s_add_u32 s6, s40, 0x2000000
	s_addc_u32 s7, s41, 0
	ds_read_b32 v226, v211
	ds_read_b32 v227, v211 offset:512
	ds_read_b32 v228, v211 offset:1024
	ds_read_b32 v229, v211 offset:1536
	ds_read_b32 v230, v211 offset:2048
	ds_read_b32 v231, v211 offset:2560
	ds_read_b32 v232, v211 offset:3072
	ds_read_b32 v233, v211 offset:3584
	ds_read_b32 v234, v211 offset:4096
	ds_read_b32 v235, v211 offset:4608
	ds_read_b32 v236, v211 offset:5120
	ds_read_b32 v237, v211 offset:5632
	ds_read_b32 v238, v211 offset:6144
	ds_read_b32 v239, v211 offset:6656
	ds_read_b32 v240, v211 offset:7168
	ds_read_b32 v241, v211 offset:7680
	s_waitcnt lgkmcnt(0)
	v_max_f32_e32 v226, v226, v226
	v_max_f32_e32 v227, v227, v227
	v_max_f32_e32 v228, v228, v228
	v_max_f32_e32 v229, v229, v229
	v_max_f32_e32 v230, v230, v230
	v_max_f32_e32 v231, v231, v231
	v_max_f32_e32 v232, v232, v232
	v_max_f32_e32 v233, v233, v233
	v_max_f32_e32 v234, v234, v234
	v_max_f32_e32 v235, v235, v235
	v_max_f32_e32 v236, v236, v236
	v_max_f32_e32 v237, v237, v237
	v_max_f32_e32 v238, v238, v238
	v_max_f32_e32 v239, v239, v239
	v_max_f32_e32 v240, v240, v240
	v_max_f32_e32 v241, v241, v241
	v_med3_f32 v226, v226, s62, v95
	v_med3_f32 v227, v227, s62, v95
	v_med3_f32 v228, v228, s62, v95
	v_med3_f32 v229, v229, s62, v95
	v_med3_f32 v230, v230, s62, v95
	v_med3_f32 v231, v231, s62, v95
	v_med3_f32 v232, v232, s62, v95
	v_med3_f32 v233, v233, s62, v95
	v_med3_f32 v234, v234, s62, v95
	v_med3_f32 v235, v235, s62, v95
	v_med3_f32 v236, v236, s62, v95
	v_med3_f32 v237, v237, s62, v95
	v_med3_f32 v238, v238, s62, v95
	v_med3_f32 v239, v239, s62, v95
	v_med3_f32 v240, v240, s62, v95
	v_med3_f32 v241, v241, s62, v95
	v_mov_b32_e32 v242, 0
	v_mov_b32_e32 v243, 0
	v_mov_b32_e32 v244, 0
	v_mov_b32_e32 v245, 0
	v_cvt_pk_fp8_f32 v242, v226, v227
	v_cvt_pk_fp8_f32 v243, v230, v231
	v_cvt_pk_fp8_f32 v244, v234, v235
	v_cvt_pk_fp8_f32 v245, v238, v239
	v_cvt_pk_fp8_f32 v242, v228, v229 op_sel:[0,0,1]
	v_cvt_pk_fp8_f32 v243, v232, v233 op_sel:[0,0,1]
	v_cvt_pk_fp8_f32 v244, v236, v237 op_sel:[0,0,1]
	v_cvt_pk_fp8_f32 v245, v240, v241 op_sel:[0,0,1]
	s_nop 0
	global_store_dwordx4 v79, v[242:245], s[6:7]
	ds_read_b32 v226, v213
	ds_read_b32 v227, v213 offset:512
	ds_read_b32 v228, v213 offset:1024
	ds_read_b32 v229, v213 offset:1536
	ds_read_b32 v230, v213 offset:2048
	ds_read_b32 v231, v213 offset:2560
	ds_read_b32 v232, v213 offset:3072
	ds_read_b32 v233, v213 offset:3584
	ds_read_b32 v234, v213 offset:4096
	ds_read_b32 v235, v213 offset:4608
	ds_read_b32 v236, v213 offset:5120
	ds_read_b32 v237, v213 offset:5632
	ds_read_b32 v238, v213 offset:6144
	ds_read_b32 v239, v213 offset:6656
	ds_read_b32 v240, v213 offset:7168
	ds_read_b32 v241, v213 offset:7680
	s_waitcnt lgkmcnt(0)
	v_max_f32_e32 v226, v226, v226
	v_max_f32_e32 v227, v227, v227
	v_max_f32_e32 v228, v228, v228
	v_max_f32_e32 v229, v229, v229
	v_max_f32_e32 v230, v230, v230
	v_max_f32_e32 v231, v231, v231
	v_max_f32_e32 v232, v232, v232
	v_max_f32_e32 v233, v233, v233
	v_max_f32_e32 v234, v234, v234
	v_max_f32_e32 v235, v235, v235
	v_max_f32_e32 v236, v236, v236
	v_max_f32_e32 v237, v237, v237
	v_max_f32_e32 v238, v238, v238
	v_max_f32_e32 v239, v239, v239
	v_max_f32_e32 v240, v240, v240
	v_max_f32_e32 v241, v241, v241
	v_med3_f32 v226, v226, s62, v95
	v_med3_f32 v227, v227, s62, v95
	v_med3_f32 v228, v228, s62, v95
	v_med3_f32 v229, v229, s62, v95
	v_med3_f32 v230, v230, s62, v95
	v_med3_f32 v231, v231, s62, v95
	v_med3_f32 v232, v232, s62, v95
	v_med3_f32 v233, v233, s62, v95
	v_med3_f32 v234, v234, s62, v95
	v_med3_f32 v235, v235, s62, v95
	v_med3_f32 v236, v236, s62, v95
	v_med3_f32 v237, v237, s62, v95
	v_med3_f32 v238, v238, s62, v95
	v_med3_f32 v239, v239, s62, v95
	v_med3_f32 v240, v240, s62, v95
	v_med3_f32 v241, v241, s62, v95
	v_mov_b32_e32 v242, 0
	v_mov_b32_e32 v243, 0
	v_mov_b32_e32 v244, 0
	v_mov_b32_e32 v245, 0
	v_cvt_pk_fp8_f32 v242, v226, v227
	v_cvt_pk_fp8_f32 v243, v230, v231
	v_cvt_pk_fp8_f32 v244, v234, v235
	v_cvt_pk_fp8_f32 v245, v238, v239
	v_cvt_pk_fp8_f32 v242, v228, v229 op_sel:[0,0,1]
	v_cvt_pk_fp8_f32 v243, v232, v233 op_sel:[0,0,1]
	v_cvt_pk_fp8_f32 v244, v236, v237 op_sel:[0,0,1]
	v_cvt_pk_fp8_f32 v245, v240, v241 op_sel:[0,0,1]
	s_nop 0
	global_store_dwordx4 v80, v[242:245], s[6:7]
	s_waitcnt vmcnt(12)
	v_mul_f32_e32 v176, 0x43000000, v176
	v_mul_f32_e32 v177, 0x43000000, v177
	v_mul_f32_e32 v178, 0x43000000, v178
	v_mul_f32_e32 v179, 0x43000000, v179
	ds_write_b128 v210, v[176:179]
	v_mul_f32_e32 v180, 0x43000000, v180
	v_mul_f32_e32 v181, 0x43000000, v181
	v_mul_f32_e32 v182, 0x43000000, v182
	v_mul_f32_e32 v183, 0x43000000, v183
	ds_write_b128 v210, v[180:183] offset:1024
	v_mul_f32_e32 v184, 0x43000000, v184
	v_mul_f32_e32 v185, 0x43000000, v185
	v_mul_f32_e32 v186, 0x43000000, v186
	v_mul_f32_e32 v187, 0x43000000, v187
	ds_write_b128 v210, v[184:187] offset:2048
	v_mul_f32_e32 v188, 0x43000000, v188
	v_mul_f32_e32 v189, 0x43000000, v189
	v_mul_f32_e32 v190, 0x43000000, v190
	v_mul_f32_e32 v191, 0x43000000, v191
	ds_write_b128 v210, v[188:191] offset:3072
	v_mul_f32_e32 v192, 0x43000000, v192
	v_mul_f32_e32 v193, 0x43000000, v193
	v_mul_f32_e32 v194, 0x43000000, v194
	v_mul_f32_e32 v195, 0x43000000, v195
	ds_write_b128 v210, v[192:195] offset:4096
	v_mul_f32_e32 v196, 0x43000000, v196
	v_mul_f32_e32 v197, 0x43000000, v197
	v_mul_f32_e32 v198, 0x43000000, v198
	v_mul_f32_e32 v199, 0x43000000, v199
	ds_write_b128 v210, v[196:199] offset:5120
	v_mul_f32_e32 v200, 0x43000000, v200
	v_mul_f32_e32 v201, 0x43000000, v201
	v_mul_f32_e32 v202, 0x43000000, v202
	v_mul_f32_e32 v203, 0x43000000, v203
	ds_write_b128 v210, v[200:203] offset:6144
	v_mul_f32_e32 v204, 0x43000000, v204
	v_mul_f32_e32 v205, 0x43000000, v205
	v_mul_f32_e32 v206, 0x43000000, v206
	v_mul_f32_e32 v207, 0x43000000, v207
	ds_write_b128 v210, v[204:207] offset:7168
	s_waitcnt lgkmcnt(0)
	s_barrier
; #define GAS __attribute__((address_space(1)))
; #define LAS __attribute__((address_space(3)))
; #define LDS_WAIT() asm volatile("s_waitcnt lgkmcnt(0)" ::: "memory")
; __device__ __forceinline__ unsigned pk4_fp8(float a, float b, float c, float d) {
;     a = fminf(fmaxf(a, -448.f), 448.f); b = fminf(fmaxf(b, -448.f), 448.f); c = fminf(fmaxf(c, -448.f), 448.f); d = fminf(fmaxf(d, -448.f), 448.f);
;     int w = __builtin_amdgcn_cvt_pk_fp8_f32(a, b, 0, false); w = __builtin_amdgcn_cvt_pk_fp8_f32(c, d, w, true); return (unsigned)w; }
;     ...
; #pragma unroll
;     for (int i = 0; i < 32; ++i) v[i] = sc >= 0 ? W[(size_t)(k0 + 2 * i + (lane >> 5)) * Nsrc + sc] : 0.f;
; #pragma unroll
;     for (int i = 0; i < 32; ++i) { const int k = k0 + 2 * i + (lane >> 5); float x = v[i] * wscale; if (KS) x *= (k < ksplit ? ksA[k] : ksB[k - ksplit]); scr[(2 * i + (lane >> 5)) * 33 + (lane & 31)] = x; }
;     LDS_WAIT(); asm volatile("" ::: "memory");
;     const int c = lane & 7;
; #pragma unroll
;     for (int j = 0; j < 4; ++j) { const int n = (lane >> 3) + 8 * j; const LAS float* s = scr + (8 * c) * 33 + n;
;         const unsigned long long o = (unsigned long long)pg8::pk4_fp8(s[0 * 33], s[1 * 33], s[2 * 33], s[3 * 33]) | ((unsigned long long)pg8::pk4_fp8(s[4 * 33], s[5 * 33], s[6 * 33], s[7 * 33]) << 32);
;         *(GAS unsigned long long*)(WT + (size_t)(n0 + n) * K + k0 + 8 * c) = o; }
	s_add_u32 s8, s38, 0x4001000
	s_addc_u32 s9, s39, 0
	global_load_dwordx4 v[176:179], v75, s[8:9]
	s_add_u32 s8, s8, 0x8000
	s_addc_u32 s9, s9, 0
	global_load_dwordx4 v[180:183], v75, s[8:9]
	s_add_u32 s8, s8, 0x8000
	s_addc_u32 s9, s9, 0
	global_load_dwordx4 v[184:187], v75, s[8:9]
	s_add_u32 s8, s8, 0x8000
	s_addc_u32 s9, s9, 0
	global_load_dwordx4 v[188:191], v75, s[8:9]
	s_add_u32 s8, s8, 0x8000
	s_addc_u32 s9, s9, 0
	global_load_dwordx4 v[192:195], v75, s[8:9]
	s_add_u32 s8, s8, 0x8000
	s_addc_u32 s9, s9, 0
	global_load_dwordx4 v[196:199], v75, s[8:9]
	s_add_u32 s8, s8, 0x8000
	s_addc_u32 s9, s9, 0
	global_load_dwordx4 v[200:203], v75, s[8:9]
	s_add_u32 s8, s8, 0x8000
	s_addc_u32 s9, s9, 0
	global_load_dwordx4 v[204:207], v75, s[8:9]
	s_add_u32 s6, s40, 0x3000000
	s_addc_u32 s7, s41, 0
	ds_read_b32 v226, v212
	ds_read_b32 v227, v212 offset:512
	ds_read_b32 v228, v212 offset:1024
	ds_read_b32 v229, v212 offset:1536
	ds_read_b32 v230, v212 offset:2048
	ds_read_b32 v231, v212 offset:2560
	ds_read_b32 v232, v212 offset:3072
	ds_read_b32 v233, v212 offset:3584
	ds_read_b32 v234, v212 offset:4096
	ds_read_b32 v235, v212 offset:4608
	ds_read_b32 v236, v212 offset:5120
	ds_read_b32 v237, v212 offset:5632
	ds_read_b32 v238, v212 offset:6144
	ds_read_b32 v239, v212 offset:6656
	ds_read_b32 v240, v212 offset:7168
	ds_read_b32 v241, v212 offset:7680
	s_waitcnt lgkmcnt(0)
	v_max_f32_e32 v226, v226, v226
	v_max_f32_e32 v227, v227, v227
	v_max_f32_e32 v228, v228, v228
	v_max_f32_e32 v229, v229, v229
	v_max_f32_e32 v230, v230, v230
	v_max_f32_e32 v231, v231, v231
	v_max_f32_e32 v232, v232, v232
	v_max_f32_e32 v233, v233, v233
	v_max_f32_e32 v234, v234, v234
	v_max_f32_e32 v235, v235, v235
	v_max_f32_e32 v236, v236, v236
	v_max_f32_e32 v237, v237, v237
	v_max_f32_e32 v238, v238, v238
	v_max_f32_e32 v239, v239, v239
	v_max_f32_e32 v240, v240, v240
	v_max_f32_e32 v241, v241, v241
	v_med3_f32 v226, v226, s62, v95
	v_med3_f32 v227, v227, s62, v95
	v_med3_f32 v228, v228, s62, v95
	v_med3_f32 v229, v229, s62, v95
	v_med3_f32 v230, v230, s62, v95
	v_med3_f32 v231, v231, s62, v95
	v_med3_f32 v232, v232, s62, v95
	v_med3_f32 v233, v233, s62, v95
	v_med3_f32 v234, v234, s62, v95
	v_med3_f32 v235, v235, s62, v95
	v_med3_f32 v236, v236, s62, v95
	v_med3_f32 v237, v237, s62, v95
	v_med3_f32 v238, v238, s62, v95
	v_med3_f32 v239, v239, s62, v95
	v_med3_f32 v240, v240, s62, v95
	v_med3_f32 v241, v241, s62, v95
	v_mov_b32_e32 v242, 0
	v_mov_b32_e32 v243, 0
	v_mov_b32_e32 v244, 0
	v_mov_b32_e32 v245, 0
	v_cvt_pk_fp8_f32 v242, v226, v227
	v_cvt_pk_fp8_f32 v243, v230, v231
	v_cvt_pk_fp8_f32 v244, v234, v235
	v_cvt_pk_fp8_f32 v245, v238, v239
	v_cvt_pk_fp8_f32 v242, v228, v229 op_sel:[0,0,1]
	v_cvt_pk_fp8_f32 v243, v232, v233 op_sel:[0,0,1]
	v_cvt_pk_fp8_f32 v244, v236, v237 op_sel:[0,0,1]
	v_cvt_pk_fp8_f32 v245, v240, v241 op_sel:[0,0,1]
	s_nop 0
	global_store_dwordx4 v79, v[242:245], s[6:7]
	ds_read_b32 v226, v214
	ds_read_b32 v227, v214 offset:512
	ds_read_b32 v228, v214 offset:1024
	ds_read_b32 v229, v214 offset:1536
	ds_read_b32 v230, v214 offset:2048
	ds_read_b32 v231, v214 offset:2560
	ds_read_b32 v232, v214 offset:3072
	ds_read_b32 v233, v214 offset:3584
	ds_read_b32 v234, v214 offset:4096
	ds_read_b32 v235, v214 offset:4608
	ds_read_b32 v236, v214 offset:5120
	ds_read_b32 v237, v214 offset:5632
	ds_read_b32 v238, v214 offset:6144
	ds_read_b32 v239, v214 offset:6656
	ds_read_b32 v240, v214 offset:7168
	ds_read_b32 v241, v214 offset:7680
	s_waitcnt lgkmcnt(0)
	v_max_f32_e32 v226, v226, v226
	v_max_f32_e32 v227, v227, v227
	v_max_f32_e32 v228, v228, v228
	v_max_f32_e32 v229, v229, v229
	v_max_f32_e32 v230, v230, v230
	v_max_f32_e32 v231, v231, v231
	v_max_f32_e32 v232, v232, v232
	v_max_f32_e32 v233, v233, v233
	v_max_f32_e32 v234, v234, v234
	v_max_f32_e32 v235, v235, v235
	v_max_f32_e32 v236, v236, v236
	v_max_f32_e32 v237, v237, v237
	v_max_f32_e32 v238, v238, v238
	v_max_f32_e32 v239, v239, v239
	v_max_f32_e32 v240, v240, v240
	v_max_f32_e32 v241, v241, v241
	v_med3_f32 v226, v226, s62, v95
	v_med3_f32 v227, v227, s62, v95
	v_med3_f32 v228, v228, s62, v95
	v_med3_f32 v229, v229, s62, v95
	v_med3_f32 v230, v230, s62, v95
	v_med3_f32 v231, v231, s62, v95
	v_med3_f32 v232, v232, s62, v95
	v_med3_f32 v233, v233, s62, v95
	v_med3_f32 v234, v234, s62, v95
	v_med3_f32 v235, v235, s62, v95
	v_med3_f32 v236, v236, s62, v95
	v_med3_f32 v237, v237, s62, v95
	v_med3_f32 v238, v238, s62, v95
	v_med3_f32 v239, v239, s62, v95
	v_med3_f32 v240, v240, s62, v95
	v_med3_f32 v241, v241, s62, v95
	v_mov_b32_e32 v242, 0
	v_mov_b32_e32 v243, 0
	v_mov_b32_e32 v244, 0
	v_mov_b32_e32 v245, 0
	v_cvt_pk_fp8_f32 v242, v226, v227
	v_cvt_pk_fp8_f32 v243, v230, v231
	v_cvt_pk_fp8_f32 v244, v234, v235
	v_cvt_pk_fp8_f32 v245, v238, v239
	v_cvt_pk_fp8_f32 v242, v228, v229 op_sel:[0,0,1]
	v_cvt_pk_fp8_f32 v243, v232, v233 op_sel:[0,0,1]
	v_cvt_pk_fp8_f32 v244, v236, v237 op_sel:[0,0,1]
	v_cvt_pk_fp8_f32 v245, v240, v241 op_sel:[0,0,1]
	s_nop 0
	global_store_dwordx4 v80, v[242:245], s[6:7]
	s_waitcnt vmcnt(12)
	v_mul_f32_e32 v144, 0x43000000, v144
	v_mul_f32_e32 v145, 0x43000000, v145
	v_mul_f32_e32 v146, 0x43000000, v146
	v_mul_f32_e32 v147, 0x43000000, v147
	ds_write_b128 v209, v[144:147]
	v_mul_f32_e32 v148, 0x43000000, v148
	v_mul_f32_e32 v149, 0x43000000, v149
	v_mul_f32_e32 v150, 0x43000000, v150
	v_mul_f32_e32 v151, 0x43000000, v151
	ds_write_b128 v209, v[148:151] offset:1024
	v_mul_f32_e32 v152, 0x43000000, v152
	v_mul_f32_e32 v153, 0x43000000, v153
	v_mul_f32_e32 v154, 0x43000000, v154
	v_mul_f32_e32 v155, 0x43000000, v155
	ds_write_b128 v209, v[152:155] offset:2048
	v_mul_f32_e32 v156, 0x43000000, v156
	v_mul_f32_e32 v157, 0x43000000, v157
	v_mul_f32_e32 v158, 0x43000000, v158
	v_mul_f32_e32 v159, 0x43000000, v159
	ds_write_b128 v209, v[156:159] offset:3072
	v_mul_f32_e32 v160, 0x43000000, v160
	v_mul_f32_e32 v161, 0x43000000, v161
	v_mul_f32_e32 v162, 0x43000000, v162
	v_mul_f32_e32 v163, 0x43000000, v163
	ds_write_b128 v209, v[160:163] offset:4096
	v_mul_f32_e32 v164, 0x43000000, v164
	v_mul_f32_e32 v165, 0x43000000, v165
	v_mul_f32_e32 v166, 0x43000000, v166
	v_mul_f32_e32 v167, 0x43000000, v167
	ds_write_b128 v209, v[164:167] offset:5120
	v_mul_f32_e32 v168, 0x43000000, v168
	v_mul_f32_e32 v169, 0x43000000, v169
	v_mul_f32_e32 v170, 0x43000000, v170
	v_mul_f32_e32 v171, 0x43000000, v171
	ds_write_b128 v209, v[168:171] offset:6144
	v_mul_f32_e32 v172, 0x43000000, v172
	v_mul_f32_e32 v173, 0x43000000, v173
	v_mul_f32_e32 v174, 0x43000000, v174
	v_mul_f32_e32 v175, 0x43000000, v175
	ds_write_b128 v209, v[172:175] offset:7168
	s_waitcnt lgkmcnt(0)
	s_barrier
; #define GAS __attribute__((address_space(1)))
; #define LAS __attribute__((address_space(3)))
; #define LDS_WAIT() asm volatile("s_waitcnt lgkmcnt(0)" ::: "memory")
; __device__ __forceinline__ unsigned pk4_fp8(float a, float b, float c, float d) {
;     a = fminf(fmaxf(a, -448.f), 448.f); b = fminf(fmaxf(b, -448.f), 448.f); c = fminf(fmaxf(c, -448.f), 448.f); d = fminf(fmaxf(d, -448.f), 448.f);
;     int w = __builtin_amdgcn_cvt_pk_fp8_f32(a, b, 0, false); w = __builtin_amdgcn_cvt_pk_fp8_f32(c, d, w, true); return (unsigned)w; }
;     ...
; #pragma unroll
;     for (int i = 0; i < 32; ++i) v[i] = sc >= 0 ? W[(size_t)(k0 + 2 * i + (lane >> 5)) * Nsrc + sc] : 0.f;
; #pragma unroll
;     for (int i = 0; i < 32; ++i) { const int k = k0 + 2 * i + (lane >> 5); float x = v[i] * wscale; if (KS) x *= (k < ksplit ? ksA[k] : ksB[k - ksplit]); scr[(2 * i + (lane >> 5)) * 33 + (lane & 31)] = x; }
;     LDS_WAIT(); asm volatile("" ::: "memory");
;     const int c = lane & 7;
; #pragma unroll
;     for (int j = 0; j < 4; ++j) { const int n = (lane >> 3) + 8 * j; const LAS float* s = scr + (8 * c) * 33 + n;
;         const unsigned long long o = (unsigned long long)pg8::pk4_fp8(s[0 * 33], s[1 * 33], s[2 * 33], s[3 * 33]) | ((unsigned long long)pg8::pk4_fp8(s[4 * 33], s[5 * 33], s[6 * 33], s[7 * 33]) << 32);
;         *(GAS unsigned long long*)(WT + (size_t)(n0 + n) * K + k0 + 8 * c) = o; }
	s_add_u32 s8, s38, 0x4002000
	s_addc_u32 s9, s39, 0
	global_load_dwordx4 v[144:147], v75, s[8:9]
	s_add_u32 s8, s8, 0x8000
	s_addc_u32 s9, s9, 0
	global_load_dwordx4 v[148:151], v75, s[8:9]
	s_add_u32 s8, s8, 0x8000
	s_addc_u32 s9, s9, 0
	global_load_dwordx4 v[152:155], v75, s[8:9]
	s_add_u32 s8, s8, 0x8000
	s_addc_u32 s9, s9, 0
	global_load_dwordx4 v[156:159], v75, s[8:9]
	s_add_u32 s8, s8, 0x8000
	s_addc_u32 s9, s9, 0
	global_load_dwordx4 v[160:163], v75, s[8:9]
	s_add_u32 s8, s8, 0x8000
	s_addc_u32 s9, s9, 0
	global_load_dwordx4 v[164:167], v75, s[8:9]
	s_add_u32 s8, s8, 0x8000
	s_addc_u32 s9, s9, 0
	global_load_dwordx4 v[168:171], v75, s[8:9]
	s_add_u32 s8, s8, 0x8000
	s_addc_u32 s9, s9, 0
	global_load_dwordx4 v[172:175], v75, s[8:9]
	s_add_u32 s6, s40, 0x1000
	s_addc_u32 s7, s41, 0
	ds_read_b32 v226, v211
	ds_read_b32 v227, v211 offset:512
	ds_read_b32 v228, v211 offset:1024
	ds_read_b32 v229, v211 offset:1536
	ds_read_b32 v230, v211 offset:2048
	ds_read_b32 v231, v211 offset:2560
	ds_read_b32 v232, v211 offset:3072
	ds_read_b32 v233, v211 offset:3584
	ds_read_b32 v234, v211 offset:4096
	ds_read_b32 v235, v211 offset:4608
	ds_read_b32 v236, v211 offset:5120
	ds_read_b32 v237, v211 offset:5632
	ds_read_b32 v238, v211 offset:6144
	ds_read_b32 v239, v211 offset:6656
	ds_read_b32 v240, v211 offset:7168
	ds_read_b32 v241, v211 offset:7680
	s_waitcnt lgkmcnt(0)
	v_max_f32_e32 v226, v226, v226
	v_max_f32_e32 v227, v227, v227
	v_max_f32_e32 v228, v228, v228
	v_max_f32_e32 v229, v229, v229
	v_max_f32_e32 v230, v230, v230
	v_max_f32_e32 v231, v231, v231
	v_max_f32_e32 v232, v232, v232
	v_max_f32_e32 v233, v233, v233
	v_max_f32_e32 v234, v234, v234
	v_max_f32_e32 v235, v235, v235
	v_max_f32_e32 v236, v236, v236
	v_max_f32_e32 v237, v237, v237
	v_max_f32_e32 v238, v238, v238
	v_max_f32_e32 v239, v239, v239
	v_max_f32_e32 v240, v240, v240
	v_max_f32_e32 v241, v241, v241
	v_med3_f32 v226, v226, s62, v95
	v_med3_f32 v227, v227, s62, v95
	v_med3_f32 v228, v228, s62, v95
	v_med3_f32 v229, v229, s62, v95
	v_med3_f32 v230, v230, s62, v95
	v_med3_f32 v231, v231, s62, v95
	v_med3_f32 v232, v232, s62, v95
	v_med3_f32 v233, v233, s62, v95
	v_med3_f32 v234, v234, s62, v95
	v_med3_f32 v235, v235, s62, v95
	v_med3_f32 v236, v236, s62, v95
	v_med3_f32 v237, v237, s62, v95
	v_med3_f32 v238, v238, s62, v95
	v_med3_f32 v239, v239, s62, v95
	v_med3_f32 v240, v240, s62, v95
	v_med3_f32 v241, v241, s62, v95
	v_mov_b32_e32 v242, 0
	v_mov_b32_e32 v243, 0
	v_mov_b32_e32 v244, 0
	v_mov_b32_e32 v245, 0
	v_cvt_pk_fp8_f32 v242, v226, v227
	v_cvt_pk_fp8_f32 v243, v230, v231
	v_cvt_pk_fp8_f32 v244, v234, v235
	v_cvt_pk_fp8_f32 v245, v238, v239
	v_cvt_pk_fp8_f32 v242, v228, v229 op_sel:[0,0,1]
	v_cvt_pk_fp8_f32 v243, v232, v233 op_sel:[0,0,1]
	v_cvt_pk_fp8_f32 v244, v236, v237 op_sel:[0,0,1]
	v_cvt_pk_fp8_f32 v245, v240, v241 op_sel:[0,0,1]
	s_nop 0
	global_store_dwordx4 v79, v[242:245], s[6:7]
	ds_read_b32 v226, v213
	ds_read_b32 v227, v213 offset:512
	ds_read_b32 v228, v213 offset:1024
	ds_read_b32 v229, v213 offset:1536
	ds_read_b32 v230, v213 offset:2048
	ds_read_b32 v231, v213 offset:2560
	ds_read_b32 v232, v213 offset:3072
	ds_read_b32 v233, v213 offset:3584
	ds_read_b32 v234, v213 offset:4096
	ds_read_b32 v235, v213 offset:4608
	ds_read_b32 v236, v213 offset:5120
	ds_read_b32 v237, v213 offset:5632
	ds_read_b32 v238, v213 offset:6144
	ds_read_b32 v239, v213 offset:6656
	ds_read_b32 v240, v213 offset:7168
	ds_read_b32 v241, v213 offset:7680
	s_waitcnt lgkmcnt(0)
	v_max_f32_e32 v226, v226, v226
	v_max_f32_e32 v227, v227, v227
	v_max_f32_e32 v228, v228, v228
	v_max_f32_e32 v229, v229, v229
	v_max_f32_e32 v230, v230, v230
	v_max_f32_e32 v231, v231, v231
	v_max_f32_e32 v232, v232, v232
	v_max_f32_e32 v233, v233, v233
	v_max_f32_e32 v234, v234, v234
	v_max_f32_e32 v235, v235, v235
	v_max_f32_e32 v236, v236, v236
	v_max_f32_e32 v237, v237, v237
	v_max_f32_e32 v238, v238, v238
	v_max_f32_e32 v239, v239, v239
	v_max_f32_e32 v240, v240, v240
	v_max_f32_e32 v241, v241, v241
	v_med3_f32 v226, v226, s62, v95
	v_med3_f32 v227, v227, s62, v95
	v_med3_f32 v228, v228, s62, v95
	v_med3_f32 v229, v229, s62, v95
	v_med3_f32 v230, v230, s62, v95
	v_med3_f32 v231, v231, s62, v95
	v_med3_f32 v232, v232, s62, v95
	v_med3_f32 v233, v233, s62, v95
	v_med3_f32 v234, v234, s62, v95
	v_med3_f32 v235, v235, s62, v95
	v_med3_f32 v236, v236, s62, v95
	v_med3_f32 v237, v237, s62, v95
	v_med3_f32 v238, v238, s62, v95
	v_med3_f32 v239, v239, s62, v95
	v_med3_f32 v240, v240, s62, v95
	v_med3_f32 v241, v241, s62, v95
	v_mov_b32_e32 v242, 0
	v_mov_b32_e32 v243, 0
	v_mov_b32_e32 v244, 0
	v_mov_b32_e32 v245, 0
	v_cvt_pk_fp8_f32 v242, v226, v227
	v_cvt_pk_fp8_f32 v243, v230, v231
	v_cvt_pk_fp8_f32 v244, v234, v235
	v_cvt_pk_fp8_f32 v245, v238, v239
	v_cvt_pk_fp8_f32 v242, v228, v229 op_sel:[0,0,1]
	v_cvt_pk_fp8_f32 v243, v232, v233 op_sel:[0,0,1]
	v_cvt_pk_fp8_f32 v244, v236, v237 op_sel:[0,0,1]
	v_cvt_pk_fp8_f32 v245, v240, v241 op_sel:[0,0,1]
	s_nop 0
	global_store_dwordx4 v80, v[242:245], s[6:7]
	s_waitcnt vmcnt(12)
	v_mul_f32_e32 v176, 0x43000000, v176
	v_mul_f32_e32 v177, 0x43000000, v177
	v_mul_f32_e32 v178, 0x43000000, v178
	v_mul_f32_e32 v179, 0x43000000, v179
	ds_write_b128 v210, v[176:179]
	v_mul_f32_e32 v180, 0x43000000, v180
	v_mul_f32_e32 v181, 0x43000000, v181
	v_mul_f32_e32 v182, 0x43000000, v182
	v_mul_f32_e32 v183, 0x43000000, v183
	ds_write_b128 v210, v[180:183] offset:1024
	v_mul_f32_e32 v184, 0x43000000, v184
	v_mul_f32_e32 v185, 0x43000000, v185
	v_mul_f32_e32 v186, 0x43000000, v186
	v_mul_f32_e32 v187, 0x43000000, v187
	ds_write_b128 v210, v[184:187] offset:2048
	v_mul_f32_e32 v188, 0x43000000, v188
	v_mul_f32_e32 v189, 0x43000000, v189
	v_mul_f32_e32 v190, 0x43000000, v190
	v_mul_f32_e32 v191, 0x43000000, v191
	ds_write_b128 v210, v[188:191] offset:3072
	v_mul_f32_e32 v192, 0x43000000, v192
	v_mul_f32_e32 v193, 0x43000000, v193
	v_mul_f32_e32 v194, 0x43000000, v194
	v_mul_f32_e32 v195, 0x43000000, v195
	ds_write_b128 v210, v[192:195] offset:4096
	v_mul_f32_e32 v196, 0x43000000, v196
	v_mul_f32_e32 v197, 0x43000000, v197
	v_mul_f32_e32 v198, 0x43000000, v198
	v_mul_f32_e32 v199, 0x43000000, v199
	ds_write_b128 v210, v[196:199] offset:5120
	v_mul_f32_e32 v200, 0x43000000, v200
	v_mul_f32_e32 v201, 0x43000000, v201
	v_mul_f32_e32 v202, 0x43000000, v202
	v_mul_f32_e32 v203, 0x43000000, v203
	ds_write_b128 v210, v[200:203] offset:6144
	v_mul_f32_e32 v204, 0x43000000, v204
	v_mul_f32_e32 v205, 0x43000000, v205
	v_mul_f32_e32 v206, 0x43000000, v206
	v_mul_f32_e32 v207, 0x43000000, v207
	ds_write_b128 v210, v[204:207] offset:7168
	s_waitcnt lgkmcnt(0)
	s_barrier
; #define GAS __attribute__((address_space(1)))
; #define LAS __attribute__((address_space(3)))
; #define LDS_WAIT() asm volatile("s_waitcnt lgkmcnt(0)" ::: "memory")
; __device__ __forceinline__ unsigned pk4_fp8(float a, float b, float c, float d) {
;     a = fminf(fmaxf(a, -448.f), 448.f); b = fminf(fmaxf(b, -448.f), 448.f); c = fminf(fmaxf(c, -448.f), 448.f); d = fminf(fmaxf(d, -448.f), 448.f);
;     int w = __builtin_amdgcn_cvt_pk_fp8_f32(a, b, 0, false); w = __builtin_amdgcn_cvt_pk_fp8_f32(c, d, w, true); return (unsigned)w; }
;     ...
; #pragma unroll
;     for (int i = 0; i < 32; ++i) v[i] = sc >= 0 ? W[(size_t)(k0 + 2 * i + (lane >> 5)) * Nsrc + sc] : 0.f;
; #pragma unroll
;     for (int i = 0; i < 32; ++i) { const int k = k0 + 2 * i + (lane >> 5); float x = v[i] * wscale; if (KS) x *= (k < ksplit ? ksA[k] : ksB[k - ksplit]); scr[(2 * i + (lane >> 5)) * 33 + (lane & 31)] = x; }
;     LDS_WAIT(); asm volatile("" ::: "memory");
;     const int c = lane & 7;
; #pragma unroll
;     for (int j = 0; j < 4; ++j) { const int n = (lane >> 3) + 8 * j; const LAS float* s = scr + (8 * c) * 33 + n;
;         const unsigned long long o = (unsigned long long)pg8::pk4_fp8(s[0 * 33], s[1 * 33], s[2 * 33], s[3 * 33]) | ((unsigned long long)pg8::pk4_fp8(s[4 * 33], s[5 * 33], s[6 * 33], s[7 * 33]) << 32);
;         *(GAS unsigned long long*)(WT + (size_t)(n0 + n) * K + k0 + 8 * c) = o; }
	s_add_u32 s8, s38, 0x4003000
	s_addc_u32 s9, s39, 0
	global_load_dwordx4 v[176:179], v75, s[8:9]
	s_add_u32 s8, s8, 0x8000
	s_addc_u32 s9, s9, 0
	global_load_dwordx4 v[180:183], v75, s[8:9]
	s_add_u32 s8, s8, 0x8000
	s_addc_u32 s9, s9, 0
	global_load_dwordx4 v[184:187], v75, s[8:9]
	s_add_u32 s8, s8, 0x8000
	s_addc_u32 s9, s9, 0
	global_load_dwordx4 v[188:191], v75, s[8:9]
	s_add_u32 s8, s8, 0x8000
	s_addc_u32 s9, s9, 0
	global_load_dwordx4 v[192:195], v75, s[8:9]
	s_add_u32 s8, s8, 0x8000
	s_addc_u32 s9, s9, 0
	global_load_dwordx4 v[196:199], v75, s[8:9]
	s_add_u32 s8, s8, 0x8000
	s_addc_u32 s9, s9, 0
	global_load_dwordx4 v[200:203], v75, s[8:9]
	s_add_u32 s8, s8, 0x8000
	s_addc_u32 s9, s9, 0
	global_load_dwordx4 v[204:207], v75, s[8:9]
	s_add_u32 s6, s40, 0x1001000
	s_addc_u32 s7, s41, 0
	ds_read_b32 v226, v212
	ds_read_b32 v227, v212 offset:512
	ds_read_b32 v228, v212 offset:1024
	ds_read_b32 v229, v212 offset:1536
	ds_read_b32 v230, v212 offset:2048
	ds_read_b32 v231, v212 offset:2560
	ds_read_b32 v232, v212 offset:3072
	ds_read_b32 v233, v212 offset:3584
	ds_read_b32 v234, v212 offset:4096
	ds_read_b32 v235, v212 offset:4608
	ds_read_b32 v236, v212 offset:5120
	ds_read_b32 v237, v212 offset:5632
	ds_read_b32 v238, v212 offset:6144
	ds_read_b32 v239, v212 offset:6656
	ds_read_b32 v240, v212 offset:7168
	ds_read_b32 v241, v212 offset:7680
	s_waitcnt lgkmcnt(0)
	v_max_f32_e32 v226, v226, v226
	v_max_f32_e32 v227, v227, v227
	v_max_f32_e32 v228, v228, v228
	v_max_f32_e32 v229, v229, v229
	v_max_f32_e32 v230, v230, v230
	v_max_f32_e32 v231, v231, v231
	v_max_f32_e32 v232, v232, v232
	v_max_f32_e32 v233, v233, v233
	v_max_f32_e32 v234, v234, v234
	v_max_f32_e32 v235, v235, v235
	v_max_f32_e32 v236, v236, v236
	v_max_f32_e32 v237, v237, v237
	v_max_f32_e32 v238, v238, v238
	v_max_f32_e32 v239, v239, v239
	v_max_f32_e32 v240, v240, v240
	v_max_f32_e32 v241, v241, v241
	v_med3_f32 v226, v226, s62, v95
	v_med3_f32 v227, v227, s62, v95
	v_med3_f32 v228, v228, s62, v95
	v_med3_f32 v229, v229, s62, v95
	v_med3_f32 v230, v230, s62, v95
	v_med3_f32 v231, v231, s62, v95
	v_med3_f32 v232, v232, s62, v95
	v_med3_f32 v233, v233, s62, v95
	v_med3_f32 v234, v234, s62, v95
	v_med3_f32 v235, v235, s62, v95
	v_med3_f32 v236, v236, s62, v95
	v_med3_f32 v237, v237, s62, v95
	v_med3_f32 v238, v238, s62, v95
	v_med3_f32 v239, v239, s62, v95
	v_med3_f32 v240, v240, s62, v95
	v_med3_f32 v241, v241, s62, v95
	v_mov_b32_e32 v242, 0
	v_mov_b32_e32 v243, 0
	v_mov_b32_e32 v244, 0
	v_mov_b32_e32 v245, 0
	v_cvt_pk_fp8_f32 v242, v226, v227
	v_cvt_pk_fp8_f32 v243, v230, v231
	v_cvt_pk_fp8_f32 v244, v234, v235
	v_cvt_pk_fp8_f32 v245, v238, v239
	v_cvt_pk_fp8_f32 v242, v228, v229 op_sel:[0,0,1]
	v_cvt_pk_fp8_f32 v243, v232, v233 op_sel:[0,0,1]
	v_cvt_pk_fp8_f32 v244, v236, v237 op_sel:[0,0,1]
	v_cvt_pk_fp8_f32 v245, v240, v241 op_sel:[0,0,1]
	s_nop 0
	global_store_dwordx4 v79, v[242:245], s[6:7]
	ds_read_b32 v226, v214
	ds_read_b32 v227, v214 offset:512
	ds_read_b32 v228, v214 offset:1024
	ds_read_b32 v229, v214 offset:1536
	ds_read_b32 v230, v214 offset:2048
	ds_read_b32 v231, v214 offset:2560
	ds_read_b32 v232, v214 offset:3072
	ds_read_b32 v233, v214 offset:3584
	ds_read_b32 v234, v214 offset:4096
	ds_read_b32 v235, v214 offset:4608
	ds_read_b32 v236, v214 offset:5120
	ds_read_b32 v237, v214 offset:5632
	ds_read_b32 v238, v214 offset:6144
	ds_read_b32 v239, v214 offset:6656
	ds_read_b32 v240, v214 offset:7168
	ds_read_b32 v241, v214 offset:7680
	s_waitcnt lgkmcnt(0)
	v_max_f32_e32 v226, v226, v226
	v_max_f32_e32 v227, v227, v227
	v_max_f32_e32 v228, v228, v228
	v_max_f32_e32 v229, v229, v229
	v_max_f32_e32 v230, v230, v230
	v_max_f32_e32 v231, v231, v231
	v_max_f32_e32 v232, v232, v232
	v_max_f32_e32 v233, v233, v233
	v_max_f32_e32 v234, v234, v234
	v_max_f32_e32 v235, v235, v235
	v_max_f32_e32 v236, v236, v236
	v_max_f32_e32 v237, v237, v237
	v_max_f32_e32 v238, v238, v238
	v_max_f32_e32 v239, v239, v239
	v_max_f32_e32 v240, v240, v240
	v_max_f32_e32 v241, v241, v241
	v_med3_f32 v226, v226, s62, v95
	v_med3_f32 v227, v227, s62, v95
	v_med3_f32 v228, v228, s62, v95
	v_med3_f32 v229, v229, s62, v95
	v_med3_f32 v230, v230, s62, v95
	v_med3_f32 v231, v231, s62, v95
	v_med3_f32 v232, v232, s62, v95
	v_med3_f32 v233, v233, s62, v95
	v_med3_f32 v234, v234, s62, v95
	v_med3_f32 v235, v235, s62, v95
	v_med3_f32 v236, v236, s62, v95
	v_med3_f32 v237, v237, s62, v95
	v_med3_f32 v238, v238, s62, v95
	v_med3_f32 v239, v239, s62, v95
	v_med3_f32 v240, v240, s62, v95
	v_med3_f32 v241, v241, s62, v95
	v_mov_b32_e32 v242, 0
	v_mov_b32_e32 v243, 0
	v_mov_b32_e32 v244, 0
	v_mov_b32_e32 v245, 0
	v_cvt_pk_fp8_f32 v242, v226, v227
	v_cvt_pk_fp8_f32 v243, v230, v231
	v_cvt_pk_fp8_f32 v244, v234, v235
	v_cvt_pk_fp8_f32 v245, v238, v239
	v_cvt_pk_fp8_f32 v242, v228, v229 op_sel:[0,0,1]
	v_cvt_pk_fp8_f32 v243, v232, v233 op_sel:[0,0,1]
	v_cvt_pk_fp8_f32 v244, v236, v237 op_sel:[0,0,1]
	v_cvt_pk_fp8_f32 v245, v240, v241 op_sel:[0,0,1]
	s_nop 0
	global_store_dwordx4 v80, v[242:245], s[6:7]
	s_waitcnt vmcnt(12)
	v_mul_f32_e32 v144, 0x43000000, v144
	v_mul_f32_e32 v145, 0x43000000, v145
	v_mul_f32_e32 v146, 0x43000000, v146
	v_mul_f32_e32 v147, 0x43000000, v147
	ds_write_b128 v209, v[144:147]
	v_mul_f32_e32 v148, 0x43000000, v148
	v_mul_f32_e32 v149, 0x43000000, v149
	v_mul_f32_e32 v150, 0x43000000, v150
	v_mul_f32_e32 v151, 0x43000000, v151
	ds_write_b128 v209, v[148:151] offset:1024
	v_mul_f32_e32 v152, 0x43000000, v152
	v_mul_f32_e32 v153, 0x43000000, v153
	v_mul_f32_e32 v154, 0x43000000, v154
	v_mul_f32_e32 v155, 0x43000000, v155
	ds_write_b128 v209, v[152:155] offset:2048
	v_mul_f32_e32 v156, 0x43000000, v156
	v_mul_f32_e32 v157, 0x43000000, v157
	v_mul_f32_e32 v158, 0x43000000, v158
	v_mul_f32_e32 v159, 0x43000000, v159
	ds_write_b128 v209, v[156:159] offset:3072
	v_mul_f32_e32 v160, 0x43000000, v160
	v_mul_f32_e32 v161, 0x43000000, v161
	v_mul_f32_e32 v162, 0x43000000, v162
	v_mul_f32_e32 v163, 0x43000000, v163
	ds_write_b128 v209, v[160:163] offset:4096
	v_mul_f32_e32 v164, 0x43000000, v164
	v_mul_f32_e32 v165, 0x43000000, v165
	v_mul_f32_e32 v166, 0x43000000, v166
	v_mul_f32_e32 v167, 0x43000000, v167
	ds_write_b128 v209, v[164:167] offset:5120
	v_mul_f32_e32 v168, 0x43000000, v168
	v_mul_f32_e32 v169, 0x43000000, v169
	v_mul_f32_e32 v170, 0x43000000, v170
	v_mul_f32_e32 v171, 0x43000000, v171
	ds_write_b128 v209, v[168:171] offset:6144
	v_mul_f32_e32 v172, 0x43000000, v172
	v_mul_f32_e32 v173, 0x43000000, v173
	v_mul_f32_e32 v174, 0x43000000, v174
	v_mul_f32_e32 v175, 0x43000000, v175
	ds_write_b128 v209, v[172:175] offset:7168
	s_waitcnt lgkmcnt(0)
	s_barrier
; #define GAS __attribute__((address_space(1)))
; #define LAS __attribute__((address_space(3)))
; #define LDS_WAIT() asm volatile("s_waitcnt lgkmcnt(0)" ::: "memory")
; __device__ __forceinline__ unsigned pk4_fp8(float a, float b, float c, float d) {
;     a = fminf(fmaxf(a, -448.f), 448.f); b = fminf(fmaxf(b, -448.f), 448.f); c = fminf(fmaxf(c, -448.f), 448.f); d = fminf(fmaxf(d, -448.f), 448.f);
;     int w = __builtin_amdgcn_cvt_pk_fp8_f32(a, b, 0, false); w = __builtin_amdgcn_cvt_pk_fp8_f32(c, d, w, true); return (unsigned)w; }
;     ...
; #pragma unroll
;     for (int i = 0; i < 32; ++i) v[i] = sc >= 0 ? W[(size_t)(k0 + 2 * i + (lane >> 5)) * Nsrc + sc] : 0.f;
; #pragma unroll
;     for (int i = 0; i < 32; ++i) { const int k = k0 + 2 * i + (lane >> 5); float x = v[i] * wscale; if (KS) x *= (k < ksplit ? ksA[k] : ksB[k - ksplit]); scr[(2 * i + (lane >> 5)) * 33 + (lane & 31)] = x; }
;     LDS_WAIT(); asm volatile("" ::: "memory");
;     const int c = lane & 7;
; #pragma unroll
;     for (int j = 0; j < 4; ++j) { const int n = (lane >> 3) + 8 * j; const LAS float* s = scr + (8 * c) * 33 + n;
;         const unsigned long long o = (unsigned long long)pg8::pk4_fp8(s[0 * 33], s[1 * 33], s[2 * 33], s[3 * 33]) | ((unsigned long long)pg8::pk4_fp8(s[4 * 33], s[5 * 33], s[6 * 33], s[7 * 33]) << 32);
;         *(GAS unsigned long long*)(WT + (size_t)(n0 + n) * K + k0 + 8 * c) = o; }
	s_add_u32 s8, s38, 0x8000000
	s_addc_u32 s9, s39, 0
	global_load_dwordx4 v[144:147], v75, s[8:9]
	s_add_u32 s8, s8, 0x8000
	s_addc_u32 s9, s9, 0
	global_load_dwordx4 v[148:151], v75, s[8:9]
	s_add_u32 s8, s8, 0x8000
	s_addc_u32 s9, s9, 0
	global_load_dwordx4 v[152:155], v75, s[8:9]
	s_add_u32 s8, s8, 0x8000
	s_addc_u32 s9, s9, 0
	global_load_dwordx4 v[156:159], v75, s[8:9]
	s_add_u32 s8, s8, 0x8000
	s_addc_u32 s9, s9, 0
	global_load_dwordx4 v[160:163], v75, s[8:9]
	s_add_u32 s8, s8, 0x8000
	s_addc_u32 s9, s9, 0
	global_load_dwordx4 v[164:167], v75, s[8:9]
	s_add_u32 s8, s8, 0x8000
	s_addc_u32 s9, s9, 0
	global_load_dwordx4 v[168:171], v75, s[8:9]
	s_add_u32 s8, s8, 0x8000
	s_addc_u32 s9, s9, 0
	global_load_dwordx4 v[172:175], v75, s[8:9]
	s_add_u32 s6, s40, 0x2001000
	s_addc_u32 s7, s41, 0
	ds_read_b32 v226, v211
	ds_read_b32 v227, v211 offset:512
	ds_read_b32 v228, v211 offset:1024
	ds_read_b32 v229, v211 offset:1536
	ds_read_b32 v230, v211 offset:2048
	ds_read_b32 v231, v211 offset:2560
	ds_read_b32 v232, v211 offset:3072
	ds_read_b32 v233, v211 offset:3584
	ds_read_b32 v234, v211 offset:4096
	ds_read_b32 v235, v211 offset:4608
	ds_read_b32 v236, v211 offset:5120
	ds_read_b32 v237, v211 offset:5632
	ds_read_b32 v238, v211 offset:6144
	ds_read_b32 v239, v211 offset:6656
	ds_read_b32 v240, v211 offset:7168
	ds_read_b32 v241, v211 offset:7680
	s_waitcnt lgkmcnt(0)
	v_max_f32_e32 v226, v226, v226
	v_max_f32_e32 v227, v227, v227
	v_max_f32_e32 v228, v228, v228
	v_max_f32_e32 v229, v229, v229
	v_max_f32_e32 v230, v230, v230
	v_max_f32_e32 v231, v231, v231
	v_max_f32_e32 v232, v232, v232
	v_max_f32_e32 v233, v233, v233
	v_max_f32_e32 v234, v234, v234
	v_max_f32_e32 v235, v235, v235
	v_max_f32_e32 v236, v236, v236
	v_max_f32_e32 v237, v237, v237
	v_max_f32_e32 v238, v238, v238
	v_max_f32_e32 v239, v239, v239
	v_max_f32_e32 v240, v240, v240
	v_max_f32_e32 v241, v241, v241
	v_med3_f32 v226, v226, s62, v95
	v_med3_f32 v227, v227, s62, v95
	v_med3_f32 v228, v228, s62, v95
	v_med3_f32 v229, v229, s62, v95
	v_med3_f32 v230, v230, s62, v95
	v_med3_f32 v231, v231, s62, v95
	v_med3_f32 v232, v232, s62, v95
	v_med3_f32 v233, v233, s62, v95
	v_med3_f32 v234, v234, s62, v95
	v_med3_f32 v235, v235, s62, v95
	v_med3_f32 v236, v236, s62, v95
	v_med3_f32 v237, v237, s62, v95
	v_med3_f32 v238, v238, s62, v95
	v_med3_f32 v239, v239, s62, v95
	v_med3_f32 v240, v240, s62, v95
	v_med3_f32 v241, v241, s62, v95
	v_mov_b32_e32 v242, 0
	v_mov_b32_e32 v243, 0
	v_mov_b32_e32 v244, 0
	v_mov_b32_e32 v245, 0
	v_cvt_pk_fp8_f32 v242, v226, v227
	v_cvt_pk_fp8_f32 v243, v230, v231
	v_cvt_pk_fp8_f32 v244, v234, v235
	v_cvt_pk_fp8_f32 v245, v238, v239
	v_cvt_pk_fp8_f32 v242, v228, v229 op_sel:[0,0,1]
	v_cvt_pk_fp8_f32 v243, v232, v233 op_sel:[0,0,1]
	v_cvt_pk_fp8_f32 v244, v236, v237 op_sel:[0,0,1]
	v_cvt_pk_fp8_f32 v245, v240, v241 op_sel:[0,0,1]
	s_nop 0
	global_store_dwordx4 v79, v[242:245], s[6:7]
	ds_read_b32 v226, v213
	ds_read_b32 v227, v213 offset:512
	ds_read_b32 v228, v213 offset:1024
	ds_read_b32 v229, v213 offset:1536
	ds_read_b32 v230, v213 offset:2048
	ds_read_b32 v231, v213 offset:2560
	ds_read_b32 v232, v213 offset:3072
	ds_read_b32 v233, v213 offset:3584
	ds_read_b32 v234, v213 offset:4096
	ds_read_b32 v235, v213 offset:4608
	ds_read_b32 v236, v213 offset:5120
	ds_read_b32 v237, v213 offset:5632
	ds_read_b32 v238, v213 offset:6144
	ds_read_b32 v239, v213 offset:6656
	ds_read_b32 v240, v213 offset:7168
	ds_read_b32 v241, v213 offset:7680
	s_waitcnt lgkmcnt(0)
	v_max_f32_e32 v226, v226, v226
	v_max_f32_e32 v227, v227, v227
	v_max_f32_e32 v228, v228, v228
	v_max_f32_e32 v229, v229, v229
	v_max_f32_e32 v230, v230, v230
	v_max_f32_e32 v231, v231, v231
	v_max_f32_e32 v232, v232, v232
	v_max_f32_e32 v233, v233, v233
	v_max_f32_e32 v234, v234, v234
	v_max_f32_e32 v235, v235, v235
	v_max_f32_e32 v236, v236, v236
	v_max_f32_e32 v237, v237, v237
	v_max_f32_e32 v238, v238, v238
	v_max_f32_e32 v239, v239, v239
	v_max_f32_e32 v240, v240, v240
	v_max_f32_e32 v241, v241, v241
	v_med3_f32 v226, v226, s62, v95
	v_med3_f32 v227, v227, s62, v95
	v_med3_f32 v228, v228, s62, v95
	v_med3_f32 v229, v229, s62, v95
	v_med3_f32 v230, v230, s62, v95
	v_med3_f32 v231, v231, s62, v95
	v_med3_f32 v232, v232, s62, v95
	v_med3_f32 v233, v233, s62, v95
	v_med3_f32 v234, v234, s62, v95
	v_med3_f32 v235, v235, s62, v95
	v_med3_f32 v236, v236, s62, v95
	v_med3_f32 v237, v237, s62, v95
	v_med3_f32 v238, v238, s62, v95
	v_med3_f32 v239, v239, s62, v95
	v_med3_f32 v240, v240, s62, v95
	v_med3_f32 v241, v241, s62, v95
	v_mov_b32_e32 v242, 0
	v_mov_b32_e32 v243, 0
	v_mov_b32_e32 v244, 0
	v_mov_b32_e32 v245, 0
	v_cvt_pk_fp8_f32 v242, v226, v227
	v_cvt_pk_fp8_f32 v243, v230, v231
	v_cvt_pk_fp8_f32 v244, v234, v235
	v_cvt_pk_fp8_f32 v245, v238, v239
	v_cvt_pk_fp8_f32 v242, v228, v229 op_sel:[0,0,1]
	v_cvt_pk_fp8_f32 v243, v232, v233 op_sel:[0,0,1]
	v_cvt_pk_fp8_f32 v244, v236, v237 op_sel:[0,0,1]
	v_cvt_pk_fp8_f32 v245, v240, v241 op_sel:[0,0,1]
	s_nop 0
	global_store_dwordx4 v80, v[242:245], s[6:7]
	s_waitcnt vmcnt(12)
	v_mul_f32_e32 v176, 0x43000000, v176
	v_mul_f32_e32 v177, 0x43000000, v177
	v_mul_f32_e32 v178, 0x43000000, v178
	v_mul_f32_e32 v179, 0x43000000, v179
	ds_write_b128 v210, v[176:179]
	v_mul_f32_e32 v180, 0x43000000, v180
	v_mul_f32_e32 v181, 0x43000000, v181
	v_mul_f32_e32 v182, 0x43000000, v182
	v_mul_f32_e32 v183, 0x43000000, v183
	ds_write_b128 v210, v[180:183] offset:1024
	v_mul_f32_e32 v184, 0x43000000, v184
	v_mul_f32_e32 v185, 0x43000000, v185
	v_mul_f32_e32 v186, 0x43000000, v186
	v_mul_f32_e32 v187, 0x43000000, v187
	ds_write_b128 v210, v[184:187] offset:2048
	v_mul_f32_e32 v188, 0x43000000, v188
	v_mul_f32_e32 v189, 0x43000000, v189
	v_mul_f32_e32 v190, 0x43000000, v190
	v_mul_f32_e32 v191, 0x43000000, v191
	ds_write_b128 v210, v[188:191] offset:3072
	v_mul_f32_e32 v192, 0x43000000, v192
	v_mul_f32_e32 v193, 0x43000000, v193
	v_mul_f32_e32 v194, 0x43000000, v194
	v_mul_f32_e32 v195, 0x43000000, v195
	ds_write_b128 v210, v[192:195] offset:4096
	v_mul_f32_e32 v196, 0x43000000, v196
	v_mul_f32_e32 v197, 0x43000000, v197
	v_mul_f32_e32 v198, 0x43000000, v198
	v_mul_f32_e32 v199, 0x43000000, v199
	ds_write_b128 v210, v[196:199] offset:5120
	v_mul_f32_e32 v200, 0x43000000, v200
	v_mul_f32_e32 v201, 0x43000000, v201
	v_mul_f32_e32 v202, 0x43000000, v202
	v_mul_f32_e32 v203, 0x43000000, v203
	ds_write_b128 v210, v[200:203] offset:6144
	v_mul_f32_e32 v204, 0x43000000, v204
	v_mul_f32_e32 v205, 0x43000000, v205
	v_mul_f32_e32 v206, 0x43000000, v206
	v_mul_f32_e32 v207, 0x43000000, v207
	ds_write_b128 v210, v[204:207] offset:7168
	s_waitcnt lgkmcnt(0)
	s_barrier
; #define GAS __attribute__((address_space(1)))
; #define LAS __attribute__((address_space(3)))
; #define LDS_WAIT() asm volatile("s_waitcnt lgkmcnt(0)" ::: "memory")
; __device__ __forceinline__ unsigned pk4_fp8(float a, float b, float c, float d) {
;     a = fminf(fmaxf(a, -448.f), 448.f); b = fminf(fmaxf(b, -448.f), 448.f); c = fminf(fmaxf(c, -448.f), 448.f); d = fminf(fmaxf(d, -448.f), 448.f);
;     int w = __builtin_amdgcn_cvt_pk_fp8_f32(a, b, 0, false); w = __builtin_amdgcn_cvt_pk_fp8_f32(c, d, w, true); return (unsigned)w; }
;     ...
; #pragma unroll
;     for (int i = 0; i < 32; ++i) v[i] = sc >= 0 ? W[(size_t)(k0 + 2 * i + (lane >> 5)) * Nsrc + sc] : 0.f;
; #pragma unroll
;     for (int i = 0; i < 32; ++i) { const int k = k0 + 2 * i + (lane >> 5); float x = v[i] * wscale; if (KS) x *= (k < ksplit ? ksA[k] : ksB[k - ksplit]); scr[(2 * i + (lane >> 5)) * 33 + (lane & 31)] = x; }
;     LDS_WAIT(); asm volatile("" ::: "memory");
;     const int c = lane & 7;
; #pragma unroll
;     for (int j = 0; j < 4; ++j) { const int n = (lane >> 3) + 8 * j; const LAS float* s = scr + (8 * c) * 33 + n;
;         const unsigned long long o = (unsigned long long)pg8::pk4_fp8(s[0 * 33], s[1 * 33], s[2 * 33], s[3 * 33]) | ((unsigned long long)pg8::pk4_fp8(s[4 * 33], s[5 * 33], s[6 * 33], s[7 * 33]) << 32);
;         *(GAS unsigned long long*)(WT + (size_t)(n0 + n) * K + k0 + 8 * c) = o; }
	s_add_u32 s8, s38, 0x8001000
	s_addc_u32 s9, s39, 0
	global_load_dwordx4 v[176:179], v75, s[8:9]
	s_add_u32 s8, s8, 0x8000
	s_addc_u32 s9, s9, 0
	global_load_dwordx4 v[180:183], v75, s[8:9]
	s_add_u32 s8, s8, 0x8000
	s_addc_u32 s9, s9, 0
	global_load_dwordx4 v[184:187], v75, s[8:9]
	s_add_u32 s8, s8, 0x8000
	s_addc_u32 s9, s9, 0
	global_load_dwordx4 v[188:191], v75, s[8:9]
	s_add_u32 s8, s8, 0x8000
	s_addc_u32 s9, s9, 0
	global_load_dwordx4 v[192:195], v75, s[8:9]
	s_add_u32 s8, s8, 0x8000
	s_addc_u32 s9, s9, 0
	global_load_dwordx4 v[196:199], v75, s[8:9]
	s_add_u32 s8, s8, 0x8000
	s_addc_u32 s9, s9, 0
	global_load_dwordx4 v[200:203], v75, s[8:9]
	s_add_u32 s8, s8, 0x8000
	s_addc_u32 s9, s9, 0
	global_load_dwordx4 v[204:207], v75, s[8:9]
	s_add_u32 s6, s40, 0x3001000
	s_addc_u32 s7, s41, 0
	ds_read_b32 v226, v212
	ds_read_b32 v227, v212 offset:512
	ds_read_b32 v228, v212 offset:1024
	ds_read_b32 v229, v212 offset:1536
	ds_read_b32 v230, v212 offset:2048
	ds_read_b32 v231, v212 offset:2560
	ds_read_b32 v232, v212 offset:3072
	ds_read_b32 v233, v212 offset:3584
	ds_read_b32 v234, v212 offset:4096
	ds_read_b32 v235, v212 offset:4608
	ds_read_b32 v236, v212 offset:5120
	ds_read_b32 v237, v212 offset:5632
	ds_read_b32 v238, v212 offset:6144
	ds_read_b32 v239, v212 offset:6656
	ds_read_b32 v240, v212 offset:7168
	ds_read_b32 v241, v212 offset:7680
	s_waitcnt lgkmcnt(0)
	v_max_f32_e32 v226, v226, v226
	v_max_f32_e32 v227, v227, v227
	v_max_f32_e32 v228, v228, v228
	v_max_f32_e32 v229, v229, v229
	v_max_f32_e32 v230, v230, v230
	v_max_f32_e32 v231, v231, v231
	v_max_f32_e32 v232, v232, v232
	v_max_f32_e32 v233, v233, v233
	v_max_f32_e32 v234, v234, v234
	v_max_f32_e32 v235, v235, v235
	v_max_f32_e32 v236, v236, v236
	v_max_f32_e32 v237, v237, v237
	v_max_f32_e32 v238, v238, v238
	v_max_f32_e32 v239, v239, v239
	v_max_f32_e32 v240, v240, v240
	v_max_f32_e32 v241, v241, v241
	v_med3_f32 v226, v226, s62, v95
	v_med3_f32 v227, v227, s62, v95
	v_med3_f32 v228, v228, s62, v95
	v_med3_f32 v229, v229, s62, v95
	v_med3_f32 v230, v230, s62, v95
	v_med3_f32 v231, v231, s62, v95
	v_med3_f32 v232, v232, s62, v95
	v_med3_f32 v233, v233, s62, v95
	v_med3_f32 v234, v234, s62, v95
	v_med3_f32 v235, v235, s62, v95
	v_med3_f32 v236, v236, s62, v95
	v_med3_f32 v237, v237, s62, v95
	v_med3_f32 v238, v238, s62, v95
	v_med3_f32 v239, v239, s62, v95
	v_med3_f32 v240, v240, s62, v95
	v_med3_f32 v241, v241, s62, v95
	v_mov_b32_e32 v242, 0
	v_mov_b32_e32 v243, 0
	v_mov_b32_e32 v244, 0
	v_mov_b32_e32 v245, 0
	v_cvt_pk_fp8_f32 v242, v226, v227
	v_cvt_pk_fp8_f32 v243, v230, v231
	v_cvt_pk_fp8_f32 v244, v234, v235
	v_cvt_pk_fp8_f32 v245, v238, v239
	v_cvt_pk_fp8_f32 v242, v228, v229 op_sel:[0,0,1]
	v_cvt_pk_fp8_f32 v243, v232, v233 op_sel:[0,0,1]
	v_cvt_pk_fp8_f32 v244, v236, v237 op_sel:[0,0,1]
	v_cvt_pk_fp8_f32 v245, v240, v241 op_sel:[0,0,1]
	s_nop 0
	global_store_dwordx4 v79, v[242:245], s[6:7]
	ds_read_b32 v226, v214
	ds_read_b32 v227, v214 offset:512
	ds_read_b32 v228, v214 offset:1024
	ds_read_b32 v229, v214 offset:1536
	ds_read_b32 v230, v214 offset:2048
	ds_read_b32 v231, v214 offset:2560
	ds_read_b32 v232, v214 offset:3072
	ds_read_b32 v233, v214 offset:3584
	ds_read_b32 v234, v214 offset:4096
	ds_read_b32 v235, v214 offset:4608
	ds_read_b32 v236, v214 offset:5120
	ds_read_b32 v237, v214 offset:5632
	ds_read_b32 v238, v214 offset:6144
	ds_read_b32 v239, v214 offset:6656
	ds_read_b32 v240, v214 offset:7168
	ds_read_b32 v241, v214 offset:7680
	s_waitcnt lgkmcnt(0)
	v_max_f32_e32 v226, v226, v226
	v_max_f32_e32 v227, v227, v227
	v_max_f32_e32 v228, v228, v228
	v_max_f32_e32 v229, v229, v229
	v_max_f32_e32 v230, v230, v230
	v_max_f32_e32 v231, v231, v231
	v_max_f32_e32 v232, v232, v232
	v_max_f32_e32 v233, v233, v233
	v_max_f32_e32 v234, v234, v234
	v_max_f32_e32 v235, v235, v235
	v_max_f32_e32 v236, v236, v236
	v_max_f32_e32 v237, v237, v237
	v_max_f32_e32 v238, v238, v238
	v_max_f32_e32 v239, v239, v239
	v_max_f32_e32 v240, v240, v240
	v_max_f32_e32 v241, v241, v241
	v_med3_f32 v226, v226, s62, v95
	v_med3_f32 v227, v227, s62, v95
	v_med3_f32 v228, v228, s62, v95
	v_med3_f32 v229, v229, s62, v95
	v_med3_f32 v230, v230, s62, v95
	v_med3_f32 v231, v231, s62, v95
	v_med3_f32 v232, v232, s62, v95
	v_med3_f32 v233, v233, s62, v95
	v_med3_f32 v234, v234, s62, v95
	v_med3_f32 v235, v235, s62, v95
	v_med3_f32 v236, v236, s62, v95
	v_med3_f32 v237, v237, s62, v95
	v_med3_f32 v238, v238, s62, v95
	v_med3_f32 v239, v239, s62, v95
	v_med3_f32 v240, v240, s62, v95
	v_med3_f32 v241, v241, s62, v95
	v_mov_b32_e32 v242, 0
	v_mov_b32_e32 v243, 0
	v_mov_b32_e32 v244, 0
	v_mov_b32_e32 v245, 0
	v_cvt_pk_fp8_f32 v242, v226, v227
	v_cvt_pk_fp8_f32 v243, v230, v231
	v_cvt_pk_fp8_f32 v244, v234, v235
	v_cvt_pk_fp8_f32 v245, v238, v239
	v_cvt_pk_fp8_f32 v242, v228, v229 op_sel:[0,0,1]
	v_cvt_pk_fp8_f32 v243, v232, v233 op_sel:[0,0,1]
	v_cvt_pk_fp8_f32 v244, v236, v237 op_sel:[0,0,1]
	v_cvt_pk_fp8_f32 v245, v240, v241 op_sel:[0,0,1]
	s_nop 0
	global_store_dwordx4 v80, v[242:245], s[6:7]
	s_waitcnt vmcnt(12)
	v_mul_f32_e32 v144, 0x43000000, v144
	v_mul_f32_e32 v145, 0x43000000, v145
	v_mul_f32_e32 v146, 0x43000000, v146
	v_mul_f32_e32 v147, 0x43000000, v147
	ds_write_b128 v209, v[144:147]
	v_mul_f32_e32 v148, 0x43000000, v148
	v_mul_f32_e32 v149, 0x43000000, v149
	v_mul_f32_e32 v150, 0x43000000, v150
	v_mul_f32_e32 v151, 0x43000000, v151
	ds_write_b128 v209, v[148:151] offset:1024
	v_mul_f32_e32 v152, 0x43000000, v152
	v_mul_f32_e32 v153, 0x43000000, v153
	v_mul_f32_e32 v154, 0x43000000, v154
	v_mul_f32_e32 v155, 0x43000000, v155
	ds_write_b128 v209, v[152:155] offset:2048
	v_mul_f32_e32 v156, 0x43000000, v156
	v_mul_f32_e32 v157, 0x43000000, v157
	v_mul_f32_e32 v158, 0x43000000, v158
	v_mul_f32_e32 v159, 0x43000000, v159
	ds_write_b128 v209, v[156:159] offset:3072
	v_mul_f32_e32 v160, 0x43000000, v160
	v_mul_f32_e32 v161, 0x43000000, v161
	v_mul_f32_e32 v162, 0x43000000, v162
	v_mul_f32_e32 v163, 0x43000000, v163
	ds_write_b128 v209, v[160:163] offset:4096
	v_mul_f32_e32 v164, 0x43000000, v164
	v_mul_f32_e32 v165, 0x43000000, v165
	v_mul_f32_e32 v166, 0x43000000, v166
	v_mul_f32_e32 v167, 0x43000000, v167
	ds_write_b128 v209, v[164:167] offset:5120
	v_mul_f32_e32 v168, 0x43000000, v168
	v_mul_f32_e32 v169, 0x43000000, v169
	v_mul_f32_e32 v170, 0x43000000, v170
	v_mul_f32_e32 v171, 0x43000000, v171
	ds_write_b128 v209, v[168:171] offset:6144
	v_mul_f32_e32 v172, 0x43000000, v172
	v_mul_f32_e32 v173, 0x43000000, v173
	v_mul_f32_e32 v174, 0x43000000, v174
	v_mul_f32_e32 v175, 0x43000000, v175
	ds_write_b128 v209, v[172:175] offset:7168
	s_waitcnt lgkmcnt(0)
	s_barrier
; #define GAS __attribute__((address_space(1)))
; #define LAS __attribute__((address_space(3)))
; #define LDS_WAIT() asm volatile("s_waitcnt lgkmcnt(0)" ::: "memory")
; __device__ __forceinline__ unsigned pk4_fp8(float a, float b, float c, float d) {
;     a = fminf(fmaxf(a, -448.f), 448.f); b = fminf(fmaxf(b, -448.f), 448.f); c = fminf(fmaxf(c, -448.f), 448.f); d = fminf(fmaxf(d, -448.f), 448.f);
;     int w = __builtin_amdgcn_cvt_pk_fp8_f32(a, b, 0, false); w = __builtin_amdgcn_cvt_pk_fp8_f32(c, d, w, true); return (unsigned)w; }
;     ...
; #pragma unroll
;     for (int i = 0; i < 32; ++i) v[i] = sc >= 0 ? W[(size_t)(k0 + 2 * i + (lane >> 5)) * Nsrc + sc] : 0.f;
; #pragma unroll
;     for (int i = 0; i < 32; ++i) { const int k = k0 + 2 * i + (lane >> 5); float x = v[i] * wscale; if (KS) x *= (k < ksplit ? ksA[k] : ksB[k - ksplit]); scr[(2 * i + (lane >> 5)) * 33 + (lane & 31)] = x; }
;     LDS_WAIT(); asm volatile("" ::: "memory");
;     const int c = lane & 7;
; #pragma unroll
;     for (int j = 0; j < 4; ++j) { const int n = (lane >> 3) + 8 * j; const LAS float* s = scr + (8 * c) * 33 + n;
;         const unsigned long long o = (unsigned long long)pg8::pk4_fp8(s[0 * 33], s[1 * 33], s[2 * 33], s[3 * 33]) | ((unsigned long long)pg8::pk4_fp8(s[4 * 33], s[5 * 33], s[6 * 33], s[7 * 33]) << 32);
;         *(GAS unsigned long long*)(WT + (size_t)(n0 + n) * K + k0 + 8 * c) = o; }
	s_add_u32 s8, s38, 0x8002000
	s_addc_u32 s9, s39, 0
	global_load_dwordx4 v[144:147], v75, s[8:9]
	s_add_u32 s8, s8, 0x8000
	s_addc_u32 s9, s9, 0
	global_load_dwordx4 v[148:151], v75, s[8:9]
	s_add_u32 s8, s8, 0x8000
	s_addc_u32 s9, s9, 0
	global_load_dwordx4 v[152:155], v75, s[8:9]
	s_add_u32 s8, s8, 0x8000
	s_addc_u32 s9, s9, 0
	global_load_dwordx4 v[156:159], v75, s[8:9]
	s_add_u32 s8, s8, 0x8000
	s_addc_u32 s9, s9, 0
	global_load_dwordx4 v[160:163], v75, s[8:9]
	s_add_u32 s8, s8, 0x8000
	s_addc_u32 s9, s9, 0
	global_load_dwordx4 v[164:167], v75, s[8:9]
	s_add_u32 s8, s8, 0x8000
	s_addc_u32 s9, s9, 0
	global_load_dwordx4 v[168:171], v75, s[8:9]
	s_add_u32 s8, s8, 0x8000
	s_addc_u32 s9, s9, 0
	global_load_dwordx4 v[172:175], v75, s[8:9]
	s_add_u32 s6, s40, 0x2000
	s_addc_u32 s7, s41, 0
	ds_read_b32 v226, v211
	ds_read_b32 v227, v211 offset:512
	ds_read_b32 v228, v211 offset:1024
	ds_read_b32 v229, v211 offset:1536
	ds_read_b32 v230, v211 offset:2048
	ds_read_b32 v231, v211 offset:2560
	ds_read_b32 v232, v211 offset:3072
	ds_read_b32 v233, v211 offset:3584
	ds_read_b32 v234, v211 offset:4096
	ds_read_b32 v235, v211 offset:4608
	ds_read_b32 v236, v211 offset:5120
	ds_read_b32 v237, v211 offset:5632
	ds_read_b32 v238, v211 offset:6144
	ds_read_b32 v239, v211 offset:6656
	ds_read_b32 v240, v211 offset:7168
	ds_read_b32 v241, v211 offset:7680
	s_waitcnt lgkmcnt(0)
	v_max_f32_e32 v226, v226, v226
	v_max_f32_e32 v227, v227, v227
	v_max_f32_e32 v228, v228, v228
	v_max_f32_e32 v229, v229, v229
	v_max_f32_e32 v230, v230, v230
	v_max_f32_e32 v231, v231, v231
	v_max_f32_e32 v232, v232, v232
	v_max_f32_e32 v233, v233, v233
	v_max_f32_e32 v234, v234, v234
	v_max_f32_e32 v235, v235, v235
	v_max_f32_e32 v236, v236, v236
	v_max_f32_e32 v237, v237, v237
	v_max_f32_e32 v238, v238, v238
	v_max_f32_e32 v239, v239, v239
	v_max_f32_e32 v240, v240, v240
	v_max_f32_e32 v241, v241, v241
	v_med3_f32 v226, v226, s62, v95
	v_med3_f32 v227, v227, s62, v95
	v_med3_f32 v228, v228, s62, v95
	v_med3_f32 v229, v229, s62, v95
	v_med3_f32 v230, v230, s62, v95
	v_med3_f32 v231, v231, s62, v95
	v_med3_f32 v232, v232, s62, v95
	v_med3_f32 v233, v233, s62, v95
	v_med3_f32 v234, v234, s62, v95
	v_med3_f32 v235, v235, s62, v95
	v_med3_f32 v236, v236, s62, v95
	v_med3_f32 v237, v237, s62, v95
	v_med3_f32 v238, v238, s62, v95
	v_med3_f32 v239, v239, s62, v95
	v_med3_f32 v240, v240, s62, v95
	v_med3_f32 v241, v241, s62, v95
	v_mov_b32_e32 v242, 0
	v_mov_b32_e32 v243, 0
	v_mov_b32_e32 v244, 0
	v_mov_b32_e32 v245, 0
	v_cvt_pk_fp8_f32 v242, v226, v227
	v_cvt_pk_fp8_f32 v243, v230, v231
	v_cvt_pk_fp8_f32 v244, v234, v235
	v_cvt_pk_fp8_f32 v245, v238, v239
	v_cvt_pk_fp8_f32 v242, v228, v229 op_sel:[0,0,1]
	v_cvt_pk_fp8_f32 v243, v232, v233 op_sel:[0,0,1]
	v_cvt_pk_fp8_f32 v244, v236, v237 op_sel:[0,0,1]
	v_cvt_pk_fp8_f32 v245, v240, v241 op_sel:[0,0,1]
	s_nop 0
	global_store_dwordx4 v79, v[242:245], s[6:7]
	ds_read_b32 v226, v213
	ds_read_b32 v227, v213 offset:512
	ds_read_b32 v228, v213 offset:1024
	ds_read_b32 v229, v213 offset:1536
	ds_read_b32 v230, v213 offset:2048
	ds_read_b32 v231, v213 offset:2560
	ds_read_b32 v232, v213 offset:3072
	ds_read_b32 v233, v213 offset:3584
	ds_read_b32 v234, v213 offset:4096
	ds_read_b32 v235, v213 offset:4608
	ds_read_b32 v236, v213 offset:5120
	ds_read_b32 v237, v213 offset:5632
	ds_read_b32 v238, v213 offset:6144
	ds_read_b32 v239, v213 offset:6656
	ds_read_b32 v240, v213 offset:7168
	ds_read_b32 v241, v213 offset:7680
	s_waitcnt lgkmcnt(0)
	v_max_f32_e32 v226, v226, v226
	v_max_f32_e32 v227, v227, v227
	v_max_f32_e32 v228, v228, v228
	v_max_f32_e32 v229, v229, v229
	v_max_f32_e32 v230, v230, v230
	v_max_f32_e32 v231, v231, v231
	v_max_f32_e32 v232, v232, v232
	v_max_f32_e32 v233, v233, v233
	v_max_f32_e32 v234, v234, v234
	v_max_f32_e32 v235, v235, v235
	v_max_f32_e32 v236, v236, v236
	v_max_f32_e32 v237, v237, v237
	v_max_f32_e32 v238, v238, v238
	v_max_f32_e32 v239, v239, v239
	v_max_f32_e32 v240, v240, v240
	v_max_f32_e32 v241, v241, v241
	v_med3_f32 v226, v226, s62, v95
	v_med3_f32 v227, v227, s62, v95
	v_med3_f32 v228, v228, s62, v95
	v_med3_f32 v229, v229, s62, v95
	v_med3_f32 v230, v230, s62, v95
	v_med3_f32 v231, v231, s62, v95
	v_med3_f32 v232, v232, s62, v95
	v_med3_f32 v233, v233, s62, v95
	v_med3_f32 v234, v234, s62, v95
	v_med3_f32 v235, v235, s62, v95
	v_med3_f32 v236, v236, s62, v95
	v_med3_f32 v237, v237, s62, v95
	v_med3_f32 v238, v238, s62, v95
	v_med3_f32 v239, v239, s62, v95
	v_med3_f32 v240, v240, s62, v95
	v_med3_f32 v241, v241, s62, v95
	v_mov_b32_e32 v242, 0
	v_mov_b32_e32 v243, 0
	v_mov_b32_e32 v244, 0
	v_mov_b32_e32 v245, 0
	v_cvt_pk_fp8_f32 v242, v226, v227
	v_cvt_pk_fp8_f32 v243, v230, v231
	v_cvt_pk_fp8_f32 v244, v234, v235
	v_cvt_pk_fp8_f32 v245, v238, v239
	v_cvt_pk_fp8_f32 v242, v228, v229 op_sel:[0,0,1]
	v_cvt_pk_fp8_f32 v243, v232, v233 op_sel:[0,0,1]
	v_cvt_pk_fp8_f32 v244, v236, v237 op_sel:[0,0,1]
	v_cvt_pk_fp8_f32 v245, v240, v241 op_sel:[0,0,1]
	s_nop 0
	global_store_dwordx4 v80, v[242:245], s[6:7]
	s_waitcnt vmcnt(12)
	v_mul_f32_e32 v176, 0x43000000, v176
	v_mul_f32_e32 v177, 0x43000000, v177
	v_mul_f32_e32 v178, 0x43000000, v178
	v_mul_f32_e32 v179, 0x43000000, v179
	ds_write_b128 v210, v[176:179]
	v_mul_f32_e32 v180, 0x43000000, v180
	v_mul_f32_e32 v181, 0x43000000, v181
	v_mul_f32_e32 v182, 0x43000000, v182
	v_mul_f32_e32 v183, 0x43000000, v183
	ds_write_b128 v210, v[180:183] offset:1024
	v_mul_f32_e32 v184, 0x43000000, v184
	v_mul_f32_e32 v185, 0x43000000, v185
	v_mul_f32_e32 v186, 0x43000000, v186
	v_mul_f32_e32 v187, 0x43000000, v187
	ds_write_b128 v210, v[184:187] offset:2048
	v_mul_f32_e32 v188, 0x43000000, v188
	v_mul_f32_e32 v189, 0x43000000, v189
	v_mul_f32_e32 v190, 0x43000000, v190
	v_mul_f32_e32 v191, 0x43000000, v191
	ds_write_b128 v210, v[188:191] offset:3072
	v_mul_f32_e32 v192, 0x43000000, v192
	v_mul_f32_e32 v193, 0x43000000, v193
	v_mul_f32_e32 v194, 0x43000000, v194
	v_mul_f32_e32 v195, 0x43000000, v195
	ds_write_b128 v210, v[192:195] offset:4096
	v_mul_f32_e32 v196, 0x43000000, v196
	v_mul_f32_e32 v197, 0x43000000, v197
	v_mul_f32_e32 v198, 0x43000000, v198
	v_mul_f32_e32 v199, 0x43000000, v199
	ds_write_b128 v210, v[196:199] offset:5120
	v_mul_f32_e32 v200, 0x43000000, v200
	v_mul_f32_e32 v201, 0x43000000, v201
	v_mul_f32_e32 v202, 0x43000000, v202
	v_mul_f32_e32 v203, 0x43000000, v203
	ds_write_b128 v210, v[200:203] offset:6144
	v_mul_f32_e32 v204, 0x43000000, v204
	v_mul_f32_e32 v205, 0x43000000, v205
	v_mul_f32_e32 v206, 0x43000000, v206
	v_mul_f32_e32 v207, 0x43000000, v207
	ds_write_b128 v210, v[204:207] offset:7168
	s_waitcnt lgkmcnt(0)
	s_barrier
; #define GAS __attribute__((address_space(1)))
; #define LAS __attribute__((address_space(3)))
; #define LDS_WAIT() asm volatile("s_waitcnt lgkmcnt(0)" ::: "memory")
; __device__ __forceinline__ unsigned pk4_fp8(float a, float b, float c, float d) {
;     a = fminf(fmaxf(a, -448.f), 448.f); b = fminf(fmaxf(b, -448.f), 448.f); c = fminf(fmaxf(c, -448.f), 448.f); d = fminf(fmaxf(d, -448.f), 448.f);
;     int w = __builtin_amdgcn_cvt_pk_fp8_f32(a, b, 0, false); w = __builtin_amdgcn_cvt_pk_fp8_f32(c, d, w, true); return (unsigned)w; }
;     ...
; #pragma unroll
;     for (int i = 0; i < 32; ++i) v[i] = sc >= 0 ? W[(size_t)(k0 + 2 * i + (lane >> 5)) * Nsrc + sc] : 0.f;
; #pragma unroll
;     for (int i = 0; i < 32; ++i) { const int k = k0 + 2 * i + (lane >> 5); float x = v[i] * wscale; if (KS) x *= (k < ksplit ? ksA[k] : ksB[k - ksplit]); scr[(2 * i + (lane >> 5)) * 33 + (lane & 31)] = x; }
;     LDS_WAIT(); asm volatile("" ::: "memory");
;     const int c = lane & 7;
; #pragma unroll
;     for (int j = 0; j < 4; ++j) { const int n = (lane >> 3) + 8 * j; const LAS float* s = scr + (8 * c) * 33 + n;
;         const unsigned long long o = (unsigned long long)pg8::pk4_fp8(s[0 * 33], s[1 * 33], s[2 * 33], s[3 * 33]) | ((unsigned long long)pg8::pk4_fp8(s[4 * 33], s[5 * 33], s[6 * 33], s[7 * 33]) << 32);
;         *(GAS unsigned long long*)(WT + (size_t)(n0 + n) * K + k0 + 8 * c) = o; }
	s_add_u32 s8, s38, 0x8003000
	s_addc_u32 s9, s39, 0
	global_load_dwordx4 v[176:179], v75, s[8:9]
	s_add_u32 s8, s8, 0x8000
	s_addc_u32 s9, s9, 0
	global_load_dwordx4 v[180:183], v75, s[8:9]
	s_add_u32 s8, s8, 0x8000
	s_addc_u32 s9, s9, 0
	global_load_dwordx4 v[184:187], v75, s[8:9]
	s_add_u32 s8, s8, 0x8000
	s_addc_u32 s9, s9, 0
	global_load_dwordx4 v[188:191], v75, s[8:9]
	s_add_u32 s8, s8, 0x8000
	s_addc_u32 s9, s9, 0
	global_load_dwordx4 v[192:195], v75, s[8:9]
	s_add_u32 s8, s8, 0x8000
	s_addc_u32 s9, s9, 0
	global_load_dwordx4 v[196:199], v75, s[8:9]
	s_add_u32 s8, s8, 0x8000
	s_addc_u32 s9, s9, 0
	global_load_dwordx4 v[200:203], v75, s[8:9]
	s_add_u32 s8, s8, 0x8000
	s_addc_u32 s9, s9, 0
	global_load_dwordx4 v[204:207], v75, s[8:9]
	s_add_u32 s6, s40, 0x1002000
	s_addc_u32 s7, s41, 0
	ds_read_b32 v226, v212
	ds_read_b32 v227, v212 offset:512
	ds_read_b32 v228, v212 offset:1024
	ds_read_b32 v229, v212 offset:1536
	ds_read_b32 v230, v212 offset:2048
	ds_read_b32 v231, v212 offset:2560
	ds_read_b32 v232, v212 offset:3072
	ds_read_b32 v233, v212 offset:3584
	ds_read_b32 v234, v212 offset:4096
	ds_read_b32 v235, v212 offset:4608
	ds_read_b32 v236, v212 offset:5120
	ds_read_b32 v237, v212 offset:5632
	ds_read_b32 v238, v212 offset:6144
	ds_read_b32 v239, v212 offset:6656
	ds_read_b32 v240, v212 offset:7168
	ds_read_b32 v241, v212 offset:7680
	s_waitcnt lgkmcnt(0)
	v_max_f32_e32 v226, v226, v226
	v_max_f32_e32 v227, v227, v227
	v_max_f32_e32 v228, v228, v228
	v_max_f32_e32 v229, v229, v229
	v_max_f32_e32 v230, v230, v230
	v_max_f32_e32 v231, v231, v231
	v_max_f32_e32 v232, v232, v232
	v_max_f32_e32 v233, v233, v233
	v_max_f32_e32 v234, v234, v234
	v_max_f32_e32 v235, v235, v235
	v_max_f32_e32 v236, v236, v236
	v_max_f32_e32 v237, v237, v237
	v_max_f32_e32 v238, v238, v238
	v_max_f32_e32 v239, v239, v239
	v_max_f32_e32 v240, v240, v240
	v_max_f32_e32 v241, v241, v241
	v_med3_f32 v226, v226, s62, v95
	v_med3_f32 v227, v227, s62, v95
	v_med3_f32 v228, v228, s62, v95
	v_med3_f32 v229, v229, s62, v95
	v_med3_f32 v230, v230, s62, v95
	v_med3_f32 v231, v231, s62, v95
	v_med3_f32 v232, v232, s62, v95
	v_med3_f32 v233, v233, s62, v95
	v_med3_f32 v234, v234, s62, v95
	v_med3_f32 v235, v235, s62, v95
	v_med3_f32 v236, v236, s62, v95
	v_med3_f32 v237, v237, s62, v95
	v_med3_f32 v238, v238, s62, v95
	v_med3_f32 v239, v239, s62, v95
	v_med3_f32 v240, v240, s62, v95
	v_med3_f32 v241, v241, s62, v95
	v_mov_b32_e32 v242, 0
	v_mov_b32_e32 v243, 0
	v_mov_b32_e32 v244, 0
	v_mov_b32_e32 v245, 0
	v_cvt_pk_fp8_f32 v242, v226, v227
	v_cvt_pk_fp8_f32 v243, v230, v231
	v_cvt_pk_fp8_f32 v244, v234, v235
	v_cvt_pk_fp8_f32 v245, v238, v239
	v_cvt_pk_fp8_f32 v242, v228, v229 op_sel:[0,0,1]
	v_cvt_pk_fp8_f32 v243, v232, v233 op_sel:[0,0,1]
	v_cvt_pk_fp8_f32 v244, v236, v237 op_sel:[0,0,1]
	v_cvt_pk_fp8_f32 v245, v240, v241 op_sel:[0,0,1]
	s_nop 0
	global_store_dwordx4 v79, v[242:245], s[6:7]
	ds_read_b32 v226, v214
	ds_read_b32 v227, v214 offset:512
	ds_read_b32 v228, v214 offset:1024
	ds_read_b32 v229, v214 offset:1536
	ds_read_b32 v230, v214 offset:2048
	ds_read_b32 v231, v214 offset:2560
	ds_read_b32 v232, v214 offset:3072
	ds_read_b32 v233, v214 offset:3584
	ds_read_b32 v234, v214 offset:4096
	ds_read_b32 v235, v214 offset:4608
	ds_read_b32 v236, v214 offset:5120
	ds_read_b32 v237, v214 offset:5632
	ds_read_b32 v238, v214 offset:6144
	ds_read_b32 v239, v214 offset:6656
	ds_read_b32 v240, v214 offset:7168
	ds_read_b32 v241, v214 offset:7680
	s_waitcnt lgkmcnt(0)
	v_max_f32_e32 v226, v226, v226
	v_max_f32_e32 v227, v227, v227
	v_max_f32_e32 v228, v228, v228
	v_max_f32_e32 v229, v229, v229
	v_max_f32_e32 v230, v230, v230
	v_max_f32_e32 v231, v231, v231
	v_max_f32_e32 v232, v232, v232
	v_max_f32_e32 v233, v233, v233
	v_max_f32_e32 v234, v234, v234
	v_max_f32_e32 v235, v235, v235
	v_max_f32_e32 v236, v236, v236
	v_max_f32_e32 v237, v237, v237
	v_max_f32_e32 v238, v238, v238
	v_max_f32_e32 v239, v239, v239
	v_max_f32_e32 v240, v240, v240
	v_max_f32_e32 v241, v241, v241
	v_med3_f32 v226, v226, s62, v95
	v_med3_f32 v227, v227, s62, v95
	v_med3_f32 v228, v228, s62, v95
	v_med3_f32 v229, v229, s62, v95
	v_med3_f32 v230, v230, s62, v95
	v_med3_f32 v231, v231, s62, v95
	v_med3_f32 v232, v232, s62, v95
	v_med3_f32 v233, v233, s62, v95
	v_med3_f32 v234, v234, s62, v95
	v_med3_f32 v235, v235, s62, v95
	v_med3_f32 v236, v236, s62, v95
	v_med3_f32 v237, v237, s62, v95
	v_med3_f32 v238, v238, s62, v95
	v_med3_f32 v239, v239, s62, v95
	v_med3_f32 v240, v240, s62, v95
	v_med3_f32 v241, v241, s62, v95
	v_mov_b32_e32 v242, 0
	v_mov_b32_e32 v243, 0
	v_mov_b32_e32 v244, 0
	v_mov_b32_e32 v245, 0
	v_cvt_pk_fp8_f32 v242, v226, v227
	v_cvt_pk_fp8_f32 v243, v230, v231
	v_cvt_pk_fp8_f32 v244, v234, v235
	v_cvt_pk_fp8_f32 v245, v238, v239
	v_cvt_pk_fp8_f32 v242, v228, v229 op_sel:[0,0,1]
	v_cvt_pk_fp8_f32 v243, v232, v233 op_sel:[0,0,1]
	v_cvt_pk_fp8_f32 v244, v236, v237 op_sel:[0,0,1]
	v_cvt_pk_fp8_f32 v245, v240, v241 op_sel:[0,0,1]
	s_nop 0
	global_store_dwordx4 v80, v[242:245], s[6:7]
	s_waitcnt vmcnt(12)
	v_mul_f32_e32 v144, 0x43000000, v144
	v_mul_f32_e32 v145, 0x43000000, v145
	v_mul_f32_e32 v146, 0x43000000, v146
	v_mul_f32_e32 v147, 0x43000000, v147
	ds_write_b128 v209, v[144:147]
	v_mul_f32_e32 v148, 0x43000000, v148
	v_mul_f32_e32 v149, 0x43000000, v149
	v_mul_f32_e32 v150, 0x43000000, v150
	v_mul_f32_e32 v151, 0x43000000, v151
	ds_write_b128 v209, v[148:151] offset:1024
	v_mul_f32_e32 v152, 0x43000000, v152
	v_mul_f32_e32 v153, 0x43000000, v153
	v_mul_f32_e32 v154, 0x43000000, v154
	v_mul_f32_e32 v155, 0x43000000, v155
	ds_write_b128 v209, v[152:155] offset:2048
	v_mul_f32_e32 v156, 0x43000000, v156
	v_mul_f32_e32 v157, 0x43000000, v157
	v_mul_f32_e32 v158, 0x43000000, v158
	v_mul_f32_e32 v159, 0x43000000, v159
	ds_write_b128 v209, v[156:159] offset:3072
	v_mul_f32_e32 v160, 0x43000000, v160
	v_mul_f32_e32 v161, 0x43000000, v161
	v_mul_f32_e32 v162, 0x43000000, v162
	v_mul_f32_e32 v163, 0x43000000, v163
	ds_write_b128 v209, v[160:163] offset:4096
	v_mul_f32_e32 v164, 0x43000000, v164
	v_mul_f32_e32 v165, 0x43000000, v165
	v_mul_f32_e32 v166, 0x43000000, v166
	v_mul_f32_e32 v167, 0x43000000, v167
	ds_write_b128 v209, v[164:167] offset:5120
	v_mul_f32_e32 v168, 0x43000000, v168
	v_mul_f32_e32 v169, 0x43000000, v169
	v_mul_f32_e32 v170, 0x43000000, v170
	v_mul_f32_e32 v171, 0x43000000, v171
	ds_write_b128 v209, v[168:171] offset:6144
	v_mul_f32_e32 v172, 0x43000000, v172
	v_mul_f32_e32 v173, 0x43000000, v173
	v_mul_f32_e32 v174, 0x43000000, v174
	v_mul_f32_e32 v175, 0x43000000, v175
	ds_write_b128 v209, v[172:175] offset:7168
	s_waitcnt lgkmcnt(0)
	s_barrier
; #define GAS __attribute__((address_space(1)))
; #define LAS __attribute__((address_space(3)))
; #define LDS_WAIT() asm volatile("s_waitcnt lgkmcnt(0)" ::: "memory")
; __device__ __forceinline__ unsigned pk4_fp8(float a, float b, float c, float d) {
;     a = fminf(fmaxf(a, -448.f), 448.f); b = fminf(fmaxf(b, -448.f), 448.f); c = fminf(fmaxf(c, -448.f), 448.f); d = fminf(fmaxf(d, -448.f), 448.f);
;     int w = __builtin_amdgcn_cvt_pk_fp8_f32(a, b, 0, false); w = __builtin_amdgcn_cvt_pk_fp8_f32(c, d, w, true); return (unsigned)w; }
;     ...
; #pragma unroll
;     for (int i = 0; i < 32; ++i) v[i] = sc >= 0 ? W[(size_t)(k0 + 2 * i + (lane >> 5)) * Nsrc + sc] : 0.f;
; #pragma unroll
;     for (int i = 0; i < 32; ++i) { const int k = k0 + 2 * i + (lane >> 5); float x = v[i] * wscale; if (KS) x *= (k < ksplit ? ksA[k] : ksB[k - ksplit]); scr[(2 * i + (lane >> 5)) * 33 + (lane & 31)] = x; }
;     LDS_WAIT(); asm volatile("" ::: "memory");
;     const int c = lane & 7;
; #pragma unroll
;     for (int j = 0; j < 4; ++j) { const int n = (lane >> 3) + 8 * j; const LAS float* s = scr + (8 * c) * 33 + n;
;         const unsigned long long o = (unsigned long long)pg8::pk4_fp8(s[0 * 33], s[1 * 33], s[2 * 33], s[3 * 33]) | ((unsigned long long)pg8::pk4_fp8(s[4 * 33], s[5 * 33], s[6 * 33], s[7 * 33]) << 32);
;         *(GAS unsigned long long*)(WT + (size_t)(n0 + n) * K + k0 + 8 * c) = o; }
	s_add_u32 s8, s38, 0xc000000
	s_addc_u32 s9, s39, 0
	global_load_dwordx4 v[144:147], v75, s[8:9]
	s_add_u32 s8, s8, 0x8000
	s_addc_u32 s9, s9, 0
	global_load_dwordx4 v[148:151], v75, s[8:9]
	s_add_u32 s8, s8, 0x8000
	s_addc_u32 s9, s9, 0
	global_load_dwordx4 v[152:155], v75, s[8:9]
	s_add_u32 s8, s8, 0x8000
	s_addc_u32 s9, s9, 0
	global_load_dwordx4 v[156:159], v75, s[8:9]
	s_add_u32 s8, s8, 0x8000
	s_addc_u32 s9, s9, 0
	global_load_dwordx4 v[160:163], v75, s[8:9]
	s_add_u32 s8, s8, 0x8000
	s_addc_u32 s9, s9, 0
	global_load_dwordx4 v[164:167], v75, s[8:9]
	s_add_u32 s8, s8, 0x8000
	s_addc_u32 s9, s9, 0
	global_load_dwordx4 v[168:171], v75, s[8:9]
	s_add_u32 s8, s8, 0x8000
	s_addc_u32 s9, s9, 0
	global_load_dwordx4 v[172:175], v75, s[8:9]
	s_add_u32 s6, s40, 0x2002000
	s_addc_u32 s7, s41, 0
	ds_read_b32 v226, v211
	ds_read_b32 v227, v211 offset:512
	ds_read_b32 v228, v211 offset:1024
	ds_read_b32 v229, v211 offset:1536
	ds_read_b32 v230, v211 offset:2048
	ds_read_b32 v231, v211 offset:2560
	ds_read_b32 v232, v211 offset:3072
	ds_read_b32 v233, v211 offset:3584
	ds_read_b32 v234, v211 offset:4096
	ds_read_b32 v235, v211 offset:4608
	ds_read_b32 v236, v211 offset:5120
	ds_read_b32 v237, v211 offset:5632
	ds_read_b32 v238, v211 offset:6144
	ds_read_b32 v239, v211 offset:6656
	ds_read_b32 v240, v211 offset:7168
	ds_read_b32 v241, v211 offset:7680
	s_waitcnt lgkmcnt(0)
	v_max_f32_e32 v226, v226, v226
	v_max_f32_e32 v227, v227, v227
	v_max_f32_e32 v228, v228, v228
	v_max_f32_e32 v229, v229, v229
	v_max_f32_e32 v230, v230, v230
	v_max_f32_e32 v231, v231, v231
	v_max_f32_e32 v232, v232, v232
	v_max_f32_e32 v233, v233, v233
	v_max_f32_e32 v234, v234, v234
	v_max_f32_e32 v235, v235, v235
	v_max_f32_e32 v236, v236, v236
	v_max_f32_e32 v237, v237, v237
	v_max_f32_e32 v238, v238, v238
	v_max_f32_e32 v239, v239, v239
	v_max_f32_e32 v240, v240, v240
	v_max_f32_e32 v241, v241, v241
	v_med3_f32 v226, v226, s62, v95
	v_med3_f32 v227, v227, s62, v95
	v_med3_f32 v228, v228, s62, v95
	v_med3_f32 v229, v229, s62, v95
	v_med3_f32 v230, v230, s62, v95
	v_med3_f32 v231, v231, s62, v95
	v_med3_f32 v232, v232, s62, v95
	v_med3_f32 v233, v233, s62, v95
	v_med3_f32 v234, v234, s62, v95
	v_med3_f32 v235, v235, s62, v95
	v_med3_f32 v236, v236, s62, v95
	v_med3_f32 v237, v237, s62, v95
	v_med3_f32 v238, v238, s62, v95
	v_med3_f32 v239, v239, s62, v95
	v_med3_f32 v240, v240, s62, v95
	v_med3_f32 v241, v241, s62, v95
	v_mov_b32_e32 v242, 0
	v_mov_b32_e32 v243, 0
	v_mov_b32_e32 v244, 0
	v_mov_b32_e32 v245, 0
	v_cvt_pk_fp8_f32 v242, v226, v227
	v_cvt_pk_fp8_f32 v243, v230, v231
	v_cvt_pk_fp8_f32 v244, v234, v235
	v_cvt_pk_fp8_f32 v245, v238, v239
	v_cvt_pk_fp8_f32 v242, v228, v229 op_sel:[0,0,1]
	v_cvt_pk_fp8_f32 v243, v232, v233 op_sel:[0,0,1]
	v_cvt_pk_fp8_f32 v244, v236, v237 op_sel:[0,0,1]
	v_cvt_pk_fp8_f32 v245, v240, v241 op_sel:[0,0,1]
	s_nop 0
	global_store_dwordx4 v79, v[242:245], s[6:7]
	ds_read_b32 v226, v213
	ds_read_b32 v227, v213 offset:512
	ds_read_b32 v228, v213 offset:1024
	ds_read_b32 v229, v213 offset:1536
	ds_read_b32 v230, v213 offset:2048
	ds_read_b32 v231, v213 offset:2560
	ds_read_b32 v232, v213 offset:3072
	ds_read_b32 v233, v213 offset:3584
	ds_read_b32 v234, v213 offset:4096
	ds_read_b32 v235, v213 offset:4608
	ds_read_b32 v236, v213 offset:5120
	ds_read_b32 v237, v213 offset:5632
	ds_read_b32 v238, v213 offset:6144
	ds_read_b32 v239, v213 offset:6656
	ds_read_b32 v240, v213 offset:7168
	ds_read_b32 v241, v213 offset:7680
	s_waitcnt lgkmcnt(0)
	v_max_f32_e32 v226, v226, v226
	v_max_f32_e32 v227, v227, v227
	v_max_f32_e32 v228, v228, v228
	v_max_f32_e32 v229, v229, v229
	v_max_f32_e32 v230, v230, v230
	v_max_f32_e32 v231, v231, v231
	v_max_f32_e32 v232, v232, v232
	v_max_f32_e32 v233, v233, v233
	v_max_f32_e32 v234, v234, v234
	v_max_f32_e32 v235, v235, v235
	v_max_f32_e32 v236, v236, v236
	v_max_f32_e32 v237, v237, v237
	v_max_f32_e32 v238, v238, v238
	v_max_f32_e32 v239, v239, v239
	v_max_f32_e32 v240, v240, v240
	v_max_f32_e32 v241, v241, v241
	v_med3_f32 v226, v226, s62, v95
	v_med3_f32 v227, v227, s62, v95
	v_med3_f32 v228, v228, s62, v95
	v_med3_f32 v229, v229, s62, v95
	v_med3_f32 v230, v230, s62, v95
	v_med3_f32 v231, v231, s62, v95
	v_med3_f32 v232, v232, s62, v95
	v_med3_f32 v233, v233, s62, v95
	v_med3_f32 v234, v234, s62, v95
	v_med3_f32 v235, v235, s62, v95
	v_med3_f32 v236, v236, s62, v95
	v_med3_f32 v237, v237, s62, v95
	v_med3_f32 v238, v238, s62, v95
	v_med3_f32 v239, v239, s62, v95
	v_med3_f32 v240, v240, s62, v95
	v_med3_f32 v241, v241, s62, v95
	v_mov_b32_e32 v242, 0
	v_mov_b32_e32 v243, 0
	v_mov_b32_e32 v244, 0
	v_mov_b32_e32 v245, 0
	v_cvt_pk_fp8_f32 v242, v226, v227
	v_cvt_pk_fp8_f32 v243, v230, v231
	v_cvt_pk_fp8_f32 v244, v234, v235
	v_cvt_pk_fp8_f32 v245, v238, v239
	v_cvt_pk_fp8_f32 v242, v228, v229 op_sel:[0,0,1]
	v_cvt_pk_fp8_f32 v243, v232, v233 op_sel:[0,0,1]
	v_cvt_pk_fp8_f32 v244, v236, v237 op_sel:[0,0,1]
	v_cvt_pk_fp8_f32 v245, v240, v241 op_sel:[0,0,1]
	s_nop 0
	global_store_dwordx4 v80, v[242:245], s[6:7]
	s_branch .Lco3_hop_skip

; #define GAS __attribute__((address_space(1)))
; #define LAS __attribute__((address_space(3)))
; #define LDS_WAIT() asm volatile("s_waitcnt lgkmcnt(0)" ::: "memory")
; __device__ __forceinline__ unsigned pk4_fp8(float a, float b, float c, float d) {
;     a = fminf(fmaxf(a, -448.f), 448.f); b = fminf(fmaxf(b, -448.f), 448.f); c = fminf(fmaxf(c, -448.f), 448.f); d = fminf(fmaxf(d, -448.f), 448.f);
;     int w = __builtin_amdgcn_cvt_pk_fp8_f32(a, b, 0, false); w = __builtin_amdgcn_cvt_pk_fp8_f32(c, d, w, true); return (unsigned)w; }
;     ...
; #pragma unroll
;     for (int i = 0; i < 32; ++i) v[i] = sc >= 0 ? W[(size_t)(k0 + 2 * i + (lane >> 5)) * Nsrc + sc] : 0.f;
; #pragma unroll
;     for (int i = 0; i < 32; ++i) { const int k = k0 + 2 * i + (lane >> 5); float x = v[i] * wscale; if (KS) x *= (k < ksplit ? ksA[k] : ksB[k - ksplit]); scr[(2 * i + (lane >> 5)) * 33 + (lane & 31)] = x; }
;     LDS_WAIT(); asm volatile("" ::: "memory");
;     const int c = lane & 7;
; #pragma unroll
;     for (int j = 0; j < 4; ++j) { const int n = (lane >> 3) + 8 * j; const LAS float* s = scr + (8 * c) * 33 + n;
;         const unsigned long long o = (unsigned long long)pg8::pk4_fp8(s[0 * 33], s[1 * 33], s[2 * 33], s[3 * 33]) | ((unsigned long long)pg8::pk4_fp8(s[4 * 33], s[5 * 33], s[6 * 33], s[7 * 33]) << 32);
;         *(GAS unsigned long long*)(WT + (size_t)(n0 + n) * K + k0 + 8 * c) = o; }
.Lco3_hop_skip:
	s_waitcnt vmcnt(12)
	v_mul_f32_e32 v176, 0x43000000, v176
	v_mul_f32_e32 v177, 0x43000000, v177
	v_mul_f32_e32 v178, 0x43000000, v178
	v_mul_f32_e32 v179, 0x43000000, v179
	ds_write_b128 v210, v[176:179]
	v_mul_f32_e32 v180, 0x43000000, v180
	v_mul_f32_e32 v181, 0x43000000, v181
	v_mul_f32_e32 v182, 0x43000000, v182
	v_mul_f32_e32 v183, 0x43000000, v183
	ds_write_b128 v210, v[180:183] offset:1024
	v_mul_f32_e32 v184, 0x43000000, v184
	v_mul_f32_e32 v185, 0x43000000, v185
	v_mul_f32_e32 v186, 0x43000000, v186
	v_mul_f32_e32 v187, 0x43000000, v187
	ds_write_b128 v210, v[184:187] offset:2048
	v_mul_f32_e32 v188, 0x43000000, v188
	v_mul_f32_e32 v189, 0x43000000, v189
	v_mul_f32_e32 v190, 0x43000000, v190
	v_mul_f32_e32 v191, 0x43000000, v191
	ds_write_b128 v210, v[188:191] offset:3072
	v_mul_f32_e32 v192, 0x43000000, v192
	v_mul_f32_e32 v193, 0x43000000, v193
	v_mul_f32_e32 v194, 0x43000000, v194
	v_mul_f32_e32 v195, 0x43000000, v195
	ds_write_b128 v210, v[192:195] offset:4096
	v_mul_f32_e32 v196, 0x43000000, v196
	v_mul_f32_e32 v197, 0x43000000, v197
	v_mul_f32_e32 v198, 0x43000000, v198
	v_mul_f32_e32 v199, 0x43000000, v199
	ds_write_b128 v210, v[196:199] offset:5120
	v_mul_f32_e32 v200, 0x43000000, v200
	v_mul_f32_e32 v201, 0x43000000, v201
	v_mul_f32_e32 v202, 0x43000000, v202
	v_mul_f32_e32 v203, 0x43000000, v203
	ds_write_b128 v210, v[200:203] offset:6144
	v_mul_f32_e32 v204, 0x43000000, v204
	v_mul_f32_e32 v205, 0x43000000, v205
	v_mul_f32_e32 v206, 0x43000000, v206
	v_mul_f32_e32 v207, 0x43000000, v207
	ds_write_b128 v210, v[204:207] offset:7168
	s_waitcnt lgkmcnt(0)
	s_barrier
	s_add_u32 s8, s38, 0xc001000
	s_addc_u32 s9, s39, 0
	global_load_dwordx4 v[176:179], v75, s[8:9]
	s_add_u32 s8, s8, 0x8000
	s_addc_u32 s9, s9, 0
	global_load_dwordx4 v[180:183], v75, s[8:9]
	s_add_u32 s8, s8, 0x8000
	s_addc_u32 s9, s9, 0
	global_load_dwordx4 v[184:187], v75, s[8:9]
	s_add_u32 s8, s8, 0x8000
	s_addc_u32 s9, s9, 0
	global_load_dwordx4 v[188:191], v75, s[8:9]
	s_add_u32 s8, s8, 0x8000
	s_addc_u32 s9, s9, 0
	global_load_dwordx4 v[192:195], v75, s[8:9]
	s_add_u32 s8, s8, 0x8000
	s_addc_u32 s9, s9, 0
	global_load_dwordx4 v[196:199], v75, s[8:9]
	s_add_u32 s8, s8, 0x8000
	s_addc_u32 s9, s9, 0
	global_load_dwordx4 v[200:203], v75, s[8:9]
	s_add_u32 s8, s8, 0x8000
	s_addc_u32 s9, s9, 0
	global_load_dwordx4 v[204:207], v75, s[8:9]
	s_add_u32 s6, s40, 0x3002000
	s_addc_u32 s7, s41, 0
	ds_read_b32 v226, v212
	ds_read_b32 v227, v212 offset:512
	ds_read_b32 v228, v212 offset:1024
	ds_read_b32 v229, v212 offset:1536
	ds_read_b32 v230, v212 offset:2048
	ds_read_b32 v231, v212 offset:2560
	ds_read_b32 v232, v212 offset:3072
	ds_read_b32 v233, v212 offset:3584
	ds_read_b32 v234, v212 offset:4096
	ds_read_b32 v235, v212 offset:4608
	ds_read_b32 v236, v212 offset:5120
	ds_read_b32 v237, v212 offset:5632
	ds_read_b32 v238, v212 offset:6144
	ds_read_b32 v239, v212 offset:6656
	ds_read_b32 v240, v212 offset:7168
	ds_read_b32 v241, v212 offset:7680
	s_waitcnt lgkmcnt(0)
	v_max_f32_e32 v226, v226, v226
	v_max_f32_e32 v227, v227, v227
	v_max_f32_e32 v228, v228, v228
	v_max_f32_e32 v229, v229, v229
	v_max_f32_e32 v230, v230, v230
	v_max_f32_e32 v231, v231, v231
	v_max_f32_e32 v232, v232, v232
	v_max_f32_e32 v233, v233, v233
	v_max_f32_e32 v234, v234, v234
	v_max_f32_e32 v235, v235, v235
	v_max_f32_e32 v236, v236, v236
	v_max_f32_e32 v237, v237, v237
	v_max_f32_e32 v238, v238, v238
	v_max_f32_e32 v239, v239, v239
	v_max_f32_e32 v240, v240, v240
	v_max_f32_e32 v241, v241, v241
	v_med3_f32 v226, v226, s62, v95
	v_med3_f32 v227, v227, s62, v95
	v_med3_f32 v228, v228, s62, v95
	v_med3_f32 v229, v229, s62, v95
	v_med3_f32 v230, v230, s62, v95
	v_med3_f32 v231, v231, s62, v95
	v_med3_f32 v232, v232, s62, v95
	v_med3_f32 v233, v233, s62, v95
	v_med3_f32 v234, v234, s62, v95
	v_med3_f32 v235, v235, s62, v95
	v_med3_f32 v236, v236, s62, v95
	v_med3_f32 v237, v237, s62, v95
	v_med3_f32 v238, v238, s62, v95
	v_med3_f32 v239, v239, s62, v95
	v_med3_f32 v240, v240, s62, v95
	v_med3_f32 v241, v241, s62, v95
	v_mov_b32_e32 v242, 0
	v_mov_b32_e32 v243, 0
	v_mov_b32_e32 v244, 0
	v_mov_b32_e32 v245, 0
	v_cvt_pk_fp8_f32 v242, v226, v227
	v_cvt_pk_fp8_f32 v243, v230, v231
	v_cvt_pk_fp8_f32 v244, v234, v235
	v_cvt_pk_fp8_f32 v245, v238, v239
	v_cvt_pk_fp8_f32 v242, v228, v229 op_sel:[0,0,1]
	v_cvt_pk_fp8_f32 v243, v232, v233 op_sel:[0,0,1]
	v_cvt_pk_fp8_f32 v244, v236, v237 op_sel:[0,0,1]
	v_cvt_pk_fp8_f32 v245, v240, v241 op_sel:[0,0,1]
	s_nop 0
	global_store_dwordx4 v79, v[242:245], s[6:7]
	ds_read_b32 v226, v214
	ds_read_b32 v227, v214 offset:512
	ds_read_b32 v228, v214 offset:1024
	ds_read_b32 v229, v214 offset:1536
	ds_read_b32 v230, v214 offset:2048
	ds_read_b32 v231, v214 offset:2560
	ds_read_b32 v232, v214 offset:3072
	ds_read_b32 v233, v214 offset:3584
	ds_read_b32 v234, v214 offset:4096
	ds_read_b32 v235, v214 offset:4608
	ds_read_b32 v236, v214 offset:5120
	ds_read_b32 v237, v214 offset:5632
	ds_read_b32 v238, v214 offset:6144
	ds_read_b32 v239, v214 offset:6656
	ds_read_b32 v240, v214 offset:7168
	ds_read_b32 v241, v214 offset:7680
	s_waitcnt lgkmcnt(0)
; #define GAS __attribute__((address_space(1)))
; #define LAS __attribute__((address_space(3)))
; #define LDS_WAIT() asm volatile("s_waitcnt lgkmcnt(0)" ::: "memory")
; __device__ __forceinline__ unsigned pk4_fp8(float a, float b, float c, float d) {
;     a = fminf(fmaxf(a, -448.f), 448.f); b = fminf(fmaxf(b, -448.f), 448.f); c = fminf(fmaxf(c, -448.f), 448.f); d = fminf(fmaxf(d, -448.f), 448.f);
;     int w = __builtin_amdgcn_cvt_pk_fp8_f32(a, b, 0, false); w = __builtin_amdgcn_cvt_pk_fp8_f32(c, d, w, true); return (unsigned)w; }
;     ...
; #pragma unroll
;     for (int i = 0; i < 32; ++i) v[i] = sc >= 0 ? W[(size_t)(k0 + 2 * i + (lane >> 5)) * Nsrc + sc] : 0.f;
; #pragma unroll
;     for (int i = 0; i < 32; ++i) { const int k = k0 + 2 * i + (lane >> 5); float x = v[i] * wscale; if (KS) x *= (k < ksplit ? ksA[k] : ksB[k - ksplit]); scr[(2 * i + (lane >> 5)) * 33 + (lane & 31)] = x; }
;     LDS_WAIT(); asm volatile("" ::: "memory");
;     const int c = lane & 7;
; #pragma unroll
;     for (int j = 0; j < 4; ++j) { const int n = (lane >> 3) + 8 * j; const LAS float* s = scr + (8 * c) * 33 + n;
;         const unsigned long long o = (unsigned long long)pg8::pk4_fp8(s[0 * 33], s[1 * 33], s[2 * 33], s[3 * 33]) | ((unsigned long long)pg8::pk4_fp8(s[4 * 33], s[5 * 33], s[6 * 33], s[7 * 33]) << 32);
;         *(GAS unsigned long long*)(WT + (size_t)(n0 + n) * K + k0 + 8 * c) = o; }
	v_max_f32_e32 v226, v226, v226
	v_max_f32_e32 v227, v227, v227
	v_max_f32_e32 v228, v228, v228
	v_max_f32_e32 v229, v229, v229
	v_max_f32_e32 v230, v230, v230
	v_max_f32_e32 v231, v231, v231
	v_max_f32_e32 v232, v232, v232
	v_max_f32_e32 v233, v233, v233
	v_max_f32_e32 v234, v234, v234
	v_max_f32_e32 v235, v235, v235
	v_max_f32_e32 v236, v236, v236
	v_max_f32_e32 v237, v237, v237
	v_max_f32_e32 v238, v238, v238
	v_max_f32_e32 v239, v239, v239
	v_max_f32_e32 v240, v240, v240
	v_max_f32_e32 v241, v241, v241
	v_med3_f32 v226, v226, s62, v95
	v_med3_f32 v227, v227, s62, v95
	v_med3_f32 v228, v228, s62, v95
	v_med3_f32 v229, v229, s62, v95
	v_med3_f32 v230, v230, s62, v95
	v_med3_f32 v231, v231, s62, v95
	v_med3_f32 v232, v232, s62, v95
	v_med3_f32 v233, v233, s62, v95
	v_med3_f32 v234, v234, s62, v95
	v_med3_f32 v235, v235, s62, v95
	v_med3_f32 v236, v236, s62, v95
	v_med3_f32 v237, v237, s62, v95
	v_med3_f32 v238, v238, s62, v95
	v_med3_f32 v239, v239, s62, v95
	v_med3_f32 v240, v240, s62, v95
	v_med3_f32 v241, v241, s62, v95
	v_mov_b32_e32 v242, 0
	v_mov_b32_e32 v243, 0
	v_mov_b32_e32 v244, 0
	v_mov_b32_e32 v245, 0
	v_cvt_pk_fp8_f32 v242, v226, v227
	v_cvt_pk_fp8_f32 v243, v230, v231
	v_cvt_pk_fp8_f32 v244, v234, v235
	v_cvt_pk_fp8_f32 v245, v238, v239
	v_cvt_pk_fp8_f32 v242, v228, v229 op_sel:[0,0,1]
	v_cvt_pk_fp8_f32 v243, v232, v233 op_sel:[0,0,1]
	v_cvt_pk_fp8_f32 v244, v236, v237 op_sel:[0,0,1]
	v_cvt_pk_fp8_f32 v245, v240, v241 op_sel:[0,0,1]
	s_nop 0
	global_store_dwordx4 v80, v[242:245], s[6:7]
	s_waitcnt vmcnt(12)
	v_mul_f32_e32 v144, 0x43000000, v144
	v_mul_f32_e32 v145, 0x43000000, v145
	v_mul_f32_e32 v146, 0x43000000, v146
	v_mul_f32_e32 v147, 0x43000000, v147
	ds_write_b128 v209, v[144:147]
	v_mul_f32_e32 v148, 0x43000000, v148
	v_mul_f32_e32 v149, 0x43000000, v149
	v_mul_f32_e32 v150, 0x43000000, v150
	v_mul_f32_e32 v151, 0x43000000, v151
	ds_write_b128 v209, v[148:151] offset:1024
	v_mul_f32_e32 v152, 0x43000000, v152
	v_mul_f32_e32 v153, 0x43000000, v153
	v_mul_f32_e32 v154, 0x43000000, v154
	v_mul_f32_e32 v155, 0x43000000, v155
	ds_write_b128 v209, v[152:155] offset:2048
	v_mul_f32_e32 v156, 0x43000000, v156
	v_mul_f32_e32 v157, 0x43000000, v157
	v_mul_f32_e32 v158, 0x43000000, v158
	v_mul_f32_e32 v159, 0x43000000, v159
	ds_write_b128 v209, v[156:159] offset:3072
	v_mul_f32_e32 v160, 0x43000000, v160
	v_mul_f32_e32 v161, 0x43000000, v161
	v_mul_f32_e32 v162, 0x43000000, v162
	v_mul_f32_e32 v163, 0x43000000, v163
	ds_write_b128 v209, v[160:163] offset:4096
	v_mul_f32_e32 v164, 0x43000000, v164
	v_mul_f32_e32 v165, 0x43000000, v165
	v_mul_f32_e32 v166, 0x43000000, v166
	v_mul_f32_e32 v167, 0x43000000, v167
	ds_write_b128 v209, v[164:167] offset:5120
	v_mul_f32_e32 v168, 0x43000000, v168
	v_mul_f32_e32 v169, 0x43000000, v169
	v_mul_f32_e32 v170, 0x43000000, v170
	v_mul_f32_e32 v171, 0x43000000, v171
	ds_write_b128 v209, v[168:171] offset:6144
	v_mul_f32_e32 v172, 0x43000000, v172
	v_mul_f32_e32 v173, 0x43000000, v173
	v_mul_f32_e32 v174, 0x43000000, v174
	v_mul_f32_e32 v175, 0x43000000, v175
	ds_write_b128 v209, v[172:175] offset:7168
	s_waitcnt lgkmcnt(0)
	s_barrier
	s_add_u32 s8, s38, 0xc002000
	s_addc_u32 s9, s39, 0
	global_load_dwordx4 v[144:147], v75, s[8:9]
	s_add_u32 s8, s8, 0x8000
	s_addc_u32 s9, s9, 0
	global_load_dwordx4 v[148:151], v75, s[8:9]
	s_add_u32 s8, s8, 0x8000
	s_addc_u32 s9, s9, 0
	global_load_dwordx4 v[152:155], v75, s[8:9]
	s_add_u32 s8, s8, 0x8000
	s_addc_u32 s9, s9, 0
	global_load_dwordx4 v[156:159], v75, s[8:9]
	s_add_u32 s8, s8, 0x8000
	s_addc_u32 s9, s9, 0
	global_load_dwordx4 v[160:163], v75, s[8:9]
	s_add_u32 s8, s8, 0x8000
	s_addc_u32 s9, s9, 0
	global_load_dwordx4 v[164:167], v75, s[8:9]
	s_add_u32 s8, s8, 0x8000
	s_addc_u32 s9, s9, 0
	global_load_dwordx4 v[168:171], v75, s[8:9]
	s_add_u32 s8, s8, 0x8000
	s_addc_u32 s9, s9, 0
	global_load_dwordx4 v[172:175], v75, s[8:9]
	s_add_u32 s6, s40, 0x3000
	s_addc_u32 s7, s41, 0
	ds_read_b32 v226, v211
	ds_read_b32 v227, v211 offset:512
	ds_read_b32 v228, v211 offset:1024
	ds_read_b32 v229, v211 offset:1536
	ds_read_b32 v230, v211 offset:2048
	ds_read_b32 v231, v211 offset:2560
	ds_read_b32 v232, v211 offset:3072
	ds_read_b32 v233, v211 offset:3584
	ds_read_b32 v234, v211 offset:4096
	ds_read_b32 v235, v211 offset:4608
	ds_read_b32 v236, v211 offset:5120
	ds_read_b32 v237, v211 offset:5632
	ds_read_b32 v238, v211 offset:6144
	ds_read_b32 v239, v211 offset:6656
	ds_read_b32 v240, v211 offset:7168
	ds_read_b32 v241, v211 offset:7680
	s_waitcnt lgkmcnt(0)
	v_max_f32_e32 v226, v226, v226
	v_max_f32_e32 v227, v227, v227
	v_max_f32_e32 v228, v228, v228
	v_max_f32_e32 v229, v229, v229
	v_max_f32_e32 v230, v230, v230
	v_max_f32_e32 v231, v231, v231
	v_max_f32_e32 v232, v232, v232
	v_max_f32_e32 v233, v233, v233
	v_max_f32_e32 v234, v234, v234
	v_max_f32_e32 v235, v235, v235
	v_max_f32_e32 v236, v236, v236
	v_max_f32_e32 v237, v237, v237
	v_max_f32_e32 v238, v238, v238
	v_max_f32_e32 v239, v239, v239
	v_max_f32_e32 v240, v240, v240
	v_max_f32_e32 v241, v241, v241
	v_med3_f32 v226, v226, s62, v95
	v_med3_f32 v227, v227, s62, v95
	v_med3_f32 v228, v228, s62, v95
	v_med3_f32 v229, v229, s62, v95
	v_med3_f32 v230, v230, s62, v95
	v_med3_f32 v231, v231, s62, v95
	v_med3_f32 v232, v232, s62, v95
	v_med3_f32 v233, v233, s62, v95
	v_med3_f32 v234, v234, s62, v95
	v_med3_f32 v235, v235, s62, v95
	v_med3_f32 v236, v236, s62, v95
	v_med3_f32 v237, v237, s62, v95
	v_med3_f32 v238, v238, s62, v95
	v_med3_f32 v239, v239, s62, v95
	v_med3_f32 v240, v240, s62, v95
	v_med3_f32 v241, v241, s62, v95
	v_mov_b32_e32 v242, 0
	v_mov_b32_e32 v243, 0
	v_mov_b32_e32 v244, 0
	v_mov_b32_e32 v245, 0
	v_cvt_pk_fp8_f32 v242, v226, v227
	v_cvt_pk_fp8_f32 v243, v230, v231
	v_cvt_pk_fp8_f32 v244, v234, v235
	v_cvt_pk_fp8_f32 v245, v238, v239
	v_cvt_pk_fp8_f32 v242, v228, v229 op_sel:[0,0,1]
	v_cvt_pk_fp8_f32 v243, v232, v233 op_sel:[0,0,1]
	v_cvt_pk_fp8_f32 v244, v236, v237 op_sel:[0,0,1]
	v_cvt_pk_fp8_f32 v245, v240, v241 op_sel:[0,0,1]
	s_nop 0
	global_store_dwordx4 v79, v[242:245], s[6:7]
	ds_read_b32 v226, v213
	ds_read_b32 v227, v213 offset:512
	ds_read_b32 v228, v213 offset:1024
	ds_read_b32 v229, v213 offset:1536
	ds_read_b32 v230, v213 offset:2048
	ds_read_b32 v231, v213 offset:2560
	ds_read_b32 v232, v213 offset:3072
	ds_read_b32 v233, v213 offset:3584
	ds_read_b32 v234, v213 offset:4096
	ds_read_b32 v235, v213 offset:4608
	ds_read_b32 v236, v213 offset:5120
	ds_read_b32 v237, v213 offset:5632
	ds_read_b32 v238, v213 offset:6144
	ds_read_b32 v239, v213 offset:6656
	ds_read_b32 v240, v213 offset:7168
	ds_read_b32 v241, v213 offset:7680
	s_waitcnt lgkmcnt(0)
; #define GAS __attribute__((address_space(1)))
; #define LAS __attribute__((address_space(3)))
; #define LDS_WAIT() asm volatile("s_waitcnt lgkmcnt(0)" ::: "memory")
; __device__ __forceinline__ unsigned pk4_fp8(float a, float b, float c, float d) {
;     a = fminf(fmaxf(a, -448.f), 448.f); b = fminf(fmaxf(b, -448.f), 448.f); c = fminf(fmaxf(c, -448.f), 448.f); d = fminf(fmaxf(d, -448.f), 448.f);
;     int w = __builtin_amdgcn_cvt_pk_fp8_f32(a, b, 0, false); w = __builtin_amdgcn_cvt_pk_fp8_f32(c, d, w, true); return (unsigned)w; }
;     ...
; #pragma unroll
;     for (int i = 0; i < 32; ++i) v[i] = sc >= 0 ? W[(size_t)(k0 + 2 * i + (lane >> 5)) * Nsrc + sc] : 0.f;
; #pragma unroll
;     for (int i = 0; i < 32; ++i) { const int k = k0 + 2 * i + (lane >> 5); float x = v[i] * wscale; if (KS) x *= (k < ksplit ? ksA[k] : ksB[k - ksplit]); scr[(2 * i + (lane >> 5)) * 33 + (lane & 31)] = x; }
;     LDS_WAIT(); asm volatile("" ::: "memory");
;     const int c = lane & 7;
; #pragma unroll
;     for (int j = 0; j < 4; ++j) { const int n = (lane >> 3) + 8 * j; const LAS float* s = scr + (8 * c) * 33 + n;
;         const unsigned long long o = (unsigned long long)pg8::pk4_fp8(s[0 * 33], s[1 * 33], s[2 * 33], s[3 * 33]) | ((unsigned long long)pg8::pk4_fp8(s[4 * 33], s[5 * 33], s[6 * 33], s[7 * 33]) << 32);
;         *(GAS unsigned long long*)(WT + (size_t)(n0 + n) * K + k0 + 8 * c) = o; }
	v_max_f32_e32 v226, v226, v226
	v_max_f32_e32 v227, v227, v227
	v_max_f32_e32 v228, v228, v228
	v_max_f32_e32 v229, v229, v229
	v_max_f32_e32 v230, v230, v230
	v_max_f32_e32 v231, v231, v231
	v_max_f32_e32 v232, v232, v232
	v_max_f32_e32 v233, v233, v233
	v_max_f32_e32 v234, v234, v234
	v_max_f32_e32 v235, v235, v235
	v_max_f32_e32 v236, v236, v236
	v_max_f32_e32 v237, v237, v237
	v_max_f32_e32 v238, v238, v238
	v_max_f32_e32 v239, v239, v239
	v_max_f32_e32 v240, v240, v240
	v_max_f32_e32 v241, v241, v241
	v_med3_f32 v226, v226, s62, v95
	v_med3_f32 v227, v227, s62, v95
	v_med3_f32 v228, v228, s62, v95
	v_med3_f32 v229, v229, s62, v95
	v_med3_f32 v230, v230, s62, v95
	v_med3_f32 v231, v231, s62, v95
	v_med3_f32 v232, v232, s62, v95
	v_med3_f32 v233, v233, s62, v95
	v_med3_f32 v234, v234, s62, v95
	v_med3_f32 v235, v235, s62, v95
	v_med3_f32 v236, v236, s62, v95
	v_med3_f32 v237, v237, s62, v95
	v_med3_f32 v238, v238, s62, v95
	v_med3_f32 v239, v239, s62, v95
	v_med3_f32 v240, v240, s62, v95
	v_med3_f32 v241, v241, s62, v95
	v_mov_b32_e32 v242, 0
	v_mov_b32_e32 v243, 0
	v_mov_b32_e32 v244, 0
	v_mov_b32_e32 v245, 0
	v_cvt_pk_fp8_f32 v242, v226, v227
	v_cvt_pk_fp8_f32 v243, v230, v231
	v_cvt_pk_fp8_f32 v244, v234, v235
	v_cvt_pk_fp8_f32 v245, v238, v239
	v_cvt_pk_fp8_f32 v242, v228, v229 op_sel:[0,0,1]
	v_cvt_pk_fp8_f32 v243, v232, v233 op_sel:[0,0,1]
	v_cvt_pk_fp8_f32 v244, v236, v237 op_sel:[0,0,1]
	v_cvt_pk_fp8_f32 v245, v240, v241 op_sel:[0,0,1]
	s_nop 0
	global_store_dwordx4 v80, v[242:245], s[6:7]
	s_waitcnt vmcnt(12)
	v_mul_f32_e32 v176, 0x43000000, v176
	v_mul_f32_e32 v177, 0x43000000, v177
	v_mul_f32_e32 v178, 0x43000000, v178
	v_mul_f32_e32 v179, 0x43000000, v179
	ds_write_b128 v210, v[176:179]
	v_mul_f32_e32 v180, 0x43000000, v180
	v_mul_f32_e32 v181, 0x43000000, v181
	v_mul_f32_e32 v182, 0x43000000, v182
	v_mul_f32_e32 v183, 0x43000000, v183
	ds_write_b128 v210, v[180:183] offset:1024
	v_mul_f32_e32 v184, 0x43000000, v184
	v_mul_f32_e32 v185, 0x43000000, v185
	v_mul_f32_e32 v186, 0x43000000, v186
	v_mul_f32_e32 v187, 0x43000000, v187
	ds_write_b128 v210, v[184:187] offset:2048
	v_mul_f32_e32 v188, 0x43000000, v188
	v_mul_f32_e32 v189, 0x43000000, v189
	v_mul_f32_e32 v190, 0x43000000, v190
	v_mul_f32_e32 v191, 0x43000000, v191
	ds_write_b128 v210, v[188:191] offset:3072
	v_mul_f32_e32 v192, 0x43000000, v192
	v_mul_f32_e32 v193, 0x43000000, v193
	v_mul_f32_e32 v194, 0x43000000, v194
	v_mul_f32_e32 v195, 0x43000000, v195
	ds_write_b128 v210, v[192:195] offset:4096
	v_mul_f32_e32 v196, 0x43000000, v196
	v_mul_f32_e32 v197, 0x43000000, v197
	v_mul_f32_e32 v198, 0x43000000, v198
	v_mul_f32_e32 v199, 0x43000000, v199
	ds_write_b128 v210, v[196:199] offset:5120
	v_mul_f32_e32 v200, 0x43000000, v200
	v_mul_f32_e32 v201, 0x43000000, v201
	v_mul_f32_e32 v202, 0x43000000, v202
	v_mul_f32_e32 v203, 0x43000000, v203
	ds_write_b128 v210, v[200:203] offset:6144
	v_mul_f32_e32 v204, 0x43000000, v204
	v_mul_f32_e32 v205, 0x43000000, v205
	v_mul_f32_e32 v206, 0x43000000, v206
	v_mul_f32_e32 v207, 0x43000000, v207
	ds_write_b128 v210, v[204:207] offset:7168
	s_waitcnt lgkmcnt(0)
	s_barrier
	s_add_u32 s8, s38, 0xc003000
	s_addc_u32 s9, s39, 0
	global_load_dwordx4 v[176:179], v75, s[8:9]
	s_add_u32 s8, s8, 0x8000
	s_addc_u32 s9, s9, 0
	global_load_dwordx4 v[180:183], v75, s[8:9]
	s_add_u32 s8, s8, 0x8000
	s_addc_u32 s9, s9, 0
	global_load_dwordx4 v[184:187], v75, s[8:9]
	s_add_u32 s8, s8, 0x8000
	s_addc_u32 s9, s9, 0
	global_load_dwordx4 v[188:191], v75, s[8:9]
	s_add_u32 s8, s8, 0x8000
	s_addc_u32 s9, s9, 0
	global_load_dwordx4 v[192:195], v75, s[8:9]
	s_add_u32 s8, s8, 0x8000
	s_addc_u32 s9, s9, 0
	global_load_dwordx4 v[196:199], v75, s[8:9]
	s_add_u32 s8, s8, 0x8000
	s_addc_u32 s9, s9, 0
	global_load_dwordx4 v[200:203], v75, s[8:9]
	s_add_u32 s8, s8, 0x8000
	s_addc_u32 s9, s9, 0
	global_load_dwordx4 v[204:207], v75, s[8:9]
	s_add_u32 s6, s40, 0x1003000
	s_addc_u32 s7, s41, 0
	ds_read_b32 v226, v212
	ds_read_b32 v227, v212 offset:512
	ds_read_b32 v228, v212 offset:1024
	ds_read_b32 v229, v212 offset:1536
	ds_read_b32 v230, v212 offset:2048
	ds_read_b32 v231, v212 offset:2560
	ds_read_b32 v232, v212 offset:3072
	ds_read_b32 v233, v212 offset:3584
	ds_read_b32 v234, v212 offset:4096
	ds_read_b32 v235, v212 offset:4608
	ds_read_b32 v236, v212 offset:5120
	ds_read_b32 v237, v212 offset:5632
	ds_read_b32 v238, v212 offset:6144
	ds_read_b32 v239, v212 offset:6656
	ds_read_b32 v240, v212 offset:7168
	ds_read_b32 v241, v212 offset:7680
	s_waitcnt lgkmcnt(0)
	v_max_f32_e32 v226, v226, v226
	v_max_f32_e32 v227, v227, v227
	v_max_f32_e32 v228, v228, v228
	v_max_f32_e32 v229, v229, v229
	v_max_f32_e32 v230, v230, v230
	v_max_f32_e32 v231, v231, v231
	v_max_f32_e32 v232, v232, v232
	v_max_f32_e32 v233, v233, v233
	v_max_f32_e32 v234, v234, v234
	v_max_f32_e32 v235, v235, v235
	v_max_f32_e32 v236, v236, v236
	v_max_f32_e32 v237, v237, v237
	v_max_f32_e32 v238, v238, v238
	v_max_f32_e32 v239, v239, v239
	v_max_f32_e32 v240, v240, v240
	v_max_f32_e32 v241, v241, v241
	v_med3_f32 v226, v226, s62, v95
	v_med3_f32 v227, v227, s62, v95
	v_med3_f32 v228, v228, s62, v95
	v_med3_f32 v229, v229, s62, v95
	v_med3_f32 v230, v230, s62, v95
	v_med3_f32 v231, v231, s62, v95
	v_med3_f32 v232, v232, s62, v95
	v_med3_f32 v233, v233, s62, v95
	v_med3_f32 v234, v234, s62, v95
	v_med3_f32 v235, v235, s62, v95
	v_med3_f32 v236, v236, s62, v95
	v_med3_f32 v237, v237, s62, v95
	v_med3_f32 v238, v238, s62, v95
	v_med3_f32 v239, v239, s62, v95
	v_med3_f32 v240, v240, s62, v95
	v_med3_f32 v241, v241, s62, v95
	v_mov_b32_e32 v242, 0
	v_mov_b32_e32 v243, 0
	v_mov_b32_e32 v244, 0
	v_mov_b32_e32 v245, 0
	v_cvt_pk_fp8_f32 v242, v226, v227
	v_cvt_pk_fp8_f32 v243, v230, v231
	v_cvt_pk_fp8_f32 v244, v234, v235
	v_cvt_pk_fp8_f32 v245, v238, v239
	v_cvt_pk_fp8_f32 v242, v228, v229 op_sel:[0,0,1]
	v_cvt_pk_fp8_f32 v243, v232, v233 op_sel:[0,0,1]
	v_cvt_pk_fp8_f32 v244, v236, v237 op_sel:[0,0,1]
	v_cvt_pk_fp8_f32 v245, v240, v241 op_sel:[0,0,1]
	s_nop 0
	global_store_dwordx4 v79, v[242:245], s[6:7]
	ds_read_b32 v226, v214
	ds_read_b32 v227, v214 offset:512
	ds_read_b32 v228, v214 offset:1024
	ds_read_b32 v229, v214 offset:1536
	ds_read_b32 v230, v214 offset:2048
	ds_read_b32 v231, v214 offset:2560
	ds_read_b32 v232, v214 offset:3072
	ds_read_b32 v233, v214 offset:3584
	ds_read_b32 v234, v214 offset:4096
	ds_read_b32 v235, v214 offset:4608
	ds_read_b32 v236, v214 offset:5120
	ds_read_b32 v237, v214 offset:5632
	ds_read_b32 v238, v214 offset:6144
	ds_read_b32 v239, v214 offset:6656
	ds_read_b32 v240, v214 offset:7168
	ds_read_b32 v241, v214 offset:7680
	s_waitcnt lgkmcnt(0)
; #define GAS __attribute__((address_space(1)))
; #define LAS __attribute__((address_space(3)))
; #define LDS_WAIT() asm volatile("s_waitcnt lgkmcnt(0)" ::: "memory")
;     const int pr = item >> 1, kb = 2 * (pr / nblk) + (item & 1), nb = pr % nblk, k0 = 64 * kb, n0 = 32 * nb;
;     const int nr = n0 + (lane & 31); const int sc = MAP == 1 ? src_col_in(nr) : nr;
;     float v[32];
; #pragma unroll
;     for (int i = 0; i < 32; ++i) v[i] = sc >= 0 ? W[(size_t)(k0 + 2 * i + (lane >> 5)) * Nsrc + sc] : 0.f;
; #pragma unroll
;     for (int i = 0; i < 32; ++i) { const int k = k0 + 2 * i + (lane >> 5); float x = v[i] * wscale; if (KS) x *= (k < ksplit ? ksA[k] : ksB[k - ksplit]); scr[(2 * i + (lane >> 5)) * 33 + (lane & 31)] = x; }
;     LDS_WAIT(); asm volatile("" ::: "memory");
;     const int c = lane & 7;
; #pragma unroll
;     for (int j = 0; j < 4; ++j) { const int n = (lane >> 3) + 8 * j; const LAS float* s = scr + (8 * c) * 33 + n;
;         const unsigned long long o = (unsigned long long)pg8::pk4_fp8(s[0 * 33], s[1 * 33], s[2 * 33], s[3 * 33]) | ((unsigned long long)pg8::pk4_fp8(s[4 * 33], s[5 * 33], s[6 * 33], s[7 * 33]) << 32);
;         *(GAS unsigned long long*)(WT + (size_t)(n0 + n) * K + k0 + 8 * c) = o; }
;     LDS_WAIT(); asm volatile("" ::: "memory");
; }
; __global__ void __launch_bounds__(NWAVES * 64, 2) hybrid_fwd(Args args) {
;     ...
;             p0_transpose_item_f8<false>(args.in[16] + (size_t)l * FF * DM, FF, DM, DM / 32, (unsigned char*)(ws + WS_WDN + l * SZ_WDN), 128.f, args.in[16], args.in[16], 0, scr, r, lane);
	v_max_f32_e32 v226, v226, v226
	v_max_f32_e32 v227, v227, v227
	v_max_f32_e32 v228, v228, v228
	v_max_f32_e32 v229, v229, v229
	v_max_f32_e32 v230, v230, v230
	v_max_f32_e32 v231, v231, v231
	v_max_f32_e32 v232, v232, v232
	v_max_f32_e32 v233, v233, v233
	v_max_f32_e32 v234, v234, v234
	v_max_f32_e32 v235, v235, v235
	v_max_f32_e32 v236, v236, v236
	v_max_f32_e32 v237, v237, v237
	v_max_f32_e32 v238, v238, v238
	v_max_f32_e32 v239, v239, v239
	v_max_f32_e32 v240, v240, v240
	v_max_f32_e32 v241, v241, v241
	v_med3_f32 v226, v226, s62, v95
	v_med3_f32 v227, v227, s62, v95
	v_med3_f32 v228, v228, s62, v95
	v_med3_f32 v229, v229, s62, v95
	v_med3_f32 v230, v230, s62, v95
	v_med3_f32 v231, v231, s62, v95
	v_med3_f32 v232, v232, s62, v95
	v_med3_f32 v233, v233, s62, v95
	v_med3_f32 v234, v234, s62, v95
	v_med3_f32 v235, v235, s62, v95
	v_med3_f32 v236, v236, s62, v95
	v_med3_f32 v237, v237, s62, v95
	v_med3_f32 v238, v238, s62, v95
	v_med3_f32 v239, v239, s62, v95
	v_med3_f32 v240, v240, s62, v95
	v_med3_f32 v241, v241, s62, v95
	v_mov_b32_e32 v242, 0
	v_mov_b32_e32 v243, 0
	v_mov_b32_e32 v244, 0
	v_mov_b32_e32 v245, 0
	v_cvt_pk_fp8_f32 v242, v226, v227
	v_cvt_pk_fp8_f32 v243, v230, v231
	v_cvt_pk_fp8_f32 v244, v234, v235
	v_cvt_pk_fp8_f32 v245, v238, v239
	v_cvt_pk_fp8_f32 v242, v228, v229 op_sel:[0,0,1]
	v_cvt_pk_fp8_f32 v243, v232, v233 op_sel:[0,0,1]
	v_cvt_pk_fp8_f32 v244, v236, v237 op_sel:[0,0,1]
	v_cvt_pk_fp8_f32 v245, v240, v241 op_sel:[0,0,1]
	s_nop 0
	global_store_dwordx4 v80, v[242:245], s[6:7]
	s_waitcnt vmcnt(12)
	v_mul_f32_e32 v144, 0x43000000, v144
	v_mul_f32_e32 v145, 0x43000000, v145
	v_mul_f32_e32 v146, 0x43000000, v146
	v_mul_f32_e32 v147, 0x43000000, v147
	ds_write_b128 v209, v[144:147]
	v_mul_f32_e32 v148, 0x43000000, v148
	v_mul_f32_e32 v149, 0x43000000, v149
	v_mul_f32_e32 v150, 0x43000000, v150
	v_mul_f32_e32 v151, 0x43000000, v151
	ds_write_b128 v209, v[148:151] offset:1024
	v_mul_f32_e32 v152, 0x43000000, v152
	v_mul_f32_e32 v153, 0x43000000, v153
	v_mul_f32_e32 v154, 0x43000000, v154
	v_mul_f32_e32 v155, 0x43000000, v155
	ds_write_b128 v209, v[152:155] offset:2048
	v_mul_f32_e32 v156, 0x43000000, v156
	v_mul_f32_e32 v157, 0x43000000, v157
	v_mul_f32_e32 v158, 0x43000000, v158
	v_mul_f32_e32 v159, 0x43000000, v159
	ds_write_b128 v209, v[156:159] offset:3072
	v_mul_f32_e32 v160, 0x43000000, v160
	v_mul_f32_e32 v161, 0x43000000, v161
	v_mul_f32_e32 v162, 0x43000000, v162
	v_mul_f32_e32 v163, 0x43000000, v163
	ds_write_b128 v209, v[160:163] offset:4096
	v_mul_f32_e32 v164, 0x43000000, v164
	v_mul_f32_e32 v165, 0x43000000, v165
	v_mul_f32_e32 v166, 0x43000000, v166
	v_mul_f32_e32 v167, 0x43000000, v167
	ds_write_b128 v209, v[164:167] offset:5120
	v_mul_f32_e32 v168, 0x43000000, v168
	v_mul_f32_e32 v169, 0x43000000, v169
	v_mul_f32_e32 v170, 0x43000000, v170
	v_mul_f32_e32 v171, 0x43000000, v171
	ds_write_b128 v209, v[168:171] offset:6144
	v_mul_f32_e32 v172, 0x43000000, v172
	v_mul_f32_e32 v173, 0x43000000, v173
	v_mul_f32_e32 v174, 0x43000000, v174
	v_mul_f32_e32 v175, 0x43000000, v175
	ds_write_b128 v209, v[172:175] offset:7168
	s_waitcnt lgkmcnt(0)
	s_barrier
	s_mov_b64 s[8:9], s[42:43]
	global_load_dwordx4 v[144:147], v75, s[8:9]
	s_add_u32 s8, s8, 0x8000
	s_addc_u32 s9, s9, 0
	global_load_dwordx4 v[148:151], v75, s[8:9]
	s_add_u32 s8, s8, 0x8000
	s_addc_u32 s9, s9, 0
	global_load_dwordx4 v[152:155], v75, s[8:9]
	s_add_u32 s8, s8, 0x8000
	s_addc_u32 s9, s9, 0
	global_load_dwordx4 v[156:159], v75, s[8:9]
	s_add_u32 s8, s8, 0x8000
	s_addc_u32 s9, s9, 0
	global_load_dwordx4 v[160:163], v75, s[8:9]
	s_add_u32 s8, s8, 0x8000
	s_addc_u32 s9, s9, 0
	global_load_dwordx4 v[164:167], v75, s[8:9]
	s_add_u32 s8, s8, 0x8000
	s_addc_u32 s9, s9, 0
	global_load_dwordx4 v[168:171], v75, s[8:9]
	s_add_u32 s8, s8, 0x8000
	s_addc_u32 s9, s9, 0
	global_load_dwordx4 v[172:175], v75, s[8:9]
	s_add_u32 s6, s40, 0x2003000
	s_addc_u32 s7, s41, 0
	ds_read_b32 v226, v211
	ds_read_b32 v227, v211 offset:512
	ds_read_b32 v228, v211 offset:1024
	ds_read_b32 v229, v211 offset:1536
	ds_read_b32 v230, v211 offset:2048
	ds_read_b32 v231, v211 offset:2560
	ds_read_b32 v232, v211 offset:3072
	ds_read_b32 v233, v211 offset:3584
	ds_read_b32 v234, v211 offset:4096
	ds_read_b32 v235, v211 offset:4608
	ds_read_b32 v236, v211 offset:5120
	ds_read_b32 v237, v211 offset:5632
	ds_read_b32 v238, v211 offset:6144
	ds_read_b32 v239, v211 offset:6656
	ds_read_b32 v240, v211 offset:7168
	ds_read_b32 v241, v211 offset:7680
	s_waitcnt lgkmcnt(0)
	v_max_f32_e32 v226, v226, v226
	v_max_f32_e32 v227, v227, v227
	v_max_f32_e32 v228, v228, v228
	v_max_f32_e32 v229, v229, v229
	v_max_f32_e32 v230, v230, v230
	v_max_f32_e32 v231, v231, v231
	v_max_f32_e32 v232, v232, v232
	v_max_f32_e32 v233, v233, v233
	v_max_f32_e32 v234, v234, v234
	v_max_f32_e32 v235, v235, v235
	v_max_f32_e32 v236, v236, v236
	v_max_f32_e32 v237, v237, v237
	v_max_f32_e32 v238, v238, v238
	v_max_f32_e32 v239, v239, v239
	v_max_f32_e32 v240, v240, v240
	v_max_f32_e32 v241, v241, v241
	v_med3_f32 v226, v226, s62, v95
	v_med3_f32 v227, v227, s62, v95
	v_med3_f32 v228, v228, s62, v95
	v_med3_f32 v229, v229, s62, v95
	v_med3_f32 v230, v230, s62, v95
	v_med3_f32 v231, v231, s62, v95
	v_med3_f32 v232, v232, s62, v95
	v_med3_f32 v233, v233, s62, v95
	v_med3_f32 v234, v234, s62, v95
	v_med3_f32 v235, v235, s62, v95
	v_med3_f32 v236, v236, s62, v95
	v_med3_f32 v237, v237, s62, v95
	v_med3_f32 v238, v238, s62, v95
	v_med3_f32 v239, v239, s62, v95
	v_med3_f32 v240, v240, s62, v95
	v_med3_f32 v241, v241, s62, v95
	v_mov_b32_e32 v242, 0
	v_mov_b32_e32 v243, 0
	v_mov_b32_e32 v244, 0
	v_mov_b32_e32 v245, 0
	v_cvt_pk_fp8_f32 v242, v226, v227
	v_cvt_pk_fp8_f32 v243, v230, v231
	v_cvt_pk_fp8_f32 v244, v234, v235
	v_cvt_pk_fp8_f32 v245, v238, v239
	v_cvt_pk_fp8_f32 v242, v228, v229 op_sel:[0,0,1]
	v_cvt_pk_fp8_f32 v243, v232, v233 op_sel:[0,0,1]
	v_cvt_pk_fp8_f32 v244, v236, v237 op_sel:[0,0,1]
	v_cvt_pk_fp8_f32 v245, v240, v241 op_sel:[0,0,1]
	s_nop 0
	global_store_dwordx4 v79, v[242:245], s[6:7]
	ds_read_b32 v226, v213
	ds_read_b32 v227, v213 offset:512
	ds_read_b32 v228, v213 offset:1024
	ds_read_b32 v229, v213 offset:1536
	ds_read_b32 v230, v213 offset:2048
	ds_read_b32 v231, v213 offset:2560
	ds_read_b32 v232, v213 offset:3072
	ds_read_b32 v233, v213 offset:3584
	ds_read_b32 v234, v213 offset:4096
	ds_read_b32 v235, v213 offset:4608
	ds_read_b32 v236, v213 offset:5120
	ds_read_b32 v237, v213 offset:5632
	ds_read_b32 v238, v213 offset:6144
	ds_read_b32 v239, v213 offset:6656
	ds_read_b32 v240, v213 offset:7168
	ds_read_b32 v241, v213 offset:7680
	s_waitcnt lgkmcnt(0)
; #define GAS __attribute__((address_space(1)))
; #define LAS __attribute__((address_space(3)))
; #define LDS_WAIT() asm volatile("s_waitcnt lgkmcnt(0)" ::: "memory")
;     const int pr = item >> 1, kb = 2 * (pr / nblk) + (item & 1), nb = pr % nblk, k0 = 64 * kb, n0 = 32 * nb;
;     const int nr = n0 + (lane & 31); const int sc = MAP == 1 ? src_col_in(nr) : nr;
;     float v[32];
; #pragma unroll
;     for (int i = 0; i < 32; ++i) v[i] = sc >= 0 ? W[(size_t)(k0 + 2 * i + (lane >> 5)) * Nsrc + sc] : 0.f;
; #pragma unroll
;     for (int i = 0; i < 32; ++i) { const int k = k0 + 2 * i + (lane >> 5); float x = v[i] * wscale; if (KS) x *= (k < ksplit ? ksA[k] : ksB[k - ksplit]); scr[(2 * i + (lane >> 5)) * 33 + (lane & 31)] = x; }
;     LDS_WAIT(); asm volatile("" ::: "memory");
;     const int c = lane & 7;
; #pragma unroll
;     for (int j = 0; j < 4; ++j) { const int n = (lane >> 3) + 8 * j; const LAS float* s = scr + (8 * c) * 33 + n;
;         const unsigned long long o = (unsigned long long)pg8::pk4_fp8(s[0 * 33], s[1 * 33], s[2 * 33], s[3 * 33]) | ((unsigned long long)pg8::pk4_fp8(s[4 * 33], s[5 * 33], s[6 * 33], s[7 * 33]) << 32);
;         *(GAS unsigned long long*)(WT + (size_t)(n0 + n) * K + k0 + 8 * c) = o; }
;     LDS_WAIT(); asm volatile("" ::: "memory");
; }
; __global__ void __launch_bounds__(NWAVES * 64, 2) hybrid_fwd(Args args) {
;     ...
;             p0_transpose_item_f8<false>(args.in[16] + (size_t)l * FF * DM, FF, DM, DM / 32, (unsigned char*)(ws + WS_WDN + l * SZ_WDN), 128.f, args.in[16], args.in[16], 0, scr, r, lane);
	v_max_f32_e32 v226, v226, v226
	v_max_f32_e32 v227, v227, v227
	v_max_f32_e32 v228, v228, v228
	v_max_f32_e32 v229, v229, v229
	v_max_f32_e32 v230, v230, v230
	v_max_f32_e32 v231, v231, v231
	v_max_f32_e32 v232, v232, v232
	v_max_f32_e32 v233, v233, v233
	v_max_f32_e32 v234, v234, v234
	v_max_f32_e32 v235, v235, v235
	v_max_f32_e32 v236, v236, v236
	v_max_f32_e32 v237, v237, v237
	v_max_f32_e32 v238, v238, v238
	v_max_f32_e32 v239, v239, v239
	v_max_f32_e32 v240, v240, v240
	v_max_f32_e32 v241, v241, v241
	v_med3_f32 v226, v226, s62, v95
	v_med3_f32 v227, v227, s62, v95
	v_med3_f32 v228, v228, s62, v95
	v_med3_f32 v229, v229, s62, v95
	v_med3_f32 v230, v230, s62, v95
	v_med3_f32 v231, v231, s62, v95
	v_med3_f32 v232, v232, s62, v95
	v_med3_f32 v233, v233, s62, v95
	v_med3_f32 v234, v234, s62, v95
	v_med3_f32 v235, v235, s62, v95
	v_med3_f32 v236, v236, s62, v95
	v_med3_f32 v237, v237, s62, v95
	v_med3_f32 v238, v238, s62, v95
	v_med3_f32 v239, v239, s62, v95
	v_med3_f32 v240, v240, s62, v95
	v_med3_f32 v241, v241, s62, v95
	v_mov_b32_e32 v242, 0
	v_mov_b32_e32 v243, 0
	v_mov_b32_e32 v244, 0
	v_mov_b32_e32 v245, 0
	v_cvt_pk_fp8_f32 v242, v226, v227
	v_cvt_pk_fp8_f32 v243, v230, v231
	v_cvt_pk_fp8_f32 v244, v234, v235
	v_cvt_pk_fp8_f32 v245, v238, v239
	v_cvt_pk_fp8_f32 v242, v228, v229 op_sel:[0,0,1]
	v_cvt_pk_fp8_f32 v243, v232, v233 op_sel:[0,0,1]
	v_cvt_pk_fp8_f32 v244, v236, v237 op_sel:[0,0,1]
	v_cvt_pk_fp8_f32 v245, v240, v241 op_sel:[0,0,1]
	s_nop 0
	global_store_dwordx4 v80, v[242:245], s[6:7]
	s_waitcnt vmcnt(12)
	v_mul_f32_e32 v176, 0x43000000, v176
	v_mul_f32_e32 v177, 0x43000000, v177
	v_mul_f32_e32 v178, 0x43000000, v178
	v_mul_f32_e32 v179, 0x43000000, v179
	ds_write_b128 v210, v[176:179]
	v_mul_f32_e32 v180, 0x43000000, v180
	v_mul_f32_e32 v181, 0x43000000, v181
	v_mul_f32_e32 v182, 0x43000000, v182
	v_mul_f32_e32 v183, 0x43000000, v183
	ds_write_b128 v210, v[180:183] offset:1024
	v_mul_f32_e32 v184, 0x43000000, v184
	v_mul_f32_e32 v185, 0x43000000, v185
	v_mul_f32_e32 v186, 0x43000000, v186
	v_mul_f32_e32 v187, 0x43000000, v187
	ds_write_b128 v210, v[184:187] offset:2048
	v_mul_f32_e32 v188, 0x43000000, v188
	v_mul_f32_e32 v189, 0x43000000, v189
	v_mul_f32_e32 v190, 0x43000000, v190
	v_mul_f32_e32 v191, 0x43000000, v191
	ds_write_b128 v210, v[188:191] offset:3072
	v_mul_f32_e32 v192, 0x43000000, v192
	v_mul_f32_e32 v193, 0x43000000, v193
	v_mul_f32_e32 v194, 0x43000000, v194
	v_mul_f32_e32 v195, 0x43000000, v195
	ds_write_b128 v210, v[192:195] offset:4096
	v_mul_f32_e32 v196, 0x43000000, v196
	v_mul_f32_e32 v197, 0x43000000, v197
	v_mul_f32_e32 v198, 0x43000000, v198
	v_mul_f32_e32 v199, 0x43000000, v199
	ds_write_b128 v210, v[196:199] offset:5120
	v_mul_f32_e32 v200, 0x43000000, v200
	v_mul_f32_e32 v201, 0x43000000, v201
	v_mul_f32_e32 v202, 0x43000000, v202
	v_mul_f32_e32 v203, 0x43000000, v203
	ds_write_b128 v210, v[200:203] offset:6144
	v_mul_f32_e32 v204, 0x43000000, v204
	v_mul_f32_e32 v205, 0x43000000, v205
	v_mul_f32_e32 v206, 0x43000000, v206
	v_mul_f32_e32 v207, 0x43000000, v207
	ds_write_b128 v210, v[204:207] offset:7168
	s_waitcnt lgkmcnt(0)
	s_barrier
	s_add_u32 s8, s42, 0x1000
	s_addc_u32 s9, s43, 0
	global_load_dwordx4 v[176:179], v75, s[8:9]
	s_add_u32 s8, s8, 0x8000
	s_addc_u32 s9, s9, 0
	global_load_dwordx4 v[180:183], v75, s[8:9]
	s_add_u32 s8, s8, 0x8000
	s_addc_u32 s9, s9, 0
	global_load_dwordx4 v[184:187], v75, s[8:9]
	s_add_u32 s8, s8, 0x8000
	s_addc_u32 s9, s9, 0
	global_load_dwordx4 v[188:191], v75, s[8:9]
	s_add_u32 s8, s8, 0x8000
	s_addc_u32 s9, s9, 0
	global_load_dwordx4 v[192:195], v75, s[8:9]
	s_add_u32 s8, s8, 0x8000
	s_addc_u32 s9, s9, 0
	global_load_dwordx4 v[196:199], v75, s[8:9]
	s_add_u32 s8, s8, 0x8000
	s_addc_u32 s9, s9, 0
	global_load_dwordx4 v[200:203], v75, s[8:9]
	s_add_u32 s8, s8, 0x8000
	s_addc_u32 s9, s9, 0
	global_load_dwordx4 v[204:207], v75, s[8:9]
	s_add_u32 s6, s40, 0x3003000
	s_addc_u32 s7, s41, 0
	ds_read_b32 v226, v212
	ds_read_b32 v227, v212 offset:512
	ds_read_b32 v228, v212 offset:1024
	ds_read_b32 v229, v212 offset:1536
	ds_read_b32 v230, v212 offset:2048
	ds_read_b32 v231, v212 offset:2560
	ds_read_b32 v232, v212 offset:3072
	ds_read_b32 v233, v212 offset:3584
	ds_read_b32 v234, v212 offset:4096
	ds_read_b32 v235, v212 offset:4608
	ds_read_b32 v236, v212 offset:5120
	ds_read_b32 v237, v212 offset:5632
	ds_read_b32 v238, v212 offset:6144
	ds_read_b32 v239, v212 offset:6656
	ds_read_b32 v240, v212 offset:7168
	ds_read_b32 v241, v212 offset:7680
	s_waitcnt lgkmcnt(0)
	v_max_f32_e32 v226, v226, v226
	v_max_f32_e32 v227, v227, v227
	v_max_f32_e32 v228, v228, v228
	v_max_f32_e32 v229, v229, v229
	v_max_f32_e32 v230, v230, v230
	v_max_f32_e32 v231, v231, v231
	v_max_f32_e32 v232, v232, v232
	v_max_f32_e32 v233, v233, v233
	v_max_f32_e32 v234, v234, v234
	v_max_f32_e32 v235, v235, v235
	v_max_f32_e32 v236, v236, v236
	v_max_f32_e32 v237, v237, v237
	v_max_f32_e32 v238, v238, v238
	v_max_f32_e32 v239, v239, v239
	v_max_f32_e32 v240, v240, v240
	v_max_f32_e32 v241, v241, v241
	v_med3_f32 v226, v226, s62, v95
	v_med3_f32 v227, v227, s62, v95
	v_med3_f32 v228, v228, s62, v95
	v_med3_f32 v229, v229, s62, v95
	v_med3_f32 v230, v230, s62, v95
	v_med3_f32 v231, v231, s62, v95
	v_med3_f32 v232, v232, s62, v95
	v_med3_f32 v233, v233, s62, v95
	v_med3_f32 v234, v234, s62, v95
	v_med3_f32 v235, v235, s62, v95
	v_med3_f32 v236, v236, s62, v95
	v_med3_f32 v237, v237, s62, v95
	v_med3_f32 v238, v238, s62, v95
	v_med3_f32 v239, v239, s62, v95
	v_med3_f32 v240, v240, s62, v95
	v_med3_f32 v241, v241, s62, v95
	v_mov_b32_e32 v242, 0
	v_mov_b32_e32 v243, 0
	v_mov_b32_e32 v244, 0
	v_mov_b32_e32 v245, 0
	v_cvt_pk_fp8_f32 v242, v226, v227
	v_cvt_pk_fp8_f32 v243, v230, v231
	v_cvt_pk_fp8_f32 v244, v234, v235
	v_cvt_pk_fp8_f32 v245, v238, v239
	v_cvt_pk_fp8_f32 v242, v228, v229 op_sel:[0,0,1]
	v_cvt_pk_fp8_f32 v243, v232, v233 op_sel:[0,0,1]
	v_cvt_pk_fp8_f32 v244, v236, v237 op_sel:[0,0,1]
	v_cvt_pk_fp8_f32 v245, v240, v241 op_sel:[0,0,1]
	s_nop 0
	global_store_dwordx4 v79, v[242:245], s[6:7]
	ds_read_b32 v226, v214
	ds_read_b32 v227, v214 offset:512
	ds_read_b32 v228, v214 offset:1024
	ds_read_b32 v229, v214 offset:1536
	ds_read_b32 v230, v214 offset:2048
	ds_read_b32 v231, v214 offset:2560
	ds_read_b32 v232, v214 offset:3072
	ds_read_b32 v233, v214 offset:3584
	ds_read_b32 v234, v214 offset:4096
	ds_read_b32 v235, v214 offset:4608
	ds_read_b32 v236, v214 offset:5120
	ds_read_b32 v237, v214 offset:5632
	ds_read_b32 v238, v214 offset:6144
	ds_read_b32 v239, v214 offset:6656
	ds_read_b32 v240, v214 offset:7168
	ds_read_b32 v241, v214 offset:7680
	s_waitcnt lgkmcnt(0)
; #define GAS __attribute__((address_space(1)))
; #define LAS __attribute__((address_space(3)))
; #define LDS_WAIT() asm volatile("s_waitcnt lgkmcnt(0)" ::: "memory")
;     const int pr = item >> 1, kb = 2 * (pr / nblk) + (item & 1), nb = pr % nblk, k0 = 64 * kb, n0 = 32 * nb;
;     const int nr = n0 + (lane & 31); const int sc = MAP == 1 ? src_col_in(nr) : nr;
;     float v[32];
; #pragma unroll
;     for (int i = 0; i < 32; ++i) v[i] = sc >= 0 ? W[(size_t)(k0 + 2 * i + (lane >> 5)) * Nsrc + sc] : 0.f;
; #pragma unroll
;     for (int i = 0; i < 32; ++i) { const int k = k0 + 2 * i + (lane >> 5); float x = v[i] * wscale; if (KS) x *= (k < ksplit ? ksA[k] : ksB[k - ksplit]); scr[(2 * i + (lane >> 5)) * 33 + (lane & 31)] = x; }
;     LDS_WAIT(); asm volatile("" ::: "memory");
;     const int c = lane & 7;
; #pragma unroll
;     for (int j = 0; j < 4; ++j) { const int n = (lane >> 3) + 8 * j; const LAS float* s = scr + (8 * c) * 33 + n;
;         const unsigned long long o = (unsigned long long)pg8::pk4_fp8(s[0 * 33], s[1 * 33], s[2 * 33], s[3 * 33]) | ((unsigned long long)pg8::pk4_fp8(s[4 * 33], s[5 * 33], s[6 * 33], s[7 * 33]) << 32);
;         *(GAS unsigned long long*)(WT + (size_t)(n0 + n) * K + k0 + 8 * c) = o; }
;     LDS_WAIT(); asm volatile("" ::: "memory");
; }
; __global__ void __launch_bounds__(NWAVES * 64, 2) hybrid_fwd(Args args) {
;     ...
;             p0_transpose_item_f8<false>(args.in[16] + (size_t)l * FF * DM, FF, DM, DM / 32, (unsigned char*)(ws + WS_WDN + l * SZ_WDN), 128.f, args.in[16], args.in[16], 0, scr, r, lane);
	v_max_f32_e32 v226, v226, v226
	v_max_f32_e32 v227, v227, v227
	v_max_f32_e32 v228, v228, v228
	v_max_f32_e32 v229, v229, v229
	v_max_f32_e32 v230, v230, v230
	v_max_f32_e32 v231, v231, v231
	v_max_f32_e32 v232, v232, v232
	v_max_f32_e32 v233, v233, v233
	v_max_f32_e32 v234, v234, v234
	v_max_f32_e32 v235, v235, v235
	v_max_f32_e32 v236, v236, v236
	v_max_f32_e32 v237, v237, v237
	v_max_f32_e32 v238, v238, v238
	v_max_f32_e32 v239, v239, v239
	v_max_f32_e32 v240, v240, v240
	v_max_f32_e32 v241, v241, v241
	v_med3_f32 v226, v226, s62, v95
	v_med3_f32 v227, v227, s62, v95
	v_med3_f32 v228, v228, s62, v95
	v_med3_f32 v229, v229, s62, v95
	v_med3_f32 v230, v230, s62, v95
	v_med3_f32 v231, v231, s62, v95
	v_med3_f32 v232, v232, s62, v95
	v_med3_f32 v233, v233, s62, v95
	v_med3_f32 v234, v234, s62, v95
	v_med3_f32 v235, v235, s62, v95
	v_med3_f32 v236, v236, s62, v95
	v_med3_f32 v237, v237, s62, v95
	v_med3_f32 v238, v238, s62, v95
	v_med3_f32 v239, v239, s62, v95
	v_med3_f32 v240, v240, s62, v95
	v_med3_f32 v241, v241, s62, v95
	v_mov_b32_e32 v242, 0
	v_mov_b32_e32 v243, 0
	v_mov_b32_e32 v244, 0
	v_mov_b32_e32 v245, 0
	v_cvt_pk_fp8_f32 v242, v226, v227
	v_cvt_pk_fp8_f32 v243, v230, v231
	v_cvt_pk_fp8_f32 v244, v234, v235
	v_cvt_pk_fp8_f32 v245, v238, v239
	v_cvt_pk_fp8_f32 v242, v228, v229 op_sel:[0,0,1]
	v_cvt_pk_fp8_f32 v243, v232, v233 op_sel:[0,0,1]
	v_cvt_pk_fp8_f32 v244, v236, v237 op_sel:[0,0,1]
	v_cvt_pk_fp8_f32 v245, v240, v241 op_sel:[0,0,1]
	s_nop 0
	global_store_dwordx4 v80, v[242:245], s[6:7]
	s_waitcnt vmcnt(12)
	v_mul_f32_e32 v144, 0x43000000, v144
	v_mul_f32_e32 v145, 0x43000000, v145
	v_mul_f32_e32 v146, 0x43000000, v146
	v_mul_f32_e32 v147, 0x43000000, v147
	ds_write_b128 v209, v[144:147]
	v_mul_f32_e32 v148, 0x43000000, v148
	v_mul_f32_e32 v149, 0x43000000, v149
	v_mul_f32_e32 v150, 0x43000000, v150
	v_mul_f32_e32 v151, 0x43000000, v151
	ds_write_b128 v209, v[148:151] offset:1024
	v_mul_f32_e32 v152, 0x43000000, v152
	v_mul_f32_e32 v153, 0x43000000, v153
	v_mul_f32_e32 v154, 0x43000000, v154
	v_mul_f32_e32 v155, 0x43000000, v155
	ds_write_b128 v209, v[152:155] offset:2048
	v_mul_f32_e32 v156, 0x43000000, v156
	v_mul_f32_e32 v157, 0x43000000, v157
	v_mul_f32_e32 v158, 0x43000000, v158
	v_mul_f32_e32 v159, 0x43000000, v159
	ds_write_b128 v209, v[156:159] offset:3072
	v_mul_f32_e32 v160, 0x43000000, v160
	v_mul_f32_e32 v161, 0x43000000, v161
	v_mul_f32_e32 v162, 0x43000000, v162
	v_mul_f32_e32 v163, 0x43000000, v163
	ds_write_b128 v209, v[160:163] offset:4096
	v_mul_f32_e32 v164, 0x43000000, v164
	v_mul_f32_e32 v165, 0x43000000, v165
	v_mul_f32_e32 v166, 0x43000000, v166
	v_mul_f32_e32 v167, 0x43000000, v167
	ds_write_b128 v209, v[164:167] offset:5120
	v_mul_f32_e32 v168, 0x43000000, v168
	v_mul_f32_e32 v169, 0x43000000, v169
	v_mul_f32_e32 v170, 0x43000000, v170
	v_mul_f32_e32 v171, 0x43000000, v171
	ds_write_b128 v209, v[168:171] offset:6144
	v_mul_f32_e32 v172, 0x43000000, v172
	v_mul_f32_e32 v173, 0x43000000, v173
	v_mul_f32_e32 v174, 0x43000000, v174
	v_mul_f32_e32 v175, 0x43000000, v175
	ds_write_b128 v209, v[172:175] offset:7168
	s_waitcnt lgkmcnt(0)
	s_barrier
	s_add_u32 s8, s42, 0x2000
	s_addc_u32 s9, s43, 0
	global_load_dwordx4 v[144:147], v75, s[8:9]
	s_add_u32 s8, s8, 0x8000
	s_addc_u32 s9, s9, 0
	global_load_dwordx4 v[148:151], v75, s[8:9]
	s_add_u32 s8, s8, 0x8000
	s_addc_u32 s9, s9, 0
	global_load_dwordx4 v[152:155], v75, s[8:9]
	s_add_u32 s8, s8, 0x8000
	s_addc_u32 s9, s9, 0
	global_load_dwordx4 v[156:159], v75, s[8:9]
	s_add_u32 s8, s8, 0x8000
	s_addc_u32 s9, s9, 0
	global_load_dwordx4 v[160:163], v75, s[8:9]
	s_add_u32 s8, s8, 0x8000
	s_addc_u32 s9, s9, 0
	global_load_dwordx4 v[164:167], v75, s[8:9]
	s_add_u32 s8, s8, 0x8000
	s_addc_u32 s9, s9, 0
	global_load_dwordx4 v[168:171], v75, s[8:9]
	s_add_u32 s8, s8, 0x8000
	s_addc_u32 s9, s9, 0
	global_load_dwordx4 v[172:175], v75, s[8:9]
	s_mov_b64 s[6:7], s[44:45]
	ds_read_b32 v226, v211
	ds_read_b32 v227, v211 offset:512
	ds_read_b32 v228, v211 offset:1024
	ds_read_b32 v229, v211 offset:1536
	ds_read_b32 v230, v211 offset:2048
	ds_read_b32 v231, v211 offset:2560
	ds_read_b32 v232, v211 offset:3072
	ds_read_b32 v233, v211 offset:3584
	ds_read_b32 v234, v211 offset:4096
	ds_read_b32 v235, v211 offset:4608
	ds_read_b32 v236, v211 offset:5120
	ds_read_b32 v237, v211 offset:5632
	ds_read_b32 v238, v211 offset:6144
	ds_read_b32 v239, v211 offset:6656
	ds_read_b32 v240, v211 offset:7168
	ds_read_b32 v241, v211 offset:7680
	s_waitcnt lgkmcnt(0)
	v_max_f32_e32 v226, v226, v226
	v_max_f32_e32 v227, v227, v227
	v_max_f32_e32 v228, v228, v228
	v_max_f32_e32 v229, v229, v229
	v_max_f32_e32 v230, v230, v230
	v_max_f32_e32 v231, v231, v231
	v_max_f32_e32 v232, v232, v232
	v_max_f32_e32 v233, v233, v233
	v_max_f32_e32 v234, v234, v234
	v_max_f32_e32 v235, v235, v235
	v_max_f32_e32 v236, v236, v236
	v_max_f32_e32 v237, v237, v237
	v_max_f32_e32 v238, v238, v238
	v_max_f32_e32 v239, v239, v239
	v_max_f32_e32 v240, v240, v240
	v_max_f32_e32 v241, v241, v241
	v_med3_f32 v226, v226, s62, v95
	v_med3_f32 v227, v227, s62, v95
	v_med3_f32 v228, v228, s62, v95
	v_med3_f32 v229, v229, s62, v95
	v_med3_f32 v230, v230, s62, v95
	v_med3_f32 v231, v231, s62, v95
	v_med3_f32 v232, v232, s62, v95
	v_med3_f32 v233, v233, s62, v95
	v_med3_f32 v234, v234, s62, v95
	v_med3_f32 v235, v235, s62, v95
	v_med3_f32 v236, v236, s62, v95
	v_med3_f32 v237, v237, s62, v95
	v_med3_f32 v238, v238, s62, v95
	v_med3_f32 v239, v239, s62, v95
	v_med3_f32 v240, v240, s62, v95
	v_med3_f32 v241, v241, s62, v95
	v_mov_b32_e32 v242, 0
	v_mov_b32_e32 v243, 0
	v_mov_b32_e32 v244, 0
	v_mov_b32_e32 v245, 0
	v_cvt_pk_fp8_f32 v242, v226, v227
	v_cvt_pk_fp8_f32 v243, v230, v231
	v_cvt_pk_fp8_f32 v244, v234, v235
	v_cvt_pk_fp8_f32 v245, v238, v239
	v_cvt_pk_fp8_f32 v242, v228, v229 op_sel:[0,0,1]
	v_cvt_pk_fp8_f32 v243, v232, v233 op_sel:[0,0,1]
	v_cvt_pk_fp8_f32 v244, v236, v237 op_sel:[0,0,1]
	v_cvt_pk_fp8_f32 v245, v240, v241 op_sel:[0,0,1]
	s_nop 0
	global_store_dwordx4 v79, v[242:245], s[6:7]
	ds_read_b32 v226, v213
	ds_read_b32 v227, v213 offset:512
	ds_read_b32 v228, v213 offset:1024
	ds_read_b32 v229, v213 offset:1536
	ds_read_b32 v230, v213 offset:2048
	ds_read_b32 v231, v213 offset:2560
	ds_read_b32 v232, v213 offset:3072
	ds_read_b32 v233, v213 offset:3584
	ds_read_b32 v234, v213 offset:4096
	ds_read_b32 v235, v213 offset:4608
	ds_read_b32 v236, v213 offset:5120
	ds_read_b32 v237, v213 offset:5632
	ds_read_b32 v238, v213 offset:6144
	ds_read_b32 v239, v213 offset:6656
	ds_read_b32 v240, v213 offset:7168
	ds_read_b32 v241, v213 offset:7680
	s_waitcnt lgkmcnt(0)
; #define GAS __attribute__((address_space(1)))
; #define LAS __attribute__((address_space(3)))
; #define LDS_WAIT() asm volatile("s_waitcnt lgkmcnt(0)" ::: "memory")
;     const int pr = item >> 1, kb = 2 * (pr / nblk) + (item & 1), nb = pr % nblk, k0 = 64 * kb, n0 = 32 * nb;
;     const int nr = n0 + (lane & 31); const int sc = MAP == 1 ? src_col_in(nr) : nr;
;     float v[32];
; #pragma unroll
;     for (int i = 0; i < 32; ++i) v[i] = sc >= 0 ? W[(size_t)(k0 + 2 * i + (lane >> 5)) * Nsrc + sc] : 0.f;
; #pragma unroll
;     for (int i = 0; i < 32; ++i) { const int k = k0 + 2 * i + (lane >> 5); float x = v[i] * wscale; if (KS) x *= (k < ksplit ? ksA[k] : ksB[k - ksplit]); scr[(2 * i + (lane >> 5)) * 33 + (lane & 31)] = x; }
;     LDS_WAIT(); asm volatile("" ::: "memory");
;     const int c = lane & 7;
; #pragma unroll
;     for (int j = 0; j < 4; ++j) { const int n = (lane >> 3) + 8 * j; const LAS float* s = scr + (8 * c) * 33 + n;
;         const unsigned long long o = (unsigned long long)pg8::pk4_fp8(s[0 * 33], s[1 * 33], s[2 * 33], s[3 * 33]) | ((unsigned long long)pg8::pk4_fp8(s[4 * 33], s[5 * 33], s[6 * 33], s[7 * 33]) << 32);
;         *(GAS unsigned long long*)(WT + (size_t)(n0 + n) * K + k0 + 8 * c) = o; }
;     LDS_WAIT(); asm volatile("" ::: "memory");
; }
; __global__ void __launch_bounds__(NWAVES * 64, 2) hybrid_fwd(Args args) {
;     ...
;             p0_transpose_item_f8<false>(args.in[16] + (size_t)l * FF * DM, FF, DM, DM / 32, (unsigned char*)(ws + WS_WDN + l * SZ_WDN), 128.f, args.in[16], args.in[16], 0, scr, r, lane);
	v_max_f32_e32 v226, v226, v226
	v_max_f32_e32 v227, v227, v227
	v_max_f32_e32 v228, v228, v228
	v_max_f32_e32 v229, v229, v229
	v_max_f32_e32 v230, v230, v230
	v_max_f32_e32 v231, v231, v231
	v_max_f32_e32 v232, v232, v232
	v_max_f32_e32 v233, v233, v233
	v_max_f32_e32 v234, v234, v234
	v_max_f32_e32 v235, v235, v235
	v_max_f32_e32 v236, v236, v236
	v_max_f32_e32 v237, v237, v237
	v_max_f32_e32 v238, v238, v238
	v_max_f32_e32 v239, v239, v239
	v_max_f32_e32 v240, v240, v240
	v_max_f32_e32 v241, v241, v241
	v_med3_f32 v226, v226, s62, v95
	v_med3_f32 v227, v227, s62, v95
	v_med3_f32 v228, v228, s62, v95
	v_med3_f32 v229, v229, s62, v95
	v_med3_f32 v230, v230, s62, v95
	v_med3_f32 v231, v231, s62, v95
	v_med3_f32 v232, v232, s62, v95
	v_med3_f32 v233, v233, s62, v95
	v_med3_f32 v234, v234, s62, v95
	v_med3_f32 v235, v235, s62, v95
	v_med3_f32 v236, v236, s62, v95
	v_med3_f32 v237, v237, s62, v95
	v_med3_f32 v238, v238, s62, v95
	v_med3_f32 v239, v239, s62, v95
	v_med3_f32 v240, v240, s62, v95
	v_med3_f32 v241, v241, s62, v95
	v_mov_b32_e32 v242, 0
	v_mov_b32_e32 v243, 0
	v_mov_b32_e32 v244, 0
	v_mov_b32_e32 v245, 0
	v_cvt_pk_fp8_f32 v242, v226, v227
	v_cvt_pk_fp8_f32 v243, v230, v231
	v_cvt_pk_fp8_f32 v244, v234, v235
	v_cvt_pk_fp8_f32 v245, v238, v239
	v_cvt_pk_fp8_f32 v242, v228, v229 op_sel:[0,0,1]
	v_cvt_pk_fp8_f32 v243, v232, v233 op_sel:[0,0,1]
	v_cvt_pk_fp8_f32 v244, v236, v237 op_sel:[0,0,1]
	v_cvt_pk_fp8_f32 v245, v240, v241 op_sel:[0,0,1]
	s_nop 0
	global_store_dwordx4 v80, v[242:245], s[6:7]
	s_waitcnt vmcnt(12)
	v_mul_f32_e32 v176, 0x43000000, v176
	v_mul_f32_e32 v177, 0x43000000, v177
	v_mul_f32_e32 v178, 0x43000000, v178
	v_mul_f32_e32 v179, 0x43000000, v179
	ds_write_b128 v210, v[176:179]
	v_mul_f32_e32 v180, 0x43000000, v180
	v_mul_f32_e32 v181, 0x43000000, v181
	v_mul_f32_e32 v182, 0x43000000, v182
	v_mul_f32_e32 v183, 0x43000000, v183
	ds_write_b128 v210, v[180:183] offset:1024
	v_mul_f32_e32 v184, 0x43000000, v184
	v_mul_f32_e32 v185, 0x43000000, v185
	v_mul_f32_e32 v186, 0x43000000, v186
	v_mul_f32_e32 v187, 0x43000000, v187
	ds_write_b128 v210, v[184:187] offset:2048
	v_mul_f32_e32 v188, 0x43000000, v188
	v_mul_f32_e32 v189, 0x43000000, v189
	v_mul_f32_e32 v190, 0x43000000, v190
	v_mul_f32_e32 v191, 0x43000000, v191
	ds_write_b128 v210, v[188:191] offset:3072
	v_mul_f32_e32 v192, 0x43000000, v192
	v_mul_f32_e32 v193, 0x43000000, v193
	v_mul_f32_e32 v194, 0x43000000, v194
	v_mul_f32_e32 v195, 0x43000000, v195
	ds_write_b128 v210, v[192:195] offset:4096
	v_mul_f32_e32 v196, 0x43000000, v196
	v_mul_f32_e32 v197, 0x43000000, v197
	v_mul_f32_e32 v198, 0x43000000, v198
	v_mul_f32_e32 v199, 0x43000000, v199
	ds_write_b128 v210, v[196:199] offset:5120
	v_mul_f32_e32 v200, 0x43000000, v200
	v_mul_f32_e32 v201, 0x43000000, v201
	v_mul_f32_e32 v202, 0x43000000, v202
	v_mul_f32_e32 v203, 0x43000000, v203
	ds_write_b128 v210, v[200:203] offset:6144
	v_mul_f32_e32 v204, 0x43000000, v204
	v_mul_f32_e32 v205, 0x43000000, v205
	v_mul_f32_e32 v206, 0x43000000, v206
	v_mul_f32_e32 v207, 0x43000000, v207
	ds_write_b128 v210, v[204:207] offset:7168
	s_waitcnt lgkmcnt(0)
	s_barrier
	s_add_u32 s8, s42, 0x3000
	s_addc_u32 s9, s43, 0
	global_load_dwordx4 v[176:179], v75, s[8:9]
	s_add_u32 s8, s8, 0x8000
	s_addc_u32 s9, s9, 0
	global_load_dwordx4 v[180:183], v75, s[8:9]
	s_add_u32 s8, s8, 0x8000
	s_addc_u32 s9, s9, 0
	global_load_dwordx4 v[184:187], v75, s[8:9]
	s_add_u32 s8, s8, 0x8000
	s_addc_u32 s9, s9, 0
	global_load_dwordx4 v[188:191], v75, s[8:9]
	s_add_u32 s8, s8, 0x8000
	s_addc_u32 s9, s9, 0
	global_load_dwordx4 v[192:195], v75, s[8:9]
	s_add_u32 s8, s8, 0x8000
	s_addc_u32 s9, s9, 0
	global_load_dwordx4 v[196:199], v75, s[8:9]
	s_add_u32 s8, s8, 0x8000
	s_addc_u32 s9, s9, 0
	global_load_dwordx4 v[200:203], v75, s[8:9]
	s_add_u32 s8, s8, 0x8000
	s_addc_u32 s9, s9, 0
	global_load_dwordx4 v[204:207], v75, s[8:9]
	s_add_u32 s6, s44, 0x1000000
	s_addc_u32 s7, s45, 0
	ds_read_b32 v226, v212
	ds_read_b32 v227, v212 offset:512
	ds_read_b32 v228, v212 offset:1024
	ds_read_b32 v229, v212 offset:1536
	ds_read_b32 v230, v212 offset:2048
	ds_read_b32 v231, v212 offset:2560
	ds_read_b32 v232, v212 offset:3072
	ds_read_b32 v233, v212 offset:3584
	ds_read_b32 v234, v212 offset:4096
	ds_read_b32 v235, v212 offset:4608
	ds_read_b32 v236, v212 offset:5120
	ds_read_b32 v237, v212 offset:5632
	ds_read_b32 v238, v212 offset:6144
	ds_read_b32 v239, v212 offset:6656
	ds_read_b32 v240, v212 offset:7168
	ds_read_b32 v241, v212 offset:7680
	s_waitcnt lgkmcnt(0)
	v_max_f32_e32 v226, v226, v226
	v_max_f32_e32 v227, v227, v227
	v_max_f32_e32 v228, v228, v228
	v_max_f32_e32 v229, v229, v229
	v_max_f32_e32 v230, v230, v230
	v_max_f32_e32 v231, v231, v231
	v_max_f32_e32 v232, v232, v232
	v_max_f32_e32 v233, v233, v233
	v_max_f32_e32 v234, v234, v234
	v_max_f32_e32 v235, v235, v235
	v_max_f32_e32 v236, v236, v236
	v_max_f32_e32 v237, v237, v237
	v_max_f32_e32 v238, v238, v238
	v_max_f32_e32 v239, v239, v239
	v_max_f32_e32 v240, v240, v240
	v_max_f32_e32 v241, v241, v241
	v_med3_f32 v226, v226, s62, v95
	v_med3_f32 v227, v227, s62, v95
	v_med3_f32 v228, v228, s62, v95
	v_med3_f32 v229, v229, s62, v95
	v_med3_f32 v230, v230, s62, v95
	v_med3_f32 v231, v231, s62, v95
	v_med3_f32 v232, v232, s62, v95
	v_med3_f32 v233, v233, s62, v95
	v_med3_f32 v234, v234, s62, v95
	v_med3_f32 v235, v235, s62, v95
	v_med3_f32 v236, v236, s62, v95
	v_med3_f32 v237, v237, s62, v95
	v_med3_f32 v238, v238, s62, v95
	v_med3_f32 v239, v239, s62, v95
	v_med3_f32 v240, v240, s62, v95
	v_med3_f32 v241, v241, s62, v95
	v_mov_b32_e32 v242, 0
	v_mov_b32_e32 v243, 0
	v_mov_b32_e32 v244, 0
	v_mov_b32_e32 v245, 0
	v_cvt_pk_fp8_f32 v242, v226, v227
	v_cvt_pk_fp8_f32 v243, v230, v231
	v_cvt_pk_fp8_f32 v244, v234, v235
	v_cvt_pk_fp8_f32 v245, v238, v239
	v_cvt_pk_fp8_f32 v242, v228, v229 op_sel:[0,0,1]
	v_cvt_pk_fp8_f32 v243, v232, v233 op_sel:[0,0,1]
	v_cvt_pk_fp8_f32 v244, v236, v237 op_sel:[0,0,1]
	v_cvt_pk_fp8_f32 v245, v240, v241 op_sel:[0,0,1]
	s_nop 0
	global_store_dwordx4 v79, v[242:245], s[6:7]
	ds_read_b32 v226, v214
	ds_read_b32 v227, v214 offset:512
	ds_read_b32 v228, v214 offset:1024
	ds_read_b32 v229, v214 offset:1536
	ds_read_b32 v230, v214 offset:2048
	ds_read_b32 v231, v214 offset:2560
	ds_read_b32 v232, v214 offset:3072
	ds_read_b32 v233, v214 offset:3584
	ds_read_b32 v234, v214 offset:4096
	ds_read_b32 v235, v214 offset:4608
	ds_read_b32 v236, v214 offset:5120
	ds_read_b32 v237, v214 offset:5632
	ds_read_b32 v238, v214 offset:6144
	ds_read_b32 v239, v214 offset:6656
	ds_read_b32 v240, v214 offset:7168
	ds_read_b32 v241, v214 offset:7680
	s_waitcnt lgkmcnt(0)
; #define GAS __attribute__((address_space(1)))
; #define LAS __attribute__((address_space(3)))
; #define LDS_WAIT() asm volatile("s_waitcnt lgkmcnt(0)" ::: "memory")
;     const int pr = item >> 1, kb = 2 * (pr / nblk) + (item & 1), nb = pr % nblk, k0 = 64 * kb, n0 = 32 * nb;
;     const int nr = n0 + (lane & 31); const int sc = MAP == 1 ? src_col_in(nr) : nr;
;     float v[32];
; #pragma unroll
;     for (int i = 0; i < 32; ++i) v[i] = sc >= 0 ? W[(size_t)(k0 + 2 * i + (lane >> 5)) * Nsrc + sc] : 0.f;
; #pragma unroll
;     for (int i = 0; i < 32; ++i) { const int k = k0 + 2 * i + (lane >> 5); float x = v[i] * wscale; if (KS) x *= (k < ksplit ? ksA[k] : ksB[k - ksplit]); scr[(2 * i + (lane >> 5)) * 33 + (lane & 31)] = x; }
;     LDS_WAIT(); asm volatile("" ::: "memory");
;     const int c = lane & 7;
; #pragma unroll
;     for (int j = 0; j < 4; ++j) { const int n = (lane >> 3) + 8 * j; const LAS float* s = scr + (8 * c) * 33 + n;
;         const unsigned long long o = (unsigned long long)pg8::pk4_fp8(s[0 * 33], s[1 * 33], s[2 * 33], s[3 * 33]) | ((unsigned long long)pg8::pk4_fp8(s[4 * 33], s[5 * 33], s[6 * 33], s[7 * 33]) << 32);
;         *(GAS unsigned long long*)(WT + (size_t)(n0 + n) * K + k0 + 8 * c) = o; }
;     LDS_WAIT(); asm volatile("" ::: "memory");
; }
; __global__ void __launch_bounds__(NWAVES * 64, 2) hybrid_fwd(Args args) {
;     ...
;             p0_transpose_item_f8<false>(args.in[16] + (size_t)l * FF * DM, FF, DM, DM / 32, (unsigned char*)(ws + WS_WDN + l * SZ_WDN), 128.f, args.in[16], args.in[16], 0, scr, r, lane);
	v_max_f32_e32 v226, v226, v226
	v_max_f32_e32 v227, v227, v227
	v_max_f32_e32 v228, v228, v228
	v_max_f32_e32 v229, v229, v229
	v_max_f32_e32 v230, v230, v230
	v_max_f32_e32 v231, v231, v231
	v_max_f32_e32 v232, v232, v232
	v_max_f32_e32 v233, v233, v233
	v_max_f32_e32 v234, v234, v234
	v_max_f32_e32 v235, v235, v235
	v_max_f32_e32 v236, v236, v236
	v_max_f32_e32 v237, v237, v237
	v_max_f32_e32 v238, v238, v238
	v_max_f32_e32 v239, v239, v239
	v_max_f32_e32 v240, v240, v240
	v_max_f32_e32 v241, v241, v241
	v_med3_f32 v226, v226, s62, v95
	v_med3_f32 v227, v227, s62, v95
	v_med3_f32 v228, v228, s62, v95
	v_med3_f32 v229, v229, s62, v95
	v_med3_f32 v230, v230, s62, v95
	v_med3_f32 v231, v231, s62, v95
	v_med3_f32 v232, v232, s62, v95
	v_med3_f32 v233, v233, s62, v95
	v_med3_f32 v234, v234, s62, v95
	v_med3_f32 v235, v235, s62, v95
	v_med3_f32 v236, v236, s62, v95
	v_med3_f32 v237, v237, s62, v95
	v_med3_f32 v238, v238, s62, v95
	v_med3_f32 v239, v239, s62, v95
	v_med3_f32 v240, v240, s62, v95
	v_med3_f32 v241, v241, s62, v95
	v_mov_b32_e32 v242, 0
	v_mov_b32_e32 v243, 0
	v_mov_b32_e32 v244, 0
	v_mov_b32_e32 v245, 0
	v_cvt_pk_fp8_f32 v242, v226, v227
	v_cvt_pk_fp8_f32 v243, v230, v231
	v_cvt_pk_fp8_f32 v244, v234, v235
	v_cvt_pk_fp8_f32 v245, v238, v239
	v_cvt_pk_fp8_f32 v242, v228, v229 op_sel:[0,0,1]
	v_cvt_pk_fp8_f32 v243, v232, v233 op_sel:[0,0,1]
	v_cvt_pk_fp8_f32 v244, v236, v237 op_sel:[0,0,1]
	v_cvt_pk_fp8_f32 v245, v240, v241 op_sel:[0,0,1]
	s_nop 0
	global_store_dwordx4 v80, v[242:245], s[6:7]
	s_waitcnt vmcnt(12)
	v_mul_f32_e32 v144, 0x43000000, v144
	v_mul_f32_e32 v145, 0x43000000, v145
	v_mul_f32_e32 v146, 0x43000000, v146
	v_mul_f32_e32 v147, 0x43000000, v147
	ds_write_b128 v209, v[144:147]
	v_mul_f32_e32 v148, 0x43000000, v148
	v_mul_f32_e32 v149, 0x43000000, v149
	v_mul_f32_e32 v150, 0x43000000, v150
	v_mul_f32_e32 v151, 0x43000000, v151
	ds_write_b128 v209, v[148:151] offset:1024
	v_mul_f32_e32 v152, 0x43000000, v152
	v_mul_f32_e32 v153, 0x43000000, v153
	v_mul_f32_e32 v154, 0x43000000, v154
	v_mul_f32_e32 v155, 0x43000000, v155
	ds_write_b128 v209, v[152:155] offset:2048
	v_mul_f32_e32 v156, 0x43000000, v156
	v_mul_f32_e32 v157, 0x43000000, v157
	v_mul_f32_e32 v158, 0x43000000, v158
	v_mul_f32_e32 v159, 0x43000000, v159
	ds_write_b128 v209, v[156:159] offset:3072
	v_mul_f32_e32 v160, 0x43000000, v160
	v_mul_f32_e32 v161, 0x43000000, v161
	v_mul_f32_e32 v162, 0x43000000, v162
	v_mul_f32_e32 v163, 0x43000000, v163
	ds_write_b128 v209, v[160:163] offset:4096
	v_mul_f32_e32 v164, 0x43000000, v164
	v_mul_f32_e32 v165, 0x43000000, v165
	v_mul_f32_e32 v166, 0x43000000, v166
	v_mul_f32_e32 v167, 0x43000000, v167
	ds_write_b128 v209, v[164:167] offset:5120
	v_mul_f32_e32 v168, 0x43000000, v168
	v_mul_f32_e32 v169, 0x43000000, v169
	v_mul_f32_e32 v170, 0x43000000, v170
	v_mul_f32_e32 v171, 0x43000000, v171
	ds_write_b128 v209, v[168:171] offset:6144
	v_mul_f32_e32 v172, 0x43000000, v172
	v_mul_f32_e32 v173, 0x43000000, v173
	v_mul_f32_e32 v174, 0x43000000, v174
	v_mul_f32_e32 v175, 0x43000000, v175
	ds_write_b128 v209, v[172:175] offset:7168
	s_waitcnt lgkmcnt(0)
	s_barrier
	s_add_u32 s8, s42, 0x4000000
	s_addc_u32 s9, s43, 0
	global_load_dwordx4 v[144:147], v75, s[8:9]
	s_add_u32 s8, s8, 0x8000
	s_addc_u32 s9, s9, 0
	global_load_dwordx4 v[148:151], v75, s[8:9]
	s_add_u32 s8, s8, 0x8000
	s_addc_u32 s9, s9, 0
	global_load_dwordx4 v[152:155], v75, s[8:9]
	s_add_u32 s8, s8, 0x8000
	s_addc_u32 s9, s9, 0
	global_load_dwordx4 v[156:159], v75, s[8:9]
	s_add_u32 s8, s8, 0x8000
	s_addc_u32 s9, s9, 0
	global_load_dwordx4 v[160:163], v75, s[8:9]
	s_add_u32 s8, s8, 0x8000
	s_addc_u32 s9, s9, 0
	global_load_dwordx4 v[164:167], v75, s[8:9]
	s_add_u32 s8, s8, 0x8000
	s_addc_u32 s9, s9, 0
	global_load_dwordx4 v[168:171], v75, s[8:9]
	s_add_u32 s8, s8, 0x8000
	s_addc_u32 s9, s9, 0
	global_load_dwordx4 v[172:175], v75, s[8:9]
	s_add_u32 s6, s44, 0x2000000
	s_addc_u32 s7, s45, 0
	ds_read_b32 v226, v211
	ds_read_b32 v227, v211 offset:512
	ds_read_b32 v228, v211 offset:1024
	ds_read_b32 v229, v211 offset:1536
	ds_read_b32 v230, v211 offset:2048
	ds_read_b32 v231, v211 offset:2560
	ds_read_b32 v232, v211 offset:3072
	ds_read_b32 v233, v211 offset:3584
	ds_read_b32 v234, v211 offset:4096
	ds_read_b32 v235, v211 offset:4608
	ds_read_b32 v236, v211 offset:5120
	ds_read_b32 v237, v211 offset:5632
	ds_read_b32 v238, v211 offset:6144
	ds_read_b32 v239, v211 offset:6656
	ds_read_b32 v240, v211 offset:7168
	ds_read_b32 v241, v211 offset:7680
	s_waitcnt lgkmcnt(0)
	v_max_f32_e32 v226, v226, v226
	v_max_f32_e32 v227, v227, v227
	v_max_f32_e32 v228, v228, v228
	v_max_f32_e32 v229, v229, v229
	v_max_f32_e32 v230, v230, v230
	v_max_f32_e32 v231, v231, v231
	v_max_f32_e32 v232, v232, v232
	v_max_f32_e32 v233, v233, v233
	v_max_f32_e32 v234, v234, v234
	v_max_f32_e32 v235, v235, v235
	v_max_f32_e32 v236, v236, v236
	v_max_f32_e32 v237, v237, v237
	v_max_f32_e32 v238, v238, v238
	v_max_f32_e32 v239, v239, v239
	v_max_f32_e32 v240, v240, v240
	v_max_f32_e32 v241, v241, v241
	v_med3_f32 v226, v226, s62, v95
	v_med3_f32 v227, v227, s62, v95
	v_med3_f32 v228, v228, s62, v95
	v_med3_f32 v229, v229, s62, v95
	v_med3_f32 v230, v230, s62, v95
	v_med3_f32 v231, v231, s62, v95
	v_med3_f32 v232, v232, s62, v95
	v_med3_f32 v233, v233, s62, v95
	v_med3_f32 v234, v234, s62, v95
	v_med3_f32 v235, v235, s62, v95
	v_med3_f32 v236, v236, s62, v95
	v_med3_f32 v237, v237, s62, v95
	v_med3_f32 v238, v238, s62, v95
	v_med3_f32 v239, v239, s62, v95
	v_med3_f32 v240, v240, s62, v95
	v_med3_f32 v241, v241, s62, v95
	v_mov_b32_e32 v242, 0
	v_mov_b32_e32 v243, 0
	v_mov_b32_e32 v244, 0
	v_mov_b32_e32 v245, 0
	v_cvt_pk_fp8_f32 v242, v226, v227
	v_cvt_pk_fp8_f32 v243, v230, v231
	v_cvt_pk_fp8_f32 v244, v234, v235
	v_cvt_pk_fp8_f32 v245, v238, v239
	v_cvt_pk_fp8_f32 v242, v228, v229 op_sel:[0,0,1]
	v_cvt_pk_fp8_f32 v243, v232, v233 op_sel:[0,0,1]
	v_cvt_pk_fp8_f32 v244, v236, v237 op_sel:[0,0,1]
	v_cvt_pk_fp8_f32 v245, v240, v241 op_sel:[0,0,1]
	s_nop 0
	global_store_dwordx4 v79, v[242:245], s[6:7]
	ds_read_b32 v226, v213
	ds_read_b32 v227, v213 offset:512
	ds_read_b32 v228, v213 offset:1024
	ds_read_b32 v229, v213 offset:1536
	ds_read_b32 v230, v213 offset:2048
	ds_read_b32 v231, v213 offset:2560
	ds_read_b32 v232, v213 offset:3072
	ds_read_b32 v233, v213 offset:3584
	ds_read_b32 v234, v213 offset:4096
	ds_read_b32 v235, v213 offset:4608
	ds_read_b32 v236, v213 offset:5120
	ds_read_b32 v237, v213 offset:5632
	ds_read_b32 v238, v213 offset:6144
	ds_read_b32 v239, v213 offset:6656
	ds_read_b32 v240, v213 offset:7168
	ds_read_b32 v241, v213 offset:7680
	s_waitcnt lgkmcnt(0)
; #define GAS __attribute__((address_space(1)))
; #define LAS __attribute__((address_space(3)))
; #define LDS_WAIT() asm volatile("s_waitcnt lgkmcnt(0)" ::: "memory")
;     const int pr = item >> 1, kb = 2 * (pr / nblk) + (item & 1), nb = pr % nblk, k0 = 64 * kb, n0 = 32 * nb;
;     const int nr = n0 + (lane & 31); const int sc = MAP == 1 ? src_col_in(nr) : nr;
;     float v[32];
; #pragma unroll
;     for (int i = 0; i < 32; ++i) v[i] = sc >= 0 ? W[(size_t)(k0 + 2 * i + (lane >> 5)) * Nsrc + sc] : 0.f;
; #pragma unroll
;     for (int i = 0; i < 32; ++i) { const int k = k0 + 2 * i + (lane >> 5); float x = v[i] * wscale; if (KS) x *= (k < ksplit ? ksA[k] : ksB[k - ksplit]); scr[(2 * i + (lane >> 5)) * 33 + (lane & 31)] = x; }
;     LDS_WAIT(); asm volatile("" ::: "memory");
;     const int c = lane & 7;
; #pragma unroll
;     for (int j = 0; j < 4; ++j) { const int n = (lane >> 3) + 8 * j; const LAS float* s = scr + (8 * c) * 33 + n;
;         const unsigned long long o = (unsigned long long)pg8::pk4_fp8(s[0 * 33], s[1 * 33], s[2 * 33], s[3 * 33]) | ((unsigned long long)pg8::pk4_fp8(s[4 * 33], s[5 * 33], s[6 * 33], s[7 * 33]) << 32);
;         *(GAS unsigned long long*)(WT + (size_t)(n0 + n) * K + k0 + 8 * c) = o; }
;     LDS_WAIT(); asm volatile("" ::: "memory");
; }
; __global__ void __launch_bounds__(NWAVES * 64, 2) hybrid_fwd(Args args) {
;     ...
;             p0_transpose_item_f8<false>(args.in[16] + (size_t)l * FF * DM, FF, DM, DM / 32, (unsigned char*)(ws + WS_WDN + l * SZ_WDN), 128.f, args.in[16], args.in[16], 0, scr, r, lane);
	v_max_f32_e32 v226, v226, v226
	v_max_f32_e32 v227, v227, v227
	v_max_f32_e32 v228, v228, v228
	v_max_f32_e32 v229, v229, v229
	v_max_f32_e32 v230, v230, v230
	v_max_f32_e32 v231, v231, v231
	v_max_f32_e32 v232, v232, v232
	v_max_f32_e32 v233, v233, v233
	v_max_f32_e32 v234, v234, v234
	v_max_f32_e32 v235, v235, v235
	v_max_f32_e32 v236, v236, v236
	v_max_f32_e32 v237, v237, v237
	v_max_f32_e32 v238, v238, v238
	v_max_f32_e32 v239, v239, v239
	v_max_f32_e32 v240, v240, v240
	v_max_f32_e32 v241, v241, v241
	v_med3_f32 v226, v226, s62, v95
	v_med3_f32 v227, v227, s62, v95
	v_med3_f32 v228, v228, s62, v95
	v_med3_f32 v229, v229, s62, v95
	v_med3_f32 v230, v230, s62, v95
	v_med3_f32 v231, v231, s62, v95
	v_med3_f32 v232, v232, s62, v95
	v_med3_f32 v233, v233, s62, v95
	v_med3_f32 v234, v234, s62, v95
	v_med3_f32 v235, v235, s62, v95
	v_med3_f32 v236, v236, s62, v95
	v_med3_f32 v237, v237, s62, v95
	v_med3_f32 v238, v238, s62, v95
	v_med3_f32 v239, v239, s62, v95
	v_med3_f32 v240, v240, s62, v95
	v_med3_f32 v241, v241, s62, v95
	v_mov_b32_e32 v242, 0
	v_mov_b32_e32 v243, 0
	v_mov_b32_e32 v244, 0
	v_mov_b32_e32 v245, 0
	v_cvt_pk_fp8_f32 v242, v226, v227
	v_cvt_pk_fp8_f32 v243, v230, v231
	v_cvt_pk_fp8_f32 v244, v234, v235
	v_cvt_pk_fp8_f32 v245, v238, v239
	v_cvt_pk_fp8_f32 v242, v228, v229 op_sel:[0,0,1]
	v_cvt_pk_fp8_f32 v243, v232, v233 op_sel:[0,0,1]
	v_cvt_pk_fp8_f32 v244, v236, v237 op_sel:[0,0,1]
	v_cvt_pk_fp8_f32 v245, v240, v241 op_sel:[0,0,1]
	s_nop 0
	global_store_dwordx4 v80, v[242:245], s[6:7]
	s_waitcnt vmcnt(12)
	v_mul_f32_e32 v176, 0x43000000, v176
	v_mul_f32_e32 v177, 0x43000000, v177
	v_mul_f32_e32 v178, 0x43000000, v178
	v_mul_f32_e32 v179, 0x43000000, v179
	ds_write_b128 v210, v[176:179]
	v_mul_f32_e32 v180, 0x43000000, v180
	v_mul_f32_e32 v181, 0x43000000, v181
	v_mul_f32_e32 v182, 0x43000000, v182
	v_mul_f32_e32 v183, 0x43000000, v183
	ds_write_b128 v210, v[180:183] offset:1024
	v_mul_f32_e32 v184, 0x43000000, v184
	v_mul_f32_e32 v185, 0x43000000, v185
	v_mul_f32_e32 v186, 0x43000000, v186
	v_mul_f32_e32 v187, 0x43000000, v187
	ds_write_b128 v210, v[184:187] offset:2048
	v_mul_f32_e32 v188, 0x43000000, v188
	v_mul_f32_e32 v189, 0x43000000, v189
	v_mul_f32_e32 v190, 0x43000000, v190
	v_mul_f32_e32 v191, 0x43000000, v191
	ds_write_b128 v210, v[188:191] offset:3072
	v_mul_f32_e32 v192, 0x43000000, v192
	v_mul_f32_e32 v193, 0x43000000, v193
	v_mul_f32_e32 v194, 0x43000000, v194
	v_mul_f32_e32 v195, 0x43000000, v195
	ds_write_b128 v210, v[192:195] offset:4096
	v_mul_f32_e32 v196, 0x43000000, v196
	v_mul_f32_e32 v197, 0x43000000, v197
	v_mul_f32_e32 v198, 0x43000000, v198
	v_mul_f32_e32 v199, 0x43000000, v199
	ds_write_b128 v210, v[196:199] offset:5120
	v_mul_f32_e32 v200, 0x43000000, v200
	v_mul_f32_e32 v201, 0x43000000, v201
	v_mul_f32_e32 v202, 0x43000000, v202
	v_mul_f32_e32 v203, 0x43000000, v203
	ds_write_b128 v210, v[200:203] offset:6144
	v_mul_f32_e32 v204, 0x43000000, v204
	v_mul_f32_e32 v205, 0x43000000, v205
	v_mul_f32_e32 v206, 0x43000000, v206
	v_mul_f32_e32 v207, 0x43000000, v207
	ds_write_b128 v210, v[204:207] offset:7168
	s_waitcnt lgkmcnt(0)
	s_barrier
	s_add_u32 s8, s42, 0x4001000
	s_addc_u32 s9, s43, 0
	global_load_dwordx4 v[176:179], v75, s[8:9]
	s_add_u32 s8, s8, 0x8000
	s_addc_u32 s9, s9, 0
	global_load_dwordx4 v[180:183], v75, s[8:9]
	s_add_u32 s8, s8, 0x8000
	s_addc_u32 s9, s9, 0
	global_load_dwordx4 v[184:187], v75, s[8:9]
	s_add_u32 s8, s8, 0x8000
	s_addc_u32 s9, s9, 0
	global_load_dwordx4 v[188:191], v75, s[8:9]
	s_add_u32 s8, s8, 0x8000
	s_addc_u32 s9, s9, 0
	global_load_dwordx4 v[192:195], v75, s[8:9]
	s_add_u32 s8, s8, 0x8000
	s_addc_u32 s9, s9, 0
	global_load_dwordx4 v[196:199], v75, s[8:9]
	s_add_u32 s8, s8, 0x8000
	s_addc_u32 s9, s9, 0
	global_load_dwordx4 v[200:203], v75, s[8:9]
	s_add_u32 s8, s8, 0x8000
	s_addc_u32 s9, s9, 0
	global_load_dwordx4 v[204:207], v75, s[8:9]
	s_add_u32 s6, s44, 0x3000000
	s_addc_u32 s7, s45, 0
	ds_read_b32 v226, v212
	ds_read_b32 v227, v212 offset:512
	ds_read_b32 v228, v212 offset:1024
	ds_read_b32 v229, v212 offset:1536
	ds_read_b32 v230, v212 offset:2048
	ds_read_b32 v231, v212 offset:2560
	ds_read_b32 v232, v212 offset:3072
	ds_read_b32 v233, v212 offset:3584
	ds_read_b32 v234, v212 offset:4096
	ds_read_b32 v235, v212 offset:4608
	ds_read_b32 v236, v212 offset:5120
	ds_read_b32 v237, v212 offset:5632
	ds_read_b32 v238, v212 offset:6144
	ds_read_b32 v239, v212 offset:6656
	ds_read_b32 v240, v212 offset:7168
	ds_read_b32 v241, v212 offset:7680
	s_waitcnt lgkmcnt(0)
	v_max_f32_e32 v226, v226, v226
	v_max_f32_e32 v227, v227, v227
	v_max_f32_e32 v228, v228, v228
	v_max_f32_e32 v229, v229, v229
	v_max_f32_e32 v230, v230, v230
	v_max_f32_e32 v231, v231, v231
	v_max_f32_e32 v232, v232, v232
	v_max_f32_e32 v233, v233, v233
	v_max_f32_e32 v234, v234, v234
	v_max_f32_e32 v235, v235, v235
	v_max_f32_e32 v236, v236, v236
	v_max_f32_e32 v237, v237, v237
	v_max_f32_e32 v238, v238, v238
	v_max_f32_e32 v239, v239, v239
	v_max_f32_e32 v240, v240, v240
	v_max_f32_e32 v241, v241, v241
	v_med3_f32 v226, v226, s62, v95
	v_med3_f32 v227, v227, s62, v95
	v_med3_f32 v228, v228, s62, v95
	v_med3_f32 v229, v229, s62, v95
	v_med3_f32 v230, v230, s62, v95
	v_med3_f32 v231, v231, s62, v95
	v_med3_f32 v232, v232, s62, v95
	v_med3_f32 v233, v233, s62, v95
	v_med3_f32 v234, v234, s62, v95
	v_med3_f32 v235, v235, s62, v95
	v_med3_f32 v236, v236, s62, v95
	v_med3_f32 v237, v237, s62, v95
	v_med3_f32 v238, v238, s62, v95
	v_med3_f32 v239, v239, s62, v95
	v_med3_f32 v240, v240, s62, v95
	v_med3_f32 v241, v241, s62, v95
	v_mov_b32_e32 v242, 0
	v_mov_b32_e32 v243, 0
	v_mov_b32_e32 v244, 0
	v_mov_b32_e32 v245, 0
	v_cvt_pk_fp8_f32 v242, v226, v227
	v_cvt_pk_fp8_f32 v243, v230, v231
	v_cvt_pk_fp8_f32 v244, v234, v235
	v_cvt_pk_fp8_f32 v245, v238, v239
	v_cvt_pk_fp8_f32 v242, v228, v229 op_sel:[0,0,1]
	v_cvt_pk_fp8_f32 v243, v232, v233 op_sel:[0,0,1]
	v_cvt_pk_fp8_f32 v244, v236, v237 op_sel:[0,0,1]
	v_cvt_pk_fp8_f32 v245, v240, v241 op_sel:[0,0,1]
	s_nop 0
	global_store_dwordx4 v79, v[242:245], s[6:7]
	ds_read_b32 v226, v214
	ds_read_b32 v227, v214 offset:512
	ds_read_b32 v228, v214 offset:1024
	ds_read_b32 v229, v214 offset:1536
	ds_read_b32 v230, v214 offset:2048
	ds_read_b32 v231, v214 offset:2560
	ds_read_b32 v232, v214 offset:3072
	ds_read_b32 v233, v214 offset:3584
	ds_read_b32 v234, v214 offset:4096
	ds_read_b32 v235, v214 offset:4608
	ds_read_b32 v236, v214 offset:5120
	ds_read_b32 v237, v214 offset:5632
	ds_read_b32 v238, v214 offset:6144
	ds_read_b32 v239, v214 offset:6656
	ds_read_b32 v240, v214 offset:7168
	ds_read_b32 v241, v214 offset:7680
	s_waitcnt lgkmcnt(0)
; #define GAS __attribute__((address_space(1)))
; #define LAS __attribute__((address_space(3)))
; #define LDS_WAIT() asm volatile("s_waitcnt lgkmcnt(0)" ::: "memory")
;     const int pr = item >> 1, kb = 2 * (pr / nblk) + (item & 1), nb = pr % nblk, k0 = 64 * kb, n0 = 32 * nb;
;     const int nr = n0 + (lane & 31); const int sc = MAP == 1 ? src_col_in(nr) : nr;
;     float v[32];
; #pragma unroll
;     for (int i = 0; i < 32; ++i) v[i] = sc >= 0 ? W[(size_t)(k0 + 2 * i + (lane >> 5)) * Nsrc + sc] : 0.f;
; #pragma unroll
;     for (int i = 0; i < 32; ++i) { const int k = k0 + 2 * i + (lane >> 5); float x = v[i] * wscale; if (KS) x *= (k < ksplit ? ksA[k] : ksB[k - ksplit]); scr[(2 * i + (lane >> 5)) * 33 + (lane & 31)] = x; }
;     LDS_WAIT(); asm volatile("" ::: "memory");
;     const int c = lane & 7;
; #pragma unroll
;     for (int j = 0; j < 4; ++j) { const int n = (lane >> 3) + 8 * j; const LAS float* s = scr + (8 * c) * 33 + n;
;         const unsigned long long o = (unsigned long long)pg8::pk4_fp8(s[0 * 33], s[1 * 33], s[2 * 33], s[3 * 33]) | ((unsigned long long)pg8::pk4_fp8(s[4 * 33], s[5 * 33], s[6 * 33], s[7 * 33]) << 32);
;         *(GAS unsigned long long*)(WT + (size_t)(n0 + n) * K + k0 + 8 * c) = o; }
;     LDS_WAIT(); asm volatile("" ::: "memory");
; }
; __global__ void __launch_bounds__(NWAVES * 64, 2) hybrid_fwd(Args args) {
;     ...
;             p0_transpose_item_f8<false>(args.in[16] + (size_t)l * FF * DM, FF, DM, DM / 32, (unsigned char*)(ws + WS_WDN + l * SZ_WDN), 128.f, args.in[16], args.in[16], 0, scr, r, lane);
	v_max_f32_e32 v226, v226, v226
	v_max_f32_e32 v227, v227, v227
	v_max_f32_e32 v228, v228, v228
	v_max_f32_e32 v229, v229, v229
	v_max_f32_e32 v230, v230, v230
	v_max_f32_e32 v231, v231, v231
	v_max_f32_e32 v232, v232, v232
	v_max_f32_e32 v233, v233, v233
	v_max_f32_e32 v234, v234, v234
	v_max_f32_e32 v235, v235, v235
	v_max_f32_e32 v236, v236, v236
	v_max_f32_e32 v237, v237, v237
	v_max_f32_e32 v238, v238, v238
	v_max_f32_e32 v239, v239, v239
	v_max_f32_e32 v240, v240, v240
	v_max_f32_e32 v241, v241, v241
	v_med3_f32 v226, v226, s62, v95
	v_med3_f32 v227, v227, s62, v95
	v_med3_f32 v228, v228, s62, v95
	v_med3_f32 v229, v229, s62, v95
	v_med3_f32 v230, v230, s62, v95
	v_med3_f32 v231, v231, s62, v95
	v_med3_f32 v232, v232, s62, v95
	v_med3_f32 v233, v233, s62, v95
	v_med3_f32 v234, v234, s62, v95
	v_med3_f32 v235, v235, s62, v95
	v_med3_f32 v236, v236, s62, v95
	v_med3_f32 v237, v237, s62, v95
	v_med3_f32 v238, v238, s62, v95
	v_med3_f32 v239, v239, s62, v95
	v_med3_f32 v240, v240, s62, v95
	v_med3_f32 v241, v241, s62, v95
	v_mov_b32_e32 v242, 0
	v_mov_b32_e32 v243, 0
	v_mov_b32_e32 v244, 0
	v_mov_b32_e32 v245, 0
	v_cvt_pk_fp8_f32 v242, v226, v227
	v_cvt_pk_fp8_f32 v243, v230, v231
	v_cvt_pk_fp8_f32 v244, v234, v235
	v_cvt_pk_fp8_f32 v245, v238, v239
	v_cvt_pk_fp8_f32 v242, v228, v229 op_sel:[0,0,1]
	v_cvt_pk_fp8_f32 v243, v232, v233 op_sel:[0,0,1]
	v_cvt_pk_fp8_f32 v244, v236, v237 op_sel:[0,0,1]
	v_cvt_pk_fp8_f32 v245, v240, v241 op_sel:[0,0,1]
	s_nop 0
	global_store_dwordx4 v80, v[242:245], s[6:7]
	s_waitcnt vmcnt(12)
	v_mul_f32_e32 v144, 0x43000000, v144
	v_mul_f32_e32 v145, 0x43000000, v145
	v_mul_f32_e32 v146, 0x43000000, v146
	v_mul_f32_e32 v147, 0x43000000, v147
	ds_write_b128 v209, v[144:147]
	v_mul_f32_e32 v148, 0x43000000, v148
	v_mul_f32_e32 v149, 0x43000000, v149
	v_mul_f32_e32 v150, 0x43000000, v150
	v_mul_f32_e32 v151, 0x43000000, v151
	ds_write_b128 v209, v[148:151] offset:1024
	v_mul_f32_e32 v152, 0x43000000, v152
	v_mul_f32_e32 v153, 0x43000000, v153
	v_mul_f32_e32 v154, 0x43000000, v154
	v_mul_f32_e32 v155, 0x43000000, v155
	ds_write_b128 v209, v[152:155] offset:2048
	v_mul_f32_e32 v156, 0x43000000, v156
	v_mul_f32_e32 v157, 0x43000000, v157
	v_mul_f32_e32 v158, 0x43000000, v158
	v_mul_f32_e32 v159, 0x43000000, v159
	ds_write_b128 v209, v[156:159] offset:3072
	v_mul_f32_e32 v160, 0x43000000, v160
	v_mul_f32_e32 v161, 0x43000000, v161
	v_mul_f32_e32 v162, 0x43000000, v162
	v_mul_f32_e32 v163, 0x43000000, v163
	ds_write_b128 v209, v[160:163] offset:4096
	v_mul_f32_e32 v164, 0x43000000, v164
	v_mul_f32_e32 v165, 0x43000000, v165
	v_mul_f32_e32 v166, 0x43000000, v166
	v_mul_f32_e32 v167, 0x43000000, v167
	ds_write_b128 v209, v[164:167] offset:5120
	v_mul_f32_e32 v168, 0x43000000, v168
	v_mul_f32_e32 v169, 0x43000000, v169
	v_mul_f32_e32 v170, 0x43000000, v170
	v_mul_f32_e32 v171, 0x43000000, v171
	ds_write_b128 v209, v[168:171] offset:6144
	v_mul_f32_e32 v172, 0x43000000, v172
	v_mul_f32_e32 v173, 0x43000000, v173
	v_mul_f32_e32 v174, 0x43000000, v174
	v_mul_f32_e32 v175, 0x43000000, v175
	ds_write_b128 v209, v[172:175] offset:7168
	s_waitcnt lgkmcnt(0)
	s_barrier
	s_add_u32 s8, s42, 0x4002000
	s_addc_u32 s9, s43, 0
	global_load_dwordx4 v[144:147], v75, s[8:9]
	s_add_u32 s8, s8, 0x8000
	s_addc_u32 s9, s9, 0
	global_load_dwordx4 v[148:151], v75, s[8:9]
	s_add_u32 s8, s8, 0x8000
	s_addc_u32 s9, s9, 0
	global_load_dwordx4 v[152:155], v75, s[8:9]
	s_add_u32 s8, s8, 0x8000
	s_addc_u32 s9, s9, 0
	global_load_dwordx4 v[156:159], v75, s[8:9]
	s_add_u32 s8, s8, 0x8000
	s_addc_u32 s9, s9, 0
	global_load_dwordx4 v[160:163], v75, s[8:9]
	s_add_u32 s8, s8, 0x8000
	s_addc_u32 s9, s9, 0
	global_load_dwordx4 v[164:167], v75, s[8:9]
	s_add_u32 s8, s8, 0x8000
	s_addc_u32 s9, s9, 0
	global_load_dwordx4 v[168:171], v75, s[8:9]
	s_add_u32 s8, s8, 0x8000
	s_addc_u32 s9, s9, 0
	global_load_dwordx4 v[172:175], v75, s[8:9]
	s_add_u32 s6, s44, 0x1000
	s_addc_u32 s7, s45, 0
	ds_read_b32 v226, v211
	ds_read_b32 v227, v211 offset:512
	ds_read_b32 v228, v211 offset:1024
	ds_read_b32 v229, v211 offset:1536
	ds_read_b32 v230, v211 offset:2048
	ds_read_b32 v231, v211 offset:2560
	ds_read_b32 v232, v211 offset:3072
	ds_read_b32 v233, v211 offset:3584
	ds_read_b32 v234, v211 offset:4096
	ds_read_b32 v235, v211 offset:4608
	ds_read_b32 v236, v211 offset:5120
	ds_read_b32 v237, v211 offset:5632
	ds_read_b32 v238, v211 offset:6144
	ds_read_b32 v239, v211 offset:6656
	ds_read_b32 v240, v211 offset:7168
	ds_read_b32 v241, v211 offset:7680
	s_waitcnt lgkmcnt(0)
	v_max_f32_e32 v226, v226, v226
	v_max_f32_e32 v227, v227, v227
	v_max_f32_e32 v228, v228, v228
	v_max_f32_e32 v229, v229, v229
	v_max_f32_e32 v230, v230, v230
	v_max_f32_e32 v231, v231, v231
	v_max_f32_e32 v232, v232, v232
	v_max_f32_e32 v233, v233, v233
	v_max_f32_e32 v234, v234, v234
	v_max_f32_e32 v235, v235, v235
	v_max_f32_e32 v236, v236, v236
	v_max_f32_e32 v237, v237, v237
	v_max_f32_e32 v238, v238, v238
	v_max_f32_e32 v239, v239, v239
	v_max_f32_e32 v240, v240, v240
	v_max_f32_e32 v241, v241, v241
	v_med3_f32 v226, v226, s62, v95
	v_med3_f32 v227, v227, s62, v95
	v_med3_f32 v228, v228, s62, v95
	v_med3_f32 v229, v229, s62, v95
	v_med3_f32 v230, v230, s62, v95
	v_med3_f32 v231, v231, s62, v95
	v_med3_f32 v232, v232, s62, v95
	v_med3_f32 v233, v233, s62, v95
	v_med3_f32 v234, v234, s62, v95
	v_med3_f32 v235, v235, s62, v95
	v_med3_f32 v236, v236, s62, v95
	v_med3_f32 v237, v237, s62, v95
	v_med3_f32 v238, v238, s62, v95
	v_med3_f32 v239, v239, s62, v95
	v_med3_f32 v240, v240, s62, v95
	v_med3_f32 v241, v241, s62, v95
	v_mov_b32_e32 v242, 0
	v_mov_b32_e32 v243, 0
	v_mov_b32_e32 v244, 0
	v_mov_b32_e32 v245, 0
	v_cvt_pk_fp8_f32 v242, v226, v227
	v_cvt_pk_fp8_f32 v243, v230, v231
	v_cvt_pk_fp8_f32 v244, v234, v235
	v_cvt_pk_fp8_f32 v245, v238, v239
	v_cvt_pk_fp8_f32 v242, v228, v229 op_sel:[0,0,1]
	v_cvt_pk_fp8_f32 v243, v232, v233 op_sel:[0,0,1]
	v_cvt_pk_fp8_f32 v244, v236, v237 op_sel:[0,0,1]
	v_cvt_pk_fp8_f32 v245, v240, v241 op_sel:[0,0,1]
	s_nop 0
	global_store_dwordx4 v79, v[242:245], s[6:7]
	ds_read_b32 v226, v213
	ds_read_b32 v227, v213 offset:512
	ds_read_b32 v228, v213 offset:1024
	ds_read_b32 v229, v213 offset:1536
	ds_read_b32 v230, v213 offset:2048
	ds_read_b32 v231, v213 offset:2560
	ds_read_b32 v232, v213 offset:3072
	ds_read_b32 v233, v213 offset:3584
	ds_read_b32 v234, v213 offset:4096
	ds_read_b32 v235, v213 offset:4608
	ds_read_b32 v236, v213 offset:5120
	ds_read_b32 v237, v213 offset:5632
	ds_read_b32 v238, v213 offset:6144
	ds_read_b32 v239, v213 offset:6656
	ds_read_b32 v240, v213 offset:7168
	ds_read_b32 v241, v213 offset:7680
	s_waitcnt lgkmcnt(0)
; #define GAS __attribute__((address_space(1)))
; #define LAS __attribute__((address_space(3)))
; #define LDS_WAIT() asm volatile("s_waitcnt lgkmcnt(0)" ::: "memory")
;     const int pr = item >> 1, kb = 2 * (pr / nblk) + (item & 1), nb = pr % nblk, k0 = 64 * kb, n0 = 32 * nb;
;     const int nr = n0 + (lane & 31); const int sc = MAP == 1 ? src_col_in(nr) : nr;
;     float v[32];
; #pragma unroll
;     for (int i = 0; i < 32; ++i) v[i] = sc >= 0 ? W[(size_t)(k0 + 2 * i + (lane >> 5)) * Nsrc + sc] : 0.f;
; #pragma unroll
;     for (int i = 0; i < 32; ++i) { const int k = k0 + 2 * i + (lane >> 5); float x = v[i] * wscale; if (KS) x *= (k < ksplit ? ksA[k] : ksB[k - ksplit]); scr[(2 * i + (lane >> 5)) * 33 + (lane & 31)] = x; }
;     LDS_WAIT(); asm volatile("" ::: "memory");
;     const int c = lane & 7;
; #pragma unroll
;     for (int j = 0; j < 4; ++j) { const int n = (lane >> 3) + 8 * j; const LAS float* s = scr + (8 * c) * 33 + n;
;         const unsigned long long o = (unsigned long long)pg8::pk4_fp8(s[0 * 33], s[1 * 33], s[2 * 33], s[3 * 33]) | ((unsigned long long)pg8::pk4_fp8(s[4 * 33], s[5 * 33], s[6 * 33], s[7 * 33]) << 32);
;         *(GAS unsigned long long*)(WT + (size_t)(n0 + n) * K + k0 + 8 * c) = o; }
;     LDS_WAIT(); asm volatile("" ::: "memory");
; }
; __global__ void __launch_bounds__(NWAVES * 64, 2) hybrid_fwd(Args args) {
;     ...
;             p0_transpose_item_f8<false>(args.in[16] + (size_t)l * FF * DM, FF, DM, DM / 32, (unsigned char*)(ws + WS_WDN + l * SZ_WDN), 128.f, args.in[16], args.in[16], 0, scr, r, lane);
	v_max_f32_e32 v226, v226, v226
	v_max_f32_e32 v227, v227, v227
	v_max_f32_e32 v228, v228, v228
	v_max_f32_e32 v229, v229, v229
	v_max_f32_e32 v230, v230, v230
	v_max_f32_e32 v231, v231, v231
	v_max_f32_e32 v232, v232, v232
	v_max_f32_e32 v233, v233, v233
	v_max_f32_e32 v234, v234, v234
	v_max_f32_e32 v235, v235, v235
	v_max_f32_e32 v236, v236, v236
	v_max_f32_e32 v237, v237, v237
	v_max_f32_e32 v238, v238, v238
	v_max_f32_e32 v239, v239, v239
	v_max_f32_e32 v240, v240, v240
	v_max_f32_e32 v241, v241, v241
	v_med3_f32 v226, v226, s62, v95
	v_med3_f32 v227, v227, s62, v95
	v_med3_f32 v228, v228, s62, v95
	v_med3_f32 v229, v229, s62, v95
	v_med3_f32 v230, v230, s62, v95
	v_med3_f32 v231, v231, s62, v95
	v_med3_f32 v232, v232, s62, v95
	v_med3_f32 v233, v233, s62, v95
	v_med3_f32 v234, v234, s62, v95
	v_med3_f32 v235, v235, s62, v95
	v_med3_f32 v236, v236, s62, v95
	v_med3_f32 v237, v237, s62, v95
	v_med3_f32 v238, v238, s62, v95
	v_med3_f32 v239, v239, s62, v95
	v_med3_f32 v240, v240, s62, v95
	v_med3_f32 v241, v241, s62, v95
	v_mov_b32_e32 v242, 0
	v_mov_b32_e32 v243, 0
	v_mov_b32_e32 v244, 0
	v_mov_b32_e32 v245, 0
	v_cvt_pk_fp8_f32 v242, v226, v227
	v_cvt_pk_fp8_f32 v243, v230, v231
	v_cvt_pk_fp8_f32 v244, v234, v235
	v_cvt_pk_fp8_f32 v245, v238, v239
	v_cvt_pk_fp8_f32 v242, v228, v229 op_sel:[0,0,1]
	v_cvt_pk_fp8_f32 v243, v232, v233 op_sel:[0,0,1]
	v_cvt_pk_fp8_f32 v244, v236, v237 op_sel:[0,0,1]
	v_cvt_pk_fp8_f32 v245, v240, v241 op_sel:[0,0,1]
	s_nop 0
	global_store_dwordx4 v80, v[242:245], s[6:7]
	s_waitcnt vmcnt(12)
	v_mul_f32_e32 v176, 0x43000000, v176
	v_mul_f32_e32 v177, 0x43000000, v177
	v_mul_f32_e32 v178, 0x43000000, v178
	v_mul_f32_e32 v179, 0x43000000, v179
	ds_write_b128 v210, v[176:179]
	v_mul_f32_e32 v180, 0x43000000, v180
	v_mul_f32_e32 v181, 0x43000000, v181
	v_mul_f32_e32 v182, 0x43000000, v182
	v_mul_f32_e32 v183, 0x43000000, v183
	ds_write_b128 v210, v[180:183] offset:1024
	v_mul_f32_e32 v184, 0x43000000, v184
	v_mul_f32_e32 v185, 0x43000000, v185
	v_mul_f32_e32 v186, 0x43000000, v186
	v_mul_f32_e32 v187, 0x43000000, v187
	ds_write_b128 v210, v[184:187] offset:2048
	v_mul_f32_e32 v188, 0x43000000, v188
	v_mul_f32_e32 v189, 0x43000000, v189
	v_mul_f32_e32 v190, 0x43000000, v190
	v_mul_f32_e32 v191, 0x43000000, v191
	ds_write_b128 v210, v[188:191] offset:3072
	v_mul_f32_e32 v192, 0x43000000, v192
	v_mul_f32_e32 v193, 0x43000000, v193
	v_mul_f32_e32 v194, 0x43000000, v194
	v_mul_f32_e32 v195, 0x43000000, v195
	ds_write_b128 v210, v[192:195] offset:4096
	v_mul_f32_e32 v196, 0x43000000, v196
	v_mul_f32_e32 v197, 0x43000000, v197
	v_mul_f32_e32 v198, 0x43000000, v198
	v_mul_f32_e32 v199, 0x43000000, v199
	ds_write_b128 v210, v[196:199] offset:5120
	v_mul_f32_e32 v200, 0x43000000, v200
	v_mul_f32_e32 v201, 0x43000000, v201
	v_mul_f32_e32 v202, 0x43000000, v202
	v_mul_f32_e32 v203, 0x43000000, v203
	ds_write_b128 v210, v[200:203] offset:6144
	v_mul_f32_e32 v204, 0x43000000, v204
	v_mul_f32_e32 v205, 0x43000000, v205
	v_mul_f32_e32 v206, 0x43000000, v206
	v_mul_f32_e32 v207, 0x43000000, v207
	ds_write_b128 v210, v[204:207] offset:7168
	s_waitcnt lgkmcnt(0)
	s_barrier
	s_add_u32 s8, s42, 0x4003000
	s_addc_u32 s9, s43, 0
	global_load_dwordx4 v[176:179], v75, s[8:9]
	s_add_u32 s8, s8, 0x8000
	s_addc_u32 s9, s9, 0
	global_load_dwordx4 v[180:183], v75, s[8:9]
	s_add_u32 s8, s8, 0x8000
	s_addc_u32 s9, s9, 0
	global_load_dwordx4 v[184:187], v75, s[8:9]
	s_add_u32 s8, s8, 0x8000
	s_addc_u32 s9, s9, 0
	global_load_dwordx4 v[188:191], v75, s[8:9]
	s_add_u32 s8, s8, 0x8000
	s_addc_u32 s9, s9, 0
	global_load_dwordx4 v[192:195], v75, s[8:9]
	s_add_u32 s8, s8, 0x8000
	s_addc_u32 s9, s9, 0
	global_load_dwordx4 v[196:199], v75, s[8:9]
	s_add_u32 s8, s8, 0x8000
	s_addc_u32 s9, s9, 0
	global_load_dwordx4 v[200:203], v75, s[8:9]
	s_add_u32 s8, s8, 0x8000
	s_addc_u32 s9, s9, 0
	global_load_dwordx4 v[204:207], v75, s[8:9]
	s_add_u32 s6, s44, 0x1001000
	s_addc_u32 s7, s45, 0
	ds_read_b32 v226, v212
	ds_read_b32 v227, v212 offset:512
	ds_read_b32 v228, v212 offset:1024
	ds_read_b32 v229, v212 offset:1536
	ds_read_b32 v230, v212 offset:2048
	ds_read_b32 v231, v212 offset:2560
	ds_read_b32 v232, v212 offset:3072
	ds_read_b32 v233, v212 offset:3584
	ds_read_b32 v234, v212 offset:4096
	ds_read_b32 v235, v212 offset:4608
	ds_read_b32 v236, v212 offset:5120
	ds_read_b32 v237, v212 offset:5632
	ds_read_b32 v238, v212 offset:6144
	ds_read_b32 v239, v212 offset:6656
	ds_read_b32 v240, v212 offset:7168
	ds_read_b32 v241, v212 offset:7680
	s_waitcnt lgkmcnt(0)
	v_max_f32_e32 v226, v226, v226
	v_max_f32_e32 v227, v227, v227
	v_max_f32_e32 v228, v228, v228
	v_max_f32_e32 v229, v229, v229
	v_max_f32_e32 v230, v230, v230
	v_max_f32_e32 v231, v231, v231
	v_max_f32_e32 v232, v232, v232
	v_max_f32_e32 v233, v233, v233
	v_max_f32_e32 v234, v234, v234
	v_max_f32_e32 v235, v235, v235
	v_max_f32_e32 v236, v236, v236
	v_max_f32_e32 v237, v237, v237
	v_max_f32_e32 v238, v238, v238
	v_max_f32_e32 v239, v239, v239
	v_max_f32_e32 v240, v240, v240
	v_max_f32_e32 v241, v241, v241
	v_med3_f32 v226, v226, s62, v95
	v_med3_f32 v227, v227, s62, v95
	v_med3_f32 v228, v228, s62, v95
	v_med3_f32 v229, v229, s62, v95
	v_med3_f32 v230, v230, s62, v95
	v_med3_f32 v231, v231, s62, v95
	v_med3_f32 v232, v232, s62, v95
	v_med3_f32 v233, v233, s62, v95
	v_med3_f32 v234, v234, s62, v95
	v_med3_f32 v235, v235, s62, v95
	v_med3_f32 v236, v236, s62, v95
	v_med3_f32 v237, v237, s62, v95
	v_med3_f32 v238, v238, s62, v95
	v_med3_f32 v239, v239, s62, v95
	v_med3_f32 v240, v240, s62, v95
	v_med3_f32 v241, v241, s62, v95
	v_mov_b32_e32 v242, 0
	v_mov_b32_e32 v243, 0
	v_mov_b32_e32 v244, 0
	v_mov_b32_e32 v245, 0
	v_cvt_pk_fp8_f32 v242, v226, v227
	v_cvt_pk_fp8_f32 v243, v230, v231
	v_cvt_pk_fp8_f32 v244, v234, v235
	v_cvt_pk_fp8_f32 v245, v238, v239
	v_cvt_pk_fp8_f32 v242, v228, v229 op_sel:[0,0,1]
	v_cvt_pk_fp8_f32 v243, v232, v233 op_sel:[0,0,1]
	v_cvt_pk_fp8_f32 v244, v236, v237 op_sel:[0,0,1]
	v_cvt_pk_fp8_f32 v245, v240, v241 op_sel:[0,0,1]
	s_nop 0
	global_store_dwordx4 v79, v[242:245], s[6:7]
	ds_read_b32 v226, v214
	ds_read_b32 v227, v214 offset:512
	ds_read_b32 v228, v214 offset:1024
	ds_read_b32 v229, v214 offset:1536
	ds_read_b32 v230, v214 offset:2048
	ds_read_b32 v231, v214 offset:2560
	ds_read_b32 v232, v214 offset:3072
	ds_read_b32 v233, v214 offset:3584
	ds_read_b32 v234, v214 offset:4096
	ds_read_b32 v235, v214 offset:4608
	ds_read_b32 v236, v214 offset:5120
	ds_read_b32 v237, v214 offset:5632
	ds_read_b32 v238, v214 offset:6144
	ds_read_b32 v239, v214 offset:6656
	ds_read_b32 v240, v214 offset:7168
	ds_read_b32 v241, v214 offset:7680
	s_waitcnt lgkmcnt(0)
; template <int MAP, bool KS, bool KPERM = false>
; __device__ __forceinline__ void p0_transpose_item(const float* W, int K, int Nsrc, int nblk, bf16* WT, const float* ksA, const float* ksB, int ksplit, LAS float* scr, int item, int lane) {
;     const int kb = item / nblk, nb = item % nblk, k0 = 64 * kb, n0 = 32 * nb;
;     const int nr = n0 + (lane & 31); const int sc = MAP == 1 ? src_col_in(nr) : (MAP == 2 ? nat_dim(nr) : nr);
;     float v[32];
; #pragma unroll
;     for (int i = 0; i < 32; ++i) { const int k = k0 + 2 * i + (lane >> 5); const int ksrc = KPERM ? ((k & ~127) + nat_dim(k & 127)) : k;
;         v[i] = sc >= 0 ? W[(size_t)ksrc * Nsrc + sc] : 0.f; }
; #pragma unroll
;     for (int i = 0; i < 32; ++i) { const int kk = 2 * i + (lane >> 5); const int k = k0 + kk;
;         if (KS) v[i] *= (k < ksplit ? ksA[k] : ksB[k - ksplit]);
;         scr[kk * 33 + (lane & 31)] = v[i]; }
;     LDS_WAIT(); asm volatile("" ::: "memory");
;     const int c = lane & 7;
; #pragma unroll
;     const int pr = item >> 1, kb = 2 * (pr / nblk) + (item & 1), nb = pr % nblk, k0 = 64 * kb, n0 = 32 * nb;
;     const int nr = n0 + (lane & 31); const int sc = MAP == 1 ? src_col_in(nr) : nr;
;     float v[32];
; #pragma unroll
;     for (int i = 0; i < 32; ++i) v[i] = sc >= 0 ? W[(size_t)(k0 + 2 * i + (lane >> 5)) * Nsrc + sc] : 0.f;
; #pragma unroll
;     for (int i = 0; i < 32; ++i) { const int k = k0 + 2 * i + (lane >> 5); float x = v[i] * wscale; if (KS) x *= (k < ksplit ? ksA[k] : ksB[k - ksplit]); scr[(2 * i + (lane >> 5)) * 33 + (lane & 31)] = x; }
;     LDS_WAIT(); asm volatile("" ::: "memory");
;     const int c = lane & 7;
; #pragma unroll
;     for (int j = 0; j < 4; ++j) { const int n = (lane >> 3) + 8 * j; const LAS float* s = scr + (8 * c) * 33 + n;
;         const unsigned long long o = (unsigned long long)pg8::pk4_fp8(s[0 * 33], s[1 * 33], s[2 * 33], s[3 * 33]) | ((unsigned long long)pg8::pk4_fp8(s[4 * 33], s[5 * 33], s[6 * 33], s[7 * 33]) << 32);
;         *(GAS unsigned long long*)(WT + (size_t)(n0 + n) * K + k0 + 8 * c) = o; }
;     LDS_WAIT(); asm volatile("" ::: "memory");
; }
; __global__ void __launch_bounds__(NWAVES * 64, 2) hybrid_fwd(Args args) {
;     ...
;             p0_transpose_item_f8<false>(args.in[16] + (size_t)l * FF * DM, FF, DM, DM / 32, (unsigned char*)(ws + WS_WDN + l * SZ_WDN), 128.f, args.in[16], args.in[16], 0, scr, r, lane);
	v_max_f32_e32 v226, v226, v226
	v_max_f32_e32 v227, v227, v227
	v_max_f32_e32 v228, v228, v228
	v_max_f32_e32 v229, v229, v229
	v_max_f32_e32 v230, v230, v230
	v_max_f32_e32 v231, v231, v231
	v_max_f32_e32 v232, v232, v232
	v_max_f32_e32 v233, v233, v233
	v_max_f32_e32 v234, v234, v234
	v_max_f32_e32 v235, v235, v235
	v_max_f32_e32 v236, v236, v236
	v_max_f32_e32 v237, v237, v237
	v_max_f32_e32 v238, v238, v238
	v_max_f32_e32 v239, v239, v239
	v_max_f32_e32 v240, v240, v240
	v_max_f32_e32 v241, v241, v241
	v_med3_f32 v226, v226, s62, v95
	v_med3_f32 v227, v227, s62, v95
	v_med3_f32 v228, v228, s62, v95
	v_med3_f32 v229, v229, s62, v95
	v_med3_f32 v230, v230, s62, v95
	v_med3_f32 v231, v231, s62, v95
	v_med3_f32 v232, v232, s62, v95
	v_med3_f32 v233, v233, s62, v95
	v_med3_f32 v234, v234, s62, v95
	v_med3_f32 v235, v235, s62, v95
	v_med3_f32 v236, v236, s62, v95
	v_med3_f32 v237, v237, s62, v95
	v_med3_f32 v238, v238, s62, v95
	v_med3_f32 v239, v239, s62, v95
	v_med3_f32 v240, v240, s62, v95
	v_med3_f32 v241, v241, s62, v95
	v_mov_b32_e32 v242, 0
	v_mov_b32_e32 v243, 0
	v_mov_b32_e32 v244, 0
	v_mov_b32_e32 v245, 0
	v_cvt_pk_fp8_f32 v242, v226, v227
	v_cvt_pk_fp8_f32 v243, v230, v231
	v_cvt_pk_fp8_f32 v244, v234, v235
	v_cvt_pk_fp8_f32 v245, v238, v239
	v_cvt_pk_fp8_f32 v242, v228, v229 op_sel:[0,0,1]
	v_cvt_pk_fp8_f32 v243, v232, v233 op_sel:[0,0,1]
	v_cvt_pk_fp8_f32 v244, v236, v237 op_sel:[0,0,1]
	v_cvt_pk_fp8_f32 v245, v240, v241 op_sel:[0,0,1]
	s_nop 0
	global_store_dwordx4 v80, v[242:245], s[6:7]
	s_waitcnt vmcnt(12)
	v_mul_f32_e32 v144, 0x43000000, v144
	v_mul_f32_e32 v145, 0x43000000, v145
	v_mul_f32_e32 v146, 0x43000000, v146
	v_mul_f32_e32 v147, 0x43000000, v147
	ds_write_b128 v209, v[144:147]
	v_mul_f32_e32 v148, 0x43000000, v148
	v_mul_f32_e32 v149, 0x43000000, v149
	v_mul_f32_e32 v150, 0x43000000, v150
	v_mul_f32_e32 v151, 0x43000000, v151
	ds_write_b128 v209, v[148:151] offset:1024
	v_mul_f32_e32 v152, 0x43000000, v152
	v_mul_f32_e32 v153, 0x43000000, v153
	v_mul_f32_e32 v154, 0x43000000, v154
	v_mul_f32_e32 v155, 0x43000000, v155
	ds_write_b128 v209, v[152:155] offset:2048
	v_mul_f32_e32 v156, 0x43000000, v156
	v_mul_f32_e32 v157, 0x43000000, v157
	v_mul_f32_e32 v158, 0x43000000, v158
	v_mul_f32_e32 v159, 0x43000000, v159
	ds_write_b128 v209, v[156:159] offset:3072
	v_mul_f32_e32 v160, 0x43000000, v160
	v_mul_f32_e32 v161, 0x43000000, v161
	v_mul_f32_e32 v162, 0x43000000, v162
	v_mul_f32_e32 v163, 0x43000000, v163
	ds_write_b128 v209, v[160:163] offset:4096
	v_mul_f32_e32 v164, 0x43000000, v164
	v_mul_f32_e32 v165, 0x43000000, v165
	v_mul_f32_e32 v166, 0x43000000, v166
	v_mul_f32_e32 v167, 0x43000000, v167
	ds_write_b128 v209, v[164:167] offset:5120
	v_mul_f32_e32 v168, 0x43000000, v168
	v_mul_f32_e32 v169, 0x43000000, v169
	v_mul_f32_e32 v170, 0x43000000, v170
	v_mul_f32_e32 v171, 0x43000000, v171
	ds_write_b128 v209, v[168:171] offset:6144
	v_mul_f32_e32 v172, 0x43000000, v172
	v_mul_f32_e32 v173, 0x43000000, v173
	v_mul_f32_e32 v174, 0x43000000, v174
	v_mul_f32_e32 v175, 0x43000000, v175
	ds_write_b128 v209, v[172:175] offset:7168
	s_waitcnt lgkmcnt(0)
	s_barrier
	s_add_i32 s24, s23, 0
	s_lshl_b32 s20, s24, 7
	s_cmp_lt_u32 s24, 40
	s_cselect_b32 s21, 0, 0x830
	s_cmp_lt_u32 s24, 72
	s_cselect_b32 s21, s21, 0xfffff030
	s_add_i32 s20, s20, s21
	s_lshl_b32 s20, s20, 2
	s_add_u32 s8, s46, s20
	s_addc_u32 s9, s47, 0
	global_load_dwordx4 v[144:147], v76, s[8:9]
	s_add_u32 s8, s8, 0x16280
	s_addc_u32 s9, s9, 0
	global_load_dwordx4 v[148:151], v76, s[8:9]
	s_add_u32 s8, s8, 0x16280
	s_addc_u32 s9, s9, 0
	global_load_dwordx4 v[152:155], v76, s[8:9]
	s_add_u32 s8, s8, 0x16280
	s_addc_u32 s9, s9, 0
	global_load_dwordx4 v[156:159], v76, s[8:9]
	s_add_u32 s8, s8, 0x16280
	s_addc_u32 s9, s9, 0
	global_load_dwordx4 v[160:163], v76, s[8:9]
	s_add_u32 s8, s8, 0x16280
	s_addc_u32 s9, s9, 0
	global_load_dwordx4 v[164:167], v76, s[8:9]
	s_add_u32 s8, s8, 0x16280
	s_addc_u32 s9, s9, 0
	global_load_dwordx4 v[168:171], v76, s[8:9]
	s_add_u32 s8, s8, 0x16280
	s_addc_u32 s9, s9, 0
	global_load_dwordx4 v[172:175], v76, s[8:9]
	s_add_u32 s6, s44, 0x2001000
	s_addc_u32 s7, s45, 0
	ds_read_b32 v226, v211
	ds_read_b32 v227, v211 offset:512
	ds_read_b32 v228, v211 offset:1024
	ds_read_b32 v229, v211 offset:1536
	ds_read_b32 v230, v211 offset:2048
	ds_read_b32 v231, v211 offset:2560
	ds_read_b32 v232, v211 offset:3072
	ds_read_b32 v233, v211 offset:3584
	ds_read_b32 v234, v211 offset:4096
	ds_read_b32 v235, v211 offset:4608
	ds_read_b32 v236, v211 offset:5120
	ds_read_b32 v237, v211 offset:5632
	ds_read_b32 v238, v211 offset:6144
	ds_read_b32 v239, v211 offset:6656
	ds_read_b32 v240, v211 offset:7168
	ds_read_b32 v241, v211 offset:7680
	s_waitcnt lgkmcnt(0)
; #define GAS __attribute__((address_space(1)))
; #define LAS __attribute__((address_space(3)))
; #define LDS_WAIT() asm volatile("s_waitcnt lgkmcnt(0)" ::: "memory")
;     const int pr = item >> 1, kb = 2 * (pr / nblk) + (item & 1), nb = pr % nblk, k0 = 64 * kb, n0 = 32 * nb;
;     const int nr = n0 + (lane & 31); const int sc = MAP == 1 ? src_col_in(nr) : nr;
;     float v[32];
; #pragma unroll
;     for (int i = 0; i < 32; ++i) v[i] = sc >= 0 ? W[(size_t)(k0 + 2 * i + (lane >> 5)) * Nsrc + sc] : 0.f;
; #pragma unroll
;     for (int i = 0; i < 32; ++i) { const int k = k0 + 2 * i + (lane >> 5); float x = v[i] * wscale; if (KS) x *= (k < ksplit ? ksA[k] : ksB[k - ksplit]); scr[(2 * i + (lane >> 5)) * 33 + (lane & 31)] = x; }
;     LDS_WAIT(); asm volatile("" ::: "memory");
;     const int c = lane & 7;
; #pragma unroll
;     for (int j = 0; j < 4; ++j) { const int n = (lane >> 3) + 8 * j; const LAS float* s = scr + (8 * c) * 33 + n;
;         const unsigned long long o = (unsigned long long)pg8::pk4_fp8(s[0 * 33], s[1 * 33], s[2 * 33], s[3 * 33]) | ((unsigned long long)pg8::pk4_fp8(s[4 * 33], s[5 * 33], s[6 * 33], s[7 * 33]) << 32);
;         *(GAS unsigned long long*)(WT + (size_t)(n0 + n) * K + k0 + 8 * c) = o; }
;     LDS_WAIT(); asm volatile("" ::: "memory");
; }
; __global__ void __launch_bounds__(NWAVES * 64, 2) hybrid_fwd(Args args) {
;     ...
;             p0_transpose_item_f8<false>(args.in[16] + (size_t)l * FF * DM, FF, DM, DM / 32, (unsigned char*)(ws + WS_WDN + l * SZ_WDN), 128.f, args.in[16], args.in[16], 0, scr, r, lane);
	v_max_f32_e32 v226, v226, v226
	v_max_f32_e32 v227, v227, v227
	v_max_f32_e32 v228, v228, v228
	v_max_f32_e32 v229, v229, v229
	v_max_f32_e32 v230, v230, v230
	v_max_f32_e32 v231, v231, v231
	v_max_f32_e32 v232, v232, v232
	v_max_f32_e32 v233, v233, v233
	v_max_f32_e32 v234, v234, v234
	v_max_f32_e32 v235, v235, v235
	v_max_f32_e32 v236, v236, v236
	v_max_f32_e32 v237, v237, v237
	v_max_f32_e32 v238, v238, v238
	v_max_f32_e32 v239, v239, v239
	v_max_f32_e32 v240, v240, v240
	v_max_f32_e32 v241, v241, v241
	v_med3_f32 v226, v226, s62, v95
	v_med3_f32 v227, v227, s62, v95
	v_med3_f32 v228, v228, s62, v95
	v_med3_f32 v229, v229, s62, v95
	v_med3_f32 v230, v230, s62, v95
	v_med3_f32 v231, v231, s62, v95
	v_med3_f32 v232, v232, s62, v95
	v_med3_f32 v233, v233, s62, v95
	v_med3_f32 v234, v234, s62, v95
	v_med3_f32 v235, v235, s62, v95
	v_med3_f32 v236, v236, s62, v95
	v_med3_f32 v237, v237, s62, v95
	v_med3_f32 v238, v238, s62, v95
	v_med3_f32 v239, v239, s62, v95
	v_med3_f32 v240, v240, s62, v95
	v_med3_f32 v241, v241, s62, v95
	v_mov_b32_e32 v242, 0
	v_mov_b32_e32 v243, 0
	v_mov_b32_e32 v244, 0
	v_mov_b32_e32 v245, 0
	v_cvt_pk_fp8_f32 v242, v226, v227
	v_cvt_pk_fp8_f32 v243, v230, v231
	v_cvt_pk_fp8_f32 v244, v234, v235
	v_cvt_pk_fp8_f32 v245, v238, v239
	v_cvt_pk_fp8_f32 v242, v228, v229 op_sel:[0,0,1]
	v_cvt_pk_fp8_f32 v243, v232, v233 op_sel:[0,0,1]
	v_cvt_pk_fp8_f32 v244, v236, v237 op_sel:[0,0,1]
	v_cvt_pk_fp8_f32 v245, v240, v241 op_sel:[0,0,1]
	s_nop 0
	global_store_dwordx4 v79, v[242:245], s[6:7]
	ds_read_b32 v226, v213
	ds_read_b32 v227, v213 offset:512
	ds_read_b32 v228, v213 offset:1024
	ds_read_b32 v229, v213 offset:1536
	ds_read_b32 v230, v213 offset:2048
	ds_read_b32 v231, v213 offset:2560
	ds_read_b32 v232, v213 offset:3072
	ds_read_b32 v233, v213 offset:3584
	ds_read_b32 v234, v213 offset:4096
	ds_read_b32 v235, v213 offset:4608
	ds_read_b32 v236, v213 offset:5120
	ds_read_b32 v237, v213 offset:5632
	ds_read_b32 v238, v213 offset:6144
	ds_read_b32 v239, v213 offset:6656
	ds_read_b32 v240, v213 offset:7168
	ds_read_b32 v241, v213 offset:7680
	s_waitcnt lgkmcnt(0)
	v_max_f32_e32 v226, v226, v226
	v_max_f32_e32 v227, v227, v227
	v_max_f32_e32 v228, v228, v228
	v_max_f32_e32 v229, v229, v229
	v_max_f32_e32 v230, v230, v230
	v_max_f32_e32 v231, v231, v231
	v_max_f32_e32 v232, v232, v232
	v_max_f32_e32 v233, v233, v233
	v_max_f32_e32 v234, v234, v234
	v_max_f32_e32 v235, v235, v235
	v_max_f32_e32 v236, v236, v236
	v_max_f32_e32 v237, v237, v237
	v_max_f32_e32 v238, v238, v238
	v_max_f32_e32 v239, v239, v239
	v_max_f32_e32 v240, v240, v240
	v_max_f32_e32 v241, v241, v241
	v_med3_f32 v226, v226, s62, v95
	v_med3_f32 v227, v227, s62, v95
	v_med3_f32 v228, v228, s62, v95
	v_med3_f32 v229, v229, s62, v95
	v_med3_f32 v230, v230, s62, v95
	v_med3_f32 v231, v231, s62, v95
	v_med3_f32 v232, v232, s62, v95
	v_med3_f32 v233, v233, s62, v95
	v_med3_f32 v234, v234, s62, v95
	v_med3_f32 v235, v235, s62, v95
	v_med3_f32 v236, v236, s62, v95
	v_med3_f32 v237, v237, s62, v95
	v_med3_f32 v238, v238, s62, v95
	v_med3_f32 v239, v239, s62, v95
	v_med3_f32 v240, v240, s62, v95
	v_med3_f32 v241, v241, s62, v95
	v_mov_b32_e32 v242, 0
	v_mov_b32_e32 v243, 0
	v_mov_b32_e32 v244, 0
	v_mov_b32_e32 v245, 0
	v_cvt_pk_fp8_f32 v242, v226, v227
	v_cvt_pk_fp8_f32 v243, v230, v231
	v_cvt_pk_fp8_f32 v244, v234, v235
	v_cvt_pk_fp8_f32 v245, v238, v239
	v_cvt_pk_fp8_f32 v242, v228, v229 op_sel:[0,0,1]
	v_cvt_pk_fp8_f32 v243, v232, v233 op_sel:[0,0,1]
	v_cvt_pk_fp8_f32 v244, v236, v237 op_sel:[0,0,1]
	v_cvt_pk_fp8_f32 v245, v240, v241 op_sel:[0,0,1]
	s_nop 0
	global_store_dwordx4 v80, v[242:245], s[6:7]
	s_waitcnt vmcnt(12)
	v_mul_f32_e32 v176, 0x43000000, v176
	v_mul_f32_e32 v177, 0x43000000, v177
	v_mul_f32_e32 v178, 0x43000000, v178
	v_mul_f32_e32 v179, 0x43000000, v179
	ds_write_b128 v210, v[176:179]
	v_mul_f32_e32 v180, 0x43000000, v180
	v_mul_f32_e32 v181, 0x43000000, v181
	v_mul_f32_e32 v182, 0x43000000, v182
	v_mul_f32_e32 v183, 0x43000000, v183
	ds_write_b128 v210, v[180:183] offset:1024
	v_mul_f32_e32 v184, 0x43000000, v184
	v_mul_f32_e32 v185, 0x43000000, v185
	v_mul_f32_e32 v186, 0x43000000, v186
	v_mul_f32_e32 v187, 0x43000000, v187
	ds_write_b128 v210, v[184:187] offset:2048
	v_mul_f32_e32 v188, 0x43000000, v188
	v_mul_f32_e32 v189, 0x43000000, v189
	v_mul_f32_e32 v190, 0x43000000, v190
	v_mul_f32_e32 v191, 0x43000000, v191
	ds_write_b128 v210, v[188:191] offset:3072
	v_mul_f32_e32 v192, 0x43000000, v192
	v_mul_f32_e32 v193, 0x43000000, v193
	v_mul_f32_e32 v194, 0x43000000, v194
	v_mul_f32_e32 v195, 0x43000000, v195
	ds_write_b128 v210, v[192:195] offset:4096
	v_mul_f32_e32 v196, 0x43000000, v196
	v_mul_f32_e32 v197, 0x43000000, v197
	v_mul_f32_e32 v198, 0x43000000, v198
	v_mul_f32_e32 v199, 0x43000000, v199
	ds_write_b128 v210, v[196:199] offset:5120
	v_mul_f32_e32 v200, 0x43000000, v200
	v_mul_f32_e32 v201, 0x43000000, v201
	v_mul_f32_e32 v202, 0x43000000, v202
	v_mul_f32_e32 v203, 0x43000000, v203
	ds_write_b128 v210, v[200:203] offset:6144
	v_mul_f32_e32 v204, 0x43000000, v204
	v_mul_f32_e32 v205, 0x43000000, v205
	v_mul_f32_e32 v206, 0x43000000, v206
	v_mul_f32_e32 v207, 0x43000000, v207
	ds_write_b128 v210, v[204:207] offset:7168
	s_waitcnt lgkmcnt(0)
	s_barrier
; #define GAS __attribute__((address_space(1)))
; #define LAS __attribute__((address_space(3)))
; template <int MAP, bool KS, bool KPERM = false>
; __device__ __forceinline__ void p0_transpose_item(const float* W, int K, int Nsrc, int nblk, bf16* WT, const float* ksA, const float* ksB, int ksplit, LAS float* scr, int item, int lane) {
;     const int kb = item / nblk, nb = item % nblk, k0 = 64 * kb, n0 = 32 * nb;
;     const int nr = n0 + (lane & 31); const int sc = MAP == 1 ? src_col_in(nr) : (MAP == 2 ? nat_dim(nr) : nr);
;     float v[32];
; #pragma unroll
;     for (int i = 0; i < 32; ++i) { const int k = k0 + 2 * i + (lane >> 5); const int ksrc = KPERM ? ((k & ~127) + nat_dim(k & 127)) : k;
;         v[i] = sc >= 0 ? W[(size_t)ksrc * Nsrc + sc] : 0.f; }
; #pragma unroll
;     for (int i = 0; i < 32; ++i) { const int kk = 2 * i + (lane >> 5); const int k = k0 + kk;
;         if (KS) v[i] *= (k < ksplit ? ksA[k] : ksB[k - ksplit]);
;         scr[kk * 33 + (lane & 31)] = v[i]; }
;     LDS_WAIT(); asm volatile("" ::: "memory");
;     const int c = lane & 7;
; #pragma unroll
;     for (int j = 0; j < 4; ++j) { const int n = (lane >> 3) + 8 * j; const LAS float* s = scr + (8 * c) * 33 + n;
;         v4u o; o.x = pk2(s[0 * 33], s[1 * 33]); o.y = pk2(s[2 * 33], s[3 * 33]); o.z = pk2(s[4 * 33], s[5 * 33]); o.w = pk2(s[6 * 33], s[7 * 33]);
;         *(GAS v4u*)(WT + (size_t)(n0 + n) * K + k0 + 8 * c) = o; }
;     LDS_WAIT(); asm volatile("" ::: "memory");
;     const int pr = item >> 1, kb = 2 * (pr / nblk) + (item & 1), nb = pr % nblk, k0 = 64 * kb, n0 = 32 * nb;
;     const int nr = n0 + (lane & 31); const int sc = MAP == 1 ? src_col_in(nr) : nr;
;     float v[32];
; #pragma unroll
;     for (int i = 0; i < 32; ++i) v[i] = sc >= 0 ? W[(size_t)(k0 + 2 * i + (lane >> 5)) * Nsrc + sc] : 0.f;
; #pragma unroll
; __global__ void __launch_bounds__(NWAVES * 64, 2) hybrid_fwd(Args args) {
;     ...
;             if (r < I_IN) { if (l >= PROJ_F8_FROM) p0_transpose_item_f8<true, 1>(args.in[2] + (size_t)l * DM * NSRC, DM, NSRC, NPROJ / 32, (unsigned char*)(ws + WS_WIN + l * SZ_WIN), WUP8_SCALE, args.in[1] + l * DM, args.in[1] + l * DM, DM, scr, r, lane);
;                 else p0_transpose_item<1, true>(args.in[2] + (size_t)l * DM * NSRC, DM, NSRC, NPROJ / 32, (bf16*)(ws + WS_WIN + l * SZ_WIN), args.in[1] + l * DM, args.in[1] + l * DM, DM, scr, r, lane); continue; } r -= I_IN;
	s_add_i32 s24, s23, 8
	s_lshl_b32 s20, s24, 7
	s_cmp_lt_u32 s24, 40
	s_cselect_b32 s21, 0, 0x830
	s_cmp_lt_u32 s24, 72
	s_cselect_b32 s21, s21, 0xfffff030
	s_add_i32 s20, s20, s21
	s_lshl_b32 s20, s20, 2
	s_add_u32 s8, s46, s20
	s_addc_u32 s9, s47, 0
	global_load_dwordx4 v[176:179], v76, s[8:9]
	s_add_u32 s8, s8, 0x16280
	s_addc_u32 s9, s9, 0
	global_load_dwordx4 v[180:183], v76, s[8:9]
	s_add_u32 s8, s8, 0x16280
	s_addc_u32 s9, s9, 0
	global_load_dwordx4 v[184:187], v76, s[8:9]
	s_add_u32 s8, s8, 0x16280
	s_addc_u32 s9, s9, 0
	global_load_dwordx4 v[188:191], v76, s[8:9]
	s_add_u32 s8, s8, 0x16280
	s_addc_u32 s9, s9, 0
	global_load_dwordx4 v[192:195], v76, s[8:9]
	s_add_u32 s8, s8, 0x16280
	s_addc_u32 s9, s9, 0
	global_load_dwordx4 v[196:199], v76, s[8:9]
	s_add_u32 s8, s8, 0x16280
	s_addc_u32 s9, s9, 0
	global_load_dwordx4 v[200:203], v76, s[8:9]
	s_add_u32 s8, s8, 0x16280
	s_addc_u32 s9, s9, 0
	global_load_dwordx4 v[204:207], v76, s[8:9]
	s_add_u32 s6, s44, 0x3001000
	s_addc_u32 s7, s45, 0
	ds_read_b32 v226, v212
	ds_read_b32 v227, v212 offset:512
	ds_read_b32 v228, v212 offset:1024
	ds_read_b32 v229, v212 offset:1536
	ds_read_b32 v230, v212 offset:2048
	ds_read_b32 v231, v212 offset:2560
	ds_read_b32 v232, v212 offset:3072
	ds_read_b32 v233, v212 offset:3584
	ds_read_b32 v234, v212 offset:4096
	ds_read_b32 v235, v212 offset:4608
	ds_read_b32 v236, v212 offset:5120
	ds_read_b32 v237, v212 offset:5632
	ds_read_b32 v238, v212 offset:6144
	ds_read_b32 v239, v212 offset:6656
	ds_read_b32 v240, v212 offset:7168
	ds_read_b32 v241, v212 offset:7680
	s_waitcnt lgkmcnt(0)
	v_max_f32_e32 v226, v226, v226
	v_max_f32_e32 v227, v227, v227
	v_max_f32_e32 v228, v228, v228
	v_max_f32_e32 v229, v229, v229
	v_max_f32_e32 v230, v230, v230
	v_max_f32_e32 v231, v231, v231
	v_max_f32_e32 v232, v232, v232
	v_max_f32_e32 v233, v233, v233
	v_max_f32_e32 v234, v234, v234
	v_max_f32_e32 v235, v235, v235
	v_max_f32_e32 v236, v236, v236
	v_max_f32_e32 v237, v237, v237
	v_max_f32_e32 v238, v238, v238
	v_max_f32_e32 v239, v239, v239
	v_max_f32_e32 v240, v240, v240
	v_max_f32_e32 v241, v241, v241
	v_med3_f32 v226, v226, s62, v95
	v_med3_f32 v227, v227, s62, v95
	v_med3_f32 v228, v228, s62, v95
	v_med3_f32 v229, v229, s62, v95
	v_med3_f32 v230, v230, s62, v95
	v_med3_f32 v231, v231, s62, v95
	v_med3_f32 v232, v232, s62, v95
	v_med3_f32 v233, v233, s62, v95
	v_med3_f32 v234, v234, s62, v95
	v_med3_f32 v235, v235, s62, v95
	v_med3_f32 v236, v236, s62, v95
	v_med3_f32 v237, v237, s62, v95
	v_med3_f32 v238, v238, s62, v95
	v_med3_f32 v239, v239, s62, v95
	v_med3_f32 v240, v240, s62, v95
	v_med3_f32 v241, v241, s62, v95
	v_mov_b32_e32 v242, 0
	v_mov_b32_e32 v243, 0
	v_mov_b32_e32 v244, 0
	v_mov_b32_e32 v245, 0
	v_cvt_pk_fp8_f32 v242, v226, v227
	v_cvt_pk_fp8_f32 v243, v230, v231
	v_cvt_pk_fp8_f32 v244, v234, v235
	v_cvt_pk_fp8_f32 v245, v238, v239
	v_cvt_pk_fp8_f32 v242, v228, v229 op_sel:[0,0,1]
	v_cvt_pk_fp8_f32 v243, v232, v233 op_sel:[0,0,1]
	v_cvt_pk_fp8_f32 v244, v236, v237 op_sel:[0,0,1]
	v_cvt_pk_fp8_f32 v245, v240, v241 op_sel:[0,0,1]
	s_nop 0
	global_store_dwordx4 v79, v[242:245], s[6:7]
	ds_read_b32 v226, v214
	ds_read_b32 v227, v214 offset:512
	ds_read_b32 v228, v214 offset:1024
	ds_read_b32 v229, v214 offset:1536
	ds_read_b32 v230, v214 offset:2048
	ds_read_b32 v231, v214 offset:2560
	ds_read_b32 v232, v214 offset:3072
	ds_read_b32 v233, v214 offset:3584
	ds_read_b32 v234, v214 offset:4096
	ds_read_b32 v235, v214 offset:4608
	ds_read_b32 v236, v214 offset:5120
	ds_read_b32 v237, v214 offset:5632
	ds_read_b32 v238, v214 offset:6144
	ds_read_b32 v239, v214 offset:6656
	ds_read_b32 v240, v214 offset:7168
	ds_read_b32 v241, v214 offset:7680
	s_waitcnt lgkmcnt(0)
	v_max_f32_e32 v226, v226, v226
	v_max_f32_e32 v227, v227, v227
	v_max_f32_e32 v228, v228, v228
	v_max_f32_e32 v229, v229, v229
	v_max_f32_e32 v230, v230, v230
	v_max_f32_e32 v231, v231, v231
	v_max_f32_e32 v232, v232, v232
	v_max_f32_e32 v233, v233, v233
	v_max_f32_e32 v234, v234, v234
	v_max_f32_e32 v235, v235, v235
	v_max_f32_e32 v236, v236, v236
	v_max_f32_e32 v237, v237, v237
	v_max_f32_e32 v238, v238, v238
	v_max_f32_e32 v239, v239, v239
	v_max_f32_e32 v240, v240, v240
	v_max_f32_e32 v241, v241, v241
	v_med3_f32 v226, v226, s62, v95
	v_med3_f32 v227, v227, s62, v95
	v_med3_f32 v228, v228, s62, v95
	v_med3_f32 v229, v229, s62, v95
	v_med3_f32 v230, v230, s62, v95
	v_med3_f32 v231, v231, s62, v95
	v_med3_f32 v232, v232, s62, v95
	v_med3_f32 v233, v233, s62, v95
	v_med3_f32 v234, v234, s62, v95
	v_med3_f32 v235, v235, s62, v95
	v_med3_f32 v236, v236, s62, v95
	v_med3_f32 v237, v237, s62, v95
	v_med3_f32 v238, v238, s62, v95
	v_med3_f32 v239, v239, s62, v95
	v_med3_f32 v240, v240, s62, v95
	v_med3_f32 v241, v241, s62, v95
	v_mov_b32_e32 v242, 0
	v_mov_b32_e32 v243, 0
	v_mov_b32_e32 v244, 0
	v_mov_b32_e32 v245, 0
	v_cvt_pk_fp8_f32 v242, v226, v227
	v_cvt_pk_fp8_f32 v243, v230, v231
	v_cvt_pk_fp8_f32 v244, v234, v235
	v_cvt_pk_fp8_f32 v245, v238, v239
	v_cvt_pk_fp8_f32 v242, v228, v229 op_sel:[0,0,1]
	v_cvt_pk_fp8_f32 v243, v232, v233 op_sel:[0,0,1]
	v_cvt_pk_fp8_f32 v244, v236, v237 op_sel:[0,0,1]
	v_cvt_pk_fp8_f32 v245, v240, v241 op_sel:[0,0,1]
	s_nop 0
	global_store_dwordx4 v80, v[242:245], s[6:7]
	s_waitcnt vmcnt(12)
	v_mul_f32_e32 v144, v42, v144
	v_mul_f32_e32 v145, v42, v145
	v_mul_f32_e32 v146, v42, v146
	v_mul_f32_e32 v147, v42, v147
	ds_write_b128 v209, v[144:147]
	v_mul_f32_e32 v148, v43, v148
	v_mul_f32_e32 v149, v43, v149
	v_mul_f32_e32 v150, v43, v150
	v_mul_f32_e32 v151, v43, v151
	ds_write_b128 v209, v[148:151] offset:1024
	v_mul_f32_e32 v152, v44, v152
	v_mul_f32_e32 v153, v44, v153
	v_mul_f32_e32 v154, v44, v154
	v_mul_f32_e32 v155, v44, v155
	ds_write_b128 v209, v[152:155] offset:2048
	v_mul_f32_e32 v156, v45, v156
	v_mul_f32_e32 v157, v45, v157
	v_mul_f32_e32 v158, v45, v158
	v_mul_f32_e32 v159, v45, v159
	ds_write_b128 v209, v[156:159] offset:3072
	v_mul_f32_e32 v160, v46, v160
	v_mul_f32_e32 v161, v46, v161
	v_mul_f32_e32 v162, v46, v162
	v_mul_f32_e32 v163, v46, v163
	ds_write_b128 v209, v[160:163] offset:4096
	v_mul_f32_e32 v164, v47, v164
	v_mul_f32_e32 v165, v47, v165
	v_mul_f32_e32 v166, v47, v166
	v_mul_f32_e32 v167, v47, v167
	ds_write_b128 v209, v[164:167] offset:5120
	v_mul_f32_e32 v168, v48, v168
	v_mul_f32_e32 v169, v48, v169
	v_mul_f32_e32 v170, v48, v170
	v_mul_f32_e32 v171, v48, v171
	ds_write_b128 v209, v[168:171] offset:6144
	v_mul_f32_e32 v172, v49, v172
	v_mul_f32_e32 v173, v49, v173
	v_mul_f32_e32 v174, v49, v174
	v_mul_f32_e32 v175, v49, v175
	ds_write_b128 v209, v[172:175] offset:7168
	s_waitcnt lgkmcnt(0)
	s_barrier
; #define GAS __attribute__((address_space(1)))
; #define LAS __attribute__((address_space(3)))
; #define LDS_WAIT() asm volatile("s_waitcnt lgkmcnt(0)" ::: "memory")
; __device__ __forceinline__ unsigned pk2(float lo, float hi) { return f2bf(lo) | (f2bf(hi) << 16); }
; __device__ __forceinline__ int nat_dim(int p) { return (p >> 1) + 64 * (p & 1); }
; template <int MAP, bool KS, bool KPERM = false>
; __device__ __forceinline__ void p0_transpose_item(const float* W, int K, int Nsrc, int nblk, bf16* WT, const float* ksA, const float* ksB, int ksplit, LAS float* scr, int item, int lane) {
;     const int kb = item / nblk, nb = item % nblk, k0 = 64 * kb, n0 = 32 * nb;
;     const int nr = n0 + (lane & 31); const int sc = MAP == 1 ? src_col_in(nr) : (MAP == 2 ? nat_dim(nr) : nr);
;     float v[32];
; #pragma unroll
;     for (int i = 0; i < 32; ++i) { const int k = k0 + 2 * i + (lane >> 5); const int ksrc = KPERM ? ((k & ~127) + nat_dim(k & 127)) : k;
;         v[i] = sc >= 0 ? W[(size_t)ksrc * Nsrc + sc] : 0.f; }
; #pragma unroll
;     for (int i = 0; i < 32; ++i) { const int kk = 2 * i + (lane >> 5); const int k = k0 + kk;
;         if (KS) v[i] *= (k < ksplit ? ksA[k] : ksB[k - ksplit]);
;         scr[kk * 33 + (lane & 31)] = v[i]; }
;     LDS_WAIT(); asm volatile("" ::: "memory");
;     const int c = lane & 7;
; #pragma unroll
;     for (int j = 0; j < 4; ++j) { const int n = (lane >> 3) + 8 * j; const LAS float* s = scr + (8 * c) * 33 + n;
;         v4u o; o.x = pk2(s[0 * 33], s[1 * 33]); o.y = pk2(s[2 * 33], s[3 * 33]); o.z = pk2(s[4 * 33], s[5 * 33]); o.w = pk2(s[6 * 33], s[7 * 33]);
;         *(GAS v4u*)(WT + (size_t)(n0 + n) * K + k0 + 8 * c) = o; }
;     LDS_WAIT(); asm volatile("" ::: "memory");
; __global__ void __launch_bounds__(NWAVES * 64, 2) hybrid_fwd(Args args) {
;     ...
;             if (r < I_IN) { if (l >= PROJ_F8_FROM) p0_transpose_item_f8<true, 1>(args.in[2] + (size_t)l * DM * NSRC, DM, NSRC, NPROJ / 32, (unsigned char*)(ws + WS_WIN + l * SZ_WIN), WUP8_SCALE, args.in[1] + l * DM, args.in[1] + l * DM, DM, scr, r, lane);
;                 else p0_transpose_item<1, true>(args.in[2] + (size_t)l * DM * NSRC, DM, NSRC, NPROJ / 32, (bf16*)(ws + WS_WIN + l * SZ_WIN), args.in[1] + l * DM, args.in[1] + l * DM, DM, scr, r, lane); continue; } r -= I_IN;
	s_add_i32 s24, s23, 16
	s_lshl_b32 s20, s24, 7
	s_cmp_lt_u32 s24, 40
	s_cselect_b32 s21, 0, 0x830
	s_cmp_lt_u32 s24, 72
	s_cselect_b32 s21, s21, 0xfffff030
	s_add_i32 s20, s20, s21
	s_lshl_b32 s20, s20, 2
	s_add_u32 s8, s46, s20
	s_addc_u32 s9, s47, 0
	global_load_dwordx4 v[144:147], v76, s[8:9]
	s_add_u32 s8, s8, 0x16280
	s_addc_u32 s9, s9, 0
	global_load_dwordx4 v[148:151], v76, s[8:9]
	s_add_u32 s8, s8, 0x16280
	s_addc_u32 s9, s9, 0
	global_load_dwordx4 v[152:155], v76, s[8:9]
	s_add_u32 s8, s8, 0x16280
	s_addc_u32 s9, s9, 0
	global_load_dwordx4 v[156:159], v76, s[8:9]
	s_add_u32 s8, s8, 0x16280
	s_addc_u32 s9, s9, 0
	global_load_dwordx4 v[160:163], v76, s[8:9]
	s_add_u32 s8, s8, 0x16280
	s_addc_u32 s9, s9, 0
	global_load_dwordx4 v[164:167], v76, s[8:9]
	s_add_u32 s8, s8, 0x16280
	s_addc_u32 s9, s9, 0
	global_load_dwordx4 v[168:171], v76, s[8:9]
	s_add_u32 s8, s8, 0x16280
	s_addc_u32 s9, s9, 0
	global_load_dwordx4 v[172:175], v76, s[8:9]
	s_add_i32 s24, s23, 0
	s_mul_i32 s20, s24, 0x100000
	s_add_u32 s6, s48, s20
	s_addc_u32 s7, s49, 0
	s_cmp_lt_u32 s24, 16
	s_cselect_b32 s20, 1, 0
	s_sub_i32 s21, s24, 16
	s_bitcmp0_b32 s21, 2
	s_cselect_b32 s21, 1, 0
	s_cmp_lt_u32 s24, 40
	s_cselect_b32 s21, s21, 0
	s_or_b32 s20, s20, s21
	s_cmp_lg_u32 s20, 0
	s_cselect_b64 s[20:21], -1, 0
	v_cndmask_b32_e64 v91, v83, v87, s[20:21]
	v_cndmask_b32_e64 v92, v84, v88, s[20:21]
	v_cndmask_b32_e64 v93, v85, v89, s[20:21]
	v_cndmask_b32_e64 v94, v86, v90, s[20:21]
	ds_read_b32 v226, v112
	ds_read_b32 v227, v112 offset:512
	ds_read_b32 v228, v112 offset:1024
	ds_read_b32 v229, v112 offset:1536
	ds_read_b32 v230, v112 offset:2048
	ds_read_b32 v231, v112 offset:2560
	ds_read_b32 v232, v112 offset:3072
	ds_read_b32 v233, v112 offset:3584
	s_waitcnt lgkmcnt(0)
	v_bfe_u32 v120, v226, 16, 1
	v_bfe_u32 v121, v227, 16, 1
	v_bfe_u32 v122, v228, 16, 1
	v_bfe_u32 v123, v229, 16, 1
	v_bfe_u32 v124, v230, 16, 1
	v_bfe_u32 v125, v231, 16, 1
	v_bfe_u32 v126, v232, 16, 1
	v_bfe_u32 v127, v233, 16, 1
	v_add3_u32 v226, v226, v120, s63
	v_add3_u32 v227, v227, v121, s63
	v_add3_u32 v228, v228, v122, s63
	v_add3_u32 v229, v229, v123, s63
	v_add3_u32 v230, v230, v124, s63
	v_add3_u32 v231, v231, v125, s63
	v_add3_u32 v232, v232, v126, s63
	v_add3_u32 v233, v233, v127, s63
	v_perm_b32 v242, v227, v226, s64
	v_perm_b32 v243, v229, v228, s64
	v_perm_b32 v244, v231, v230, s64
	v_perm_b32 v245, v233, v232, s64
	s_nop 0
	global_store_dwordx4 v91, v[242:245], s[6:7]
	ds_read_b32 v226, v114
	ds_read_b32 v227, v114 offset:512
	ds_read_b32 v228, v114 offset:1024
	ds_read_b32 v229, v114 offset:1536
	ds_read_b32 v230, v114 offset:2048
	ds_read_b32 v231, v114 offset:2560
	ds_read_b32 v232, v114 offset:3072
	ds_read_b32 v233, v114 offset:3584
	s_waitcnt lgkmcnt(0)
	v_bfe_u32 v120, v226, 16, 1
	v_bfe_u32 v121, v227, 16, 1
	v_bfe_u32 v122, v228, 16, 1
	v_bfe_u32 v123, v229, 16, 1
	v_bfe_u32 v124, v230, 16, 1
	v_bfe_u32 v125, v231, 16, 1
	v_bfe_u32 v126, v232, 16, 1
	v_bfe_u32 v127, v233, 16, 1
	v_add3_u32 v226, v226, v120, s63
	v_add3_u32 v227, v227, v121, s63
	v_add3_u32 v228, v228, v122, s63
	v_add3_u32 v229, v229, v123, s63
	v_add3_u32 v230, v230, v124, s63
	v_add3_u32 v231, v231, v125, s63
	v_add3_u32 v232, v232, v126, s63
	v_add3_u32 v233, v233, v127, s63
	v_perm_b32 v242, v227, v226, s64
	v_perm_b32 v243, v229, v228, s64
	v_perm_b32 v244, v231, v230, s64
	v_perm_b32 v245, v233, v232, s64
	s_nop 0
	global_store_dwordx4 v92, v[242:245], s[6:7]
	ds_read_b32 v226, v116
	ds_read_b32 v227, v116 offset:512
	ds_read_b32 v228, v116 offset:1024
	ds_read_b32 v229, v116 offset:1536
	ds_read_b32 v230, v116 offset:2048
	ds_read_b32 v231, v116 offset:2560
	ds_read_b32 v232, v116 offset:3072
	ds_read_b32 v233, v116 offset:3584
	s_waitcnt lgkmcnt(0)
	v_bfe_u32 v120, v226, 16, 1
	v_bfe_u32 v121, v227, 16, 1
	v_bfe_u32 v122, v228, 16, 1
	v_bfe_u32 v123, v229, 16, 1
	v_bfe_u32 v124, v230, 16, 1
	v_bfe_u32 v125, v231, 16, 1
	v_bfe_u32 v126, v232, 16, 1
	v_bfe_u32 v127, v233, 16, 1
	v_add3_u32 v226, v226, v120, s63
	v_add3_u32 v227, v227, v121, s63
	v_add3_u32 v228, v228, v122, s63
	v_add3_u32 v229, v229, v123, s63
	v_add3_u32 v230, v230, v124, s63
	v_add3_u32 v231, v231, v125, s63
	v_add3_u32 v232, v232, v126, s63
	v_add3_u32 v233, v233, v127, s63
	v_perm_b32 v242, v227, v226, s64
	v_perm_b32 v243, v229, v228, s64
	v_perm_b32 v244, v231, v230, s64
	v_perm_b32 v245, v233, v232, s64
	s_nop 0
	global_store_dwordx4 v93, v[242:245], s[6:7]
	ds_read_b32 v226, v118
	ds_read_b32 v227, v118 offset:512
	ds_read_b32 v228, v118 offset:1024
	ds_read_b32 v229, v118 offset:1536
	ds_read_b32 v230, v118 offset:2048
	ds_read_b32 v231, v118 offset:2560
	ds_read_b32 v232, v118 offset:3072
	ds_read_b32 v233, v118 offset:3584
	s_waitcnt lgkmcnt(0)
	v_bfe_u32 v120, v226, 16, 1
	v_bfe_u32 v121, v227, 16, 1
	v_bfe_u32 v122, v228, 16, 1
	v_bfe_u32 v123, v229, 16, 1
	v_bfe_u32 v124, v230, 16, 1
	v_bfe_u32 v125, v231, 16, 1
	v_bfe_u32 v126, v232, 16, 1
	v_bfe_u32 v127, v233, 16, 1
	v_add3_u32 v226, v226, v120, s63
	v_add3_u32 v227, v227, v121, s63
	v_add3_u32 v228, v228, v122, s63
	v_add3_u32 v229, v229, v123, s63
	v_add3_u32 v230, v230, v124, s63
	v_add3_u32 v231, v231, v125, s63
	v_add3_u32 v232, v232, v126, s63
	v_add3_u32 v233, v233, v127, s63
	v_perm_b32 v242, v227, v226, s64
	v_perm_b32 v243, v229, v228, s64
	v_perm_b32 v244, v231, v230, s64
	v_perm_b32 v245, v233, v232, s64
	s_nop 0
	global_store_dwordx4 v94, v[242:245], s[6:7]
	s_waitcnt vmcnt(14)
	v_mul_f32_e32 v176, v42, v176
	v_mul_f32_e32 v177, v42, v177
	v_mul_f32_e32 v178, v42, v178
	v_mul_f32_e32 v179, v42, v179
	ds_write_b128 v210, v[176:179]
	v_mul_f32_e32 v180, v43, v180
	v_mul_f32_e32 v181, v43, v181
	v_mul_f32_e32 v182, v43, v182
	v_mul_f32_e32 v183, v43, v183
	ds_write_b128 v210, v[180:183] offset:1024
	v_mul_f32_e32 v184, v44, v184
	v_mul_f32_e32 v185, v44, v185
	v_mul_f32_e32 v186, v44, v186
	v_mul_f32_e32 v187, v44, v187
	ds_write_b128 v210, v[184:187] offset:2048
	v_mul_f32_e32 v188, v45, v188
	v_mul_f32_e32 v189, v45, v189
	v_mul_f32_e32 v190, v45, v190
	v_mul_f32_e32 v191, v45, v191
	ds_write_b128 v210, v[188:191] offset:3072
	v_mul_f32_e32 v192, v46, v192
	v_mul_f32_e32 v193, v46, v193
	v_mul_f32_e32 v194, v46, v194
	v_mul_f32_e32 v195, v46, v195
	ds_write_b128 v210, v[192:195] offset:4096
	v_mul_f32_e32 v196, v47, v196
	v_mul_f32_e32 v197, v47, v197
	v_mul_f32_e32 v198, v47, v198
	v_mul_f32_e32 v199, v47, v199
	ds_write_b128 v210, v[196:199] offset:5120
	v_mul_f32_e32 v200, v48, v200
	v_mul_f32_e32 v201, v48, v201
	v_mul_f32_e32 v202, v48, v202
	v_mul_f32_e32 v203, v48, v203
	ds_write_b128 v210, v[200:203] offset:6144
	v_mul_f32_e32 v204, v49, v204
	v_mul_f32_e32 v205, v49, v205
	v_mul_f32_e32 v206, v49, v206
	v_mul_f32_e32 v207, v49, v207
	ds_write_b128 v210, v[204:207] offset:7168
	s_waitcnt lgkmcnt(0)
	s_barrier
; #define GAS __attribute__((address_space(1)))
; #define LAS __attribute__((address_space(3)))
; #define LDS_WAIT() asm volatile("s_waitcnt lgkmcnt(0)" ::: "memory")
; __device__ __forceinline__ unsigned pk2(float lo, float hi) { return f2bf(lo) | (f2bf(hi) << 16); }
; __device__ __forceinline__ int nat_dim(int p) { return (p >> 1) + 64 * (p & 1); }
; template <int MAP, bool KS, bool KPERM = false>
; __device__ __forceinline__ void p0_transpose_item(const float* W, int K, int Nsrc, int nblk, bf16* WT, const float* ksA, const float* ksB, int ksplit, LAS float* scr, int item, int lane) {
;     const int kb = item / nblk, nb = item % nblk, k0 = 64 * kb, n0 = 32 * nb;
;     const int nr = n0 + (lane & 31); const int sc = MAP == 1 ? src_col_in(nr) : (MAP == 2 ? nat_dim(nr) : nr);
;     float v[32];
; #pragma unroll
;     for (int i = 0; i < 32; ++i) { const int k = k0 + 2 * i + (lane >> 5); const int ksrc = KPERM ? ((k & ~127) + nat_dim(k & 127)) : k;
;         v[i] = sc >= 0 ? W[(size_t)ksrc * Nsrc + sc] : 0.f; }
; #pragma unroll
;     for (int i = 0; i < 32; ++i) { const int kk = 2 * i + (lane >> 5); const int k = k0 + kk;
;         if (KS) v[i] *= (k < ksplit ? ksA[k] : ksB[k - ksplit]);
;         scr[kk * 33 + (lane & 31)] = v[i]; }
;     LDS_WAIT(); asm volatile("" ::: "memory");
;     const int c = lane & 7;
; #pragma unroll
;     for (int j = 0; j < 4; ++j) { const int n = (lane >> 3) + 8 * j; const LAS float* s = scr + (8 * c) * 33 + n;
;         v4u o; o.x = pk2(s[0 * 33], s[1 * 33]); o.y = pk2(s[2 * 33], s[3 * 33]); o.z = pk2(s[4 * 33], s[5 * 33]); o.w = pk2(s[6 * 33], s[7 * 33]);
;         *(GAS v4u*)(WT + (size_t)(n0 + n) * K + k0 + 8 * c) = o; }
;     LDS_WAIT(); asm volatile("" ::: "memory");
; __global__ void __launch_bounds__(NWAVES * 64, 2) hybrid_fwd(Args args) {
;     ...
;             if (r < I_IN) { if (l >= PROJ_F8_FROM) p0_transpose_item_f8<true, 1>(args.in[2] + (size_t)l * DM * NSRC, DM, NSRC, NPROJ / 32, (unsigned char*)(ws + WS_WIN + l * SZ_WIN), WUP8_SCALE, args.in[1] + l * DM, args.in[1] + l * DM, DM, scr, r, lane);
;                 else p0_transpose_item<1, true>(args.in[2] + (size_t)l * DM * NSRC, DM, NSRC, NPROJ / 32, (bf16*)(ws + WS_WIN + l * SZ_WIN), args.in[1] + l * DM, args.in[1] + l * DM, DM, scr, r, lane); continue; } r -= I_IN;
	s_add_i32 s24, s23, 24
	s_lshl_b32 s20, s24, 7
	s_cmp_lt_u32 s24, 40
	s_cselect_b32 s21, 0, 0x830
	s_cmp_lt_u32 s24, 72
	s_cselect_b32 s21, s21, 0xfffff030
	s_add_i32 s20, s20, s21
	s_lshl_b32 s20, s20, 2
	s_add_u32 s8, s46, s20
	s_addc_u32 s9, s47, 0
	global_load_dwordx4 v[176:179], v76, s[8:9]
	s_add_u32 s8, s8, 0x16280
	s_addc_u32 s9, s9, 0
	global_load_dwordx4 v[180:183], v76, s[8:9]
	s_add_u32 s8, s8, 0x16280
	s_addc_u32 s9, s9, 0
	global_load_dwordx4 v[184:187], v76, s[8:9]
	s_add_u32 s8, s8, 0x16280
	s_addc_u32 s9, s9, 0
	global_load_dwordx4 v[188:191], v76, s[8:9]
	s_add_u32 s8, s8, 0x16280
	s_addc_u32 s9, s9, 0
	global_load_dwordx4 v[192:195], v76, s[8:9]
	s_add_u32 s8, s8, 0x16280
	s_addc_u32 s9, s9, 0
	global_load_dwordx4 v[196:199], v76, s[8:9]
	s_add_u32 s8, s8, 0x16280
	s_addc_u32 s9, s9, 0
	global_load_dwordx4 v[200:203], v76, s[8:9]
	s_add_u32 s8, s8, 0x16280
	s_addc_u32 s9, s9, 0
	global_load_dwordx4 v[204:207], v76, s[8:9]
	s_add_i32 s24, s23, 8
	s_mul_i32 s20, s24, 0x100000
	s_add_u32 s6, s48, s20
	s_addc_u32 s7, s49, 0
	s_cmp_lt_u32 s24, 16
	s_cselect_b32 s20, 1, 0
	s_sub_i32 s21, s24, 16
	s_bitcmp0_b32 s21, 2
	s_cselect_b32 s21, 1, 0
	s_cmp_lt_u32 s24, 40
	s_cselect_b32 s21, s21, 0
	s_or_b32 s20, s20, s21
	s_cmp_lg_u32 s20, 0
	s_cselect_b64 s[20:21], -1, 0
	v_cndmask_b32_e64 v91, v83, v87, s[20:21]
	v_cndmask_b32_e64 v92, v84, v88, s[20:21]
	v_cndmask_b32_e64 v93, v85, v89, s[20:21]
	v_cndmask_b32_e64 v94, v86, v90, s[20:21]
	ds_read_b32 v226, v113
	ds_read_b32 v227, v113 offset:512
	ds_read_b32 v228, v113 offset:1024
	ds_read_b32 v229, v113 offset:1536
	ds_read_b32 v230, v113 offset:2048
	ds_read_b32 v231, v113 offset:2560
	ds_read_b32 v232, v113 offset:3072
	ds_read_b32 v233, v113 offset:3584
	s_waitcnt lgkmcnt(0)
	v_bfe_u32 v120, v226, 16, 1
	v_bfe_u32 v121, v227, 16, 1
	v_bfe_u32 v122, v228, 16, 1
	v_bfe_u32 v123, v229, 16, 1
	v_bfe_u32 v124, v230, 16, 1
	v_bfe_u32 v125, v231, 16, 1
	v_bfe_u32 v126, v232, 16, 1
	v_bfe_u32 v127, v233, 16, 1
	v_add3_u32 v226, v226, v120, s63
	v_add3_u32 v227, v227, v121, s63
	v_add3_u32 v228, v228, v122, s63
	v_add3_u32 v229, v229, v123, s63
	v_add3_u32 v230, v230, v124, s63
	v_add3_u32 v231, v231, v125, s63
	v_add3_u32 v232, v232, v126, s63
	v_add3_u32 v233, v233, v127, s63
	v_perm_b32 v242, v227, v226, s64
	v_perm_b32 v243, v229, v228, s64
	v_perm_b32 v244, v231, v230, s64
	v_perm_b32 v245, v233, v232, s64
	s_nop 0
	global_store_dwordx4 v91, v[242:245], s[6:7]
	ds_read_b32 v226, v115
	ds_read_b32 v227, v115 offset:512
	ds_read_b32 v228, v115 offset:1024
	ds_read_b32 v229, v115 offset:1536
	ds_read_b32 v230, v115 offset:2048
	ds_read_b32 v231, v115 offset:2560
	ds_read_b32 v232, v115 offset:3072
	ds_read_b32 v233, v115 offset:3584
	s_waitcnt lgkmcnt(0)
	v_bfe_u32 v120, v226, 16, 1
	v_bfe_u32 v121, v227, 16, 1
	v_bfe_u32 v122, v228, 16, 1
	v_bfe_u32 v123, v229, 16, 1
	v_bfe_u32 v124, v230, 16, 1
	v_bfe_u32 v125, v231, 16, 1
	v_bfe_u32 v126, v232, 16, 1
	v_bfe_u32 v127, v233, 16, 1
	v_add3_u32 v226, v226, v120, s63
	v_add3_u32 v227, v227, v121, s63
	v_add3_u32 v228, v228, v122, s63
	v_add3_u32 v229, v229, v123, s63
	v_add3_u32 v230, v230, v124, s63
	v_add3_u32 v231, v231, v125, s63
	v_add3_u32 v232, v232, v126, s63
	v_add3_u32 v233, v233, v127, s63
	v_perm_b32 v242, v227, v226, s64
	v_perm_b32 v243, v229, v228, s64
	v_perm_b32 v244, v231, v230, s64
	v_perm_b32 v245, v233, v232, s64
	s_nop 0
	global_store_dwordx4 v92, v[242:245], s[6:7]
	ds_read_b32 v226, v117
	ds_read_b32 v227, v117 offset:512
	ds_read_b32 v228, v117 offset:1024
	ds_read_b32 v229, v117 offset:1536
	ds_read_b32 v230, v117 offset:2048
	ds_read_b32 v231, v117 offset:2560
	ds_read_b32 v232, v117 offset:3072
	ds_read_b32 v233, v117 offset:3584
	s_waitcnt lgkmcnt(0)
	v_bfe_u32 v120, v226, 16, 1
	v_bfe_u32 v121, v227, 16, 1
	v_bfe_u32 v122, v228, 16, 1
	v_bfe_u32 v123, v229, 16, 1
	v_bfe_u32 v124, v230, 16, 1
	v_bfe_u32 v125, v231, 16, 1
	v_bfe_u32 v126, v232, 16, 1
	v_bfe_u32 v127, v233, 16, 1
	v_add3_u32 v226, v226, v120, s63
	v_add3_u32 v227, v227, v121, s63
	v_add3_u32 v228, v228, v122, s63
	v_add3_u32 v229, v229, v123, s63
	v_add3_u32 v230, v230, v124, s63
	v_add3_u32 v231, v231, v125, s63
	v_add3_u32 v232, v232, v126, s63
	v_add3_u32 v233, v233, v127, s63
	v_perm_b32 v242, v227, v226, s64
	v_perm_b32 v243, v229, v228, s64
	v_perm_b32 v244, v231, v230, s64
	v_perm_b32 v245, v233, v232, s64
	s_nop 0
	global_store_dwordx4 v93, v[242:245], s[6:7]
	ds_read_b32 v226, v119
	ds_read_b32 v227, v119 offset:512
	ds_read_b32 v228, v119 offset:1024
	ds_read_b32 v229, v119 offset:1536
	ds_read_b32 v230, v119 offset:2048
	ds_read_b32 v231, v119 offset:2560
	ds_read_b32 v232, v119 offset:3072
	ds_read_b32 v233, v119 offset:3584
	s_waitcnt lgkmcnt(0)
	v_bfe_u32 v120, v226, 16, 1
	v_bfe_u32 v121, v227, 16, 1
	v_bfe_u32 v122, v228, 16, 1
	v_bfe_u32 v123, v229, 16, 1
	v_bfe_u32 v124, v230, 16, 1
	v_bfe_u32 v125, v231, 16, 1
	v_bfe_u32 v126, v232, 16, 1
	v_bfe_u32 v127, v233, 16, 1
	v_add3_u32 v226, v226, v120, s63
	v_add3_u32 v227, v227, v121, s63
	v_add3_u32 v228, v228, v122, s63
	v_add3_u32 v229, v229, v123, s63
	v_add3_u32 v230, v230, v124, s63
	v_add3_u32 v231, v231, v125, s63
	v_add3_u32 v232, v232, v126, s63
	v_add3_u32 v233, v233, v127, s63
	v_perm_b32 v242, v227, v226, s64
	v_perm_b32 v243, v229, v228, s64
	v_perm_b32 v244, v231, v230, s64
	v_perm_b32 v245, v233, v232, s64
	s_nop 0
	global_store_dwordx4 v94, v[242:245], s[6:7]
	s_waitcnt vmcnt(16)
	v_mul_f32_e32 v144, v42, v144
	v_mul_f32_e32 v145, v42, v145
	v_mul_f32_e32 v146, v42, v146
	v_mul_f32_e32 v147, v42, v147
	ds_write_b128 v209, v[144:147]
	v_mul_f32_e32 v148, v43, v148
	v_mul_f32_e32 v149, v43, v149
	v_mul_f32_e32 v150, v43, v150
	v_mul_f32_e32 v151, v43, v151
	ds_write_b128 v209, v[148:151] offset:1024
	v_mul_f32_e32 v152, v44, v152
	v_mul_f32_e32 v153, v44, v153
	v_mul_f32_e32 v154, v44, v154
	v_mul_f32_e32 v155, v44, v155
	ds_write_b128 v209, v[152:155] offset:2048
	v_mul_f32_e32 v156, v45, v156
	v_mul_f32_e32 v157, v45, v157
	v_mul_f32_e32 v158, v45, v158
	v_mul_f32_e32 v159, v45, v159
	ds_write_b128 v209, v[156:159] offset:3072
	v_mul_f32_e32 v160, v46, v160
	v_mul_f32_e32 v161, v46, v161
	v_mul_f32_e32 v162, v46, v162
	v_mul_f32_e32 v163, v46, v163
	ds_write_b128 v209, v[160:163] offset:4096
	v_mul_f32_e32 v164, v47, v164
	v_mul_f32_e32 v165, v47, v165
	v_mul_f32_e32 v166, v47, v166
	v_mul_f32_e32 v167, v47, v167
	ds_write_b128 v209, v[164:167] offset:5120
	v_mul_f32_e32 v168, v48, v168
	v_mul_f32_e32 v169, v48, v169
	v_mul_f32_e32 v170, v48, v170
	v_mul_f32_e32 v171, v48, v171
	ds_write_b128 v209, v[168:171] offset:6144
	v_mul_f32_e32 v172, v49, v172
	v_mul_f32_e32 v173, v49, v173
	v_mul_f32_e32 v174, v49, v174
	v_mul_f32_e32 v175, v49, v175
	ds_write_b128 v209, v[172:175] offset:7168
	s_waitcnt lgkmcnt(0)
	s_barrier
; #define GAS __attribute__((address_space(1)))
; #define LAS __attribute__((address_space(3)))
; #define LDS_WAIT() asm volatile("s_waitcnt lgkmcnt(0)" ::: "memory")
; __device__ __forceinline__ unsigned pk2(float lo, float hi) { return f2bf(lo) | (f2bf(hi) << 16); }
; __device__ __forceinline__ int nat_dim(int p) { return (p >> 1) + 64 * (p & 1); }
; template <int MAP, bool KS, bool KPERM = false>
; __device__ __forceinline__ void p0_transpose_item(const float* W, int K, int Nsrc, int nblk, bf16* WT, const float* ksA, const float* ksB, int ksplit, LAS float* scr, int item, int lane) {
;     const int kb = item / nblk, nb = item % nblk, k0 = 64 * kb, n0 = 32 * nb;
;     const int nr = n0 + (lane & 31); const int sc = MAP == 1 ? src_col_in(nr) : (MAP == 2 ? nat_dim(nr) : nr);
;     float v[32];
; #pragma unroll
;     for (int i = 0; i < 32; ++i) { const int k = k0 + 2 * i + (lane >> 5); const int ksrc = KPERM ? ((k & ~127) + nat_dim(k & 127)) : k;
;         v[i] = sc >= 0 ? W[(size_t)ksrc * Nsrc + sc] : 0.f; }
; #pragma unroll
;     for (int i = 0; i < 32; ++i) { const int kk = 2 * i + (lane >> 5); const int k = k0 + kk;
;         if (KS) v[i] *= (k < ksplit ? ksA[k] : ksB[k - ksplit]);
;         scr[kk * 33 + (lane & 31)] = v[i]; }
;     LDS_WAIT(); asm volatile("" ::: "memory");
;     const int c = lane & 7;
; #pragma unroll
;     for (int j = 0; j < 4; ++j) { const int n = (lane >> 3) + 8 * j; const LAS float* s = scr + (8 * c) * 33 + n;
;         v4u o; o.x = pk2(s[0 * 33], s[1 * 33]); o.y = pk2(s[2 * 33], s[3 * 33]); o.z = pk2(s[4 * 33], s[5 * 33]); o.w = pk2(s[6 * 33], s[7 * 33]);
;         *(GAS v4u*)(WT + (size_t)(n0 + n) * K + k0 + 8 * c) = o; }
;     LDS_WAIT(); asm volatile("" ::: "memory");
; __global__ void __launch_bounds__(NWAVES * 64, 2) hybrid_fwd(Args args) {
;     ...
;             if (r < I_IN) { if (l >= PROJ_F8_FROM) p0_transpose_item_f8<true, 1>(args.in[2] + (size_t)l * DM * NSRC, DM, NSRC, NPROJ / 32, (unsigned char*)(ws + WS_WIN + l * SZ_WIN), WUP8_SCALE, args.in[1] + l * DM, args.in[1] + l * DM, DM, scr, r, lane);
;                 else p0_transpose_item<1, true>(args.in[2] + (size_t)l * DM * NSRC, DM, NSRC, NPROJ / 32, (bf16*)(ws + WS_WIN + l * SZ_WIN), args.in[1] + l * DM, args.in[1] + l * DM, DM, scr, r, lane); continue; } r -= I_IN;
	s_add_i32 s24, s23, 32
	s_lshl_b32 s20, s24, 7
	s_cmp_lt_u32 s24, 40
	s_cselect_b32 s21, 0, 0x830
	s_cmp_lt_u32 s24, 72
	s_cselect_b32 s21, s21, 0xfffff030
	s_add_i32 s20, s20, s21
	s_lshl_b32 s20, s20, 2
	s_add_u32 s8, s46, s20
	s_addc_u32 s9, s47, 0
	global_load_dwordx4 v[144:147], v76, s[8:9]
	s_add_u32 s8, s8, 0x16280
	s_addc_u32 s9, s9, 0
	global_load_dwordx4 v[148:151], v76, s[8:9]
	s_add_u32 s8, s8, 0x16280
	s_addc_u32 s9, s9, 0
	global_load_dwordx4 v[152:155], v76, s[8:9]
	s_add_u32 s8, s8, 0x16280
	s_addc_u32 s9, s9, 0
	global_load_dwordx4 v[156:159], v76, s[8:9]
	s_add_u32 s8, s8, 0x16280
	s_addc_u32 s9, s9, 0
	global_load_dwordx4 v[160:163], v76, s[8:9]
	s_add_u32 s8, s8, 0x16280
	s_addc_u32 s9, s9, 0
	global_load_dwordx4 v[164:167], v76, s[8:9]
	s_add_u32 s8, s8, 0x16280
	s_addc_u32 s9, s9, 0
	global_load_dwordx4 v[168:171], v76, s[8:9]
	s_add_u32 s8, s8, 0x16280
	s_addc_u32 s9, s9, 0
	global_load_dwordx4 v[172:175], v76, s[8:9]
	s_add_i32 s24, s23, 16
	s_mul_i32 s20, s24, 0x100000
	s_add_u32 s6, s48, s20
	s_addc_u32 s7, s49, 0
	s_cmp_lt_u32 s24, 16
	s_cselect_b32 s20, 1, 0
	s_sub_i32 s21, s24, 16
	s_bitcmp0_b32 s21, 2
	s_cselect_b32 s21, 1, 0
	s_cmp_lt_u32 s24, 40
	s_cselect_b32 s21, s21, 0
	s_or_b32 s20, s20, s21
	s_cmp_lg_u32 s20, 0
	s_cselect_b64 s[20:21], -1, 0
	v_cndmask_b32_e64 v91, v83, v87, s[20:21]
	v_cndmask_b32_e64 v92, v84, v88, s[20:21]
	v_cndmask_b32_e64 v93, v85, v89, s[20:21]
	v_cndmask_b32_e64 v94, v86, v90, s[20:21]
	ds_read_b32 v226, v112
	ds_read_b32 v227, v112 offset:512
	ds_read_b32 v228, v112 offset:1024
	ds_read_b32 v229, v112 offset:1536
	ds_read_b32 v230, v112 offset:2048
	ds_read_b32 v231, v112 offset:2560
	ds_read_b32 v232, v112 offset:3072
	ds_read_b32 v233, v112 offset:3584
	s_waitcnt lgkmcnt(0)
	v_bfe_u32 v120, v226, 16, 1
	v_bfe_u32 v121, v227, 16, 1
	v_bfe_u32 v122, v228, 16, 1
	v_bfe_u32 v123, v229, 16, 1
	v_bfe_u32 v124, v230, 16, 1
	v_bfe_u32 v125, v231, 16, 1
	v_bfe_u32 v126, v232, 16, 1
	v_bfe_u32 v127, v233, 16, 1
	v_add3_u32 v226, v226, v120, s63
	v_add3_u32 v227, v227, v121, s63
	v_add3_u32 v228, v228, v122, s63
	v_add3_u32 v229, v229, v123, s63
	v_add3_u32 v230, v230, v124, s63
	v_add3_u32 v231, v231, v125, s63
	v_add3_u32 v232, v232, v126, s63
	v_add3_u32 v233, v233, v127, s63
	v_perm_b32 v242, v227, v226, s64
	v_perm_b32 v243, v229, v228, s64
	v_perm_b32 v244, v231, v230, s64
	v_perm_b32 v245, v233, v232, s64
	s_nop 0
	global_store_dwordx4 v91, v[242:245], s[6:7]
	ds_read_b32 v226, v114
	ds_read_b32 v227, v114 offset:512
	ds_read_b32 v228, v114 offset:1024
	ds_read_b32 v229, v114 offset:1536
	ds_read_b32 v230, v114 offset:2048
	ds_read_b32 v231, v114 offset:2560
	ds_read_b32 v232, v114 offset:3072
	ds_read_b32 v233, v114 offset:3584
	s_waitcnt lgkmcnt(0)
	v_bfe_u32 v120, v226, 16, 1
	v_bfe_u32 v121, v227, 16, 1
	v_bfe_u32 v122, v228, 16, 1
	v_bfe_u32 v123, v229, 16, 1
	v_bfe_u32 v124, v230, 16, 1
	v_bfe_u32 v125, v231, 16, 1
	v_bfe_u32 v126, v232, 16, 1
	v_bfe_u32 v127, v233, 16, 1
	v_add3_u32 v226, v226, v120, s63
	v_add3_u32 v227, v227, v121, s63
	v_add3_u32 v228, v228, v122, s63
	v_add3_u32 v229, v229, v123, s63
	v_add3_u32 v230, v230, v124, s63
	v_add3_u32 v231, v231, v125, s63
	v_add3_u32 v232, v232, v126, s63
	v_add3_u32 v233, v233, v127, s63
	v_perm_b32 v242, v227, v226, s64
	v_perm_b32 v243, v229, v228, s64
	v_perm_b32 v244, v231, v230, s64
	v_perm_b32 v245, v233, v232, s64
	s_nop 0
	global_store_dwordx4 v92, v[242:245], s[6:7]
	ds_read_b32 v226, v116
	ds_read_b32 v227, v116 offset:512
	ds_read_b32 v228, v116 offset:1024
	ds_read_b32 v229, v116 offset:1536
	ds_read_b32 v230, v116 offset:2048
	ds_read_b32 v231, v116 offset:2560
	ds_read_b32 v232, v116 offset:3072
	ds_read_b32 v233, v116 offset:3584
	s_waitcnt lgkmcnt(0)
	v_bfe_u32 v120, v226, 16, 1
	v_bfe_u32 v121, v227, 16, 1
	v_bfe_u32 v122, v228, 16, 1
	v_bfe_u32 v123, v229, 16, 1
	v_bfe_u32 v124, v230, 16, 1
	v_bfe_u32 v125, v231, 16, 1
	v_bfe_u32 v126, v232, 16, 1
	v_bfe_u32 v127, v233, 16, 1
	v_add3_u32 v226, v226, v120, s63
	v_add3_u32 v227, v227, v121, s63
	v_add3_u32 v228, v228, v122, s63
	v_add3_u32 v229, v229, v123, s63
	v_add3_u32 v230, v230, v124, s63
	v_add3_u32 v231, v231, v125, s63
	v_add3_u32 v232, v232, v126, s63
	v_add3_u32 v233, v233, v127, s63
	v_perm_b32 v242, v227, v226, s64
	v_perm_b32 v243, v229, v228, s64
	v_perm_b32 v244, v231, v230, s64
	v_perm_b32 v245, v233, v232, s64
	s_nop 0
	global_store_dwordx4 v93, v[242:245], s[6:7]
	ds_read_b32 v226, v118
	ds_read_b32 v227, v118 offset:512
	ds_read_b32 v228, v118 offset:1024
	ds_read_b32 v229, v118 offset:1536
	ds_read_b32 v230, v118 offset:2048
	ds_read_b32 v231, v118 offset:2560
	ds_read_b32 v232, v118 offset:3072
	ds_read_b32 v233, v118 offset:3584
	s_waitcnt lgkmcnt(0)
	v_bfe_u32 v120, v226, 16, 1
	v_bfe_u32 v121, v227, 16, 1
	v_bfe_u32 v122, v228, 16, 1
	v_bfe_u32 v123, v229, 16, 1
	v_bfe_u32 v124, v230, 16, 1
	v_bfe_u32 v125, v231, 16, 1
	v_bfe_u32 v126, v232, 16, 1
	v_bfe_u32 v127, v233, 16, 1
	v_add3_u32 v226, v226, v120, s63
	v_add3_u32 v227, v227, v121, s63
	v_add3_u32 v228, v228, v122, s63
	v_add3_u32 v229, v229, v123, s63
	v_add3_u32 v230, v230, v124, s63
	v_add3_u32 v231, v231, v125, s63
	v_add3_u32 v232, v232, v126, s63
	v_add3_u32 v233, v233, v127, s63
	v_perm_b32 v242, v227, v226, s64
	v_perm_b32 v243, v229, v228, s64
	v_perm_b32 v244, v231, v230, s64
	v_perm_b32 v245, v233, v232, s64
	s_nop 0
	global_store_dwordx4 v94, v[242:245], s[6:7]
	s_waitcnt vmcnt(16)
	v_mul_f32_e32 v176, v42, v176
	v_mul_f32_e32 v177, v42, v177
	v_mul_f32_e32 v178, v42, v178
	v_mul_f32_e32 v179, v42, v179
	ds_write_b128 v210, v[176:179]
	v_mul_f32_e32 v180, v43, v180
	v_mul_f32_e32 v181, v43, v181
	v_mul_f32_e32 v182, v43, v182
	v_mul_f32_e32 v183, v43, v183
	ds_write_b128 v210, v[180:183] offset:1024
	v_mul_f32_e32 v184, v44, v184
	v_mul_f32_e32 v185, v44, v185
	v_mul_f32_e32 v186, v44, v186
	v_mul_f32_e32 v187, v44, v187
	ds_write_b128 v210, v[184:187] offset:2048
	v_mul_f32_e32 v188, v45, v188
	v_mul_f32_e32 v189, v45, v189
	v_mul_f32_e32 v190, v45, v190
	v_mul_f32_e32 v191, v45, v191
	ds_write_b128 v210, v[188:191] offset:3072
	v_mul_f32_e32 v192, v46, v192
	v_mul_f32_e32 v193, v46, v193
	v_mul_f32_e32 v194, v46, v194
	v_mul_f32_e32 v195, v46, v195
	ds_write_b128 v210, v[192:195] offset:4096
	v_mul_f32_e32 v196, v47, v196
	v_mul_f32_e32 v197, v47, v197
	v_mul_f32_e32 v198, v47, v198
	v_mul_f32_e32 v199, v47, v199
	ds_write_b128 v210, v[196:199] offset:5120
	v_mul_f32_e32 v200, v48, v200
	v_mul_f32_e32 v201, v48, v201
	v_mul_f32_e32 v202, v48, v202
	v_mul_f32_e32 v203, v48, v203
	ds_write_b128 v210, v[200:203] offset:6144
	v_mul_f32_e32 v204, v49, v204
	v_mul_f32_e32 v205, v49, v205
	v_mul_f32_e32 v206, v49, v206
	v_mul_f32_e32 v207, v49, v207
	ds_write_b128 v210, v[204:207] offset:7168
	s_waitcnt lgkmcnt(0)
	s_barrier
; #define GAS __attribute__((address_space(1)))
; #define LAS __attribute__((address_space(3)))
; #define LDS_WAIT() asm volatile("s_waitcnt lgkmcnt(0)" ::: "memory")
; __device__ __forceinline__ int src_col_in(int c) {
;     if (c < 5120) { const int blk = c >> 7, p = c & 127; const bool rope = blk < 16 || ((((blk - 16) >> 2) & 1) == 0); const int d = rope ? (p >> 1) + 64 * (p & 1) : p; return blk * 128 + d; }
;     if (c < OFF_Z) return c + 2096;
; template <int MAP, bool KS, bool KPERM = false>
; __device__ __forceinline__ void p0_transpose_item(const float* W, int K, int Nsrc, int nblk, bf16* WT, const float* ksA, const float* ksB, int ksplit, LAS float* scr, int item, int lane) {
;     const int kb = item / nblk, nb = item % nblk, k0 = 64 * kb, n0 = 32 * nb;
;     const int nr = n0 + (lane & 31); const int sc = MAP == 1 ? src_col_in(nr) : (MAP == 2 ? nat_dim(nr) : nr);
;     float v[32];
; #pragma unroll
;     for (int i = 0; i < 32; ++i) { const int k = k0 + 2 * i + (lane >> 5); const int ksrc = KPERM ? ((k & ~127) + nat_dim(k & 127)) : k;
;         v[i] = sc >= 0 ? W[(size_t)ksrc * Nsrc + sc] : 0.f; }
; #pragma unroll
;     for (int i = 0; i < 32; ++i) { const int kk = 2 * i + (lane >> 5); const int k = k0 + kk;
;         if (KS) v[i] *= (k < ksplit ? ksA[k] : ksB[k - ksplit]);
;         scr[kk * 33 + (lane & 31)] = v[i]; }
;     LDS_WAIT(); asm volatile("" ::: "memory");
;     const int c = lane & 7;
; #pragma unroll
;     for (int j = 0; j < 4; ++j) { const int n = (lane >> 3) + 8 * j; const LAS float* s = scr + (8 * c) * 33 + n;
;         v4u o; o.x = pk2(s[0 * 33], s[1 * 33]); o.y = pk2(s[2 * 33], s[3 * 33]); o.z = pk2(s[4 * 33], s[5 * 33]); o.w = pk2(s[6 * 33], s[7 * 33]);
;         *(GAS v4u*)(WT + (size_t)(n0 + n) * K + k0 + 8 * c) = o; }
;     LDS_WAIT(); asm volatile("" ::: "memory");
; __global__ void __launch_bounds__(NWAVES * 64, 2) hybrid_fwd(Args args) {
;     ...
;             if (r < I_IN) { if (l >= PROJ_F8_FROM) p0_transpose_item_f8<true, 1>(args.in[2] + (size_t)l * DM * NSRC, DM, NSRC, NPROJ / 32, (unsigned char*)(ws + WS_WIN + l * SZ_WIN), WUP8_SCALE, args.in[1] + l * DM, args.in[1] + l * DM, DM, scr, r, lane);
;                 else p0_transpose_item<1, true>(args.in[2] + (size_t)l * DM * NSRC, DM, NSRC, NPROJ / 32, (bf16*)(ws + WS_WIN + l * SZ_WIN), args.in[1] + l * DM, args.in[1] + l * DM, DM, scr, r, lane); continue; } r -= I_IN;
	s_add_i32 s24, s23, 40
	s_lshl_b32 s20, s24, 7
	s_cmp_lt_u32 s24, 40
	s_cselect_b32 s21, 0, 0x830
	s_cmp_lt_u32 s24, 72
	s_cselect_b32 s21, s21, 0xfffff030
	s_add_i32 s20, s20, s21
	s_lshl_b32 s20, s20, 2
	s_add_u32 s8, s46, s20
	s_addc_u32 s9, s47, 0
	global_load_dwordx4 v[176:179], v76, s[8:9]
	s_add_u32 s8, s8, 0x16280
	s_addc_u32 s9, s9, 0
	global_load_dwordx4 v[180:183], v76, s[8:9]
	s_add_u32 s8, s8, 0x16280
	s_addc_u32 s9, s9, 0
	global_load_dwordx4 v[184:187], v76, s[8:9]
	s_add_u32 s8, s8, 0x16280
	s_addc_u32 s9, s9, 0
	global_load_dwordx4 v[188:191], v76, s[8:9]
	s_add_u32 s8, s8, 0x16280
	s_addc_u32 s9, s9, 0
	global_load_dwordx4 v[192:195], v76, s[8:9]
	s_add_u32 s8, s8, 0x16280
	s_addc_u32 s9, s9, 0
	global_load_dwordx4 v[196:199], v76, s[8:9]
	s_add_u32 s8, s8, 0x16280
	s_addc_u32 s9, s9, 0
	global_load_dwordx4 v[200:203], v76, s[8:9]
	s_add_u32 s8, s8, 0x16280
	s_addc_u32 s9, s9, 0
	global_load_dwordx4 v[204:207], v76, s[8:9]
	s_add_i32 s24, s23, 24
	s_mul_i32 s20, s24, 0x100000
	s_add_u32 s6, s48, s20
	s_addc_u32 s7, s49, 0
	s_cmp_lt_u32 s24, 16
	s_cselect_b32 s20, 1, 0
	s_sub_i32 s21, s24, 16
	s_bitcmp0_b32 s21, 2
	s_cselect_b32 s21, 1, 0
	s_cmp_lt_u32 s24, 40
	s_cselect_b32 s21, s21, 0
	s_or_b32 s20, s20, s21
	s_cmp_lg_u32 s20, 0
	s_cselect_b64 s[20:21], -1, 0
	v_cndmask_b32_e64 v91, v83, v87, s[20:21]
	v_cndmask_b32_e64 v92, v84, v88, s[20:21]
	v_cndmask_b32_e64 v93, v85, v89, s[20:21]
	v_cndmask_b32_e64 v94, v86, v90, s[20:21]
	ds_read_b32 v226, v113
	ds_read_b32 v227, v113 offset:512
	ds_read_b32 v228, v113 offset:1024
	ds_read_b32 v229, v113 offset:1536
	ds_read_b32 v230, v113 offset:2048
	ds_read_b32 v231, v113 offset:2560
	ds_read_b32 v232, v113 offset:3072
	ds_read_b32 v233, v113 offset:3584
	s_waitcnt lgkmcnt(0)
	v_bfe_u32 v120, v226, 16, 1
	v_bfe_u32 v121, v227, 16, 1
	v_bfe_u32 v122, v228, 16, 1
	v_bfe_u32 v123, v229, 16, 1
	v_bfe_u32 v124, v230, 16, 1
	v_bfe_u32 v125, v231, 16, 1
	v_bfe_u32 v126, v232, 16, 1
	v_bfe_u32 v127, v233, 16, 1
	v_add3_u32 v226, v226, v120, s63
	v_add3_u32 v227, v227, v121, s63
	v_add3_u32 v228, v228, v122, s63
	v_add3_u32 v229, v229, v123, s63
	v_add3_u32 v230, v230, v124, s63
	v_add3_u32 v231, v231, v125, s63
	v_add3_u32 v232, v232, v126, s63
	v_add3_u32 v233, v233, v127, s63
	v_perm_b32 v242, v227, v226, s64
	v_perm_b32 v243, v229, v228, s64
	v_perm_b32 v244, v231, v230, s64
	v_perm_b32 v245, v233, v232, s64
	s_nop 0
	global_store_dwordx4 v91, v[242:245], s[6:7]
	ds_read_b32 v226, v115
	ds_read_b32 v227, v115 offset:512
	ds_read_b32 v228, v115 offset:1024
	ds_read_b32 v229, v115 offset:1536
	ds_read_b32 v230, v115 offset:2048
	ds_read_b32 v231, v115 offset:2560
	ds_read_b32 v232, v115 offset:3072
	ds_read_b32 v233, v115 offset:3584
	s_waitcnt lgkmcnt(0)
	v_bfe_u32 v120, v226, 16, 1
	v_bfe_u32 v121, v227, 16, 1
	v_bfe_u32 v122, v228, 16, 1
	v_bfe_u32 v123, v229, 16, 1
	v_bfe_u32 v124, v230, 16, 1
	v_bfe_u32 v125, v231, 16, 1
	v_bfe_u32 v126, v232, 16, 1
	v_bfe_u32 v127, v233, 16, 1
	v_add3_u32 v226, v226, v120, s63
	v_add3_u32 v227, v227, v121, s63
	v_add3_u32 v228, v228, v122, s63
	v_add3_u32 v229, v229, v123, s63
	v_add3_u32 v230, v230, v124, s63
	v_add3_u32 v231, v231, v125, s63
	v_add3_u32 v232, v232, v126, s63
	v_add3_u32 v233, v233, v127, s63
	v_perm_b32 v242, v227, v226, s64
	v_perm_b32 v243, v229, v228, s64
	v_perm_b32 v244, v231, v230, s64
	v_perm_b32 v245, v233, v232, s64
	s_nop 0
	global_store_dwordx4 v92, v[242:245], s[6:7]
	ds_read_b32 v226, v117
	ds_read_b32 v227, v117 offset:512
	ds_read_b32 v228, v117 offset:1024
	ds_read_b32 v229, v117 offset:1536
	ds_read_b32 v230, v117 offset:2048
	ds_read_b32 v231, v117 offset:2560
	ds_read_b32 v232, v117 offset:3072
	ds_read_b32 v233, v117 offset:3584
	s_waitcnt lgkmcnt(0)
	v_bfe_u32 v120, v226, 16, 1
	v_bfe_u32 v121, v227, 16, 1
	v_bfe_u32 v122, v228, 16, 1
	v_bfe_u32 v123, v229, 16, 1
	v_bfe_u32 v124, v230, 16, 1
	v_bfe_u32 v125, v231, 16, 1
	v_bfe_u32 v126, v232, 16, 1
	v_bfe_u32 v127, v233, 16, 1
	v_add3_u32 v226, v226, v120, s63
	v_add3_u32 v227, v227, v121, s63
	v_add3_u32 v228, v228, v122, s63
	v_add3_u32 v229, v229, v123, s63
	v_add3_u32 v230, v230, v124, s63
	v_add3_u32 v231, v231, v125, s63
	v_add3_u32 v232, v232, v126, s63
	v_add3_u32 v233, v233, v127, s63
	v_perm_b32 v242, v227, v226, s64
	v_perm_b32 v243, v229, v228, s64
	v_perm_b32 v244, v231, v230, s64
	v_perm_b32 v245, v233, v232, s64
	s_nop 0
	global_store_dwordx4 v93, v[242:245], s[6:7]
	ds_read_b32 v226, v119
	ds_read_b32 v227, v119 offset:512
	ds_read_b32 v228, v119 offset:1024
	ds_read_b32 v229, v119 offset:1536
	ds_read_b32 v230, v119 offset:2048
	ds_read_b32 v231, v119 offset:2560
	ds_read_b32 v232, v119 offset:3072
	ds_read_b32 v233, v119 offset:3584
	s_waitcnt lgkmcnt(0)
	v_bfe_u32 v120, v226, 16, 1
	v_bfe_u32 v121, v227, 16, 1
	v_bfe_u32 v122, v228, 16, 1
	v_bfe_u32 v123, v229, 16, 1
	v_bfe_u32 v124, v230, 16, 1
	v_bfe_u32 v125, v231, 16, 1
	v_bfe_u32 v126, v232, 16, 1
	v_bfe_u32 v127, v233, 16, 1
	v_add3_u32 v226, v226, v120, s63
	v_add3_u32 v227, v227, v121, s63
	v_add3_u32 v228, v228, v122, s63
	v_add3_u32 v229, v229, v123, s63
	v_add3_u32 v230, v230, v124, s63
	v_add3_u32 v231, v231, v125, s63
	v_add3_u32 v232, v232, v126, s63
	v_add3_u32 v233, v233, v127, s63
	v_perm_b32 v242, v227, v226, s64
	v_perm_b32 v243, v229, v228, s64
	v_perm_b32 v244, v231, v230, s64
	v_perm_b32 v245, v233, v232, s64
	s_nop 0
	global_store_dwordx4 v94, v[242:245], s[6:7]
	s_waitcnt vmcnt(16)
	v_mul_f32_e32 v144, v42, v144
	v_mul_f32_e32 v145, v42, v145
	v_mul_f32_e32 v146, v42, v146
	v_mul_f32_e32 v147, v42, v147
	ds_write_b128 v209, v[144:147]
	v_mul_f32_e32 v148, v43, v148
	v_mul_f32_e32 v149, v43, v149
	v_mul_f32_e32 v150, v43, v150
	v_mul_f32_e32 v151, v43, v151
	ds_write_b128 v209, v[148:151] offset:1024
	v_mul_f32_e32 v152, v44, v152
	v_mul_f32_e32 v153, v44, v153
	v_mul_f32_e32 v154, v44, v154
	v_mul_f32_e32 v155, v44, v155
	ds_write_b128 v209, v[152:155] offset:2048
	v_mul_f32_e32 v156, v45, v156
	v_mul_f32_e32 v157, v45, v157
	v_mul_f32_e32 v158, v45, v158
	v_mul_f32_e32 v159, v45, v159
	ds_write_b128 v209, v[156:159] offset:3072
	v_mul_f32_e32 v160, v46, v160
	v_mul_f32_e32 v161, v46, v161
	v_mul_f32_e32 v162, v46, v162
	v_mul_f32_e32 v163, v46, v163
	ds_write_b128 v209, v[160:163] offset:4096
	v_mul_f32_e32 v164, v47, v164
	v_mul_f32_e32 v165, v47, v165
	v_mul_f32_e32 v166, v47, v166
	v_mul_f32_e32 v167, v47, v167
	ds_write_b128 v209, v[164:167] offset:5120
	v_mul_f32_e32 v168, v48, v168
	v_mul_f32_e32 v169, v48, v169
	v_mul_f32_e32 v170, v48, v170
	v_mul_f32_e32 v171, v48, v171
	ds_write_b128 v209, v[168:171] offset:6144
	v_mul_f32_e32 v172, v49, v172
	v_mul_f32_e32 v173, v49, v173
	v_mul_f32_e32 v174, v49, v174
	v_mul_f32_e32 v175, v49, v175
	ds_write_b128 v209, v[172:175] offset:7168
	s_waitcnt lgkmcnt(0)
	s_barrier
; #define GAS __attribute__((address_space(1)))
; #define LAS __attribute__((address_space(3)))
; #define LDS_WAIT() asm volatile("s_waitcnt lgkmcnt(0)" ::: "memory")
; __device__ __forceinline__ unsigned pk2(float lo, float hi) { return f2bf(lo) | (f2bf(hi) << 16); }
; __device__ __forceinline__ int nat_dim(int p) { return (p >> 1) + 64 * (p & 1); }
; template <int MAP, bool KS, bool KPERM = false>
; __device__ __forceinline__ void p0_transpose_item(const float* W, int K, int Nsrc, int nblk, bf16* WT, const float* ksA, const float* ksB, int ksplit, LAS float* scr, int item, int lane) {
;     const int kb = item / nblk, nb = item % nblk, k0 = 64 * kb, n0 = 32 * nb;
;     const int nr = n0 + (lane & 31); const int sc = MAP == 1 ? src_col_in(nr) : (MAP == 2 ? nat_dim(nr) : nr);
;     float v[32];
; #pragma unroll
;     for (int i = 0; i < 32; ++i) { const int k = k0 + 2 * i + (lane >> 5); const int ksrc = KPERM ? ((k & ~127) + nat_dim(k & 127)) : k;
;         v[i] = sc >= 0 ? W[(size_t)ksrc * Nsrc + sc] : 0.f; }
; #pragma unroll
;     for (int i = 0; i < 32; ++i) { const int kk = 2 * i + (lane >> 5); const int k = k0 + kk;
;         if (KS) v[i] *= (k < ksplit ? ksA[k] : ksB[k - ksplit]);
;         scr[kk * 33 + (lane & 31)] = v[i]; }
;     LDS_WAIT(); asm volatile("" ::: "memory");
;     const int c = lane & 7;
; #pragma unroll
;     for (int j = 0; j < 4; ++j) { const int n = (lane >> 3) + 8 * j; const LAS float* s = scr + (8 * c) * 33 + n;
;         v4u o; o.x = pk2(s[0 * 33], s[1 * 33]); o.y = pk2(s[2 * 33], s[3 * 33]); o.z = pk2(s[4 * 33], s[5 * 33]); o.w = pk2(s[6 * 33], s[7 * 33]);
;         *(GAS v4u*)(WT + (size_t)(n0 + n) * K + k0 + 8 * c) = o; }
;     LDS_WAIT(); asm volatile("" ::: "memory");
; __global__ void __launch_bounds__(NWAVES * 64, 2) hybrid_fwd(Args args) {
;     ...
;             if (r < I_IN) { if (l >= PROJ_F8_FROM) p0_transpose_item_f8<true, 1>(args.in[2] + (size_t)l * DM * NSRC, DM, NSRC, NPROJ / 32, (unsigned char*)(ws + WS_WIN + l * SZ_WIN), WUP8_SCALE, args.in[1] + l * DM, args.in[1] + l * DM, DM, scr, r, lane);
;                 else p0_transpose_item<1, true>(args.in[2] + (size_t)l * DM * NSRC, DM, NSRC, NPROJ / 32, (bf16*)(ws + WS_WIN + l * SZ_WIN), args.in[1] + l * DM, args.in[1] + l * DM, DM, scr, r, lane); continue; } r -= I_IN;
	s_add_i32 s24, s23, 48
	s_lshl_b32 s20, s24, 7
	s_cmp_lt_u32 s24, 40
	s_cselect_b32 s21, 0, 0x830
	s_cmp_lt_u32 s24, 72
	s_cselect_b32 s21, s21, 0xfffff030
	s_add_i32 s20, s20, s21
	s_lshl_b32 s20, s20, 2
	s_add_u32 s8, s46, s20
	s_addc_u32 s9, s47, 0
	global_load_dwordx4 v[144:147], v76, s[8:9]
	s_add_u32 s8, s8, 0x16280
	s_addc_u32 s9, s9, 0
	global_load_dwordx4 v[148:151], v76, s[8:9]
	s_add_u32 s8, s8, 0x16280
	s_addc_u32 s9, s9, 0
	global_load_dwordx4 v[152:155], v76, s[8:9]
	s_add_u32 s8, s8, 0x16280
	s_addc_u32 s9, s9, 0
	global_load_dwordx4 v[156:159], v76, s[8:9]
	s_add_u32 s8, s8, 0x16280
	s_addc_u32 s9, s9, 0
	global_load_dwordx4 v[160:163], v76, s[8:9]
	s_add_u32 s8, s8, 0x16280
	s_addc_u32 s9, s9, 0
	global_load_dwordx4 v[164:167], v76, s[8:9]
	s_add_u32 s8, s8, 0x16280
	s_addc_u32 s9, s9, 0
	global_load_dwordx4 v[168:171], v76, s[8:9]
	s_add_u32 s8, s8, 0x16280
	s_addc_u32 s9, s9, 0
	global_load_dwordx4 v[172:175], v76, s[8:9]
	s_add_i32 s24, s23, 32
	s_mul_i32 s20, s24, 0x100000
	s_add_u32 s6, s48, s20
	s_addc_u32 s7, s49, 0
	s_cmp_lt_u32 s24, 16
	s_cselect_b32 s20, 1, 0
	s_sub_i32 s21, s24, 16
	s_bitcmp0_b32 s21, 2
	s_cselect_b32 s21, 1, 0
	s_cmp_lt_u32 s24, 40
	s_cselect_b32 s21, s21, 0
	s_or_b32 s20, s20, s21
	s_cmp_lg_u32 s20, 0
	s_cselect_b64 s[20:21], -1, 0
	v_cndmask_b32_e64 v91, v83, v87, s[20:21]
	v_cndmask_b32_e64 v92, v84, v88, s[20:21]
	v_cndmask_b32_e64 v93, v85, v89, s[20:21]
	v_cndmask_b32_e64 v94, v86, v90, s[20:21]
	ds_read_b32 v226, v112
	ds_read_b32 v227, v112 offset:512
	ds_read_b32 v228, v112 offset:1024
	ds_read_b32 v229, v112 offset:1536
	ds_read_b32 v230, v112 offset:2048
	ds_read_b32 v231, v112 offset:2560
	ds_read_b32 v232, v112 offset:3072
	ds_read_b32 v233, v112 offset:3584
	s_waitcnt lgkmcnt(0)
	v_bfe_u32 v120, v226, 16, 1
	v_bfe_u32 v121, v227, 16, 1
	v_bfe_u32 v122, v228, 16, 1
	v_bfe_u32 v123, v229, 16, 1
	v_bfe_u32 v124, v230, 16, 1
	v_bfe_u32 v125, v231, 16, 1
	v_bfe_u32 v126, v232, 16, 1
	v_bfe_u32 v127, v233, 16, 1
	v_add3_u32 v226, v226, v120, s63
	v_add3_u32 v227, v227, v121, s63
	v_add3_u32 v228, v228, v122, s63
	v_add3_u32 v229, v229, v123, s63
	v_add3_u32 v230, v230, v124, s63
	v_add3_u32 v231, v231, v125, s63
	v_add3_u32 v232, v232, v126, s63
	v_add3_u32 v233, v233, v127, s63
	v_perm_b32 v242, v227, v226, s64
	v_perm_b32 v243, v229, v228, s64
	v_perm_b32 v244, v231, v230, s64
	v_perm_b32 v245, v233, v232, s64
	s_nop 0
	global_store_dwordx4 v91, v[242:245], s[6:7]
	ds_read_b32 v226, v114
	ds_read_b32 v227, v114 offset:512
	ds_read_b32 v228, v114 offset:1024
	ds_read_b32 v229, v114 offset:1536
	ds_read_b32 v230, v114 offset:2048
	ds_read_b32 v231, v114 offset:2560
	ds_read_b32 v232, v114 offset:3072
	ds_read_b32 v233, v114 offset:3584
	s_waitcnt lgkmcnt(0)
	v_bfe_u32 v120, v226, 16, 1
	v_bfe_u32 v121, v227, 16, 1
	v_bfe_u32 v122, v228, 16, 1
	v_bfe_u32 v123, v229, 16, 1
	v_bfe_u32 v124, v230, 16, 1
	v_bfe_u32 v125, v231, 16, 1
	v_bfe_u32 v126, v232, 16, 1
	v_bfe_u32 v127, v233, 16, 1
	v_add3_u32 v226, v226, v120, s63
	v_add3_u32 v227, v227, v121, s63
	v_add3_u32 v228, v228, v122, s63
	v_add3_u32 v229, v229, v123, s63
	v_add3_u32 v230, v230, v124, s63
	v_add3_u32 v231, v231, v125, s63
	v_add3_u32 v232, v232, v126, s63
	v_add3_u32 v233, v233, v127, s63
	v_perm_b32 v242, v227, v226, s64
	v_perm_b32 v243, v229, v228, s64
	v_perm_b32 v244, v231, v230, s64
	v_perm_b32 v245, v233, v232, s64
	s_nop 0
	global_store_dwordx4 v92, v[242:245], s[6:7]
	ds_read_b32 v226, v116
	ds_read_b32 v227, v116 offset:512
	ds_read_b32 v228, v116 offset:1024
	ds_read_b32 v229, v116 offset:1536
	ds_read_b32 v230, v116 offset:2048
	ds_read_b32 v231, v116 offset:2560
	ds_read_b32 v232, v116 offset:3072
	ds_read_b32 v233, v116 offset:3584
	s_waitcnt lgkmcnt(0)
	v_bfe_u32 v120, v226, 16, 1
	v_bfe_u32 v121, v227, 16, 1
	v_bfe_u32 v122, v228, 16, 1
	v_bfe_u32 v123, v229, 16, 1
	v_bfe_u32 v124, v230, 16, 1
	v_bfe_u32 v125, v231, 16, 1
	v_bfe_u32 v126, v232, 16, 1
	v_bfe_u32 v127, v233, 16, 1
	v_add3_u32 v226, v226, v120, s63
	v_add3_u32 v227, v227, v121, s63
	v_add3_u32 v228, v228, v122, s63
	v_add3_u32 v229, v229, v123, s63
	v_add3_u32 v230, v230, v124, s63
	v_add3_u32 v231, v231, v125, s63
	v_add3_u32 v232, v232, v126, s63
	v_add3_u32 v233, v233, v127, s63
	v_perm_b32 v242, v227, v226, s64
	v_perm_b32 v243, v229, v228, s64
	v_perm_b32 v244, v231, v230, s64
	v_perm_b32 v245, v233, v232, s64
	s_nop 0
	global_store_dwordx4 v93, v[242:245], s[6:7]
	ds_read_b32 v226, v118
	ds_read_b32 v227, v118 offset:512
	ds_read_b32 v228, v118 offset:1024
	ds_read_b32 v229, v118 offset:1536
	ds_read_b32 v230, v118 offset:2048
	ds_read_b32 v231, v118 offset:2560
	ds_read_b32 v232, v118 offset:3072
	ds_read_b32 v233, v118 offset:3584
	s_waitcnt lgkmcnt(0)
	v_bfe_u32 v120, v226, 16, 1
	v_bfe_u32 v121, v227, 16, 1
	v_bfe_u32 v122, v228, 16, 1
	v_bfe_u32 v123, v229, 16, 1
	v_bfe_u32 v124, v230, 16, 1
	v_bfe_u32 v125, v231, 16, 1
	v_bfe_u32 v126, v232, 16, 1
	v_bfe_u32 v127, v233, 16, 1
	v_add3_u32 v226, v226, v120, s63
	v_add3_u32 v227, v227, v121, s63
	v_add3_u32 v228, v228, v122, s63
	v_add3_u32 v229, v229, v123, s63
	v_add3_u32 v230, v230, v124, s63
	v_add3_u32 v231, v231, v125, s63
	v_add3_u32 v232, v232, v126, s63
	v_add3_u32 v233, v233, v127, s63
	v_perm_b32 v242, v227, v226, s64
	v_perm_b32 v243, v229, v228, s64
	v_perm_b32 v244, v231, v230, s64
	v_perm_b32 v245, v233, v232, s64
	s_nop 0
	global_store_dwordx4 v94, v[242:245], s[6:7]
	s_waitcnt vmcnt(16)
	v_mul_f32_e32 v176, v42, v176
	v_mul_f32_e32 v177, v42, v177
	v_mul_f32_e32 v178, v42, v178
	v_mul_f32_e32 v179, v42, v179
	ds_write_b128 v210, v[176:179]
	v_mul_f32_e32 v180, v43, v180
	v_mul_f32_e32 v181, v43, v181
	v_mul_f32_e32 v182, v43, v182
	v_mul_f32_e32 v183, v43, v183
	ds_write_b128 v210, v[180:183] offset:1024
	v_mul_f32_e32 v184, v44, v184
	v_mul_f32_e32 v185, v44, v185
	v_mul_f32_e32 v186, v44, v186
	v_mul_f32_e32 v187, v44, v187
	ds_write_b128 v210, v[184:187] offset:2048
	v_mul_f32_e32 v188, v45, v188
	v_mul_f32_e32 v189, v45, v189
	v_mul_f32_e32 v190, v45, v190
	v_mul_f32_e32 v191, v45, v191
	ds_write_b128 v210, v[188:191] offset:3072
	v_mul_f32_e32 v192, v46, v192
	v_mul_f32_e32 v193, v46, v193
	v_mul_f32_e32 v194, v46, v194
	v_mul_f32_e32 v195, v46, v195
	ds_write_b128 v210, v[192:195] offset:4096
	v_mul_f32_e32 v196, v47, v196
	v_mul_f32_e32 v197, v47, v197
	v_mul_f32_e32 v198, v47, v198
	v_mul_f32_e32 v199, v47, v199
	ds_write_b128 v210, v[196:199] offset:5120
	v_mul_f32_e32 v200, v48, v200
	v_mul_f32_e32 v201, v48, v201
	v_mul_f32_e32 v202, v48, v202
	v_mul_f32_e32 v203, v48, v203
	ds_write_b128 v210, v[200:203] offset:6144
	v_mul_f32_e32 v204, v49, v204
	v_mul_f32_e32 v205, v49, v205
	v_mul_f32_e32 v206, v49, v206
	v_mul_f32_e32 v207, v49, v207
	ds_write_b128 v210, v[204:207] offset:7168
	s_waitcnt lgkmcnt(0)
	s_barrier
; #define GAS __attribute__((address_space(1)))
; #define LAS __attribute__((address_space(3)))
; #define LDS_WAIT() asm volatile("s_waitcnt lgkmcnt(0)" ::: "memory")
; __device__ __forceinline__ unsigned pk2(float lo, float hi) { return f2bf(lo) | (f2bf(hi) << 16); }
; __device__ __forceinline__ int nat_dim(int p) { return (p >> 1) + 64 * (p & 1); }
; template <int MAP, bool KS, bool KPERM = false>
; __device__ __forceinline__ void p0_transpose_item(const float* W, int K, int Nsrc, int nblk, bf16* WT, const float* ksA, const float* ksB, int ksplit, LAS float* scr, int item, int lane) {
;     const int kb = item / nblk, nb = item % nblk, k0 = 64 * kb, n0 = 32 * nb;
;     const int nr = n0 + (lane & 31); const int sc = MAP == 1 ? src_col_in(nr) : (MAP == 2 ? nat_dim(nr) : nr);
;     float v[32];
; #pragma unroll
;     for (int i = 0; i < 32; ++i) { const int k = k0 + 2 * i + (lane >> 5); const int ksrc = KPERM ? ((k & ~127) + nat_dim(k & 127)) : k;
;         v[i] = sc >= 0 ? W[(size_t)ksrc * Nsrc + sc] : 0.f; }
; #pragma unroll
;     for (int i = 0; i < 32; ++i) { const int kk = 2 * i + (lane >> 5); const int k = k0 + kk;
;         if (KS) v[i] *= (k < ksplit ? ksA[k] : ksB[k - ksplit]);
;         scr[kk * 33 + (lane & 31)] = v[i]; }
;     LDS_WAIT(); asm volatile("" ::: "memory");
;     const int c = lane & 7;
; #pragma unroll
;     for (int j = 0; j < 4; ++j) { const int n = (lane >> 3) + 8 * j; const LAS float* s = scr + (8 * c) * 33 + n;
;         v4u o; o.x = pk2(s[0 * 33], s[1 * 33]); o.y = pk2(s[2 * 33], s[3 * 33]); o.z = pk2(s[4 * 33], s[5 * 33]); o.w = pk2(s[6 * 33], s[7 * 33]);
;         *(GAS v4u*)(WT + (size_t)(n0 + n) * K + k0 + 8 * c) = o; }
;     LDS_WAIT(); asm volatile("" ::: "memory");
; __global__ void __launch_bounds__(NWAVES * 64, 2) hybrid_fwd(Args args) {
;     ...
;             if (r < I_IN) { if (l >= PROJ_F8_FROM) p0_transpose_item_f8<true, 1>(args.in[2] + (size_t)l * DM * NSRC, DM, NSRC, NPROJ / 32, (unsigned char*)(ws + WS_WIN + l * SZ_WIN), WUP8_SCALE, args.in[1] + l * DM, args.in[1] + l * DM, DM, scr, r, lane);
;                 else p0_transpose_item<1, true>(args.in[2] + (size_t)l * DM * NSRC, DM, NSRC, NPROJ / 32, (bf16*)(ws + WS_WIN + l * SZ_WIN), args.in[1] + l * DM, args.in[1] + l * DM, DM, scr, r, lane); continue; } r -= I_IN;
	s_add_i32 s24, s23, 56
	s_lshl_b32 s20, s24, 7
	s_cmp_lt_u32 s24, 40
	s_cselect_b32 s21, 0, 0x830
	s_cmp_lt_u32 s24, 72
	s_cselect_b32 s21, s21, 0xfffff030
	s_add_i32 s20, s20, s21
	s_lshl_b32 s20, s20, 2
	s_add_u32 s8, s46, s20
	s_addc_u32 s9, s47, 0
	global_load_dwordx4 v[176:179], v76, s[8:9]
	s_add_u32 s8, s8, 0x16280
	s_addc_u32 s9, s9, 0
	global_load_dwordx4 v[180:183], v76, s[8:9]
	s_add_u32 s8, s8, 0x16280
	s_addc_u32 s9, s9, 0
	global_load_dwordx4 v[184:187], v76, s[8:9]
	s_add_u32 s8, s8, 0x16280
	s_addc_u32 s9, s9, 0
	global_load_dwordx4 v[188:191], v76, s[8:9]
	s_add_u32 s8, s8, 0x16280
	s_addc_u32 s9, s9, 0
	global_load_dwordx4 v[192:195], v76, s[8:9]
	s_add_u32 s8, s8, 0x16280
	s_addc_u32 s9, s9, 0
	global_load_dwordx4 v[196:199], v76, s[8:9]
	s_add_u32 s8, s8, 0x16280
	s_addc_u32 s9, s9, 0
	global_load_dwordx4 v[200:203], v76, s[8:9]
	s_add_u32 s8, s8, 0x16280
	s_addc_u32 s9, s9, 0
	global_load_dwordx4 v[204:207], v76, s[8:9]
	s_add_i32 s24, s23, 40
	s_mul_i32 s20, s24, 0x100000
	s_add_u32 s6, s48, s20
	s_addc_u32 s7, s49, 0
	s_cmp_lt_u32 s24, 16
	s_cselect_b32 s20, 1, 0
	s_sub_i32 s21, s24, 16
	s_bitcmp0_b32 s21, 2
	s_cselect_b32 s21, 1, 0
	s_cmp_lt_u32 s24, 40
	s_cselect_b32 s21, s21, 0
	s_or_b32 s20, s20, s21
	s_cmp_lg_u32 s20, 0
	s_cselect_b64 s[20:21], -1, 0
	v_cndmask_b32_e64 v91, v83, v87, s[20:21]
	v_cndmask_b32_e64 v92, v84, v88, s[20:21]
	v_cndmask_b32_e64 v93, v85, v89, s[20:21]
	v_cndmask_b32_e64 v94, v86, v90, s[20:21]
	ds_read_b32 v226, v113
	ds_read_b32 v227, v113 offset:512
	ds_read_b32 v228, v113 offset:1024
	ds_read_b32 v229, v113 offset:1536
	ds_read_b32 v230, v113 offset:2048
	ds_read_b32 v231, v113 offset:2560
	ds_read_b32 v232, v113 offset:3072
	ds_read_b32 v233, v113 offset:3584
	s_waitcnt lgkmcnt(0)
	v_bfe_u32 v120, v226, 16, 1
	v_bfe_u32 v121, v227, 16, 1
	v_bfe_u32 v122, v228, 16, 1
	v_bfe_u32 v123, v229, 16, 1
	v_bfe_u32 v124, v230, 16, 1
	v_bfe_u32 v125, v231, 16, 1
	v_bfe_u32 v126, v232, 16, 1
	v_bfe_u32 v127, v233, 16, 1
	v_add3_u32 v226, v226, v120, s63
	v_add3_u32 v227, v227, v121, s63
	v_add3_u32 v228, v228, v122, s63
	v_add3_u32 v229, v229, v123, s63
	v_add3_u32 v230, v230, v124, s63
	v_add3_u32 v231, v231, v125, s63
	v_add3_u32 v232, v232, v126, s63
	v_add3_u32 v233, v233, v127, s63
	v_perm_b32 v242, v227, v226, s64
	v_perm_b32 v243, v229, v228, s64
	v_perm_b32 v244, v231, v230, s64
	v_perm_b32 v245, v233, v232, s64
	s_nop 0
	global_store_dwordx4 v91, v[242:245], s[6:7]
	ds_read_b32 v226, v115
	ds_read_b32 v227, v115 offset:512
	ds_read_b32 v228, v115 offset:1024
	ds_read_b32 v229, v115 offset:1536
	ds_read_b32 v230, v115 offset:2048
	ds_read_b32 v231, v115 offset:2560
	ds_read_b32 v232, v115 offset:3072
	ds_read_b32 v233, v115 offset:3584
	s_waitcnt lgkmcnt(0)
	v_bfe_u32 v120, v226, 16, 1
	v_bfe_u32 v121, v227, 16, 1
	v_bfe_u32 v122, v228, 16, 1
	v_bfe_u32 v123, v229, 16, 1
	v_bfe_u32 v124, v230, 16, 1
	v_bfe_u32 v125, v231, 16, 1
	v_bfe_u32 v126, v232, 16, 1
	v_bfe_u32 v127, v233, 16, 1
	v_add3_u32 v226, v226, v120, s63
	v_add3_u32 v227, v227, v121, s63
	v_add3_u32 v228, v228, v122, s63
	v_add3_u32 v229, v229, v123, s63
	v_add3_u32 v230, v230, v124, s63
	v_add3_u32 v231, v231, v125, s63
	v_add3_u32 v232, v232, v126, s63
	v_add3_u32 v233, v233, v127, s63
	v_perm_b32 v242, v227, v226, s64
	v_perm_b32 v243, v229, v228, s64
	v_perm_b32 v244, v231, v230, s64
	v_perm_b32 v245, v233, v232, s64
	s_nop 0
	global_store_dwordx4 v92, v[242:245], s[6:7]
	ds_read_b32 v226, v117
	ds_read_b32 v227, v117 offset:512
	ds_read_b32 v228, v117 offset:1024
	ds_read_b32 v229, v117 offset:1536
	ds_read_b32 v230, v117 offset:2048
	ds_read_b32 v231, v117 offset:2560
	ds_read_b32 v232, v117 offset:3072
	ds_read_b32 v233, v117 offset:3584
	s_waitcnt lgkmcnt(0)
	v_bfe_u32 v120, v226, 16, 1
	v_bfe_u32 v121, v227, 16, 1
	v_bfe_u32 v122, v228, 16, 1
	v_bfe_u32 v123, v229, 16, 1
	v_bfe_u32 v124, v230, 16, 1
	v_bfe_u32 v125, v231, 16, 1
	v_bfe_u32 v126, v232, 16, 1
	v_bfe_u32 v127, v233, 16, 1
	v_add3_u32 v226, v226, v120, s63
	v_add3_u32 v227, v227, v121, s63
	v_add3_u32 v228, v228, v122, s63
	v_add3_u32 v229, v229, v123, s63
	v_add3_u32 v230, v230, v124, s63
	v_add3_u32 v231, v231, v125, s63
	v_add3_u32 v232, v232, v126, s63
	v_add3_u32 v233, v233, v127, s63
	v_perm_b32 v242, v227, v226, s64
	v_perm_b32 v243, v229, v228, s64
	v_perm_b32 v244, v231, v230, s64
	v_perm_b32 v245, v233, v232, s64
	s_nop 0
	global_store_dwordx4 v93, v[242:245], s[6:7]
	ds_read_b32 v226, v119
	ds_read_b32 v227, v119 offset:512
	ds_read_b32 v228, v119 offset:1024
	ds_read_b32 v229, v119 offset:1536
	ds_read_b32 v230, v119 offset:2048
	ds_read_b32 v231, v119 offset:2560
	ds_read_b32 v232, v119 offset:3072
	ds_read_b32 v233, v119 offset:3584
	s_waitcnt lgkmcnt(0)
	v_bfe_u32 v120, v226, 16, 1
	v_bfe_u32 v121, v227, 16, 1
	v_bfe_u32 v122, v228, 16, 1
	v_bfe_u32 v123, v229, 16, 1
	v_bfe_u32 v124, v230, 16, 1
	v_bfe_u32 v125, v231, 16, 1
	v_bfe_u32 v126, v232, 16, 1
	v_bfe_u32 v127, v233, 16, 1
	v_add3_u32 v226, v226, v120, s63
	v_add3_u32 v227, v227, v121, s63
	v_add3_u32 v228, v228, v122, s63
	v_add3_u32 v229, v229, v123, s63
	v_add3_u32 v230, v230, v124, s63
	v_add3_u32 v231, v231, v125, s63
	v_add3_u32 v232, v232, v126, s63
	v_add3_u32 v233, v233, v127, s63
	v_perm_b32 v242, v227, v226, s64
	v_perm_b32 v243, v229, v228, s64
	v_perm_b32 v244, v231, v230, s64
	v_perm_b32 v245, v233, v232, s64
	s_nop 0
	global_store_dwordx4 v94, v[242:245], s[6:7]
	s_waitcnt vmcnt(16)
	v_mul_f32_e32 v144, v42, v144
	v_mul_f32_e32 v145, v42, v145
	v_mul_f32_e32 v146, v42, v146
	v_mul_f32_e32 v147, v42, v147
	ds_write_b128 v209, v[144:147]
	v_mul_f32_e32 v148, v43, v148
	v_mul_f32_e32 v149, v43, v149
	v_mul_f32_e32 v150, v43, v150
	v_mul_f32_e32 v151, v43, v151
	ds_write_b128 v209, v[148:151] offset:1024
	v_mul_f32_e32 v152, v44, v152
	v_mul_f32_e32 v153, v44, v153
	v_mul_f32_e32 v154, v44, v154
	v_mul_f32_e32 v155, v44, v155
	ds_write_b128 v209, v[152:155] offset:2048
	v_mul_f32_e32 v156, v45, v156
	v_mul_f32_e32 v157, v45, v157
	v_mul_f32_e32 v158, v45, v158
	v_mul_f32_e32 v159, v45, v159
	ds_write_b128 v209, v[156:159] offset:3072
	v_mul_f32_e32 v160, v46, v160
	v_mul_f32_e32 v161, v46, v161
	v_mul_f32_e32 v162, v46, v162
	v_mul_f32_e32 v163, v46, v163
	ds_write_b128 v209, v[160:163] offset:4096
	v_mul_f32_e32 v164, v47, v164
	v_mul_f32_e32 v165, v47, v165
	v_mul_f32_e32 v166, v47, v166
	v_mul_f32_e32 v167, v47, v167
	ds_write_b128 v209, v[164:167] offset:5120
	v_mul_f32_e32 v168, v48, v168
	v_mul_f32_e32 v169, v48, v169
	v_mul_f32_e32 v170, v48, v170
	v_mul_f32_e32 v171, v48, v171
	ds_write_b128 v209, v[168:171] offset:6144
	v_mul_f32_e32 v172, v49, v172
	v_mul_f32_e32 v173, v49, v173
	v_mul_f32_e32 v174, v49, v174
	v_mul_f32_e32 v175, v49, v175
	ds_write_b128 v209, v[172:175] offset:7168
	s_waitcnt lgkmcnt(0)
	s_barrier
; #define GAS __attribute__((address_space(1)))
; #define LAS __attribute__((address_space(3)))
; __device__ __forceinline__ int src_col_in(int c) {
;     if (c < 5120) { const int blk = c >> 7, p = c & 127; const bool rope = blk < 16 || ((((blk - 16) >> 2) & 1) == 0); const int d = rope ? (p >> 1) + 64 * (p & 1) : p; return blk * 128 + d; }
;     if (c < OFF_Z) return c + 2096;
;     if (c < OFF_G) return c - 4048;
; template <int MAP, bool KS, bool KPERM = false>
; __device__ __forceinline__ void p0_transpose_item(const float* W, int K, int Nsrc, int nblk, bf16* WT, const float* ksA, const float* ksB, int ksplit, LAS float* scr, int item, int lane) {
;     const int kb = item / nblk, nb = item % nblk, k0 = 64 * kb, n0 = 32 * nb;
;     const int nr = n0 + (lane & 31); const int sc = MAP == 1 ? src_col_in(nr) : (MAP == 2 ? nat_dim(nr) : nr);
;     float v[32];
; #pragma unroll
;     for (int i = 0; i < 32; ++i) { const int k = k0 + 2 * i + (lane >> 5); const int ksrc = KPERM ? ((k & ~127) + nat_dim(k & 127)) : k;
;         v[i] = sc >= 0 ? W[(size_t)ksrc * Nsrc + sc] : 0.f; }
; #pragma unroll
;     for (int i = 0; i < 32; ++i) { const int kk = 2 * i + (lane >> 5); const int k = k0 + kk;
;         if (KS) v[i] *= (k < ksplit ? ksA[k] : ksB[k - ksplit]);
;         scr[kk * 33 + (lane & 31)] = v[i]; }
;     LDS_WAIT(); asm volatile("" ::: "memory");
;     const int c = lane & 7;
; #pragma unroll
;     for (int j = 0; j < 4; ++j) { const int n = (lane >> 3) + 8 * j; const LAS float* s = scr + (8 * c) * 33 + n;
;         v4u o; o.x = pk2(s[0 * 33], s[1 * 33]); o.y = pk2(s[2 * 33], s[3 * 33]); o.z = pk2(s[4 * 33], s[5 * 33]); o.w = pk2(s[6 * 33], s[7 * 33]);
;         *(GAS v4u*)(WT + (size_t)(n0 + n) * K + k0 + 8 * c) = o; }
;     LDS_WAIT(); asm volatile("" ::: "memory");
; __global__ void __launch_bounds__(NWAVES * 64, 2) hybrid_fwd(Args args) {
;     ...
;             if (r < I_IN) { if (l >= PROJ_F8_FROM) p0_transpose_item_f8<true, 1>(args.in[2] + (size_t)l * DM * NSRC, DM, NSRC, NPROJ / 32, (unsigned char*)(ws + WS_WIN + l * SZ_WIN), WUP8_SCALE, args.in[1] + l * DM, args.in[1] + l * DM, DM, scr, r, lane);
;                 else p0_transpose_item<1, true>(args.in[2] + (size_t)l * DM * NSRC, DM, NSRC, NPROJ / 32, (bf16*)(ws + WS_WIN + l * SZ_WIN), args.in[1] + l * DM, args.in[1] + l * DM, DM, scr, r, lane); continue; } r -= I_IN;
	s_add_i32 s24, s23, 64
	s_lshl_b32 s20, s24, 7
	s_cmp_lt_u32 s24, 40
	s_cselect_b32 s21, 0, 0x830
	s_cmp_lt_u32 s24, 72
	s_cselect_b32 s21, s21, 0xfffff030
	s_add_i32 s20, s20, s21
	s_lshl_b32 s20, s20, 2
	s_add_u32 s8, s46, s20
	s_addc_u32 s9, s47, 0
	global_load_dwordx4 v[144:147], v76, s[8:9]
	s_add_u32 s8, s8, 0x16280
	s_addc_u32 s9, s9, 0
	global_load_dwordx4 v[148:151], v76, s[8:9]
	s_add_u32 s8, s8, 0x16280
	s_addc_u32 s9, s9, 0
	global_load_dwordx4 v[152:155], v76, s[8:9]
	s_add_u32 s8, s8, 0x16280
	s_addc_u32 s9, s9, 0
	global_load_dwordx4 v[156:159], v76, s[8:9]
	s_add_u32 s8, s8, 0x16280
	s_addc_u32 s9, s9, 0
	global_load_dwordx4 v[160:163], v76, s[8:9]
	s_add_u32 s8, s8, 0x16280
	s_addc_u32 s9, s9, 0
	global_load_dwordx4 v[164:167], v76, s[8:9]
	s_add_u32 s8, s8, 0x16280
	s_addc_u32 s9, s9, 0
	global_load_dwordx4 v[168:171], v76, s[8:9]
	s_add_u32 s8, s8, 0x16280
	s_addc_u32 s9, s9, 0
	global_load_dwordx4 v[172:175], v76, s[8:9]
	s_add_i32 s24, s23, 48
	s_mul_i32 s20, s24, 0x100000
	s_add_u32 s6, s48, s20
	s_addc_u32 s7, s49, 0
	s_cmp_lt_u32 s24, 16
	s_cselect_b32 s20, 1, 0
	s_sub_i32 s21, s24, 16
	s_bitcmp0_b32 s21, 2
	s_cselect_b32 s21, 1, 0
	s_cmp_lt_u32 s24, 40
	s_cselect_b32 s21, s21, 0
	s_or_b32 s20, s20, s21
	s_cmp_lg_u32 s20, 0
	s_cselect_b64 s[20:21], -1, 0
	v_cndmask_b32_e64 v91, v83, v87, s[20:21]
	v_cndmask_b32_e64 v92, v84, v88, s[20:21]
	v_cndmask_b32_e64 v93, v85, v89, s[20:21]
	v_cndmask_b32_e64 v94, v86, v90, s[20:21]
	ds_read_b32 v226, v112
	ds_read_b32 v227, v112 offset:512
	ds_read_b32 v228, v112 offset:1024
	ds_read_b32 v229, v112 offset:1536
	ds_read_b32 v230, v112 offset:2048
	ds_read_b32 v231, v112 offset:2560
	ds_read_b32 v232, v112 offset:3072
	ds_read_b32 v233, v112 offset:3584
	s_waitcnt lgkmcnt(0)
	v_bfe_u32 v120, v226, 16, 1
	v_bfe_u32 v121, v227, 16, 1
	v_bfe_u32 v122, v228, 16, 1
	v_bfe_u32 v123, v229, 16, 1
	v_bfe_u32 v124, v230, 16, 1
	v_bfe_u32 v125, v231, 16, 1
	v_bfe_u32 v126, v232, 16, 1
	v_bfe_u32 v127, v233, 16, 1
	v_add3_u32 v226, v226, v120, s63
	v_add3_u32 v227, v227, v121, s63
	v_add3_u32 v228, v228, v122, s63
	v_add3_u32 v229, v229, v123, s63
	v_add3_u32 v230, v230, v124, s63
	v_add3_u32 v231, v231, v125, s63
	v_add3_u32 v232, v232, v126, s63
	v_add3_u32 v233, v233, v127, s63
	v_perm_b32 v242, v227, v226, s64
	v_perm_b32 v243, v229, v228, s64
	v_perm_b32 v244, v231, v230, s64
	v_perm_b32 v245, v233, v232, s64
	s_nop 0
	global_store_dwordx4 v91, v[242:245], s[6:7]
	ds_read_b32 v226, v114
	ds_read_b32 v227, v114 offset:512
	ds_read_b32 v228, v114 offset:1024
	ds_read_b32 v229, v114 offset:1536
	ds_read_b32 v230, v114 offset:2048
	ds_read_b32 v231, v114 offset:2560
	ds_read_b32 v232, v114 offset:3072
	ds_read_b32 v233, v114 offset:3584
	s_waitcnt lgkmcnt(0)
	v_bfe_u32 v120, v226, 16, 1
	v_bfe_u32 v121, v227, 16, 1
	v_bfe_u32 v122, v228, 16, 1
	v_bfe_u32 v123, v229, 16, 1
	v_bfe_u32 v124, v230, 16, 1
	v_bfe_u32 v125, v231, 16, 1
	v_bfe_u32 v126, v232, 16, 1
	v_bfe_u32 v127, v233, 16, 1
	v_add3_u32 v226, v226, v120, s63
	v_add3_u32 v227, v227, v121, s63
	v_add3_u32 v228, v228, v122, s63
	v_add3_u32 v229, v229, v123, s63
	v_add3_u32 v230, v230, v124, s63
	v_add3_u32 v231, v231, v125, s63
	v_add3_u32 v232, v232, v126, s63
	v_add3_u32 v233, v233, v127, s63
	v_perm_b32 v242, v227, v226, s64
	v_perm_b32 v243, v229, v228, s64
	v_perm_b32 v244, v231, v230, s64
	v_perm_b32 v245, v233, v232, s64
	s_nop 0
	global_store_dwordx4 v92, v[242:245], s[6:7]
	ds_read_b32 v226, v116
	ds_read_b32 v227, v116 offset:512
	ds_read_b32 v228, v116 offset:1024
	ds_read_b32 v229, v116 offset:1536
	ds_read_b32 v230, v116 offset:2048
	ds_read_b32 v231, v116 offset:2560
	ds_read_b32 v232, v116 offset:3072
	ds_read_b32 v233, v116 offset:3584
	s_waitcnt lgkmcnt(0)
	v_bfe_u32 v120, v226, 16, 1
	v_bfe_u32 v121, v227, 16, 1
	v_bfe_u32 v122, v228, 16, 1
	v_bfe_u32 v123, v229, 16, 1
	v_bfe_u32 v124, v230, 16, 1
	v_bfe_u32 v125, v231, 16, 1
	v_bfe_u32 v126, v232, 16, 1
	v_bfe_u32 v127, v233, 16, 1
	v_add3_u32 v226, v226, v120, s63
	v_add3_u32 v227, v227, v121, s63
	v_add3_u32 v228, v228, v122, s63
	v_add3_u32 v229, v229, v123, s63
	v_add3_u32 v230, v230, v124, s63
	v_add3_u32 v231, v231, v125, s63
	v_add3_u32 v232, v232, v126, s63
	v_add3_u32 v233, v233, v127, s63
	v_perm_b32 v242, v227, v226, s64
	v_perm_b32 v243, v229, v228, s64
	v_perm_b32 v244, v231, v230, s64
	v_perm_b32 v245, v233, v232, s64
	s_nop 0
	global_store_dwordx4 v93, v[242:245], s[6:7]
	ds_read_b32 v226, v118
	ds_read_b32 v227, v118 offset:512
	ds_read_b32 v228, v118 offset:1024
	ds_read_b32 v229, v118 offset:1536
	ds_read_b32 v230, v118 offset:2048
	ds_read_b32 v231, v118 offset:2560
	ds_read_b32 v232, v118 offset:3072
	ds_read_b32 v233, v118 offset:3584
	s_waitcnt lgkmcnt(0)
	v_bfe_u32 v120, v226, 16, 1
	v_bfe_u32 v121, v227, 16, 1
	v_bfe_u32 v122, v228, 16, 1
	v_bfe_u32 v123, v229, 16, 1
	v_bfe_u32 v124, v230, 16, 1
	v_bfe_u32 v125, v231, 16, 1
	v_bfe_u32 v126, v232, 16, 1
	v_bfe_u32 v127, v233, 16, 1
	v_add3_u32 v226, v226, v120, s63
	v_add3_u32 v227, v227, v121, s63
	v_add3_u32 v228, v228, v122, s63
	v_add3_u32 v229, v229, v123, s63
	v_add3_u32 v230, v230, v124, s63
	v_add3_u32 v231, v231, v125, s63
	v_add3_u32 v232, v232, v126, s63
	v_add3_u32 v233, v233, v127, s63
	v_perm_b32 v242, v227, v226, s64
	v_perm_b32 v243, v229, v228, s64
	v_perm_b32 v244, v231, v230, s64
	v_perm_b32 v245, v233, v232, s64
	s_nop 0
	global_store_dwordx4 v94, v[242:245], s[6:7]
	s_waitcnt vmcnt(16)
	v_mul_f32_e32 v176, v42, v176
	v_mul_f32_e32 v177, v42, v177
	v_mul_f32_e32 v178, v42, v178
	v_mul_f32_e32 v179, v42, v179
	ds_write_b128 v210, v[176:179]
	v_mul_f32_e32 v180, v43, v180
	v_mul_f32_e32 v181, v43, v181
	v_mul_f32_e32 v182, v43, v182
	v_mul_f32_e32 v183, v43, v183
	ds_write_b128 v210, v[180:183] offset:1024
	v_mul_f32_e32 v184, v44, v184
	v_mul_f32_e32 v185, v44, v185
	v_mul_f32_e32 v186, v44, v186
	v_mul_f32_e32 v187, v44, v187
	ds_write_b128 v210, v[184:187] offset:2048
	v_mul_f32_e32 v188, v45, v188
	v_mul_f32_e32 v189, v45, v189
	v_mul_f32_e32 v190, v45, v190
	v_mul_f32_e32 v191, v45, v191
	ds_write_b128 v210, v[188:191] offset:3072
	v_mul_f32_e32 v192, v46, v192
	v_mul_f32_e32 v193, v46, v193
	v_mul_f32_e32 v194, v46, v194
	v_mul_f32_e32 v195, v46, v195
	ds_write_b128 v210, v[192:195] offset:4096
	v_mul_f32_e32 v196, v47, v196
	v_mul_f32_e32 v197, v47, v197
	v_mul_f32_e32 v198, v47, v198
	v_mul_f32_e32 v199, v47, v199
	ds_write_b128 v210, v[196:199] offset:5120
	v_mul_f32_e32 v200, v48, v200
	v_mul_f32_e32 v201, v48, v201
	v_mul_f32_e32 v202, v48, v202
	v_mul_f32_e32 v203, v48, v203
	ds_write_b128 v210, v[200:203] offset:6144
	v_mul_f32_e32 v204, v49, v204
	v_mul_f32_e32 v205, v49, v205
	v_mul_f32_e32 v206, v49, v206
	v_mul_f32_e32 v207, v49, v207
	ds_write_b128 v210, v[204:207] offset:7168
	s_waitcnt lgkmcnt(0)
	s_barrier
; #define GAS __attribute__((address_space(1)))
; #define LAS __attribute__((address_space(3)))
; #define LDS_WAIT() asm volatile("s_waitcnt lgkmcnt(0)" ::: "memory")
; __device__ __forceinline__ unsigned pk2(float lo, float hi) { return f2bf(lo) | (f2bf(hi) << 16); }
; __device__ __forceinline__ int nat_dim(int p) { return (p >> 1) + 64 * (p & 1); }
; __device__ __forceinline__ int src_col_in(int c) {
;     if (c < 5120) { const int blk = c >> 7, p = c & 127; const bool rope = blk < 16 || ((((blk - 16) >> 2) & 1) == 0); const int d = rope ? (p >> 1) + 64 * (p & 1) : p; return blk * 128 + d; }
;     if (c < OFF_Z) return c + 2096;
;     if (c < OFF_G) return c - 4048;
;     if (c < OFF_DT) return 5120 + (c - OFF_G);
;     if (c < NSRC) return c;
;     return -1;
; }
; template <int MAP, bool KS, bool KPERM = false>
; __device__ __forceinline__ void p0_transpose_item(const float* W, int K, int Nsrc, int nblk, bf16* WT, const float* ksA, const float* ksB, int ksplit, LAS float* scr, int item, int lane) {
;     const int kb = item / nblk, nb = item % nblk, k0 = 64 * kb, n0 = 32 * nb;
;     const int nr = n0 + (lane & 31); const int sc = MAP == 1 ? src_col_in(nr) : (MAP == 2 ? nat_dim(nr) : nr);
;     float v[32];
; #pragma unroll
;     for (int i = 0; i < 32; ++i) { const int k = k0 + 2 * i + (lane >> 5); const int ksrc = KPERM ? ((k & ~127) + nat_dim(k & 127)) : k;
;         v[i] = sc >= 0 ? W[(size_t)ksrc * Nsrc + sc] : 0.f; }
; #pragma unroll
;     for (int i = 0; i < 32; ++i) { const int kk = 2 * i + (lane >> 5); const int k = k0 + kk;
;         if (KS) v[i] *= (k < ksplit ? ksA[k] : ksB[k - ksplit]);
;         scr[kk * 33 + (lane & 31)] = v[i]; }
;     LDS_WAIT(); asm volatile("" ::: "memory");
;     const int c = lane & 7;
; #pragma unroll
;     for (int j = 0; j < 4; ++j) { const int n = (lane >> 3) + 8 * j; const LAS float* s = scr + (8 * c) * 33 + n;
;         v4u o; o.x = pk2(s[0 * 33], s[1 * 33]); o.y = pk2(s[2 * 33], s[3 * 33]); o.z = pk2(s[4 * 33], s[5 * 33]); o.w = pk2(s[6 * 33], s[7 * 33]);
;         *(GAS v4u*)(WT + (size_t)(n0 + n) * K + k0 + 8 * c) = o; }
;     LDS_WAIT(); asm volatile("" ::: "memory");
; }
	s_add_i32 s24, s23, 72
	s_lshl_b32 s20, s24, 7
	s_cmp_lt_u32 s24, 40
	s_cselect_b32 s21, 0, 0x830
	s_cmp_lt_u32 s24, 72
	s_cselect_b32 s21, s21, 0xfffff030
	s_add_i32 s20, s20, s21
	s_lshl_b32 s20, s20, 2
	s_add_u32 s8, s46, s20
	s_addc_u32 s9, s47, 0
	global_load_dwordx4 v[176:179], v76, s[8:9]
	s_add_u32 s8, s8, 0x16280
	s_addc_u32 s9, s9, 0
	global_load_dwordx4 v[180:183], v76, s[8:9]
	s_add_u32 s8, s8, 0x16280
	s_addc_u32 s9, s9, 0
	global_load_dwordx4 v[184:187], v76, s[8:9]
	s_add_u32 s8, s8, 0x16280
	s_addc_u32 s9, s9, 0
	global_load_dwordx4 v[188:191], v76, s[8:9]
	s_add_u32 s8, s8, 0x16280
	s_addc_u32 s9, s9, 0
	global_load_dwordx4 v[192:195], v76, s[8:9]
	s_add_u32 s8, s8, 0x16280
	s_addc_u32 s9, s9, 0
	global_load_dwordx4 v[196:199], v76, s[8:9]
	s_add_u32 s8, s8, 0x16280
	s_addc_u32 s9, s9, 0
	global_load_dwordx4 v[200:203], v76, s[8:9]
	s_add_u32 s8, s8, 0x16280
	s_addc_u32 s9, s9, 0
	global_load_dwordx4 v[204:207], v76, s[8:9]
	s_add_i32 s24, s23, 56
	s_mul_i32 s20, s24, 0x100000
	s_add_u32 s6, s48, s20
	s_addc_u32 s7, s49, 0
	s_cmp_lt_u32 s24, 16
	s_cselect_b32 s20, 1, 0
	s_sub_i32 s21, s24, 16
	s_bitcmp0_b32 s21, 2
	s_cselect_b32 s21, 1, 0
	s_cmp_lt_u32 s24, 40
	s_cselect_b32 s21, s21, 0
	s_or_b32 s20, s20, s21
	s_cmp_lg_u32 s20, 0
	s_cselect_b64 s[20:21], -1, 0
	v_cndmask_b32_e64 v91, v83, v87, s[20:21]
	v_cndmask_b32_e64 v92, v84, v88, s[20:21]
	v_cndmask_b32_e64 v93, v85, v89, s[20:21]
	v_cndmask_b32_e64 v94, v86, v90, s[20:21]
	ds_read_b32 v226, v113
	ds_read_b32 v227, v113 offset:512
	ds_read_b32 v228, v113 offset:1024
	ds_read_b32 v229, v113 offset:1536
	ds_read_b32 v230, v113 offset:2048
	ds_read_b32 v231, v113 offset:2560
	ds_read_b32 v232, v113 offset:3072
	ds_read_b32 v233, v113 offset:3584
	s_waitcnt lgkmcnt(0)
	v_bfe_u32 v120, v226, 16, 1
	v_bfe_u32 v121, v227, 16, 1
	v_bfe_u32 v122, v228, 16, 1
	v_bfe_u32 v123, v229, 16, 1
	v_bfe_u32 v124, v230, 16, 1
	v_bfe_u32 v125, v231, 16, 1
	v_bfe_u32 v126, v232, 16, 1
	v_bfe_u32 v127, v233, 16, 1
	v_add3_u32 v226, v226, v120, s63
	v_add3_u32 v227, v227, v121, s63
	v_add3_u32 v228, v228, v122, s63
	v_add3_u32 v229, v229, v123, s63
	v_add3_u32 v230, v230, v124, s63
	v_add3_u32 v231, v231, v125, s63
	v_add3_u32 v232, v232, v126, s63
	v_add3_u32 v233, v233, v127, s63
	v_perm_b32 v242, v227, v226, s64
	v_perm_b32 v243, v229, v228, s64
	v_perm_b32 v244, v231, v230, s64
	v_perm_b32 v245, v233, v232, s64
	s_nop 0
	global_store_dwordx4 v91, v[242:245], s[6:7]
	ds_read_b32 v226, v115
	ds_read_b32 v227, v115 offset:512
	ds_read_b32 v228, v115 offset:1024
	ds_read_b32 v229, v115 offset:1536
	ds_read_b32 v230, v115 offset:2048
	ds_read_b32 v231, v115 offset:2560
	ds_read_b32 v232, v115 offset:3072
	ds_read_b32 v233, v115 offset:3584
	s_waitcnt lgkmcnt(0)
	v_bfe_u32 v120, v226, 16, 1
	v_bfe_u32 v121, v227, 16, 1
	v_bfe_u32 v122, v228, 16, 1
	v_bfe_u32 v123, v229, 16, 1
	v_bfe_u32 v124, v230, 16, 1
	v_bfe_u32 v125, v231, 16, 1
	v_bfe_u32 v126, v232, 16, 1
	v_bfe_u32 v127, v233, 16, 1
	v_add3_u32 v226, v226, v120, s63
	v_add3_u32 v227, v227, v121, s63
	v_add3_u32 v228, v228, v122, s63
	v_add3_u32 v229, v229, v123, s63
	v_add3_u32 v230, v230, v124, s63
	v_add3_u32 v231, v231, v125, s63
	v_add3_u32 v232, v232, v126, s63
	v_add3_u32 v233, v233, v127, s63
	v_perm_b32 v242, v227, v226, s64
	v_perm_b32 v243, v229, v228, s64
	v_perm_b32 v244, v231, v230, s64
	v_perm_b32 v245, v233, v232, s64
	s_nop 0
	global_store_dwordx4 v92, v[242:245], s[6:7]
	ds_read_b32 v226, v117
	ds_read_b32 v227, v117 offset:512
	ds_read_b32 v228, v117 offset:1024
	ds_read_b32 v229, v117 offset:1536
	ds_read_b32 v230, v117 offset:2048
	ds_read_b32 v231, v117 offset:2560
	ds_read_b32 v232, v117 offset:3072
	ds_read_b32 v233, v117 offset:3584
	s_waitcnt lgkmcnt(0)
	v_bfe_u32 v120, v226, 16, 1
	v_bfe_u32 v121, v227, 16, 1
	v_bfe_u32 v122, v228, 16, 1
	v_bfe_u32 v123, v229, 16, 1
	v_bfe_u32 v124, v230, 16, 1
	v_bfe_u32 v125, v231, 16, 1
	v_bfe_u32 v126, v232, 16, 1
	v_bfe_u32 v127, v233, 16, 1
	v_add3_u32 v226, v226, v120, s63
	v_add3_u32 v227, v227, v121, s63
	v_add3_u32 v228, v228, v122, s63
	v_add3_u32 v229, v229, v123, s63
	v_add3_u32 v230, v230, v124, s63
	v_add3_u32 v231, v231, v125, s63
	v_add3_u32 v232, v232, v126, s63
	v_add3_u32 v233, v233, v127, s63
	v_perm_b32 v242, v227, v226, s64
	v_perm_b32 v243, v229, v228, s64
	v_perm_b32 v244, v231, v230, s64
	v_perm_b32 v245, v233, v232, s64
	s_nop 0
	global_store_dwordx4 v93, v[242:245], s[6:7]
	ds_read_b32 v226, v119
	ds_read_b32 v227, v119 offset:512
	ds_read_b32 v228, v119 offset:1024
	ds_read_b32 v229, v119 offset:1536
	ds_read_b32 v230, v119 offset:2048
	ds_read_b32 v231, v119 offset:2560
	ds_read_b32 v232, v119 offset:3072
	ds_read_b32 v233, v119 offset:3584
	s_waitcnt lgkmcnt(0)
	v_bfe_u32 v120, v226, 16, 1
	v_bfe_u32 v121, v227, 16, 1
	v_bfe_u32 v122, v228, 16, 1
	v_bfe_u32 v123, v229, 16, 1
	v_bfe_u32 v124, v230, 16, 1
	v_bfe_u32 v125, v231, 16, 1
	v_bfe_u32 v126, v232, 16, 1
	v_bfe_u32 v127, v233, 16, 1
	v_add3_u32 v226, v226, v120, s63
	v_add3_u32 v227, v227, v121, s63
	v_add3_u32 v228, v228, v122, s63
	v_add3_u32 v229, v229, v123, s63
	v_add3_u32 v230, v230, v124, s63
	v_add3_u32 v231, v231, v125, s63
	v_add3_u32 v232, v232, v126, s63
	v_add3_u32 v233, v233, v127, s63
	v_perm_b32 v242, v227, v226, s64
	v_perm_b32 v243, v229, v228, s64
	v_perm_b32 v244, v231, v230, s64
	v_perm_b32 v245, v233, v232, s64
	s_nop 0
	global_store_dwordx4 v94, v[242:245], s[6:7]
	s_waitcnt vmcnt(16)
	v_mul_f32_e32 v144, v42, v144
	v_mul_f32_e32 v145, v42, v145
	v_mul_f32_e32 v146, v42, v146
	v_mul_f32_e32 v147, v42, v147
	ds_write_b128 v209, v[144:147]
	v_mul_f32_e32 v148, v43, v148
	v_mul_f32_e32 v149, v43, v149
	v_mul_f32_e32 v150, v43, v150
	v_mul_f32_e32 v151, v43, v151
	ds_write_b128 v209, v[148:151] offset:1024
	v_mul_f32_e32 v152, v44, v152
	v_mul_f32_e32 v153, v44, v153
	v_mul_f32_e32 v154, v44, v154
	v_mul_f32_e32 v155, v44, v155
	ds_write_b128 v209, v[152:155] offset:2048
	v_mul_f32_e32 v156, v45, v156
	v_mul_f32_e32 v157, v45, v157
	v_mul_f32_e32 v158, v45, v158
	v_mul_f32_e32 v159, v45, v159
	ds_write_b128 v209, v[156:159] offset:3072
	v_mul_f32_e32 v160, v46, v160
	v_mul_f32_e32 v161, v46, v161
	v_mul_f32_e32 v162, v46, v162
	v_mul_f32_e32 v163, v46, v163
	ds_write_b128 v209, v[160:163] offset:4096
	v_mul_f32_e32 v164, v47, v164
	v_mul_f32_e32 v165, v47, v165
	v_mul_f32_e32 v166, v47, v166
	v_mul_f32_e32 v167, v47, v167
	ds_write_b128 v209, v[164:167] offset:5120
	v_mul_f32_e32 v168, v48, v168
	v_mul_f32_e32 v169, v48, v169
	v_mul_f32_e32 v170, v48, v170
	v_mul_f32_e32 v171, v48, v171
	ds_write_b128 v209, v[168:171] offset:6144
	v_mul_f32_e32 v172, v49, v172
	v_mul_f32_e32 v173, v49, v173
	v_mul_f32_e32 v174, v49, v174
	v_mul_f32_e32 v175, v49, v175
	ds_write_b128 v209, v[172:175] offset:7168
	s_waitcnt lgkmcnt(0)
	s_barrier
; #define GAS __attribute__((address_space(1)))
; #define LAS __attribute__((address_space(3)))
; #define LDS_WAIT() asm volatile("s_waitcnt lgkmcnt(0)" ::: "memory")
; __device__ __forceinline__ unsigned pk2(float lo, float hi) { return f2bf(lo) | (f2bf(hi) << 16); }
; __device__ __forceinline__ int nat_dim(int p) { return (p >> 1) + 64 * (p & 1); }
; __device__ __forceinline__ int src_col_in(int c) {
;     if (c < 5120) { const int blk = c >> 7, p = c & 127; const bool rope = blk < 16 || ((((blk - 16) >> 2) & 1) == 0); const int d = rope ? (p >> 1) + 64 * (p & 1) : p; return blk * 128 + d; }
;     if (c < OFF_Z) return c + 2096;
;     if (c < OFF_G) return c - 4048;
;     if (c < OFF_DT) return 5120 + (c - OFF_G);
;     if (c < NSRC) return c;
;     return -1;
; }
; template <int MAP, bool KS, bool KPERM = false>
; __device__ __forceinline__ void p0_transpose_item(const float* W, int K, int Nsrc, int nblk, bf16* WT, const float* ksA, const float* ksB, int ksplit, LAS float* scr, int item, int lane) {
;     const int kb = item / nblk, nb = item % nblk, k0 = 64 * kb, n0 = 32 * nb;
;     const int nr = n0 + (lane & 31); const int sc = MAP == 1 ? src_col_in(nr) : (MAP == 2 ? nat_dim(nr) : nr);
;     float v[32];
; #pragma unroll
;     for (int i = 0; i < 32; ++i) { const int k = k0 + 2 * i + (lane >> 5); const int ksrc = KPERM ? ((k & ~127) + nat_dim(k & 127)) : k;
;         v[i] = sc >= 0 ? W[(size_t)ksrc * Nsrc + sc] : 0.f; }
; #pragma unroll
;     for (int i = 0; i < 32; ++i) { const int kk = 2 * i + (lane >> 5); const int k = k0 + kk;
;         if (KS) v[i] *= (k < ksplit ? ksA[k] : ksB[k - ksplit]);
;         scr[kk * 33 + (lane & 31)] = v[i]; }
;     LDS_WAIT(); asm volatile("" ::: "memory");
;     const int c = lane & 7;
; #pragma unroll
;     for (int j = 0; j < 4; ++j) { const int n = (lane >> 3) + 8 * j; const LAS float* s = scr + (8 * c) * 33 + n;
;         v4u o; o.x = pk2(s[0 * 33], s[1 * 33]); o.y = pk2(s[2 * 33], s[3 * 33]); o.z = pk2(s[4 * 33], s[5 * 33]); o.w = pk2(s[6 * 33], s[7 * 33]);
;         *(GAS v4u*)(WT + (size_t)(n0 + n) * K + k0 + 8 * c) = o; }
;     LDS_WAIT(); asm volatile("" ::: "memory");
; }
	s_add_i32 s24, s23, 80
	s_lshl_b32 s20, s24, 7
	s_cmp_lt_u32 s24, 40
	s_cselect_b32 s21, 0, 0x830
	s_cmp_lt_u32 s24, 72
	s_cselect_b32 s21, s21, 0xfffff030
	s_add_i32 s20, s20, s21
	s_lshl_b32 s20, s20, 2
	s_add_u32 s8, s46, s20
	s_addc_u32 s9, s47, 0
	global_load_dwordx4 v[144:147], v76, s[8:9]
	s_add_u32 s8, s8, 0x16280
	s_addc_u32 s9, s9, 0
	global_load_dwordx4 v[148:151], v76, s[8:9]
	s_add_u32 s8, s8, 0x16280
	s_addc_u32 s9, s9, 0
	global_load_dwordx4 v[152:155], v76, s[8:9]
	s_add_u32 s8, s8, 0x16280
	s_addc_u32 s9, s9, 0
	global_load_dwordx4 v[156:159], v76, s[8:9]
	s_add_u32 s8, s8, 0x16280
	s_addc_u32 s9, s9, 0
	global_load_dwordx4 v[160:163], v76, s[8:9]
	s_add_u32 s8, s8, 0x16280
	s_addc_u32 s9, s9, 0
	global_load_dwordx4 v[164:167], v76, s[8:9]
	s_add_u32 s8, s8, 0x16280
	s_addc_u32 s9, s9, 0
	global_load_dwordx4 v[168:171], v76, s[8:9]
	s_add_u32 s8, s8, 0x16280
	s_addc_u32 s9, s9, 0
	global_load_dwordx4 v[172:175], v76, s[8:9]
	s_add_i32 s24, s23, 64
	s_mul_i32 s20, s24, 0x100000
	s_add_u32 s6, s48, s20
	s_addc_u32 s7, s49, 0
	s_cmp_lt_u32 s24, 16
	s_cselect_b32 s20, 1, 0
	s_sub_i32 s21, s24, 16
	s_bitcmp0_b32 s21, 2
	s_cselect_b32 s21, 1, 0
	s_cmp_lt_u32 s24, 40
	s_cselect_b32 s21, s21, 0
	s_or_b32 s20, s20, s21
	s_cmp_lg_u32 s20, 0
	s_cselect_b64 s[20:21], -1, 0
	v_cndmask_b32_e64 v91, v83, v87, s[20:21]
	v_cndmask_b32_e64 v92, v84, v88, s[20:21]
	v_cndmask_b32_e64 v93, v85, v89, s[20:21]
	v_cndmask_b32_e64 v94, v86, v90, s[20:21]
	ds_read_b32 v226, v112
	ds_read_b32 v227, v112 offset:512
	ds_read_b32 v228, v112 offset:1024
	ds_read_b32 v229, v112 offset:1536
	ds_read_b32 v230, v112 offset:2048
	ds_read_b32 v231, v112 offset:2560
	ds_read_b32 v232, v112 offset:3072
	ds_read_b32 v233, v112 offset:3584
	s_waitcnt lgkmcnt(0)
	v_bfe_u32 v120, v226, 16, 1
	v_bfe_u32 v121, v227, 16, 1
	v_bfe_u32 v122, v228, 16, 1
	v_bfe_u32 v123, v229, 16, 1
	v_bfe_u32 v124, v230, 16, 1
	v_bfe_u32 v125, v231, 16, 1
	v_bfe_u32 v126, v232, 16, 1
	v_bfe_u32 v127, v233, 16, 1
	v_add3_u32 v226, v226, v120, s63
	v_add3_u32 v227, v227, v121, s63
	v_add3_u32 v228, v228, v122, s63
	v_add3_u32 v229, v229, v123, s63
	v_add3_u32 v230, v230, v124, s63
	v_add3_u32 v231, v231, v125, s63
	v_add3_u32 v232, v232, v126, s63
	v_add3_u32 v233, v233, v127, s63
	v_perm_b32 v242, v227, v226, s64
	v_perm_b32 v243, v229, v228, s64
	v_perm_b32 v244, v231, v230, s64
	v_perm_b32 v245, v233, v232, s64
	s_nop 0
	global_store_dwordx4 v91, v[242:245], s[6:7]
	ds_read_b32 v226, v114
	ds_read_b32 v227, v114 offset:512
	ds_read_b32 v228, v114 offset:1024
	ds_read_b32 v229, v114 offset:1536
	ds_read_b32 v230, v114 offset:2048
	ds_read_b32 v231, v114 offset:2560
	ds_read_b32 v232, v114 offset:3072
	ds_read_b32 v233, v114 offset:3584
	s_waitcnt lgkmcnt(0)
	v_bfe_u32 v120, v226, 16, 1
	v_bfe_u32 v121, v227, 16, 1
	v_bfe_u32 v122, v228, 16, 1
	v_bfe_u32 v123, v229, 16, 1
	v_bfe_u32 v124, v230, 16, 1
	v_bfe_u32 v125, v231, 16, 1
	v_bfe_u32 v126, v232, 16, 1
	v_bfe_u32 v127, v233, 16, 1
	v_add3_u32 v226, v226, v120, s63
	v_add3_u32 v227, v227, v121, s63
	v_add3_u32 v228, v228, v122, s63
	v_add3_u32 v229, v229, v123, s63
	v_add3_u32 v230, v230, v124, s63
	v_add3_u32 v231, v231, v125, s63
	v_add3_u32 v232, v232, v126, s63
	v_add3_u32 v233, v233, v127, s63
	v_perm_b32 v242, v227, v226, s64
	v_perm_b32 v243, v229, v228, s64
	v_perm_b32 v244, v231, v230, s64
	v_perm_b32 v245, v233, v232, s64
	s_nop 0
	global_store_dwordx4 v92, v[242:245], s[6:7]
	ds_read_b32 v226, v116
	ds_read_b32 v227, v116 offset:512
	ds_read_b32 v228, v116 offset:1024
	ds_read_b32 v229, v116 offset:1536
	ds_read_b32 v230, v116 offset:2048
	ds_read_b32 v231, v116 offset:2560
	ds_read_b32 v232, v116 offset:3072
	ds_read_b32 v233, v116 offset:3584
	s_waitcnt lgkmcnt(0)
	v_bfe_u32 v120, v226, 16, 1
	v_bfe_u32 v121, v227, 16, 1
	v_bfe_u32 v122, v228, 16, 1
	v_bfe_u32 v123, v229, 16, 1
	v_bfe_u32 v124, v230, 16, 1
	v_bfe_u32 v125, v231, 16, 1
	v_bfe_u32 v126, v232, 16, 1
	v_bfe_u32 v127, v233, 16, 1
	v_add3_u32 v226, v226, v120, s63
	v_add3_u32 v227, v227, v121, s63
	v_add3_u32 v228, v228, v122, s63
	v_add3_u32 v229, v229, v123, s63
	v_add3_u32 v230, v230, v124, s63
	v_add3_u32 v231, v231, v125, s63
	v_add3_u32 v232, v232, v126, s63
	v_add3_u32 v233, v233, v127, s63
	v_perm_b32 v242, v227, v226, s64
	v_perm_b32 v243, v229, v228, s64
	v_perm_b32 v244, v231, v230, s64
	v_perm_b32 v245, v233, v232, s64
	s_nop 0
	global_store_dwordx4 v93, v[242:245], s[6:7]
	ds_read_b32 v226, v118
	ds_read_b32 v227, v118 offset:512
	ds_read_b32 v228, v118 offset:1024
	ds_read_b32 v229, v118 offset:1536
	ds_read_b32 v230, v118 offset:2048
	ds_read_b32 v231, v118 offset:2560
	ds_read_b32 v232, v118 offset:3072
	ds_read_b32 v233, v118 offset:3584
	s_waitcnt lgkmcnt(0)
	v_bfe_u32 v120, v226, 16, 1
	v_bfe_u32 v121, v227, 16, 1
	v_bfe_u32 v122, v228, 16, 1
	v_bfe_u32 v123, v229, 16, 1
	v_bfe_u32 v124, v230, 16, 1
	v_bfe_u32 v125, v231, 16, 1
	v_bfe_u32 v126, v232, 16, 1
	v_bfe_u32 v127, v233, 16, 1
	v_add3_u32 v226, v226, v120, s63
	v_add3_u32 v227, v227, v121, s63
	v_add3_u32 v228, v228, v122, s63
	v_add3_u32 v229, v229, v123, s63
	v_add3_u32 v230, v230, v124, s63
	v_add3_u32 v231, v231, v125, s63
	v_add3_u32 v232, v232, v126, s63
	v_add3_u32 v233, v233, v127, s63
	v_perm_b32 v242, v227, v226, s64
	v_perm_b32 v243, v229, v228, s64
	v_perm_b32 v244, v231, v230, s64
	v_perm_b32 v245, v233, v232, s64
	s_nop 0
	global_store_dwordx4 v94, v[242:245], s[6:7]
	s_waitcnt vmcnt(16)
	v_mul_f32_e32 v176, v42, v176
	v_mul_f32_e32 v177, v42, v177
	v_mul_f32_e32 v178, v42, v178
	v_mul_f32_e32 v179, v42, v179
	ds_write_b128 v210, v[176:179]
	v_mul_f32_e32 v180, v43, v180
	v_mul_f32_e32 v181, v43, v181
	v_mul_f32_e32 v182, v43, v182
	v_mul_f32_e32 v183, v43, v183
	ds_write_b128 v210, v[180:183] offset:1024
	v_mul_f32_e32 v184, v44, v184
	v_mul_f32_e32 v185, v44, v185
	v_mul_f32_e32 v186, v44, v186
	v_mul_f32_e32 v187, v44, v187
	ds_write_b128 v210, v[184:187] offset:2048
	v_mul_f32_e32 v188, v45, v188
	v_mul_f32_e32 v189, v45, v189
	v_mul_f32_e32 v190, v45, v190
	v_mul_f32_e32 v191, v45, v191
	ds_write_b128 v210, v[188:191] offset:3072
	v_mul_f32_e32 v192, v46, v192
	v_mul_f32_e32 v193, v46, v193
	v_mul_f32_e32 v194, v46, v194
	v_mul_f32_e32 v195, v46, v195
	ds_write_b128 v210, v[192:195] offset:4096
	v_mul_f32_e32 v196, v47, v196
	v_mul_f32_e32 v197, v47, v197
	v_mul_f32_e32 v198, v47, v198
	v_mul_f32_e32 v199, v47, v199
	ds_write_b128 v210, v[196:199] offset:5120
	v_mul_f32_e32 v200, v48, v200
	v_mul_f32_e32 v201, v48, v201
	v_mul_f32_e32 v202, v48, v202
	v_mul_f32_e32 v203, v48, v203
	ds_write_b128 v210, v[200:203] offset:6144
	v_mul_f32_e32 v204, v49, v204
	v_mul_f32_e32 v205, v49, v205
	v_mul_f32_e32 v206, v49, v206
	v_mul_f32_e32 v207, v49, v207
	ds_write_b128 v210, v[204:207] offset:7168
	s_waitcnt lgkmcnt(0)
	s_barrier
; #define GAS __attribute__((address_space(1)))
; #define LAS __attribute__((address_space(3)))
; #define LDS_WAIT() asm volatile("s_waitcnt lgkmcnt(0)" ::: "memory")
; __device__ __forceinline__ unsigned pk2(float lo, float hi) { return f2bf(lo) | (f2bf(hi) << 16); }
; __device__ __forceinline__ int nat_dim(int p) { return (p >> 1) + 64 * (p & 1); }
; template <int MAP, bool KS, bool KPERM = false>
; __device__ __forceinline__ void p0_transpose_item(const float* W, int K, int Nsrc, int nblk, bf16* WT, const float* ksA, const float* ksB, int ksplit, LAS float* scr, int item, int lane) {
;     const int kb = item / nblk, nb = item % nblk, k0 = 64 * kb, n0 = 32 * nb;
;     const int nr = n0 + (lane & 31); const int sc = MAP == 1 ? src_col_in(nr) : (MAP == 2 ? nat_dim(nr) : nr);
;     float v[32];
; #pragma unroll
;     for (int i = 0; i < 32; ++i) { const int k = k0 + 2 * i + (lane >> 5); const int ksrc = KPERM ? ((k & ~127) + nat_dim(k & 127)) : k;
;         v[i] = sc >= 0 ? W[(size_t)ksrc * Nsrc + sc] : 0.f; }
; #pragma unroll
;     for (int i = 0; i < 32; ++i) { const int kk = 2 * i + (lane >> 5); const int k = k0 + kk;
;         if (KS) v[i] *= (k < ksplit ? ksA[k] : ksB[k - ksplit]);
;         scr[kk * 33 + (lane & 31)] = v[i]; }
;     LDS_WAIT(); asm volatile("" ::: "memory");
;     const int c = lane & 7;
; #pragma unroll
;     for (int j = 0; j < 4; ++j) { const int n = (lane >> 3) + 8 * j; const LAS float* s = scr + (8 * c) * 33 + n;
;         v4u o; o.x = pk2(s[0 * 33], s[1 * 33]); o.y = pk2(s[2 * 33], s[3 * 33]); o.z = pk2(s[4 * 33], s[5 * 33]); o.w = pk2(s[6 * 33], s[7 * 33]);
;         *(GAS v4u*)(WT + (size_t)(n0 + n) * K + k0 + 8 * c) = o; }
;     LDS_WAIT(); asm volatile("" ::: "memory");
; }
;     const int pr = item >> 1, kb = 2 * (pr / nblk) + (item & 1), nb = pr % nblk, k0 = 64 * kb, n0 = 32 * nb;
;     const int nr = n0 + (lane & 31); const int sc = MAP == 1 ? src_col_in(nr) : nr;
;     float v[32];
; #pragma unroll
;     for (int i = 0; i < 32; ++i) v[i] = sc >= 0 ? W[(size_t)(k0 + 2 * i + (lane >> 5)) * Nsrc + sc] : 0.f;
; #pragma unroll
;     for (int i = 0; i < 32; ++i) { const int k = k0 + 2 * i + (lane >> 5); float x = v[i] * wscale; if (KS) x *= (k < ksplit ? ksA[k] : ksB[k - ksplit]); scr[(2 * i + (lane >> 5)) * 33 + (lane & 31)] = x; }
	s_add_i32 s24, s23, 0
	s_lshl_b32 s20, s24, 7
	s_cmp_lt_u32 s24, 40
	s_cselect_b32 s21, 0, 0x830
	s_cmp_lt_u32 s24, 72
	s_cselect_b32 s21, s21, 0xfffff030
	s_add_i32 s20, s20, s21
	s_lshl_b32 s20, s20, 2
	s_add_u32 s8, s50, s20
	s_addc_u32 s9, s51, 0
	global_load_dwordx4 v[176:179], v76, s[8:9]
	s_add_u32 s8, s8, 0x16280
	s_addc_u32 s9, s9, 0
	global_load_dwordx4 v[180:183], v76, s[8:9]
	s_add_u32 s8, s8, 0x16280
	s_addc_u32 s9, s9, 0
	global_load_dwordx4 v[184:187], v76, s[8:9]
	s_add_u32 s8, s8, 0x16280
	s_addc_u32 s9, s9, 0
	global_load_dwordx4 v[188:191], v76, s[8:9]
	s_add_u32 s8, s8, 0x16280
	s_addc_u32 s9, s9, 0
	global_load_dwordx4 v[192:195], v76, s[8:9]
	s_add_u32 s8, s8, 0x16280
	s_addc_u32 s9, s9, 0
	global_load_dwordx4 v[196:199], v76, s[8:9]
	s_add_u32 s8, s8, 0x16280
	s_addc_u32 s9, s9, 0
	global_load_dwordx4 v[200:203], v76, s[8:9]
	s_add_u32 s8, s8, 0x16280
	s_addc_u32 s9, s9, 0
	global_load_dwordx4 v[204:207], v76, s[8:9]
	s_add_i32 s24, s23, 72
	s_mul_i32 s20, s24, 0x100000
	s_add_u32 s6, s48, s20
	s_addc_u32 s7, s49, 0
	s_cmp_lt_u32 s24, 16
	s_cselect_b32 s20, 1, 0
	s_sub_i32 s21, s24, 16
	s_bitcmp0_b32 s21, 2
	s_cselect_b32 s21, 1, 0
	s_cmp_lt_u32 s24, 40
	s_cselect_b32 s21, s21, 0
	s_or_b32 s20, s20, s21
	s_cmp_lg_u32 s20, 0
	s_cselect_b64 s[20:21], -1, 0
	v_cndmask_b32_e64 v91, v83, v87, s[20:21]
	v_cndmask_b32_e64 v92, v84, v88, s[20:21]
	v_cndmask_b32_e64 v93, v85, v89, s[20:21]
	v_cndmask_b32_e64 v94, v86, v90, s[20:21]
	ds_read_b32 v226, v113
	ds_read_b32 v227, v113 offset:512
	ds_read_b32 v228, v113 offset:1024
	ds_read_b32 v229, v113 offset:1536
	ds_read_b32 v230, v113 offset:2048
	ds_read_b32 v231, v113 offset:2560
	ds_read_b32 v232, v113 offset:3072
	ds_read_b32 v233, v113 offset:3584
	s_waitcnt lgkmcnt(0)
	v_bfe_u32 v120, v226, 16, 1
	v_bfe_u32 v121, v227, 16, 1
	v_bfe_u32 v122, v228, 16, 1
	v_bfe_u32 v123, v229, 16, 1
	v_bfe_u32 v124, v230, 16, 1
	v_bfe_u32 v125, v231, 16, 1
	v_bfe_u32 v126, v232, 16, 1
	v_bfe_u32 v127, v233, 16, 1
	v_add3_u32 v226, v226, v120, s63
	v_add3_u32 v227, v227, v121, s63
	v_add3_u32 v228, v228, v122, s63
	v_add3_u32 v229, v229, v123, s63
	v_add3_u32 v230, v230, v124, s63
	v_add3_u32 v231, v231, v125, s63
	v_add3_u32 v232, v232, v126, s63
	v_add3_u32 v233, v233, v127, s63
	v_perm_b32 v242, v227, v226, s64
	v_perm_b32 v243, v229, v228, s64
	v_perm_b32 v244, v231, v230, s64
	v_perm_b32 v245, v233, v232, s64
	s_nop 0
	global_store_dwordx4 v91, v[242:245], s[6:7]
	ds_read_b32 v226, v115
	ds_read_b32 v227, v115 offset:512
	ds_read_b32 v228, v115 offset:1024
	ds_read_b32 v229, v115 offset:1536
	ds_read_b32 v230, v115 offset:2048
	ds_read_b32 v231, v115 offset:2560
	ds_read_b32 v232, v115 offset:3072
	ds_read_b32 v233, v115 offset:3584
	s_waitcnt lgkmcnt(0)
	v_bfe_u32 v120, v226, 16, 1
	v_bfe_u32 v121, v227, 16, 1
	v_bfe_u32 v122, v228, 16, 1
	v_bfe_u32 v123, v229, 16, 1
	v_bfe_u32 v124, v230, 16, 1
	v_bfe_u32 v125, v231, 16, 1
	v_bfe_u32 v126, v232, 16, 1
	v_bfe_u32 v127, v233, 16, 1
	v_add3_u32 v226, v226, v120, s63
	v_add3_u32 v227, v227, v121, s63
	v_add3_u32 v228, v228, v122, s63
	v_add3_u32 v229, v229, v123, s63
	v_add3_u32 v230, v230, v124, s63
	v_add3_u32 v231, v231, v125, s63
	v_add3_u32 v232, v232, v126, s63
	v_add3_u32 v233, v233, v127, s63
	v_perm_b32 v242, v227, v226, s64
	v_perm_b32 v243, v229, v228, s64
	v_perm_b32 v244, v231, v230, s64
	v_perm_b32 v245, v233, v232, s64
	s_nop 0
	global_store_dwordx4 v92, v[242:245], s[6:7]
	ds_read_b32 v226, v117
	ds_read_b32 v227, v117 offset:512
	ds_read_b32 v228, v117 offset:1024
	ds_read_b32 v229, v117 offset:1536
	ds_read_b32 v230, v117 offset:2048
	ds_read_b32 v231, v117 offset:2560
	ds_read_b32 v232, v117 offset:3072
	ds_read_b32 v233, v117 offset:3584
	s_waitcnt lgkmcnt(0)
	v_bfe_u32 v120, v226, 16, 1
	v_bfe_u32 v121, v227, 16, 1
	v_bfe_u32 v122, v228, 16, 1
	v_bfe_u32 v123, v229, 16, 1
	v_bfe_u32 v124, v230, 16, 1
	v_bfe_u32 v125, v231, 16, 1
	v_bfe_u32 v126, v232, 16, 1
	v_bfe_u32 v127, v233, 16, 1
	v_add3_u32 v226, v226, v120, s63
	v_add3_u32 v227, v227, v121, s63
	v_add3_u32 v228, v228, v122, s63
	v_add3_u32 v229, v229, v123, s63
	v_add3_u32 v230, v230, v124, s63
	v_add3_u32 v231, v231, v125, s63
	v_add3_u32 v232, v232, v126, s63
	v_add3_u32 v233, v233, v127, s63
	v_perm_b32 v242, v227, v226, s64
	v_perm_b32 v243, v229, v228, s64
	v_perm_b32 v244, v231, v230, s64
	v_perm_b32 v245, v233, v232, s64
	s_nop 0
	global_store_dwordx4 v93, v[242:245], s[6:7]
	ds_read_b32 v226, v119
	ds_read_b32 v227, v119 offset:512
	ds_read_b32 v228, v119 offset:1024
	ds_read_b32 v229, v119 offset:1536
	ds_read_b32 v230, v119 offset:2048
	ds_read_b32 v231, v119 offset:2560
	ds_read_b32 v232, v119 offset:3072
	ds_read_b32 v233, v119 offset:3584
	s_waitcnt lgkmcnt(0)
	v_bfe_u32 v120, v226, 16, 1
	v_bfe_u32 v121, v227, 16, 1
	v_bfe_u32 v122, v228, 16, 1
	v_bfe_u32 v123, v229, 16, 1
	v_bfe_u32 v124, v230, 16, 1
	v_bfe_u32 v125, v231, 16, 1
	v_bfe_u32 v126, v232, 16, 1
	v_bfe_u32 v127, v233, 16, 1
	v_add3_u32 v226, v226, v120, s63
	v_add3_u32 v227, v227, v121, s63
	v_add3_u32 v228, v228, v122, s63
	v_add3_u32 v229, v229, v123, s63
	v_add3_u32 v230, v230, v124, s63
	v_add3_u32 v231, v231, v125, s63
	v_add3_u32 v232, v232, v126, s63
	v_add3_u32 v233, v233, v127, s63
	v_perm_b32 v242, v227, v226, s64
	v_perm_b32 v243, v229, v228, s64
	v_perm_b32 v244, v231, v230, s64
	v_perm_b32 v245, v233, v232, s64
	s_nop 0
	global_store_dwordx4 v94, v[242:245], s[6:7]
	s_waitcnt vmcnt(16)
	v_mul_f32_e32 v144, v42, v144
	v_mul_f32_e32 v145, v42, v145
	v_mul_f32_e32 v146, v42, v146
	v_mul_f32_e32 v147, v42, v147
	ds_write_b128 v209, v[144:147]
	v_mul_f32_e32 v148, v43, v148
	v_mul_f32_e32 v149, v43, v149
	v_mul_f32_e32 v150, v43, v150
	v_mul_f32_e32 v151, v43, v151
	ds_write_b128 v209, v[148:151] offset:1024
	v_mul_f32_e32 v152, v44, v152
	v_mul_f32_e32 v153, v44, v153
	v_mul_f32_e32 v154, v44, v154
	v_mul_f32_e32 v155, v44, v155
	ds_write_b128 v209, v[152:155] offset:2048
	v_mul_f32_e32 v156, v45, v156
	v_mul_f32_e32 v157, v45, v157
	v_mul_f32_e32 v158, v45, v158
	v_mul_f32_e32 v159, v45, v159
	ds_write_b128 v209, v[156:159] offset:3072
	v_mul_f32_e32 v160, v46, v160
	v_mul_f32_e32 v161, v46, v161
	v_mul_f32_e32 v162, v46, v162
	v_mul_f32_e32 v163, v46, v163
	ds_write_b128 v209, v[160:163] offset:4096
	v_mul_f32_e32 v164, v47, v164
	v_mul_f32_e32 v165, v47, v165
	v_mul_f32_e32 v166, v47, v166
	v_mul_f32_e32 v167, v47, v167
	ds_write_b128 v209, v[164:167] offset:5120
	v_mul_f32_e32 v168, v48, v168
	v_mul_f32_e32 v169, v48, v169
	v_mul_f32_e32 v170, v48, v170
	v_mul_f32_e32 v171, v48, v171
	ds_write_b128 v209, v[168:171] offset:6144
	v_mul_f32_e32 v172, v49, v172
	v_mul_f32_e32 v173, v49, v173
	v_mul_f32_e32 v174, v49, v174
	v_mul_f32_e32 v175, v49, v175
	ds_write_b128 v209, v[172:175] offset:7168
	s_waitcnt lgkmcnt(0)
	s_barrier
; #define GAS __attribute__((address_space(1)))
; #define LAS __attribute__((address_space(3)))
; #define LDS_WAIT() asm volatile("s_waitcnt lgkmcnt(0)" ::: "memory")
; __device__ __forceinline__ unsigned pk2(float lo, float hi) { return f2bf(lo) | (f2bf(hi) << 16); }
; __device__ __forceinline__ int nat_dim(int p) { return (p >> 1) + 64 * (p & 1); }
; template <int MAP, bool KS, bool KPERM = false>
; __device__ __forceinline__ void p0_transpose_item(const float* W, int K, int Nsrc, int nblk, bf16* WT, const float* ksA, const float* ksB, int ksplit, LAS float* scr, int item, int lane) {
;     const int kb = item / nblk, nb = item % nblk, k0 = 64 * kb, n0 = 32 * nb;
;     const int nr = n0 + (lane & 31); const int sc = MAP == 1 ? src_col_in(nr) : (MAP == 2 ? nat_dim(nr) : nr);
;     float v[32];
; #pragma unroll
;     for (int i = 0; i < 32; ++i) { const int k = k0 + 2 * i + (lane >> 5); const int ksrc = KPERM ? ((k & ~127) + nat_dim(k & 127)) : k;
;         v[i] = sc >= 0 ? W[(size_t)ksrc * Nsrc + sc] : 0.f; }
; #pragma unroll
;     for (int i = 0; i < 32; ++i) { const int kk = 2 * i + (lane >> 5); const int k = k0 + kk;
;         if (KS) v[i] *= (k < ksplit ? ksA[k] : ksB[k - ksplit]);
;         scr[kk * 33 + (lane & 31)] = v[i]; }
;     LDS_WAIT(); asm volatile("" ::: "memory");
;     const int c = lane & 7;
; #pragma unroll
;     for (int j = 0; j < 4; ++j) { const int n = (lane >> 3) + 8 * j; const LAS float* s = scr + (8 * c) * 33 + n;
;         v4u o; o.x = pk2(s[0 * 33], s[1 * 33]); o.y = pk2(s[2 * 33], s[3 * 33]); o.z = pk2(s[4 * 33], s[5 * 33]); o.w = pk2(s[6 * 33], s[7 * 33]);
;         *(GAS v4u*)(WT + (size_t)(n0 + n) * K + k0 + 8 * c) = o; }
;     LDS_WAIT(); asm volatile("" ::: "memory");
; }
;     const int pr = item >> 1, kb = 2 * (pr / nblk) + (item & 1), nb = pr % nblk, k0 = 64 * kb, n0 = 32 * nb;
;     const int nr = n0 + (lane & 31); const int sc = MAP == 1 ? src_col_in(nr) : nr;
;     float v[32];
; #pragma unroll
;     for (int i = 0; i < 32; ++i) v[i] = sc >= 0 ? W[(size_t)(k0 + 2 * i + (lane >> 5)) * Nsrc + sc] : 0.f;
; #pragma unroll
;     for (int i = 0; i < 32; ++i) { const int k = k0 + 2 * i + (lane >> 5); float x = v[i] * wscale; if (KS) x *= (k < ksplit ? ksA[k] : ksB[k - ksplit]); scr[(2 * i + (lane >> 5)) * 33 + (lane & 31)] = x; }
	s_add_i32 s24, s23, 8
	s_lshl_b32 s20, s24, 7
	s_cmp_lt_u32 s24, 40
	s_cselect_b32 s21, 0, 0x830
	s_cmp_lt_u32 s24, 72
	s_cselect_b32 s21, s21, 0xfffff030
	s_add_i32 s20, s20, s21
	s_lshl_b32 s20, s20, 2
	s_add_u32 s8, s50, s20
	s_addc_u32 s9, s51, 0
	global_load_dwordx4 v[144:147], v76, s[8:9]
	s_add_u32 s8, s8, 0x16280
	s_addc_u32 s9, s9, 0
	global_load_dwordx4 v[148:151], v76, s[8:9]
	s_add_u32 s8, s8, 0x16280
	s_addc_u32 s9, s9, 0
	global_load_dwordx4 v[152:155], v76, s[8:9]
	s_add_u32 s8, s8, 0x16280
	s_addc_u32 s9, s9, 0
	global_load_dwordx4 v[156:159], v76, s[8:9]
	s_add_u32 s8, s8, 0x16280
	s_addc_u32 s9, s9, 0
	global_load_dwordx4 v[160:163], v76, s[8:9]
	s_add_u32 s8, s8, 0x16280
	s_addc_u32 s9, s9, 0
	global_load_dwordx4 v[164:167], v76, s[8:9]
	s_add_u32 s8, s8, 0x16280
	s_addc_u32 s9, s9, 0
	global_load_dwordx4 v[168:171], v76, s[8:9]
	s_add_u32 s8, s8, 0x16280
	s_addc_u32 s9, s9, 0
	global_load_dwordx4 v[172:175], v76, s[8:9]
	s_add_i32 s24, s23, 80
	s_mul_i32 s20, s24, 0x100000
	s_add_u32 s6, s48, s20
	s_addc_u32 s7, s49, 0
	s_cmp_lt_u32 s24, 16
	s_cselect_b32 s20, 1, 0
	s_sub_i32 s21, s24, 16
	s_bitcmp0_b32 s21, 2
	s_cselect_b32 s21, 1, 0
	s_cmp_lt_u32 s24, 40
	s_cselect_b32 s21, s21, 0
	s_or_b32 s20, s20, s21
	s_cmp_lg_u32 s20, 0
	s_cselect_b64 s[20:21], -1, 0
	v_cndmask_b32_e64 v91, v83, v87, s[20:21]
	v_cndmask_b32_e64 v92, v84, v88, s[20:21]
	v_cndmask_b32_e64 v93, v85, v89, s[20:21]
	v_cndmask_b32_e64 v94, v86, v90, s[20:21]
	ds_read_b32 v226, v112
	ds_read_b32 v227, v112 offset:512
	ds_read_b32 v228, v112 offset:1024
	ds_read_b32 v229, v112 offset:1536
	ds_read_b32 v230, v112 offset:2048
	ds_read_b32 v231, v112 offset:2560
	ds_read_b32 v232, v112 offset:3072
	ds_read_b32 v233, v112 offset:3584
	s_waitcnt lgkmcnt(0)
	v_bfe_u32 v120, v226, 16, 1
	v_bfe_u32 v121, v227, 16, 1
	v_bfe_u32 v122, v228, 16, 1
	v_bfe_u32 v123, v229, 16, 1
	v_bfe_u32 v124, v230, 16, 1
	v_bfe_u32 v125, v231, 16, 1
	v_bfe_u32 v126, v232, 16, 1
	v_bfe_u32 v127, v233, 16, 1
	v_add3_u32 v226, v226, v120, s63
	v_add3_u32 v227, v227, v121, s63
	v_add3_u32 v228, v228, v122, s63
	v_add3_u32 v229, v229, v123, s63
	v_add3_u32 v230, v230, v124, s63
	v_add3_u32 v231, v231, v125, s63
	v_add3_u32 v232, v232, v126, s63
	v_add3_u32 v233, v233, v127, s63
	v_perm_b32 v242, v227, v226, s64
	v_perm_b32 v243, v229, v228, s64
	v_perm_b32 v244, v231, v230, s64
	v_perm_b32 v245, v233, v232, s64
	s_nop 0
	global_store_dwordx4 v91, v[242:245], s[6:7]
	ds_read_b32 v226, v114
	ds_read_b32 v227, v114 offset:512
	ds_read_b32 v228, v114 offset:1024
	ds_read_b32 v229, v114 offset:1536
	ds_read_b32 v230, v114 offset:2048
	ds_read_b32 v231, v114 offset:2560
	ds_read_b32 v232, v114 offset:3072
	ds_read_b32 v233, v114 offset:3584
	s_waitcnt lgkmcnt(0)
	v_bfe_u32 v120, v226, 16, 1
	v_bfe_u32 v121, v227, 16, 1
	v_bfe_u32 v122, v228, 16, 1
	v_bfe_u32 v123, v229, 16, 1
	v_bfe_u32 v124, v230, 16, 1
	v_bfe_u32 v125, v231, 16, 1
	v_bfe_u32 v126, v232, 16, 1
	v_bfe_u32 v127, v233, 16, 1
	v_add3_u32 v226, v226, v120, s63
	v_add3_u32 v227, v227, v121, s63
	v_add3_u32 v228, v228, v122, s63
	v_add3_u32 v229, v229, v123, s63
	v_add3_u32 v230, v230, v124, s63
	v_add3_u32 v231, v231, v125, s63
	v_add3_u32 v232, v232, v126, s63
	v_add3_u32 v233, v233, v127, s63
	v_perm_b32 v242, v227, v226, s64
	v_perm_b32 v243, v229, v228, s64
	v_perm_b32 v244, v231, v230, s64
	v_perm_b32 v245, v233, v232, s64
	s_nop 0
	global_store_dwordx4 v92, v[242:245], s[6:7]
	ds_read_b32 v226, v116
	ds_read_b32 v227, v116 offset:512
	ds_read_b32 v228, v116 offset:1024
	ds_read_b32 v229, v116 offset:1536
	ds_read_b32 v230, v116 offset:2048
	ds_read_b32 v231, v116 offset:2560
	ds_read_b32 v232, v116 offset:3072
	ds_read_b32 v233, v116 offset:3584
	s_waitcnt lgkmcnt(0)
	v_bfe_u32 v120, v226, 16, 1
	v_bfe_u32 v121, v227, 16, 1
	v_bfe_u32 v122, v228, 16, 1
	v_bfe_u32 v123, v229, 16, 1
	v_bfe_u32 v124, v230, 16, 1
	v_bfe_u32 v125, v231, 16, 1
	v_bfe_u32 v126, v232, 16, 1
	v_bfe_u32 v127, v233, 16, 1
	v_add3_u32 v226, v226, v120, s63
	v_add3_u32 v227, v227, v121, s63
	v_add3_u32 v228, v228, v122, s63
	v_add3_u32 v229, v229, v123, s63
	v_add3_u32 v230, v230, v124, s63
	v_add3_u32 v231, v231, v125, s63
	v_add3_u32 v232, v232, v126, s63
	v_add3_u32 v233, v233, v127, s63
	v_perm_b32 v242, v227, v226, s64
	v_perm_b32 v243, v229, v228, s64
	v_perm_b32 v244, v231, v230, s64
	v_perm_b32 v245, v233, v232, s64
	s_nop 0
	global_store_dwordx4 v93, v[242:245], s[6:7]
	ds_read_b32 v226, v118
	ds_read_b32 v227, v118 offset:512
	ds_read_b32 v228, v118 offset:1024
	ds_read_b32 v229, v118 offset:1536
	ds_read_b32 v230, v118 offset:2048
	ds_read_b32 v231, v118 offset:2560
	ds_read_b32 v232, v118 offset:3072
	ds_read_b32 v233, v118 offset:3584
	s_waitcnt lgkmcnt(0)
	v_bfe_u32 v120, v226, 16, 1
	v_bfe_u32 v121, v227, 16, 1
	v_bfe_u32 v122, v228, 16, 1
	v_bfe_u32 v123, v229, 16, 1
	v_bfe_u32 v124, v230, 16, 1
	v_bfe_u32 v125, v231, 16, 1
	v_bfe_u32 v126, v232, 16, 1
	v_bfe_u32 v127, v233, 16, 1
	v_add3_u32 v226, v226, v120, s63
	v_add3_u32 v227, v227, v121, s63
	v_add3_u32 v228, v228, v122, s63
	v_add3_u32 v229, v229, v123, s63
	v_add3_u32 v230, v230, v124, s63
	v_add3_u32 v231, v231, v125, s63
	v_add3_u32 v232, v232, v126, s63
	v_add3_u32 v233, v233, v127, s63
	v_perm_b32 v242, v227, v226, s64
	v_perm_b32 v243, v229, v228, s64
	v_perm_b32 v244, v231, v230, s64
	v_perm_b32 v245, v233, v232, s64
	s_nop 0
	global_store_dwordx4 v94, v[242:245], s[6:7]
	s_waitcnt vmcnt(16)
	v_mul_f32_e32 v176, v50, v176
	v_mul_f32_e32 v177, v50, v177
	v_mul_f32_e32 v178, v50, v178
	v_mul_f32_e32 v179, v50, v179
	ds_write_b128 v210, v[176:179]
	v_mul_f32_e32 v180, v51, v180
	v_mul_f32_e32 v181, v51, v181
	v_mul_f32_e32 v182, v51, v182
	v_mul_f32_e32 v183, v51, v183
	ds_write_b128 v210, v[180:183] offset:1024
	v_mul_f32_e32 v184, v52, v184
	v_mul_f32_e32 v185, v52, v185
	v_mul_f32_e32 v186, v52, v186
	v_mul_f32_e32 v187, v52, v187
	ds_write_b128 v210, v[184:187] offset:2048
	v_mul_f32_e32 v188, v53, v188
	v_mul_f32_e32 v189, v53, v189
	v_mul_f32_e32 v190, v53, v190
	v_mul_f32_e32 v191, v53, v191
	ds_write_b128 v210, v[188:191] offset:3072
	v_mul_f32_e32 v192, v54, v192
	v_mul_f32_e32 v193, v54, v193
	v_mul_f32_e32 v194, v54, v194
	v_mul_f32_e32 v195, v54, v195
	ds_write_b128 v210, v[192:195] offset:4096
	v_mul_f32_e32 v196, v55, v196
	v_mul_f32_e32 v197, v55, v197
	v_mul_f32_e32 v198, v55, v198
	v_mul_f32_e32 v199, v55, v199
	ds_write_b128 v210, v[196:199] offset:5120
	v_mul_f32_e32 v200, v56, v200
	v_mul_f32_e32 v201, v56, v201
	v_mul_f32_e32 v202, v56, v202
	v_mul_f32_e32 v203, v56, v203
	ds_write_b128 v210, v[200:203] offset:6144
	v_mul_f32_e32 v204, v57, v204
	v_mul_f32_e32 v205, v57, v205
	v_mul_f32_e32 v206, v57, v206
	v_mul_f32_e32 v207, v57, v207
	ds_write_b128 v210, v[204:207] offset:7168
	s_waitcnt lgkmcnt(0)
	s_barrier
; #define GAS __attribute__((address_space(1)))
; #define LAS __attribute__((address_space(3)))
; #define LDS_WAIT() asm volatile("s_waitcnt lgkmcnt(0)" ::: "memory")
; __device__ __forceinline__ unsigned pk4_fp8(float a, float b, float c, float d) {
;     a = fminf(fmaxf(a, -448.f), 448.f); b = fminf(fmaxf(b, -448.f), 448.f); c = fminf(fmaxf(c, -448.f), 448.f); d = fminf(fmaxf(d, -448.f), 448.f);
;     int w = __builtin_amdgcn_cvt_pk_fp8_f32(a, b, 0, false); w = __builtin_amdgcn_cvt_pk_fp8_f32(c, d, w, true); return (unsigned)w; }
;     const int pr = item >> 1, kb = 2 * (pr / nblk) + (item & 1), nb = pr % nblk, k0 = 64 * kb, n0 = 32 * nb;
;     const int nr = n0 + (lane & 31); const int sc = MAP == 1 ? src_col_in(nr) : nr;
;     float v[32];
; #pragma unroll
;     for (int i = 0; i < 32; ++i) v[i] = sc >= 0 ? W[(size_t)(k0 + 2 * i + (lane >> 5)) * Nsrc + sc] : 0.f;
; #pragma unroll
;     for (int i = 0; i < 32; ++i) { const int k = k0 + 2 * i + (lane >> 5); float x = v[i] * wscale; if (KS) x *= (k < ksplit ? ksA[k] : ksB[k - ksplit]); scr[(2 * i + (lane >> 5)) * 33 + (lane & 31)] = x; }
;     LDS_WAIT(); asm volatile("" ::: "memory");
;     const int c = lane & 7;
; #pragma unroll
;     for (int j = 0; j < 4; ++j) { const int n = (lane >> 3) + 8 * j; const LAS float* s = scr + (8 * c) * 33 + n;
;         const unsigned long long o = (unsigned long long)pg8::pk4_fp8(s[0 * 33], s[1 * 33], s[2 * 33], s[3 * 33]) | ((unsigned long long)pg8::pk4_fp8(s[4 * 33], s[5 * 33], s[6 * 33], s[7 * 33]) << 32);
;         *(GAS unsigned long long*)(WT + (size_t)(n0 + n) * K + k0 + 8 * c) = o; }
;     LDS_WAIT(); asm volatile("" ::: "memory");
; }
	s_add_i32 s24, s23, 16
	s_lshl_b32 s20, s24, 7
	s_cmp_lt_u32 s24, 40
	s_cselect_b32 s21, 0, 0x830
	s_cmp_lt_u32 s24, 72
	s_cselect_b32 s21, s21, 0xfffff030
	s_add_i32 s20, s20, s21
	s_lshl_b32 s20, s20, 2
	s_add_u32 s8, s50, s20
	s_addc_u32 s9, s51, 0
	global_load_dwordx4 v[176:179], v76, s[8:9]
	s_add_u32 s8, s8, 0x16280
	s_addc_u32 s9, s9, 0
	global_load_dwordx4 v[180:183], v76, s[8:9]
	s_add_u32 s8, s8, 0x16280
	s_addc_u32 s9, s9, 0
	global_load_dwordx4 v[184:187], v76, s[8:9]
	s_add_u32 s8, s8, 0x16280
	s_addc_u32 s9, s9, 0
	global_load_dwordx4 v[188:191], v76, s[8:9]
	s_add_u32 s8, s8, 0x16280
	s_addc_u32 s9, s9, 0
	global_load_dwordx4 v[192:195], v76, s[8:9]
	s_add_u32 s8, s8, 0x16280
	s_addc_u32 s9, s9, 0
	global_load_dwordx4 v[196:199], v76, s[8:9]
	s_add_u32 s8, s8, 0x16280
	s_addc_u32 s9, s9, 0
	global_load_dwordx4 v[200:203], v76, s[8:9]
	s_add_u32 s8, s8, 0x16280
	s_addc_u32 s9, s9, 0
	global_load_dwordx4 v[204:207], v76, s[8:9]
	s_add_i32 s24, s23, 0
	s_mul_i32 s20, s24, 0x80000
	s_add_u32 s6, s52, s20
	s_addc_u32 s7, s53, 0
	s_cmp_lt_u32 s24, 16
	s_cselect_b32 s20, 1, 0
	s_sub_i32 s21, s24, 16
	s_bitcmp0_b32 s21, 2
	s_cselect_b32 s21, 1, 0
	s_cmp_lt_u32 s24, 40
	s_cselect_b32 s21, s21, 0
	s_or_b32 s20, s20, s21
	s_cmp_lg_u32 s20, 0
	s_cselect_b64 s[20:21], -1, 0
	v_cndmask_b32_e64 v91, v77, v81, s[20:21]
	v_cndmask_b32_e64 v92, v78, v82, s[20:21]
	ds_read_b32 v226, v212
	ds_read_b32 v227, v212 offset:512
	ds_read_b32 v228, v212 offset:1024
	ds_read_b32 v229, v212 offset:1536
	ds_read_b32 v230, v212 offset:2048
	ds_read_b32 v231, v212 offset:2560
	ds_read_b32 v232, v212 offset:3072
	ds_read_b32 v233, v212 offset:3584
	ds_read_b32 v234, v212 offset:4096
	ds_read_b32 v235, v212 offset:4608
	ds_read_b32 v236, v212 offset:5120
	ds_read_b32 v237, v212 offset:5632
	ds_read_b32 v238, v212 offset:6144
	ds_read_b32 v239, v212 offset:6656
	ds_read_b32 v240, v212 offset:7168
	ds_read_b32 v241, v212 offset:7680
	s_waitcnt lgkmcnt(0)
	v_max_f32_e32 v226, v226, v226
	v_max_f32_e32 v227, v227, v227
	v_max_f32_e32 v228, v228, v228
	v_max_f32_e32 v229, v229, v229
	v_max_f32_e32 v230, v230, v230
	v_max_f32_e32 v231, v231, v231
	v_max_f32_e32 v232, v232, v232
	v_max_f32_e32 v233, v233, v233
	v_max_f32_e32 v234, v234, v234
	v_max_f32_e32 v235, v235, v235
	v_max_f32_e32 v236, v236, v236
	v_max_f32_e32 v237, v237, v237
	v_max_f32_e32 v238, v238, v238
	v_max_f32_e32 v239, v239, v239
	v_max_f32_e32 v240, v240, v240
	v_max_f32_e32 v241, v241, v241
	v_med3_f32 v226, v226, s62, v95
	v_med3_f32 v227, v227, s62, v95
	v_med3_f32 v228, v228, s62, v95
	v_med3_f32 v229, v229, s62, v95
	v_med3_f32 v230, v230, s62, v95
	v_med3_f32 v231, v231, s62, v95
	v_med3_f32 v232, v232, s62, v95
	v_med3_f32 v233, v233, s62, v95
	v_med3_f32 v234, v234, s62, v95
	v_med3_f32 v235, v235, s62, v95
	v_med3_f32 v236, v236, s62, v95
	v_med3_f32 v237, v237, s62, v95
	v_med3_f32 v238, v238, s62, v95
	v_med3_f32 v239, v239, s62, v95
	v_med3_f32 v240, v240, s62, v95
	v_med3_f32 v241, v241, s62, v95
	v_mov_b32_e32 v242, 0
	v_mov_b32_e32 v243, 0
	v_mov_b32_e32 v244, 0
	v_mov_b32_e32 v245, 0
	v_cvt_pk_fp8_f32 v242, v226, v227
	v_cvt_pk_fp8_f32 v243, v230, v231
	v_cvt_pk_fp8_f32 v244, v234, v235
	v_cvt_pk_fp8_f32 v245, v238, v239
	v_cvt_pk_fp8_f32 v242, v228, v229 op_sel:[0,0,1]
	v_cvt_pk_fp8_f32 v243, v232, v233 op_sel:[0,0,1]
	v_cvt_pk_fp8_f32 v244, v236, v237 op_sel:[0,0,1]
	v_cvt_pk_fp8_f32 v245, v240, v241 op_sel:[0,0,1]
	s_nop 0
	global_store_dwordx4 v91, v[242:245], s[6:7]
	ds_read_b32 v226, v214
	ds_read_b32 v227, v214 offset:512
	ds_read_b32 v228, v214 offset:1024
	ds_read_b32 v229, v214 offset:1536
	ds_read_b32 v230, v214 offset:2048
	ds_read_b32 v231, v214 offset:2560
	ds_read_b32 v232, v214 offset:3072
	ds_read_b32 v233, v214 offset:3584
	ds_read_b32 v234, v214 offset:4096
	ds_read_b32 v235, v214 offset:4608
	ds_read_b32 v236, v214 offset:5120
	ds_read_b32 v237, v214 offset:5632
	ds_read_b32 v238, v214 offset:6144
	ds_read_b32 v239, v214 offset:6656
	ds_read_b32 v240, v214 offset:7168
	ds_read_b32 v241, v214 offset:7680
	s_waitcnt lgkmcnt(0)
	v_max_f32_e32 v226, v226, v226
	v_max_f32_e32 v227, v227, v227
	v_max_f32_e32 v228, v228, v228
	v_max_f32_e32 v229, v229, v229
	v_max_f32_e32 v230, v230, v230
	v_max_f32_e32 v231, v231, v231
	v_max_f32_e32 v232, v232, v232
	v_max_f32_e32 v233, v233, v233
	v_max_f32_e32 v234, v234, v234
	v_max_f32_e32 v235, v235, v235
	v_max_f32_e32 v236, v236, v236
	v_max_f32_e32 v237, v237, v237
	v_max_f32_e32 v238, v238, v238
	v_max_f32_e32 v239, v239, v239
	v_max_f32_e32 v240, v240, v240
	v_max_f32_e32 v241, v241, v241
	v_med3_f32 v226, v226, s62, v95
	v_med3_f32 v227, v227, s62, v95
	v_med3_f32 v228, v228, s62, v95
	v_med3_f32 v229, v229, s62, v95
	v_med3_f32 v230, v230, s62, v95
	v_med3_f32 v231, v231, s62, v95
	v_med3_f32 v232, v232, s62, v95
	v_med3_f32 v233, v233, s62, v95
	v_med3_f32 v234, v234, s62, v95
	v_med3_f32 v235, v235, s62, v95
	v_med3_f32 v236, v236, s62, v95
	v_med3_f32 v237, v237, s62, v95
	v_med3_f32 v238, v238, s62, v95
	v_med3_f32 v239, v239, s62, v95
	v_med3_f32 v240, v240, s62, v95
	v_med3_f32 v241, v241, s62, v95
	v_mov_b32_e32 v242, 0
	v_mov_b32_e32 v243, 0
	v_mov_b32_e32 v244, 0
	v_mov_b32_e32 v245, 0
	v_cvt_pk_fp8_f32 v242, v226, v227
	v_cvt_pk_fp8_f32 v243, v230, v231
	v_cvt_pk_fp8_f32 v244, v234, v235
	v_cvt_pk_fp8_f32 v245, v238, v239
	v_cvt_pk_fp8_f32 v242, v228, v229 op_sel:[0,0,1]
	v_cvt_pk_fp8_f32 v243, v232, v233 op_sel:[0,0,1]
	v_cvt_pk_fp8_f32 v244, v236, v237 op_sel:[0,0,1]
	v_cvt_pk_fp8_f32 v245, v240, v241 op_sel:[0,0,1]
	s_nop 0
	global_store_dwordx4 v92, v[242:245], s[6:7]
	s_waitcnt vmcnt(14)
	v_mul_f32_e32 v144, v50, v144
	v_mul_f32_e32 v145, v50, v145
	v_mul_f32_e32 v146, v50, v146
	v_mul_f32_e32 v147, v50, v147
	ds_write_b128 v209, v[144:147]
	v_mul_f32_e32 v148, v51, v148
	v_mul_f32_e32 v149, v51, v149
	v_mul_f32_e32 v150, v51, v150
	v_mul_f32_e32 v151, v51, v151
	ds_write_b128 v209, v[148:151] offset:1024
	v_mul_f32_e32 v152, v52, v152
	v_mul_f32_e32 v153, v52, v153
	v_mul_f32_e32 v154, v52, v154
	v_mul_f32_e32 v155, v52, v155
	ds_write_b128 v209, v[152:155] offset:2048
	v_mul_f32_e32 v156, v53, v156
	v_mul_f32_e32 v157, v53, v157
	v_mul_f32_e32 v158, v53, v158
	v_mul_f32_e32 v159, v53, v159
	ds_write_b128 v209, v[156:159] offset:3072
	v_mul_f32_e32 v160, v54, v160
	v_mul_f32_e32 v161, v54, v161
	v_mul_f32_e32 v162, v54, v162
	v_mul_f32_e32 v163, v54, v163
	ds_write_b128 v209, v[160:163] offset:4096
	v_mul_f32_e32 v164, v55, v164
	v_mul_f32_e32 v165, v55, v165
	v_mul_f32_e32 v166, v55, v166
	v_mul_f32_e32 v167, v55, v167
	ds_write_b128 v209, v[164:167] offset:5120
	v_mul_f32_e32 v168, v56, v168
	v_mul_f32_e32 v169, v56, v169
	v_mul_f32_e32 v170, v56, v170
	v_mul_f32_e32 v171, v56, v171
	ds_write_b128 v209, v[168:171] offset:6144
	v_mul_f32_e32 v172, v57, v172
	v_mul_f32_e32 v173, v57, v173
	v_mul_f32_e32 v174, v57, v174
	v_mul_f32_e32 v175, v57, v175
	ds_write_b128 v209, v[172:175] offset:7168
	s_waitcnt lgkmcnt(0)
	s_barrier
; #define GAS __attribute__((address_space(1)))
; #define LAS __attribute__((address_space(3)))
; #define LDS_WAIT() asm volatile("s_waitcnt lgkmcnt(0)" ::: "memory")
; __device__ __forceinline__ unsigned pk4_fp8(float a, float b, float c, float d) {
;     a = fminf(fmaxf(a, -448.f), 448.f); b = fminf(fmaxf(b, -448.f), 448.f); c = fminf(fmaxf(c, -448.f), 448.f); d = fminf(fmaxf(d, -448.f), 448.f);
;     int w = __builtin_amdgcn_cvt_pk_fp8_f32(a, b, 0, false); w = __builtin_amdgcn_cvt_pk_fp8_f32(c, d, w, true); return (unsigned)w; }
;     const int pr = item >> 1, kb = 2 * (pr / nblk) + (item & 1), nb = pr % nblk, k0 = 64 * kb, n0 = 32 * nb;
;     const int nr = n0 + (lane & 31); const int sc = MAP == 1 ? src_col_in(nr) : nr;
;     float v[32];
; #pragma unroll
;     for (int i = 0; i < 32; ++i) v[i] = sc >= 0 ? W[(size_t)(k0 + 2 * i + (lane >> 5)) * Nsrc + sc] : 0.f;
; #pragma unroll
;     for (int i = 0; i < 32; ++i) { const int k = k0 + 2 * i + (lane >> 5); float x = v[i] * wscale; if (KS) x *= (k < ksplit ? ksA[k] : ksB[k - ksplit]); scr[(2 * i + (lane >> 5)) * 33 + (lane & 31)] = x; }
;     LDS_WAIT(); asm volatile("" ::: "memory");
;     const int c = lane & 7;
; #pragma unroll
;     for (int j = 0; j < 4; ++j) { const int n = (lane >> 3) + 8 * j; const LAS float* s = scr + (8 * c) * 33 + n;
;         const unsigned long long o = (unsigned long long)pg8::pk4_fp8(s[0 * 33], s[1 * 33], s[2 * 33], s[3 * 33]) | ((unsigned long long)pg8::pk4_fp8(s[4 * 33], s[5 * 33], s[6 * 33], s[7 * 33]) << 32);
;         *(GAS unsigned long long*)(WT + (size_t)(n0 + n) * K + k0 + 8 * c) = o; }
;     LDS_WAIT(); asm volatile("" ::: "memory");
; }
	s_add_i32 s24, s23, 24
	s_lshl_b32 s20, s24, 7
	s_cmp_lt_u32 s24, 40
	s_cselect_b32 s21, 0, 0x830
	s_cmp_lt_u32 s24, 72
	s_cselect_b32 s21, s21, 0xfffff030
	s_add_i32 s20, s20, s21
	s_lshl_b32 s20, s20, 2
	s_add_u32 s8, s50, s20
	s_addc_u32 s9, s51, 0
	global_load_dwordx4 v[144:147], v76, s[8:9]
	s_add_u32 s8, s8, 0x16280
	s_addc_u32 s9, s9, 0
	global_load_dwordx4 v[148:151], v76, s[8:9]
	s_add_u32 s8, s8, 0x16280
	s_addc_u32 s9, s9, 0
	global_load_dwordx4 v[152:155], v76, s[8:9]
	s_add_u32 s8, s8, 0x16280
	s_addc_u32 s9, s9, 0
	global_load_dwordx4 v[156:159], v76, s[8:9]
	s_add_u32 s8, s8, 0x16280
	s_addc_u32 s9, s9, 0
	global_load_dwordx4 v[160:163], v76, s[8:9]
	s_add_u32 s8, s8, 0x16280
	s_addc_u32 s9, s9, 0
	global_load_dwordx4 v[164:167], v76, s[8:9]
	s_add_u32 s8, s8, 0x16280
	s_addc_u32 s9, s9, 0
	global_load_dwordx4 v[168:171], v76, s[8:9]
	s_add_u32 s8, s8, 0x16280
	s_addc_u32 s9, s9, 0
	global_load_dwordx4 v[172:175], v76, s[8:9]
	s_add_i32 s24, s23, 8
	s_mul_i32 s20, s24, 0x80000
	s_add_u32 s6, s52, s20
	s_addc_u32 s7, s53, 0
	s_cmp_lt_u32 s24, 16
	s_cselect_b32 s20, 1, 0
	s_sub_i32 s21, s24, 16
	s_bitcmp0_b32 s21, 2
	s_cselect_b32 s21, 1, 0
	s_cmp_lt_u32 s24, 40
	s_cselect_b32 s21, s21, 0
	s_or_b32 s20, s20, s21
	s_cmp_lg_u32 s20, 0
	s_cselect_b64 s[20:21], -1, 0
	v_cndmask_b32_e64 v91, v77, v81, s[20:21]
	v_cndmask_b32_e64 v92, v78, v82, s[20:21]
	ds_read_b32 v226, v211
	ds_read_b32 v227, v211 offset:512
	ds_read_b32 v228, v211 offset:1024
	ds_read_b32 v229, v211 offset:1536
	ds_read_b32 v230, v211 offset:2048
	ds_read_b32 v231, v211 offset:2560
	ds_read_b32 v232, v211 offset:3072
	ds_read_b32 v233, v211 offset:3584
	ds_read_b32 v234, v211 offset:4096
	ds_read_b32 v235, v211 offset:4608
	ds_read_b32 v236, v211 offset:5120
	ds_read_b32 v237, v211 offset:5632
	ds_read_b32 v238, v211 offset:6144
	ds_read_b32 v239, v211 offset:6656
	ds_read_b32 v240, v211 offset:7168
	ds_read_b32 v241, v211 offset:7680
	s_waitcnt lgkmcnt(0)
	v_max_f32_e32 v226, v226, v226
	v_max_f32_e32 v227, v227, v227
	v_max_f32_e32 v228, v228, v228
	v_max_f32_e32 v229, v229, v229
	v_max_f32_e32 v230, v230, v230
	v_max_f32_e32 v231, v231, v231
	v_max_f32_e32 v232, v232, v232
	v_max_f32_e32 v233, v233, v233
	v_max_f32_e32 v234, v234, v234
	v_max_f32_e32 v235, v235, v235
	v_max_f32_e32 v236, v236, v236
	v_max_f32_e32 v237, v237, v237
	v_max_f32_e32 v238, v238, v238
	v_max_f32_e32 v239, v239, v239
	v_max_f32_e32 v240, v240, v240
	v_max_f32_e32 v241, v241, v241
	v_med3_f32 v226, v226, s62, v95
	v_med3_f32 v227, v227, s62, v95
	v_med3_f32 v228, v228, s62, v95
	v_med3_f32 v229, v229, s62, v95
	v_med3_f32 v230, v230, s62, v95
	v_med3_f32 v231, v231, s62, v95
	v_med3_f32 v232, v232, s62, v95
	v_med3_f32 v233, v233, s62, v95
	v_med3_f32 v234, v234, s62, v95
	v_med3_f32 v235, v235, s62, v95
	v_med3_f32 v236, v236, s62, v95
	v_med3_f32 v237, v237, s62, v95
	v_med3_f32 v238, v238, s62, v95
	v_med3_f32 v239, v239, s62, v95
	v_med3_f32 v240, v240, s62, v95
	v_med3_f32 v241, v241, s62, v95
	v_mov_b32_e32 v242, 0
	v_mov_b32_e32 v243, 0
	v_mov_b32_e32 v244, 0
	v_mov_b32_e32 v245, 0
	v_cvt_pk_fp8_f32 v242, v226, v227
	v_cvt_pk_fp8_f32 v243, v230, v231
	v_cvt_pk_fp8_f32 v244, v234, v235
	v_cvt_pk_fp8_f32 v245, v238, v239
	v_cvt_pk_fp8_f32 v242, v228, v229 op_sel:[0,0,1]
	v_cvt_pk_fp8_f32 v243, v232, v233 op_sel:[0,0,1]
	v_cvt_pk_fp8_f32 v244, v236, v237 op_sel:[0,0,1]
	v_cvt_pk_fp8_f32 v245, v240, v241 op_sel:[0,0,1]
	s_nop 0
	global_store_dwordx4 v91, v[242:245], s[6:7]
	ds_read_b32 v226, v213
	ds_read_b32 v227, v213 offset:512
	ds_read_b32 v228, v213 offset:1024
	ds_read_b32 v229, v213 offset:1536
	ds_read_b32 v230, v213 offset:2048
	ds_read_b32 v231, v213 offset:2560
	ds_read_b32 v232, v213 offset:3072
	ds_read_b32 v233, v213 offset:3584
	ds_read_b32 v234, v213 offset:4096
	ds_read_b32 v235, v213 offset:4608
	ds_read_b32 v236, v213 offset:5120
	ds_read_b32 v237, v213 offset:5632
	ds_read_b32 v238, v213 offset:6144
	ds_read_b32 v239, v213 offset:6656
	ds_read_b32 v240, v213 offset:7168
	ds_read_b32 v241, v213 offset:7680
	s_waitcnt lgkmcnt(0)
	v_max_f32_e32 v226, v226, v226
	v_max_f32_e32 v227, v227, v227
	v_max_f32_e32 v228, v228, v228
	v_max_f32_e32 v229, v229, v229
	v_max_f32_e32 v230, v230, v230
	v_max_f32_e32 v231, v231, v231
	v_max_f32_e32 v232, v232, v232
	v_max_f32_e32 v233, v233, v233
	v_max_f32_e32 v234, v234, v234
	v_max_f32_e32 v235, v235, v235
	v_max_f32_e32 v236, v236, v236
	v_max_f32_e32 v237, v237, v237
	v_max_f32_e32 v238, v238, v238
	v_max_f32_e32 v239, v239, v239
	v_max_f32_e32 v240, v240, v240
	v_max_f32_e32 v241, v241, v241
	v_med3_f32 v226, v226, s62, v95
	v_med3_f32 v227, v227, s62, v95
	v_med3_f32 v228, v228, s62, v95
	v_med3_f32 v229, v229, s62, v95
	v_med3_f32 v230, v230, s62, v95
	v_med3_f32 v231, v231, s62, v95
	v_med3_f32 v232, v232, s62, v95
	v_med3_f32 v233, v233, s62, v95
	v_med3_f32 v234, v234, s62, v95
	v_med3_f32 v235, v235, s62, v95
	v_med3_f32 v236, v236, s62, v95
	v_med3_f32 v237, v237, s62, v95
	v_med3_f32 v238, v238, s62, v95
	v_med3_f32 v239, v239, s62, v95
	v_med3_f32 v240, v240, s62, v95
	v_med3_f32 v241, v241, s62, v95
	v_mov_b32_e32 v242, 0
	v_mov_b32_e32 v243, 0
	v_mov_b32_e32 v244, 0
	v_mov_b32_e32 v245, 0
	v_cvt_pk_fp8_f32 v242, v226, v227
	v_cvt_pk_fp8_f32 v243, v230, v231
	v_cvt_pk_fp8_f32 v244, v234, v235
	v_cvt_pk_fp8_f32 v245, v238, v239
	v_cvt_pk_fp8_f32 v242, v228, v229 op_sel:[0,0,1]
	v_cvt_pk_fp8_f32 v243, v232, v233 op_sel:[0,0,1]
	v_cvt_pk_fp8_f32 v244, v236, v237 op_sel:[0,0,1]
	v_cvt_pk_fp8_f32 v245, v240, v241 op_sel:[0,0,1]
	s_nop 0
	global_store_dwordx4 v92, v[242:245], s[6:7]
	s_waitcnt vmcnt(12)
	v_mul_f32_e32 v176, v50, v176
	v_mul_f32_e32 v177, v50, v177
	v_mul_f32_e32 v178, v50, v178
	v_mul_f32_e32 v179, v50, v179
	ds_write_b128 v210, v[176:179]
	v_mul_f32_e32 v180, v51, v180
	v_mul_f32_e32 v181, v51, v181
	v_mul_f32_e32 v182, v51, v182
	v_mul_f32_e32 v183, v51, v183
	ds_write_b128 v210, v[180:183] offset:1024
	v_mul_f32_e32 v184, v52, v184
	v_mul_f32_e32 v185, v52, v185
	v_mul_f32_e32 v186, v52, v186
	v_mul_f32_e32 v187, v52, v187
	ds_write_b128 v210, v[184:187] offset:2048
	v_mul_f32_e32 v188, v53, v188
	v_mul_f32_e32 v189, v53, v189
	v_mul_f32_e32 v190, v53, v190
	v_mul_f32_e32 v191, v53, v191
	ds_write_b128 v210, v[188:191] offset:3072
	v_mul_f32_e32 v192, v54, v192
	v_mul_f32_e32 v193, v54, v193
	v_mul_f32_e32 v194, v54, v194
	v_mul_f32_e32 v195, v54, v195
	ds_write_b128 v210, v[192:195] offset:4096
	v_mul_f32_e32 v196, v55, v196
	v_mul_f32_e32 v197, v55, v197
	v_mul_f32_e32 v198, v55, v198
	v_mul_f32_e32 v199, v55, v199
	ds_write_b128 v210, v[196:199] offset:5120
	v_mul_f32_e32 v200, v56, v200
	v_mul_f32_e32 v201, v56, v201
	v_mul_f32_e32 v202, v56, v202
	v_mul_f32_e32 v203, v56, v203
	ds_write_b128 v210, v[200:203] offset:6144
	v_mul_f32_e32 v204, v57, v204
	v_mul_f32_e32 v205, v57, v205
	v_mul_f32_e32 v206, v57, v206
	v_mul_f32_e32 v207, v57, v207
	ds_write_b128 v210, v[204:207] offset:7168
	s_waitcnt lgkmcnt(0)
	s_barrier
; #define GAS __attribute__((address_space(1)))
; #define LAS __attribute__((address_space(3)))
; #define LDS_WAIT() asm volatile("s_waitcnt lgkmcnt(0)" ::: "memory")
; __device__ __forceinline__ unsigned pk4_fp8(float a, float b, float c, float d) {
;     a = fminf(fmaxf(a, -448.f), 448.f); b = fminf(fmaxf(b, -448.f), 448.f); c = fminf(fmaxf(c, -448.f), 448.f); d = fminf(fmaxf(d, -448.f), 448.f);
;     int w = __builtin_amdgcn_cvt_pk_fp8_f32(a, b, 0, false); w = __builtin_amdgcn_cvt_pk_fp8_f32(c, d, w, true); return (unsigned)w; }
;     const int pr = item >> 1, kb = 2 * (pr / nblk) + (item & 1), nb = pr % nblk, k0 = 64 * kb, n0 = 32 * nb;
;     const int nr = n0 + (lane & 31); const int sc = MAP == 1 ? src_col_in(nr) : nr;
;     float v[32];
; #pragma unroll
;     for (int i = 0; i < 32; ++i) v[i] = sc >= 0 ? W[(size_t)(k0 + 2 * i + (lane >> 5)) * Nsrc + sc] : 0.f;
; #pragma unroll
;     for (int i = 0; i < 32; ++i) { const int k = k0 + 2 * i + (lane >> 5); float x = v[i] * wscale; if (KS) x *= (k < ksplit ? ksA[k] : ksB[k - ksplit]); scr[(2 * i + (lane >> 5)) * 33 + (lane & 31)] = x; }
;     LDS_WAIT(); asm volatile("" ::: "memory");
;     const int c = lane & 7;
; #pragma unroll
;     for (int j = 0; j < 4; ++j) { const int n = (lane >> 3) + 8 * j; const LAS float* s = scr + (8 * c) * 33 + n;
;         const unsigned long long o = (unsigned long long)pg8::pk4_fp8(s[0 * 33], s[1 * 33], s[2 * 33], s[3 * 33]) | ((unsigned long long)pg8::pk4_fp8(s[4 * 33], s[5 * 33], s[6 * 33], s[7 * 33]) << 32);
;         *(GAS unsigned long long*)(WT + (size_t)(n0 + n) * K + k0 + 8 * c) = o; }
;     LDS_WAIT(); asm volatile("" ::: "memory");
; }
	s_add_i32 s24, s23, 32
	s_lshl_b32 s20, s24, 7
	s_cmp_lt_u32 s24, 40
	s_cselect_b32 s21, 0, 0x830
	s_cmp_lt_u32 s24, 72
	s_cselect_b32 s21, s21, 0xfffff030
	s_add_i32 s20, s20, s21
	s_lshl_b32 s20, s20, 2
	s_add_u32 s8, s50, s20
	s_addc_u32 s9, s51, 0
	global_load_dwordx4 v[176:179], v76, s[8:9]
	s_add_u32 s8, s8, 0x16280
	s_addc_u32 s9, s9, 0
	global_load_dwordx4 v[180:183], v76, s[8:9]
	s_add_u32 s8, s8, 0x16280
	s_addc_u32 s9, s9, 0
	global_load_dwordx4 v[184:187], v76, s[8:9]
	s_add_u32 s8, s8, 0x16280
	s_addc_u32 s9, s9, 0
	global_load_dwordx4 v[188:191], v76, s[8:9]
	s_add_u32 s8, s8, 0x16280
	s_addc_u32 s9, s9, 0
	global_load_dwordx4 v[192:195], v76, s[8:9]
	s_add_u32 s8, s8, 0x16280
	s_addc_u32 s9, s9, 0
	global_load_dwordx4 v[196:199], v76, s[8:9]
	s_add_u32 s8, s8, 0x16280
	s_addc_u32 s9, s9, 0
	global_load_dwordx4 v[200:203], v76, s[8:9]
	s_add_u32 s8, s8, 0x16280
	s_addc_u32 s9, s9, 0
	global_load_dwordx4 v[204:207], v76, s[8:9]
	s_add_i32 s24, s23, 16
	s_mul_i32 s20, s24, 0x80000
	s_add_u32 s6, s52, s20
	s_addc_u32 s7, s53, 0
	s_cmp_lt_u32 s24, 16
	s_cselect_b32 s20, 1, 0
	s_sub_i32 s21, s24, 16
	s_bitcmp0_b32 s21, 2
	s_cselect_b32 s21, 1, 0
	s_cmp_lt_u32 s24, 40
	s_cselect_b32 s21, s21, 0
	s_or_b32 s20, s20, s21
	s_cmp_lg_u32 s20, 0
	s_cselect_b64 s[20:21], -1, 0
	v_cndmask_b32_e64 v91, v77, v81, s[20:21]
	v_cndmask_b32_e64 v92, v78, v82, s[20:21]
	ds_read_b32 v226, v212
	ds_read_b32 v227, v212 offset:512
	ds_read_b32 v228, v212 offset:1024
	ds_read_b32 v229, v212 offset:1536
	ds_read_b32 v230, v212 offset:2048
	ds_read_b32 v231, v212 offset:2560
	ds_read_b32 v232, v212 offset:3072
	ds_read_b32 v233, v212 offset:3584
	ds_read_b32 v234, v212 offset:4096
	ds_read_b32 v235, v212 offset:4608
	ds_read_b32 v236, v212 offset:5120
	ds_read_b32 v237, v212 offset:5632
	ds_read_b32 v238, v212 offset:6144
	ds_read_b32 v239, v212 offset:6656
	ds_read_b32 v240, v212 offset:7168
	ds_read_b32 v241, v212 offset:7680
	s_waitcnt lgkmcnt(0)
	v_max_f32_e32 v226, v226, v226
	v_max_f32_e32 v227, v227, v227
	v_max_f32_e32 v228, v228, v228
	v_max_f32_e32 v229, v229, v229
	v_max_f32_e32 v230, v230, v230
	v_max_f32_e32 v231, v231, v231
	v_max_f32_e32 v232, v232, v232
	v_max_f32_e32 v233, v233, v233
	v_max_f32_e32 v234, v234, v234
	v_max_f32_e32 v235, v235, v235
	v_max_f32_e32 v236, v236, v236
	v_max_f32_e32 v237, v237, v237
	v_max_f32_e32 v238, v238, v238
	v_max_f32_e32 v239, v239, v239
	v_max_f32_e32 v240, v240, v240
	v_max_f32_e32 v241, v241, v241
	v_med3_f32 v226, v226, s62, v95
	v_med3_f32 v227, v227, s62, v95
	v_med3_f32 v228, v228, s62, v95
	v_med3_f32 v229, v229, s62, v95
	v_med3_f32 v230, v230, s62, v95
	v_med3_f32 v231, v231, s62, v95
	v_med3_f32 v232, v232, s62, v95
	v_med3_f32 v233, v233, s62, v95
	v_med3_f32 v234, v234, s62, v95
	v_med3_f32 v235, v235, s62, v95
	v_med3_f32 v236, v236, s62, v95
	v_med3_f32 v237, v237, s62, v95
	v_med3_f32 v238, v238, s62, v95
	v_med3_f32 v239, v239, s62, v95
	v_med3_f32 v240, v240, s62, v95
	v_med3_f32 v241, v241, s62, v95
	v_mov_b32_e32 v242, 0
	v_mov_b32_e32 v243, 0
	v_mov_b32_e32 v244, 0
	v_mov_b32_e32 v245, 0
	v_cvt_pk_fp8_f32 v242, v226, v227
	v_cvt_pk_fp8_f32 v243, v230, v231
	v_cvt_pk_fp8_f32 v244, v234, v235
	v_cvt_pk_fp8_f32 v245, v238, v239
	v_cvt_pk_fp8_f32 v242, v228, v229 op_sel:[0,0,1]
	v_cvt_pk_fp8_f32 v243, v232, v233 op_sel:[0,0,1]
	v_cvt_pk_fp8_f32 v244, v236, v237 op_sel:[0,0,1]
	v_cvt_pk_fp8_f32 v245, v240, v241 op_sel:[0,0,1]
	s_nop 0
	global_store_dwordx4 v91, v[242:245], s[6:7]
	ds_read_b32 v226, v214
	ds_read_b32 v227, v214 offset:512
	ds_read_b32 v228, v214 offset:1024
	ds_read_b32 v229, v214 offset:1536
	ds_read_b32 v230, v214 offset:2048
	ds_read_b32 v231, v214 offset:2560
	ds_read_b32 v232, v214 offset:3072
	ds_read_b32 v233, v214 offset:3584
	ds_read_b32 v234, v214 offset:4096
	ds_read_b32 v235, v214 offset:4608
	ds_read_b32 v236, v214 offset:5120
	ds_read_b32 v237, v214 offset:5632
	ds_read_b32 v238, v214 offset:6144
	ds_read_b32 v239, v214 offset:6656
	ds_read_b32 v240, v214 offset:7168
	ds_read_b32 v241, v214 offset:7680
	s_waitcnt lgkmcnt(0)
	v_max_f32_e32 v226, v226, v226
	v_max_f32_e32 v227, v227, v227
	v_max_f32_e32 v228, v228, v228
	v_max_f32_e32 v229, v229, v229
	v_max_f32_e32 v230, v230, v230
	v_max_f32_e32 v231, v231, v231
	v_max_f32_e32 v232, v232, v232
	v_max_f32_e32 v233, v233, v233
	v_max_f32_e32 v234, v234, v234
	v_max_f32_e32 v235, v235, v235
	v_max_f32_e32 v236, v236, v236
	v_max_f32_e32 v237, v237, v237
	v_max_f32_e32 v238, v238, v238
	v_max_f32_e32 v239, v239, v239
	v_max_f32_e32 v240, v240, v240
	v_max_f32_e32 v241, v241, v241
	v_med3_f32 v226, v226, s62, v95
	v_med3_f32 v227, v227, s62, v95
	v_med3_f32 v228, v228, s62, v95
	v_med3_f32 v229, v229, s62, v95
	v_med3_f32 v230, v230, s62, v95
	v_med3_f32 v231, v231, s62, v95
	v_med3_f32 v232, v232, s62, v95
	v_med3_f32 v233, v233, s62, v95
	v_med3_f32 v234, v234, s62, v95
	v_med3_f32 v235, v235, s62, v95
	v_med3_f32 v236, v236, s62, v95
	v_med3_f32 v237, v237, s62, v95
	v_med3_f32 v238, v238, s62, v95
	v_med3_f32 v239, v239, s62, v95
	v_med3_f32 v240, v240, s62, v95
	v_med3_f32 v241, v241, s62, v95
	v_mov_b32_e32 v242, 0
	v_mov_b32_e32 v243, 0
	v_mov_b32_e32 v244, 0
	v_mov_b32_e32 v245, 0
	v_cvt_pk_fp8_f32 v242, v226, v227
	v_cvt_pk_fp8_f32 v243, v230, v231
	v_cvt_pk_fp8_f32 v244, v234, v235
	v_cvt_pk_fp8_f32 v245, v238, v239
	v_cvt_pk_fp8_f32 v242, v228, v229 op_sel:[0,0,1]
	v_cvt_pk_fp8_f32 v243, v232, v233 op_sel:[0,0,1]
	v_cvt_pk_fp8_f32 v244, v236, v237 op_sel:[0,0,1]
	v_cvt_pk_fp8_f32 v245, v240, v241 op_sel:[0,0,1]
	s_nop 0
	global_store_dwordx4 v92, v[242:245], s[6:7]
	s_waitcnt vmcnt(12)
	v_mul_f32_e32 v144, v50, v144
	v_mul_f32_e32 v145, v50, v145
	v_mul_f32_e32 v146, v50, v146
	v_mul_f32_e32 v147, v50, v147
	ds_write_b128 v209, v[144:147]
	v_mul_f32_e32 v148, v51, v148
	v_mul_f32_e32 v149, v51, v149
	v_mul_f32_e32 v150, v51, v150
	v_mul_f32_e32 v151, v51, v151
	ds_write_b128 v209, v[148:151] offset:1024
	v_mul_f32_e32 v152, v52, v152
	v_mul_f32_e32 v153, v52, v153
	v_mul_f32_e32 v154, v52, v154
	v_mul_f32_e32 v155, v52, v155
	ds_write_b128 v209, v[152:155] offset:2048
	v_mul_f32_e32 v156, v53, v156
	v_mul_f32_e32 v157, v53, v157
	v_mul_f32_e32 v158, v53, v158
	v_mul_f32_e32 v159, v53, v159
	ds_write_b128 v209, v[156:159] offset:3072
	v_mul_f32_e32 v160, v54, v160
	v_mul_f32_e32 v161, v54, v161
	v_mul_f32_e32 v162, v54, v162
	v_mul_f32_e32 v163, v54, v163
	ds_write_b128 v209, v[160:163] offset:4096
	v_mul_f32_e32 v164, v55, v164
	v_mul_f32_e32 v165, v55, v165
	v_mul_f32_e32 v166, v55, v166
	v_mul_f32_e32 v167, v55, v167
	ds_write_b128 v209, v[164:167] offset:5120
	v_mul_f32_e32 v168, v56, v168
	v_mul_f32_e32 v169, v56, v169
	v_mul_f32_e32 v170, v56, v170
	v_mul_f32_e32 v171, v56, v171
	ds_write_b128 v209, v[168:171] offset:6144
	v_mul_f32_e32 v172, v57, v172
	v_mul_f32_e32 v173, v57, v173
	v_mul_f32_e32 v174, v57, v174
	v_mul_f32_e32 v175, v57, v175
	ds_write_b128 v209, v[172:175] offset:7168
	s_waitcnt lgkmcnt(0)
	s_barrier
; #define GAS __attribute__((address_space(1)))
; #define LAS __attribute__((address_space(3)))
; #define LDS_WAIT() asm volatile("s_waitcnt lgkmcnt(0)" ::: "memory")
; __device__ __forceinline__ unsigned pk4_fp8(float a, float b, float c, float d) {
;     a = fminf(fmaxf(a, -448.f), 448.f); b = fminf(fmaxf(b, -448.f), 448.f); c = fminf(fmaxf(c, -448.f), 448.f); d = fminf(fmaxf(d, -448.f), 448.f);
;     int w = __builtin_amdgcn_cvt_pk_fp8_f32(a, b, 0, false); w = __builtin_amdgcn_cvt_pk_fp8_f32(c, d, w, true); return (unsigned)w; }
;     const int pr = item >> 1, kb = 2 * (pr / nblk) + (item & 1), nb = pr % nblk, k0 = 64 * kb, n0 = 32 * nb;
;     const int nr = n0 + (lane & 31); const int sc = MAP == 1 ? src_col_in(nr) : nr;
;     float v[32];
; #pragma unroll
;     for (int i = 0; i < 32; ++i) v[i] = sc >= 0 ? W[(size_t)(k0 + 2 * i + (lane >> 5)) * Nsrc + sc] : 0.f;
; #pragma unroll
;     for (int i = 0; i < 32; ++i) { const int k = k0 + 2 * i + (lane >> 5); float x = v[i] * wscale; if (KS) x *= (k < ksplit ? ksA[k] : ksB[k - ksplit]); scr[(2 * i + (lane >> 5)) * 33 + (lane & 31)] = x; }
;     LDS_WAIT(); asm volatile("" ::: "memory");
;     const int c = lane & 7;
; #pragma unroll
;     for (int j = 0; j < 4; ++j) { const int n = (lane >> 3) + 8 * j; const LAS float* s = scr + (8 * c) * 33 + n;
;         const unsigned long long o = (unsigned long long)pg8::pk4_fp8(s[0 * 33], s[1 * 33], s[2 * 33], s[3 * 33]) | ((unsigned long long)pg8::pk4_fp8(s[4 * 33], s[5 * 33], s[6 * 33], s[7 * 33]) << 32);
;         *(GAS unsigned long long*)(WT + (size_t)(n0 + n) * K + k0 + 8 * c) = o; }
;     LDS_WAIT(); asm volatile("" ::: "memory");
; }
	s_add_i32 s24, s23, 40
	s_lshl_b32 s20, s24, 7
	s_cmp_lt_u32 s24, 40
	s_cselect_b32 s21, 0, 0x830
	s_cmp_lt_u32 s24, 72
	s_cselect_b32 s21, s21, 0xfffff030
	s_add_i32 s20, s20, s21
	s_lshl_b32 s20, s20, 2
	s_add_u32 s8, s50, s20
	s_addc_u32 s9, s51, 0
	global_load_dwordx4 v[144:147], v76, s[8:9]
	s_add_u32 s8, s8, 0x16280
	s_addc_u32 s9, s9, 0
	global_load_dwordx4 v[148:151], v76, s[8:9]
	s_add_u32 s8, s8, 0x16280
	s_addc_u32 s9, s9, 0
	global_load_dwordx4 v[152:155], v76, s[8:9]
	s_add_u32 s8, s8, 0x16280
	s_addc_u32 s9, s9, 0
	global_load_dwordx4 v[156:159], v76, s[8:9]
	s_add_u32 s8, s8, 0x16280
	s_addc_u32 s9, s9, 0
	global_load_dwordx4 v[160:163], v76, s[8:9]
	s_add_u32 s8, s8, 0x16280
	s_addc_u32 s9, s9, 0
	global_load_dwordx4 v[164:167], v76, s[8:9]
	s_add_u32 s8, s8, 0x16280
	s_addc_u32 s9, s9, 0
	global_load_dwordx4 v[168:171], v76, s[8:9]
	s_add_u32 s8, s8, 0x16280
	s_addc_u32 s9, s9, 0
	global_load_dwordx4 v[172:175], v76, s[8:9]
	s_add_i32 s24, s23, 24
	s_mul_i32 s20, s24, 0x80000
	s_add_u32 s6, s52, s20
	s_addc_u32 s7, s53, 0
	s_cmp_lt_u32 s24, 16
	s_cselect_b32 s20, 1, 0
	s_sub_i32 s21, s24, 16
	s_bitcmp0_b32 s21, 2
	s_cselect_b32 s21, 1, 0
	s_cmp_lt_u32 s24, 40
	s_cselect_b32 s21, s21, 0
	s_or_b32 s20, s20, s21
	s_cmp_lg_u32 s20, 0
	s_cselect_b64 s[20:21], -1, 0
	v_cndmask_b32_e64 v91, v77, v81, s[20:21]
	v_cndmask_b32_e64 v92, v78, v82, s[20:21]
	ds_read_b32 v226, v211
	ds_read_b32 v227, v211 offset:512
	ds_read_b32 v228, v211 offset:1024
	ds_read_b32 v229, v211 offset:1536
	ds_read_b32 v230, v211 offset:2048
	ds_read_b32 v231, v211 offset:2560
	ds_read_b32 v232, v211 offset:3072
	ds_read_b32 v233, v211 offset:3584
	ds_read_b32 v234, v211 offset:4096
	ds_read_b32 v235, v211 offset:4608
	ds_read_b32 v236, v211 offset:5120
	ds_read_b32 v237, v211 offset:5632
	ds_read_b32 v238, v211 offset:6144
	ds_read_b32 v239, v211 offset:6656
	ds_read_b32 v240, v211 offset:7168
	ds_read_b32 v241, v211 offset:7680
	s_waitcnt lgkmcnt(0)
	v_max_f32_e32 v226, v226, v226
	v_max_f32_e32 v227, v227, v227
	v_max_f32_e32 v228, v228, v228
	v_max_f32_e32 v229, v229, v229
	v_max_f32_e32 v230, v230, v230
	v_max_f32_e32 v231, v231, v231
	v_max_f32_e32 v232, v232, v232
	v_max_f32_e32 v233, v233, v233
	v_max_f32_e32 v234, v234, v234
	v_max_f32_e32 v235, v235, v235
	v_max_f32_e32 v236, v236, v236
	v_max_f32_e32 v237, v237, v237
	v_max_f32_e32 v238, v238, v238
	v_max_f32_e32 v239, v239, v239
	v_max_f32_e32 v240, v240, v240
	v_max_f32_e32 v241, v241, v241
	v_med3_f32 v226, v226, s62, v95
	v_med3_f32 v227, v227, s62, v95
	v_med3_f32 v228, v228, s62, v95
	v_med3_f32 v229, v229, s62, v95
	v_med3_f32 v230, v230, s62, v95
	v_med3_f32 v231, v231, s62, v95
	v_med3_f32 v232, v232, s62, v95
	v_med3_f32 v233, v233, s62, v95
	v_med3_f32 v234, v234, s62, v95
	v_med3_f32 v235, v235, s62, v95
	v_med3_f32 v236, v236, s62, v95
	v_med3_f32 v237, v237, s62, v95
	v_med3_f32 v238, v238, s62, v95
	v_med3_f32 v239, v239, s62, v95
	v_med3_f32 v240, v240, s62, v95
	v_med3_f32 v241, v241, s62, v95
	v_mov_b32_e32 v242, 0
	v_mov_b32_e32 v243, 0
	v_mov_b32_e32 v244, 0
	v_mov_b32_e32 v245, 0
	v_cvt_pk_fp8_f32 v242, v226, v227
	v_cvt_pk_fp8_f32 v243, v230, v231
	v_cvt_pk_fp8_f32 v244, v234, v235
	v_cvt_pk_fp8_f32 v245, v238, v239
	v_cvt_pk_fp8_f32 v242, v228, v229 op_sel:[0,0,1]
	v_cvt_pk_fp8_f32 v243, v232, v233 op_sel:[0,0,1]
	v_cvt_pk_fp8_f32 v244, v236, v237 op_sel:[0,0,1]
	v_cvt_pk_fp8_f32 v245, v240, v241 op_sel:[0,0,1]
	s_nop 0
	global_store_dwordx4 v91, v[242:245], s[6:7]
	ds_read_b32 v226, v213
	ds_read_b32 v227, v213 offset:512
	ds_read_b32 v228, v213 offset:1024
	ds_read_b32 v229, v213 offset:1536
	ds_read_b32 v230, v213 offset:2048
	ds_read_b32 v231, v213 offset:2560
	ds_read_b32 v232, v213 offset:3072
	ds_read_b32 v233, v213 offset:3584
	ds_read_b32 v234, v213 offset:4096
	ds_read_b32 v235, v213 offset:4608
	ds_read_b32 v236, v213 offset:5120
	ds_read_b32 v237, v213 offset:5632
	ds_read_b32 v238, v213 offset:6144
	ds_read_b32 v239, v213 offset:6656
	ds_read_b32 v240, v213 offset:7168
	ds_read_b32 v241, v213 offset:7680
	s_waitcnt lgkmcnt(0)
	v_max_f32_e32 v226, v226, v226
	v_max_f32_e32 v227, v227, v227
	v_max_f32_e32 v228, v228, v228
	v_max_f32_e32 v229, v229, v229
	v_max_f32_e32 v230, v230, v230
	v_max_f32_e32 v231, v231, v231
	v_max_f32_e32 v232, v232, v232
	v_max_f32_e32 v233, v233, v233
	v_max_f32_e32 v234, v234, v234
	v_max_f32_e32 v235, v235, v235
	v_max_f32_e32 v236, v236, v236
	v_max_f32_e32 v237, v237, v237
	v_max_f32_e32 v238, v238, v238
	v_max_f32_e32 v239, v239, v239
	v_max_f32_e32 v240, v240, v240
	v_max_f32_e32 v241, v241, v241
	v_med3_f32 v226, v226, s62, v95
	v_med3_f32 v227, v227, s62, v95
	v_med3_f32 v228, v228, s62, v95
	v_med3_f32 v229, v229, s62, v95
	v_med3_f32 v230, v230, s62, v95
	v_med3_f32 v231, v231, s62, v95
	v_med3_f32 v232, v232, s62, v95
	v_med3_f32 v233, v233, s62, v95
	v_med3_f32 v234, v234, s62, v95
	v_med3_f32 v235, v235, s62, v95
	v_med3_f32 v236, v236, s62, v95
	v_med3_f32 v237, v237, s62, v95
	v_med3_f32 v238, v238, s62, v95
	v_med3_f32 v239, v239, s62, v95
	v_med3_f32 v240, v240, s62, v95
	v_med3_f32 v241, v241, s62, v95
	v_mov_b32_e32 v242, 0
	v_mov_b32_e32 v243, 0
	v_mov_b32_e32 v244, 0
	v_mov_b32_e32 v245, 0
	v_cvt_pk_fp8_f32 v242, v226, v227
	v_cvt_pk_fp8_f32 v243, v230, v231
	v_cvt_pk_fp8_f32 v244, v234, v235
	v_cvt_pk_fp8_f32 v245, v238, v239
	v_cvt_pk_fp8_f32 v242, v228, v229 op_sel:[0,0,1]
	v_cvt_pk_fp8_f32 v243, v232, v233 op_sel:[0,0,1]
	v_cvt_pk_fp8_f32 v244, v236, v237 op_sel:[0,0,1]
	v_cvt_pk_fp8_f32 v245, v240, v241 op_sel:[0,0,1]
	s_nop 0
	global_store_dwordx4 v92, v[242:245], s[6:7]
	s_waitcnt vmcnt(12)
	v_mul_f32_e32 v176, v50, v176
	v_mul_f32_e32 v177, v50, v177
	v_mul_f32_e32 v178, v50, v178
	v_mul_f32_e32 v179, v50, v179
	ds_write_b128 v210, v[176:179]
	v_mul_f32_e32 v180, v51, v180
	v_mul_f32_e32 v181, v51, v181
	v_mul_f32_e32 v182, v51, v182
	v_mul_f32_e32 v183, v51, v183
	ds_write_b128 v210, v[180:183] offset:1024
	v_mul_f32_e32 v184, v52, v184
	v_mul_f32_e32 v185, v52, v185
	v_mul_f32_e32 v186, v52, v186
	v_mul_f32_e32 v187, v52, v187
	ds_write_b128 v210, v[184:187] offset:2048
	v_mul_f32_e32 v188, v53, v188
	v_mul_f32_e32 v189, v53, v189
	v_mul_f32_e32 v190, v53, v190
	v_mul_f32_e32 v191, v53, v191
	ds_write_b128 v210, v[188:191] offset:3072
	v_mul_f32_e32 v192, v54, v192
	v_mul_f32_e32 v193, v54, v193
	v_mul_f32_e32 v194, v54, v194
	v_mul_f32_e32 v195, v54, v195
	ds_write_b128 v210, v[192:195] offset:4096
	v_mul_f32_e32 v196, v55, v196
	v_mul_f32_e32 v197, v55, v197
	v_mul_f32_e32 v198, v55, v198
	v_mul_f32_e32 v199, v55, v199
	ds_write_b128 v210, v[196:199] offset:5120
	v_mul_f32_e32 v200, v56, v200
	v_mul_f32_e32 v201, v56, v201
	v_mul_f32_e32 v202, v56, v202
	v_mul_f32_e32 v203, v56, v203
	ds_write_b128 v210, v[200:203] offset:6144
	v_mul_f32_e32 v204, v57, v204
	v_mul_f32_e32 v205, v57, v205
	v_mul_f32_e32 v206, v57, v206
	v_mul_f32_e32 v207, v57, v207
	ds_write_b128 v210, v[204:207] offset:7168
	s_waitcnt lgkmcnt(0)
	s_barrier
; #define GAS __attribute__((address_space(1)))
; #define LAS __attribute__((address_space(3)))
; #define LDS_WAIT() asm volatile("s_waitcnt lgkmcnt(0)" ::: "memory")
; __device__ __forceinline__ unsigned pk4_fp8(float a, float b, float c, float d) {
;     a = fminf(fmaxf(a, -448.f), 448.f); b = fminf(fmaxf(b, -448.f), 448.f); c = fminf(fmaxf(c, -448.f), 448.f); d = fminf(fmaxf(d, -448.f), 448.f);
;     int w = __builtin_amdgcn_cvt_pk_fp8_f32(a, b, 0, false); w = __builtin_amdgcn_cvt_pk_fp8_f32(c, d, w, true); return (unsigned)w; }
;     const int pr = item >> 1, kb = 2 * (pr / nblk) + (item & 1), nb = pr % nblk, k0 = 64 * kb, n0 = 32 * nb;
;     const int nr = n0 + (lane & 31); const int sc = MAP == 1 ? src_col_in(nr) : nr;
;     float v[32];
; #pragma unroll
;     for (int i = 0; i < 32; ++i) v[i] = sc >= 0 ? W[(size_t)(k0 + 2 * i + (lane >> 5)) * Nsrc + sc] : 0.f;
; #pragma unroll
;     for (int i = 0; i < 32; ++i) { const int k = k0 + 2 * i + (lane >> 5); float x = v[i] * wscale; if (KS) x *= (k < ksplit ? ksA[k] : ksB[k - ksplit]); scr[(2 * i + (lane >> 5)) * 33 + (lane & 31)] = x; }
;     LDS_WAIT(); asm volatile("" ::: "memory");
;     const int c = lane & 7;
; #pragma unroll
;     for (int j = 0; j < 4; ++j) { const int n = (lane >> 3) + 8 * j; const LAS float* s = scr + (8 * c) * 33 + n;
;         const unsigned long long o = (unsigned long long)pg8::pk4_fp8(s[0 * 33], s[1 * 33], s[2 * 33], s[3 * 33]) | ((unsigned long long)pg8::pk4_fp8(s[4 * 33], s[5 * 33], s[6 * 33], s[7 * 33]) << 32);
;         *(GAS unsigned long long*)(WT + (size_t)(n0 + n) * K + k0 + 8 * c) = o; }
;     LDS_WAIT(); asm volatile("" ::: "memory");
; }
	s_add_i32 s24, s23, 48
	s_lshl_b32 s20, s24, 7
	s_cmp_lt_u32 s24, 40
	s_cselect_b32 s21, 0, 0x830
	s_cmp_lt_u32 s24, 72
	s_cselect_b32 s21, s21, 0xfffff030
	s_add_i32 s20, s20, s21
	s_lshl_b32 s20, s20, 2
	s_add_u32 s8, s50, s20
	s_addc_u32 s9, s51, 0
	global_load_dwordx4 v[176:179], v76, s[8:9]
	s_add_u32 s8, s8, 0x16280
	s_addc_u32 s9, s9, 0
	global_load_dwordx4 v[180:183], v76, s[8:9]
	s_add_u32 s8, s8, 0x16280
	s_addc_u32 s9, s9, 0
	global_load_dwordx4 v[184:187], v76, s[8:9]
	s_add_u32 s8, s8, 0x16280
	s_addc_u32 s9, s9, 0
	global_load_dwordx4 v[188:191], v76, s[8:9]
	s_add_u32 s8, s8, 0x16280
	s_addc_u32 s9, s9, 0
	global_load_dwordx4 v[192:195], v76, s[8:9]
	s_add_u32 s8, s8, 0x16280
	s_addc_u32 s9, s9, 0
	global_load_dwordx4 v[196:199], v76, s[8:9]
	s_add_u32 s8, s8, 0x16280
	s_addc_u32 s9, s9, 0
	global_load_dwordx4 v[200:203], v76, s[8:9]
	s_add_u32 s8, s8, 0x16280
	s_addc_u32 s9, s9, 0
	global_load_dwordx4 v[204:207], v76, s[8:9]
	s_add_i32 s24, s23, 32
	s_mul_i32 s20, s24, 0x80000
	s_add_u32 s6, s52, s20
	s_addc_u32 s7, s53, 0
	s_cmp_lt_u32 s24, 16
	s_cselect_b32 s20, 1, 0
	s_sub_i32 s21, s24, 16
	s_bitcmp0_b32 s21, 2
	s_cselect_b32 s21, 1, 0
	s_cmp_lt_u32 s24, 40
	s_cselect_b32 s21, s21, 0
	s_or_b32 s20, s20, s21
	s_cmp_lg_u32 s20, 0
	s_cselect_b64 s[20:21], -1, 0
	v_cndmask_b32_e64 v91, v77, v81, s[20:21]
	v_cndmask_b32_e64 v92, v78, v82, s[20:21]
	ds_read_b32 v226, v212
	ds_read_b32 v227, v212 offset:512
	ds_read_b32 v228, v212 offset:1024
	ds_read_b32 v229, v212 offset:1536
	ds_read_b32 v230, v212 offset:2048
	ds_read_b32 v231, v212 offset:2560
	ds_read_b32 v232, v212 offset:3072
	ds_read_b32 v233, v212 offset:3584
	ds_read_b32 v234, v212 offset:4096
	ds_read_b32 v235, v212 offset:4608
	ds_read_b32 v236, v212 offset:5120
	ds_read_b32 v237, v212 offset:5632
	ds_read_b32 v238, v212 offset:6144
	ds_read_b32 v239, v212 offset:6656
	ds_read_b32 v240, v212 offset:7168
	ds_read_b32 v241, v212 offset:7680
	s_waitcnt lgkmcnt(0)
	v_max_f32_e32 v226, v226, v226
	v_max_f32_e32 v227, v227, v227
	v_max_f32_e32 v228, v228, v228
	v_max_f32_e32 v229, v229, v229
	v_max_f32_e32 v230, v230, v230
	v_max_f32_e32 v231, v231, v231
	v_max_f32_e32 v232, v232, v232
	v_max_f32_e32 v233, v233, v233
	v_max_f32_e32 v234, v234, v234
	v_max_f32_e32 v235, v235, v235
	v_max_f32_e32 v236, v236, v236
	v_max_f32_e32 v237, v237, v237
	v_max_f32_e32 v238, v238, v238
	v_max_f32_e32 v239, v239, v239
	v_max_f32_e32 v240, v240, v240
	v_max_f32_e32 v241, v241, v241
	v_med3_f32 v226, v226, s62, v95
	v_med3_f32 v227, v227, s62, v95
	v_med3_f32 v228, v228, s62, v95
	v_med3_f32 v229, v229, s62, v95
	v_med3_f32 v230, v230, s62, v95
	v_med3_f32 v231, v231, s62, v95
	v_med3_f32 v232, v232, s62, v95
	v_med3_f32 v233, v233, s62, v95
	v_med3_f32 v234, v234, s62, v95
	v_med3_f32 v235, v235, s62, v95
	v_med3_f32 v236, v236, s62, v95
	v_med3_f32 v237, v237, s62, v95
	v_med3_f32 v238, v238, s62, v95
	v_med3_f32 v239, v239, s62, v95
	v_med3_f32 v240, v240, s62, v95
	v_med3_f32 v241, v241, s62, v95
	v_mov_b32_e32 v242, 0
	v_mov_b32_e32 v243, 0
	v_mov_b32_e32 v244, 0
	v_mov_b32_e32 v245, 0
	v_cvt_pk_fp8_f32 v242, v226, v227
	v_cvt_pk_fp8_f32 v243, v230, v231
	v_cvt_pk_fp8_f32 v244, v234, v235
	v_cvt_pk_fp8_f32 v245, v238, v239
	v_cvt_pk_fp8_f32 v242, v228, v229 op_sel:[0,0,1]
	v_cvt_pk_fp8_f32 v243, v232, v233 op_sel:[0,0,1]
	v_cvt_pk_fp8_f32 v244, v236, v237 op_sel:[0,0,1]
	v_cvt_pk_fp8_f32 v245, v240, v241 op_sel:[0,0,1]
	s_nop 0
	global_store_dwordx4 v91, v[242:245], s[6:7]
	ds_read_b32 v226, v214
	ds_read_b32 v227, v214 offset:512
	ds_read_b32 v228, v214 offset:1024
	ds_read_b32 v229, v214 offset:1536
	ds_read_b32 v230, v214 offset:2048
	ds_read_b32 v231, v214 offset:2560
	ds_read_b32 v232, v214 offset:3072
	ds_read_b32 v233, v214 offset:3584
	ds_read_b32 v234, v214 offset:4096
	ds_read_b32 v235, v214 offset:4608
	ds_read_b32 v236, v214 offset:5120
	ds_read_b32 v237, v214 offset:5632
	ds_read_b32 v238, v214 offset:6144
	ds_read_b32 v239, v214 offset:6656
	ds_read_b32 v240, v214 offset:7168
	ds_read_b32 v241, v214 offset:7680
	s_waitcnt lgkmcnt(0)
	v_max_f32_e32 v226, v226, v226
	v_max_f32_e32 v227, v227, v227
	v_max_f32_e32 v228, v228, v228
	v_max_f32_e32 v229, v229, v229
	v_max_f32_e32 v230, v230, v230
	v_max_f32_e32 v231, v231, v231
	v_max_f32_e32 v232, v232, v232
	v_max_f32_e32 v233, v233, v233
	v_max_f32_e32 v234, v234, v234
	v_max_f32_e32 v235, v235, v235
	v_max_f32_e32 v236, v236, v236
	v_max_f32_e32 v237, v237, v237
	v_max_f32_e32 v238, v238, v238
	v_max_f32_e32 v239, v239, v239
	v_max_f32_e32 v240, v240, v240
	v_max_f32_e32 v241, v241, v241
	v_med3_f32 v226, v226, s62, v95
	v_med3_f32 v227, v227, s62, v95
	v_med3_f32 v228, v228, s62, v95
	v_med3_f32 v229, v229, s62, v95
	v_med3_f32 v230, v230, s62, v95
	v_med3_f32 v231, v231, s62, v95
	v_med3_f32 v232, v232, s62, v95
	v_med3_f32 v233, v233, s62, v95
	v_med3_f32 v234, v234, s62, v95
	v_med3_f32 v235, v235, s62, v95
	v_med3_f32 v236, v236, s62, v95
	v_med3_f32 v237, v237, s62, v95
	v_med3_f32 v238, v238, s62, v95
	v_med3_f32 v239, v239, s62, v95
	v_med3_f32 v240, v240, s62, v95
	v_med3_f32 v241, v241, s62, v95
	v_mov_b32_e32 v242, 0
	v_mov_b32_e32 v243, 0
	v_mov_b32_e32 v244, 0
	v_mov_b32_e32 v245, 0
	v_cvt_pk_fp8_f32 v242, v226, v227
	v_cvt_pk_fp8_f32 v243, v230, v231
	v_cvt_pk_fp8_f32 v244, v234, v235
	v_cvt_pk_fp8_f32 v245, v238, v239
	v_cvt_pk_fp8_f32 v242, v228, v229 op_sel:[0,0,1]
	v_cvt_pk_fp8_f32 v243, v232, v233 op_sel:[0,0,1]
	v_cvt_pk_fp8_f32 v244, v236, v237 op_sel:[0,0,1]
	v_cvt_pk_fp8_f32 v245, v240, v241 op_sel:[0,0,1]
	s_nop 0
	global_store_dwordx4 v92, v[242:245], s[6:7]
	s_waitcnt vmcnt(12)
	v_mul_f32_e32 v144, v50, v144
	v_mul_f32_e32 v145, v50, v145
	v_mul_f32_e32 v146, v50, v146
	v_mul_f32_e32 v147, v50, v147
	ds_write_b128 v209, v[144:147]
	v_mul_f32_e32 v148, v51, v148
	v_mul_f32_e32 v149, v51, v149
	v_mul_f32_e32 v150, v51, v150
	v_mul_f32_e32 v151, v51, v151
	ds_write_b128 v209, v[148:151] offset:1024
	v_mul_f32_e32 v152, v52, v152
	v_mul_f32_e32 v153, v52, v153
	v_mul_f32_e32 v154, v52, v154
	v_mul_f32_e32 v155, v52, v155
	ds_write_b128 v209, v[152:155] offset:2048
	v_mul_f32_e32 v156, v53, v156
	v_mul_f32_e32 v157, v53, v157
	v_mul_f32_e32 v158, v53, v158
	v_mul_f32_e32 v159, v53, v159
	ds_write_b128 v209, v[156:159] offset:3072
	v_mul_f32_e32 v160, v54, v160
	v_mul_f32_e32 v161, v54, v161
	v_mul_f32_e32 v162, v54, v162
	v_mul_f32_e32 v163, v54, v163
	ds_write_b128 v209, v[160:163] offset:4096
	v_mul_f32_e32 v164, v55, v164
	v_mul_f32_e32 v165, v55, v165
	v_mul_f32_e32 v166, v55, v166
	v_mul_f32_e32 v167, v55, v167
	ds_write_b128 v209, v[164:167] offset:5120
	v_mul_f32_e32 v168, v56, v168
	v_mul_f32_e32 v169, v56, v169
	v_mul_f32_e32 v170, v56, v170
	v_mul_f32_e32 v171, v56, v171
	ds_write_b128 v209, v[168:171] offset:6144
	v_mul_f32_e32 v172, v57, v172
	v_mul_f32_e32 v173, v57, v173
	v_mul_f32_e32 v174, v57, v174
	v_mul_f32_e32 v175, v57, v175
	ds_write_b128 v209, v[172:175] offset:7168
	s_waitcnt lgkmcnt(0)
	s_barrier
; #define GAS __attribute__((address_space(1)))
; #define LAS __attribute__((address_space(3)))
; #define LDS_WAIT() asm volatile("s_waitcnt lgkmcnt(0)" ::: "memory")
; __device__ __forceinline__ unsigned pk4_fp8(float a, float b, float c, float d) {
;     a = fminf(fmaxf(a, -448.f), 448.f); b = fminf(fmaxf(b, -448.f), 448.f); c = fminf(fmaxf(c, -448.f), 448.f); d = fminf(fmaxf(d, -448.f), 448.f);
;     int w = __builtin_amdgcn_cvt_pk_fp8_f32(a, b, 0, false); w = __builtin_amdgcn_cvt_pk_fp8_f32(c, d, w, true); return (unsigned)w; }
;     const int pr = item >> 1, kb = 2 * (pr / nblk) + (item & 1), nb = pr % nblk, k0 = 64 * kb, n0 = 32 * nb;
;     const int nr = n0 + (lane & 31); const int sc = MAP == 1 ? src_col_in(nr) : nr;
;     float v[32];
; #pragma unroll
;     for (int i = 0; i < 32; ++i) v[i] = sc >= 0 ? W[(size_t)(k0 + 2 * i + (lane >> 5)) * Nsrc + sc] : 0.f;
; #pragma unroll
;     for (int i = 0; i < 32; ++i) { const int k = k0 + 2 * i + (lane >> 5); float x = v[i] * wscale; if (KS) x *= (k < ksplit ? ksA[k] : ksB[k - ksplit]); scr[(2 * i + (lane >> 5)) * 33 + (lane & 31)] = x; }
;     LDS_WAIT(); asm volatile("" ::: "memory");
;     const int c = lane & 7;
; #pragma unroll
;     for (int j = 0; j < 4; ++j) { const int n = (lane >> 3) + 8 * j; const LAS float* s = scr + (8 * c) * 33 + n;
;         const unsigned long long o = (unsigned long long)pg8::pk4_fp8(s[0 * 33], s[1 * 33], s[2 * 33], s[3 * 33]) | ((unsigned long long)pg8::pk4_fp8(s[4 * 33], s[5 * 33], s[6 * 33], s[7 * 33]) << 32);
;         *(GAS unsigned long long*)(WT + (size_t)(n0 + n) * K + k0 + 8 * c) = o; }
;     LDS_WAIT(); asm volatile("" ::: "memory");
; }
	s_add_i32 s24, s23, 56
	s_lshl_b32 s20, s24, 7
	s_cmp_lt_u32 s24, 40
	s_cselect_b32 s21, 0, 0x830
	s_cmp_lt_u32 s24, 72
	s_cselect_b32 s21, s21, 0xfffff030
	s_add_i32 s20, s20, s21
	s_lshl_b32 s20, s20, 2
	s_add_u32 s8, s50, s20
	s_addc_u32 s9, s51, 0
	global_load_dwordx4 v[144:147], v76, s[8:9]
	s_add_u32 s8, s8, 0x16280
	s_addc_u32 s9, s9, 0
	global_load_dwordx4 v[148:151], v76, s[8:9]
	s_add_u32 s8, s8, 0x16280
	s_addc_u32 s9, s9, 0
	global_load_dwordx4 v[152:155], v76, s[8:9]
	s_add_u32 s8, s8, 0x16280
	s_addc_u32 s9, s9, 0
	global_load_dwordx4 v[156:159], v76, s[8:9]
	s_add_u32 s8, s8, 0x16280
	s_addc_u32 s9, s9, 0
	global_load_dwordx4 v[160:163], v76, s[8:9]
	s_add_u32 s8, s8, 0x16280
	s_addc_u32 s9, s9, 0
	global_load_dwordx4 v[164:167], v76, s[8:9]
	s_add_u32 s8, s8, 0x16280
	s_addc_u32 s9, s9, 0
	global_load_dwordx4 v[168:171], v76, s[8:9]
	s_add_u32 s8, s8, 0x16280
	s_addc_u32 s9, s9, 0
	global_load_dwordx4 v[172:175], v76, s[8:9]
	s_add_i32 s24, s23, 40
	s_mul_i32 s20, s24, 0x80000
	s_add_u32 s6, s52, s20
	s_addc_u32 s7, s53, 0
	s_cmp_lt_u32 s24, 16
	s_cselect_b32 s20, 1, 0
	s_sub_i32 s21, s24, 16
	s_bitcmp0_b32 s21, 2
	s_cselect_b32 s21, 1, 0
	s_cmp_lt_u32 s24, 40
	s_cselect_b32 s21, s21, 0
	s_or_b32 s20, s20, s21
	s_cmp_lg_u32 s20, 0
	s_cselect_b64 s[20:21], -1, 0
	v_cndmask_b32_e64 v91, v77, v81, s[20:21]
	v_cndmask_b32_e64 v92, v78, v82, s[20:21]
	ds_read_b32 v226, v211
	ds_read_b32 v227, v211 offset:512
	ds_read_b32 v228, v211 offset:1024
	ds_read_b32 v229, v211 offset:1536
	ds_read_b32 v230, v211 offset:2048
	ds_read_b32 v231, v211 offset:2560
	ds_read_b32 v232, v211 offset:3072
	ds_read_b32 v233, v211 offset:3584
	ds_read_b32 v234, v211 offset:4096
	ds_read_b32 v235, v211 offset:4608
	ds_read_b32 v236, v211 offset:5120
	ds_read_b32 v237, v211 offset:5632
	ds_read_b32 v238, v211 offset:6144
	ds_read_b32 v239, v211 offset:6656
	ds_read_b32 v240, v211 offset:7168
	ds_read_b32 v241, v211 offset:7680
	s_waitcnt lgkmcnt(0)
	v_max_f32_e32 v226, v226, v226
	v_max_f32_e32 v227, v227, v227
	v_max_f32_e32 v228, v228, v228
	v_max_f32_e32 v229, v229, v229
	v_max_f32_e32 v230, v230, v230
	v_max_f32_e32 v231, v231, v231
	v_max_f32_e32 v232, v232, v232
	v_max_f32_e32 v233, v233, v233
	v_max_f32_e32 v234, v234, v234
	v_max_f32_e32 v235, v235, v235
	v_max_f32_e32 v236, v236, v236
	v_max_f32_e32 v237, v237, v237
	v_max_f32_e32 v238, v238, v238
	v_max_f32_e32 v239, v239, v239
	v_max_f32_e32 v240, v240, v240
	v_max_f32_e32 v241, v241, v241
	v_med3_f32 v226, v226, s62, v95
	v_med3_f32 v227, v227, s62, v95
	v_med3_f32 v228, v228, s62, v95
	v_med3_f32 v229, v229, s62, v95
	v_med3_f32 v230, v230, s62, v95
	v_med3_f32 v231, v231, s62, v95
	v_med3_f32 v232, v232, s62, v95
	v_med3_f32 v233, v233, s62, v95
	v_med3_f32 v234, v234, s62, v95
	v_med3_f32 v235, v235, s62, v95
	v_med3_f32 v236, v236, s62, v95
	v_med3_f32 v237, v237, s62, v95
	v_med3_f32 v238, v238, s62, v95
	v_med3_f32 v239, v239, s62, v95
	v_med3_f32 v240, v240, s62, v95
	v_med3_f32 v241, v241, s62, v95
	v_mov_b32_e32 v242, 0
	v_mov_b32_e32 v243, 0
	v_mov_b32_e32 v244, 0
	v_mov_b32_e32 v245, 0
	v_cvt_pk_fp8_f32 v242, v226, v227
	v_cvt_pk_fp8_f32 v243, v230, v231
	v_cvt_pk_fp8_f32 v244, v234, v235
	v_cvt_pk_fp8_f32 v245, v238, v239
	v_cvt_pk_fp8_f32 v242, v228, v229 op_sel:[0,0,1]
	v_cvt_pk_fp8_f32 v243, v232, v233 op_sel:[0,0,1]
	v_cvt_pk_fp8_f32 v244, v236, v237 op_sel:[0,0,1]
	v_cvt_pk_fp8_f32 v245, v240, v241 op_sel:[0,0,1]
	s_nop 0
	global_store_dwordx4 v91, v[242:245], s[6:7]
	ds_read_b32 v226, v213
	ds_read_b32 v227, v213 offset:512
	ds_read_b32 v228, v213 offset:1024
	ds_read_b32 v229, v213 offset:1536
	ds_read_b32 v230, v213 offset:2048
	ds_read_b32 v231, v213 offset:2560
	ds_read_b32 v232, v213 offset:3072
	ds_read_b32 v233, v213 offset:3584
	ds_read_b32 v234, v213 offset:4096
	ds_read_b32 v235, v213 offset:4608
	ds_read_b32 v236, v213 offset:5120
	ds_read_b32 v237, v213 offset:5632
	ds_read_b32 v238, v213 offset:6144
	ds_read_b32 v239, v213 offset:6656
	ds_read_b32 v240, v213 offset:7168
	ds_read_b32 v241, v213 offset:7680
	s_waitcnt lgkmcnt(0)
	v_max_f32_e32 v226, v226, v226
	v_max_f32_e32 v227, v227, v227
	v_max_f32_e32 v228, v228, v228
	v_max_f32_e32 v229, v229, v229
	v_max_f32_e32 v230, v230, v230
	v_max_f32_e32 v231, v231, v231
	v_max_f32_e32 v232, v232, v232
	v_max_f32_e32 v233, v233, v233
	v_max_f32_e32 v234, v234, v234
	v_max_f32_e32 v235, v235, v235
	v_max_f32_e32 v236, v236, v236
	v_max_f32_e32 v237, v237, v237
	v_max_f32_e32 v238, v238, v238
	v_max_f32_e32 v239, v239, v239
	v_max_f32_e32 v240, v240, v240
	v_max_f32_e32 v241, v241, v241
	v_med3_f32 v226, v226, s62, v95
	v_med3_f32 v227, v227, s62, v95
	v_med3_f32 v228, v228, s62, v95
	v_med3_f32 v229, v229, s62, v95
	v_med3_f32 v230, v230, s62, v95
	v_med3_f32 v231, v231, s62, v95
	v_med3_f32 v232, v232, s62, v95
	v_med3_f32 v233, v233, s62, v95
	v_med3_f32 v234, v234, s62, v95
	v_med3_f32 v235, v235, s62, v95
	v_med3_f32 v236, v236, s62, v95
	v_med3_f32 v237, v237, s62, v95
	v_med3_f32 v238, v238, s62, v95
	v_med3_f32 v239, v239, s62, v95
	v_med3_f32 v240, v240, s62, v95
	v_med3_f32 v241, v241, s62, v95
	v_mov_b32_e32 v242, 0
	v_mov_b32_e32 v243, 0
	v_mov_b32_e32 v244, 0
	v_mov_b32_e32 v245, 0
	v_cvt_pk_fp8_f32 v242, v226, v227
	v_cvt_pk_fp8_f32 v243, v230, v231
	v_cvt_pk_fp8_f32 v244, v234, v235
	v_cvt_pk_fp8_f32 v245, v238, v239
	v_cvt_pk_fp8_f32 v242, v228, v229 op_sel:[0,0,1]
	v_cvt_pk_fp8_f32 v243, v232, v233 op_sel:[0,0,1]
	v_cvt_pk_fp8_f32 v244, v236, v237 op_sel:[0,0,1]
	v_cvt_pk_fp8_f32 v245, v240, v241 op_sel:[0,0,1]
	s_nop 0
	global_store_dwordx4 v92, v[242:245], s[6:7]
	s_waitcnt vmcnt(12)
	v_mul_f32_e32 v176, v50, v176
	v_mul_f32_e32 v177, v50, v177
	v_mul_f32_e32 v178, v50, v178
	v_mul_f32_e32 v179, v50, v179
	ds_write_b128 v210, v[176:179]
	v_mul_f32_e32 v180, v51, v180
	v_mul_f32_e32 v181, v51, v181
	v_mul_f32_e32 v182, v51, v182
	v_mul_f32_e32 v183, v51, v183
	ds_write_b128 v210, v[180:183] offset:1024
	v_mul_f32_e32 v184, v52, v184
	v_mul_f32_e32 v185, v52, v185
	v_mul_f32_e32 v186, v52, v186
	v_mul_f32_e32 v187, v52, v187
	ds_write_b128 v210, v[184:187] offset:2048
	v_mul_f32_e32 v188, v53, v188
	v_mul_f32_e32 v189, v53, v189
	v_mul_f32_e32 v190, v53, v190
	v_mul_f32_e32 v191, v53, v191
	ds_write_b128 v210, v[188:191] offset:3072
	v_mul_f32_e32 v192, v54, v192
	v_mul_f32_e32 v193, v54, v193
	v_mul_f32_e32 v194, v54, v194
	v_mul_f32_e32 v195, v54, v195
	ds_write_b128 v210, v[192:195] offset:4096
	v_mul_f32_e32 v196, v55, v196
	v_mul_f32_e32 v197, v55, v197
	v_mul_f32_e32 v198, v55, v198
	v_mul_f32_e32 v199, v55, v199
	ds_write_b128 v210, v[196:199] offset:5120
	v_mul_f32_e32 v200, v56, v200
	v_mul_f32_e32 v201, v56, v201
	v_mul_f32_e32 v202, v56, v202
	v_mul_f32_e32 v203, v56, v203
	ds_write_b128 v210, v[200:203] offset:6144
	v_mul_f32_e32 v204, v57, v204
	v_mul_f32_e32 v205, v57, v205
	v_mul_f32_e32 v206, v57, v206
	v_mul_f32_e32 v207, v57, v207
	ds_write_b128 v210, v[204:207] offset:7168
	s_waitcnt lgkmcnt(0)
	s_barrier
; #define GAS __attribute__((address_space(1)))
; #define LAS __attribute__((address_space(3)))
; #define LDS_WAIT() asm volatile("s_waitcnt lgkmcnt(0)" ::: "memory")
; __device__ __forceinline__ unsigned pk4_fp8(float a, float b, float c, float d) {
;     a = fminf(fmaxf(a, -448.f), 448.f); b = fminf(fmaxf(b, -448.f), 448.f); c = fminf(fmaxf(c, -448.f), 448.f); d = fminf(fmaxf(d, -448.f), 448.f);
;     int w = __builtin_amdgcn_cvt_pk_fp8_f32(a, b, 0, false); w = __builtin_amdgcn_cvt_pk_fp8_f32(c, d, w, true); return (unsigned)w; }
;     const int pr = item >> 1, kb = 2 * (pr / nblk) + (item & 1), nb = pr % nblk, k0 = 64 * kb, n0 = 32 * nb;
;     const int nr = n0 + (lane & 31); const int sc = MAP == 1 ? src_col_in(nr) : nr;
;     float v[32];
; #pragma unroll
;     for (int i = 0; i < 32; ++i) v[i] = sc >= 0 ? W[(size_t)(k0 + 2 * i + (lane >> 5)) * Nsrc + sc] : 0.f;
; #pragma unroll
;     for (int i = 0; i < 32; ++i) { const int k = k0 + 2 * i + (lane >> 5); float x = v[i] * wscale; if (KS) x *= (k < ksplit ? ksA[k] : ksB[k - ksplit]); scr[(2 * i + (lane >> 5)) * 33 + (lane & 31)] = x; }
;     LDS_WAIT(); asm volatile("" ::: "memory");
;     const int c = lane & 7;
; #pragma unroll
;     for (int j = 0; j < 4; ++j) { const int n = (lane >> 3) + 8 * j; const LAS float* s = scr + (8 * c) * 33 + n;
;         const unsigned long long o = (unsigned long long)pg8::pk4_fp8(s[0 * 33], s[1 * 33], s[2 * 33], s[3 * 33]) | ((unsigned long long)pg8::pk4_fp8(s[4 * 33], s[5 * 33], s[6 * 33], s[7 * 33]) << 32);
;         *(GAS unsigned long long*)(WT + (size_t)(n0 + n) * K + k0 + 8 * c) = o; }
;     LDS_WAIT(); asm volatile("" ::: "memory");
; }
	s_add_i32 s24, s23, 64
	s_lshl_b32 s20, s24, 7
	s_cmp_lt_u32 s24, 40
	s_cselect_b32 s21, 0, 0x830
	s_cmp_lt_u32 s24, 72
	s_cselect_b32 s21, s21, 0xfffff030
	s_add_i32 s20, s20, s21
	s_lshl_b32 s20, s20, 2
	s_add_u32 s8, s50, s20
	s_addc_u32 s9, s51, 0
	global_load_dwordx4 v[176:179], v76, s[8:9]
	s_add_u32 s8, s8, 0x16280
	s_addc_u32 s9, s9, 0
	global_load_dwordx4 v[180:183], v76, s[8:9]
	s_add_u32 s8, s8, 0x16280
	s_addc_u32 s9, s9, 0
	global_load_dwordx4 v[184:187], v76, s[8:9]
	s_add_u32 s8, s8, 0x16280
	s_addc_u32 s9, s9, 0
	global_load_dwordx4 v[188:191], v76, s[8:9]
	s_add_u32 s8, s8, 0x16280
	s_addc_u32 s9, s9, 0
	global_load_dwordx4 v[192:195], v76, s[8:9]
	s_add_u32 s8, s8, 0x16280
	s_addc_u32 s9, s9, 0
	global_load_dwordx4 v[196:199], v76, s[8:9]
	s_add_u32 s8, s8, 0x16280
	s_addc_u32 s9, s9, 0
	global_load_dwordx4 v[200:203], v76, s[8:9]
	s_add_u32 s8, s8, 0x16280
	s_addc_u32 s9, s9, 0
	global_load_dwordx4 v[204:207], v76, s[8:9]
	s_add_i32 s24, s23, 48
	s_mul_i32 s20, s24, 0x80000
	s_add_u32 s6, s52, s20
	s_addc_u32 s7, s53, 0
	s_cmp_lt_u32 s24, 16
	s_cselect_b32 s20, 1, 0
	s_sub_i32 s21, s24, 16
	s_bitcmp0_b32 s21, 2
	s_cselect_b32 s21, 1, 0
	s_cmp_lt_u32 s24, 40
	s_cselect_b32 s21, s21, 0
	s_or_b32 s20, s20, s21
	s_cmp_lg_u32 s20, 0
	s_cselect_b64 s[20:21], -1, 0
	v_cndmask_b32_e64 v91, v77, v81, s[20:21]
	v_cndmask_b32_e64 v92, v78, v82, s[20:21]
	ds_read_b32 v226, v212
	ds_read_b32 v227, v212 offset:512
	ds_read_b32 v228, v212 offset:1024
	ds_read_b32 v229, v212 offset:1536
	ds_read_b32 v230, v212 offset:2048
	ds_read_b32 v231, v212 offset:2560
	ds_read_b32 v232, v212 offset:3072
	ds_read_b32 v233, v212 offset:3584
	ds_read_b32 v234, v212 offset:4096
	ds_read_b32 v235, v212 offset:4608
	ds_read_b32 v236, v212 offset:5120
	ds_read_b32 v237, v212 offset:5632
	ds_read_b32 v238, v212 offset:6144
	ds_read_b32 v239, v212 offset:6656
	ds_read_b32 v240, v212 offset:7168
	ds_read_b32 v241, v212 offset:7680
	s_waitcnt lgkmcnt(0)
	v_max_f32_e32 v226, v226, v226
	v_max_f32_e32 v227, v227, v227
	v_max_f32_e32 v228, v228, v228
	v_max_f32_e32 v229, v229, v229
	v_max_f32_e32 v230, v230, v230
	v_max_f32_e32 v231, v231, v231
	v_max_f32_e32 v232, v232, v232
	v_max_f32_e32 v233, v233, v233
	v_max_f32_e32 v234, v234, v234
	v_max_f32_e32 v235, v235, v235
	v_max_f32_e32 v236, v236, v236
	v_max_f32_e32 v237, v237, v237
	v_max_f32_e32 v238, v238, v238
	v_max_f32_e32 v239, v239, v239
	v_max_f32_e32 v240, v240, v240
	v_max_f32_e32 v241, v241, v241
	v_med3_f32 v226, v226, s62, v95
	v_med3_f32 v227, v227, s62, v95
	v_med3_f32 v228, v228, s62, v95
	v_med3_f32 v229, v229, s62, v95
	v_med3_f32 v230, v230, s62, v95
	v_med3_f32 v231, v231, s62, v95
	v_med3_f32 v232, v232, s62, v95
	v_med3_f32 v233, v233, s62, v95
	v_med3_f32 v234, v234, s62, v95
	v_med3_f32 v235, v235, s62, v95
	v_med3_f32 v236, v236, s62, v95
	v_med3_f32 v237, v237, s62, v95
	v_med3_f32 v238, v238, s62, v95
	v_med3_f32 v239, v239, s62, v95
	v_med3_f32 v240, v240, s62, v95
	v_med3_f32 v241, v241, s62, v95
	v_mov_b32_e32 v242, 0
	v_mov_b32_e32 v243, 0
	v_mov_b32_e32 v244, 0
	v_mov_b32_e32 v245, 0
	v_cvt_pk_fp8_f32 v242, v226, v227
	v_cvt_pk_fp8_f32 v243, v230, v231
	v_cvt_pk_fp8_f32 v244, v234, v235
	v_cvt_pk_fp8_f32 v245, v238, v239
	v_cvt_pk_fp8_f32 v242, v228, v229 op_sel:[0,0,1]
	v_cvt_pk_fp8_f32 v243, v232, v233 op_sel:[0,0,1]
	v_cvt_pk_fp8_f32 v244, v236, v237 op_sel:[0,0,1]
	v_cvt_pk_fp8_f32 v245, v240, v241 op_sel:[0,0,1]
	s_nop 0
	global_store_dwordx4 v91, v[242:245], s[6:7]
	ds_read_b32 v226, v214
	ds_read_b32 v227, v214 offset:512
	ds_read_b32 v228, v214 offset:1024
	ds_read_b32 v229, v214 offset:1536
	ds_read_b32 v230, v214 offset:2048
	ds_read_b32 v231, v214 offset:2560
	ds_read_b32 v232, v214 offset:3072
	ds_read_b32 v233, v214 offset:3584
	ds_read_b32 v234, v214 offset:4096
	ds_read_b32 v235, v214 offset:4608
	ds_read_b32 v236, v214 offset:5120
	ds_read_b32 v237, v214 offset:5632
	ds_read_b32 v238, v214 offset:6144
	ds_read_b32 v239, v214 offset:6656
	ds_read_b32 v240, v214 offset:7168
	ds_read_b32 v241, v214 offset:7680
	s_waitcnt lgkmcnt(0)
	v_max_f32_e32 v226, v226, v226
	v_max_f32_e32 v227, v227, v227
	v_max_f32_e32 v228, v228, v228
	v_max_f32_e32 v229, v229, v229
	v_max_f32_e32 v230, v230, v230
	v_max_f32_e32 v231, v231, v231
	v_max_f32_e32 v232, v232, v232
	v_max_f32_e32 v233, v233, v233
	v_max_f32_e32 v234, v234, v234
	v_max_f32_e32 v235, v235, v235
	v_max_f32_e32 v236, v236, v236
	v_max_f32_e32 v237, v237, v237
	v_max_f32_e32 v238, v238, v238
	v_max_f32_e32 v239, v239, v239
	v_max_f32_e32 v240, v240, v240
	v_max_f32_e32 v241, v241, v241
	v_med3_f32 v226, v226, s62, v95
	v_med3_f32 v227, v227, s62, v95
	v_med3_f32 v228, v228, s62, v95
	v_med3_f32 v229, v229, s62, v95
	v_med3_f32 v230, v230, s62, v95
	v_med3_f32 v231, v231, s62, v95
	v_med3_f32 v232, v232, s62, v95
	v_med3_f32 v233, v233, s62, v95
	v_med3_f32 v234, v234, s62, v95
	v_med3_f32 v235, v235, s62, v95
	v_med3_f32 v236, v236, s62, v95
	v_med3_f32 v237, v237, s62, v95
	v_med3_f32 v238, v238, s62, v95
	v_med3_f32 v239, v239, s62, v95
	v_med3_f32 v240, v240, s62, v95
	v_med3_f32 v241, v241, s62, v95
	v_mov_b32_e32 v242, 0
	v_mov_b32_e32 v243, 0
	v_mov_b32_e32 v244, 0
	v_mov_b32_e32 v245, 0
	v_cvt_pk_fp8_f32 v242, v226, v227
	v_cvt_pk_fp8_f32 v243, v230, v231
	v_cvt_pk_fp8_f32 v244, v234, v235
	v_cvt_pk_fp8_f32 v245, v238, v239
	v_cvt_pk_fp8_f32 v242, v228, v229 op_sel:[0,0,1]
	v_cvt_pk_fp8_f32 v243, v232, v233 op_sel:[0,0,1]
	v_cvt_pk_fp8_f32 v244, v236, v237 op_sel:[0,0,1]
	v_cvt_pk_fp8_f32 v245, v240, v241 op_sel:[0,0,1]
	s_nop 0
	global_store_dwordx4 v92, v[242:245], s[6:7]
	s_waitcnt vmcnt(12)
	v_mul_f32_e32 v144, v50, v144
	v_mul_f32_e32 v145, v50, v145
	v_mul_f32_e32 v146, v50, v146
	v_mul_f32_e32 v147, v50, v147
	ds_write_b128 v209, v[144:147]
	v_mul_f32_e32 v148, v51, v148
	v_mul_f32_e32 v149, v51, v149
	v_mul_f32_e32 v150, v51, v150
	v_mul_f32_e32 v151, v51, v151
	ds_write_b128 v209, v[148:151] offset:1024
	v_mul_f32_e32 v152, v52, v152
	v_mul_f32_e32 v153, v52, v153
	v_mul_f32_e32 v154, v52, v154
	v_mul_f32_e32 v155, v52, v155
	ds_write_b128 v209, v[152:155] offset:2048
	v_mul_f32_e32 v156, v53, v156
	v_mul_f32_e32 v157, v53, v157
	v_mul_f32_e32 v158, v53, v158
	v_mul_f32_e32 v159, v53, v159
	ds_write_b128 v209, v[156:159] offset:3072
	v_mul_f32_e32 v160, v54, v160
	v_mul_f32_e32 v161, v54, v161
	v_mul_f32_e32 v162, v54, v162
	v_mul_f32_e32 v163, v54, v163
	ds_write_b128 v209, v[160:163] offset:4096
	v_mul_f32_e32 v164, v55, v164
	v_mul_f32_e32 v165, v55, v165
	v_mul_f32_e32 v166, v55, v166
	v_mul_f32_e32 v167, v55, v167
	ds_write_b128 v209, v[164:167] offset:5120
	v_mul_f32_e32 v168, v56, v168
	v_mul_f32_e32 v169, v56, v169
	v_mul_f32_e32 v170, v56, v170
	v_mul_f32_e32 v171, v56, v171
	ds_write_b128 v209, v[168:171] offset:6144
	v_mul_f32_e32 v172, v57, v172
	v_mul_f32_e32 v173, v57, v173
	v_mul_f32_e32 v174, v57, v174
	v_mul_f32_e32 v175, v57, v175
	ds_write_b128 v209, v[172:175] offset:7168
	s_waitcnt lgkmcnt(0)
	s_barrier
; #define GAS __attribute__((address_space(1)))
; #define LAS __attribute__((address_space(3)))
; #define LDS_WAIT() asm volatile("s_waitcnt lgkmcnt(0)" ::: "memory")
; __device__ __forceinline__ unsigned pk4_fp8(float a, float b, float c, float d) {
;     a = fminf(fmaxf(a, -448.f), 448.f); b = fminf(fmaxf(b, -448.f), 448.f); c = fminf(fmaxf(c, -448.f), 448.f); d = fminf(fmaxf(d, -448.f), 448.f);
;     int w = __builtin_amdgcn_cvt_pk_fp8_f32(a, b, 0, false); w = __builtin_amdgcn_cvt_pk_fp8_f32(c, d, w, true); return (unsigned)w; }
;     const int pr = item >> 1, kb = 2 * (pr / nblk) + (item & 1), nb = pr % nblk, k0 = 64 * kb, n0 = 32 * nb;
;     const int nr = n0 + (lane & 31); const int sc = MAP == 1 ? src_col_in(nr) : nr;
;     float v[32];
; #pragma unroll
;     for (int i = 0; i < 32; ++i) v[i] = sc >= 0 ? W[(size_t)(k0 + 2 * i + (lane >> 5)) * Nsrc + sc] : 0.f;
; #pragma unroll
;     for (int i = 0; i < 32; ++i) { const int k = k0 + 2 * i + (lane >> 5); float x = v[i] * wscale; if (KS) x *= (k < ksplit ? ksA[k] : ksB[k - ksplit]); scr[(2 * i + (lane >> 5)) * 33 + (lane & 31)] = x; }
;     LDS_WAIT(); asm volatile("" ::: "memory");
;     const int c = lane & 7;
; #pragma unroll
;     for (int j = 0; j < 4; ++j) { const int n = (lane >> 3) + 8 * j; const LAS float* s = scr + (8 * c) * 33 + n;
;         const unsigned long long o = (unsigned long long)pg8::pk4_fp8(s[0 * 33], s[1 * 33], s[2 * 33], s[3 * 33]) | ((unsigned long long)pg8::pk4_fp8(s[4 * 33], s[5 * 33], s[6 * 33], s[7 * 33]) << 32);
;         *(GAS unsigned long long*)(WT + (size_t)(n0 + n) * K + k0 + 8 * c) = o; }
;     LDS_WAIT(); asm volatile("" ::: "memory");
; }
	s_add_i32 s24, s23, 72
	s_lshl_b32 s20, s24, 7
	s_cmp_lt_u32 s24, 40
	s_cselect_b32 s21, 0, 0x830
	s_cmp_lt_u32 s24, 72
	s_cselect_b32 s21, s21, 0xfffff030
	s_add_i32 s20, s20, s21
	s_lshl_b32 s20, s20, 2
	s_add_u32 s8, s50, s20
	s_addc_u32 s9, s51, 0
	global_load_dwordx4 v[144:147], v76, s[8:9]
	s_add_u32 s8, s8, 0x16280
	s_addc_u32 s9, s9, 0
	global_load_dwordx4 v[148:151], v76, s[8:9]
	s_add_u32 s8, s8, 0x16280
	s_addc_u32 s9, s9, 0
	global_load_dwordx4 v[152:155], v76, s[8:9]
	s_add_u32 s8, s8, 0x16280
	s_addc_u32 s9, s9, 0
	global_load_dwordx4 v[156:159], v76, s[8:9]
	s_add_u32 s8, s8, 0x16280
	s_addc_u32 s9, s9, 0
	global_load_dwordx4 v[160:163], v76, s[8:9]
	s_add_u32 s8, s8, 0x16280
	s_addc_u32 s9, s9, 0
	global_load_dwordx4 v[164:167], v76, s[8:9]
	s_add_u32 s8, s8, 0x16280
	s_addc_u32 s9, s9, 0
	global_load_dwordx4 v[168:171], v76, s[8:9]
	s_add_u32 s8, s8, 0x16280
	s_addc_u32 s9, s9, 0
	global_load_dwordx4 v[172:175], v76, s[8:9]
	s_add_i32 s24, s23, 56
	s_mul_i32 s20, s24, 0x80000
	s_add_u32 s6, s52, s20
	s_addc_u32 s7, s53, 0
	s_cmp_lt_u32 s24, 16
	s_cselect_b32 s20, 1, 0
	s_sub_i32 s21, s24, 16
	s_bitcmp0_b32 s21, 2
	s_cselect_b32 s21, 1, 0
	s_cmp_lt_u32 s24, 40
	s_cselect_b32 s21, s21, 0
	s_or_b32 s20, s20, s21
	s_cmp_lg_u32 s20, 0
	s_cselect_b64 s[20:21], -1, 0
	v_cndmask_b32_e64 v91, v77, v81, s[20:21]
	v_cndmask_b32_e64 v92, v78, v82, s[20:21]
	ds_read_b32 v226, v211
	ds_read_b32 v227, v211 offset:512
	ds_read_b32 v228, v211 offset:1024
	ds_read_b32 v229, v211 offset:1536
	ds_read_b32 v230, v211 offset:2048
	ds_read_b32 v231, v211 offset:2560
	ds_read_b32 v232, v211 offset:3072
	ds_read_b32 v233, v211 offset:3584
	ds_read_b32 v234, v211 offset:4096
	ds_read_b32 v235, v211 offset:4608
	ds_read_b32 v236, v211 offset:5120
	ds_read_b32 v237, v211 offset:5632
	ds_read_b32 v238, v211 offset:6144
	ds_read_b32 v239, v211 offset:6656
	ds_read_b32 v240, v211 offset:7168
	ds_read_b32 v241, v211 offset:7680
	s_waitcnt lgkmcnt(0)
	v_max_f32_e32 v226, v226, v226
	v_max_f32_e32 v227, v227, v227
	v_max_f32_e32 v228, v228, v228
	v_max_f32_e32 v229, v229, v229
	v_max_f32_e32 v230, v230, v230
	v_max_f32_e32 v231, v231, v231
	v_max_f32_e32 v232, v232, v232
	v_max_f32_e32 v233, v233, v233
	v_max_f32_e32 v234, v234, v234
	v_max_f32_e32 v235, v235, v235
	v_max_f32_e32 v236, v236, v236
	v_max_f32_e32 v237, v237, v237
	v_max_f32_e32 v238, v238, v238
	v_max_f32_e32 v239, v239, v239
	v_max_f32_e32 v240, v240, v240
	v_max_f32_e32 v241, v241, v241
	v_med3_f32 v226, v226, s62, v95
	v_med3_f32 v227, v227, s62, v95
	v_med3_f32 v228, v228, s62, v95
	v_med3_f32 v229, v229, s62, v95
	v_med3_f32 v230, v230, s62, v95
	v_med3_f32 v231, v231, s62, v95
	v_med3_f32 v232, v232, s62, v95
	v_med3_f32 v233, v233, s62, v95
	v_med3_f32 v234, v234, s62, v95
	v_med3_f32 v235, v235, s62, v95
	v_med3_f32 v236, v236, s62, v95
	v_med3_f32 v237, v237, s62, v95
	v_med3_f32 v238, v238, s62, v95
	v_med3_f32 v239, v239, s62, v95
	v_med3_f32 v240, v240, s62, v95
	v_med3_f32 v241, v241, s62, v95
	v_mov_b32_e32 v242, 0
	v_mov_b32_e32 v243, 0
	v_mov_b32_e32 v244, 0
	v_mov_b32_e32 v245, 0
	v_cvt_pk_fp8_f32 v242, v226, v227
	v_cvt_pk_fp8_f32 v243, v230, v231
	v_cvt_pk_fp8_f32 v244, v234, v235
	v_cvt_pk_fp8_f32 v245, v238, v239
	v_cvt_pk_fp8_f32 v242, v228, v229 op_sel:[0,0,1]
	v_cvt_pk_fp8_f32 v243, v232, v233 op_sel:[0,0,1]
	v_cvt_pk_fp8_f32 v244, v236, v237 op_sel:[0,0,1]
	v_cvt_pk_fp8_f32 v245, v240, v241 op_sel:[0,0,1]
	s_nop 0
	global_store_dwordx4 v91, v[242:245], s[6:7]
	ds_read_b32 v226, v213
	ds_read_b32 v227, v213 offset:512
	ds_read_b32 v228, v213 offset:1024
	ds_read_b32 v229, v213 offset:1536
	ds_read_b32 v230, v213 offset:2048
	ds_read_b32 v231, v213 offset:2560
	ds_read_b32 v232, v213 offset:3072
	ds_read_b32 v233, v213 offset:3584
	ds_read_b32 v234, v213 offset:4096
	ds_read_b32 v235, v213 offset:4608
	ds_read_b32 v236, v213 offset:5120
	ds_read_b32 v237, v213 offset:5632
	ds_read_b32 v238, v213 offset:6144
	ds_read_b32 v239, v213 offset:6656
	ds_read_b32 v240, v213 offset:7168
	ds_read_b32 v241, v213 offset:7680
	s_waitcnt lgkmcnt(0)
	v_max_f32_e32 v226, v226, v226
	v_max_f32_e32 v227, v227, v227
	v_max_f32_e32 v228, v228, v228
	v_max_f32_e32 v229, v229, v229
	v_max_f32_e32 v230, v230, v230
	v_max_f32_e32 v231, v231, v231
	v_max_f32_e32 v232, v232, v232
	v_max_f32_e32 v233, v233, v233
	v_max_f32_e32 v234, v234, v234
	v_max_f32_e32 v235, v235, v235
	v_max_f32_e32 v236, v236, v236
	v_max_f32_e32 v237, v237, v237
	v_max_f32_e32 v238, v238, v238
	v_max_f32_e32 v239, v239, v239
	v_max_f32_e32 v240, v240, v240
	v_max_f32_e32 v241, v241, v241
	v_med3_f32 v226, v226, s62, v95
	v_med3_f32 v227, v227, s62, v95
	v_med3_f32 v228, v228, s62, v95
	v_med3_f32 v229, v229, s62, v95
	v_med3_f32 v230, v230, s62, v95
	v_med3_f32 v231, v231, s62, v95
	v_med3_f32 v232, v232, s62, v95
	v_med3_f32 v233, v233, s62, v95
	v_med3_f32 v234, v234, s62, v95
	v_med3_f32 v235, v235, s62, v95
	v_med3_f32 v236, v236, s62, v95
	v_med3_f32 v237, v237, s62, v95
	v_med3_f32 v238, v238, s62, v95
	v_med3_f32 v239, v239, s62, v95
	v_med3_f32 v240, v240, s62, v95
	v_med3_f32 v241, v241, s62, v95
	v_mov_b32_e32 v242, 0
	v_mov_b32_e32 v243, 0
	v_mov_b32_e32 v244, 0
	v_mov_b32_e32 v245, 0
	v_cvt_pk_fp8_f32 v242, v226, v227
	v_cvt_pk_fp8_f32 v243, v230, v231
	v_cvt_pk_fp8_f32 v244, v234, v235
	v_cvt_pk_fp8_f32 v245, v238, v239
	v_cvt_pk_fp8_f32 v242, v228, v229 op_sel:[0,0,1]
	v_cvt_pk_fp8_f32 v243, v232, v233 op_sel:[0,0,1]
	v_cvt_pk_fp8_f32 v244, v236, v237 op_sel:[0,0,1]
	v_cvt_pk_fp8_f32 v245, v240, v241 op_sel:[0,0,1]
	s_nop 0
	global_store_dwordx4 v92, v[242:245], s[6:7]
	s_waitcnt vmcnt(12)
	v_mul_f32_e32 v176, v50, v176
	v_mul_f32_e32 v177, v50, v177
	v_mul_f32_e32 v178, v50, v178
	v_mul_f32_e32 v179, v50, v179
	ds_write_b128 v210, v[176:179]
	v_mul_f32_e32 v180, v51, v180
	v_mul_f32_e32 v181, v51, v181
	v_mul_f32_e32 v182, v51, v182
	v_mul_f32_e32 v183, v51, v183
	ds_write_b128 v210, v[180:183] offset:1024
	v_mul_f32_e32 v184, v52, v184
	v_mul_f32_e32 v185, v52, v185
	v_mul_f32_e32 v186, v52, v186
	v_mul_f32_e32 v187, v52, v187
	ds_write_b128 v210, v[184:187] offset:2048
	v_mul_f32_e32 v188, v53, v188
	v_mul_f32_e32 v189, v53, v189
	v_mul_f32_e32 v190, v53, v190
	v_mul_f32_e32 v191, v53, v191
	ds_write_b128 v210, v[188:191] offset:3072
	v_mul_f32_e32 v192, v54, v192
	v_mul_f32_e32 v193, v54, v193
	v_mul_f32_e32 v194, v54, v194
	v_mul_f32_e32 v195, v54, v195
	ds_write_b128 v210, v[192:195] offset:4096
	v_mul_f32_e32 v196, v55, v196
	v_mul_f32_e32 v197, v55, v197
	v_mul_f32_e32 v198, v55, v198
	v_mul_f32_e32 v199, v55, v199
	ds_write_b128 v210, v[196:199] offset:5120
	v_mul_f32_e32 v200, v56, v200
	v_mul_f32_e32 v201, v56, v201
	v_mul_f32_e32 v202, v56, v202
	v_mul_f32_e32 v203, v56, v203
	ds_write_b128 v210, v[200:203] offset:6144
	v_mul_f32_e32 v204, v57, v204
	v_mul_f32_e32 v205, v57, v205
	v_mul_f32_e32 v206, v57, v206
	v_mul_f32_e32 v207, v57, v207
	ds_write_b128 v210, v[204:207] offset:7168
	s_waitcnt lgkmcnt(0)
	s_barrier
; #define GAS __attribute__((address_space(1)))
; #define LAS __attribute__((address_space(3)))
; #define LDS_WAIT() asm volatile("s_waitcnt lgkmcnt(0)" ::: "memory")
; __device__ __forceinline__ unsigned pk4_fp8(float a, float b, float c, float d) {
;     a = fminf(fmaxf(a, -448.f), 448.f); b = fminf(fmaxf(b, -448.f), 448.f); c = fminf(fmaxf(c, -448.f), 448.f); d = fminf(fmaxf(d, -448.f), 448.f);
;     int w = __builtin_amdgcn_cvt_pk_fp8_f32(a, b, 0, false); w = __builtin_amdgcn_cvt_pk_fp8_f32(c, d, w, true); return (unsigned)w; }
;     const int pr = item >> 1, kb = 2 * (pr / nblk) + (item & 1), nb = pr % nblk, k0 = 64 * kb, n0 = 32 * nb;
;     const int nr = n0 + (lane & 31); const int sc = MAP == 1 ? src_col_in(nr) : nr;
;     float v[32];
; #pragma unroll
;     for (int i = 0; i < 32; ++i) v[i] = sc >= 0 ? W[(size_t)(k0 + 2 * i + (lane >> 5)) * Nsrc + sc] : 0.f;
; #pragma unroll
;     for (int i = 0; i < 32; ++i) { const int k = k0 + 2 * i + (lane >> 5); float x = v[i] * wscale; if (KS) x *= (k < ksplit ? ksA[k] : ksB[k - ksplit]); scr[(2 * i + (lane >> 5)) * 33 + (lane & 31)] = x; }
;     LDS_WAIT(); asm volatile("" ::: "memory");
;     const int c = lane & 7;
; #pragma unroll
;     for (int j = 0; j < 4; ++j) { const int n = (lane >> 3) + 8 * j; const LAS float* s = scr + (8 * c) * 33 + n;
;         const unsigned long long o = (unsigned long long)pg8::pk4_fp8(s[0 * 33], s[1 * 33], s[2 * 33], s[3 * 33]) | ((unsigned long long)pg8::pk4_fp8(s[4 * 33], s[5 * 33], s[6 * 33], s[7 * 33]) << 32);
;         *(GAS unsigned long long*)(WT + (size_t)(n0 + n) * K + k0 + 8 * c) = o; }
;     LDS_WAIT(); asm volatile("" ::: "memory");
; }
	s_add_i32 s24, s23, 80
	s_lshl_b32 s20, s24, 7
	s_cmp_lt_u32 s24, 40
	s_cselect_b32 s21, 0, 0x830
	s_cmp_lt_u32 s24, 72
	s_cselect_b32 s21, s21, 0xfffff030
	s_add_i32 s20, s20, s21
	s_lshl_b32 s20, s20, 2
	s_add_u32 s8, s50, s20
	s_addc_u32 s9, s51, 0
	global_load_dwordx4 v[176:179], v76, s[8:9]
	s_add_u32 s8, s8, 0x16280
	s_addc_u32 s9, s9, 0
	global_load_dwordx4 v[180:183], v76, s[8:9]
	s_add_u32 s8, s8, 0x16280
	s_addc_u32 s9, s9, 0
	global_load_dwordx4 v[184:187], v76, s[8:9]
	s_add_u32 s8, s8, 0x16280
	s_addc_u32 s9, s9, 0
	global_load_dwordx4 v[188:191], v76, s[8:9]
	s_add_u32 s8, s8, 0x16280
	s_addc_u32 s9, s9, 0
	global_load_dwordx4 v[192:195], v76, s[8:9]
	s_add_u32 s8, s8, 0x16280
	s_addc_u32 s9, s9, 0
	global_load_dwordx4 v[196:199], v76, s[8:9]
	s_add_u32 s8, s8, 0x16280
	s_addc_u32 s9, s9, 0
	global_load_dwordx4 v[200:203], v76, s[8:9]
	s_add_u32 s8, s8, 0x16280
	s_addc_u32 s9, s9, 0
	global_load_dwordx4 v[204:207], v76, s[8:9]
	s_add_i32 s24, s23, 64
	s_mul_i32 s20, s24, 0x80000
	s_add_u32 s6, s52, s20
	s_addc_u32 s7, s53, 0
	s_cmp_lt_u32 s24, 16
	s_cselect_b32 s20, 1, 0
	s_sub_i32 s21, s24, 16
	s_bitcmp0_b32 s21, 2
	s_cselect_b32 s21, 1, 0
	s_cmp_lt_u32 s24, 40
	s_cselect_b32 s21, s21, 0
	s_or_b32 s20, s20, s21
	s_cmp_lg_u32 s20, 0
	s_cselect_b64 s[20:21], -1, 0
	v_cndmask_b32_e64 v91, v77, v81, s[20:21]
	v_cndmask_b32_e64 v92, v78, v82, s[20:21]
	ds_read_b32 v226, v212
	ds_read_b32 v227, v212 offset:512
	ds_read_b32 v228, v212 offset:1024
	ds_read_b32 v229, v212 offset:1536
	ds_read_b32 v230, v212 offset:2048
	ds_read_b32 v231, v212 offset:2560
	ds_read_b32 v232, v212 offset:3072
	ds_read_b32 v233, v212 offset:3584
	ds_read_b32 v234, v212 offset:4096
	ds_read_b32 v235, v212 offset:4608
	ds_read_b32 v236, v212 offset:5120
	ds_read_b32 v237, v212 offset:5632
	ds_read_b32 v238, v212 offset:6144
	ds_read_b32 v239, v212 offset:6656
	ds_read_b32 v240, v212 offset:7168
	ds_read_b32 v241, v212 offset:7680
	s_waitcnt lgkmcnt(0)
	v_max_f32_e32 v226, v226, v226
	v_max_f32_e32 v227, v227, v227
	v_max_f32_e32 v228, v228, v228
	v_max_f32_e32 v229, v229, v229
	v_max_f32_e32 v230, v230, v230
	v_max_f32_e32 v231, v231, v231
	v_max_f32_e32 v232, v232, v232
	v_max_f32_e32 v233, v233, v233
	v_max_f32_e32 v234, v234, v234
	v_max_f32_e32 v235, v235, v235
	v_max_f32_e32 v236, v236, v236
	v_max_f32_e32 v237, v237, v237
	v_max_f32_e32 v238, v238, v238
	v_max_f32_e32 v239, v239, v239
	v_max_f32_e32 v240, v240, v240
	v_max_f32_e32 v241, v241, v241
	v_med3_f32 v226, v226, s62, v95
	v_med3_f32 v227, v227, s62, v95
	v_med3_f32 v228, v228, s62, v95
	v_med3_f32 v229, v229, s62, v95
	v_med3_f32 v230, v230, s62, v95
	v_med3_f32 v231, v231, s62, v95
	v_med3_f32 v232, v232, s62, v95
	v_med3_f32 v233, v233, s62, v95
	v_med3_f32 v234, v234, s62, v95
	v_med3_f32 v235, v235, s62, v95
	v_med3_f32 v236, v236, s62, v95
	v_med3_f32 v237, v237, s62, v95
	v_med3_f32 v238, v238, s62, v95
	v_med3_f32 v239, v239, s62, v95
	v_med3_f32 v240, v240, s62, v95
	v_med3_f32 v241, v241, s62, v95
	v_mov_b32_e32 v242, 0
	v_mov_b32_e32 v243, 0
	v_mov_b32_e32 v244, 0
	v_mov_b32_e32 v245, 0
	v_cvt_pk_fp8_f32 v242, v226, v227
	v_cvt_pk_fp8_f32 v243, v230, v231
	v_cvt_pk_fp8_f32 v244, v234, v235
	v_cvt_pk_fp8_f32 v245, v238, v239
	v_cvt_pk_fp8_f32 v242, v228, v229 op_sel:[0,0,1]
	v_cvt_pk_fp8_f32 v243, v232, v233 op_sel:[0,0,1]
	v_cvt_pk_fp8_f32 v244, v236, v237 op_sel:[0,0,1]
	v_cvt_pk_fp8_f32 v245, v240, v241 op_sel:[0,0,1]
	s_nop 0
	global_store_dwordx4 v91, v[242:245], s[6:7]
	ds_read_b32 v226, v214
	ds_read_b32 v227, v214 offset:512
	ds_read_b32 v228, v214 offset:1024
	ds_read_b32 v229, v214 offset:1536
	ds_read_b32 v230, v214 offset:2048
	ds_read_b32 v231, v214 offset:2560
	ds_read_b32 v232, v214 offset:3072
	ds_read_b32 v233, v214 offset:3584
	ds_read_b32 v234, v214 offset:4096
	ds_read_b32 v235, v214 offset:4608
	ds_read_b32 v236, v214 offset:5120
	ds_read_b32 v237, v214 offset:5632
	ds_read_b32 v238, v214 offset:6144
	ds_read_b32 v239, v214 offset:6656
	ds_read_b32 v240, v214 offset:7168
	ds_read_b32 v241, v214 offset:7680
	s_waitcnt lgkmcnt(0)
	v_max_f32_e32 v226, v226, v226
	v_max_f32_e32 v227, v227, v227
	v_max_f32_e32 v228, v228, v228
	v_max_f32_e32 v229, v229, v229
	v_max_f32_e32 v230, v230, v230
	v_max_f32_e32 v231, v231, v231
	v_max_f32_e32 v232, v232, v232
	v_max_f32_e32 v233, v233, v233
	v_max_f32_e32 v234, v234, v234
	v_max_f32_e32 v235, v235, v235
	v_max_f32_e32 v236, v236, v236
	v_max_f32_e32 v237, v237, v237
	v_max_f32_e32 v238, v238, v238
	v_max_f32_e32 v239, v239, v239
	v_max_f32_e32 v240, v240, v240
	v_max_f32_e32 v241, v241, v241
	v_med3_f32 v226, v226, s62, v95
	v_med3_f32 v227, v227, s62, v95
	v_med3_f32 v228, v228, s62, v95
	v_med3_f32 v229, v229, s62, v95
	v_med3_f32 v230, v230, s62, v95
	v_med3_f32 v231, v231, s62, v95
	v_med3_f32 v232, v232, s62, v95
	v_med3_f32 v233, v233, s62, v95
	v_med3_f32 v234, v234, s62, v95
	v_med3_f32 v235, v235, s62, v95
	v_med3_f32 v236, v236, s62, v95
	v_med3_f32 v237, v237, s62, v95
	v_med3_f32 v238, v238, s62, v95
	v_med3_f32 v239, v239, s62, v95
	v_med3_f32 v240, v240, s62, v95
	v_med3_f32 v241, v241, s62, v95
	v_mov_b32_e32 v242, 0
	v_mov_b32_e32 v243, 0
	v_mov_b32_e32 v244, 0
	v_mov_b32_e32 v245, 0
	v_cvt_pk_fp8_f32 v242, v226, v227
	v_cvt_pk_fp8_f32 v243, v230, v231
	v_cvt_pk_fp8_f32 v244, v234, v235
	v_cvt_pk_fp8_f32 v245, v238, v239
	v_cvt_pk_fp8_f32 v242, v228, v229 op_sel:[0,0,1]
	v_cvt_pk_fp8_f32 v243, v232, v233 op_sel:[0,0,1]
	v_cvt_pk_fp8_f32 v244, v236, v237 op_sel:[0,0,1]
	v_cvt_pk_fp8_f32 v245, v240, v241 op_sel:[0,0,1]
	s_nop 0
	global_store_dwordx4 v92, v[242:245], s[6:7]
	s_waitcnt vmcnt(12)
	v_mul_f32_e32 v144, v50, v144
	v_mul_f32_e32 v145, v50, v145
	v_mul_f32_e32 v146, v50, v146
	v_mul_f32_e32 v147, v50, v147
	ds_write_b128 v209, v[144:147]
	v_mul_f32_e32 v148, v51, v148
	v_mul_f32_e32 v149, v51, v149
	v_mul_f32_e32 v150, v51, v150
	v_mul_f32_e32 v151, v51, v151
	ds_write_b128 v209, v[148:151] offset:1024
	v_mul_f32_e32 v152, v52, v152
	v_mul_f32_e32 v153, v52, v153
	v_mul_f32_e32 v154, v52, v154
	v_mul_f32_e32 v155, v52, v155
	ds_write_b128 v209, v[152:155] offset:2048
	v_mul_f32_e32 v156, v53, v156
	v_mul_f32_e32 v157, v53, v157
	v_mul_f32_e32 v158, v53, v158
	v_mul_f32_e32 v159, v53, v159
	ds_write_b128 v209, v[156:159] offset:3072
	v_mul_f32_e32 v160, v54, v160
	v_mul_f32_e32 v161, v54, v161
	v_mul_f32_e32 v162, v54, v162
	v_mul_f32_e32 v163, v54, v163
	ds_write_b128 v209, v[160:163] offset:4096
	v_mul_f32_e32 v164, v55, v164
	v_mul_f32_e32 v165, v55, v165
	v_mul_f32_e32 v166, v55, v166
	v_mul_f32_e32 v167, v55, v167
	ds_write_b128 v209, v[164:167] offset:5120
	v_mul_f32_e32 v168, v56, v168
	v_mul_f32_e32 v169, v56, v169
	v_mul_f32_e32 v170, v56, v170
	v_mul_f32_e32 v171, v56, v171
	ds_write_b128 v209, v[168:171] offset:6144
	v_mul_f32_e32 v172, v57, v172
	v_mul_f32_e32 v173, v57, v173
	v_mul_f32_e32 v174, v57, v174
	v_mul_f32_e32 v175, v57, v175
	ds_write_b128 v209, v[172:175] offset:7168
	s_waitcnt lgkmcnt(0)
	s_barrier
; #define GAS __attribute__((address_space(1)))
; #define LAS __attribute__((address_space(3)))
; #define LDS_WAIT() asm volatile("s_waitcnt lgkmcnt(0)" ::: "memory")
; __device__ __forceinline__ int nat_dim(int p) { return (p >> 1) + 64 * (p & 1); }
; template <int MAP, bool KS, bool KPERM = false>
; __device__ __forceinline__ void p0_transpose_item(const float* W, int K, int Nsrc, int nblk, bf16* WT, const float* ksA, const float* ksB, int ksplit, LAS float* scr, int item, int lane) {
;     const int kb = item / nblk, nb = item % nblk, k0 = 64 * kb, n0 = 32 * nb;
;     const int nr = n0 + (lane & 31); const int sc = MAP == 1 ? src_col_in(nr) : (MAP == 2 ? nat_dim(nr) : nr);
;     float v[32];
; #pragma unroll
;     for (int i = 0; i < 32; ++i) { const int k = k0 + 2 * i + (lane >> 5); const int ksrc = KPERM ? ((k & ~127) + nat_dim(k & 127)) : k;
;         v[i] = sc >= 0 ? W[(size_t)ksrc * Nsrc + sc] : 0.f; }
; #pragma unroll
;     for (int i = 0; i < 32; ++i) { const int kk = 2 * i + (lane >> 5); const int k = k0 + kk;
;         if (KS) v[i] *= (k < ksplit ? ksA[k] : ksB[k - ksplit]);
;         scr[kk * 33 + (lane & 31)] = v[i]; }
;     LDS_WAIT(); asm volatile("" ::: "memory");
;     const int pr = item >> 1, kb = 2 * (pr / nblk) + (item & 1), nb = pr % nblk, k0 = 64 * kb, n0 = 32 * nb;
;     const int nr = n0 + (lane & 31); const int sc = MAP == 1 ? src_col_in(nr) : nr;
;     float v[32];
; #pragma unroll
;     for (int i = 0; i < 32; ++i) v[i] = sc >= 0 ? W[(size_t)(k0 + 2 * i + (lane >> 5)) * Nsrc + sc] : 0.f;
; #pragma unroll
;     for (int i = 0; i < 32; ++i) { const int k = k0 + 2 * i + (lane >> 5); float x = v[i] * wscale; if (KS) x *= (k < ksplit ? ksA[k] : ksB[k - ksplit]); scr[(2 * i + (lane >> 5)) * 33 + (lane & 31)] = x; }
;     LDS_WAIT(); asm volatile("" ::: "memory");
;     const int c = lane & 7;
; #pragma unroll
;     for (int j = 0; j < 4; ++j) { const int n = (lane >> 3) + 8 * j; const LAS float* s = scr + (8 * c) * 33 + n;
;         const unsigned long long o = (unsigned long long)pg8::pk4_fp8(s[0 * 33], s[1 * 33], s[2 * 33], s[3 * 33]) | ((unsigned long long)pg8::pk4_fp8(s[4 * 33], s[5 * 33], s[6 * 33], s[7 * 33]) << 32);
;         *(GAS unsigned long long*)(WT + (size_t)(n0 + n) * K + k0 + 8 * c) = o; }
;     LDS_WAIT(); asm volatile("" ::: "memory");
; }
	s_mov_b64 s[8:9], s[54:55]
	global_load_dwordx4 v[144:147], v75, s[8:9]
	s_add_u32 s8, s8, 0x8000
	s_addc_u32 s9, s9, 0
	global_load_dwordx4 v[148:151], v75, s[8:9]
	s_add_u32 s8, s8, 0x8000
	s_addc_u32 s9, s9, 0
	global_load_dwordx4 v[152:155], v75, s[8:9]
	s_add_u32 s8, s8, 0x8000
	s_addc_u32 s9, s9, 0
	global_load_dwordx4 v[156:159], v75, s[8:9]
	s_add_u32 s8, s8, 0x8000
	s_addc_u32 s9, s9, 0
	global_load_dwordx4 v[160:163], v75, s[8:9]
	s_add_u32 s8, s8, 0x8000
	s_addc_u32 s9, s9, 0
	global_load_dwordx4 v[164:167], v75, s[8:9]
	s_add_u32 s8, s8, 0x8000
	s_addc_u32 s9, s9, 0
	global_load_dwordx4 v[168:171], v75, s[8:9]
	s_add_u32 s8, s8, 0x8000
	s_addc_u32 s9, s9, 0
	global_load_dwordx4 v[172:175], v75, s[8:9]
	s_add_i32 s24, s23, 72
	s_mul_i32 s20, s24, 0x80000
	s_add_u32 s6, s52, s20
	s_addc_u32 s7, s53, 0
	s_cmp_lt_u32 s24, 16
	s_cselect_b32 s20, 1, 0
	s_sub_i32 s21, s24, 16
	s_bitcmp0_b32 s21, 2
	s_cselect_b32 s21, 1, 0
	s_cmp_lt_u32 s24, 40
	s_cselect_b32 s21, s21, 0
	s_or_b32 s20, s20, s21
	s_cmp_lg_u32 s20, 0
	s_cselect_b64 s[20:21], -1, 0
	v_cndmask_b32_e64 v91, v77, v81, s[20:21]
	v_cndmask_b32_e64 v92, v78, v82, s[20:21]
	ds_read_b32 v226, v211
	ds_read_b32 v227, v211 offset:512
	ds_read_b32 v228, v211 offset:1024
	ds_read_b32 v229, v211 offset:1536
	ds_read_b32 v230, v211 offset:2048
	ds_read_b32 v231, v211 offset:2560
	ds_read_b32 v232, v211 offset:3072
	ds_read_b32 v233, v211 offset:3584
	ds_read_b32 v234, v211 offset:4096
	ds_read_b32 v235, v211 offset:4608
	ds_read_b32 v236, v211 offset:5120
	ds_read_b32 v237, v211 offset:5632
	ds_read_b32 v238, v211 offset:6144
	ds_read_b32 v239, v211 offset:6656
	ds_read_b32 v240, v211 offset:7168
	ds_read_b32 v241, v211 offset:7680
	s_waitcnt lgkmcnt(0)
	v_max_f32_e32 v226, v226, v226
	v_max_f32_e32 v227, v227, v227
	v_max_f32_e32 v228, v228, v228
	v_max_f32_e32 v229, v229, v229
	v_max_f32_e32 v230, v230, v230
	v_max_f32_e32 v231, v231, v231
	v_max_f32_e32 v232, v232, v232
	v_max_f32_e32 v233, v233, v233
	v_max_f32_e32 v234, v234, v234
	v_max_f32_e32 v235, v235, v235
	v_max_f32_e32 v236, v236, v236
	v_max_f32_e32 v237, v237, v237
	v_max_f32_e32 v238, v238, v238
	v_max_f32_e32 v239, v239, v239
	v_max_f32_e32 v240, v240, v240
	v_max_f32_e32 v241, v241, v241
	v_med3_f32 v226, v226, s62, v95
	v_med3_f32 v227, v227, s62, v95
	v_med3_f32 v228, v228, s62, v95
	v_med3_f32 v229, v229, s62, v95
	v_med3_f32 v230, v230, s62, v95
	v_med3_f32 v231, v231, s62, v95
	v_med3_f32 v232, v232, s62, v95
	v_med3_f32 v233, v233, s62, v95
	v_med3_f32 v234, v234, s62, v95
	v_med3_f32 v235, v235, s62, v95
	v_med3_f32 v236, v236, s62, v95
	v_med3_f32 v237, v237, s62, v95
	v_med3_f32 v238, v238, s62, v95
	v_med3_f32 v239, v239, s62, v95
	v_med3_f32 v240, v240, s62, v95
	v_med3_f32 v241, v241, s62, v95
	v_mov_b32_e32 v242, 0
	v_mov_b32_e32 v243, 0
	v_mov_b32_e32 v244, 0
	v_mov_b32_e32 v245, 0
	v_cvt_pk_fp8_f32 v242, v226, v227
	v_cvt_pk_fp8_f32 v243, v230, v231
	v_cvt_pk_fp8_f32 v244, v234, v235
	v_cvt_pk_fp8_f32 v245, v238, v239
	v_cvt_pk_fp8_f32 v242, v228, v229 op_sel:[0,0,1]
	v_cvt_pk_fp8_f32 v243, v232, v233 op_sel:[0,0,1]
	v_cvt_pk_fp8_f32 v244, v236, v237 op_sel:[0,0,1]
	v_cvt_pk_fp8_f32 v245, v240, v241 op_sel:[0,0,1]
	s_nop 0
	global_store_dwordx4 v91, v[242:245], s[6:7]
	ds_read_b32 v226, v213
	ds_read_b32 v227, v213 offset:512
	ds_read_b32 v228, v213 offset:1024
	ds_read_b32 v229, v213 offset:1536
	ds_read_b32 v230, v213 offset:2048
	ds_read_b32 v231, v213 offset:2560
	ds_read_b32 v232, v213 offset:3072
	ds_read_b32 v233, v213 offset:3584
	ds_read_b32 v234, v213 offset:4096
	ds_read_b32 v235, v213 offset:4608
	ds_read_b32 v236, v213 offset:5120
	ds_read_b32 v237, v213 offset:5632
	ds_read_b32 v238, v213 offset:6144
	ds_read_b32 v239, v213 offset:6656
	ds_read_b32 v240, v213 offset:7168
	ds_read_b32 v241, v213 offset:7680
	s_waitcnt lgkmcnt(0)
	v_max_f32_e32 v226, v226, v226
	v_max_f32_e32 v227, v227, v227
	v_max_f32_e32 v228, v228, v228
	v_max_f32_e32 v229, v229, v229
	v_max_f32_e32 v230, v230, v230
	v_max_f32_e32 v231, v231, v231
	v_max_f32_e32 v232, v232, v232
	v_max_f32_e32 v233, v233, v233
	v_max_f32_e32 v234, v234, v234
	v_max_f32_e32 v235, v235, v235
	v_max_f32_e32 v236, v236, v236
	v_max_f32_e32 v237, v237, v237
	v_max_f32_e32 v238, v238, v238
	v_max_f32_e32 v239, v239, v239
	v_max_f32_e32 v240, v240, v240
	v_max_f32_e32 v241, v241, v241
	v_med3_f32 v226, v226, s62, v95
	v_med3_f32 v227, v227, s62, v95
	v_med3_f32 v228, v228, s62, v95
	v_med3_f32 v229, v229, s62, v95
	v_med3_f32 v230, v230, s62, v95
	v_med3_f32 v231, v231, s62, v95
	v_med3_f32 v232, v232, s62, v95
	v_med3_f32 v233, v233, s62, v95
	v_med3_f32 v234, v234, s62, v95
	v_med3_f32 v235, v235, s62, v95
	v_med3_f32 v236, v236, s62, v95
	v_med3_f32 v237, v237, s62, v95
	v_med3_f32 v238, v238, s62, v95
	v_med3_f32 v239, v239, s62, v95
	v_med3_f32 v240, v240, s62, v95
	v_med3_f32 v241, v241, s62, v95
	v_mov_b32_e32 v242, 0
	v_mov_b32_e32 v243, 0
	v_mov_b32_e32 v244, 0
	v_mov_b32_e32 v245, 0
	v_cvt_pk_fp8_f32 v242, v226, v227
	v_cvt_pk_fp8_f32 v243, v230, v231
	v_cvt_pk_fp8_f32 v244, v234, v235
	v_cvt_pk_fp8_f32 v245, v238, v239
	v_cvt_pk_fp8_f32 v242, v228, v229 op_sel:[0,0,1]
	v_cvt_pk_fp8_f32 v243, v232, v233 op_sel:[0,0,1]
	v_cvt_pk_fp8_f32 v244, v236, v237 op_sel:[0,0,1]
	v_cvt_pk_fp8_f32 v245, v240, v241 op_sel:[0,0,1]
	s_nop 0
	global_store_dwordx4 v92, v[242:245], s[6:7]
	s_waitcnt vmcnt(12)
	v_mul_f32_e32 v176, v50, v176
	v_mul_f32_e32 v177, v50, v177
	v_mul_f32_e32 v178, v50, v178
	v_mul_f32_e32 v179, v50, v179
	ds_write_b128 v210, v[176:179]
	v_mul_f32_e32 v180, v51, v180
	v_mul_f32_e32 v181, v51, v181
	v_mul_f32_e32 v182, v51, v182
	v_mul_f32_e32 v183, v51, v183
	ds_write_b128 v210, v[180:183] offset:1024
	v_mul_f32_e32 v184, v52, v184
	v_mul_f32_e32 v185, v52, v185
	v_mul_f32_e32 v186, v52, v186
	v_mul_f32_e32 v187, v52, v187
	ds_write_b128 v210, v[184:187] offset:2048
	v_mul_f32_e32 v188, v53, v188
	v_mul_f32_e32 v189, v53, v189
	v_mul_f32_e32 v190, v53, v190
	v_mul_f32_e32 v191, v53, v191
	ds_write_b128 v210, v[188:191] offset:3072
	v_mul_f32_e32 v192, v54, v192
	v_mul_f32_e32 v193, v54, v193
	v_mul_f32_e32 v194, v54, v194
	v_mul_f32_e32 v195, v54, v195
	ds_write_b128 v210, v[192:195] offset:4096
	v_mul_f32_e32 v196, v55, v196
	v_mul_f32_e32 v197, v55, v197
	v_mul_f32_e32 v198, v55, v198
	v_mul_f32_e32 v199, v55, v199
	ds_write_b128 v210, v[196:199] offset:5120
	v_mul_f32_e32 v200, v56, v200
	v_mul_f32_e32 v201, v56, v201
	v_mul_f32_e32 v202, v56, v202
	v_mul_f32_e32 v203, v56, v203
	ds_write_b128 v210, v[200:203] offset:6144
	v_mul_f32_e32 v204, v57, v204
	v_mul_f32_e32 v205, v57, v205
	v_mul_f32_e32 v206, v57, v206
	v_mul_f32_e32 v207, v57, v207
	ds_write_b128 v210, v[204:207] offset:7168
	s_waitcnt lgkmcnt(0)
	s_barrier
; #define GAS __attribute__((address_space(1)))
; #define LAS __attribute__((address_space(3)))
; #define LDS_WAIT() asm volatile("s_waitcnt lgkmcnt(0)" ::: "memory")
; __device__ __forceinline__ int nat_dim(int p) { return (p >> 1) + 64 * (p & 1); }
; template <int MAP, bool KS, bool KPERM = false>
; __device__ __forceinline__ void p0_transpose_item(const float* W, int K, int Nsrc, int nblk, bf16* WT, const float* ksA, const float* ksB, int ksplit, LAS float* scr, int item, int lane) {
;     const int kb = item / nblk, nb = item % nblk, k0 = 64 * kb, n0 = 32 * nb;
;     const int nr = n0 + (lane & 31); const int sc = MAP == 1 ? src_col_in(nr) : (MAP == 2 ? nat_dim(nr) : nr);
;     float v[32];
; #pragma unroll
;     for (int i = 0; i < 32; ++i) { const int k = k0 + 2 * i + (lane >> 5); const int ksrc = KPERM ? ((k & ~127) + nat_dim(k & 127)) : k;
;         v[i] = sc >= 0 ? W[(size_t)ksrc * Nsrc + sc] : 0.f; }
; #pragma unroll
;     for (int i = 0; i < 32; ++i) { const int kk = 2 * i + (lane >> 5); const int k = k0 + kk;
;         if (KS) v[i] *= (k < ksplit ? ksA[k] : ksB[k - ksplit]);
;         scr[kk * 33 + (lane & 31)] = v[i]; }
;     LDS_WAIT(); asm volatile("" ::: "memory");
;     const int pr = item >> 1, kb = 2 * (pr / nblk) + (item & 1), nb = pr % nblk, k0 = 64 * kb, n0 = 32 * nb;
;     const int nr = n0 + (lane & 31); const int sc = MAP == 1 ? src_col_in(nr) : nr;
;     float v[32];
; #pragma unroll
;     for (int i = 0; i < 32; ++i) v[i] = sc >= 0 ? W[(size_t)(k0 + 2 * i + (lane >> 5)) * Nsrc + sc] : 0.f;
; #pragma unroll
;     for (int i = 0; i < 32; ++i) { const int k = k0 + 2 * i + (lane >> 5); float x = v[i] * wscale; if (KS) x *= (k < ksplit ? ksA[k] : ksB[k - ksplit]); scr[(2 * i + (lane >> 5)) * 33 + (lane & 31)] = x; }
;     LDS_WAIT(); asm volatile("" ::: "memory");
;     const int c = lane & 7;
; #pragma unroll
;     for (int j = 0; j < 4; ++j) { const int n = (lane >> 3) + 8 * j; const LAS float* s = scr + (8 * c) * 33 + n;
;         const unsigned long long o = (unsigned long long)pg8::pk4_fp8(s[0 * 33], s[1 * 33], s[2 * 33], s[3 * 33]) | ((unsigned long long)pg8::pk4_fp8(s[4 * 33], s[5 * 33], s[6 * 33], s[7 * 33]) << 32);
;         *(GAS unsigned long long*)(WT + (size_t)(n0 + n) * K + k0 + 8 * c) = o; }
;     LDS_WAIT(); asm volatile("" ::: "memory");
; }
	s_add_u32 s8, s54, 0x1000
	s_addc_u32 s9, s55, 0
	global_load_dwordx4 v[176:179], v75, s[8:9]
	s_add_u32 s8, s8, 0x8000
	s_addc_u32 s9, s9, 0
	global_load_dwordx4 v[180:183], v75, s[8:9]
	s_add_u32 s8, s8, 0x8000
	s_addc_u32 s9, s9, 0
	global_load_dwordx4 v[184:187], v75, s[8:9]
	s_add_u32 s8, s8, 0x8000
	s_addc_u32 s9, s9, 0
	global_load_dwordx4 v[188:191], v75, s[8:9]
	s_add_u32 s8, s8, 0x8000
	s_addc_u32 s9, s9, 0
	global_load_dwordx4 v[192:195], v75, s[8:9]
	s_add_u32 s8, s8, 0x8000
	s_addc_u32 s9, s9, 0
	global_load_dwordx4 v[196:199], v75, s[8:9]
	s_add_u32 s8, s8, 0x8000
	s_addc_u32 s9, s9, 0
	global_load_dwordx4 v[200:203], v75, s[8:9]
	s_add_u32 s8, s8, 0x8000
	s_addc_u32 s9, s9, 0
	global_load_dwordx4 v[204:207], v75, s[8:9]
	s_add_i32 s24, s23, 80
	s_mul_i32 s20, s24, 0x80000
	s_add_u32 s6, s52, s20
	s_addc_u32 s7, s53, 0
	s_cmp_lt_u32 s24, 16
	s_cselect_b32 s20, 1, 0
	s_sub_i32 s21, s24, 16
	s_bitcmp0_b32 s21, 2
	s_cselect_b32 s21, 1, 0
	s_cmp_lt_u32 s24, 40
	s_cselect_b32 s21, s21, 0
	s_or_b32 s20, s20, s21
	s_cmp_lg_u32 s20, 0
	s_cselect_b64 s[20:21], -1, 0
	v_cndmask_b32_e64 v91, v77, v81, s[20:21]
	v_cndmask_b32_e64 v92, v78, v82, s[20:21]
	ds_read_b32 v226, v212
	ds_read_b32 v227, v212 offset:512
	ds_read_b32 v228, v212 offset:1024
	ds_read_b32 v229, v212 offset:1536
	ds_read_b32 v230, v212 offset:2048
	ds_read_b32 v231, v212 offset:2560
	ds_read_b32 v232, v212 offset:3072
	ds_read_b32 v233, v212 offset:3584
	ds_read_b32 v234, v212 offset:4096
	ds_read_b32 v235, v212 offset:4608
	ds_read_b32 v236, v212 offset:5120
	ds_read_b32 v237, v212 offset:5632
	ds_read_b32 v238, v212 offset:6144
	ds_read_b32 v239, v212 offset:6656
	ds_read_b32 v240, v212 offset:7168
	ds_read_b32 v241, v212 offset:7680
	s_waitcnt lgkmcnt(0)
	v_max_f32_e32 v226, v226, v226
	v_max_f32_e32 v227, v227, v227
	v_max_f32_e32 v228, v228, v228
	v_max_f32_e32 v229, v229, v229
	v_max_f32_e32 v230, v230, v230
	v_max_f32_e32 v231, v231, v231
	v_max_f32_e32 v232, v232, v232
	v_max_f32_e32 v233, v233, v233
	v_max_f32_e32 v234, v234, v234
	v_max_f32_e32 v235, v235, v235
	v_max_f32_e32 v236, v236, v236
	v_max_f32_e32 v237, v237, v237
	v_max_f32_e32 v238, v238, v238
	v_max_f32_e32 v239, v239, v239
	v_max_f32_e32 v240, v240, v240
	v_max_f32_e32 v241, v241, v241
	v_med3_f32 v226, v226, s62, v95
	v_med3_f32 v227, v227, s62, v95
	v_med3_f32 v228, v228, s62, v95
	v_med3_f32 v229, v229, s62, v95
	v_med3_f32 v230, v230, s62, v95
	v_med3_f32 v231, v231, s62, v95
	v_med3_f32 v232, v232, s62, v95
	v_med3_f32 v233, v233, s62, v95
	v_med3_f32 v234, v234, s62, v95
	v_med3_f32 v235, v235, s62, v95
	v_med3_f32 v236, v236, s62, v95
	v_med3_f32 v237, v237, s62, v95
	v_med3_f32 v238, v238, s62, v95
	v_med3_f32 v239, v239, s62, v95
	v_med3_f32 v240, v240, s62, v95
	v_med3_f32 v241, v241, s62, v95
	v_mov_b32_e32 v242, 0
	v_mov_b32_e32 v243, 0
	v_mov_b32_e32 v244, 0
	v_mov_b32_e32 v245, 0
	v_cvt_pk_fp8_f32 v242, v226, v227
	v_cvt_pk_fp8_f32 v243, v230, v231
	v_cvt_pk_fp8_f32 v244, v234, v235
	v_cvt_pk_fp8_f32 v245, v238, v239
	v_cvt_pk_fp8_f32 v242, v228, v229 op_sel:[0,0,1]
	v_cvt_pk_fp8_f32 v243, v232, v233 op_sel:[0,0,1]
	v_cvt_pk_fp8_f32 v244, v236, v237 op_sel:[0,0,1]
	v_cvt_pk_fp8_f32 v245, v240, v241 op_sel:[0,0,1]
	s_nop 0
	global_store_dwordx4 v91, v[242:245], s[6:7]
	ds_read_b32 v226, v214
	ds_read_b32 v227, v214 offset:512
	ds_read_b32 v228, v214 offset:1024
	ds_read_b32 v229, v214 offset:1536
	ds_read_b32 v230, v214 offset:2048
	ds_read_b32 v231, v214 offset:2560
	ds_read_b32 v232, v214 offset:3072
	ds_read_b32 v233, v214 offset:3584
	ds_read_b32 v234, v214 offset:4096
	ds_read_b32 v235, v214 offset:4608
	ds_read_b32 v236, v214 offset:5120
	ds_read_b32 v237, v214 offset:5632
	ds_read_b32 v238, v214 offset:6144
	ds_read_b32 v239, v214 offset:6656
	ds_read_b32 v240, v214 offset:7168
	ds_read_b32 v241, v214 offset:7680
	s_waitcnt lgkmcnt(0)
	v_max_f32_e32 v226, v226, v226
	v_max_f32_e32 v227, v227, v227
	v_max_f32_e32 v228, v228, v228
	v_max_f32_e32 v229, v229, v229
	v_max_f32_e32 v230, v230, v230
	v_max_f32_e32 v231, v231, v231
	v_max_f32_e32 v232, v232, v232
	v_max_f32_e32 v233, v233, v233
	v_max_f32_e32 v234, v234, v234
	v_max_f32_e32 v235, v235, v235
	v_max_f32_e32 v236, v236, v236
	v_max_f32_e32 v237, v237, v237
	v_max_f32_e32 v238, v238, v238
	v_max_f32_e32 v239, v239, v239
	v_max_f32_e32 v240, v240, v240
	v_max_f32_e32 v241, v241, v241
	v_med3_f32 v226, v226, s62, v95
	v_med3_f32 v227, v227, s62, v95
	v_med3_f32 v228, v228, s62, v95
	v_med3_f32 v229, v229, s62, v95
	v_med3_f32 v230, v230, s62, v95
	v_med3_f32 v231, v231, s62, v95
	v_med3_f32 v232, v232, s62, v95
	v_med3_f32 v233, v233, s62, v95
	v_med3_f32 v234, v234, s62, v95
	v_med3_f32 v235, v235, s62, v95
	v_med3_f32 v236, v236, s62, v95
	v_med3_f32 v237, v237, s62, v95
	v_med3_f32 v238, v238, s62, v95
	v_med3_f32 v239, v239, s62, v95
	v_med3_f32 v240, v240, s62, v95
	v_med3_f32 v241, v241, s62, v95
	v_mov_b32_e32 v242, 0
	v_mov_b32_e32 v243, 0
	v_mov_b32_e32 v244, 0
	v_mov_b32_e32 v245, 0
	v_cvt_pk_fp8_f32 v242, v226, v227
	v_cvt_pk_fp8_f32 v243, v230, v231
	v_cvt_pk_fp8_f32 v244, v234, v235
	v_cvt_pk_fp8_f32 v245, v238, v239
	v_cvt_pk_fp8_f32 v242, v228, v229 op_sel:[0,0,1]
	v_cvt_pk_fp8_f32 v243, v232, v233 op_sel:[0,0,1]
	v_cvt_pk_fp8_f32 v244, v236, v237 op_sel:[0,0,1]
	v_cvt_pk_fp8_f32 v245, v240, v241 op_sel:[0,0,1]
	s_nop 0
	global_store_dwordx4 v92, v[242:245], s[6:7]
	s_waitcnt vmcnt(12)
	v_mul_f32_e32 v144, v58, v144
	v_mul_f32_e32 v145, v58, v145
	v_mul_f32_e32 v146, v58, v146
	v_mul_f32_e32 v147, v58, v147
	ds_write_b128 v209, v[144:147]
	v_mul_f32_e32 v148, v59, v148
	v_mul_f32_e32 v149, v59, v149
	v_mul_f32_e32 v150, v59, v150
	v_mul_f32_e32 v151, v59, v151
	ds_write_b128 v209, v[148:151] offset:1024
	v_mul_f32_e32 v152, v60, v152
	v_mul_f32_e32 v153, v60, v153
	v_mul_f32_e32 v154, v60, v154
	v_mul_f32_e32 v155, v60, v155
	ds_write_b128 v209, v[152:155] offset:2048
	v_mul_f32_e32 v156, v61, v156
	v_mul_f32_e32 v157, v61, v157
	v_mul_f32_e32 v158, v61, v158
	v_mul_f32_e32 v159, v61, v159
	ds_write_b128 v209, v[156:159] offset:3072
	v_mul_f32_e32 v160, v62, v160
	v_mul_f32_e32 v161, v62, v161
	v_mul_f32_e32 v162, v62, v162
	v_mul_f32_e32 v163, v62, v163
	ds_write_b128 v209, v[160:163] offset:4096
	v_mul_f32_e32 v164, v63, v164
	v_mul_f32_e32 v165, v63, v165
	v_mul_f32_e32 v166, v63, v166
	v_mul_f32_e32 v167, v63, v167
	ds_write_b128 v209, v[164:167] offset:5120
	v_mul_f32_e32 v168, v64, v168
	v_mul_f32_e32 v169, v64, v169
	v_mul_f32_e32 v170, v64, v170
	v_mul_f32_e32 v171, v64, v171
	ds_write_b128 v209, v[168:171] offset:6144
	v_mul_f32_e32 v172, v65, v172
	v_mul_f32_e32 v173, v65, v173
	v_mul_f32_e32 v174, v65, v174
	v_mul_f32_e32 v175, v65, v175
	ds_write_b128 v209, v[172:175] offset:7168
	s_waitcnt lgkmcnt(0)
	s_barrier
; #define GAS __attribute__((address_space(1)))
; #define LAS __attribute__((address_space(3)))
; #define LDS_WAIT() asm volatile("s_waitcnt lgkmcnt(0)" ::: "memory")
; __device__ __forceinline__ unsigned pk2(float lo, float hi) { return f2bf(lo) | (f2bf(hi) << 16); }
; __device__ __forceinline__ int nat_dim(int p) { return (p >> 1) + 64 * (p & 1); }
; template <int MAP, bool KS, bool KPERM = false>
; __device__ __forceinline__ void p0_transpose_item(const float* W, int K, int Nsrc, int nblk, bf16* WT, const float* ksA, const float* ksB, int ksplit, LAS float* scr, int item, int lane) {
;     const int kb = item / nblk, nb = item % nblk, k0 = 64 * kb, n0 = 32 * nb;
;     const int nr = n0 + (lane & 31); const int sc = MAP == 1 ? src_col_in(nr) : (MAP == 2 ? nat_dim(nr) : nr);
;     float v[32];
; #pragma unroll
;     for (int i = 0; i < 32; ++i) { const int k = k0 + 2 * i + (lane >> 5); const int ksrc = KPERM ? ((k & ~127) + nat_dim(k & 127)) : k;
;         v[i] = sc >= 0 ? W[(size_t)ksrc * Nsrc + sc] : 0.f; }
; #pragma unroll
;     for (int i = 0; i < 32; ++i) { const int kk = 2 * i + (lane >> 5); const int k = k0 + kk;
;         if (KS) v[i] *= (k < ksplit ? ksA[k] : ksB[k - ksplit]);
;         scr[kk * 33 + (lane & 31)] = v[i]; }
;     LDS_WAIT(); asm volatile("" ::: "memory");
;     const int c = lane & 7;
; #pragma unroll
;     for (int j = 0; j < 4; ++j) { const int n = (lane >> 3) + 8 * j; const LAS float* s = scr + (8 * c) * 33 + n;
;         v4u o; o.x = pk2(s[0 * 33], s[1 * 33]); o.y = pk2(s[2 * 33], s[3 * 33]); o.z = pk2(s[4 * 33], s[5 * 33]); o.w = pk2(s[6 * 33], s[7 * 33]);
;         *(GAS v4u*)(WT + (size_t)(n0 + n) * K + k0 + 8 * c) = o; }
;     LDS_WAIT(); asm volatile("" ::: "memory");
; }
; __global__ void __launch_bounds__(NWAVES * 64, 2) hybrid_fwd(Args args) {
;     ...
;             if (r < I_O) { if (l >= WO_F8_FROM) p0_transpose_item_f8<true>(args.in[13] + (size_t)l * DM * DM, DM, DM, DM / 32, (unsigned char*)(ws + WS_WO + l * SZ_WO), 64.f, args.in[6] + l * 2048, args.in[12] + l * 2048, 2048, scr, r, lane);
;                 else p0_transpose_item<0, true>(args.in[13] + (size_t)l * DM * DM, DM, DM, DM / 32, (bf16*)(ws + WS_WO + l * SZ_WO), args.in[6] + l * 2048, args.in[12] + l * 2048, 2048, scr, r, lane); continue; } r -= I_O;
	s_add_u32 s8, s54, 0x2000
	s_addc_u32 s9, s55, 0
	global_load_dwordx4 v[144:147], v75, s[8:9]
	s_add_u32 s8, s8, 0x8000
	s_addc_u32 s9, s9, 0
	global_load_dwordx4 v[148:151], v75, s[8:9]
	s_add_u32 s8, s8, 0x8000
	s_addc_u32 s9, s9, 0
	global_load_dwordx4 v[152:155], v75, s[8:9]
	s_add_u32 s8, s8, 0x8000
	s_addc_u32 s9, s9, 0
	global_load_dwordx4 v[156:159], v75, s[8:9]
	s_add_u32 s8, s8, 0x8000
	s_addc_u32 s9, s9, 0
	global_load_dwordx4 v[160:163], v75, s[8:9]
	s_add_u32 s8, s8, 0x8000
	s_addc_u32 s9, s9, 0
	global_load_dwordx4 v[164:167], v75, s[8:9]
	s_add_u32 s8, s8, 0x8000
	s_addc_u32 s9, s9, 0
	global_load_dwordx4 v[168:171], v75, s[8:9]
	s_add_u32 s8, s8, 0x8000
	s_addc_u32 s9, s9, 0
	global_load_dwordx4 v[172:175], v75, s[8:9]
	s_mov_b64 s[6:7], s[56:57]
	ds_read_b32 v226, v112
	ds_read_b32 v227, v112 offset:512
	ds_read_b32 v228, v112 offset:1024
	ds_read_b32 v229, v112 offset:1536
	ds_read_b32 v230, v112 offset:2048
	ds_read_b32 v231, v112 offset:2560
	ds_read_b32 v232, v112 offset:3072
	ds_read_b32 v233, v112 offset:3584
	s_waitcnt lgkmcnt(0)
	v_bfe_u32 v120, v226, 16, 1
	v_bfe_u32 v121, v227, 16, 1
	v_bfe_u32 v122, v228, 16, 1
	v_bfe_u32 v123, v229, 16, 1
	v_bfe_u32 v124, v230, 16, 1
	v_bfe_u32 v125, v231, 16, 1
	v_bfe_u32 v126, v232, 16, 1
	v_bfe_u32 v127, v233, 16, 1
	v_add3_u32 v226, v226, v120, s63
	v_add3_u32 v227, v227, v121, s63
	v_add3_u32 v228, v228, v122, s63
	v_add3_u32 v229, v229, v123, s63
	v_add3_u32 v230, v230, v124, s63
	v_add3_u32 v231, v231, v125, s63
	v_add3_u32 v232, v232, v126, s63
	v_add3_u32 v233, v233, v127, s63
	v_perm_b32 v242, v227, v226, s64
	v_perm_b32 v243, v229, v228, s64
	v_perm_b32 v244, v231, v230, s64
	v_perm_b32 v245, v233, v232, s64
	s_nop 0
	global_store_dwordx4 v83, v[242:245], s[6:7]
	ds_read_b32 v226, v114
	ds_read_b32 v227, v114 offset:512
	ds_read_b32 v228, v114 offset:1024
	ds_read_b32 v229, v114 offset:1536
	ds_read_b32 v230, v114 offset:2048
	ds_read_b32 v231, v114 offset:2560
	ds_read_b32 v232, v114 offset:3072
	ds_read_b32 v233, v114 offset:3584
	s_waitcnt lgkmcnt(0)
	v_bfe_u32 v120, v226, 16, 1
	v_bfe_u32 v121, v227, 16, 1
	v_bfe_u32 v122, v228, 16, 1
	v_bfe_u32 v123, v229, 16, 1
	v_bfe_u32 v124, v230, 16, 1
	v_bfe_u32 v125, v231, 16, 1
	v_bfe_u32 v126, v232, 16, 1
	v_bfe_u32 v127, v233, 16, 1
	v_add3_u32 v226, v226, v120, s63
	v_add3_u32 v227, v227, v121, s63
	v_add3_u32 v228, v228, v122, s63
	v_add3_u32 v229, v229, v123, s63
	v_add3_u32 v230, v230, v124, s63
	v_add3_u32 v231, v231, v125, s63
	v_add3_u32 v232, v232, v126, s63
	v_add3_u32 v233, v233, v127, s63
	v_perm_b32 v242, v227, v226, s64
	v_perm_b32 v243, v229, v228, s64
	v_perm_b32 v244, v231, v230, s64
	v_perm_b32 v245, v233, v232, s64
	s_nop 0
	global_store_dwordx4 v84, v[242:245], s[6:7]
	ds_read_b32 v226, v116
	ds_read_b32 v227, v116 offset:512
	ds_read_b32 v228, v116 offset:1024
	ds_read_b32 v229, v116 offset:1536
	ds_read_b32 v230, v116 offset:2048
	ds_read_b32 v231, v116 offset:2560
	ds_read_b32 v232, v116 offset:3072
	ds_read_b32 v233, v116 offset:3584
	s_waitcnt lgkmcnt(0)
	v_bfe_u32 v120, v226, 16, 1
	v_bfe_u32 v121, v227, 16, 1
	v_bfe_u32 v122, v228, 16, 1
	v_bfe_u32 v123, v229, 16, 1
	v_bfe_u32 v124, v230, 16, 1
	v_bfe_u32 v125, v231, 16, 1
	v_bfe_u32 v126, v232, 16, 1
	v_bfe_u32 v127, v233, 16, 1
	v_add3_u32 v226, v226, v120, s63
	v_add3_u32 v227, v227, v121, s63
	v_add3_u32 v228, v228, v122, s63
	v_add3_u32 v229, v229, v123, s63
	v_add3_u32 v230, v230, v124, s63
	v_add3_u32 v231, v231, v125, s63
	v_add3_u32 v232, v232, v126, s63
	v_add3_u32 v233, v233, v127, s63
	v_perm_b32 v242, v227, v226, s64
	v_perm_b32 v243, v229, v228, s64
	v_perm_b32 v244, v231, v230, s64
	v_perm_b32 v245, v233, v232, s64
	s_nop 0
	global_store_dwordx4 v85, v[242:245], s[6:7]
	ds_read_b32 v226, v118
	ds_read_b32 v227, v118 offset:512
	ds_read_b32 v228, v118 offset:1024
	ds_read_b32 v229, v118 offset:1536
	ds_read_b32 v230, v118 offset:2048
	ds_read_b32 v231, v118 offset:2560
	ds_read_b32 v232, v118 offset:3072
	ds_read_b32 v233, v118 offset:3584
	s_waitcnt lgkmcnt(0)
	v_bfe_u32 v120, v226, 16, 1
	v_bfe_u32 v121, v227, 16, 1
	v_bfe_u32 v122, v228, 16, 1
	v_bfe_u32 v123, v229, 16, 1
	v_bfe_u32 v124, v230, 16, 1
	v_bfe_u32 v125, v231, 16, 1
	v_bfe_u32 v126, v232, 16, 1
	v_bfe_u32 v127, v233, 16, 1
	v_add3_u32 v226, v226, v120, s63
	v_add3_u32 v227, v227, v121, s63
	v_add3_u32 v228, v228, v122, s63
	v_add3_u32 v229, v229, v123, s63
	v_add3_u32 v230, v230, v124, s63
	v_add3_u32 v231, v231, v125, s63
	v_add3_u32 v232, v232, v126, s63
	v_add3_u32 v233, v233, v127, s63
	v_perm_b32 v242, v227, v226, s64
	v_perm_b32 v243, v229, v228, s64
	v_perm_b32 v244, v231, v230, s64
	v_perm_b32 v245, v233, v232, s64
	s_nop 0
	global_store_dwordx4 v86, v[242:245], s[6:7]
	s_waitcnt vmcnt(14)
	v_mul_f32_e32 v176, v58, v176
	v_mul_f32_e32 v177, v58, v177
	v_mul_f32_e32 v178, v58, v178
	v_mul_f32_e32 v179, v58, v179
	ds_write_b128 v210, v[176:179]
	v_mul_f32_e32 v180, v59, v180
	v_mul_f32_e32 v181, v59, v181
	v_mul_f32_e32 v182, v59, v182
	v_mul_f32_e32 v183, v59, v183
	ds_write_b128 v210, v[180:183] offset:1024
	v_mul_f32_e32 v184, v60, v184
	v_mul_f32_e32 v185, v60, v185
	v_mul_f32_e32 v186, v60, v186
	v_mul_f32_e32 v187, v60, v187
	ds_write_b128 v210, v[184:187] offset:2048
	v_mul_f32_e32 v188, v61, v188
	v_mul_f32_e32 v189, v61, v189
	v_mul_f32_e32 v190, v61, v190
	v_mul_f32_e32 v191, v61, v191
	ds_write_b128 v210, v[188:191] offset:3072
	v_mul_f32_e32 v192, v62, v192
	v_mul_f32_e32 v193, v62, v193
	v_mul_f32_e32 v194, v62, v194
	v_mul_f32_e32 v195, v62, v195
	ds_write_b128 v210, v[192:195] offset:4096
	v_mul_f32_e32 v196, v63, v196
	v_mul_f32_e32 v197, v63, v197
	v_mul_f32_e32 v198, v63, v198
	v_mul_f32_e32 v199, v63, v199
	ds_write_b128 v210, v[196:199] offset:5120
	v_mul_f32_e32 v200, v64, v200
	v_mul_f32_e32 v201, v64, v201
	v_mul_f32_e32 v202, v64, v202
	v_mul_f32_e32 v203, v64, v203
	ds_write_b128 v210, v[200:203] offset:6144
	v_mul_f32_e32 v204, v65, v204
	v_mul_f32_e32 v205, v65, v205
	v_mul_f32_e32 v206, v65, v206
	v_mul_f32_e32 v207, v65, v207
	ds_write_b128 v210, v[204:207] offset:7168
	s_waitcnt lgkmcnt(0)
	s_barrier
; #define GAS __attribute__((address_space(1)))
; #define LAS __attribute__((address_space(3)))
; #define LDS_WAIT() asm volatile("s_waitcnt lgkmcnt(0)" ::: "memory")
; __device__ __forceinline__ unsigned pk2(float lo, float hi) { return f2bf(lo) | (f2bf(hi) << 16); }
; __device__ __forceinline__ int nat_dim(int p) { return (p >> 1) + 64 * (p & 1); }
; template <int MAP, bool KS, bool KPERM = false>
; __device__ __forceinline__ void p0_transpose_item(const float* W, int K, int Nsrc, int nblk, bf16* WT, const float* ksA, const float* ksB, int ksplit, LAS float* scr, int item, int lane) {
;     const int kb = item / nblk, nb = item % nblk, k0 = 64 * kb, n0 = 32 * nb;
;     const int nr = n0 + (lane & 31); const int sc = MAP == 1 ? src_col_in(nr) : (MAP == 2 ? nat_dim(nr) : nr);
;     float v[32];
; #pragma unroll
;     for (int i = 0; i < 32; ++i) { const int k = k0 + 2 * i + (lane >> 5); const int ksrc = KPERM ? ((k & ~127) + nat_dim(k & 127)) : k;
;         v[i] = sc >= 0 ? W[(size_t)ksrc * Nsrc + sc] : 0.f; }
; #pragma unroll
;     for (int i = 0; i < 32; ++i) { const int kk = 2 * i + (lane >> 5); const int k = k0 + kk;
;         if (KS) v[i] *= (k < ksplit ? ksA[k] : ksB[k - ksplit]);
;         scr[kk * 33 + (lane & 31)] = v[i]; }
;     LDS_WAIT(); asm volatile("" ::: "memory");
;     const int c = lane & 7;
; #pragma unroll
;     for (int j = 0; j < 4; ++j) { const int n = (lane >> 3) + 8 * j; const LAS float* s = scr + (8 * c) * 33 + n;
;         v4u o; o.x = pk2(s[0 * 33], s[1 * 33]); o.y = pk2(s[2 * 33], s[3 * 33]); o.z = pk2(s[4 * 33], s[5 * 33]); o.w = pk2(s[6 * 33], s[7 * 33]);
;         *(GAS v4u*)(WT + (size_t)(n0 + n) * K + k0 + 8 * c) = o; }
;     LDS_WAIT(); asm volatile("" ::: "memory");
; }
; __global__ void __launch_bounds__(NWAVES * 64, 2) hybrid_fwd(Args args) {
;     ...
;             if (r < I_O) { if (l >= WO_F8_FROM) p0_transpose_item_f8<true>(args.in[13] + (size_t)l * DM * DM, DM, DM, DM / 32, (unsigned char*)(ws + WS_WO + l * SZ_WO), 64.f, args.in[6] + l * 2048, args.in[12] + l * 2048, 2048, scr, r, lane);
;                 else p0_transpose_item<0, true>(args.in[13] + (size_t)l * DM * DM, DM, DM, DM / 32, (bf16*)(ws + WS_WO + l * SZ_WO), args.in[6] + l * 2048, args.in[12] + l * 2048, 2048, scr, r, lane); continue; } r -= I_O;
	s_add_u32 s8, s54, 0x3000
	s_addc_u32 s9, s55, 0
	global_load_dwordx4 v[176:179], v75, s[8:9]
	s_add_u32 s8, s8, 0x8000
	s_addc_u32 s9, s9, 0
	global_load_dwordx4 v[180:183], v75, s[8:9]
	s_add_u32 s8, s8, 0x8000
	s_addc_u32 s9, s9, 0
	global_load_dwordx4 v[184:187], v75, s[8:9]
	s_add_u32 s8, s8, 0x8000
	s_addc_u32 s9, s9, 0
	global_load_dwordx4 v[188:191], v75, s[8:9]
	s_add_u32 s8, s8, 0x8000
	s_addc_u32 s9, s9, 0
	global_load_dwordx4 v[192:195], v75, s[8:9]
	s_add_u32 s8, s8, 0x8000
	s_addc_u32 s9, s9, 0
	global_load_dwordx4 v[196:199], v75, s[8:9]
	s_add_u32 s8, s8, 0x8000
	s_addc_u32 s9, s9, 0
	global_load_dwordx4 v[200:203], v75, s[8:9]
	s_add_u32 s8, s8, 0x8000
	s_addc_u32 s9, s9, 0
	global_load_dwordx4 v[204:207], v75, s[8:9]
	s_add_u32 s6, s56, 0x800000
	s_addc_u32 s7, s57, 0
	ds_read_b32 v226, v113
	ds_read_b32 v227, v113 offset:512
	ds_read_b32 v228, v113 offset:1024
	ds_read_b32 v229, v113 offset:1536
	ds_read_b32 v230, v113 offset:2048
	ds_read_b32 v231, v113 offset:2560
	ds_read_b32 v232, v113 offset:3072
	ds_read_b32 v233, v113 offset:3584
	s_waitcnt lgkmcnt(0)
	v_bfe_u32 v120, v226, 16, 1
	v_bfe_u32 v121, v227, 16, 1
	v_bfe_u32 v122, v228, 16, 1
	v_bfe_u32 v123, v229, 16, 1
	v_bfe_u32 v124, v230, 16, 1
	v_bfe_u32 v125, v231, 16, 1
	v_bfe_u32 v126, v232, 16, 1
	v_bfe_u32 v127, v233, 16, 1
	v_add3_u32 v226, v226, v120, s63
	v_add3_u32 v227, v227, v121, s63
	v_add3_u32 v228, v228, v122, s63
	v_add3_u32 v229, v229, v123, s63
	v_add3_u32 v230, v230, v124, s63
	v_add3_u32 v231, v231, v125, s63
	v_add3_u32 v232, v232, v126, s63
	v_add3_u32 v233, v233, v127, s63
	v_perm_b32 v242, v227, v226, s64
	v_perm_b32 v243, v229, v228, s64
	v_perm_b32 v244, v231, v230, s64
	v_perm_b32 v245, v233, v232, s64
	s_nop 0
	global_store_dwordx4 v83, v[242:245], s[6:7]
	ds_read_b32 v226, v115
	ds_read_b32 v227, v115 offset:512
	ds_read_b32 v228, v115 offset:1024
	ds_read_b32 v229, v115 offset:1536
	ds_read_b32 v230, v115 offset:2048
	ds_read_b32 v231, v115 offset:2560
	ds_read_b32 v232, v115 offset:3072
	ds_read_b32 v233, v115 offset:3584
	s_waitcnt lgkmcnt(0)
	v_bfe_u32 v120, v226, 16, 1
	v_bfe_u32 v121, v227, 16, 1
	v_bfe_u32 v122, v228, 16, 1
	v_bfe_u32 v123, v229, 16, 1
	v_bfe_u32 v124, v230, 16, 1
	v_bfe_u32 v125, v231, 16, 1
	v_bfe_u32 v126, v232, 16, 1
	v_bfe_u32 v127, v233, 16, 1
	v_add3_u32 v226, v226, v120, s63
	v_add3_u32 v227, v227, v121, s63
	v_add3_u32 v228, v228, v122, s63
	v_add3_u32 v229, v229, v123, s63
	v_add3_u32 v230, v230, v124, s63
	v_add3_u32 v231, v231, v125, s63
	v_add3_u32 v232, v232, v126, s63
	v_add3_u32 v233, v233, v127, s63
	v_perm_b32 v242, v227, v226, s64
	v_perm_b32 v243, v229, v228, s64
	v_perm_b32 v244, v231, v230, s64
	v_perm_b32 v245, v233, v232, s64
	s_nop 0
	global_store_dwordx4 v84, v[242:245], s[6:7]
	ds_read_b32 v226, v117
	ds_read_b32 v227, v117 offset:512
	ds_read_b32 v228, v117 offset:1024
	ds_read_b32 v229, v117 offset:1536
	ds_read_b32 v230, v117 offset:2048
	ds_read_b32 v231, v117 offset:2560
	ds_read_b32 v232, v117 offset:3072
	ds_read_b32 v233, v117 offset:3584
	s_waitcnt lgkmcnt(0)
	v_bfe_u32 v120, v226, 16, 1
	v_bfe_u32 v121, v227, 16, 1
	v_bfe_u32 v122, v228, 16, 1
	v_bfe_u32 v123, v229, 16, 1
	v_bfe_u32 v124, v230, 16, 1
	v_bfe_u32 v125, v231, 16, 1
	v_bfe_u32 v126, v232, 16, 1
	v_bfe_u32 v127, v233, 16, 1
	v_add3_u32 v226, v226, v120, s63
	v_add3_u32 v227, v227, v121, s63
	v_add3_u32 v228, v228, v122, s63
	v_add3_u32 v229, v229, v123, s63
	v_add3_u32 v230, v230, v124, s63
	v_add3_u32 v231, v231, v125, s63
	v_add3_u32 v232, v232, v126, s63
	v_add3_u32 v233, v233, v127, s63
	v_perm_b32 v242, v227, v226, s64
	v_perm_b32 v243, v229, v228, s64
	v_perm_b32 v244, v231, v230, s64
	v_perm_b32 v245, v233, v232, s64
	s_nop 0
	global_store_dwordx4 v85, v[242:245], s[6:7]
	ds_read_b32 v226, v119
	ds_read_b32 v227, v119 offset:512
	ds_read_b32 v228, v119 offset:1024
	ds_read_b32 v229, v119 offset:1536
	ds_read_b32 v230, v119 offset:2048
	ds_read_b32 v231, v119 offset:2560
	ds_read_b32 v232, v119 offset:3072
	ds_read_b32 v233, v119 offset:3584
	s_waitcnt lgkmcnt(0)
	v_bfe_u32 v120, v226, 16, 1
	v_bfe_u32 v121, v227, 16, 1
	v_bfe_u32 v122, v228, 16, 1
	v_bfe_u32 v123, v229, 16, 1
	v_bfe_u32 v124, v230, 16, 1
	v_bfe_u32 v125, v231, 16, 1
	v_bfe_u32 v126, v232, 16, 1
	v_bfe_u32 v127, v233, 16, 1
	v_add3_u32 v226, v226, v120, s63
	v_add3_u32 v227, v227, v121, s63
	v_add3_u32 v228, v228, v122, s63
	v_add3_u32 v229, v229, v123, s63
	v_add3_u32 v230, v230, v124, s63
	v_add3_u32 v231, v231, v125, s63
	v_add3_u32 v232, v232, v126, s63
	v_add3_u32 v233, v233, v127, s63
	v_perm_b32 v242, v227, v226, s64
	v_perm_b32 v243, v229, v228, s64
	v_perm_b32 v244, v231, v230, s64
	v_perm_b32 v245, v233, v232, s64
	s_nop 0
	global_store_dwordx4 v86, v[242:245], s[6:7]
	s_waitcnt vmcnt(16)
	v_mul_f32_e32 v144, v58, v144
	v_mul_f32_e32 v145, v58, v145
	v_mul_f32_e32 v146, v58, v146
	v_mul_f32_e32 v147, v58, v147
	ds_write_b128 v209, v[144:147]
	v_mul_f32_e32 v148, v59, v148
	v_mul_f32_e32 v149, v59, v149
	v_mul_f32_e32 v150, v59, v150
	v_mul_f32_e32 v151, v59, v151
	ds_write_b128 v209, v[148:151] offset:1024
	v_mul_f32_e32 v152, v60, v152
	v_mul_f32_e32 v153, v60, v153
	v_mul_f32_e32 v154, v60, v154
	v_mul_f32_e32 v155, v60, v155
	ds_write_b128 v209, v[152:155] offset:2048
	v_mul_f32_e32 v156, v61, v156
	v_mul_f32_e32 v157, v61, v157
	v_mul_f32_e32 v158, v61, v158
	v_mul_f32_e32 v159, v61, v159
	ds_write_b128 v209, v[156:159] offset:3072
	v_mul_f32_e32 v160, v62, v160
	v_mul_f32_e32 v161, v62, v161
	v_mul_f32_e32 v162, v62, v162
	v_mul_f32_e32 v163, v62, v163
	ds_write_b128 v209, v[160:163] offset:4096
	v_mul_f32_e32 v164, v63, v164
	v_mul_f32_e32 v165, v63, v165
	v_mul_f32_e32 v166, v63, v166
	v_mul_f32_e32 v167, v63, v167
	ds_write_b128 v209, v[164:167] offset:5120
	v_mul_f32_e32 v168, v64, v168
	v_mul_f32_e32 v169, v64, v169
	v_mul_f32_e32 v170, v64, v170
	v_mul_f32_e32 v171, v64, v171
	ds_write_b128 v209, v[168:171] offset:6144
	v_mul_f32_e32 v172, v65, v172
	v_mul_f32_e32 v173, v65, v173
	v_mul_f32_e32 v174, v65, v174
	v_mul_f32_e32 v175, v65, v175
	ds_write_b128 v209, v[172:175] offset:7168
	s_waitcnt lgkmcnt(0)
	s_barrier
; #define GAS __attribute__((address_space(1)))
; #define LAS __attribute__((address_space(3)))
; #define LDS_WAIT() asm volatile("s_waitcnt lgkmcnt(0)" ::: "memory")
; __device__ __forceinline__ unsigned pk2(float lo, float hi) { return f2bf(lo) | (f2bf(hi) << 16); }
; __device__ __forceinline__ int nat_dim(int p) { return (p >> 1) + 64 * (p & 1); }
; template <int MAP, bool KS, bool KPERM = false>
; __device__ __forceinline__ void p0_transpose_item(const float* W, int K, int Nsrc, int nblk, bf16* WT, const float* ksA, const float* ksB, int ksplit, LAS float* scr, int item, int lane) {
;     const int kb = item / nblk, nb = item % nblk, k0 = 64 * kb, n0 = 32 * nb;
;     const int nr = n0 + (lane & 31); const int sc = MAP == 1 ? src_col_in(nr) : (MAP == 2 ? nat_dim(nr) : nr);
;     float v[32];
; #pragma unroll
;     for (int i = 0; i < 32; ++i) { const int k = k0 + 2 * i + (lane >> 5); const int ksrc = KPERM ? ((k & ~127) + nat_dim(k & 127)) : k;
;         v[i] = sc >= 0 ? W[(size_t)ksrc * Nsrc + sc] : 0.f; }
; #pragma unroll
;     for (int i = 0; i < 32; ++i) { const int kk = 2 * i + (lane >> 5); const int k = k0 + kk;
;         if (KS) v[i] *= (k < ksplit ? ksA[k] : ksB[k - ksplit]);
;         scr[kk * 33 + (lane & 31)] = v[i]; }
;     LDS_WAIT(); asm volatile("" ::: "memory");
;     const int c = lane & 7;
; #pragma unroll
;     for (int j = 0; j < 4; ++j) { const int n = (lane >> 3) + 8 * j; const LAS float* s = scr + (8 * c) * 33 + n;
;         v4u o; o.x = pk2(s[0 * 33], s[1 * 33]); o.y = pk2(s[2 * 33], s[3 * 33]); o.z = pk2(s[4 * 33], s[5 * 33]); o.w = pk2(s[6 * 33], s[7 * 33]);
;         *(GAS v4u*)(WT + (size_t)(n0 + n) * K + k0 + 8 * c) = o; }
;     LDS_WAIT(); asm volatile("" ::: "memory");
; }
; __global__ void __launch_bounds__(NWAVES * 64, 2) hybrid_fwd(Args args) {
;     ...
;             if (r < I_O) { if (l >= WO_F8_FROM) p0_transpose_item_f8<true>(args.in[13] + (size_t)l * DM * DM, DM, DM, DM / 32, (unsigned char*)(ws + WS_WO + l * SZ_WO), 64.f, args.in[6] + l * 2048, args.in[12] + l * 2048, 2048, scr, r, lane);
;                 else p0_transpose_item<0, true>(args.in[13] + (size_t)l * DM * DM, DM, DM, DM / 32, (bf16*)(ws + WS_WO + l * SZ_WO), args.in[6] + l * 2048, args.in[12] + l * 2048, 2048, scr, r, lane); continue; } r -= I_O;
	s_mov_b64 s[8:9], s[58:59]
	global_load_dwordx4 v[144:147], v75, s[8:9]
	s_add_u32 s8, s8, 0x8000
	s_addc_u32 s9, s9, 0
	global_load_dwordx4 v[148:151], v75, s[8:9]
	s_add_u32 s8, s8, 0x8000
	s_addc_u32 s9, s9, 0
	global_load_dwordx4 v[152:155], v75, s[8:9]
	s_add_u32 s8, s8, 0x8000
	s_addc_u32 s9, s9, 0
	global_load_dwordx4 v[156:159], v75, s[8:9]
	s_add_u32 s8, s8, 0x8000
	s_addc_u32 s9, s9, 0
	global_load_dwordx4 v[160:163], v75, s[8:9]
	s_add_u32 s8, s8, 0x8000
	s_addc_u32 s9, s9, 0
	global_load_dwordx4 v[164:167], v75, s[8:9]
	s_add_u32 s8, s8, 0x8000
	s_addc_u32 s9, s9, 0
	global_load_dwordx4 v[168:171], v75, s[8:9]
	s_add_u32 s8, s8, 0x8000
	s_addc_u32 s9, s9, 0
	global_load_dwordx4 v[172:175], v75, s[8:9]
	s_add_u32 s6, s56, 0x1000000
	s_addc_u32 s7, s57, 0
	ds_read_b32 v226, v112
	ds_read_b32 v227, v112 offset:512
	ds_read_b32 v228, v112 offset:1024
	ds_read_b32 v229, v112 offset:1536
	ds_read_b32 v230, v112 offset:2048
	ds_read_b32 v231, v112 offset:2560
	ds_read_b32 v232, v112 offset:3072
	ds_read_b32 v233, v112 offset:3584
	s_waitcnt lgkmcnt(0)
	v_bfe_u32 v120, v226, 16, 1
	v_bfe_u32 v121, v227, 16, 1
	v_bfe_u32 v122, v228, 16, 1
	v_bfe_u32 v123, v229, 16, 1
	v_bfe_u32 v124, v230, 16, 1
	v_bfe_u32 v125, v231, 16, 1
	v_bfe_u32 v126, v232, 16, 1
	v_bfe_u32 v127, v233, 16, 1
	v_add3_u32 v226, v226, v120, s63
	v_add3_u32 v227, v227, v121, s63
	v_add3_u32 v228, v228, v122, s63
	v_add3_u32 v229, v229, v123, s63
	v_add3_u32 v230, v230, v124, s63
	v_add3_u32 v231, v231, v125, s63
	v_add3_u32 v232, v232, v126, s63
	v_add3_u32 v233, v233, v127, s63
	v_perm_b32 v242, v227, v226, s64
	v_perm_b32 v243, v229, v228, s64
	v_perm_b32 v244, v231, v230, s64
	v_perm_b32 v245, v233, v232, s64
	s_nop 0
	global_store_dwordx4 v83, v[242:245], s[6:7]
	ds_read_b32 v226, v114
	ds_read_b32 v227, v114 offset:512
	ds_read_b32 v228, v114 offset:1024
	ds_read_b32 v229, v114 offset:1536
	ds_read_b32 v230, v114 offset:2048
	ds_read_b32 v231, v114 offset:2560
	ds_read_b32 v232, v114 offset:3072
	ds_read_b32 v233, v114 offset:3584
	s_waitcnt lgkmcnt(0)
	v_bfe_u32 v120, v226, 16, 1
	v_bfe_u32 v121, v227, 16, 1
	v_bfe_u32 v122, v228, 16, 1
	v_bfe_u32 v123, v229, 16, 1
	v_bfe_u32 v124, v230, 16, 1
	v_bfe_u32 v125, v231, 16, 1
	v_bfe_u32 v126, v232, 16, 1
	v_bfe_u32 v127, v233, 16, 1
	v_add3_u32 v226, v226, v120, s63
	v_add3_u32 v227, v227, v121, s63
	v_add3_u32 v228, v228, v122, s63
	v_add3_u32 v229, v229, v123, s63
	v_add3_u32 v230, v230, v124, s63
	v_add3_u32 v231, v231, v125, s63
	v_add3_u32 v232, v232, v126, s63
	v_add3_u32 v233, v233, v127, s63
	v_perm_b32 v242, v227, v226, s64
	v_perm_b32 v243, v229, v228, s64
	v_perm_b32 v244, v231, v230, s64
	v_perm_b32 v245, v233, v232, s64
	s_nop 0
	global_store_dwordx4 v84, v[242:245], s[6:7]
	ds_read_b32 v226, v116
	ds_read_b32 v227, v116 offset:512
	ds_read_b32 v228, v116 offset:1024
	ds_read_b32 v229, v116 offset:1536
	ds_read_b32 v230, v116 offset:2048
	ds_read_b32 v231, v116 offset:2560
	ds_read_b32 v232, v116 offset:3072
	ds_read_b32 v233, v116 offset:3584
	s_waitcnt lgkmcnt(0)
	v_bfe_u32 v120, v226, 16, 1
	v_bfe_u32 v121, v227, 16, 1
	v_bfe_u32 v122, v228, 16, 1
	v_bfe_u32 v123, v229, 16, 1
	v_bfe_u32 v124, v230, 16, 1
	v_bfe_u32 v125, v231, 16, 1
	v_bfe_u32 v126, v232, 16, 1
	v_bfe_u32 v127, v233, 16, 1
	v_add3_u32 v226, v226, v120, s63
	v_add3_u32 v227, v227, v121, s63
	v_add3_u32 v228, v228, v122, s63
	v_add3_u32 v229, v229, v123, s63
	v_add3_u32 v230, v230, v124, s63
	v_add3_u32 v231, v231, v125, s63
	v_add3_u32 v232, v232, v126, s63
	v_add3_u32 v233, v233, v127, s63
	v_perm_b32 v242, v227, v226, s64
	v_perm_b32 v243, v229, v228, s64
	v_perm_b32 v244, v231, v230, s64
	v_perm_b32 v245, v233, v232, s64
	s_nop 0
	global_store_dwordx4 v85, v[242:245], s[6:7]
	ds_read_b32 v226, v118
	ds_read_b32 v227, v118 offset:512
	ds_read_b32 v228, v118 offset:1024
	ds_read_b32 v229, v118 offset:1536
	ds_read_b32 v230, v118 offset:2048
	ds_read_b32 v231, v118 offset:2560
	ds_read_b32 v232, v118 offset:3072
	ds_read_b32 v233, v118 offset:3584
	s_waitcnt lgkmcnt(0)
	v_bfe_u32 v120, v226, 16, 1
	v_bfe_u32 v121, v227, 16, 1
	v_bfe_u32 v122, v228, 16, 1
	v_bfe_u32 v123, v229, 16, 1
	v_bfe_u32 v124, v230, 16, 1
	v_bfe_u32 v125, v231, 16, 1
	v_bfe_u32 v126, v232, 16, 1
	v_bfe_u32 v127, v233, 16, 1
	v_add3_u32 v226, v226, v120, s63
	v_add3_u32 v227, v227, v121, s63
	v_add3_u32 v228, v228, v122, s63
	v_add3_u32 v229, v229, v123, s63
	v_add3_u32 v230, v230, v124, s63
	v_add3_u32 v231, v231, v125, s63
	v_add3_u32 v232, v232, v126, s63
	v_add3_u32 v233, v233, v127, s63
	v_perm_b32 v242, v227, v226, s64
	v_perm_b32 v243, v229, v228, s64
	v_perm_b32 v244, v231, v230, s64
	v_perm_b32 v245, v233, v232, s64
	s_nop 0
	global_store_dwordx4 v86, v[242:245], s[6:7]
	s_waitcnt vmcnt(16)
	v_mul_f32_e32 v176, v58, v176
	v_mul_f32_e32 v177, v58, v177
	v_mul_f32_e32 v178, v58, v178
	v_mul_f32_e32 v179, v58, v179
	ds_write_b128 v210, v[176:179]
	v_mul_f32_e32 v180, v59, v180
	v_mul_f32_e32 v181, v59, v181
	v_mul_f32_e32 v182, v59, v182
	v_mul_f32_e32 v183, v59, v183
	ds_write_b128 v210, v[180:183] offset:1024
	v_mul_f32_e32 v184, v60, v184
	v_mul_f32_e32 v185, v60, v185
	v_mul_f32_e32 v186, v60, v186
	v_mul_f32_e32 v187, v60, v187
	ds_write_b128 v210, v[184:187] offset:2048
	v_mul_f32_e32 v188, v61, v188
	v_mul_f32_e32 v189, v61, v189
	v_mul_f32_e32 v190, v61, v190
	v_mul_f32_e32 v191, v61, v191
	ds_write_b128 v210, v[188:191] offset:3072
	v_mul_f32_e32 v192, v62, v192
	v_mul_f32_e32 v193, v62, v193
	v_mul_f32_e32 v194, v62, v194
	v_mul_f32_e32 v195, v62, v195
	ds_write_b128 v210, v[192:195] offset:4096
	v_mul_f32_e32 v196, v63, v196
	v_mul_f32_e32 v197, v63, v197
	v_mul_f32_e32 v198, v63, v198
	v_mul_f32_e32 v199, v63, v199
	ds_write_b128 v210, v[196:199] offset:5120
	v_mul_f32_e32 v200, v64, v200
	v_mul_f32_e32 v201, v64, v201
	v_mul_f32_e32 v202, v64, v202
	v_mul_f32_e32 v203, v64, v203
	ds_write_b128 v210, v[200:203] offset:6144
	v_mul_f32_e32 v204, v65, v204
	v_mul_f32_e32 v205, v65, v205
	v_mul_f32_e32 v206, v65, v206
	v_mul_f32_e32 v207, v65, v207
	ds_write_b128 v210, v[204:207] offset:7168
	s_waitcnt lgkmcnt(0)
	s_barrier
; #define GAS __attribute__((address_space(1)))
; #define LAS __attribute__((address_space(3)))
; #define LDS_WAIT() asm volatile("s_waitcnt lgkmcnt(0)" ::: "memory")
; __device__ __forceinline__ unsigned pk2(float lo, float hi) { return f2bf(lo) | (f2bf(hi) << 16); }
; __device__ __forceinline__ int nat_dim(int p) { return (p >> 1) + 64 * (p & 1); }
; template <int MAP, bool KS, bool KPERM = false>
; __device__ __forceinline__ void p0_transpose_item(const float* W, int K, int Nsrc, int nblk, bf16* WT, const float* ksA, const float* ksB, int ksplit, LAS float* scr, int item, int lane) {
;     const int kb = item / nblk, nb = item % nblk, k0 = 64 * kb, n0 = 32 * nb;
;     const int nr = n0 + (lane & 31); const int sc = MAP == 1 ? src_col_in(nr) : (MAP == 2 ? nat_dim(nr) : nr);
;     float v[32];
; #pragma unroll
;     for (int i = 0; i < 32; ++i) { const int k = k0 + 2 * i + (lane >> 5); const int ksrc = KPERM ? ((k & ~127) + nat_dim(k & 127)) : k;
;         v[i] = sc >= 0 ? W[(size_t)ksrc * Nsrc + sc] : 0.f; }
; #pragma unroll
;     for (int i = 0; i < 32; ++i) { const int kk = 2 * i + (lane >> 5); const int k = k0 + kk;
;         if (KS) v[i] *= (k < ksplit ? ksA[k] : ksB[k - ksplit]);
;         scr[kk * 33 + (lane & 31)] = v[i]; }
;     LDS_WAIT(); asm volatile("" ::: "memory");
;     const int c = lane & 7;
; #pragma unroll
;     for (int j = 0; j < 4; ++j) { const int n = (lane >> 3) + 8 * j; const LAS float* s = scr + (8 * c) * 33 + n;
;         v4u o; o.x = pk2(s[0 * 33], s[1 * 33]); o.y = pk2(s[2 * 33], s[3 * 33]); o.z = pk2(s[4 * 33], s[5 * 33]); o.w = pk2(s[6 * 33], s[7 * 33]);
;         *(GAS v4u*)(WT + (size_t)(n0 + n) * K + k0 + 8 * c) = o; }
	s_add_u32 s8, s58, 0x1000
	s_addc_u32 s9, s59, 0
	global_load_dwordx4 v[176:179], v75, s[8:9]
	s_add_u32 s8, s8, 0x8000
	s_addc_u32 s9, s9, 0
	global_load_dwordx4 v[180:183], v75, s[8:9]
	s_add_u32 s8, s8, 0x8000
	s_addc_u32 s9, s9, 0
	global_load_dwordx4 v[184:187], v75, s[8:9]
	s_add_u32 s8, s8, 0x8000
	s_addc_u32 s9, s9, 0
	global_load_dwordx4 v[188:191], v75, s[8:9]
	s_add_u32 s8, s8, 0x8000
	s_addc_u32 s9, s9, 0
	global_load_dwordx4 v[192:195], v75, s[8:9]
	s_add_u32 s8, s8, 0x8000
	s_addc_u32 s9, s9, 0
	global_load_dwordx4 v[196:199], v75, s[8:9]
	s_add_u32 s8, s8, 0x8000
	s_addc_u32 s9, s9, 0
	global_load_dwordx4 v[200:203], v75, s[8:9]
	s_add_u32 s8, s8, 0x8000
	s_addc_u32 s9, s9, 0
	global_load_dwordx4 v[204:207], v75, s[8:9]
	s_add_u32 s6, s56, 0x1800000
	s_addc_u32 s7, s57, 0
	ds_read_b32 v226, v113
	ds_read_b32 v227, v113 offset:512
	ds_read_b32 v228, v113 offset:1024
	ds_read_b32 v229, v113 offset:1536
	ds_read_b32 v230, v113 offset:2048
	ds_read_b32 v231, v113 offset:2560
	ds_read_b32 v232, v113 offset:3072
	ds_read_b32 v233, v113 offset:3584
	s_waitcnt lgkmcnt(0)
	v_bfe_u32 v120, v226, 16, 1
	v_bfe_u32 v121, v227, 16, 1
	v_bfe_u32 v122, v228, 16, 1
	v_bfe_u32 v123, v229, 16, 1
	v_bfe_u32 v124, v230, 16, 1
	v_bfe_u32 v125, v231, 16, 1
	v_bfe_u32 v126, v232, 16, 1
	v_bfe_u32 v127, v233, 16, 1
	v_add3_u32 v226, v226, v120, s63
	v_add3_u32 v227, v227, v121, s63
	v_add3_u32 v228, v228, v122, s63
	v_add3_u32 v229, v229, v123, s63
	v_add3_u32 v230, v230, v124, s63
	v_add3_u32 v231, v231, v125, s63
	v_add3_u32 v232, v232, v126, s63
	v_add3_u32 v233, v233, v127, s63
	v_perm_b32 v242, v227, v226, s64
	v_perm_b32 v243, v229, v228, s64
	v_perm_b32 v244, v231, v230, s64
	v_perm_b32 v245, v233, v232, s64
	s_nop 0
	global_store_dwordx4 v83, v[242:245], s[6:7]
	ds_read_b32 v226, v115
	ds_read_b32 v227, v115 offset:512
	ds_read_b32 v228, v115 offset:1024
	ds_read_b32 v229, v115 offset:1536
	ds_read_b32 v230, v115 offset:2048
	ds_read_b32 v231, v115 offset:2560
	ds_read_b32 v232, v115 offset:3072
	ds_read_b32 v233, v115 offset:3584
	s_waitcnt lgkmcnt(0)
	v_bfe_u32 v120, v226, 16, 1
	v_bfe_u32 v121, v227, 16, 1
	v_bfe_u32 v122, v228, 16, 1
	v_bfe_u32 v123, v229, 16, 1
	v_bfe_u32 v124, v230, 16, 1
	v_bfe_u32 v125, v231, 16, 1
	v_bfe_u32 v126, v232, 16, 1
	v_bfe_u32 v127, v233, 16, 1
	v_add3_u32 v226, v226, v120, s63
	v_add3_u32 v227, v227, v121, s63
	v_add3_u32 v228, v228, v122, s63
	v_add3_u32 v229, v229, v123, s63
	v_add3_u32 v230, v230, v124, s63
	v_add3_u32 v231, v231, v125, s63
	v_add3_u32 v232, v232, v126, s63
	v_add3_u32 v233, v233, v127, s63
	v_perm_b32 v242, v227, v226, s64
	v_perm_b32 v243, v229, v228, s64
	v_perm_b32 v244, v231, v230, s64
	v_perm_b32 v245, v233, v232, s64
	s_nop 0
	global_store_dwordx4 v84, v[242:245], s[6:7]
	ds_read_b32 v226, v117
	ds_read_b32 v227, v117 offset:512
	ds_read_b32 v228, v117 offset:1024
	ds_read_b32 v229, v117 offset:1536
	ds_read_b32 v230, v117 offset:2048
	ds_read_b32 v231, v117 offset:2560
	ds_read_b32 v232, v117 offset:3072
	ds_read_b32 v233, v117 offset:3584
	s_waitcnt lgkmcnt(0)
	v_bfe_u32 v120, v226, 16, 1
	v_bfe_u32 v121, v227, 16, 1
	v_bfe_u32 v122, v228, 16, 1
	v_bfe_u32 v123, v229, 16, 1
	v_bfe_u32 v124, v230, 16, 1
	v_bfe_u32 v125, v231, 16, 1
	v_bfe_u32 v126, v232, 16, 1
	v_bfe_u32 v127, v233, 16, 1
	v_add3_u32 v226, v226, v120, s63
	v_add3_u32 v227, v227, v121, s63
	v_add3_u32 v228, v228, v122, s63
	v_add3_u32 v229, v229, v123, s63
	v_add3_u32 v230, v230, v124, s63
	v_add3_u32 v231, v231, v125, s63
	v_add3_u32 v232, v232, v126, s63
	v_add3_u32 v233, v233, v127, s63
	v_perm_b32 v242, v227, v226, s64
	v_perm_b32 v243, v229, v228, s64
	v_perm_b32 v244, v231, v230, s64
	v_perm_b32 v245, v233, v232, s64
	s_nop 0
	global_store_dwordx4 v85, v[242:245], s[6:7]
	ds_read_b32 v226, v119
	ds_read_b32 v227, v119 offset:512
	ds_read_b32 v228, v119 offset:1024
	ds_read_b32 v229, v119 offset:1536
	ds_read_b32 v230, v119 offset:2048
	ds_read_b32 v231, v119 offset:2560
	ds_read_b32 v232, v119 offset:3072
	ds_read_b32 v233, v119 offset:3584
	s_waitcnt lgkmcnt(0)
	v_bfe_u32 v120, v226, 16, 1
	v_bfe_u32 v121, v227, 16, 1
	v_bfe_u32 v122, v228, 16, 1
	v_bfe_u32 v123, v229, 16, 1
	v_bfe_u32 v124, v230, 16, 1
	v_bfe_u32 v125, v231, 16, 1
	v_bfe_u32 v126, v232, 16, 1
	v_bfe_u32 v127, v233, 16, 1
	v_add3_u32 v226, v226, v120, s63
	v_add3_u32 v227, v227, v121, s63
	v_add3_u32 v228, v228, v122, s63
	v_add3_u32 v229, v229, v123, s63
	v_add3_u32 v230, v230, v124, s63
	v_add3_u32 v231, v231, v125, s63
	v_add3_u32 v232, v232, v126, s63
	v_add3_u32 v233, v233, v127, s63
	v_perm_b32 v242, v227, v226, s64
	v_perm_b32 v243, v229, v228, s64
	v_perm_b32 v244, v231, v230, s64
	v_perm_b32 v245, v233, v232, s64
	s_nop 0
	global_store_dwordx4 v86, v[242:245], s[6:7]
	s_waitcnt vmcnt(16)
	v_mul_f32_e32 v144, v66, v144
	v_mul_f32_e32 v145, v66, v145
	v_mul_f32_e32 v146, v66, v146
	v_mul_f32_e32 v147, v66, v147
	ds_write_b128 v209, v[144:147]
	v_mul_f32_e32 v148, v67, v148
	v_mul_f32_e32 v149, v67, v149
	v_mul_f32_e32 v150, v67, v150
	v_mul_f32_e32 v151, v67, v151
	ds_write_b128 v209, v[148:151] offset:1024
	v_mul_f32_e32 v152, v68, v152
	v_mul_f32_e32 v153, v68, v153
	v_mul_f32_e32 v154, v68, v154
	v_mul_f32_e32 v155, v68, v155
	ds_write_b128 v209, v[152:155] offset:2048
	v_mul_f32_e32 v156, v69, v156
	v_mul_f32_e32 v157, v69, v157
	v_mul_f32_e32 v158, v69, v158
	v_mul_f32_e32 v159, v69, v159
	ds_write_b128 v209, v[156:159] offset:3072
	v_mul_f32_e32 v160, v70, v160
	v_mul_f32_e32 v161, v70, v161
	v_mul_f32_e32 v162, v70, v162
	v_mul_f32_e32 v163, v70, v163
	ds_write_b128 v209, v[160:163] offset:4096
	v_mul_f32_e32 v164, v71, v164
	v_mul_f32_e32 v165, v71, v165
	v_mul_f32_e32 v166, v71, v166
	v_mul_f32_e32 v167, v71, v167
	ds_write_b128 v209, v[164:167] offset:5120
	v_mul_f32_e32 v168, v72, v168
	v_mul_f32_e32 v169, v72, v169
	v_mul_f32_e32 v170, v72, v170
	v_mul_f32_e32 v171, v72, v171
	ds_write_b128 v209, v[168:171] offset:6144
	v_mul_f32_e32 v172, v73, v172
	v_mul_f32_e32 v173, v73, v173
	v_mul_f32_e32 v174, v73, v174
	v_mul_f32_e32 v175, v73, v175
	ds_write_b128 v209, v[172:175] offset:7168
	s_waitcnt lgkmcnt(0)
	s_barrier
; #define GAS __attribute__((address_space(1)))
; #define LAS __attribute__((address_space(3)))
; #define LDS_WAIT() asm volatile("s_waitcnt lgkmcnt(0)" ::: "memory")
; __device__ __forceinline__ unsigned pk4_fp8(float a, float b, float c, float d) {
;     a = fminf(fmaxf(a, -448.f), 448.f); b = fminf(fmaxf(b, -448.f), 448.f); c = fminf(fmaxf(c, -448.f), 448.f); d = fminf(fmaxf(d, -448.f), 448.f);
;     int w = __builtin_amdgcn_cvt_pk_fp8_f32(a, b, 0, false); w = __builtin_amdgcn_cvt_pk_fp8_f32(c, d, w, true); return (unsigned)w; }
;     const int pr = item >> 1, kb = 2 * (pr / nblk) + (item & 1), nb = pr % nblk, k0 = 64 * kb, n0 = 32 * nb;
;     const int nr = n0 + (lane & 31); const int sc = MAP == 1 ? src_col_in(nr) : nr;
;     float v[32];
; #pragma unroll
;     for (int i = 0; i < 32; ++i) v[i] = sc >= 0 ? W[(size_t)(k0 + 2 * i + (lane >> 5)) * Nsrc + sc] : 0.f;
; #pragma unroll
;     for (int i = 0; i < 32; ++i) { const int k = k0 + 2 * i + (lane >> 5); float x = v[i] * wscale; if (KS) x *= (k < ksplit ? ksA[k] : ksB[k - ksplit]); scr[(2 * i + (lane >> 5)) * 33 + (lane & 31)] = x; }
;     LDS_WAIT(); asm volatile("" ::: "memory");
;     const int c = lane & 7;
; #pragma unroll
;     for (int j = 0; j < 4; ++j) { const int n = (lane >> 3) + 8 * j; const LAS float* s = scr + (8 * c) * 33 + n;
;         const unsigned long long o = (unsigned long long)pg8::pk4_fp8(s[0 * 33], s[1 * 33], s[2 * 33], s[3 * 33]) | ((unsigned long long)pg8::pk4_fp8(s[4 * 33], s[5 * 33], s[6 * 33], s[7 * 33]) << 32);
;         *(GAS unsigned long long*)(WT + (size_t)(n0 + n) * K + k0 + 8 * c) = o; }
;     LDS_WAIT(); asm volatile("" ::: "memory");
	s_add_u32 s8, s58, 0x2000
	s_addc_u32 s9, s59, 0
	global_load_dwordx4 v[144:147], v75, s[8:9]
	s_add_u32 s8, s8, 0x8000
	s_addc_u32 s9, s9, 0
	global_load_dwordx4 v[148:151], v75, s[8:9]
	s_add_u32 s8, s8, 0x8000
	s_addc_u32 s9, s9, 0
	global_load_dwordx4 v[152:155], v75, s[8:9]
	s_add_u32 s8, s8, 0x8000
	s_addc_u32 s9, s9, 0
	global_load_dwordx4 v[156:159], v75, s[8:9]
	s_add_u32 s8, s8, 0x8000
	s_addc_u32 s9, s9, 0
	global_load_dwordx4 v[160:163], v75, s[8:9]
	s_add_u32 s8, s8, 0x8000
	s_addc_u32 s9, s9, 0
	global_load_dwordx4 v[164:167], v75, s[8:9]
	s_add_u32 s8, s8, 0x8000
	s_addc_u32 s9, s9, 0
	global_load_dwordx4 v[168:171], v75, s[8:9]
	s_add_u32 s8, s8, 0x8000
	s_addc_u32 s9, s9, 0
	global_load_dwordx4 v[172:175], v75, s[8:9]
	s_mov_b64 s[6:7], s[60:61]
	ds_read_b32 v226, v211
	ds_read_b32 v227, v211 offset:512
	ds_read_b32 v228, v211 offset:1024
	ds_read_b32 v229, v211 offset:1536
	ds_read_b32 v230, v211 offset:2048
	ds_read_b32 v231, v211 offset:2560
	ds_read_b32 v232, v211 offset:3072
	ds_read_b32 v233, v211 offset:3584
	ds_read_b32 v234, v211 offset:4096
	ds_read_b32 v235, v211 offset:4608
	ds_read_b32 v236, v211 offset:5120
	ds_read_b32 v237, v211 offset:5632
	ds_read_b32 v238, v211 offset:6144
	ds_read_b32 v239, v211 offset:6656
	ds_read_b32 v240, v211 offset:7168
	ds_read_b32 v241, v211 offset:7680
	s_waitcnt lgkmcnt(0)
	v_max_f32_e32 v226, v226, v226
	v_max_f32_e32 v227, v227, v227
	v_max_f32_e32 v228, v228, v228
	v_max_f32_e32 v229, v229, v229
	v_max_f32_e32 v230, v230, v230
	v_max_f32_e32 v231, v231, v231
	v_max_f32_e32 v232, v232, v232
	v_max_f32_e32 v233, v233, v233
	v_max_f32_e32 v234, v234, v234
	v_max_f32_e32 v235, v235, v235
	v_max_f32_e32 v236, v236, v236
	v_max_f32_e32 v237, v237, v237
	v_max_f32_e32 v238, v238, v238
	v_max_f32_e32 v239, v239, v239
	v_max_f32_e32 v240, v240, v240
	v_max_f32_e32 v241, v241, v241
	v_med3_f32 v226, v226, s62, v95
	v_med3_f32 v227, v227, s62, v95
	v_med3_f32 v228, v228, s62, v95
	v_med3_f32 v229, v229, s62, v95
	v_med3_f32 v230, v230, s62, v95
	v_med3_f32 v231, v231, s62, v95
	v_med3_f32 v232, v232, s62, v95
	v_med3_f32 v233, v233, s62, v95
	v_med3_f32 v234, v234, s62, v95
	v_med3_f32 v235, v235, s62, v95
	v_med3_f32 v236, v236, s62, v95
	v_med3_f32 v237, v237, s62, v95
	v_med3_f32 v238, v238, s62, v95
	v_med3_f32 v239, v239, s62, v95
	v_med3_f32 v240, v240, s62, v95
	v_med3_f32 v241, v241, s62, v95
	v_mov_b32_e32 v242, 0
	v_mov_b32_e32 v243, 0
	v_mov_b32_e32 v244, 0
	v_mov_b32_e32 v245, 0
	v_cvt_pk_fp8_f32 v242, v226, v227
	v_cvt_pk_fp8_f32 v243, v230, v231
	v_cvt_pk_fp8_f32 v244, v234, v235
	v_cvt_pk_fp8_f32 v245, v238, v239
	v_cvt_pk_fp8_f32 v242, v228, v229 op_sel:[0,0,1]
	v_cvt_pk_fp8_f32 v243, v232, v233 op_sel:[0,0,1]
	v_cvt_pk_fp8_f32 v244, v236, v237 op_sel:[0,0,1]
	v_cvt_pk_fp8_f32 v245, v240, v241 op_sel:[0,0,1]
	s_nop 0
	global_store_dwordx4 v77, v[242:245], s[6:7]
	ds_read_b32 v226, v213
	ds_read_b32 v227, v213 offset:512
	ds_read_b32 v228, v213 offset:1024
	ds_read_b32 v229, v213 offset:1536
	ds_read_b32 v230, v213 offset:2048
	ds_read_b32 v231, v213 offset:2560
	ds_read_b32 v232, v213 offset:3072
	ds_read_b32 v233, v213 offset:3584
	ds_read_b32 v234, v213 offset:4096
	ds_read_b32 v235, v213 offset:4608
	ds_read_b32 v236, v213 offset:5120
	ds_read_b32 v237, v213 offset:5632
	ds_read_b32 v238, v213 offset:6144
	ds_read_b32 v239, v213 offset:6656
	ds_read_b32 v240, v213 offset:7168
	ds_read_b32 v241, v213 offset:7680
	s_waitcnt lgkmcnt(0)
	v_max_f32_e32 v226, v226, v226
	v_max_f32_e32 v227, v227, v227
	v_max_f32_e32 v228, v228, v228
	v_max_f32_e32 v229, v229, v229
	v_max_f32_e32 v230, v230, v230
	v_max_f32_e32 v231, v231, v231
	v_max_f32_e32 v232, v232, v232
	v_max_f32_e32 v233, v233, v233
	v_max_f32_e32 v234, v234, v234
	v_max_f32_e32 v235, v235, v235
	v_max_f32_e32 v236, v236, v236
	v_max_f32_e32 v237, v237, v237
	v_max_f32_e32 v238, v238, v238
	v_max_f32_e32 v239, v239, v239
	v_max_f32_e32 v240, v240, v240
	v_max_f32_e32 v241, v241, v241
	v_med3_f32 v226, v226, s62, v95
	v_med3_f32 v227, v227, s62, v95
	v_med3_f32 v228, v228, s62, v95
	v_med3_f32 v229, v229, s62, v95
	v_med3_f32 v230, v230, s62, v95
	v_med3_f32 v231, v231, s62, v95
	v_med3_f32 v232, v232, s62, v95
	v_med3_f32 v233, v233, s62, v95
	v_med3_f32 v234, v234, s62, v95
	v_med3_f32 v235, v235, s62, v95
	v_med3_f32 v236, v236, s62, v95
	v_med3_f32 v237, v237, s62, v95
	v_med3_f32 v238, v238, s62, v95
	v_med3_f32 v239, v239, s62, v95
	v_med3_f32 v240, v240, s62, v95
	v_med3_f32 v241, v241, s62, v95
	v_mov_b32_e32 v242, 0
	v_mov_b32_e32 v243, 0
	v_mov_b32_e32 v244, 0
	v_mov_b32_e32 v245, 0
	v_cvt_pk_fp8_f32 v242, v226, v227
	v_cvt_pk_fp8_f32 v243, v230, v231
	v_cvt_pk_fp8_f32 v244, v234, v235
	v_cvt_pk_fp8_f32 v245, v238, v239
	v_cvt_pk_fp8_f32 v242, v228, v229 op_sel:[0,0,1]
	v_cvt_pk_fp8_f32 v243, v232, v233 op_sel:[0,0,1]
	v_cvt_pk_fp8_f32 v244, v236, v237 op_sel:[0,0,1]
	v_cvt_pk_fp8_f32 v245, v240, v241 op_sel:[0,0,1]
	s_nop 0
	global_store_dwordx4 v78, v[242:245], s[6:7]
	s_waitcnt vmcnt(14)
	v_mul_f32_e32 v176, v66, v176
	v_mul_f32_e32 v177, v66, v177
	v_mul_f32_e32 v178, v66, v178
	v_mul_f32_e32 v179, v66, v179
	ds_write_b128 v210, v[176:179]
	v_mul_f32_e32 v180, v67, v180
	v_mul_f32_e32 v181, v67, v181
	v_mul_f32_e32 v182, v67, v182
	v_mul_f32_e32 v183, v67, v183
	ds_write_b128 v210, v[180:183] offset:1024
	v_mul_f32_e32 v184, v68, v184
	v_mul_f32_e32 v185, v68, v185
	v_mul_f32_e32 v186, v68, v186
	v_mul_f32_e32 v187, v68, v187
	ds_write_b128 v210, v[184:187] offset:2048
	v_mul_f32_e32 v188, v69, v188
	v_mul_f32_e32 v189, v69, v189
	v_mul_f32_e32 v190, v69, v190
	v_mul_f32_e32 v191, v69, v191
	ds_write_b128 v210, v[188:191] offset:3072
	v_mul_f32_e32 v192, v70, v192
	v_mul_f32_e32 v193, v70, v193
	v_mul_f32_e32 v194, v70, v194
	v_mul_f32_e32 v195, v70, v195
	ds_write_b128 v210, v[192:195] offset:4096
	v_mul_f32_e32 v196, v71, v196
	v_mul_f32_e32 v197, v71, v197
	v_mul_f32_e32 v198, v71, v198
	v_mul_f32_e32 v199, v71, v199
	ds_write_b128 v210, v[196:199] offset:5120
	v_mul_f32_e32 v200, v72, v200
	v_mul_f32_e32 v201, v72, v201
	v_mul_f32_e32 v202, v72, v202
	v_mul_f32_e32 v203, v72, v203
	ds_write_b128 v210, v[200:203] offset:6144
	v_mul_f32_e32 v204, v73, v204
	v_mul_f32_e32 v205, v73, v205
	v_mul_f32_e32 v206, v73, v206
	v_mul_f32_e32 v207, v73, v207
	ds_write_b128 v210, v[204:207] offset:7168
	s_waitcnt lgkmcnt(0)
	s_barrier
; #define GAS __attribute__((address_space(1)))
; #define LAS __attribute__((address_space(3)))
; #define LDS_WAIT() asm volatile("s_waitcnt lgkmcnt(0)" ::: "memory")
; __device__ __forceinline__ unsigned pk4_fp8(float a, float b, float c, float d) {
;     a = fminf(fmaxf(a, -448.f), 448.f); b = fminf(fmaxf(b, -448.f), 448.f); c = fminf(fmaxf(c, -448.f), 448.f); d = fminf(fmaxf(d, -448.f), 448.f);
;     int w = __builtin_amdgcn_cvt_pk_fp8_f32(a, b, 0, false); w = __builtin_amdgcn_cvt_pk_fp8_f32(c, d, w, true); return (unsigned)w; }
;     const int pr = item >> 1, kb = 2 * (pr / nblk) + (item & 1), nb = pr % nblk, k0 = 64 * kb, n0 = 32 * nb;
;     const int nr = n0 + (lane & 31); const int sc = MAP == 1 ? src_col_in(nr) : nr;
;     float v[32];
; #pragma unroll
;     for (int i = 0; i < 32; ++i) v[i] = sc >= 0 ? W[(size_t)(k0 + 2 * i + (lane >> 5)) * Nsrc + sc] : 0.f;
; #pragma unroll
;     for (int i = 0; i < 32; ++i) { const int k = k0 + 2 * i + (lane >> 5); float x = v[i] * wscale; if (KS) x *= (k < ksplit ? ksA[k] : ksB[k - ksplit]); scr[(2 * i + (lane >> 5)) * 33 + (lane & 31)] = x; }
;     LDS_WAIT(); asm volatile("" ::: "memory");
;     const int c = lane & 7;
; #pragma unroll
;     for (int j = 0; j < 4; ++j) { const int n = (lane >> 3) + 8 * j; const LAS float* s = scr + (8 * c) * 33 + n;
;         const unsigned long long o = (unsigned long long)pg8::pk4_fp8(s[0 * 33], s[1 * 33], s[2 * 33], s[3 * 33]) | ((unsigned long long)pg8::pk4_fp8(s[4 * 33], s[5 * 33], s[6 * 33], s[7 * 33]) << 32);
;         *(GAS unsigned long long*)(WT + (size_t)(n0 + n) * K + k0 + 8 * c) = o; }
;     LDS_WAIT(); asm volatile("" ::: "memory");
	s_add_u32 s8, s58, 0x3000
	s_addc_u32 s9, s59, 0
	global_load_dwordx4 v[176:179], v75, s[8:9]
	s_add_u32 s8, s8, 0x8000
	s_addc_u32 s9, s9, 0
	global_load_dwordx4 v[180:183], v75, s[8:9]
	s_add_u32 s8, s8, 0x8000
	s_addc_u32 s9, s9, 0
	global_load_dwordx4 v[184:187], v75, s[8:9]
	s_add_u32 s8, s8, 0x8000
	s_addc_u32 s9, s9, 0
	global_load_dwordx4 v[188:191], v75, s[8:9]
	s_add_u32 s8, s8, 0x8000
	s_addc_u32 s9, s9, 0
	global_load_dwordx4 v[192:195], v75, s[8:9]
	s_add_u32 s8, s8, 0x8000
	s_addc_u32 s9, s9, 0
	global_load_dwordx4 v[196:199], v75, s[8:9]
	s_add_u32 s8, s8, 0x8000
	s_addc_u32 s9, s9, 0
	global_load_dwordx4 v[200:203], v75, s[8:9]
	s_add_u32 s8, s8, 0x8000
	s_addc_u32 s9, s9, 0
	global_load_dwordx4 v[204:207], v75, s[8:9]
	s_add_u32 s6, s60, 0x400000
	s_addc_u32 s7, s61, 0
	ds_read_b32 v226, v212
	ds_read_b32 v227, v212 offset:512
	ds_read_b32 v228, v212 offset:1024
	ds_read_b32 v229, v212 offset:1536
	ds_read_b32 v230, v212 offset:2048
	ds_read_b32 v231, v212 offset:2560
	ds_read_b32 v232, v212 offset:3072
	ds_read_b32 v233, v212 offset:3584
	ds_read_b32 v234, v212 offset:4096
	ds_read_b32 v235, v212 offset:4608
	ds_read_b32 v236, v212 offset:5120
	ds_read_b32 v237, v212 offset:5632
	ds_read_b32 v238, v212 offset:6144
	ds_read_b32 v239, v212 offset:6656
	ds_read_b32 v240, v212 offset:7168
	ds_read_b32 v241, v212 offset:7680
	s_waitcnt lgkmcnt(0)
	v_max_f32_e32 v226, v226, v226
	v_max_f32_e32 v227, v227, v227
	v_max_f32_e32 v228, v228, v228
	v_max_f32_e32 v229, v229, v229
	v_max_f32_e32 v230, v230, v230
	v_max_f32_e32 v231, v231, v231
	v_max_f32_e32 v232, v232, v232
	v_max_f32_e32 v233, v233, v233
	v_max_f32_e32 v234, v234, v234
	v_max_f32_e32 v235, v235, v235
	v_max_f32_e32 v236, v236, v236
	v_max_f32_e32 v237, v237, v237
	v_max_f32_e32 v238, v238, v238
	v_max_f32_e32 v239, v239, v239
	v_max_f32_e32 v240, v240, v240
	v_max_f32_e32 v241, v241, v241
	v_med3_f32 v226, v226, s62, v95
	v_med3_f32 v227, v227, s62, v95
	v_med3_f32 v228, v228, s62, v95
	v_med3_f32 v229, v229, s62, v95
	v_med3_f32 v230, v230, s62, v95
	v_med3_f32 v231, v231, s62, v95
	v_med3_f32 v232, v232, s62, v95
	v_med3_f32 v233, v233, s62, v95
	v_med3_f32 v234, v234, s62, v95
	v_med3_f32 v235, v235, s62, v95
	v_med3_f32 v236, v236, s62, v95
	v_med3_f32 v237, v237, s62, v95
	v_med3_f32 v238, v238, s62, v95
	v_med3_f32 v239, v239, s62, v95
	v_med3_f32 v240, v240, s62, v95
	v_med3_f32 v241, v241, s62, v95
	v_mov_b32_e32 v242, 0
	v_mov_b32_e32 v243, 0
	v_mov_b32_e32 v244, 0
	v_mov_b32_e32 v245, 0
	v_cvt_pk_fp8_f32 v242, v226, v227
	v_cvt_pk_fp8_f32 v243, v230, v231
	v_cvt_pk_fp8_f32 v244, v234, v235
	v_cvt_pk_fp8_f32 v245, v238, v239
	v_cvt_pk_fp8_f32 v242, v228, v229 op_sel:[0,0,1]
	v_cvt_pk_fp8_f32 v243, v232, v233 op_sel:[0,0,1]
	v_cvt_pk_fp8_f32 v244, v236, v237 op_sel:[0,0,1]
	v_cvt_pk_fp8_f32 v245, v240, v241 op_sel:[0,0,1]
	s_nop 0
	global_store_dwordx4 v77, v[242:245], s[6:7]
	ds_read_b32 v226, v214
	ds_read_b32 v227, v214 offset:512
	ds_read_b32 v228, v214 offset:1024
	ds_read_b32 v229, v214 offset:1536
	ds_read_b32 v230, v214 offset:2048
	ds_read_b32 v231, v214 offset:2560
	ds_read_b32 v232, v214 offset:3072
	ds_read_b32 v233, v214 offset:3584
	ds_read_b32 v234, v214 offset:4096
	ds_read_b32 v235, v214 offset:4608
	ds_read_b32 v236, v214 offset:5120
	ds_read_b32 v237, v214 offset:5632
	ds_read_b32 v238, v214 offset:6144
	ds_read_b32 v239, v214 offset:6656
	ds_read_b32 v240, v214 offset:7168
	ds_read_b32 v241, v214 offset:7680
	s_waitcnt lgkmcnt(0)
	v_max_f32_e32 v226, v226, v226
	v_max_f32_e32 v227, v227, v227
	v_max_f32_e32 v228, v228, v228
	v_max_f32_e32 v229, v229, v229
	v_max_f32_e32 v230, v230, v230
	v_max_f32_e32 v231, v231, v231
	v_max_f32_e32 v232, v232, v232
	v_max_f32_e32 v233, v233, v233
	v_max_f32_e32 v234, v234, v234
	v_max_f32_e32 v235, v235, v235
	v_max_f32_e32 v236, v236, v236
	v_max_f32_e32 v237, v237, v237
	v_max_f32_e32 v238, v238, v238
	v_max_f32_e32 v239, v239, v239
	v_max_f32_e32 v240, v240, v240
	v_max_f32_e32 v241, v241, v241
	v_med3_f32 v226, v226, s62, v95
	v_med3_f32 v227, v227, s62, v95
	v_med3_f32 v228, v228, s62, v95
	v_med3_f32 v229, v229, s62, v95
	v_med3_f32 v230, v230, s62, v95
	v_med3_f32 v231, v231, s62, v95
	v_med3_f32 v232, v232, s62, v95
	v_med3_f32 v233, v233, s62, v95
	v_med3_f32 v234, v234, s62, v95
	v_med3_f32 v235, v235, s62, v95
	v_med3_f32 v236, v236, s62, v95
	v_med3_f32 v237, v237, s62, v95
	v_med3_f32 v238, v238, s62, v95
	v_med3_f32 v239, v239, s62, v95
	v_med3_f32 v240, v240, s62, v95
	v_med3_f32 v241, v241, s62, v95
	v_mov_b32_e32 v242, 0
	v_mov_b32_e32 v243, 0
	v_mov_b32_e32 v244, 0
	v_mov_b32_e32 v245, 0
	v_cvt_pk_fp8_f32 v242, v226, v227
	v_cvt_pk_fp8_f32 v243, v230, v231
	v_cvt_pk_fp8_f32 v244, v234, v235
	v_cvt_pk_fp8_f32 v245, v238, v239
	v_cvt_pk_fp8_f32 v242, v228, v229 op_sel:[0,0,1]
	v_cvt_pk_fp8_f32 v243, v232, v233 op_sel:[0,0,1]
	v_cvt_pk_fp8_f32 v244, v236, v237 op_sel:[0,0,1]
	v_cvt_pk_fp8_f32 v245, v240, v241 op_sel:[0,0,1]
	s_nop 0
	global_store_dwordx4 v78, v[242:245], s[6:7]
	s_waitcnt vmcnt(12)
	v_mul_f32_e32 v144, v66, v144
	v_mul_f32_e32 v145, v66, v145
	v_mul_f32_e32 v146, v66, v146
	v_mul_f32_e32 v147, v66, v147
	ds_write_b128 v209, v[144:147]
	v_mul_f32_e32 v148, v67, v148
	v_mul_f32_e32 v149, v67, v149
	v_mul_f32_e32 v150, v67, v150
	v_mul_f32_e32 v151, v67, v151
	ds_write_b128 v209, v[148:151] offset:1024
	v_mul_f32_e32 v152, v68, v152
	v_mul_f32_e32 v153, v68, v153
	v_mul_f32_e32 v154, v68, v154
	v_mul_f32_e32 v155, v68, v155
	ds_write_b128 v209, v[152:155] offset:2048
	v_mul_f32_e32 v156, v69, v156
	v_mul_f32_e32 v157, v69, v157
	v_mul_f32_e32 v158, v69, v158
	v_mul_f32_e32 v159, v69, v159
	ds_write_b128 v209, v[156:159] offset:3072
	v_mul_f32_e32 v160, v70, v160
	v_mul_f32_e32 v161, v70, v161
	v_mul_f32_e32 v162, v70, v162
	v_mul_f32_e32 v163, v70, v163
	ds_write_b128 v209, v[160:163] offset:4096
	v_mul_f32_e32 v164, v71, v164
	v_mul_f32_e32 v165, v71, v165
	v_mul_f32_e32 v166, v71, v166
	v_mul_f32_e32 v167, v71, v167
	ds_write_b128 v209, v[164:167] offset:5120
	v_mul_f32_e32 v168, v72, v168
	v_mul_f32_e32 v169, v72, v169
	v_mul_f32_e32 v170, v72, v170
	v_mul_f32_e32 v171, v72, v171
	ds_write_b128 v209, v[168:171] offset:6144
	v_mul_f32_e32 v172, v73, v172
	v_mul_f32_e32 v173, v73, v173
	v_mul_f32_e32 v174, v73, v174
	v_mul_f32_e32 v175, v73, v175
	ds_write_b128 v209, v[172:175] offset:7168
	s_waitcnt lgkmcnt(0)
	s_barrier
; #define GAS __attribute__((address_space(1)))
; #define LAS __attribute__((address_space(3)))
; #define LDS_WAIT() asm volatile("s_waitcnt lgkmcnt(0)" ::: "memory")
; __device__ __forceinline__ unsigned pk4_fp8(float a, float b, float c, float d) {
;     a = fminf(fmaxf(a, -448.f), 448.f); b = fminf(fmaxf(b, -448.f), 448.f); c = fminf(fmaxf(c, -448.f), 448.f); d = fminf(fmaxf(d, -448.f), 448.f);
;     int w = __builtin_amdgcn_cvt_pk_fp8_f32(a, b, 0, false); w = __builtin_amdgcn_cvt_pk_fp8_f32(c, d, w, true); return (unsigned)w; }
;     const int pr = item >> 1, kb = 2 * (pr / nblk) + (item & 1), nb = pr % nblk, k0 = 64 * kb, n0 = 32 * nb;
;     const int nr = n0 + (lane & 31); const int sc = MAP == 1 ? src_col_in(nr) : nr;
;     float v[32];
; #pragma unroll
;     for (int i = 0; i < 32; ++i) v[i] = sc >= 0 ? W[(size_t)(k0 + 2 * i + (lane >> 5)) * Nsrc + sc] : 0.f;
; #pragma unroll
;     for (int i = 0; i < 32; ++i) { const int k = k0 + 2 * i + (lane >> 5); float x = v[i] * wscale; if (KS) x *= (k < ksplit ? ksA[k] : ksB[k - ksplit]); scr[(2 * i + (lane >> 5)) * 33 + (lane & 31)] = x; }
;     LDS_WAIT(); asm volatile("" ::: "memory");
;     const int c = lane & 7;
; #pragma unroll
;     for (int j = 0; j < 4; ++j) { const int n = (lane >> 3) + 8 * j; const LAS float* s = scr + (8 * c) * 33 + n;
;         const unsigned long long o = (unsigned long long)pg8::pk4_fp8(s[0 * 33], s[1 * 33], s[2 * 33], s[3 * 33]) | ((unsigned long long)pg8::pk4_fp8(s[4 * 33], s[5 * 33], s[6 * 33], s[7 * 33]) << 32);
;         *(GAS unsigned long long*)(WT + (size_t)(n0 + n) * K + k0 + 8 * c) = o; }
;     LDS_WAIT(); asm volatile("" ::: "memory");
	s_add_u32 s6, s60, 0x800000
	s_addc_u32 s7, s61, 0
	ds_read_b32 v226, v211
	ds_read_b32 v227, v211 offset:512
	ds_read_b32 v228, v211 offset:1024
	ds_read_b32 v229, v211 offset:1536
	ds_read_b32 v230, v211 offset:2048
	ds_read_b32 v231, v211 offset:2560
	ds_read_b32 v232, v211 offset:3072
	ds_read_b32 v233, v211 offset:3584
	ds_read_b32 v234, v211 offset:4096
	ds_read_b32 v235, v211 offset:4608
	ds_read_b32 v236, v211 offset:5120
	ds_read_b32 v237, v211 offset:5632
	ds_read_b32 v238, v211 offset:6144
	ds_read_b32 v239, v211 offset:6656
	ds_read_b32 v240, v211 offset:7168
	ds_read_b32 v241, v211 offset:7680
	s_waitcnt lgkmcnt(0)
	v_max_f32_e32 v226, v226, v226
	v_max_f32_e32 v227, v227, v227
	v_max_f32_e32 v228, v228, v228
	v_max_f32_e32 v229, v229, v229
	v_max_f32_e32 v230, v230, v230
	v_max_f32_e32 v231, v231, v231
	v_max_f32_e32 v232, v232, v232
	v_max_f32_e32 v233, v233, v233
	v_max_f32_e32 v234, v234, v234
	v_max_f32_e32 v235, v235, v235
	v_max_f32_e32 v236, v236, v236
	v_max_f32_e32 v237, v237, v237
	v_max_f32_e32 v238, v238, v238
	v_max_f32_e32 v239, v239, v239
	v_max_f32_e32 v240, v240, v240
	v_max_f32_e32 v241, v241, v241
	v_med3_f32 v226, v226, s62, v95
	v_med3_f32 v227, v227, s62, v95
	v_med3_f32 v228, v228, s62, v95
	v_med3_f32 v229, v229, s62, v95
	v_med3_f32 v230, v230, s62, v95
	v_med3_f32 v231, v231, s62, v95
	v_med3_f32 v232, v232, s62, v95
	v_med3_f32 v233, v233, s62, v95
	v_med3_f32 v234, v234, s62, v95
	v_med3_f32 v235, v235, s62, v95
	v_med3_f32 v236, v236, s62, v95
	v_med3_f32 v237, v237, s62, v95
	v_med3_f32 v238, v238, s62, v95
	v_med3_f32 v239, v239, s62, v95
	v_med3_f32 v240, v240, s62, v95
	v_med3_f32 v241, v241, s62, v95
	v_mov_b32_e32 v242, 0
	v_mov_b32_e32 v243, 0
	v_mov_b32_e32 v244, 0
	v_mov_b32_e32 v245, 0
	v_cvt_pk_fp8_f32 v242, v226, v227
	v_cvt_pk_fp8_f32 v243, v230, v231
	v_cvt_pk_fp8_f32 v244, v234, v235
	v_cvt_pk_fp8_f32 v245, v238, v239
	v_cvt_pk_fp8_f32 v242, v228, v229 op_sel:[0,0,1]
	v_cvt_pk_fp8_f32 v243, v232, v233 op_sel:[0,0,1]
	v_cvt_pk_fp8_f32 v244, v236, v237 op_sel:[0,0,1]
	v_cvt_pk_fp8_f32 v245, v240, v241 op_sel:[0,0,1]
	s_nop 0
	global_store_dwordx4 v77, v[242:245], s[6:7]
	ds_read_b32 v226, v213
	ds_read_b32 v227, v213 offset:512
	ds_read_b32 v228, v213 offset:1024
	ds_read_b32 v229, v213 offset:1536
	ds_read_b32 v230, v213 offset:2048
	ds_read_b32 v231, v213 offset:2560
	ds_read_b32 v232, v213 offset:3072
	ds_read_b32 v233, v213 offset:3584
	ds_read_b32 v234, v213 offset:4096
	ds_read_b32 v235, v213 offset:4608
	ds_read_b32 v236, v213 offset:5120
	ds_read_b32 v237, v213 offset:5632
	ds_read_b32 v238, v213 offset:6144
	ds_read_b32 v239, v213 offset:6656
	ds_read_b32 v240, v213 offset:7168
	ds_read_b32 v241, v213 offset:7680
	s_waitcnt lgkmcnt(0)
	v_max_f32_e32 v226, v226, v226
	v_max_f32_e32 v227, v227, v227
	v_max_f32_e32 v228, v228, v228
	v_max_f32_e32 v229, v229, v229
	v_max_f32_e32 v230, v230, v230
	v_max_f32_e32 v231, v231, v231
	v_max_f32_e32 v232, v232, v232
	v_max_f32_e32 v233, v233, v233
	v_max_f32_e32 v234, v234, v234
	v_max_f32_e32 v235, v235, v235
	v_max_f32_e32 v236, v236, v236
	v_max_f32_e32 v237, v237, v237
	v_max_f32_e32 v238, v238, v238
	v_max_f32_e32 v239, v239, v239
	v_max_f32_e32 v240, v240, v240
	v_max_f32_e32 v241, v241, v241
	v_med3_f32 v226, v226, s62, v95
	v_med3_f32 v227, v227, s62, v95
	v_med3_f32 v228, v228, s62, v95
	v_med3_f32 v229, v229, s62, v95
	v_med3_f32 v230, v230, s62, v95
	v_med3_f32 v231, v231, s62, v95
	v_med3_f32 v232, v232, s62, v95
	v_med3_f32 v233, v233, s62, v95
	v_med3_f32 v234, v234, s62, v95
	v_med3_f32 v235, v235, s62, v95
	v_med3_f32 v236, v236, s62, v95
	v_med3_f32 v237, v237, s62, v95
	v_med3_f32 v238, v238, s62, v95
	v_med3_f32 v239, v239, s62, v95
	v_med3_f32 v240, v240, s62, v95
	v_med3_f32 v241, v241, s62, v95
	v_mov_b32_e32 v242, 0
	v_mov_b32_e32 v243, 0
	v_mov_b32_e32 v244, 0
	v_mov_b32_e32 v245, 0
	v_cvt_pk_fp8_f32 v242, v226, v227
	v_cvt_pk_fp8_f32 v243, v230, v231
	v_cvt_pk_fp8_f32 v244, v234, v235
	v_cvt_pk_fp8_f32 v245, v238, v239
	v_cvt_pk_fp8_f32 v242, v228, v229 op_sel:[0,0,1]
	v_cvt_pk_fp8_f32 v243, v232, v233 op_sel:[0,0,1]
	v_cvt_pk_fp8_f32 v244, v236, v237 op_sel:[0,0,1]
	v_cvt_pk_fp8_f32 v245, v240, v241 op_sel:[0,0,1]
	s_nop 0
	global_store_dwordx4 v78, v[242:245], s[6:7]
	s_waitcnt vmcnt(4)
	v_mul_f32_e32 v176, v66, v176
	v_mul_f32_e32 v177, v66, v177
	v_mul_f32_e32 v178, v66, v178
	v_mul_f32_e32 v179, v66, v179
	ds_write_b128 v210, v[176:179]
	v_mul_f32_e32 v180, v67, v180
	v_mul_f32_e32 v181, v67, v181
	v_mul_f32_e32 v182, v67, v182
	v_mul_f32_e32 v183, v67, v183
	ds_write_b128 v210, v[180:183] offset:1024
	v_mul_f32_e32 v184, v68, v184
	v_mul_f32_e32 v185, v68, v185
	v_mul_f32_e32 v186, v68, v186
	v_mul_f32_e32 v187, v68, v187
	ds_write_b128 v210, v[184:187] offset:2048
	v_mul_f32_e32 v188, v69, v188
	v_mul_f32_e32 v189, v69, v189
	v_mul_f32_e32 v190, v69, v190
	v_mul_f32_e32 v191, v69, v191
	ds_write_b128 v210, v[188:191] offset:3072
	v_mul_f32_e32 v192, v70, v192
	v_mul_f32_e32 v193, v70, v193
	v_mul_f32_e32 v194, v70, v194
	v_mul_f32_e32 v195, v70, v195
	ds_write_b128 v210, v[192:195] offset:4096
	v_mul_f32_e32 v196, v71, v196
	v_mul_f32_e32 v197, v71, v197
	v_mul_f32_e32 v198, v71, v198
	v_mul_f32_e32 v199, v71, v199
	ds_write_b128 v210, v[196:199] offset:5120
	v_mul_f32_e32 v200, v72, v200
	v_mul_f32_e32 v201, v72, v201
	v_mul_f32_e32 v202, v72, v202
	v_mul_f32_e32 v203, v72, v203
	ds_write_b128 v210, v[200:203] offset:6144
	v_mul_f32_e32 v204, v73, v204
	v_mul_f32_e32 v205, v73, v205
	v_mul_f32_e32 v206, v73, v206
	v_mul_f32_e32 v207, v73, v207
	ds_write_b128 v210, v[204:207] offset:7168
	s_waitcnt lgkmcnt(0)
	s_barrier
; #define GAS __attribute__((address_space(1)))
; #define LAS __attribute__((address_space(3)))
; #define LDS_WAIT() asm volatile("s_waitcnt lgkmcnt(0)" ::: "memory")
; __device__ __forceinline__ unsigned pk4_fp8(float a, float b, float c, float d) {
;     a = fminf(fmaxf(a, -448.f), 448.f); b = fminf(fmaxf(b, -448.f), 448.f); c = fminf(fmaxf(c, -448.f), 448.f); d = fminf(fmaxf(d, -448.f), 448.f);
;     int w = __builtin_amdgcn_cvt_pk_fp8_f32(a, b, 0, false); w = __builtin_amdgcn_cvt_pk_fp8_f32(c, d, w, true); return (unsigned)w; }
;     const int pr = item >> 1, kb = 2 * (pr / nblk) + (item & 1), nb = pr % nblk, k0 = 64 * kb, n0 = 32 * nb;
;     const int nr = n0 + (lane & 31); const int sc = MAP == 1 ? src_col_in(nr) : nr;
;     float v[32];
; #pragma unroll
;     for (int i = 0; i < 32; ++i) v[i] = sc >= 0 ? W[(size_t)(k0 + 2 * i + (lane >> 5)) * Nsrc + sc] : 0.f;
; #pragma unroll
;     for (int i = 0; i < 32; ++i) { const int k = k0 + 2 * i + (lane >> 5); float x = v[i] * wscale; if (KS) x *= (k < ksplit ? ksA[k] : ksB[k - ksplit]); scr[(2 * i + (lane >> 5)) * 33 + (lane & 31)] = x; }
;     LDS_WAIT(); asm volatile("" ::: "memory");
;     const int c = lane & 7;
; #pragma unroll
;     for (int j = 0; j < 4; ++j) { const int n = (lane >> 3) + 8 * j; const LAS float* s = scr + (8 * c) * 33 + n;
;         const unsigned long long o = (unsigned long long)pg8::pk4_fp8(s[0 * 33], s[1 * 33], s[2 * 33], s[3 * 33]) | ((unsigned long long)pg8::pk4_fp8(s[4 * 33], s[5 * 33], s[6 * 33], s[7 * 33]) << 32);
;         *(GAS unsigned long long*)(WT + (size_t)(n0 + n) * K + k0 + 8 * c) = o; }
;     LDS_WAIT(); asm volatile("" ::: "memory");
	s_add_u32 s6, s60, 0xc00000
	s_addc_u32 s7, s61, 0
	ds_read_b32 v226, v212
	ds_read_b32 v227, v212 offset:512
	ds_read_b32 v228, v212 offset:1024
	ds_read_b32 v229, v212 offset:1536
	ds_read_b32 v230, v212 offset:2048
	ds_read_b32 v231, v212 offset:2560
	ds_read_b32 v232, v212 offset:3072
	ds_read_b32 v233, v212 offset:3584
	ds_read_b32 v234, v212 offset:4096
	ds_read_b32 v235, v212 offset:4608
	ds_read_b32 v236, v212 offset:5120
	ds_read_b32 v237, v212 offset:5632
	ds_read_b32 v238, v212 offset:6144
	ds_read_b32 v239, v212 offset:6656
	ds_read_b32 v240, v212 offset:7168
	ds_read_b32 v241, v212 offset:7680
	s_waitcnt lgkmcnt(0)
	v_max_f32_e32 v226, v226, v226
	v_max_f32_e32 v227, v227, v227
	v_max_f32_e32 v228, v228, v228
	v_max_f32_e32 v229, v229, v229
	v_max_f32_e32 v230, v230, v230
	v_max_f32_e32 v231, v231, v231
	v_max_f32_e32 v232, v232, v232
	v_max_f32_e32 v233, v233, v233
	v_max_f32_e32 v234, v234, v234
	v_max_f32_e32 v235, v235, v235
	v_max_f32_e32 v236, v236, v236
	v_max_f32_e32 v237, v237, v237
	v_max_f32_e32 v238, v238, v238
	v_max_f32_e32 v239, v239, v239
	v_max_f32_e32 v240, v240, v240
	v_max_f32_e32 v241, v241, v241
	v_med3_f32 v226, v226, s62, v95
	v_med3_f32 v227, v227, s62, v95
	v_med3_f32 v228, v228, s62, v95
	v_med3_f32 v229, v229, s62, v95
	v_med3_f32 v230, v230, s62, v95
	v_med3_f32 v231, v231, s62, v95
	v_med3_f32 v232, v232, s62, v95
	v_med3_f32 v233, v233, s62, v95
	v_med3_f32 v234, v234, s62, v95
	v_med3_f32 v235, v235, s62, v95
	v_med3_f32 v236, v236, s62, v95
	v_med3_f32 v237, v237, s62, v95
	v_med3_f32 v238, v238, s62, v95
	v_med3_f32 v239, v239, s62, v95
	v_med3_f32 v240, v240, s62, v95
	v_med3_f32 v241, v241, s62, v95
	v_mov_b32_e32 v242, 0
	v_mov_b32_e32 v243, 0
	v_mov_b32_e32 v244, 0
	v_mov_b32_e32 v245, 0
	v_cvt_pk_fp8_f32 v242, v226, v227
	v_cvt_pk_fp8_f32 v243, v230, v231
	v_cvt_pk_fp8_f32 v244, v234, v235
	v_cvt_pk_fp8_f32 v245, v238, v239
	v_cvt_pk_fp8_f32 v242, v228, v229 op_sel:[0,0,1]
	v_cvt_pk_fp8_f32 v243, v232, v233 op_sel:[0,0,1]
	v_cvt_pk_fp8_f32 v244, v236, v237 op_sel:[0,0,1]
	v_cvt_pk_fp8_f32 v245, v240, v241 op_sel:[0,0,1]
	s_nop 0
	global_store_dwordx4 v77, v[242:245], s[6:7]
	ds_read_b32 v226, v214
	ds_read_b32 v227, v214 offset:512
	ds_read_b32 v228, v214 offset:1024
	ds_read_b32 v229, v214 offset:1536
	ds_read_b32 v230, v214 offset:2048
	ds_read_b32 v231, v214 offset:2560
	ds_read_b32 v232, v214 offset:3072
	ds_read_b32 v233, v214 offset:3584
	ds_read_b32 v234, v214 offset:4096
	ds_read_b32 v235, v214 offset:4608
	ds_read_b32 v236, v214 offset:5120
	ds_read_b32 v237, v214 offset:5632
	ds_read_b32 v238, v214 offset:6144
	ds_read_b32 v239, v214 offset:6656
	ds_read_b32 v240, v214 offset:7168
	ds_read_b32 v241, v214 offset:7680
	s_waitcnt lgkmcnt(0)
	v_max_f32_e32 v226, v226, v226
	v_max_f32_e32 v227, v227, v227
	v_max_f32_e32 v228, v228, v228
	v_max_f32_e32 v229, v229, v229
	v_max_f32_e32 v230, v230, v230
	v_max_f32_e32 v231, v231, v231
	v_max_f32_e32 v232, v232, v232
	v_max_f32_e32 v233, v233, v233
	v_max_f32_e32 v234, v234, v234
	v_max_f32_e32 v235, v235, v235
	v_max_f32_e32 v236, v236, v236
	v_max_f32_e32 v237, v237, v237
	v_max_f32_e32 v238, v238, v238
	v_max_f32_e32 v239, v239, v239
	v_max_f32_e32 v240, v240, v240
	v_max_f32_e32 v241, v241, v241
	v_med3_f32 v226, v226, s62, v95
	v_med3_f32 v227, v227, s62, v95
	v_med3_f32 v228, v228, s62, v95
	v_med3_f32 v229, v229, s62, v95
	v_med3_f32 v230, v230, s62, v95
	v_med3_f32 v231, v231, s62, v95
	v_med3_f32 v232, v232, s62, v95
	v_med3_f32 v233, v233, s62, v95
	v_med3_f32 v234, v234, s62, v95
	v_med3_f32 v235, v235, s62, v95
	v_med3_f32 v236, v236, s62, v95
	v_med3_f32 v237, v237, s62, v95
	v_med3_f32 v238, v238, s62, v95
	v_med3_f32 v239, v239, s62, v95
	v_med3_f32 v240, v240, s62, v95
	v_med3_f32 v241, v241, s62, v95
	v_mov_b32_e32 v242, 0
	v_mov_b32_e32 v243, 0
	v_mov_b32_e32 v244, 0
	v_mov_b32_e32 v245, 0
	v_cvt_pk_fp8_f32 v242, v226, v227
	v_cvt_pk_fp8_f32 v243, v230, v231
	v_cvt_pk_fp8_f32 v244, v234, v235
	v_cvt_pk_fp8_f32 v245, v238, v239
	v_cvt_pk_fp8_f32 v242, v228, v229 op_sel:[0,0,1]
	v_cvt_pk_fp8_f32 v243, v232, v233 op_sel:[0,0,1]
	v_cvt_pk_fp8_f32 v244, v236, v237 op_sel:[0,0,1]
	v_cvt_pk_fp8_f32 v245, v240, v241 op_sel:[0,0,1]
	s_nop 0
	global_store_dwordx4 v78, v[242:245], s[6:7]
	s_waitcnt lgkmcnt(0)
	s_barrier
; __global__ void __launch_bounds__(NWAVES * 64, 2) hybrid_fwd(Args args) {
;     ...
;     for (int L = 0; L < DEPTH; ++L) {
;         { unsigned long long wz = 0; asm volatile("" : "+s"(wz)); ws = args.ws + wz; }
;         bf16* Hres = (bf16*)(ws + WS_H);     static_assert(DEPTH == 2 && WO_F8_FROM == 1 && PROJ_F8_FROM == 1, "the phase instantiations below are written for this precision plan");
;         bf16* XN = (bf16*)(ws + WS_XN); bf16* PROJ = (bf16*)(ws + WS_PROJ); bf16* ACT = (bf16*)(ws + WS_ACT); unsigned char* CAT = (unsigned char*)(ws + WS_CAT);     const bool wo_f8 = L >= WO_F8_FROM;
;         float* ATT = (float*)(ws + WS_ATT); bf16* XBC = (bf16*)(ws + WS_XBC); bf16* Y = (bf16*)(ws + WS_Y);
;         bf16* KC = (bf16*)(ws + WS_KC); bf16* VC = (bf16*)(ws + WS_VC); float* DT = (float*)(ws + WS_DT); float* ADT = (float*)(ws + WS_ADT);
;         float* COS = (float*)(ws + WS_COS); float* SIN = (float*)(ws + WS_SIN); unsigned* BMP = (unsigned*)(ws + WS_BMP);
;         bf16* AO = (bf16*)(ws + WS_ACT);     float* STT = (float*)(ws + WS_ST); bf16* PREVB = (bf16*)(ws + WS_PREV);     float* ACSG = (float*)(ws + WS_ACSG); float* DEC = (float*)(ws + WS_DEC);
;         {
;             const bool split = (L < PROJ_F8_FROM) && (F.G == 256);
;             if (L >= PROJ_F8_FROM) { pg8::StaticOrder So; So.init(S, NPROJ, F.G, (int)blockIdx.x); pg8::Gemm g{XN, (const bf16*)(ws + WS_WIN + L * SZ_WIN), S, NPROJ, DM / 2};
;                 pg8::EpiProj E{PROJ, NPROJ, COS, SIN, QSCALE, 1.f / (XN8_SCALE * WUP8_SCALE), 0};
;                 pg8::gemm_phase<pg8::EpiProj, pg8::StaticOrder, true, true, true>(F.lds + RING_OFF, g, So, E); }
	v_readlane_b32 s12, v253, 35
	v_readlane_b32 s18, v253, 41
	v_readlane_b32 s19, v253, 42
	s_add_u32 s81, s18, 0x1f600000
	s_addc_u32 s94, s19, 0
	s_add_u32 s24, s18, 0xf600000
	v_or_b32_e32 v2, 2, v6
	v_mov_b32_e32 v3, 0x630
	v_readlane_b32 s13, v253, 36
	v_readlane_b32 s14, v253, 37
	v_readlane_b32 s15, v253, 38
	s_addc_u32 s25, s19, 0
	v_mad_u32_u24 v58, v2, s0, v3
	v_mov_b32_e32 v3, 0xc60
	s_add_u32 s26, s18, 0xb600000
	v_mad_u32_u24 v59, v2, s0, v3
	v_readlane_b32 s0, v253, 19
	s_addc_u32 s27, s19, 0
	v_readlane_b32 s2, v253, 21
	v_readlane_b32 s10, v253, 29
	v_readlane_b32 s3, v253, 22
	v_readlane_b32 s11, v253, 30
	s_add_u32 s2, s10, 0x4000000
	v_readlane_b32 s40, v253, 3
	s_addc_u32 s3, s11, 0
	v_readlane_b32 s52, v253, 15
	v_readlane_b32 s53, v253, 16
	s_add_u32 s22, s52, 0x2000
	v_readlane_b32 s8, v253, 27
	s_addc_u32 s23, s53, 0
	v_readlane_b32 s9, v253, 28
	s_add_u32 s84, s8, 0x2000
	s_addc_u32 s85, s9, 0
	s_add_u32 s33, s18, 0x200000
	v_readlane_b32 s44, v253, 7
	s_addc_u32 s38, s19, 0
	v_mov_b32_e32 v9, v11
	v_readlane_b32 s1, v253, 20
	v_readlane_b32 s45, v253, 8
	s_add_u32 s86, s44, 0xb140000
	v_mul_u32_u24_e32 v57, 0x84, v2
	v_readlane_b32 s42, v253, 5
	v_lshl_add_u64 v[2:3], s[18:19], 0, v[8:9]
	s_mov_b64 s[0:1], 0xd600000
	s_addc_u32 s87, s45, 0
	v_readlane_b32 s12, v253, 31
	v_readlane_b32 s13, v253, 32
	v_readlane_b32 s14, v253, 33
	v_readlane_b32 s15, v253, 34
	v_readlane_b32 s43, v253, 6
	v_readlane_b32 s54, v253, 17
	v_readlane_b32 s55, v253, 18
	v_lshl_add_u64 v[12:13], v[2:3], 0, s[0:1]
	s_add_u32 s88, s42, 0x4000
	s_mov_b64 s[0:1], 0x5c00000
	v_readlane_b32 s41, v253, 4
	v_readlane_b32 s46, v253, 9
	v_readlane_b32 s47, v253, 10
	v_readlane_b32 s48, v253, 11
	v_readlane_b32 s49, v253, 12
	v_readlane_b32 s50, v253, 13
	s_addc_u32 s89, s43, 0
	v_lshlrev_b32_e32 v4, 6, v18
	v_lshl_add_u64 v[14:15], v[2:3], 0, s[0:1]
	s_lshl_b32 s0, s80, 5
	s_movk_i32 s12, 0xe000
	s_movk_i32 s14, 0xe008
	s_movk_i32 s18, 0xe010
	s_movk_i32 s78, 0xe018
	s_movk_i32 s92, 0xe0d0
	s_movk_i32 s28, 0xe0d8
	s_movk_i32 s34, 0xe0e0
	s_movk_i32 s52, 0xe0e8
	s_movk_i32 s54, 0xe0f0
	s_movk_i32 s56, 0xe0f8
	v_or_b32_e32 v26, 0x2000, v18
	v_or_b32_e32 v27, 0x4000, v18
	v_or_b32_e32 v28, 0x6000, v18
	v_or_b32_e32 v29, 0x8000, v18
	v_or_b32_e32 v30, 0xa000, v18
	v_or_b32_e32 v31, 0xc000, v18
	v_or_b32_e32 v32, 0xe000, v18
	v_or_b32_e32 v33, 0x10000, v18
	v_or_b32_e32 v34, 0x12000, v18
	v_or_b32_e32 v35, 0x14000, v18
	v_or_b32_e32 v36, 0x16000, v18
	v_or_b32_e32 v37, 0x18000, v18
	v_or_b32_e32 v38, 0x1a000, v18
	v_or_b32_e32 v39, 0x1c000, v18
	v_or_b32_e32 v40, 0x1e000, v18
	v_or_b32_e32 v41, 0x20000, v18
	v_or_b32_e32 v42, 0x22000, v18
	v_or_b32_e32 v43, 0x24000, v18
	v_or_b32_e32 v44, 0x26000, v18
	v_or_b32_e32 v45, 0x28000, v18
	v_or_b32_e32 v46, 0x2a000, v18
	v_or_b32_e32 v47, 0x2c000, v18
	v_or_b32_e32 v48, 0x2e000, v18
	v_or_b32_e32 v49, 0x30000, v18
	v_or_b32_e32 v50, 0x32000, v18
	v_or_b32_e32 v51, 0x34000, v18
	v_or_b32_e32 v52, 0x36000, v18
	v_or_b32_e32 v53, 0x38000, v18
	v_or_b32_e32 v54, 0x3a000, v18
	v_or_b32_e32 v55, 0x3c000, v18
	v_or_b32_e32 v56, 0x3e000, v18
	v_and_b32_e32 v60, 64, v4
	v_mov_b32_e32 v7, v11
	s_lshl_b32 s39, s80, 6
	s_add_i32 s40, s0, 0xfff4c000
	s_lshl_b32 s41, s83, 8
	s_lshl_b32 s42, s80, 4
	s_lshl_b32 s43, s83, 7
	s_mov_b32 s91, 0
	s_mov_b32 s44, 0xc3e00000
	s_movk_i32 s45, 0x7fff
	s_mov_b32 s46, 0xffff0000
	s_movk_i32 s47, 0x2c2f
	s_movk_i32 s48, 0x2c50
	s_mov_b32 s49, 0xb140
	v_add_u32_e32 v61, 0x400, v19
	v_add_u32_e32 v62, 0x800, v19
	v_add_u32_e32 v63, 0xc00, v19
	v_mov_b32_e32 v64, 0x43e00000
	s_mov_b32 s50, s80
	s_mov_b32 s13, -1
	s_mov_b32 s15, -1
	s_mov_b32 s19, -1
	s_mov_b32 s79, -1
	s_mov_b32 s93, -1
	s_mov_b32 s29, -1
	s_mov_b32 s35, -1
	s_mov_b32 s53, -1
	s_mov_b32 s55, -1
	s_mov_b32 s57, -1
	v_readlane_b32 s16, v253, 39
	v_readlane_b32 s17, v253, 40
	v_readlane_b32 s4, v253, 23
	v_readlane_b32 s5, v253, 24
	v_readlane_b32 s6, v253, 25
	v_readlane_b32 s7, v253, 26
	v_readlane_b32 s51, v253, 14
	s_branch .LBB0_15

; #define GAS __attribute__((address_space(1)))
; #define LAS __attribute__((address_space(3)))
; #define LDS_WAIT() asm volatile("s_waitcnt lgkmcnt(0)" ::: "memory")
;     const int pr = item >> 1, kb = 2 * (pr / nblk) + (item & 1), nb = pr % nblk, k0 = 64 * kb, n0 = 32 * nb;
;     const int nr = n0 + (lane & 31); const int sc = MAP == 1 ? src_col_in(nr) : nr;
;     float v[32];
; #pragma unroll
;     for (int i = 0; i < 32; ++i) v[i] = sc >= 0 ? W[(size_t)(k0 + 2 * i + (lane >> 5)) * Nsrc + sc] : 0.f;
; #pragma unroll
;     for (int i = 0; i < 32; ++i) { const int k = k0 + 2 * i + (lane >> 5); float x = v[i] * wscale; if (KS) x *= (k < ksplit ? ksA[k] : ksB[k - ksplit]); scr[(2 * i + (lane >> 5)) * 33 + (lane & 31)] = x; }
;     LDS_WAIT(); asm volatile("" ::: "memory");
;     const int c = lane & 7;
; #pragma unroll
;     for (int j = 0; j < 4; ++j) { const int n = (lane >> 3) + 8 * j; const LAS float* s = scr + (8 * c) * 33 + n;
;         const unsigned long long o = (unsigned long long)pg8::pk4_fp8(s[0 * 33], s[1 * 33], s[2 * 33], s[3 * 33]) | ((unsigned long long)pg8::pk4_fp8(s[4 * 33], s[5 * 33], s[6 * 33], s[7 * 33]) << 32);
;         *(GAS unsigned long long*)(WT + (size_t)(n0 + n) * K + k0 + 8 * c) = o; }
;     LDS_WAIT(); asm volatile("" ::: "memory");
; __global__ void __launch_bounds__(NWAVES * 64, 2) hybrid_fwd(Args args) {
;     ...
;             p0_transpose_item_f8<false>(args.in[16] + (size_t)l * FF * DM, FF, DM, DM / 32, (unsigned char*)(ws + WS_WDN + l * SZ_WDN), 128.f, args.in[16], args.in[16], 0, scr, r, lane);
.LBB0_575:
	s_waitcnt vmcnt(0)
	s_barrier
	s_cmpk_lt_u32 s77, 0xa0
	s_cbranch_scc1 .Llite_skip
	s_sub_i32 s16, s77, 160
	v_and_b32_e32 v133, 63, v0
	v_lshrrev_b32_e32 v134, 6, v0
	v_lshrrev_b32_e32 v130, 5, v133
	v_lshl_add_u32 v131, v134, 4, v130
	v_and_b32_e32 v132, 31, v133
	v_xor_b32_e32 v132, v132, v134
	v_lshlrev_b32_e32 v132, 4, v132
	v_lshl_add_u32 v120, v131, 9, v132
	v_add_u32_e32 v121, 0x10000, v120
	v_and_b32_e32 v132, 31, v133
	v_lshlrev_b32_e32 v132, 4, v132
	s_mov_b32 s21, 0x4000
	v_mad_u32_u24 v126, v131, s21, v132
	v_and_b32_e32 v130, 7, v133
	v_lshrrev_b32_e32 v131, 5, v133
	v_lshl_add_u32 v131, v134, 2, v131
	v_xor_b32_e32 v131, v131, v130
	v_lshlrev_b32_e32 v131, 4, v131
	v_lshl_add_u32 v131, v130, 13, v131
	v_bfe_u32 v132, v133, 3, 2
	v_lshl_add_u32 v122, v132, 2, v131
	v_add_u32_e32 v123, 0x10000, v122
	v_and_b32_e32 v130, 7, v133
	v_lshrrev_b32_e32 v131, 5, v133
	v_lshl_add_u32 v131, v134, 2, v131
	v_add_u32_e32 v131, 2, v131
	v_xor_b32_e32 v131, v131, v130
	v_lshlrev_b32_e32 v131, 4, v131
	v_lshl_add_u32 v131, v130, 13, v131
	v_bfe_u32 v132, v133, 3, 2
	v_lshl_add_u32 v124, v132, 2, v131
	v_add_u32_e32 v125, 0x10000, v124
	v_lshrrev_b32_e32 v130, 3, v133
	v_lshl_add_u32 v130, v134, 4, v130
	v_and_b32_e32 v131, 7, v133
	v_lshlrev_b32_e32 v131, 4, v131
	v_lshl_add_u32 v127, v130, 14, v131
	v_lshrrev_b32_e32 v130, 3, v133
	v_lshl_add_u32 v130, v134, 4, v130
	v_add_u32_e32 v130, 8, v130
	v_and_b32_e32 v131, 7, v133
	v_lshlrev_b32_e32 v131, 4, v131
	v_lshl_add_u32 v128, v130, 14, v131
	v_mov_b32_e32 v129, 0x43e00000
	s_mov_b32 s20, 0xc3e00000
	v_readlane_b32 s2, v253, 35
	v_readlane_b32 s3, v253, 36
	v_readlane_b32 s4, v253, 41
	v_readlane_b32 s5, v253, 42
	s_add_u32 s2, s2, 0x10000000
	s_addc_u32 s3, s3, 0
	s_add_u32 s4, s4, 0x27600000
	s_addc_u32 s5, s5, 0
	s_add_i32 s17, s16, 0
	s_min_u32 s17, s17, 0x7ff
	s_lshr_b32 s18, s17, 5
	s_add_i32 s18, s18, 64
	s_and_b32 s19, s17, 31
	s_lshl_b32 s18, s18, 21
	s_lshl_b32 s19, s19, 9
	s_add_u32 s18, s18, s19
	s_add_u32 s12, s2, s18
	s_addc_u32 s13, s3, 0
	global_load_dwordx4 v[36:39], v126, s[12:13]
	s_add_u32 s12, s12, 0x8000
	s_addc_u32 s13, s13, 0
	global_load_dwordx4 v[40:43], v126, s[12:13]
	s_add_u32 s12, s12, 0x8000
	s_addc_u32 s13, s13, 0
	global_load_dwordx4 v[44:47], v126, s[12:13]
	s_add_u32 s12, s12, 0x8000
	s_addc_u32 s13, s13, 0
	global_load_dwordx4 v[48:51], v126, s[12:13]
	s_add_u32 s12, s12, 0x8000
	s_addc_u32 s13, s13, 0
	global_load_dwordx4 v[52:55], v126, s[12:13]
	s_add_u32 s12, s12, 0x8000
	s_addc_u32 s13, s13, 0
	global_load_dwordx4 v[56:59], v126, s[12:13]
	s_add_u32 s12, s12, 0x8000
	s_addc_u32 s13, s13, 0
	global_load_dwordx4 v[60:63], v126, s[12:13]
	s_add_u32 s12, s12, 0x8000
	s_addc_u32 s13, s13, 0
	global_load_dwordx4 v[64:67], v126, s[12:13]
	s_add_i32 s17, s16, 96
	s_min_u32 s17, s17, 0x7ff
	s_lshr_b32 s18, s17, 5
	s_add_i32 s18, s18, 64
	s_and_b32 s19, s17, 31
	s_lshl_b32 s18, s18, 21
	s_lshl_b32 s19, s19, 9
	s_add_u32 s18, s18, s19
	s_add_u32 s12, s2, s18
	s_addc_u32 s13, s3, 0
	global_load_dwordx4 v[68:71], v126, s[12:13]
	s_add_u32 s12, s12, 0x8000
	s_addc_u32 s13, s13, 0
	global_load_dwordx4 v[72:75], v126, s[12:13]
	s_add_u32 s12, s12, 0x8000
	s_addc_u32 s13, s13, 0
	global_load_dwordx4 v[76:79], v126, s[12:13]
	s_add_u32 s12, s12, 0x8000
	s_addc_u32 s13, s13, 0
	global_load_dwordx4 v[80:83], v126, s[12:13]
	s_add_u32 s12, s12, 0x8000
	s_addc_u32 s13, s13, 0
	global_load_dwordx4 v[84:87], v126, s[12:13]
	s_add_u32 s12, s12, 0x8000
	s_addc_u32 s13, s13, 0
	global_load_dwordx4 v[88:91], v126, s[12:13]
	s_add_u32 s12, s12, 0x8000
	s_addc_u32 s13, s13, 0
	global_load_dwordx4 v[92:95], v126, s[12:13]
	s_add_u32 s12, s12, 0x8000
	s_addc_u32 s13, s13, 0
	global_load_dwordx4 v[96:99], v126, s[12:13]
	s_waitcnt vmcnt(8)
	v_mul_f32_e32 v36, 0x43000000, v36
	v_mul_f32_e32 v37, 0x43000000, v37
	v_mul_f32_e32 v38, 0x43000000, v38
	v_mul_f32_e32 v39, 0x43000000, v39
	ds_write_b128 v120, v[36:39]
	v_mul_f32_e32 v40, 0x43000000, v40
	v_mul_f32_e32 v41, 0x43000000, v41
	v_mul_f32_e32 v42, 0x43000000, v42
	v_mul_f32_e32 v43, 0x43000000, v43
	ds_write_b128 v120, v[40:43] offset:1024
	v_mul_f32_e32 v44, 0x43000000, v44
	v_mul_f32_e32 v45, 0x43000000, v45
	v_mul_f32_e32 v46, 0x43000000, v46
	v_mul_f32_e32 v47, 0x43000000, v47
	ds_write_b128 v120, v[44:47] offset:2048
	v_mul_f32_e32 v48, 0x43000000, v48
	v_mul_f32_e32 v49, 0x43000000, v49
	v_mul_f32_e32 v50, 0x43000000, v50
	v_mul_f32_e32 v51, 0x43000000, v51
	ds_write_b128 v120, v[48:51] offset:3072
	v_mul_f32_e32 v52, 0x43000000, v52
	v_mul_f32_e32 v53, 0x43000000, v53
	v_mul_f32_e32 v54, 0x43000000, v54
	v_mul_f32_e32 v55, 0x43000000, v55
	ds_write_b128 v120, v[52:55] offset:4096
	v_mul_f32_e32 v56, 0x43000000, v56
	v_mul_f32_e32 v57, 0x43000000, v57
	v_mul_f32_e32 v58, 0x43000000, v58
	v_mul_f32_e32 v59, 0x43000000, v59
	ds_write_b128 v120, v[56:59] offset:5120
	v_mul_f32_e32 v60, 0x43000000, v60
	v_mul_f32_e32 v61, 0x43000000, v61
	v_mul_f32_e32 v62, 0x43000000, v62
	v_mul_f32_e32 v63, 0x43000000, v63
	ds_write_b128 v120, v[60:63] offset:6144
	v_mul_f32_e32 v64, 0x43000000, v64
	v_mul_f32_e32 v65, 0x43000000, v65
	v_mul_f32_e32 v66, 0x43000000, v66
	v_mul_f32_e32 v67, 0x43000000, v67
	ds_write_b128 v120, v[64:67] offset:7168
	s_waitcnt lgkmcnt(0)
	s_barrier
; #define GAS __attribute__((address_space(1)))
; #define LAS __attribute__((address_space(3)))
; #define LDS_WAIT() asm volatile("s_waitcnt lgkmcnt(0)" ::: "memory")
;     const int pr = item >> 1, kb = 2 * (pr / nblk) + (item & 1), nb = pr % nblk, k0 = 64 * kb, n0 = 32 * nb;
;     const int nr = n0 + (lane & 31); const int sc = MAP == 1 ? src_col_in(nr) : nr;
;     float v[32];
; #pragma unroll
;     for (int i = 0; i < 32; ++i) v[i] = sc >= 0 ? W[(size_t)(k0 + 2 * i + (lane >> 5)) * Nsrc + sc] : 0.f;
; #pragma unroll
;     for (int i = 0; i < 32; ++i) { const int k = k0 + 2 * i + (lane >> 5); float x = v[i] * wscale; if (KS) x *= (k < ksplit ? ksA[k] : ksB[k - ksplit]); scr[(2 * i + (lane >> 5)) * 33 + (lane & 31)] = x; }
;     LDS_WAIT(); asm volatile("" ::: "memory");
;     const int c = lane & 7;
; #pragma unroll
;     for (int j = 0; j < 4; ++j) { const int n = (lane >> 3) + 8 * j; const LAS float* s = scr + (8 * c) * 33 + n;
;         const unsigned long long o = (unsigned long long)pg8::pk4_fp8(s[0 * 33], s[1 * 33], s[2 * 33], s[3 * 33]) | ((unsigned long long)pg8::pk4_fp8(s[4 * 33], s[5 * 33], s[6 * 33], s[7 * 33]) << 32);
;         *(GAS unsigned long long*)(WT + (size_t)(n0 + n) * K + k0 + 8 * c) = o; }
;     LDS_WAIT(); asm volatile("" ::: "memory");
; __global__ void __launch_bounds__(NWAVES * 64, 2) hybrid_fwd(Args args) {
;     ...
;             p0_transpose_item_f8<false>(args.in[16] + (size_t)l * FF * DM, FF, DM, DM / 32, (unsigned char*)(ws + WS_WDN + l * SZ_WDN), 128.f, args.in[16], args.in[16], 0, scr, r, lane);
	s_add_i32 s17, s16, 192
	s_min_u32 s17, s17, 0x7ff
	s_lshr_b32 s18, s17, 5
	s_add_i32 s18, s18, 64
	s_and_b32 s19, s17, 31
	s_lshl_b32 s18, s18, 21
	s_lshl_b32 s19, s19, 9
	s_add_u32 s18, s18, s19
	s_add_u32 s12, s2, s18
	s_addc_u32 s13, s3, 0
	global_load_dwordx4 v[36:39], v126, s[12:13]
	s_add_u32 s12, s12, 0x8000
	s_addc_u32 s13, s13, 0
	global_load_dwordx4 v[40:43], v126, s[12:13]
	s_add_u32 s12, s12, 0x8000
	s_addc_u32 s13, s13, 0
	global_load_dwordx4 v[44:47], v126, s[12:13]
	s_add_u32 s12, s12, 0x8000
	s_addc_u32 s13, s13, 0
	global_load_dwordx4 v[48:51], v126, s[12:13]
	s_add_u32 s12, s12, 0x8000
	s_addc_u32 s13, s13, 0
	global_load_dwordx4 v[52:55], v126, s[12:13]
	s_add_u32 s12, s12, 0x8000
	s_addc_u32 s13, s13, 0
	global_load_dwordx4 v[56:59], v126, s[12:13]
	s_add_u32 s12, s12, 0x8000
	s_addc_u32 s13, s13, 0
	global_load_dwordx4 v[60:63], v126, s[12:13]
	s_add_u32 s12, s12, 0x8000
	s_addc_u32 s13, s13, 0
	global_load_dwordx4 v[64:67], v126, s[12:13]
	s_add_i32 s17, s16, 0
	s_min_u32 s17, s17, 0x7ff
	s_lshr_b32 s18, s17, 5
	s_add_i32 s18, s18, 64
	s_and_b32 s19, s17, 31
	s_lshl_b32 s19, s19, 21
	s_lshl_b32 s18, s18, 7
	s_add_u32 s18, s18, s19
	s_add_u32 s14, s4, s18
	s_addc_u32 s15, s5, 0
	ds_read_b32 v100, v122
	ds_read_b32 v101, v122 offset:512
	ds_read_b32 v102, v122 offset:1024
	ds_read_b32 v103, v122 offset:1536
	ds_read_b32 v104, v122 offset:2048
	ds_read_b32 v105, v122 offset:2560
	ds_read_b32 v106, v122 offset:3072
	ds_read_b32 v107, v122 offset:3584
	ds_read_b32 v108, v122 offset:4096
	ds_read_b32 v109, v122 offset:4608
	ds_read_b32 v110, v122 offset:5120
	ds_read_b32 v111, v122 offset:5632
	ds_read_b32 v112, v122 offset:6144
	ds_read_b32 v113, v122 offset:6656
	ds_read_b32 v114, v122 offset:7168
	ds_read_b32 v115, v122 offset:7680
	s_waitcnt lgkmcnt(0)
	v_max_f32_e32 v100, v100, v100
	v_max_f32_e32 v101, v101, v101
	v_max_f32_e32 v102, v102, v102
	v_max_f32_e32 v103, v103, v103
	v_max_f32_e32 v104, v104, v104
	v_max_f32_e32 v105, v105, v105
	v_max_f32_e32 v106, v106, v106
	v_max_f32_e32 v107, v107, v107
	v_max_f32_e32 v108, v108, v108
	v_max_f32_e32 v109, v109, v109
	v_max_f32_e32 v110, v110, v110
	v_max_f32_e32 v111, v111, v111
	v_max_f32_e32 v112, v112, v112
	v_max_f32_e32 v113, v113, v113
	v_max_f32_e32 v114, v114, v114
	v_max_f32_e32 v115, v115, v115
	v_med3_f32 v100, v100, s20, v129
	v_med3_f32 v101, v101, s20, v129
	v_med3_f32 v102, v102, s20, v129
	v_med3_f32 v103, v103, s20, v129
	v_med3_f32 v104, v104, s20, v129
	v_med3_f32 v105, v105, s20, v129
	v_med3_f32 v106, v106, s20, v129
	v_med3_f32 v107, v107, s20, v129
	v_med3_f32 v108, v108, s20, v129
	v_med3_f32 v109, v109, s20, v129
	v_med3_f32 v110, v110, s20, v129
	v_med3_f32 v111, v111, s20, v129
	v_med3_f32 v112, v112, s20, v129
	v_med3_f32 v113, v113, s20, v129
	v_med3_f32 v114, v114, s20, v129
	v_med3_f32 v115, v115, s20, v129
	v_mov_b32_e32 v116, 0
	v_mov_b32_e32 v117, 0
	v_mov_b32_e32 v118, 0
	v_mov_b32_e32 v119, 0
	v_cvt_pk_fp8_f32 v116, v100, v101
	v_cvt_pk_fp8_f32 v117, v104, v105
	v_cvt_pk_fp8_f32 v118, v108, v109
	v_cvt_pk_fp8_f32 v119, v112, v113
	v_cvt_pk_fp8_f32 v116, v102, v103 op_sel:[0,0,1]
	v_cvt_pk_fp8_f32 v117, v106, v107 op_sel:[0,0,1]
	v_cvt_pk_fp8_f32 v118, v110, v111 op_sel:[0,0,1]
	v_cvt_pk_fp8_f32 v119, v114, v115 op_sel:[0,0,1]
	s_nop 0
	global_store_dwordx4 v127, v[116:119], s[14:15]
	ds_read_b32 v100, v124
	ds_read_b32 v101, v124 offset:512
	ds_read_b32 v102, v124 offset:1024
	ds_read_b32 v103, v124 offset:1536
	ds_read_b32 v104, v124 offset:2048
	ds_read_b32 v105, v124 offset:2560
	ds_read_b32 v106, v124 offset:3072
	ds_read_b32 v107, v124 offset:3584
	ds_read_b32 v108, v124 offset:4096
	ds_read_b32 v109, v124 offset:4608
	ds_read_b32 v110, v124 offset:5120
	ds_read_b32 v111, v124 offset:5632
	ds_read_b32 v112, v124 offset:6144
	ds_read_b32 v113, v124 offset:6656
	ds_read_b32 v114, v124 offset:7168
	ds_read_b32 v115, v124 offset:7680
	s_waitcnt lgkmcnt(0)
	v_max_f32_e32 v100, v100, v100
	v_max_f32_e32 v101, v101, v101
	v_max_f32_e32 v102, v102, v102
	v_max_f32_e32 v103, v103, v103
	v_max_f32_e32 v104, v104, v104
	v_max_f32_e32 v105, v105, v105
	v_max_f32_e32 v106, v106, v106
	v_max_f32_e32 v107, v107, v107
	v_max_f32_e32 v108, v108, v108
	v_max_f32_e32 v109, v109, v109
	v_max_f32_e32 v110, v110, v110
	v_max_f32_e32 v111, v111, v111
	v_max_f32_e32 v112, v112, v112
	v_max_f32_e32 v113, v113, v113
	v_max_f32_e32 v114, v114, v114
	v_max_f32_e32 v115, v115, v115
	v_med3_f32 v100, v100, s20, v129
	v_med3_f32 v101, v101, s20, v129
	v_med3_f32 v102, v102, s20, v129
	v_med3_f32 v103, v103, s20, v129
	v_med3_f32 v104, v104, s20, v129
	v_med3_f32 v105, v105, s20, v129
	v_med3_f32 v106, v106, s20, v129
	v_med3_f32 v107, v107, s20, v129
	v_med3_f32 v108, v108, s20, v129
	v_med3_f32 v109, v109, s20, v129
	v_med3_f32 v110, v110, s20, v129
	v_med3_f32 v111, v111, s20, v129
	v_med3_f32 v112, v112, s20, v129
	v_med3_f32 v113, v113, s20, v129
	v_med3_f32 v114, v114, s20, v129
	v_med3_f32 v115, v115, s20, v129
	v_mov_b32_e32 v116, 0
	v_mov_b32_e32 v117, 0
	v_mov_b32_e32 v118, 0
	v_mov_b32_e32 v119, 0
	v_cvt_pk_fp8_f32 v116, v100, v101
	v_cvt_pk_fp8_f32 v117, v104, v105
	v_cvt_pk_fp8_f32 v118, v108, v109
	v_cvt_pk_fp8_f32 v119, v112, v113
	v_cvt_pk_fp8_f32 v116, v102, v103 op_sel:[0,0,1]
	v_cvt_pk_fp8_f32 v117, v106, v107 op_sel:[0,0,1]
	v_cvt_pk_fp8_f32 v118, v110, v111 op_sel:[0,0,1]
	v_cvt_pk_fp8_f32 v119, v114, v115 op_sel:[0,0,1]
	s_nop 0
	global_store_dwordx4 v128, v[116:119], s[14:15]
	s_waitcnt vmcnt(10)
	v_mul_f32_e32 v68, 0x43000000, v68
	v_mul_f32_e32 v69, 0x43000000, v69
	v_mul_f32_e32 v70, 0x43000000, v70
	v_mul_f32_e32 v71, 0x43000000, v71
	ds_write_b128 v121, v[68:71]
	v_mul_f32_e32 v72, 0x43000000, v72
	v_mul_f32_e32 v73, 0x43000000, v73
	v_mul_f32_e32 v74, 0x43000000, v74
	v_mul_f32_e32 v75, 0x43000000, v75
	ds_write_b128 v121, v[72:75] offset:1024
	v_mul_f32_e32 v76, 0x43000000, v76
	v_mul_f32_e32 v77, 0x43000000, v77
	v_mul_f32_e32 v78, 0x43000000, v78
	v_mul_f32_e32 v79, 0x43000000, v79
	ds_write_b128 v121, v[76:79] offset:2048
	v_mul_f32_e32 v80, 0x43000000, v80
	v_mul_f32_e32 v81, 0x43000000, v81
	v_mul_f32_e32 v82, 0x43000000, v82
	v_mul_f32_e32 v83, 0x43000000, v83
	ds_write_b128 v121, v[80:83] offset:3072
	v_mul_f32_e32 v84, 0x43000000, v84
	v_mul_f32_e32 v85, 0x43000000, v85
	v_mul_f32_e32 v86, 0x43000000, v86
	v_mul_f32_e32 v87, 0x43000000, v87
	ds_write_b128 v121, v[84:87] offset:4096
	v_mul_f32_e32 v88, 0x43000000, v88
	v_mul_f32_e32 v89, 0x43000000, v89
	v_mul_f32_e32 v90, 0x43000000, v90
	v_mul_f32_e32 v91, 0x43000000, v91
	ds_write_b128 v121, v[88:91] offset:5120
	v_mul_f32_e32 v92, 0x43000000, v92
	v_mul_f32_e32 v93, 0x43000000, v93
	v_mul_f32_e32 v94, 0x43000000, v94
	v_mul_f32_e32 v95, 0x43000000, v95
	ds_write_b128 v121, v[92:95] offset:6144
	v_mul_f32_e32 v96, 0x43000000, v96
	v_mul_f32_e32 v97, 0x43000000, v97
	v_mul_f32_e32 v98, 0x43000000, v98
	v_mul_f32_e32 v99, 0x43000000, v99
	ds_write_b128 v121, v[96:99] offset:7168
	s_waitcnt lgkmcnt(0)
	s_barrier
; #define GAS __attribute__((address_space(1)))
; #define LAS __attribute__((address_space(3)))
; #define LDS_WAIT() asm volatile("s_waitcnt lgkmcnt(0)" ::: "memory")
;     const int pr = item >> 1, kb = 2 * (pr / nblk) + (item & 1), nb = pr % nblk, k0 = 64 * kb, n0 = 32 * nb;
;     const int nr = n0 + (lane & 31); const int sc = MAP == 1 ? src_col_in(nr) : nr;
;     float v[32];
; #pragma unroll
;     for (int i = 0; i < 32; ++i) v[i] = sc >= 0 ? W[(size_t)(k0 + 2 * i + (lane >> 5)) * Nsrc + sc] : 0.f;
; #pragma unroll
;     for (int i = 0; i < 32; ++i) { const int k = k0 + 2 * i + (lane >> 5); float x = v[i] * wscale; if (KS) x *= (k < ksplit ? ksA[k] : ksB[k - ksplit]); scr[(2 * i + (lane >> 5)) * 33 + (lane & 31)] = x; }
;     LDS_WAIT(); asm volatile("" ::: "memory");
;     const int c = lane & 7;
; #pragma unroll
;     for (int j = 0; j < 4; ++j) { const int n = (lane >> 3) + 8 * j; const LAS float* s = scr + (8 * c) * 33 + n;
;         const unsigned long long o = (unsigned long long)pg8::pk4_fp8(s[0 * 33], s[1 * 33], s[2 * 33], s[3 * 33]) | ((unsigned long long)pg8::pk4_fp8(s[4 * 33], s[5 * 33], s[6 * 33], s[7 * 33]) << 32);
;         *(GAS unsigned long long*)(WT + (size_t)(n0 + n) * K + k0 + 8 * c) = o; }
;     LDS_WAIT(); asm volatile("" ::: "memory");
; __global__ void __launch_bounds__(NWAVES * 64, 2) hybrid_fwd(Args args) {
;     ...
;             p0_transpose_item_f8<false>(args.in[16] + (size_t)l * FF * DM, FF, DM, DM / 32, (unsigned char*)(ws + WS_WDN + l * SZ_WDN), 128.f, args.in[16], args.in[16], 0, scr, r, lane);
	s_add_i32 s17, s16, 288
	s_min_u32 s17, s17, 0x7ff
	s_lshr_b32 s18, s17, 5
	s_add_i32 s18, s18, 64
	s_and_b32 s19, s17, 31
	s_lshl_b32 s18, s18, 21
	s_lshl_b32 s19, s19, 9
	s_add_u32 s18, s18, s19
	s_add_u32 s12, s2, s18
	s_addc_u32 s13, s3, 0
	global_load_dwordx4 v[68:71], v126, s[12:13]
	s_add_u32 s12, s12, 0x8000
	s_addc_u32 s13, s13, 0
	global_load_dwordx4 v[72:75], v126, s[12:13]
	s_add_u32 s12, s12, 0x8000
	s_addc_u32 s13, s13, 0
	global_load_dwordx4 v[76:79], v126, s[12:13]
	s_add_u32 s12, s12, 0x8000
	s_addc_u32 s13, s13, 0
	global_load_dwordx4 v[80:83], v126, s[12:13]
	s_add_u32 s12, s12, 0x8000
	s_addc_u32 s13, s13, 0
	global_load_dwordx4 v[84:87], v126, s[12:13]
	s_add_u32 s12, s12, 0x8000
	s_addc_u32 s13, s13, 0
	global_load_dwordx4 v[88:91], v126, s[12:13]
	s_add_u32 s12, s12, 0x8000
	s_addc_u32 s13, s13, 0
	global_load_dwordx4 v[92:95], v126, s[12:13]
	s_add_u32 s12, s12, 0x8000
	s_addc_u32 s13, s13, 0
	global_load_dwordx4 v[96:99], v126, s[12:13]
	s_add_i32 s17, s16, 96
	s_min_u32 s17, s17, 0x7ff
	s_lshr_b32 s18, s17, 5
	s_add_i32 s18, s18, 64
	s_and_b32 s19, s17, 31
	s_lshl_b32 s19, s19, 21
	s_lshl_b32 s18, s18, 7
	s_add_u32 s18, s18, s19
	s_add_u32 s14, s4, s18
	s_addc_u32 s15, s5, 0
	ds_read_b32 v100, v123
	ds_read_b32 v101, v123 offset:512
	ds_read_b32 v102, v123 offset:1024
	ds_read_b32 v103, v123 offset:1536
	ds_read_b32 v104, v123 offset:2048
	ds_read_b32 v105, v123 offset:2560
	ds_read_b32 v106, v123 offset:3072
	ds_read_b32 v107, v123 offset:3584
	ds_read_b32 v108, v123 offset:4096
	ds_read_b32 v109, v123 offset:4608
	ds_read_b32 v110, v123 offset:5120
	ds_read_b32 v111, v123 offset:5632
	ds_read_b32 v112, v123 offset:6144
	ds_read_b32 v113, v123 offset:6656
	ds_read_b32 v114, v123 offset:7168
	ds_read_b32 v115, v123 offset:7680
	s_waitcnt lgkmcnt(0)
	v_max_f32_e32 v100, v100, v100
	v_max_f32_e32 v101, v101, v101
	v_max_f32_e32 v102, v102, v102
	v_max_f32_e32 v103, v103, v103
	v_max_f32_e32 v104, v104, v104
	v_max_f32_e32 v105, v105, v105
	v_max_f32_e32 v106, v106, v106
	v_max_f32_e32 v107, v107, v107
	v_max_f32_e32 v108, v108, v108
	v_max_f32_e32 v109, v109, v109
	v_max_f32_e32 v110, v110, v110
	v_max_f32_e32 v111, v111, v111
	v_max_f32_e32 v112, v112, v112
	v_max_f32_e32 v113, v113, v113
	v_max_f32_e32 v114, v114, v114
	v_max_f32_e32 v115, v115, v115
	v_med3_f32 v100, v100, s20, v129
	v_med3_f32 v101, v101, s20, v129
	v_med3_f32 v102, v102, s20, v129
	v_med3_f32 v103, v103, s20, v129
	v_med3_f32 v104, v104, s20, v129
	v_med3_f32 v105, v105, s20, v129
	v_med3_f32 v106, v106, s20, v129
	v_med3_f32 v107, v107, s20, v129
	v_med3_f32 v108, v108, s20, v129
	v_med3_f32 v109, v109, s20, v129
	v_med3_f32 v110, v110, s20, v129
	v_med3_f32 v111, v111, s20, v129
	v_med3_f32 v112, v112, s20, v129
	v_med3_f32 v113, v113, s20, v129
	v_med3_f32 v114, v114, s20, v129
	v_med3_f32 v115, v115, s20, v129
	v_mov_b32_e32 v116, 0
	v_mov_b32_e32 v117, 0
	v_mov_b32_e32 v118, 0
	v_mov_b32_e32 v119, 0
	v_cvt_pk_fp8_f32 v116, v100, v101
	v_cvt_pk_fp8_f32 v117, v104, v105
	v_cvt_pk_fp8_f32 v118, v108, v109
	v_cvt_pk_fp8_f32 v119, v112, v113
	v_cvt_pk_fp8_f32 v116, v102, v103 op_sel:[0,0,1]
	v_cvt_pk_fp8_f32 v117, v106, v107 op_sel:[0,0,1]
	v_cvt_pk_fp8_f32 v118, v110, v111 op_sel:[0,0,1]
	v_cvt_pk_fp8_f32 v119, v114, v115 op_sel:[0,0,1]
	s_nop 0
	global_store_dwordx4 v127, v[116:119], s[14:15]
	ds_read_b32 v100, v125
	ds_read_b32 v101, v125 offset:512
	ds_read_b32 v102, v125 offset:1024
	ds_read_b32 v103, v125 offset:1536
	ds_read_b32 v104, v125 offset:2048
	ds_read_b32 v105, v125 offset:2560
	ds_read_b32 v106, v125 offset:3072
	ds_read_b32 v107, v125 offset:3584
	ds_read_b32 v108, v125 offset:4096
	ds_read_b32 v109, v125 offset:4608
	ds_read_b32 v110, v125 offset:5120
	ds_read_b32 v111, v125 offset:5632
	ds_read_b32 v112, v125 offset:6144
	ds_read_b32 v113, v125 offset:6656
	ds_read_b32 v114, v125 offset:7168
	ds_read_b32 v115, v125 offset:7680
	s_waitcnt lgkmcnt(0)
	v_max_f32_e32 v100, v100, v100
	v_max_f32_e32 v101, v101, v101
	v_max_f32_e32 v102, v102, v102
	v_max_f32_e32 v103, v103, v103
	v_max_f32_e32 v104, v104, v104
	v_max_f32_e32 v105, v105, v105
	v_max_f32_e32 v106, v106, v106
	v_max_f32_e32 v107, v107, v107
	v_max_f32_e32 v108, v108, v108
	v_max_f32_e32 v109, v109, v109
	v_max_f32_e32 v110, v110, v110
	v_max_f32_e32 v111, v111, v111
	v_max_f32_e32 v112, v112, v112
	v_max_f32_e32 v113, v113, v113
	v_max_f32_e32 v114, v114, v114
	v_max_f32_e32 v115, v115, v115
	v_med3_f32 v100, v100, s20, v129
	v_med3_f32 v101, v101, s20, v129
	v_med3_f32 v102, v102, s20, v129
	v_med3_f32 v103, v103, s20, v129
	v_med3_f32 v104, v104, s20, v129
	v_med3_f32 v105, v105, s20, v129
	v_med3_f32 v106, v106, s20, v129
	v_med3_f32 v107, v107, s20, v129
	v_med3_f32 v108, v108, s20, v129
	v_med3_f32 v109, v109, s20, v129
	v_med3_f32 v110, v110, s20, v129
	v_med3_f32 v111, v111, s20, v129
	v_med3_f32 v112, v112, s20, v129
	v_med3_f32 v113, v113, s20, v129
	v_med3_f32 v114, v114, s20, v129
	v_med3_f32 v115, v115, s20, v129
	v_mov_b32_e32 v116, 0
	v_mov_b32_e32 v117, 0
	v_mov_b32_e32 v118, 0
	v_mov_b32_e32 v119, 0
	v_cvt_pk_fp8_f32 v116, v100, v101
	v_cvt_pk_fp8_f32 v117, v104, v105
	v_cvt_pk_fp8_f32 v118, v108, v109
	v_cvt_pk_fp8_f32 v119, v112, v113
	v_cvt_pk_fp8_f32 v116, v102, v103 op_sel:[0,0,1]
	v_cvt_pk_fp8_f32 v117, v106, v107 op_sel:[0,0,1]
	v_cvt_pk_fp8_f32 v118, v110, v111 op_sel:[0,0,1]
	v_cvt_pk_fp8_f32 v119, v114, v115 op_sel:[0,0,1]
	s_nop 0
	global_store_dwordx4 v128, v[116:119], s[14:15]
	s_waitcnt vmcnt(12)
	v_mul_f32_e32 v36, 0x43000000, v36
	v_mul_f32_e32 v37, 0x43000000, v37
	v_mul_f32_e32 v38, 0x43000000, v38
	v_mul_f32_e32 v39, 0x43000000, v39
	ds_write_b128 v120, v[36:39]
	v_mul_f32_e32 v40, 0x43000000, v40
	v_mul_f32_e32 v41, 0x43000000, v41
	v_mul_f32_e32 v42, 0x43000000, v42
	v_mul_f32_e32 v43, 0x43000000, v43
	ds_write_b128 v120, v[40:43] offset:1024
	v_mul_f32_e32 v44, 0x43000000, v44
	v_mul_f32_e32 v45, 0x43000000, v45
	v_mul_f32_e32 v46, 0x43000000, v46
	v_mul_f32_e32 v47, 0x43000000, v47
	ds_write_b128 v120, v[44:47] offset:2048
	v_mul_f32_e32 v48, 0x43000000, v48
	v_mul_f32_e32 v49, 0x43000000, v49
	v_mul_f32_e32 v50, 0x43000000, v50
	v_mul_f32_e32 v51, 0x43000000, v51
	ds_write_b128 v120, v[48:51] offset:3072
	v_mul_f32_e32 v52, 0x43000000, v52
	v_mul_f32_e32 v53, 0x43000000, v53
	v_mul_f32_e32 v54, 0x43000000, v54
	v_mul_f32_e32 v55, 0x43000000, v55
	ds_write_b128 v120, v[52:55] offset:4096
	v_mul_f32_e32 v56, 0x43000000, v56
	v_mul_f32_e32 v57, 0x43000000, v57
	v_mul_f32_e32 v58, 0x43000000, v58
	v_mul_f32_e32 v59, 0x43000000, v59
	ds_write_b128 v120, v[56:59] offset:5120
	v_mul_f32_e32 v60, 0x43000000, v60
	v_mul_f32_e32 v61, 0x43000000, v61
	v_mul_f32_e32 v62, 0x43000000, v62
	v_mul_f32_e32 v63, 0x43000000, v63
	ds_write_b128 v120, v[60:63] offset:6144
	v_mul_f32_e32 v64, 0x43000000, v64
	v_mul_f32_e32 v65, 0x43000000, v65
	v_mul_f32_e32 v66, 0x43000000, v66
	v_mul_f32_e32 v67, 0x43000000, v67
	ds_write_b128 v120, v[64:67] offset:7168
	s_waitcnt lgkmcnt(0)
	s_barrier
; #define GAS __attribute__((address_space(1)))
; #define LAS __attribute__((address_space(3)))
; #define LDS_WAIT() asm volatile("s_waitcnt lgkmcnt(0)" ::: "memory")
;     const int pr = item >> 1, kb = 2 * (pr / nblk) + (item & 1), nb = pr % nblk, k0 = 64 * kb, n0 = 32 * nb;
;     const int nr = n0 + (lane & 31); const int sc = MAP == 1 ? src_col_in(nr) : nr;
;     float v[32];
; #pragma unroll
;     for (int i = 0; i < 32; ++i) v[i] = sc >= 0 ? W[(size_t)(k0 + 2 * i + (lane >> 5)) * Nsrc + sc] : 0.f;
; #pragma unroll
;     for (int i = 0; i < 32; ++i) { const int k = k0 + 2 * i + (lane >> 5); float x = v[i] * wscale; if (KS) x *= (k < ksplit ? ksA[k] : ksB[k - ksplit]); scr[(2 * i + (lane >> 5)) * 33 + (lane & 31)] = x; }
;     LDS_WAIT(); asm volatile("" ::: "memory");
;     const int c = lane & 7;
; #pragma unroll
;     for (int j = 0; j < 4; ++j) { const int n = (lane >> 3) + 8 * j; const LAS float* s = scr + (8 * c) * 33 + n;
;         const unsigned long long o = (unsigned long long)pg8::pk4_fp8(s[0 * 33], s[1 * 33], s[2 * 33], s[3 * 33]) | ((unsigned long long)pg8::pk4_fp8(s[4 * 33], s[5 * 33], s[6 * 33], s[7 * 33]) << 32);
;         *(GAS unsigned long long*)(WT + (size_t)(n0 + n) * K + k0 + 8 * c) = o; }
;     LDS_WAIT(); asm volatile("" ::: "memory");
; __global__ void __launch_bounds__(NWAVES * 64, 2) hybrid_fwd(Args args) {
;     ...
;             p0_transpose_item_f8<false>(args.in[16] + (size_t)l * FF * DM, FF, DM, DM / 32, (unsigned char*)(ws + WS_WDN + l * SZ_WDN), 128.f, args.in[16], args.in[16], 0, scr, r, lane);
	s_add_i32 s17, s16, 384
	s_min_u32 s17, s17, 0x7ff
	s_lshr_b32 s18, s17, 5
	s_add_i32 s18, s18, 64
	s_and_b32 s19, s17, 31
	s_lshl_b32 s18, s18, 21
	s_lshl_b32 s19, s19, 9
	s_add_u32 s18, s18, s19
	s_add_u32 s12, s2, s18
	s_addc_u32 s13, s3, 0
	global_load_dwordx4 v[36:39], v126, s[12:13]
	s_add_u32 s12, s12, 0x8000
	s_addc_u32 s13, s13, 0
	global_load_dwordx4 v[40:43], v126, s[12:13]
	s_add_u32 s12, s12, 0x8000
	s_addc_u32 s13, s13, 0
	global_load_dwordx4 v[44:47], v126, s[12:13]
	s_add_u32 s12, s12, 0x8000
	s_addc_u32 s13, s13, 0
	global_load_dwordx4 v[48:51], v126, s[12:13]
	s_add_u32 s12, s12, 0x8000
	s_addc_u32 s13, s13, 0
	global_load_dwordx4 v[52:55], v126, s[12:13]
	s_add_u32 s12, s12, 0x8000
	s_addc_u32 s13, s13, 0
	global_load_dwordx4 v[56:59], v126, s[12:13]
	s_add_u32 s12, s12, 0x8000
	s_addc_u32 s13, s13, 0
	global_load_dwordx4 v[60:63], v126, s[12:13]
	s_add_u32 s12, s12, 0x8000
	s_addc_u32 s13, s13, 0
	global_load_dwordx4 v[64:67], v126, s[12:13]
	s_add_i32 s17, s16, 192
	s_min_u32 s17, s17, 0x7ff
	s_lshr_b32 s18, s17, 5
	s_add_i32 s18, s18, 64
	s_and_b32 s19, s17, 31
	s_lshl_b32 s19, s19, 21
	s_lshl_b32 s18, s18, 7
	s_add_u32 s18, s18, s19
	s_add_u32 s14, s4, s18
	s_addc_u32 s15, s5, 0
	ds_read_b32 v100, v122
	ds_read_b32 v101, v122 offset:512
	ds_read_b32 v102, v122 offset:1024
	ds_read_b32 v103, v122 offset:1536
	ds_read_b32 v104, v122 offset:2048
	ds_read_b32 v105, v122 offset:2560
	ds_read_b32 v106, v122 offset:3072
	ds_read_b32 v107, v122 offset:3584
	ds_read_b32 v108, v122 offset:4096
	ds_read_b32 v109, v122 offset:4608
	ds_read_b32 v110, v122 offset:5120
	ds_read_b32 v111, v122 offset:5632
	ds_read_b32 v112, v122 offset:6144
	ds_read_b32 v113, v122 offset:6656
	ds_read_b32 v114, v122 offset:7168
	ds_read_b32 v115, v122 offset:7680
	s_waitcnt lgkmcnt(0)
	v_max_f32_e32 v100, v100, v100
	v_max_f32_e32 v101, v101, v101
	v_max_f32_e32 v102, v102, v102
	v_max_f32_e32 v103, v103, v103
	v_max_f32_e32 v104, v104, v104
	v_max_f32_e32 v105, v105, v105
	v_max_f32_e32 v106, v106, v106
	v_max_f32_e32 v107, v107, v107
	v_max_f32_e32 v108, v108, v108
	v_max_f32_e32 v109, v109, v109
	v_max_f32_e32 v110, v110, v110
	v_max_f32_e32 v111, v111, v111
	v_max_f32_e32 v112, v112, v112
	v_max_f32_e32 v113, v113, v113
	v_max_f32_e32 v114, v114, v114
	v_max_f32_e32 v115, v115, v115
	v_med3_f32 v100, v100, s20, v129
	v_med3_f32 v101, v101, s20, v129
	v_med3_f32 v102, v102, s20, v129
	v_med3_f32 v103, v103, s20, v129
	v_med3_f32 v104, v104, s20, v129
	v_med3_f32 v105, v105, s20, v129
	v_med3_f32 v106, v106, s20, v129
	v_med3_f32 v107, v107, s20, v129
	v_med3_f32 v108, v108, s20, v129
	v_med3_f32 v109, v109, s20, v129
	v_med3_f32 v110, v110, s20, v129
	v_med3_f32 v111, v111, s20, v129
	v_med3_f32 v112, v112, s20, v129
	v_med3_f32 v113, v113, s20, v129
	v_med3_f32 v114, v114, s20, v129
	v_med3_f32 v115, v115, s20, v129
	v_mov_b32_e32 v116, 0
	v_mov_b32_e32 v117, 0
	v_mov_b32_e32 v118, 0
	v_mov_b32_e32 v119, 0
	v_cvt_pk_fp8_f32 v116, v100, v101
	v_cvt_pk_fp8_f32 v117, v104, v105
	v_cvt_pk_fp8_f32 v118, v108, v109
	v_cvt_pk_fp8_f32 v119, v112, v113
	v_cvt_pk_fp8_f32 v116, v102, v103 op_sel:[0,0,1]
	v_cvt_pk_fp8_f32 v117, v106, v107 op_sel:[0,0,1]
	v_cvt_pk_fp8_f32 v118, v110, v111 op_sel:[0,0,1]
	v_cvt_pk_fp8_f32 v119, v114, v115 op_sel:[0,0,1]
	s_nop 0
	global_store_dwordx4 v127, v[116:119], s[14:15]
	ds_read_b32 v100, v124
	ds_read_b32 v101, v124 offset:512
	ds_read_b32 v102, v124 offset:1024
	ds_read_b32 v103, v124 offset:1536
	ds_read_b32 v104, v124 offset:2048
	ds_read_b32 v105, v124 offset:2560
	ds_read_b32 v106, v124 offset:3072
	ds_read_b32 v107, v124 offset:3584
	ds_read_b32 v108, v124 offset:4096
	ds_read_b32 v109, v124 offset:4608
	ds_read_b32 v110, v124 offset:5120
	ds_read_b32 v111, v124 offset:5632
	ds_read_b32 v112, v124 offset:6144
	ds_read_b32 v113, v124 offset:6656
	ds_read_b32 v114, v124 offset:7168
	ds_read_b32 v115, v124 offset:7680
	s_waitcnt lgkmcnt(0)
	v_max_f32_e32 v100, v100, v100
	v_max_f32_e32 v101, v101, v101
	v_max_f32_e32 v102, v102, v102
	v_max_f32_e32 v103, v103, v103
	v_max_f32_e32 v104, v104, v104
	v_max_f32_e32 v105, v105, v105
	v_max_f32_e32 v106, v106, v106
	v_max_f32_e32 v107, v107, v107
	v_max_f32_e32 v108, v108, v108
	v_max_f32_e32 v109, v109, v109
	v_max_f32_e32 v110, v110, v110
	v_max_f32_e32 v111, v111, v111
	v_max_f32_e32 v112, v112, v112
	v_max_f32_e32 v113, v113, v113
	v_max_f32_e32 v114, v114, v114
	v_max_f32_e32 v115, v115, v115
	v_med3_f32 v100, v100, s20, v129
	v_med3_f32 v101, v101, s20, v129
	v_med3_f32 v102, v102, s20, v129
	v_med3_f32 v103, v103, s20, v129
	v_med3_f32 v104, v104, s20, v129
	v_med3_f32 v105, v105, s20, v129
	v_med3_f32 v106, v106, s20, v129
	v_med3_f32 v107, v107, s20, v129
	v_med3_f32 v108, v108, s20, v129
	v_med3_f32 v109, v109, s20, v129
	v_med3_f32 v110, v110, s20, v129
	v_med3_f32 v111, v111, s20, v129
	v_med3_f32 v112, v112, s20, v129
	v_med3_f32 v113, v113, s20, v129
	v_med3_f32 v114, v114, s20, v129
	v_med3_f32 v115, v115, s20, v129
	v_mov_b32_e32 v116, 0
	v_mov_b32_e32 v117, 0
	v_mov_b32_e32 v118, 0
	v_mov_b32_e32 v119, 0
	v_cvt_pk_fp8_f32 v116, v100, v101
	v_cvt_pk_fp8_f32 v117, v104, v105
	v_cvt_pk_fp8_f32 v118, v108, v109
	v_cvt_pk_fp8_f32 v119, v112, v113
	v_cvt_pk_fp8_f32 v116, v102, v103 op_sel:[0,0,1]
	v_cvt_pk_fp8_f32 v117, v106, v107 op_sel:[0,0,1]
	v_cvt_pk_fp8_f32 v118, v110, v111 op_sel:[0,0,1]
	v_cvt_pk_fp8_f32 v119, v114, v115 op_sel:[0,0,1]
	s_nop 0
	global_store_dwordx4 v128, v[116:119], s[14:15]
	s_waitcnt vmcnt(12)
	v_mul_f32_e32 v68, 0x43000000, v68
	v_mul_f32_e32 v69, 0x43000000, v69
	v_mul_f32_e32 v70, 0x43000000, v70
	v_mul_f32_e32 v71, 0x43000000, v71
	ds_write_b128 v121, v[68:71]
	v_mul_f32_e32 v72, 0x43000000, v72
	v_mul_f32_e32 v73, 0x43000000, v73
	v_mul_f32_e32 v74, 0x43000000, v74
	v_mul_f32_e32 v75, 0x43000000, v75
	ds_write_b128 v121, v[72:75] offset:1024
	v_mul_f32_e32 v76, 0x43000000, v76
	v_mul_f32_e32 v77, 0x43000000, v77
	v_mul_f32_e32 v78, 0x43000000, v78
	v_mul_f32_e32 v79, 0x43000000, v79
	ds_write_b128 v121, v[76:79] offset:2048
	v_mul_f32_e32 v80, 0x43000000, v80
	v_mul_f32_e32 v81, 0x43000000, v81
	v_mul_f32_e32 v82, 0x43000000, v82
	v_mul_f32_e32 v83, 0x43000000, v83
	ds_write_b128 v121, v[80:83] offset:3072
	v_mul_f32_e32 v84, 0x43000000, v84
	v_mul_f32_e32 v85, 0x43000000, v85
	v_mul_f32_e32 v86, 0x43000000, v86
	v_mul_f32_e32 v87, 0x43000000, v87
	ds_write_b128 v121, v[84:87] offset:4096
	v_mul_f32_e32 v88, 0x43000000, v88
	v_mul_f32_e32 v89, 0x43000000, v89
	v_mul_f32_e32 v90, 0x43000000, v90
	v_mul_f32_e32 v91, 0x43000000, v91
	ds_write_b128 v121, v[88:91] offset:5120
	v_mul_f32_e32 v92, 0x43000000, v92
	v_mul_f32_e32 v93, 0x43000000, v93
	v_mul_f32_e32 v94, 0x43000000, v94
	v_mul_f32_e32 v95, 0x43000000, v95
	ds_write_b128 v121, v[92:95] offset:6144
	v_mul_f32_e32 v96, 0x43000000, v96
	v_mul_f32_e32 v97, 0x43000000, v97
	v_mul_f32_e32 v98, 0x43000000, v98
	v_mul_f32_e32 v99, 0x43000000, v99
	ds_write_b128 v121, v[96:99] offset:7168
	s_waitcnt lgkmcnt(0)
	s_barrier
; #define GAS __attribute__((address_space(1)))
; #define LAS __attribute__((address_space(3)))
; #define LDS_WAIT() asm volatile("s_waitcnt lgkmcnt(0)" ::: "memory")
;     const int pr = item >> 1, kb = 2 * (pr / nblk) + (item & 1), nb = pr % nblk, k0 = 64 * kb, n0 = 32 * nb;
;     const int nr = n0 + (lane & 31); const int sc = MAP == 1 ? src_col_in(nr) : nr;
;     float v[32];
; #pragma unroll
;     for (int i = 0; i < 32; ++i) v[i] = sc >= 0 ? W[(size_t)(k0 + 2 * i + (lane >> 5)) * Nsrc + sc] : 0.f;
; #pragma unroll
;     for (int i = 0; i < 32; ++i) { const int k = k0 + 2 * i + (lane >> 5); float x = v[i] * wscale; if (KS) x *= (k < ksplit ? ksA[k] : ksB[k - ksplit]); scr[(2 * i + (lane >> 5)) * 33 + (lane & 31)] = x; }
;     LDS_WAIT(); asm volatile("" ::: "memory");
;     const int c = lane & 7;
; #pragma unroll
;     for (int j = 0; j < 4; ++j) { const int n = (lane >> 3) + 8 * j; const LAS float* s = scr + (8 * c) * 33 + n;
;         const unsigned long long o = (unsigned long long)pg8::pk4_fp8(s[0 * 33], s[1 * 33], s[2 * 33], s[3 * 33]) | ((unsigned long long)pg8::pk4_fp8(s[4 * 33], s[5 * 33], s[6 * 33], s[7 * 33]) << 32);
;         *(GAS unsigned long long*)(WT + (size_t)(n0 + n) * K + k0 + 8 * c) = o; }
;     LDS_WAIT(); asm volatile("" ::: "memory");
; __global__ void __launch_bounds__(NWAVES * 64, 2) hybrid_fwd(Args args) {
;     ...
;             p0_transpose_item_f8<false>(args.in[16] + (size_t)l * FF * DM, FF, DM, DM / 32, (unsigned char*)(ws + WS_WDN + l * SZ_WDN), 128.f, args.in[16], args.in[16], 0, scr, r, lane);
	s_add_i32 s17, s16, 480
	s_min_u32 s17, s17, 0x7ff
	s_lshr_b32 s18, s17, 5
	s_add_i32 s18, s18, 64
	s_and_b32 s19, s17, 31
	s_lshl_b32 s18, s18, 21
	s_lshl_b32 s19, s19, 9
	s_add_u32 s18, s18, s19
	s_add_u32 s12, s2, s18
	s_addc_u32 s13, s3, 0
	global_load_dwordx4 v[68:71], v126, s[12:13]
	s_add_u32 s12, s12, 0x8000
	s_addc_u32 s13, s13, 0
	global_load_dwordx4 v[72:75], v126, s[12:13]
	s_add_u32 s12, s12, 0x8000
	s_addc_u32 s13, s13, 0
	global_load_dwordx4 v[76:79], v126, s[12:13]
	s_add_u32 s12, s12, 0x8000
	s_addc_u32 s13, s13, 0
	global_load_dwordx4 v[80:83], v126, s[12:13]
	s_add_u32 s12, s12, 0x8000
	s_addc_u32 s13, s13, 0
	global_load_dwordx4 v[84:87], v126, s[12:13]
	s_add_u32 s12, s12, 0x8000
	s_addc_u32 s13, s13, 0
	global_load_dwordx4 v[88:91], v126, s[12:13]
	s_add_u32 s12, s12, 0x8000
	s_addc_u32 s13, s13, 0
	global_load_dwordx4 v[92:95], v126, s[12:13]
	s_add_u32 s12, s12, 0x8000
	s_addc_u32 s13, s13, 0
	global_load_dwordx4 v[96:99], v126, s[12:13]
	s_add_i32 s17, s16, 288
	s_min_u32 s17, s17, 0x7ff
	s_lshr_b32 s18, s17, 5
	s_add_i32 s18, s18, 64
	s_and_b32 s19, s17, 31
	s_lshl_b32 s19, s19, 21
	s_lshl_b32 s18, s18, 7
	s_add_u32 s18, s18, s19
	s_add_u32 s14, s4, s18
	s_addc_u32 s15, s5, 0
	ds_read_b32 v100, v123
	ds_read_b32 v101, v123 offset:512
	ds_read_b32 v102, v123 offset:1024
	ds_read_b32 v103, v123 offset:1536
	ds_read_b32 v104, v123 offset:2048
	ds_read_b32 v105, v123 offset:2560
	ds_read_b32 v106, v123 offset:3072
	ds_read_b32 v107, v123 offset:3584
	ds_read_b32 v108, v123 offset:4096
	ds_read_b32 v109, v123 offset:4608
	ds_read_b32 v110, v123 offset:5120
	ds_read_b32 v111, v123 offset:5632
	ds_read_b32 v112, v123 offset:6144
	ds_read_b32 v113, v123 offset:6656
	ds_read_b32 v114, v123 offset:7168
	ds_read_b32 v115, v123 offset:7680
	s_waitcnt lgkmcnt(0)
	v_max_f32_e32 v100, v100, v100
	v_max_f32_e32 v101, v101, v101
	v_max_f32_e32 v102, v102, v102
	v_max_f32_e32 v103, v103, v103
	v_max_f32_e32 v104, v104, v104
	v_max_f32_e32 v105, v105, v105
	v_max_f32_e32 v106, v106, v106
	v_max_f32_e32 v107, v107, v107
	v_max_f32_e32 v108, v108, v108
	v_max_f32_e32 v109, v109, v109
	v_max_f32_e32 v110, v110, v110
	v_max_f32_e32 v111, v111, v111
	v_max_f32_e32 v112, v112, v112
	v_max_f32_e32 v113, v113, v113
	v_max_f32_e32 v114, v114, v114
	v_max_f32_e32 v115, v115, v115
	v_med3_f32 v100, v100, s20, v129
	v_med3_f32 v101, v101, s20, v129
	v_med3_f32 v102, v102, s20, v129
	v_med3_f32 v103, v103, s20, v129
	v_med3_f32 v104, v104, s20, v129
	v_med3_f32 v105, v105, s20, v129
	v_med3_f32 v106, v106, s20, v129
	v_med3_f32 v107, v107, s20, v129
	v_med3_f32 v108, v108, s20, v129
	v_med3_f32 v109, v109, s20, v129
	v_med3_f32 v110, v110, s20, v129
	v_med3_f32 v111, v111, s20, v129
	v_med3_f32 v112, v112, s20, v129
	v_med3_f32 v113, v113, s20, v129
	v_med3_f32 v114, v114, s20, v129
	v_med3_f32 v115, v115, s20, v129
	v_mov_b32_e32 v116, 0
	v_mov_b32_e32 v117, 0
	v_mov_b32_e32 v118, 0
	v_mov_b32_e32 v119, 0
	v_cvt_pk_fp8_f32 v116, v100, v101
	v_cvt_pk_fp8_f32 v117, v104, v105
	v_cvt_pk_fp8_f32 v118, v108, v109
	v_cvt_pk_fp8_f32 v119, v112, v113
	v_cvt_pk_fp8_f32 v116, v102, v103 op_sel:[0,0,1]
	v_cvt_pk_fp8_f32 v117, v106, v107 op_sel:[0,0,1]
	v_cvt_pk_fp8_f32 v118, v110, v111 op_sel:[0,0,1]
	v_cvt_pk_fp8_f32 v119, v114, v115 op_sel:[0,0,1]
	s_nop 0
	global_store_dwordx4 v127, v[116:119], s[14:15]
	ds_read_b32 v100, v125
	ds_read_b32 v101, v125 offset:512
	ds_read_b32 v102, v125 offset:1024
	ds_read_b32 v103, v125 offset:1536
	ds_read_b32 v104, v125 offset:2048
	ds_read_b32 v105, v125 offset:2560
	ds_read_b32 v106, v125 offset:3072
	ds_read_b32 v107, v125 offset:3584
	ds_read_b32 v108, v125 offset:4096
	ds_read_b32 v109, v125 offset:4608
	ds_read_b32 v110, v125 offset:5120
	ds_read_b32 v111, v125 offset:5632
	ds_read_b32 v112, v125 offset:6144
	ds_read_b32 v113, v125 offset:6656
	ds_read_b32 v114, v125 offset:7168
	ds_read_b32 v115, v125 offset:7680
	s_waitcnt lgkmcnt(0)
	v_max_f32_e32 v100, v100, v100
	v_max_f32_e32 v101, v101, v101
	v_max_f32_e32 v102, v102, v102
	v_max_f32_e32 v103, v103, v103
	v_max_f32_e32 v104, v104, v104
	v_max_f32_e32 v105, v105, v105
	v_max_f32_e32 v106, v106, v106
	v_max_f32_e32 v107, v107, v107
	v_max_f32_e32 v108, v108, v108
	v_max_f32_e32 v109, v109, v109
	v_max_f32_e32 v110, v110, v110
	v_max_f32_e32 v111, v111, v111
	v_max_f32_e32 v112, v112, v112
	v_max_f32_e32 v113, v113, v113
	v_max_f32_e32 v114, v114, v114
	v_max_f32_e32 v115, v115, v115
	v_med3_f32 v100, v100, s20, v129
	v_med3_f32 v101, v101, s20, v129
	v_med3_f32 v102, v102, s20, v129
	v_med3_f32 v103, v103, s20, v129
	v_med3_f32 v104, v104, s20, v129
	v_med3_f32 v105, v105, s20, v129
	v_med3_f32 v106, v106, s20, v129
	v_med3_f32 v107, v107, s20, v129
	v_med3_f32 v108, v108, s20, v129
	v_med3_f32 v109, v109, s20, v129
	v_med3_f32 v110, v110, s20, v129
	v_med3_f32 v111, v111, s20, v129
	v_med3_f32 v112, v112, s20, v129
	v_med3_f32 v113, v113, s20, v129
	v_med3_f32 v114, v114, s20, v129
	v_med3_f32 v115, v115, s20, v129
	v_mov_b32_e32 v116, 0
	v_mov_b32_e32 v117, 0
	v_mov_b32_e32 v118, 0
	v_mov_b32_e32 v119, 0
	v_cvt_pk_fp8_f32 v116, v100, v101
	v_cvt_pk_fp8_f32 v117, v104, v105
	v_cvt_pk_fp8_f32 v118, v108, v109
	v_cvt_pk_fp8_f32 v119, v112, v113
	v_cvt_pk_fp8_f32 v116, v102, v103 op_sel:[0,0,1]
	v_cvt_pk_fp8_f32 v117, v106, v107 op_sel:[0,0,1]
	v_cvt_pk_fp8_f32 v118, v110, v111 op_sel:[0,0,1]
	v_cvt_pk_fp8_f32 v119, v114, v115 op_sel:[0,0,1]
	s_nop 0
	global_store_dwordx4 v128, v[116:119], s[14:15]
	s_waitcnt vmcnt(12)
	v_mul_f32_e32 v36, 0x43000000, v36
	v_mul_f32_e32 v37, 0x43000000, v37
	v_mul_f32_e32 v38, 0x43000000, v38
	v_mul_f32_e32 v39, 0x43000000, v39
	ds_write_b128 v120, v[36:39]
	v_mul_f32_e32 v40, 0x43000000, v40
	v_mul_f32_e32 v41, 0x43000000, v41
	v_mul_f32_e32 v42, 0x43000000, v42
	v_mul_f32_e32 v43, 0x43000000, v43
	ds_write_b128 v120, v[40:43] offset:1024
	v_mul_f32_e32 v44, 0x43000000, v44
	v_mul_f32_e32 v45, 0x43000000, v45
	v_mul_f32_e32 v46, 0x43000000, v46
	v_mul_f32_e32 v47, 0x43000000, v47
	ds_write_b128 v120, v[44:47] offset:2048
	v_mul_f32_e32 v48, 0x43000000, v48
	v_mul_f32_e32 v49, 0x43000000, v49
	v_mul_f32_e32 v50, 0x43000000, v50
	v_mul_f32_e32 v51, 0x43000000, v51
	ds_write_b128 v120, v[48:51] offset:3072
	v_mul_f32_e32 v52, 0x43000000, v52
	v_mul_f32_e32 v53, 0x43000000, v53
	v_mul_f32_e32 v54, 0x43000000, v54
	v_mul_f32_e32 v55, 0x43000000, v55
	ds_write_b128 v120, v[52:55] offset:4096
	v_mul_f32_e32 v56, 0x43000000, v56
	v_mul_f32_e32 v57, 0x43000000, v57
	v_mul_f32_e32 v58, 0x43000000, v58
	v_mul_f32_e32 v59, 0x43000000, v59
	ds_write_b128 v120, v[56:59] offset:5120
	v_mul_f32_e32 v60, 0x43000000, v60
	v_mul_f32_e32 v61, 0x43000000, v61
	v_mul_f32_e32 v62, 0x43000000, v62
	v_mul_f32_e32 v63, 0x43000000, v63
	ds_write_b128 v120, v[60:63] offset:6144
	v_mul_f32_e32 v64, 0x43000000, v64
	v_mul_f32_e32 v65, 0x43000000, v65
	v_mul_f32_e32 v66, 0x43000000, v66
	v_mul_f32_e32 v67, 0x43000000, v67
	ds_write_b128 v120, v[64:67] offset:7168
	s_waitcnt lgkmcnt(0)
	s_barrier
; #define GAS __attribute__((address_space(1)))
; #define LAS __attribute__((address_space(3)))
; #define LDS_WAIT() asm volatile("s_waitcnt lgkmcnt(0)" ::: "memory")
;     const int pr = item >> 1, kb = 2 * (pr / nblk) + (item & 1), nb = pr % nblk, k0 = 64 * kb, n0 = 32 * nb;
;     const int nr = n0 + (lane & 31); const int sc = MAP == 1 ? src_col_in(nr) : nr;
;     float v[32];
; #pragma unroll
;     for (int i = 0; i < 32; ++i) v[i] = sc >= 0 ? W[(size_t)(k0 + 2 * i + (lane >> 5)) * Nsrc + sc] : 0.f;
; #pragma unroll
;     for (int i = 0; i < 32; ++i) { const int k = k0 + 2 * i + (lane >> 5); float x = v[i] * wscale; if (KS) x *= (k < ksplit ? ksA[k] : ksB[k - ksplit]); scr[(2 * i + (lane >> 5)) * 33 + (lane & 31)] = x; }
;     LDS_WAIT(); asm volatile("" ::: "memory");
;     const int c = lane & 7;
; #pragma unroll
;     for (int j = 0; j < 4; ++j) { const int n = (lane >> 3) + 8 * j; const LAS float* s = scr + (8 * c) * 33 + n;
;         const unsigned long long o = (unsigned long long)pg8::pk4_fp8(s[0 * 33], s[1 * 33], s[2 * 33], s[3 * 33]) | ((unsigned long long)pg8::pk4_fp8(s[4 * 33], s[5 * 33], s[6 * 33], s[7 * 33]) << 32);
;         *(GAS unsigned long long*)(WT + (size_t)(n0 + n) * K + k0 + 8 * c) = o; }
;     LDS_WAIT(); asm volatile("" ::: "memory");
; __global__ void __launch_bounds__(NWAVES * 64, 2) hybrid_fwd(Args args) {
;     ...
;             p0_transpose_item_f8<false>(args.in[16] + (size_t)l * FF * DM, FF, DM, DM / 32, (unsigned char*)(ws + WS_WDN + l * SZ_WDN), 128.f, args.in[16], args.in[16], 0, scr, r, lane);
	s_add_i32 s17, s16, 576
	s_min_u32 s17, s17, 0x7ff
	s_lshr_b32 s18, s17, 5
	s_add_i32 s18, s18, 64
	s_and_b32 s19, s17, 31
	s_lshl_b32 s18, s18, 21
	s_lshl_b32 s19, s19, 9
	s_add_u32 s18, s18, s19
	s_add_u32 s12, s2, s18
	s_addc_u32 s13, s3, 0
	global_load_dwordx4 v[36:39], v126, s[12:13]
	s_add_u32 s12, s12, 0x8000
	s_addc_u32 s13, s13, 0
	global_load_dwordx4 v[40:43], v126, s[12:13]
	s_add_u32 s12, s12, 0x8000
	s_addc_u32 s13, s13, 0
	global_load_dwordx4 v[44:47], v126, s[12:13]
	s_add_u32 s12, s12, 0x8000
	s_addc_u32 s13, s13, 0
	global_load_dwordx4 v[48:51], v126, s[12:13]
	s_add_u32 s12, s12, 0x8000
	s_addc_u32 s13, s13, 0
	global_load_dwordx4 v[52:55], v126, s[12:13]
	s_add_u32 s12, s12, 0x8000
	s_addc_u32 s13, s13, 0
	global_load_dwordx4 v[56:59], v126, s[12:13]
	s_add_u32 s12, s12, 0x8000
	s_addc_u32 s13, s13, 0
	global_load_dwordx4 v[60:63], v126, s[12:13]
	s_add_u32 s12, s12, 0x8000
	s_addc_u32 s13, s13, 0
	global_load_dwordx4 v[64:67], v126, s[12:13]
	s_add_i32 s17, s16, 384
	s_min_u32 s17, s17, 0x7ff
	s_lshr_b32 s18, s17, 5
	s_add_i32 s18, s18, 64
	s_and_b32 s19, s17, 31
	s_lshl_b32 s19, s19, 21
	s_lshl_b32 s18, s18, 7
	s_add_u32 s18, s18, s19
	s_add_u32 s14, s4, s18
	s_addc_u32 s15, s5, 0
	ds_read_b32 v100, v122
	ds_read_b32 v101, v122 offset:512
	ds_read_b32 v102, v122 offset:1024
	ds_read_b32 v103, v122 offset:1536
	ds_read_b32 v104, v122 offset:2048
	ds_read_b32 v105, v122 offset:2560
	ds_read_b32 v106, v122 offset:3072
	ds_read_b32 v107, v122 offset:3584
	ds_read_b32 v108, v122 offset:4096
	ds_read_b32 v109, v122 offset:4608
	ds_read_b32 v110, v122 offset:5120
	ds_read_b32 v111, v122 offset:5632
	ds_read_b32 v112, v122 offset:6144
	ds_read_b32 v113, v122 offset:6656
	ds_read_b32 v114, v122 offset:7168
	ds_read_b32 v115, v122 offset:7680
	s_waitcnt lgkmcnt(0)
	v_max_f32_e32 v100, v100, v100
	v_max_f32_e32 v101, v101, v101
	v_max_f32_e32 v102, v102, v102
	v_max_f32_e32 v103, v103, v103
	v_max_f32_e32 v104, v104, v104
	v_max_f32_e32 v105, v105, v105
	v_max_f32_e32 v106, v106, v106
	v_max_f32_e32 v107, v107, v107
	v_max_f32_e32 v108, v108, v108
	v_max_f32_e32 v109, v109, v109
	v_max_f32_e32 v110, v110, v110
	v_max_f32_e32 v111, v111, v111
	v_max_f32_e32 v112, v112, v112
	v_max_f32_e32 v113, v113, v113
	v_max_f32_e32 v114, v114, v114
	v_max_f32_e32 v115, v115, v115
	v_med3_f32 v100, v100, s20, v129
	v_med3_f32 v101, v101, s20, v129
	v_med3_f32 v102, v102, s20, v129
	v_med3_f32 v103, v103, s20, v129
	v_med3_f32 v104, v104, s20, v129
	v_med3_f32 v105, v105, s20, v129
	v_med3_f32 v106, v106, s20, v129
	v_med3_f32 v107, v107, s20, v129
	v_med3_f32 v108, v108, s20, v129
	v_med3_f32 v109, v109, s20, v129
	v_med3_f32 v110, v110, s20, v129
	v_med3_f32 v111, v111, s20, v129
	v_med3_f32 v112, v112, s20, v129
	v_med3_f32 v113, v113, s20, v129
	v_med3_f32 v114, v114, s20, v129
	v_med3_f32 v115, v115, s20, v129
	v_mov_b32_e32 v116, 0
	v_mov_b32_e32 v117, 0
	v_mov_b32_e32 v118, 0
	v_mov_b32_e32 v119, 0
	v_cvt_pk_fp8_f32 v116, v100, v101
	v_cvt_pk_fp8_f32 v117, v104, v105
	v_cvt_pk_fp8_f32 v118, v108, v109
	v_cvt_pk_fp8_f32 v119, v112, v113
	v_cvt_pk_fp8_f32 v116, v102, v103 op_sel:[0,0,1]
	v_cvt_pk_fp8_f32 v117, v106, v107 op_sel:[0,0,1]
	v_cvt_pk_fp8_f32 v118, v110, v111 op_sel:[0,0,1]
	v_cvt_pk_fp8_f32 v119, v114, v115 op_sel:[0,0,1]
	s_nop 0
	global_store_dwordx4 v127, v[116:119], s[14:15]
	ds_read_b32 v100, v124
	ds_read_b32 v101, v124 offset:512
	ds_read_b32 v102, v124 offset:1024
	ds_read_b32 v103, v124 offset:1536
	ds_read_b32 v104, v124 offset:2048
	ds_read_b32 v105, v124 offset:2560
	ds_read_b32 v106, v124 offset:3072
	ds_read_b32 v107, v124 offset:3584
	ds_read_b32 v108, v124 offset:4096
	ds_read_b32 v109, v124 offset:4608
	ds_read_b32 v110, v124 offset:5120
	ds_read_b32 v111, v124 offset:5632
	ds_read_b32 v112, v124 offset:6144
	ds_read_b32 v113, v124 offset:6656
	ds_read_b32 v114, v124 offset:7168
	ds_read_b32 v115, v124 offset:7680
	s_waitcnt lgkmcnt(0)
	v_max_f32_e32 v100, v100, v100
	v_max_f32_e32 v101, v101, v101
	v_max_f32_e32 v102, v102, v102
	v_max_f32_e32 v103, v103, v103
	v_max_f32_e32 v104, v104, v104
	v_max_f32_e32 v105, v105, v105
	v_max_f32_e32 v106, v106, v106
	v_max_f32_e32 v107, v107, v107
	v_max_f32_e32 v108, v108, v108
	v_max_f32_e32 v109, v109, v109
	v_max_f32_e32 v110, v110, v110
	v_max_f32_e32 v111, v111, v111
	v_max_f32_e32 v112, v112, v112
	v_max_f32_e32 v113, v113, v113
	v_max_f32_e32 v114, v114, v114
	v_max_f32_e32 v115, v115, v115
	v_med3_f32 v100, v100, s20, v129
	v_med3_f32 v101, v101, s20, v129
	v_med3_f32 v102, v102, s20, v129
	v_med3_f32 v103, v103, s20, v129
	v_med3_f32 v104, v104, s20, v129
	v_med3_f32 v105, v105, s20, v129
	v_med3_f32 v106, v106, s20, v129
	v_med3_f32 v107, v107, s20, v129
	v_med3_f32 v108, v108, s20, v129
	v_med3_f32 v109, v109, s20, v129
	v_med3_f32 v110, v110, s20, v129
	v_med3_f32 v111, v111, s20, v129
	v_med3_f32 v112, v112, s20, v129
	v_med3_f32 v113, v113, s20, v129
	v_med3_f32 v114, v114, s20, v129
	v_med3_f32 v115, v115, s20, v129
	v_mov_b32_e32 v116, 0
	v_mov_b32_e32 v117, 0
	v_mov_b32_e32 v118, 0
	v_mov_b32_e32 v119, 0
	v_cvt_pk_fp8_f32 v116, v100, v101
	v_cvt_pk_fp8_f32 v117, v104, v105
	v_cvt_pk_fp8_f32 v118, v108, v109
	v_cvt_pk_fp8_f32 v119, v112, v113
	v_cvt_pk_fp8_f32 v116, v102, v103 op_sel:[0,0,1]
	v_cvt_pk_fp8_f32 v117, v106, v107 op_sel:[0,0,1]
	v_cvt_pk_fp8_f32 v118, v110, v111 op_sel:[0,0,1]
	v_cvt_pk_fp8_f32 v119, v114, v115 op_sel:[0,0,1]
	s_nop 0
	global_store_dwordx4 v128, v[116:119], s[14:15]
	s_waitcnt vmcnt(12)
	v_mul_f32_e32 v68, 0x43000000, v68
	v_mul_f32_e32 v69, 0x43000000, v69
	v_mul_f32_e32 v70, 0x43000000, v70
	v_mul_f32_e32 v71, 0x43000000, v71
	ds_write_b128 v121, v[68:71]
	v_mul_f32_e32 v72, 0x43000000, v72
	v_mul_f32_e32 v73, 0x43000000, v73
	v_mul_f32_e32 v74, 0x43000000, v74
	v_mul_f32_e32 v75, 0x43000000, v75
	ds_write_b128 v121, v[72:75] offset:1024
	v_mul_f32_e32 v76, 0x43000000, v76
	v_mul_f32_e32 v77, 0x43000000, v77
	v_mul_f32_e32 v78, 0x43000000, v78
	v_mul_f32_e32 v79, 0x43000000, v79
	ds_write_b128 v121, v[76:79] offset:2048
	v_mul_f32_e32 v80, 0x43000000, v80
	v_mul_f32_e32 v81, 0x43000000, v81
	v_mul_f32_e32 v82, 0x43000000, v82
	v_mul_f32_e32 v83, 0x43000000, v83
	ds_write_b128 v121, v[80:83] offset:3072
	v_mul_f32_e32 v84, 0x43000000, v84
	v_mul_f32_e32 v85, 0x43000000, v85
	v_mul_f32_e32 v86, 0x43000000, v86
	v_mul_f32_e32 v87, 0x43000000, v87
	ds_write_b128 v121, v[84:87] offset:4096
	v_mul_f32_e32 v88, 0x43000000, v88
	v_mul_f32_e32 v89, 0x43000000, v89
	v_mul_f32_e32 v90, 0x43000000, v90
	v_mul_f32_e32 v91, 0x43000000, v91
	ds_write_b128 v121, v[88:91] offset:5120
	v_mul_f32_e32 v92, 0x43000000, v92
	v_mul_f32_e32 v93, 0x43000000, v93
	v_mul_f32_e32 v94, 0x43000000, v94
	v_mul_f32_e32 v95, 0x43000000, v95
	ds_write_b128 v121, v[92:95] offset:6144
	v_mul_f32_e32 v96, 0x43000000, v96
	v_mul_f32_e32 v97, 0x43000000, v97
	v_mul_f32_e32 v98, 0x43000000, v98
	v_mul_f32_e32 v99, 0x43000000, v99
	ds_write_b128 v121, v[96:99] offset:7168
	s_waitcnt lgkmcnt(0)
	s_barrier
; #define GAS __attribute__((address_space(1)))
; #define LAS __attribute__((address_space(3)))
; #define LDS_WAIT() asm volatile("s_waitcnt lgkmcnt(0)" ::: "memory")
;     const int pr = item >> 1, kb = 2 * (pr / nblk) + (item & 1), nb = pr % nblk, k0 = 64 * kb, n0 = 32 * nb;
;     const int nr = n0 + (lane & 31); const int sc = MAP == 1 ? src_col_in(nr) : nr;
;     float v[32];
; #pragma unroll
;     for (int i = 0; i < 32; ++i) v[i] = sc >= 0 ? W[(size_t)(k0 + 2 * i + (lane >> 5)) * Nsrc + sc] : 0.f;
; #pragma unroll
;     for (int i = 0; i < 32; ++i) { const int k = k0 + 2 * i + (lane >> 5); float x = v[i] * wscale; if (KS) x *= (k < ksplit ? ksA[k] : ksB[k - ksplit]); scr[(2 * i + (lane >> 5)) * 33 + (lane & 31)] = x; }
;     LDS_WAIT(); asm volatile("" ::: "memory");
;     const int c = lane & 7;
; #pragma unroll
;     for (int j = 0; j < 4; ++j) { const int n = (lane >> 3) + 8 * j; const LAS float* s = scr + (8 * c) * 33 + n;
;         const unsigned long long o = (unsigned long long)pg8::pk4_fp8(s[0 * 33], s[1 * 33], s[2 * 33], s[3 * 33]) | ((unsigned long long)pg8::pk4_fp8(s[4 * 33], s[5 * 33], s[6 * 33], s[7 * 33]) << 32);
;         *(GAS unsigned long long*)(WT + (size_t)(n0 + n) * K + k0 + 8 * c) = o; }
;     LDS_WAIT(); asm volatile("" ::: "memory");
; __global__ void __launch_bounds__(NWAVES * 64, 2) hybrid_fwd(Args args) {
;     ...
;             p0_transpose_item_f8<false>(args.in[16] + (size_t)l * FF * DM, FF, DM, DM / 32, (unsigned char*)(ws + WS_WDN + l * SZ_WDN), 128.f, args.in[16], args.in[16], 0, scr, r, lane);
	s_add_i32 s17, s16, 672
	s_min_u32 s17, s17, 0x7ff
	s_lshr_b32 s18, s17, 5
	s_add_i32 s18, s18, 64
	s_and_b32 s19, s17, 31
	s_lshl_b32 s18, s18, 21
	s_lshl_b32 s19, s19, 9
	s_add_u32 s18, s18, s19
	s_add_u32 s12, s2, s18
	s_addc_u32 s13, s3, 0
	global_load_dwordx4 v[68:71], v126, s[12:13]
	s_add_u32 s12, s12, 0x8000
	s_addc_u32 s13, s13, 0
	global_load_dwordx4 v[72:75], v126, s[12:13]
	s_add_u32 s12, s12, 0x8000
	s_addc_u32 s13, s13, 0
	global_load_dwordx4 v[76:79], v126, s[12:13]
	s_add_u32 s12, s12, 0x8000
	s_addc_u32 s13, s13, 0
	global_load_dwordx4 v[80:83], v126, s[12:13]
	s_add_u32 s12, s12, 0x8000
	s_addc_u32 s13, s13, 0
	global_load_dwordx4 v[84:87], v126, s[12:13]
	s_add_u32 s12, s12, 0x8000
	s_addc_u32 s13, s13, 0
	global_load_dwordx4 v[88:91], v126, s[12:13]
	s_add_u32 s12, s12, 0x8000
	s_addc_u32 s13, s13, 0
	global_load_dwordx4 v[92:95], v126, s[12:13]
	s_add_u32 s12, s12, 0x8000
	s_addc_u32 s13, s13, 0
	global_load_dwordx4 v[96:99], v126, s[12:13]
	s_add_i32 s17, s16, 480
	s_min_u32 s17, s17, 0x7ff
	s_lshr_b32 s18, s17, 5
	s_add_i32 s18, s18, 64
	s_and_b32 s19, s17, 31
	s_lshl_b32 s19, s19, 21
	s_lshl_b32 s18, s18, 7
	s_add_u32 s18, s18, s19
	s_add_u32 s14, s4, s18
	s_addc_u32 s15, s5, 0
	ds_read_b32 v100, v123
	ds_read_b32 v101, v123 offset:512
	ds_read_b32 v102, v123 offset:1024
	ds_read_b32 v103, v123 offset:1536
	ds_read_b32 v104, v123 offset:2048
	ds_read_b32 v105, v123 offset:2560
	ds_read_b32 v106, v123 offset:3072
	ds_read_b32 v107, v123 offset:3584
	ds_read_b32 v108, v123 offset:4096
	ds_read_b32 v109, v123 offset:4608
	ds_read_b32 v110, v123 offset:5120
	ds_read_b32 v111, v123 offset:5632
	ds_read_b32 v112, v123 offset:6144
	ds_read_b32 v113, v123 offset:6656
	ds_read_b32 v114, v123 offset:7168
	ds_read_b32 v115, v123 offset:7680
	s_waitcnt lgkmcnt(0)
	v_max_f32_e32 v100, v100, v100
	v_max_f32_e32 v101, v101, v101
	v_max_f32_e32 v102, v102, v102
	v_max_f32_e32 v103, v103, v103
	v_max_f32_e32 v104, v104, v104
	v_max_f32_e32 v105, v105, v105
	v_max_f32_e32 v106, v106, v106
	v_max_f32_e32 v107, v107, v107
	v_max_f32_e32 v108, v108, v108
	v_max_f32_e32 v109, v109, v109
	v_max_f32_e32 v110, v110, v110
	v_max_f32_e32 v111, v111, v111
	v_max_f32_e32 v112, v112, v112
	v_max_f32_e32 v113, v113, v113
	v_max_f32_e32 v114, v114, v114
	v_max_f32_e32 v115, v115, v115
	v_med3_f32 v100, v100, s20, v129
	v_med3_f32 v101, v101, s20, v129
	v_med3_f32 v102, v102, s20, v129
	v_med3_f32 v103, v103, s20, v129
	v_med3_f32 v104, v104, s20, v129
	v_med3_f32 v105, v105, s20, v129
	v_med3_f32 v106, v106, s20, v129
	v_med3_f32 v107, v107, s20, v129
	v_med3_f32 v108, v108, s20, v129
	v_med3_f32 v109, v109, s20, v129
	v_med3_f32 v110, v110, s20, v129
	v_med3_f32 v111, v111, s20, v129
	v_med3_f32 v112, v112, s20, v129
	v_med3_f32 v113, v113, s20, v129
	v_med3_f32 v114, v114, s20, v129
	v_med3_f32 v115, v115, s20, v129
	v_mov_b32_e32 v116, 0
	v_mov_b32_e32 v117, 0
	v_mov_b32_e32 v118, 0
	v_mov_b32_e32 v119, 0
	v_cvt_pk_fp8_f32 v116, v100, v101
	v_cvt_pk_fp8_f32 v117, v104, v105
	v_cvt_pk_fp8_f32 v118, v108, v109
	v_cvt_pk_fp8_f32 v119, v112, v113
	v_cvt_pk_fp8_f32 v116, v102, v103 op_sel:[0,0,1]
	v_cvt_pk_fp8_f32 v117, v106, v107 op_sel:[0,0,1]
	v_cvt_pk_fp8_f32 v118, v110, v111 op_sel:[0,0,1]
	v_cvt_pk_fp8_f32 v119, v114, v115 op_sel:[0,0,1]
	s_nop 0
	global_store_dwordx4 v127, v[116:119], s[14:15]
	ds_read_b32 v100, v125
	ds_read_b32 v101, v125 offset:512
	ds_read_b32 v102, v125 offset:1024
	ds_read_b32 v103, v125 offset:1536
	ds_read_b32 v104, v125 offset:2048
	ds_read_b32 v105, v125 offset:2560
	ds_read_b32 v106, v125 offset:3072
	ds_read_b32 v107, v125 offset:3584
	ds_read_b32 v108, v125 offset:4096
	ds_read_b32 v109, v125 offset:4608
	ds_read_b32 v110, v125 offset:5120
	ds_read_b32 v111, v125 offset:5632
	ds_read_b32 v112, v125 offset:6144
	ds_read_b32 v113, v125 offset:6656
	ds_read_b32 v114, v125 offset:7168
	ds_read_b32 v115, v125 offset:7680
	s_waitcnt lgkmcnt(0)
	v_max_f32_e32 v100, v100, v100
	v_max_f32_e32 v101, v101, v101
	v_max_f32_e32 v102, v102, v102
	v_max_f32_e32 v103, v103, v103
	v_max_f32_e32 v104, v104, v104
	v_max_f32_e32 v105, v105, v105
	v_max_f32_e32 v106, v106, v106
	v_max_f32_e32 v107, v107, v107
	v_max_f32_e32 v108, v108, v108
	v_max_f32_e32 v109, v109, v109
	v_max_f32_e32 v110, v110, v110
	v_max_f32_e32 v111, v111, v111
	v_max_f32_e32 v112, v112, v112
	v_max_f32_e32 v113, v113, v113
	v_max_f32_e32 v114, v114, v114
	v_max_f32_e32 v115, v115, v115
	v_med3_f32 v100, v100, s20, v129
	v_med3_f32 v101, v101, s20, v129
	v_med3_f32 v102, v102, s20, v129
	v_med3_f32 v103, v103, s20, v129
	v_med3_f32 v104, v104, s20, v129
	v_med3_f32 v105, v105, s20, v129
	v_med3_f32 v106, v106, s20, v129
	v_med3_f32 v107, v107, s20, v129
	v_med3_f32 v108, v108, s20, v129
	v_med3_f32 v109, v109, s20, v129
	v_med3_f32 v110, v110, s20, v129
	v_med3_f32 v111, v111, s20, v129
	v_med3_f32 v112, v112, s20, v129
	v_med3_f32 v113, v113, s20, v129
	v_med3_f32 v114, v114, s20, v129
	v_med3_f32 v115, v115, s20, v129
	v_mov_b32_e32 v116, 0
	v_mov_b32_e32 v117, 0
	v_mov_b32_e32 v118, 0
	v_mov_b32_e32 v119, 0
	v_cvt_pk_fp8_f32 v116, v100, v101
	v_cvt_pk_fp8_f32 v117, v104, v105
	v_cvt_pk_fp8_f32 v118, v108, v109
	v_cvt_pk_fp8_f32 v119, v112, v113
	v_cvt_pk_fp8_f32 v116, v102, v103 op_sel:[0,0,1]
	v_cvt_pk_fp8_f32 v117, v106, v107 op_sel:[0,0,1]
	v_cvt_pk_fp8_f32 v118, v110, v111 op_sel:[0,0,1]
	v_cvt_pk_fp8_f32 v119, v114, v115 op_sel:[0,0,1]
	s_nop 0
	global_store_dwordx4 v128, v[116:119], s[14:15]
	s_waitcnt vmcnt(12)
	v_mul_f32_e32 v36, 0x43000000, v36
	v_mul_f32_e32 v37, 0x43000000, v37
	v_mul_f32_e32 v38, 0x43000000, v38
	v_mul_f32_e32 v39, 0x43000000, v39
	ds_write_b128 v120, v[36:39]
	v_mul_f32_e32 v40, 0x43000000, v40
	v_mul_f32_e32 v41, 0x43000000, v41
	v_mul_f32_e32 v42, 0x43000000, v42
	v_mul_f32_e32 v43, 0x43000000, v43
	ds_write_b128 v120, v[40:43] offset:1024
	v_mul_f32_e32 v44, 0x43000000, v44
	v_mul_f32_e32 v45, 0x43000000, v45
	v_mul_f32_e32 v46, 0x43000000, v46
	v_mul_f32_e32 v47, 0x43000000, v47
	ds_write_b128 v120, v[44:47] offset:2048
	v_mul_f32_e32 v48, 0x43000000, v48
	v_mul_f32_e32 v49, 0x43000000, v49
	v_mul_f32_e32 v50, 0x43000000, v50
	v_mul_f32_e32 v51, 0x43000000, v51
	ds_write_b128 v120, v[48:51] offset:3072
	v_mul_f32_e32 v52, 0x43000000, v52
	v_mul_f32_e32 v53, 0x43000000, v53
	v_mul_f32_e32 v54, 0x43000000, v54
	v_mul_f32_e32 v55, 0x43000000, v55
	ds_write_b128 v120, v[52:55] offset:4096
	v_mul_f32_e32 v56, 0x43000000, v56
	v_mul_f32_e32 v57, 0x43000000, v57
	v_mul_f32_e32 v58, 0x43000000, v58
	v_mul_f32_e32 v59, 0x43000000, v59
	ds_write_b128 v120, v[56:59] offset:5120
	v_mul_f32_e32 v60, 0x43000000, v60
	v_mul_f32_e32 v61, 0x43000000, v61
	v_mul_f32_e32 v62, 0x43000000, v62
	v_mul_f32_e32 v63, 0x43000000, v63
	ds_write_b128 v120, v[60:63] offset:6144
	v_mul_f32_e32 v64, 0x43000000, v64
	v_mul_f32_e32 v65, 0x43000000, v65
	v_mul_f32_e32 v66, 0x43000000, v66
	v_mul_f32_e32 v67, 0x43000000, v67
	ds_write_b128 v120, v[64:67] offset:7168
	s_waitcnt lgkmcnt(0)
	s_barrier
; #define GAS __attribute__((address_space(1)))
; #define LAS __attribute__((address_space(3)))
; #define LDS_WAIT() asm volatile("s_waitcnt lgkmcnt(0)" ::: "memory")
;     const int pr = item >> 1, kb = 2 * (pr / nblk) + (item & 1), nb = pr % nblk, k0 = 64 * kb, n0 = 32 * nb;
;     const int nr = n0 + (lane & 31); const int sc = MAP == 1 ? src_col_in(nr) : nr;
;     float v[32];
; #pragma unroll
;     for (int i = 0; i < 32; ++i) v[i] = sc >= 0 ? W[(size_t)(k0 + 2 * i + (lane >> 5)) * Nsrc + sc] : 0.f;
; #pragma unroll
;     for (int i = 0; i < 32; ++i) { const int k = k0 + 2 * i + (lane >> 5); float x = v[i] * wscale; if (KS) x *= (k < ksplit ? ksA[k] : ksB[k - ksplit]); scr[(2 * i + (lane >> 5)) * 33 + (lane & 31)] = x; }
;     LDS_WAIT(); asm volatile("" ::: "memory");
;     const int c = lane & 7;
; #pragma unroll
;     for (int j = 0; j < 4; ++j) { const int n = (lane >> 3) + 8 * j; const LAS float* s = scr + (8 * c) * 33 + n;
;         const unsigned long long o = (unsigned long long)pg8::pk4_fp8(s[0 * 33], s[1 * 33], s[2 * 33], s[3 * 33]) | ((unsigned long long)pg8::pk4_fp8(s[4 * 33], s[5 * 33], s[6 * 33], s[7 * 33]) << 32);
;         *(GAS unsigned long long*)(WT + (size_t)(n0 + n) * K + k0 + 8 * c) = o; }
;     LDS_WAIT(); asm volatile("" ::: "memory");
; __global__ void __launch_bounds__(NWAVES * 64, 2) hybrid_fwd(Args args) {
;     ...
;             p0_transpose_item_f8<false>(args.in[16] + (size_t)l * FF * DM, FF, DM, DM / 32, (unsigned char*)(ws + WS_WDN + l * SZ_WDN), 128.f, args.in[16], args.in[16], 0, scr, r, lane);
	s_add_i32 s17, s16, 768
	s_min_u32 s17, s17, 0x7ff
	s_lshr_b32 s18, s17, 5
	s_add_i32 s18, s18, 64
	s_and_b32 s19, s17, 31
	s_lshl_b32 s18, s18, 21
	s_lshl_b32 s19, s19, 9
	s_add_u32 s18, s18, s19
	s_add_u32 s12, s2, s18
	s_addc_u32 s13, s3, 0
	global_load_dwordx4 v[36:39], v126, s[12:13]
	s_add_u32 s12, s12, 0x8000
	s_addc_u32 s13, s13, 0
	global_load_dwordx4 v[40:43], v126, s[12:13]
	s_add_u32 s12, s12, 0x8000
	s_addc_u32 s13, s13, 0
	global_load_dwordx4 v[44:47], v126, s[12:13]
	s_add_u32 s12, s12, 0x8000
	s_addc_u32 s13, s13, 0
	global_load_dwordx4 v[48:51], v126, s[12:13]
	s_add_u32 s12, s12, 0x8000
	s_addc_u32 s13, s13, 0
	global_load_dwordx4 v[52:55], v126, s[12:13]
	s_add_u32 s12, s12, 0x8000
	s_addc_u32 s13, s13, 0
	global_load_dwordx4 v[56:59], v126, s[12:13]
	s_add_u32 s12, s12, 0x8000
	s_addc_u32 s13, s13, 0
	global_load_dwordx4 v[60:63], v126, s[12:13]
	s_add_u32 s12, s12, 0x8000
	s_addc_u32 s13, s13, 0
	global_load_dwordx4 v[64:67], v126, s[12:13]
	s_add_i32 s17, s16, 576
	s_min_u32 s17, s17, 0x7ff
	s_lshr_b32 s18, s17, 5
	s_add_i32 s18, s18, 64
	s_and_b32 s19, s17, 31
	s_lshl_b32 s19, s19, 21
	s_lshl_b32 s18, s18, 7
	s_add_u32 s18, s18, s19
	s_add_u32 s14, s4, s18
	s_addc_u32 s15, s5, 0
	ds_read_b32 v100, v122
	ds_read_b32 v101, v122 offset:512
	ds_read_b32 v102, v122 offset:1024
	ds_read_b32 v103, v122 offset:1536
	ds_read_b32 v104, v122 offset:2048
	ds_read_b32 v105, v122 offset:2560
	ds_read_b32 v106, v122 offset:3072
	ds_read_b32 v107, v122 offset:3584
	ds_read_b32 v108, v122 offset:4096
	ds_read_b32 v109, v122 offset:4608
	ds_read_b32 v110, v122 offset:5120
	ds_read_b32 v111, v122 offset:5632
	ds_read_b32 v112, v122 offset:6144
	ds_read_b32 v113, v122 offset:6656
	ds_read_b32 v114, v122 offset:7168
	ds_read_b32 v115, v122 offset:7680
	s_waitcnt lgkmcnt(0)
	v_max_f32_e32 v100, v100, v100
	v_max_f32_e32 v101, v101, v101
	v_max_f32_e32 v102, v102, v102
	v_max_f32_e32 v103, v103, v103
	v_max_f32_e32 v104, v104, v104
	v_max_f32_e32 v105, v105, v105
	v_max_f32_e32 v106, v106, v106
	v_max_f32_e32 v107, v107, v107
	v_max_f32_e32 v108, v108, v108
	v_max_f32_e32 v109, v109, v109
	v_max_f32_e32 v110, v110, v110
	v_max_f32_e32 v111, v111, v111
	v_max_f32_e32 v112, v112, v112
	v_max_f32_e32 v113, v113, v113
	v_max_f32_e32 v114, v114, v114
	v_max_f32_e32 v115, v115, v115
	v_med3_f32 v100, v100, s20, v129
	v_med3_f32 v101, v101, s20, v129
	v_med3_f32 v102, v102, s20, v129
	v_med3_f32 v103, v103, s20, v129
	v_med3_f32 v104, v104, s20, v129
	v_med3_f32 v105, v105, s20, v129
	v_med3_f32 v106, v106, s20, v129
	v_med3_f32 v107, v107, s20, v129
	v_med3_f32 v108, v108, s20, v129
	v_med3_f32 v109, v109, s20, v129
	v_med3_f32 v110, v110, s20, v129
	v_med3_f32 v111, v111, s20, v129
	v_med3_f32 v112, v112, s20, v129
	v_med3_f32 v113, v113, s20, v129
	v_med3_f32 v114, v114, s20, v129
	v_med3_f32 v115, v115, s20, v129
	v_mov_b32_e32 v116, 0
	v_mov_b32_e32 v117, 0
	v_mov_b32_e32 v118, 0
	v_mov_b32_e32 v119, 0
	v_cvt_pk_fp8_f32 v116, v100, v101
	v_cvt_pk_fp8_f32 v117, v104, v105
	v_cvt_pk_fp8_f32 v118, v108, v109
	v_cvt_pk_fp8_f32 v119, v112, v113
	v_cvt_pk_fp8_f32 v116, v102, v103 op_sel:[0,0,1]
	v_cvt_pk_fp8_f32 v117, v106, v107 op_sel:[0,0,1]
	v_cvt_pk_fp8_f32 v118, v110, v111 op_sel:[0,0,1]
	v_cvt_pk_fp8_f32 v119, v114, v115 op_sel:[0,0,1]
	s_nop 0
	global_store_dwordx4 v127, v[116:119], s[14:15]
	ds_read_b32 v100, v124
	ds_read_b32 v101, v124 offset:512
	ds_read_b32 v102, v124 offset:1024
	ds_read_b32 v103, v124 offset:1536
	ds_read_b32 v104, v124 offset:2048
	ds_read_b32 v105, v124 offset:2560
	ds_read_b32 v106, v124 offset:3072
	ds_read_b32 v107, v124 offset:3584
	ds_read_b32 v108, v124 offset:4096
	ds_read_b32 v109, v124 offset:4608
	ds_read_b32 v110, v124 offset:5120
	ds_read_b32 v111, v124 offset:5632
	ds_read_b32 v112, v124 offset:6144
	ds_read_b32 v113, v124 offset:6656
	ds_read_b32 v114, v124 offset:7168
	ds_read_b32 v115, v124 offset:7680
	s_waitcnt lgkmcnt(0)
	v_max_f32_e32 v100, v100, v100
	v_max_f32_e32 v101, v101, v101
	v_max_f32_e32 v102, v102, v102
	v_max_f32_e32 v103, v103, v103
	v_max_f32_e32 v104, v104, v104
	v_max_f32_e32 v105, v105, v105
	v_max_f32_e32 v106, v106, v106
	v_max_f32_e32 v107, v107, v107
	v_max_f32_e32 v108, v108, v108
	v_max_f32_e32 v109, v109, v109
	v_max_f32_e32 v110, v110, v110
	v_max_f32_e32 v111, v111, v111
	v_max_f32_e32 v112, v112, v112
	v_max_f32_e32 v113, v113, v113
	v_max_f32_e32 v114, v114, v114
	v_max_f32_e32 v115, v115, v115
	v_med3_f32 v100, v100, s20, v129
	v_med3_f32 v101, v101, s20, v129
	v_med3_f32 v102, v102, s20, v129
	v_med3_f32 v103, v103, s20, v129
	v_med3_f32 v104, v104, s20, v129
	v_med3_f32 v105, v105, s20, v129
	v_med3_f32 v106, v106, s20, v129
	v_med3_f32 v107, v107, s20, v129
	v_med3_f32 v108, v108, s20, v129
	v_med3_f32 v109, v109, s20, v129
	v_med3_f32 v110, v110, s20, v129
	v_med3_f32 v111, v111, s20, v129
	v_med3_f32 v112, v112, s20, v129
	v_med3_f32 v113, v113, s20, v129
	v_med3_f32 v114, v114, s20, v129
	v_med3_f32 v115, v115, s20, v129
	v_mov_b32_e32 v116, 0
	v_mov_b32_e32 v117, 0
	v_mov_b32_e32 v118, 0
	v_mov_b32_e32 v119, 0
	v_cvt_pk_fp8_f32 v116, v100, v101
	v_cvt_pk_fp8_f32 v117, v104, v105
	v_cvt_pk_fp8_f32 v118, v108, v109
	v_cvt_pk_fp8_f32 v119, v112, v113
	v_cvt_pk_fp8_f32 v116, v102, v103 op_sel:[0,0,1]
	v_cvt_pk_fp8_f32 v117, v106, v107 op_sel:[0,0,1]
	v_cvt_pk_fp8_f32 v118, v110, v111 op_sel:[0,0,1]
	v_cvt_pk_fp8_f32 v119, v114, v115 op_sel:[0,0,1]
	s_nop 0
	global_store_dwordx4 v128, v[116:119], s[14:15]
	s_waitcnt vmcnt(12)
	v_mul_f32_e32 v68, 0x43000000, v68
	v_mul_f32_e32 v69, 0x43000000, v69
	v_mul_f32_e32 v70, 0x43000000, v70
	v_mul_f32_e32 v71, 0x43000000, v71
	ds_write_b128 v121, v[68:71]
	v_mul_f32_e32 v72, 0x43000000, v72
	v_mul_f32_e32 v73, 0x43000000, v73
	v_mul_f32_e32 v74, 0x43000000, v74
	v_mul_f32_e32 v75, 0x43000000, v75
	ds_write_b128 v121, v[72:75] offset:1024
	v_mul_f32_e32 v76, 0x43000000, v76
	v_mul_f32_e32 v77, 0x43000000, v77
	v_mul_f32_e32 v78, 0x43000000, v78
	v_mul_f32_e32 v79, 0x43000000, v79
	ds_write_b128 v121, v[76:79] offset:2048
	v_mul_f32_e32 v80, 0x43000000, v80
	v_mul_f32_e32 v81, 0x43000000, v81
	v_mul_f32_e32 v82, 0x43000000, v82
	v_mul_f32_e32 v83, 0x43000000, v83
	ds_write_b128 v121, v[80:83] offset:3072
	v_mul_f32_e32 v84, 0x43000000, v84
	v_mul_f32_e32 v85, 0x43000000, v85
	v_mul_f32_e32 v86, 0x43000000, v86
	v_mul_f32_e32 v87, 0x43000000, v87
	ds_write_b128 v121, v[84:87] offset:4096
	v_mul_f32_e32 v88, 0x43000000, v88
	v_mul_f32_e32 v89, 0x43000000, v89
	v_mul_f32_e32 v90, 0x43000000, v90
	v_mul_f32_e32 v91, 0x43000000, v91
	ds_write_b128 v121, v[88:91] offset:5120
	v_mul_f32_e32 v92, 0x43000000, v92
	v_mul_f32_e32 v93, 0x43000000, v93
	v_mul_f32_e32 v94, 0x43000000, v94
	v_mul_f32_e32 v95, 0x43000000, v95
	ds_write_b128 v121, v[92:95] offset:6144
	v_mul_f32_e32 v96, 0x43000000, v96
	v_mul_f32_e32 v97, 0x43000000, v97
	v_mul_f32_e32 v98, 0x43000000, v98
	v_mul_f32_e32 v99, 0x43000000, v99
	ds_write_b128 v121, v[96:99] offset:7168
	s_waitcnt lgkmcnt(0)
	s_barrier
; #define GAS __attribute__((address_space(1)))
; #define LAS __attribute__((address_space(3)))
; #define LDS_WAIT() asm volatile("s_waitcnt lgkmcnt(0)" ::: "memory")
;     const int pr = item >> 1, kb = 2 * (pr / nblk) + (item & 1), nb = pr % nblk, k0 = 64 * kb, n0 = 32 * nb;
;     const int nr = n0 + (lane & 31); const int sc = MAP == 1 ? src_col_in(nr) : nr;
;     float v[32];
; #pragma unroll
;     for (int i = 0; i < 32; ++i) v[i] = sc >= 0 ? W[(size_t)(k0 + 2 * i + (lane >> 5)) * Nsrc + sc] : 0.f;
; #pragma unroll
;     for (int i = 0; i < 32; ++i) { const int k = k0 + 2 * i + (lane >> 5); float x = v[i] * wscale; if (KS) x *= (k < ksplit ? ksA[k] : ksB[k - ksplit]); scr[(2 * i + (lane >> 5)) * 33 + (lane & 31)] = x; }
;     LDS_WAIT(); asm volatile("" ::: "memory");
;     const int c = lane & 7;
; #pragma unroll
;     for (int j = 0; j < 4; ++j) { const int n = (lane >> 3) + 8 * j; const LAS float* s = scr + (8 * c) * 33 + n;
;         const unsigned long long o = (unsigned long long)pg8::pk4_fp8(s[0 * 33], s[1 * 33], s[2 * 33], s[3 * 33]) | ((unsigned long long)pg8::pk4_fp8(s[4 * 33], s[5 * 33], s[6 * 33], s[7 * 33]) << 32);
;         *(GAS unsigned long long*)(WT + (size_t)(n0 + n) * K + k0 + 8 * c) = o; }
;     LDS_WAIT(); asm volatile("" ::: "memory");
; __global__ void __launch_bounds__(NWAVES * 64, 2) hybrid_fwd(Args args) {
;     ...
;             p0_transpose_item_f8<false>(args.in[16] + (size_t)l * FF * DM, FF, DM, DM / 32, (unsigned char*)(ws + WS_WDN + l * SZ_WDN), 128.f, args.in[16], args.in[16], 0, scr, r, lane);
	s_add_i32 s17, s16, 864
	s_min_u32 s17, s17, 0x7ff
	s_lshr_b32 s18, s17, 5
	s_add_i32 s18, s18, 64
	s_and_b32 s19, s17, 31
	s_lshl_b32 s18, s18, 21
	s_lshl_b32 s19, s19, 9
	s_add_u32 s18, s18, s19
	s_add_u32 s12, s2, s18
	s_addc_u32 s13, s3, 0
	global_load_dwordx4 v[68:71], v126, s[12:13]
	s_add_u32 s12, s12, 0x8000
	s_addc_u32 s13, s13, 0
	global_load_dwordx4 v[72:75], v126, s[12:13]
	s_add_u32 s12, s12, 0x8000
	s_addc_u32 s13, s13, 0
	global_load_dwordx4 v[76:79], v126, s[12:13]
	s_add_u32 s12, s12, 0x8000
	s_addc_u32 s13, s13, 0
	global_load_dwordx4 v[80:83], v126, s[12:13]
	s_add_u32 s12, s12, 0x8000
	s_addc_u32 s13, s13, 0
	global_load_dwordx4 v[84:87], v126, s[12:13]
	s_add_u32 s12, s12, 0x8000
	s_addc_u32 s13, s13, 0
	global_load_dwordx4 v[88:91], v126, s[12:13]
	s_add_u32 s12, s12, 0x8000
	s_addc_u32 s13, s13, 0
	global_load_dwordx4 v[92:95], v126, s[12:13]
	s_add_u32 s12, s12, 0x8000
	s_addc_u32 s13, s13, 0
	global_load_dwordx4 v[96:99], v126, s[12:13]
	s_add_i32 s17, s16, 672
	s_min_u32 s17, s17, 0x7ff
	s_lshr_b32 s18, s17, 5
	s_add_i32 s18, s18, 64
	s_and_b32 s19, s17, 31
	s_lshl_b32 s19, s19, 21
	s_lshl_b32 s18, s18, 7
	s_add_u32 s18, s18, s19
	s_add_u32 s14, s4, s18
	s_addc_u32 s15, s5, 0
	ds_read_b32 v100, v123
	ds_read_b32 v101, v123 offset:512
	ds_read_b32 v102, v123 offset:1024
	ds_read_b32 v103, v123 offset:1536
	ds_read_b32 v104, v123 offset:2048
	ds_read_b32 v105, v123 offset:2560
	ds_read_b32 v106, v123 offset:3072
	ds_read_b32 v107, v123 offset:3584
	ds_read_b32 v108, v123 offset:4096
	ds_read_b32 v109, v123 offset:4608
	ds_read_b32 v110, v123 offset:5120
	ds_read_b32 v111, v123 offset:5632
	ds_read_b32 v112, v123 offset:6144
	ds_read_b32 v113, v123 offset:6656
	ds_read_b32 v114, v123 offset:7168
	ds_read_b32 v115, v123 offset:7680
	s_waitcnt lgkmcnt(0)
	v_max_f32_e32 v100, v100, v100
	v_max_f32_e32 v101, v101, v101
	v_max_f32_e32 v102, v102, v102
	v_max_f32_e32 v103, v103, v103
	v_max_f32_e32 v104, v104, v104
	v_max_f32_e32 v105, v105, v105
	v_max_f32_e32 v106, v106, v106
	v_max_f32_e32 v107, v107, v107
	v_max_f32_e32 v108, v108, v108
	v_max_f32_e32 v109, v109, v109
	v_max_f32_e32 v110, v110, v110
	v_max_f32_e32 v111, v111, v111
	v_max_f32_e32 v112, v112, v112
	v_max_f32_e32 v113, v113, v113
	v_max_f32_e32 v114, v114, v114
	v_max_f32_e32 v115, v115, v115
	v_med3_f32 v100, v100, s20, v129
	v_med3_f32 v101, v101, s20, v129
	v_med3_f32 v102, v102, s20, v129
	v_med3_f32 v103, v103, s20, v129
	v_med3_f32 v104, v104, s20, v129
	v_med3_f32 v105, v105, s20, v129
	v_med3_f32 v106, v106, s20, v129
	v_med3_f32 v107, v107, s20, v129
	v_med3_f32 v108, v108, s20, v129
	v_med3_f32 v109, v109, s20, v129
	v_med3_f32 v110, v110, s20, v129
	v_med3_f32 v111, v111, s20, v129
	v_med3_f32 v112, v112, s20, v129
	v_med3_f32 v113, v113, s20, v129
	v_med3_f32 v114, v114, s20, v129
	v_med3_f32 v115, v115, s20, v129
	v_mov_b32_e32 v116, 0
	v_mov_b32_e32 v117, 0
	v_mov_b32_e32 v118, 0
	v_mov_b32_e32 v119, 0
	v_cvt_pk_fp8_f32 v116, v100, v101
	v_cvt_pk_fp8_f32 v117, v104, v105
	v_cvt_pk_fp8_f32 v118, v108, v109
	v_cvt_pk_fp8_f32 v119, v112, v113
	v_cvt_pk_fp8_f32 v116, v102, v103 op_sel:[0,0,1]
	v_cvt_pk_fp8_f32 v117, v106, v107 op_sel:[0,0,1]
	v_cvt_pk_fp8_f32 v118, v110, v111 op_sel:[0,0,1]
	v_cvt_pk_fp8_f32 v119, v114, v115 op_sel:[0,0,1]
	s_nop 0
	global_store_dwordx4 v127, v[116:119], s[14:15]
	ds_read_b32 v100, v125
	ds_read_b32 v101, v125 offset:512
	ds_read_b32 v102, v125 offset:1024
	ds_read_b32 v103, v125 offset:1536
	ds_read_b32 v104, v125 offset:2048
	ds_read_b32 v105, v125 offset:2560
	ds_read_b32 v106, v125 offset:3072
	ds_read_b32 v107, v125 offset:3584
	ds_read_b32 v108, v125 offset:4096
	ds_read_b32 v109, v125 offset:4608
	ds_read_b32 v110, v125 offset:5120
	ds_read_b32 v111, v125 offset:5632
	ds_read_b32 v112, v125 offset:6144
	ds_read_b32 v113, v125 offset:6656
	ds_read_b32 v114, v125 offset:7168
	ds_read_b32 v115, v125 offset:7680
	s_waitcnt lgkmcnt(0)
	v_max_f32_e32 v100, v100, v100
	v_max_f32_e32 v101, v101, v101
	v_max_f32_e32 v102, v102, v102
	v_max_f32_e32 v103, v103, v103
	v_max_f32_e32 v104, v104, v104
	v_max_f32_e32 v105, v105, v105
	v_max_f32_e32 v106, v106, v106
	v_max_f32_e32 v107, v107, v107
	v_max_f32_e32 v108, v108, v108
	v_max_f32_e32 v109, v109, v109
	v_max_f32_e32 v110, v110, v110
	v_max_f32_e32 v111, v111, v111
	v_max_f32_e32 v112, v112, v112
	v_max_f32_e32 v113, v113, v113
	v_max_f32_e32 v114, v114, v114
	v_max_f32_e32 v115, v115, v115
	v_med3_f32 v100, v100, s20, v129
	v_med3_f32 v101, v101, s20, v129
	v_med3_f32 v102, v102, s20, v129
	v_med3_f32 v103, v103, s20, v129
	v_med3_f32 v104, v104, s20, v129
	v_med3_f32 v105, v105, s20, v129
	v_med3_f32 v106, v106, s20, v129
	v_med3_f32 v107, v107, s20, v129
	v_med3_f32 v108, v108, s20, v129
	v_med3_f32 v109, v109, s20, v129
	v_med3_f32 v110, v110, s20, v129
	v_med3_f32 v111, v111, s20, v129
	v_med3_f32 v112, v112, s20, v129
	v_med3_f32 v113, v113, s20, v129
	v_med3_f32 v114, v114, s20, v129
	v_med3_f32 v115, v115, s20, v129
	v_mov_b32_e32 v116, 0
	v_mov_b32_e32 v117, 0
	v_mov_b32_e32 v118, 0
	v_mov_b32_e32 v119, 0
	v_cvt_pk_fp8_f32 v116, v100, v101
	v_cvt_pk_fp8_f32 v117, v104, v105
	v_cvt_pk_fp8_f32 v118, v108, v109
	v_cvt_pk_fp8_f32 v119, v112, v113
	v_cvt_pk_fp8_f32 v116, v102, v103 op_sel:[0,0,1]
	v_cvt_pk_fp8_f32 v117, v106, v107 op_sel:[0,0,1]
	v_cvt_pk_fp8_f32 v118, v110, v111 op_sel:[0,0,1]
	v_cvt_pk_fp8_f32 v119, v114, v115 op_sel:[0,0,1]
	s_nop 0
	global_store_dwordx4 v128, v[116:119], s[14:15]
	s_waitcnt vmcnt(12)
	v_mul_f32_e32 v36, 0x43000000, v36
	v_mul_f32_e32 v37, 0x43000000, v37
	v_mul_f32_e32 v38, 0x43000000, v38
	v_mul_f32_e32 v39, 0x43000000, v39
	ds_write_b128 v120, v[36:39]
	v_mul_f32_e32 v40, 0x43000000, v40
	v_mul_f32_e32 v41, 0x43000000, v41
	v_mul_f32_e32 v42, 0x43000000, v42
	v_mul_f32_e32 v43, 0x43000000, v43
	ds_write_b128 v120, v[40:43] offset:1024
	v_mul_f32_e32 v44, 0x43000000, v44
	v_mul_f32_e32 v45, 0x43000000, v45
	v_mul_f32_e32 v46, 0x43000000, v46
	v_mul_f32_e32 v47, 0x43000000, v47
	ds_write_b128 v120, v[44:47] offset:2048
	v_mul_f32_e32 v48, 0x43000000, v48
	v_mul_f32_e32 v49, 0x43000000, v49
	v_mul_f32_e32 v50, 0x43000000, v50
	v_mul_f32_e32 v51, 0x43000000, v51
	ds_write_b128 v120, v[48:51] offset:3072
	v_mul_f32_e32 v52, 0x43000000, v52
	v_mul_f32_e32 v53, 0x43000000, v53
	v_mul_f32_e32 v54, 0x43000000, v54
	v_mul_f32_e32 v55, 0x43000000, v55
	ds_write_b128 v120, v[52:55] offset:4096
	v_mul_f32_e32 v56, 0x43000000, v56
	v_mul_f32_e32 v57, 0x43000000, v57
	v_mul_f32_e32 v58, 0x43000000, v58
	v_mul_f32_e32 v59, 0x43000000, v59
	ds_write_b128 v120, v[56:59] offset:5120
	v_mul_f32_e32 v60, 0x43000000, v60
	v_mul_f32_e32 v61, 0x43000000, v61
	v_mul_f32_e32 v62, 0x43000000, v62
	v_mul_f32_e32 v63, 0x43000000, v63
	ds_write_b128 v120, v[60:63] offset:6144
	v_mul_f32_e32 v64, 0x43000000, v64
	v_mul_f32_e32 v65, 0x43000000, v65
	v_mul_f32_e32 v66, 0x43000000, v66
	v_mul_f32_e32 v67, 0x43000000, v67
	ds_write_b128 v120, v[64:67] offset:7168
	s_waitcnt lgkmcnt(0)
	s_barrier
; #define GAS __attribute__((address_space(1)))
; #define LAS __attribute__((address_space(3)))
; #define LDS_WAIT() asm volatile("s_waitcnt lgkmcnt(0)" ::: "memory")
;     const int pr = item >> 1, kb = 2 * (pr / nblk) + (item & 1), nb = pr % nblk, k0 = 64 * kb, n0 = 32 * nb;
;     const int nr = n0 + (lane & 31); const int sc = MAP == 1 ? src_col_in(nr) : nr;
;     float v[32];
; #pragma unroll
;     for (int i = 0; i < 32; ++i) v[i] = sc >= 0 ? W[(size_t)(k0 + 2 * i + (lane >> 5)) * Nsrc + sc] : 0.f;
; #pragma unroll
;     for (int i = 0; i < 32; ++i) { const int k = k0 + 2 * i + (lane >> 5); float x = v[i] * wscale; if (KS) x *= (k < ksplit ? ksA[k] : ksB[k - ksplit]); scr[(2 * i + (lane >> 5)) * 33 + (lane & 31)] = x; }
;     LDS_WAIT(); asm volatile("" ::: "memory");
;     const int c = lane & 7;
; #pragma unroll
;     for (int j = 0; j < 4; ++j) { const int n = (lane >> 3) + 8 * j; const LAS float* s = scr + (8 * c) * 33 + n;
;         const unsigned long long o = (unsigned long long)pg8::pk4_fp8(s[0 * 33], s[1 * 33], s[2 * 33], s[3 * 33]) | ((unsigned long long)pg8::pk4_fp8(s[4 * 33], s[5 * 33], s[6 * 33], s[7 * 33]) << 32);
;         *(GAS unsigned long long*)(WT + (size_t)(n0 + n) * K + k0 + 8 * c) = o; }
;     LDS_WAIT(); asm volatile("" ::: "memory");
; __global__ void __launch_bounds__(NWAVES * 64, 2) hybrid_fwd(Args args) {
;     ...
;             p0_transpose_item_f8<false>(args.in[16] + (size_t)l * FF * DM, FF, DM, DM / 32, (unsigned char*)(ws + WS_WDN + l * SZ_WDN), 128.f, args.in[16], args.in[16], 0, scr, r, lane);
	s_add_i32 s17, s16, 960
	s_min_u32 s17, s17, 0x7ff
	s_lshr_b32 s18, s17, 5
	s_add_i32 s18, s18, 64
	s_and_b32 s19, s17, 31
	s_lshl_b32 s18, s18, 21
	s_lshl_b32 s19, s19, 9
	s_add_u32 s18, s18, s19
	s_add_u32 s12, s2, s18
	s_addc_u32 s13, s3, 0
	global_load_dwordx4 v[36:39], v126, s[12:13]
	s_add_u32 s12, s12, 0x8000
	s_addc_u32 s13, s13, 0
	global_load_dwordx4 v[40:43], v126, s[12:13]
	s_add_u32 s12, s12, 0x8000
	s_addc_u32 s13, s13, 0
	global_load_dwordx4 v[44:47], v126, s[12:13]
	s_add_u32 s12, s12, 0x8000
	s_addc_u32 s13, s13, 0
	global_load_dwordx4 v[48:51], v126, s[12:13]
	s_add_u32 s12, s12, 0x8000
	s_addc_u32 s13, s13, 0
	global_load_dwordx4 v[52:55], v126, s[12:13]
	s_add_u32 s12, s12, 0x8000
	s_addc_u32 s13, s13, 0
	global_load_dwordx4 v[56:59], v126, s[12:13]
	s_add_u32 s12, s12, 0x8000
	s_addc_u32 s13, s13, 0
	global_load_dwordx4 v[60:63], v126, s[12:13]
	s_add_u32 s12, s12, 0x8000
	s_addc_u32 s13, s13, 0
	global_load_dwordx4 v[64:67], v126, s[12:13]
	s_add_i32 s17, s16, 768
	s_min_u32 s17, s17, 0x7ff
	s_lshr_b32 s18, s17, 5
	s_add_i32 s18, s18, 64
	s_and_b32 s19, s17, 31
	s_lshl_b32 s19, s19, 21
	s_lshl_b32 s18, s18, 7
	s_add_u32 s18, s18, s19
	s_add_u32 s14, s4, s18
	s_addc_u32 s15, s5, 0
	ds_read_b32 v100, v122
	ds_read_b32 v101, v122 offset:512
	ds_read_b32 v102, v122 offset:1024
	ds_read_b32 v103, v122 offset:1536
	ds_read_b32 v104, v122 offset:2048
	ds_read_b32 v105, v122 offset:2560
	ds_read_b32 v106, v122 offset:3072
	ds_read_b32 v107, v122 offset:3584
	ds_read_b32 v108, v122 offset:4096
	ds_read_b32 v109, v122 offset:4608
	ds_read_b32 v110, v122 offset:5120
	ds_read_b32 v111, v122 offset:5632
	ds_read_b32 v112, v122 offset:6144
	ds_read_b32 v113, v122 offset:6656
	ds_read_b32 v114, v122 offset:7168
	ds_read_b32 v115, v122 offset:7680
	s_waitcnt lgkmcnt(0)
	v_max_f32_e32 v100, v100, v100
	v_max_f32_e32 v101, v101, v101
	v_max_f32_e32 v102, v102, v102
	v_max_f32_e32 v103, v103, v103
	v_max_f32_e32 v104, v104, v104
	v_max_f32_e32 v105, v105, v105
	v_max_f32_e32 v106, v106, v106
	v_max_f32_e32 v107, v107, v107
	v_max_f32_e32 v108, v108, v108
	v_max_f32_e32 v109, v109, v109
	v_max_f32_e32 v110, v110, v110
	v_max_f32_e32 v111, v111, v111
	v_max_f32_e32 v112, v112, v112
	v_max_f32_e32 v113, v113, v113
	v_max_f32_e32 v114, v114, v114
	v_max_f32_e32 v115, v115, v115
	v_med3_f32 v100, v100, s20, v129
	v_med3_f32 v101, v101, s20, v129
	v_med3_f32 v102, v102, s20, v129
	v_med3_f32 v103, v103, s20, v129
	v_med3_f32 v104, v104, s20, v129
	v_med3_f32 v105, v105, s20, v129
	v_med3_f32 v106, v106, s20, v129
	v_med3_f32 v107, v107, s20, v129
	v_med3_f32 v108, v108, s20, v129
	v_med3_f32 v109, v109, s20, v129
	v_med3_f32 v110, v110, s20, v129
	v_med3_f32 v111, v111, s20, v129
	v_med3_f32 v112, v112, s20, v129
	v_med3_f32 v113, v113, s20, v129
	v_med3_f32 v114, v114, s20, v129
	v_med3_f32 v115, v115, s20, v129
	v_mov_b32_e32 v116, 0
	v_mov_b32_e32 v117, 0
	v_mov_b32_e32 v118, 0
	v_mov_b32_e32 v119, 0
	v_cvt_pk_fp8_f32 v116, v100, v101
	v_cvt_pk_fp8_f32 v117, v104, v105
	v_cvt_pk_fp8_f32 v118, v108, v109
	v_cvt_pk_fp8_f32 v119, v112, v113
	v_cvt_pk_fp8_f32 v116, v102, v103 op_sel:[0,0,1]
	v_cvt_pk_fp8_f32 v117, v106, v107 op_sel:[0,0,1]
	v_cvt_pk_fp8_f32 v118, v110, v111 op_sel:[0,0,1]
	v_cvt_pk_fp8_f32 v119, v114, v115 op_sel:[0,0,1]
	s_nop 0
	global_store_dwordx4 v127, v[116:119], s[14:15]
	ds_read_b32 v100, v124
	ds_read_b32 v101, v124 offset:512
	ds_read_b32 v102, v124 offset:1024
	ds_read_b32 v103, v124 offset:1536
	ds_read_b32 v104, v124 offset:2048
	ds_read_b32 v105, v124 offset:2560
	ds_read_b32 v106, v124 offset:3072
	ds_read_b32 v107, v124 offset:3584
	ds_read_b32 v108, v124 offset:4096
	ds_read_b32 v109, v124 offset:4608
	ds_read_b32 v110, v124 offset:5120
	ds_read_b32 v111, v124 offset:5632
	ds_read_b32 v112, v124 offset:6144
	ds_read_b32 v113, v124 offset:6656
	ds_read_b32 v114, v124 offset:7168
	ds_read_b32 v115, v124 offset:7680
	s_waitcnt lgkmcnt(0)
	v_max_f32_e32 v100, v100, v100
	v_max_f32_e32 v101, v101, v101
	v_max_f32_e32 v102, v102, v102
	v_max_f32_e32 v103, v103, v103
	v_max_f32_e32 v104, v104, v104
	v_max_f32_e32 v105, v105, v105
	v_max_f32_e32 v106, v106, v106
	v_max_f32_e32 v107, v107, v107
	v_max_f32_e32 v108, v108, v108
	v_max_f32_e32 v109, v109, v109
	v_max_f32_e32 v110, v110, v110
	v_max_f32_e32 v111, v111, v111
	v_max_f32_e32 v112, v112, v112
	v_max_f32_e32 v113, v113, v113
	v_max_f32_e32 v114, v114, v114
	v_max_f32_e32 v115, v115, v115
	v_med3_f32 v100, v100, s20, v129
	v_med3_f32 v101, v101, s20, v129
	v_med3_f32 v102, v102, s20, v129
	v_med3_f32 v103, v103, s20, v129
	v_med3_f32 v104, v104, s20, v129
	v_med3_f32 v105, v105, s20, v129
	v_med3_f32 v106, v106, s20, v129
	v_med3_f32 v107, v107, s20, v129
	v_med3_f32 v108, v108, s20, v129
	v_med3_f32 v109, v109, s20, v129
	v_med3_f32 v110, v110, s20, v129
	v_med3_f32 v111, v111, s20, v129
	v_med3_f32 v112, v112, s20, v129
	v_med3_f32 v113, v113, s20, v129
	v_med3_f32 v114, v114, s20, v129
	v_med3_f32 v115, v115, s20, v129
	v_mov_b32_e32 v116, 0
	v_mov_b32_e32 v117, 0
	v_mov_b32_e32 v118, 0
	v_mov_b32_e32 v119, 0
	v_cvt_pk_fp8_f32 v116, v100, v101
	v_cvt_pk_fp8_f32 v117, v104, v105
	v_cvt_pk_fp8_f32 v118, v108, v109
	v_cvt_pk_fp8_f32 v119, v112, v113
	v_cvt_pk_fp8_f32 v116, v102, v103 op_sel:[0,0,1]
	v_cvt_pk_fp8_f32 v117, v106, v107 op_sel:[0,0,1]
	v_cvt_pk_fp8_f32 v118, v110, v111 op_sel:[0,0,1]
	v_cvt_pk_fp8_f32 v119, v114, v115 op_sel:[0,0,1]
	s_nop 0
	global_store_dwordx4 v128, v[116:119], s[14:15]
	s_waitcnt vmcnt(12)
	v_mul_f32_e32 v68, 0x43000000, v68
	v_mul_f32_e32 v69, 0x43000000, v69
	v_mul_f32_e32 v70, 0x43000000, v70
	v_mul_f32_e32 v71, 0x43000000, v71
	ds_write_b128 v121, v[68:71]
	v_mul_f32_e32 v72, 0x43000000, v72
	v_mul_f32_e32 v73, 0x43000000, v73
	v_mul_f32_e32 v74, 0x43000000, v74
	v_mul_f32_e32 v75, 0x43000000, v75
	ds_write_b128 v121, v[72:75] offset:1024
	v_mul_f32_e32 v76, 0x43000000, v76
	v_mul_f32_e32 v77, 0x43000000, v77
	v_mul_f32_e32 v78, 0x43000000, v78
	v_mul_f32_e32 v79, 0x43000000, v79
	ds_write_b128 v121, v[76:79] offset:2048
	v_mul_f32_e32 v80, 0x43000000, v80
	v_mul_f32_e32 v81, 0x43000000, v81
	v_mul_f32_e32 v82, 0x43000000, v82
	v_mul_f32_e32 v83, 0x43000000, v83
	ds_write_b128 v121, v[80:83] offset:3072
	v_mul_f32_e32 v84, 0x43000000, v84
	v_mul_f32_e32 v85, 0x43000000, v85
	v_mul_f32_e32 v86, 0x43000000, v86
	v_mul_f32_e32 v87, 0x43000000, v87
	ds_write_b128 v121, v[84:87] offset:4096
	v_mul_f32_e32 v88, 0x43000000, v88
	v_mul_f32_e32 v89, 0x43000000, v89
	v_mul_f32_e32 v90, 0x43000000, v90
	v_mul_f32_e32 v91, 0x43000000, v91
	ds_write_b128 v121, v[88:91] offset:5120
	v_mul_f32_e32 v92, 0x43000000, v92
	v_mul_f32_e32 v93, 0x43000000, v93
	v_mul_f32_e32 v94, 0x43000000, v94
	v_mul_f32_e32 v95, 0x43000000, v95
	ds_write_b128 v121, v[92:95] offset:6144
	v_mul_f32_e32 v96, 0x43000000, v96
	v_mul_f32_e32 v97, 0x43000000, v97
	v_mul_f32_e32 v98, 0x43000000, v98
	v_mul_f32_e32 v99, 0x43000000, v99
	ds_write_b128 v121, v[96:99] offset:7168
	s_waitcnt lgkmcnt(0)
	s_barrier
; #define GAS __attribute__((address_space(1)))
; #define LAS __attribute__((address_space(3)))
; #define LDS_WAIT() asm volatile("s_waitcnt lgkmcnt(0)" ::: "memory")
;     const int pr = item >> 1, kb = 2 * (pr / nblk) + (item & 1), nb = pr % nblk, k0 = 64 * kb, n0 = 32 * nb;
;     const int nr = n0 + (lane & 31); const int sc = MAP == 1 ? src_col_in(nr) : nr;
;     float v[32];
; #pragma unroll
;     for (int i = 0; i < 32; ++i) v[i] = sc >= 0 ? W[(size_t)(k0 + 2 * i + (lane >> 5)) * Nsrc + sc] : 0.f;
; #pragma unroll
;     for (int i = 0; i < 32; ++i) { const int k = k0 + 2 * i + (lane >> 5); float x = v[i] * wscale; if (KS) x *= (k < ksplit ? ksA[k] : ksB[k - ksplit]); scr[(2 * i + (lane >> 5)) * 33 + (lane & 31)] = x; }
;     LDS_WAIT(); asm volatile("" ::: "memory");
;     const int c = lane & 7;
; #pragma unroll
;     for (int j = 0; j < 4; ++j) { const int n = (lane >> 3) + 8 * j; const LAS float* s = scr + (8 * c) * 33 + n;
;         const unsigned long long o = (unsigned long long)pg8::pk4_fp8(s[0 * 33], s[1 * 33], s[2 * 33], s[3 * 33]) | ((unsigned long long)pg8::pk4_fp8(s[4 * 33], s[5 * 33], s[6 * 33], s[7 * 33]) << 32);
;         *(GAS unsigned long long*)(WT + (size_t)(n0 + n) * K + k0 + 8 * c) = o; }
;     LDS_WAIT(); asm volatile("" ::: "memory");
; __global__ void __launch_bounds__(NWAVES * 64, 2) hybrid_fwd(Args args) {
;     ...
;             p0_transpose_item_f8<false>(args.in[16] + (size_t)l * FF * DM, FF, DM, DM / 32, (unsigned char*)(ws + WS_WDN + l * SZ_WDN), 128.f, args.in[16], args.in[16], 0, scr, r, lane);
	s_add_i32 s17, s16, 1056
	s_min_u32 s17, s17, 0x7ff
	s_lshr_b32 s18, s17, 5
	s_add_i32 s18, s18, 64
	s_and_b32 s19, s17, 31
	s_lshl_b32 s18, s18, 21
	s_lshl_b32 s19, s19, 9
	s_add_u32 s18, s18, s19
	s_add_u32 s12, s2, s18
	s_addc_u32 s13, s3, 0
	global_load_dwordx4 v[68:71], v126, s[12:13]
	s_add_u32 s12, s12, 0x8000
	s_addc_u32 s13, s13, 0
	global_load_dwordx4 v[72:75], v126, s[12:13]
	s_add_u32 s12, s12, 0x8000
	s_addc_u32 s13, s13, 0
	global_load_dwordx4 v[76:79], v126, s[12:13]
	s_add_u32 s12, s12, 0x8000
	s_addc_u32 s13, s13, 0
	global_load_dwordx4 v[80:83], v126, s[12:13]
	s_add_u32 s12, s12, 0x8000
	s_addc_u32 s13, s13, 0
	global_load_dwordx4 v[84:87], v126, s[12:13]
	s_add_u32 s12, s12, 0x8000
	s_addc_u32 s13, s13, 0
	global_load_dwordx4 v[88:91], v126, s[12:13]
	s_add_u32 s12, s12, 0x8000
	s_addc_u32 s13, s13, 0
	global_load_dwordx4 v[92:95], v126, s[12:13]
	s_add_u32 s12, s12, 0x8000
	s_addc_u32 s13, s13, 0
	global_load_dwordx4 v[96:99], v126, s[12:13]
	s_add_i32 s17, s16, 864
	s_min_u32 s17, s17, 0x7ff
	s_lshr_b32 s18, s17, 5
	s_add_i32 s18, s18, 64
	s_and_b32 s19, s17, 31
	s_lshl_b32 s19, s19, 21
	s_lshl_b32 s18, s18, 7
	s_add_u32 s18, s18, s19
	s_add_u32 s14, s4, s18
	s_addc_u32 s15, s5, 0
	ds_read_b32 v100, v123
	ds_read_b32 v101, v123 offset:512
	ds_read_b32 v102, v123 offset:1024
	ds_read_b32 v103, v123 offset:1536
	ds_read_b32 v104, v123 offset:2048
	ds_read_b32 v105, v123 offset:2560
	ds_read_b32 v106, v123 offset:3072
	ds_read_b32 v107, v123 offset:3584
	ds_read_b32 v108, v123 offset:4096
	ds_read_b32 v109, v123 offset:4608
	ds_read_b32 v110, v123 offset:5120
	ds_read_b32 v111, v123 offset:5632
	ds_read_b32 v112, v123 offset:6144
	ds_read_b32 v113, v123 offset:6656
	ds_read_b32 v114, v123 offset:7168
	ds_read_b32 v115, v123 offset:7680
	s_waitcnt lgkmcnt(0)
	v_max_f32_e32 v100, v100, v100
	v_max_f32_e32 v101, v101, v101
	v_max_f32_e32 v102, v102, v102
	v_max_f32_e32 v103, v103, v103
	v_max_f32_e32 v104, v104, v104
	v_max_f32_e32 v105, v105, v105
	v_max_f32_e32 v106, v106, v106
	v_max_f32_e32 v107, v107, v107
	v_max_f32_e32 v108, v108, v108
	v_max_f32_e32 v109, v109, v109
	v_max_f32_e32 v110, v110, v110
	v_max_f32_e32 v111, v111, v111
	v_max_f32_e32 v112, v112, v112
	v_max_f32_e32 v113, v113, v113
	v_max_f32_e32 v114, v114, v114
	v_max_f32_e32 v115, v115, v115
	v_med3_f32 v100, v100, s20, v129
	v_med3_f32 v101, v101, s20, v129
	v_med3_f32 v102, v102, s20, v129
	v_med3_f32 v103, v103, s20, v129
	v_med3_f32 v104, v104, s20, v129
	v_med3_f32 v105, v105, s20, v129
	v_med3_f32 v106, v106, s20, v129
	v_med3_f32 v107, v107, s20, v129
	v_med3_f32 v108, v108, s20, v129
	v_med3_f32 v109, v109, s20, v129
	v_med3_f32 v110, v110, s20, v129
	v_med3_f32 v111, v111, s20, v129
	v_med3_f32 v112, v112, s20, v129
	v_med3_f32 v113, v113, s20, v129
	v_med3_f32 v114, v114, s20, v129
	v_med3_f32 v115, v115, s20, v129
	v_mov_b32_e32 v116, 0
	v_mov_b32_e32 v117, 0
	v_mov_b32_e32 v118, 0
	v_mov_b32_e32 v119, 0
	v_cvt_pk_fp8_f32 v116, v100, v101
	v_cvt_pk_fp8_f32 v117, v104, v105
	v_cvt_pk_fp8_f32 v118, v108, v109
	v_cvt_pk_fp8_f32 v119, v112, v113
	v_cvt_pk_fp8_f32 v116, v102, v103 op_sel:[0,0,1]
	v_cvt_pk_fp8_f32 v117, v106, v107 op_sel:[0,0,1]
	v_cvt_pk_fp8_f32 v118, v110, v111 op_sel:[0,0,1]
	v_cvt_pk_fp8_f32 v119, v114, v115 op_sel:[0,0,1]
	s_nop 0
	global_store_dwordx4 v127, v[116:119], s[14:15]
	ds_read_b32 v100, v125
	ds_read_b32 v101, v125 offset:512
	ds_read_b32 v102, v125 offset:1024
	ds_read_b32 v103, v125 offset:1536
	ds_read_b32 v104, v125 offset:2048
	ds_read_b32 v105, v125 offset:2560
	ds_read_b32 v106, v125 offset:3072
	ds_read_b32 v107, v125 offset:3584
	ds_read_b32 v108, v125 offset:4096
	ds_read_b32 v109, v125 offset:4608
	ds_read_b32 v110, v125 offset:5120
	ds_read_b32 v111, v125 offset:5632
	ds_read_b32 v112, v125 offset:6144
	ds_read_b32 v113, v125 offset:6656
	ds_read_b32 v114, v125 offset:7168
	ds_read_b32 v115, v125 offset:7680
	s_waitcnt lgkmcnt(0)
	v_max_f32_e32 v100, v100, v100
	v_max_f32_e32 v101, v101, v101
	v_max_f32_e32 v102, v102, v102
	v_max_f32_e32 v103, v103, v103
	v_max_f32_e32 v104, v104, v104
	v_max_f32_e32 v105, v105, v105
	v_max_f32_e32 v106, v106, v106
	v_max_f32_e32 v107, v107, v107
	v_max_f32_e32 v108, v108, v108
	v_max_f32_e32 v109, v109, v109
	v_max_f32_e32 v110, v110, v110
	v_max_f32_e32 v111, v111, v111
	v_max_f32_e32 v112, v112, v112
	v_max_f32_e32 v113, v113, v113
	v_max_f32_e32 v114, v114, v114
	v_max_f32_e32 v115, v115, v115
	v_med3_f32 v100, v100, s20, v129
	v_med3_f32 v101, v101, s20, v129
	v_med3_f32 v102, v102, s20, v129
	v_med3_f32 v103, v103, s20, v129
	v_med3_f32 v104, v104, s20, v129
	v_med3_f32 v105, v105, s20, v129
	v_med3_f32 v106, v106, s20, v129
	v_med3_f32 v107, v107, s20, v129
	v_med3_f32 v108, v108, s20, v129
	v_med3_f32 v109, v109, s20, v129
	v_med3_f32 v110, v110, s20, v129
	v_med3_f32 v111, v111, s20, v129
	v_med3_f32 v112, v112, s20, v129
	v_med3_f32 v113, v113, s20, v129
	v_med3_f32 v114, v114, s20, v129
	v_med3_f32 v115, v115, s20, v129
	v_mov_b32_e32 v116, 0
	v_mov_b32_e32 v117, 0
	v_mov_b32_e32 v118, 0
	v_mov_b32_e32 v119, 0
	v_cvt_pk_fp8_f32 v116, v100, v101
	v_cvt_pk_fp8_f32 v117, v104, v105
	v_cvt_pk_fp8_f32 v118, v108, v109
	v_cvt_pk_fp8_f32 v119, v112, v113
	v_cvt_pk_fp8_f32 v116, v102, v103 op_sel:[0,0,1]
	v_cvt_pk_fp8_f32 v117, v106, v107 op_sel:[0,0,1]
	v_cvt_pk_fp8_f32 v118, v110, v111 op_sel:[0,0,1]
	v_cvt_pk_fp8_f32 v119, v114, v115 op_sel:[0,0,1]
	s_nop 0
	global_store_dwordx4 v128, v[116:119], s[14:15]
	s_waitcnt vmcnt(12)
	v_mul_f32_e32 v36, 0x43000000, v36
	v_mul_f32_e32 v37, 0x43000000, v37
	v_mul_f32_e32 v38, 0x43000000, v38
	v_mul_f32_e32 v39, 0x43000000, v39
	ds_write_b128 v120, v[36:39]
	v_mul_f32_e32 v40, 0x43000000, v40
	v_mul_f32_e32 v41, 0x43000000, v41
	v_mul_f32_e32 v42, 0x43000000, v42
	v_mul_f32_e32 v43, 0x43000000, v43
	ds_write_b128 v120, v[40:43] offset:1024
	v_mul_f32_e32 v44, 0x43000000, v44
	v_mul_f32_e32 v45, 0x43000000, v45
	v_mul_f32_e32 v46, 0x43000000, v46
	v_mul_f32_e32 v47, 0x43000000, v47
	ds_write_b128 v120, v[44:47] offset:2048
	v_mul_f32_e32 v48, 0x43000000, v48
	v_mul_f32_e32 v49, 0x43000000, v49
	v_mul_f32_e32 v50, 0x43000000, v50
	v_mul_f32_e32 v51, 0x43000000, v51
	ds_write_b128 v120, v[48:51] offset:3072
	v_mul_f32_e32 v52, 0x43000000, v52
	v_mul_f32_e32 v53, 0x43000000, v53
	v_mul_f32_e32 v54, 0x43000000, v54
	v_mul_f32_e32 v55, 0x43000000, v55
	ds_write_b128 v120, v[52:55] offset:4096
	v_mul_f32_e32 v56, 0x43000000, v56
	v_mul_f32_e32 v57, 0x43000000, v57
	v_mul_f32_e32 v58, 0x43000000, v58
	v_mul_f32_e32 v59, 0x43000000, v59
	ds_write_b128 v120, v[56:59] offset:5120
	v_mul_f32_e32 v60, 0x43000000, v60
	v_mul_f32_e32 v61, 0x43000000, v61
	v_mul_f32_e32 v62, 0x43000000, v62
	v_mul_f32_e32 v63, 0x43000000, v63
	ds_write_b128 v120, v[60:63] offset:6144
	v_mul_f32_e32 v64, 0x43000000, v64
	v_mul_f32_e32 v65, 0x43000000, v65
	v_mul_f32_e32 v66, 0x43000000, v66
	v_mul_f32_e32 v67, 0x43000000, v67
	ds_write_b128 v120, v[64:67] offset:7168
	s_waitcnt lgkmcnt(0)
	s_barrier
; #define GAS __attribute__((address_space(1)))
; #define LAS __attribute__((address_space(3)))
; #define LDS_WAIT() asm volatile("s_waitcnt lgkmcnt(0)" ::: "memory")
;     const int pr = item >> 1, kb = 2 * (pr / nblk) + (item & 1), nb = pr % nblk, k0 = 64 * kb, n0 = 32 * nb;
;     const int nr = n0 + (lane & 31); const int sc = MAP == 1 ? src_col_in(nr) : nr;
;     float v[32];
; #pragma unroll
;     for (int i = 0; i < 32; ++i) v[i] = sc >= 0 ? W[(size_t)(k0 + 2 * i + (lane >> 5)) * Nsrc + sc] : 0.f;
; #pragma unroll
;     for (int i = 0; i < 32; ++i) { const int k = k0 + 2 * i + (lane >> 5); float x = v[i] * wscale; if (KS) x *= (k < ksplit ? ksA[k] : ksB[k - ksplit]); scr[(2 * i + (lane >> 5)) * 33 + (lane & 31)] = x; }
;     LDS_WAIT(); asm volatile("" ::: "memory");
;     const int c = lane & 7;
; #pragma unroll
;     for (int j = 0; j < 4; ++j) { const int n = (lane >> 3) + 8 * j; const LAS float* s = scr + (8 * c) * 33 + n;
;         const unsigned long long o = (unsigned long long)pg8::pk4_fp8(s[0 * 33], s[1 * 33], s[2 * 33], s[3 * 33]) | ((unsigned long long)pg8::pk4_fp8(s[4 * 33], s[5 * 33], s[6 * 33], s[7 * 33]) << 32);
;         *(GAS unsigned long long*)(WT + (size_t)(n0 + n) * K + k0 + 8 * c) = o; }
;     LDS_WAIT(); asm volatile("" ::: "memory");
; __global__ void __launch_bounds__(NWAVES * 64, 2) hybrid_fwd(Args args) {
;     ...
;             p0_transpose_item_f8<false>(args.in[16] + (size_t)l * FF * DM, FF, DM, DM / 32, (unsigned char*)(ws + WS_WDN + l * SZ_WDN), 128.f, args.in[16], args.in[16], 0, scr, r, lane);
	s_add_i32 s17, s16, 1152
	s_min_u32 s17, s17, 0x7ff
	s_lshr_b32 s18, s17, 5
	s_add_i32 s18, s18, 64
	s_and_b32 s19, s17, 31
	s_lshl_b32 s18, s18, 21
	s_lshl_b32 s19, s19, 9
	s_add_u32 s18, s18, s19
	s_add_u32 s12, s2, s18
	s_addc_u32 s13, s3, 0
	global_load_dwordx4 v[36:39], v126, s[12:13]
	s_add_u32 s12, s12, 0x8000
	s_addc_u32 s13, s13, 0
	global_load_dwordx4 v[40:43], v126, s[12:13]
	s_add_u32 s12, s12, 0x8000
	s_addc_u32 s13, s13, 0
	global_load_dwordx4 v[44:47], v126, s[12:13]
	s_add_u32 s12, s12, 0x8000
	s_addc_u32 s13, s13, 0
	global_load_dwordx4 v[48:51], v126, s[12:13]
	s_add_u32 s12, s12, 0x8000
	s_addc_u32 s13, s13, 0
	global_load_dwordx4 v[52:55], v126, s[12:13]
	s_add_u32 s12, s12, 0x8000
	s_addc_u32 s13, s13, 0
	global_load_dwordx4 v[56:59], v126, s[12:13]
	s_add_u32 s12, s12, 0x8000
	s_addc_u32 s13, s13, 0
	global_load_dwordx4 v[60:63], v126, s[12:13]
	s_add_u32 s12, s12, 0x8000
	s_addc_u32 s13, s13, 0
	global_load_dwordx4 v[64:67], v126, s[12:13]
	s_add_i32 s17, s16, 960
	s_min_u32 s17, s17, 0x7ff
	s_lshr_b32 s18, s17, 5
	s_add_i32 s18, s18, 64
	s_and_b32 s19, s17, 31
	s_lshl_b32 s19, s19, 21
	s_lshl_b32 s18, s18, 7
	s_add_u32 s18, s18, s19
	s_add_u32 s14, s4, s18
	s_addc_u32 s15, s5, 0
	ds_read_b32 v100, v122
	ds_read_b32 v101, v122 offset:512
	ds_read_b32 v102, v122 offset:1024
	ds_read_b32 v103, v122 offset:1536
	ds_read_b32 v104, v122 offset:2048
	ds_read_b32 v105, v122 offset:2560
	ds_read_b32 v106, v122 offset:3072
	ds_read_b32 v107, v122 offset:3584
	ds_read_b32 v108, v122 offset:4096
	ds_read_b32 v109, v122 offset:4608
	ds_read_b32 v110, v122 offset:5120
	ds_read_b32 v111, v122 offset:5632
	ds_read_b32 v112, v122 offset:6144
	ds_read_b32 v113, v122 offset:6656
	ds_read_b32 v114, v122 offset:7168
	ds_read_b32 v115, v122 offset:7680
	s_waitcnt lgkmcnt(0)
	v_max_f32_e32 v100, v100, v100
	v_max_f32_e32 v101, v101, v101
	v_max_f32_e32 v102, v102, v102
	v_max_f32_e32 v103, v103, v103
	v_max_f32_e32 v104, v104, v104
	v_max_f32_e32 v105, v105, v105
	v_max_f32_e32 v106, v106, v106
	v_max_f32_e32 v107, v107, v107
	v_max_f32_e32 v108, v108, v108
	v_max_f32_e32 v109, v109, v109
	v_max_f32_e32 v110, v110, v110
	v_max_f32_e32 v111, v111, v111
	v_max_f32_e32 v112, v112, v112
	v_max_f32_e32 v113, v113, v113
	v_max_f32_e32 v114, v114, v114
	v_max_f32_e32 v115, v115, v115
	v_med3_f32 v100, v100, s20, v129
	v_med3_f32 v101, v101, s20, v129
	v_med3_f32 v102, v102, s20, v129
	v_med3_f32 v103, v103, s20, v129
	v_med3_f32 v104, v104, s20, v129
	v_med3_f32 v105, v105, s20, v129
	v_med3_f32 v106, v106, s20, v129
	v_med3_f32 v107, v107, s20, v129
	v_med3_f32 v108, v108, s20, v129
	v_med3_f32 v109, v109, s20, v129
	v_med3_f32 v110, v110, s20, v129
	v_med3_f32 v111, v111, s20, v129
	v_med3_f32 v112, v112, s20, v129
	v_med3_f32 v113, v113, s20, v129
	v_med3_f32 v114, v114, s20, v129
	v_med3_f32 v115, v115, s20, v129
	v_mov_b32_e32 v116, 0
	v_mov_b32_e32 v117, 0
	v_mov_b32_e32 v118, 0
	v_mov_b32_e32 v119, 0
	v_cvt_pk_fp8_f32 v116, v100, v101
	v_cvt_pk_fp8_f32 v117, v104, v105
	v_cvt_pk_fp8_f32 v118, v108, v109
	v_cvt_pk_fp8_f32 v119, v112, v113
	v_cvt_pk_fp8_f32 v116, v102, v103 op_sel:[0,0,1]
	v_cvt_pk_fp8_f32 v117, v106, v107 op_sel:[0,0,1]
	v_cvt_pk_fp8_f32 v118, v110, v111 op_sel:[0,0,1]
	v_cvt_pk_fp8_f32 v119, v114, v115 op_sel:[0,0,1]
	s_nop 0
	global_store_dwordx4 v127, v[116:119], s[14:15]
	ds_read_b32 v100, v124
	ds_read_b32 v101, v124 offset:512
	ds_read_b32 v102, v124 offset:1024
	ds_read_b32 v103, v124 offset:1536
	ds_read_b32 v104, v124 offset:2048
	ds_read_b32 v105, v124 offset:2560
	ds_read_b32 v106, v124 offset:3072
	ds_read_b32 v107, v124 offset:3584
	ds_read_b32 v108, v124 offset:4096
	ds_read_b32 v109, v124 offset:4608
	ds_read_b32 v110, v124 offset:5120
	ds_read_b32 v111, v124 offset:5632
	ds_read_b32 v112, v124 offset:6144
	ds_read_b32 v113, v124 offset:6656
	ds_read_b32 v114, v124 offset:7168
	ds_read_b32 v115, v124 offset:7680
	s_waitcnt lgkmcnt(0)
	v_max_f32_e32 v100, v100, v100
	v_max_f32_e32 v101, v101, v101
	v_max_f32_e32 v102, v102, v102
	v_max_f32_e32 v103, v103, v103
	v_max_f32_e32 v104, v104, v104
	v_max_f32_e32 v105, v105, v105
	v_max_f32_e32 v106, v106, v106
	v_max_f32_e32 v107, v107, v107
	v_max_f32_e32 v108, v108, v108
	v_max_f32_e32 v109, v109, v109
	v_max_f32_e32 v110, v110, v110
	v_max_f32_e32 v111, v111, v111
	v_max_f32_e32 v112, v112, v112
	v_max_f32_e32 v113, v113, v113
	v_max_f32_e32 v114, v114, v114
	v_max_f32_e32 v115, v115, v115
	v_med3_f32 v100, v100, s20, v129
	v_med3_f32 v101, v101, s20, v129
	v_med3_f32 v102, v102, s20, v129
	v_med3_f32 v103, v103, s20, v129
	v_med3_f32 v104, v104, s20, v129
	v_med3_f32 v105, v105, s20, v129
	v_med3_f32 v106, v106, s20, v129
	v_med3_f32 v107, v107, s20, v129
	v_med3_f32 v108, v108, s20, v129
	v_med3_f32 v109, v109, s20, v129
	v_med3_f32 v110, v110, s20, v129
	v_med3_f32 v111, v111, s20, v129
	v_med3_f32 v112, v112, s20, v129
	v_med3_f32 v113, v113, s20, v129
	v_med3_f32 v114, v114, s20, v129
	v_med3_f32 v115, v115, s20, v129
	v_mov_b32_e32 v116, 0
	v_mov_b32_e32 v117, 0
	v_mov_b32_e32 v118, 0
	v_mov_b32_e32 v119, 0
	v_cvt_pk_fp8_f32 v116, v100, v101
	v_cvt_pk_fp8_f32 v117, v104, v105
	v_cvt_pk_fp8_f32 v118, v108, v109
	v_cvt_pk_fp8_f32 v119, v112, v113
	v_cvt_pk_fp8_f32 v116, v102, v103 op_sel:[0,0,1]
	v_cvt_pk_fp8_f32 v117, v106, v107 op_sel:[0,0,1]
	v_cvt_pk_fp8_f32 v118, v110, v111 op_sel:[0,0,1]
	v_cvt_pk_fp8_f32 v119, v114, v115 op_sel:[0,0,1]
	s_nop 0
	global_store_dwordx4 v128, v[116:119], s[14:15]
	s_waitcnt vmcnt(12)
	v_mul_f32_e32 v68, 0x43000000, v68
	v_mul_f32_e32 v69, 0x43000000, v69
	v_mul_f32_e32 v70, 0x43000000, v70
	v_mul_f32_e32 v71, 0x43000000, v71
	ds_write_b128 v121, v[68:71]
	v_mul_f32_e32 v72, 0x43000000, v72
	v_mul_f32_e32 v73, 0x43000000, v73
	v_mul_f32_e32 v74, 0x43000000, v74
	v_mul_f32_e32 v75, 0x43000000, v75
	ds_write_b128 v121, v[72:75] offset:1024
	v_mul_f32_e32 v76, 0x43000000, v76
	v_mul_f32_e32 v77, 0x43000000, v77
	v_mul_f32_e32 v78, 0x43000000, v78
	v_mul_f32_e32 v79, 0x43000000, v79
	ds_write_b128 v121, v[76:79] offset:2048
	v_mul_f32_e32 v80, 0x43000000, v80
	v_mul_f32_e32 v81, 0x43000000, v81
	v_mul_f32_e32 v82, 0x43000000, v82
	v_mul_f32_e32 v83, 0x43000000, v83
	ds_write_b128 v121, v[80:83] offset:3072
	v_mul_f32_e32 v84, 0x43000000, v84
	v_mul_f32_e32 v85, 0x43000000, v85
	v_mul_f32_e32 v86, 0x43000000, v86
	v_mul_f32_e32 v87, 0x43000000, v87
	ds_write_b128 v121, v[84:87] offset:4096
	v_mul_f32_e32 v88, 0x43000000, v88
	v_mul_f32_e32 v89, 0x43000000, v89
	v_mul_f32_e32 v90, 0x43000000, v90
	v_mul_f32_e32 v91, 0x43000000, v91
	ds_write_b128 v121, v[88:91] offset:5120
	v_mul_f32_e32 v92, 0x43000000, v92
	v_mul_f32_e32 v93, 0x43000000, v93
	v_mul_f32_e32 v94, 0x43000000, v94
	v_mul_f32_e32 v95, 0x43000000, v95
	ds_write_b128 v121, v[92:95] offset:6144
	v_mul_f32_e32 v96, 0x43000000, v96
	v_mul_f32_e32 v97, 0x43000000, v97
	v_mul_f32_e32 v98, 0x43000000, v98
	v_mul_f32_e32 v99, 0x43000000, v99
	ds_write_b128 v121, v[96:99] offset:7168
	s_waitcnt lgkmcnt(0)
	s_barrier
; #define GAS __attribute__((address_space(1)))
; #define LAS __attribute__((address_space(3)))
; #define LDS_WAIT() asm volatile("s_waitcnt lgkmcnt(0)" ::: "memory")
; __device__ __forceinline__ unsigned pk4_fp8(float a, float b, float c, float d) {
;     a = fminf(fmaxf(a, -448.f), 448.f); b = fminf(fmaxf(b, -448.f), 448.f); c = fminf(fmaxf(c, -448.f), 448.f); d = fminf(fmaxf(d, -448.f), 448.f);
;     int w = __builtin_amdgcn_cvt_pk_fp8_f32(a, b, 0, false); w = __builtin_amdgcn_cvt_pk_fp8_f32(c, d, w, true); return (unsigned)w; }
;     ...
;     for (int i = 0; i < 32; ++i) v[i] = sc >= 0 ? W[(size_t)(k0 + 2 * i + (lane >> 5)) * Nsrc + sc] : 0.f;
; #pragma unroll
;     for (int i = 0; i < 32; ++i) { const int k = k0 + 2 * i + (lane >> 5); float x = v[i] * wscale; if (KS) x *= (k < ksplit ? ksA[k] : ksB[k - ksplit]); scr[(2 * i + (lane >> 5)) * 33 + (lane & 31)] = x; }
;     LDS_WAIT(); asm volatile("" ::: "memory");
;     const int c = lane & 7;
; #pragma unroll
;     for (int j = 0; j < 4; ++j) { const int n = (lane >> 3) + 8 * j; const LAS float* s = scr + (8 * c) * 33 + n;
;         const unsigned long long o = (unsigned long long)pg8::pk4_fp8(s[0 * 33], s[1 * 33], s[2 * 33], s[3 * 33]) | ((unsigned long long)pg8::pk4_fp8(s[4 * 33], s[5 * 33], s[6 * 33], s[7 * 33]) << 32);
;         *(GAS unsigned long long*)(WT + (size_t)(n0 + n) * K + k0 + 8 * c) = o; }
;     LDS_WAIT(); asm volatile("" ::: "memory");
	s_add_i32 s17, s16, 1248
	s_min_u32 s17, s17, 0x7ff
	s_lshr_b32 s18, s17, 5
	s_add_i32 s18, s18, 64
	s_and_b32 s19, s17, 31
	s_lshl_b32 s18, s18, 21
	s_lshl_b32 s19, s19, 9
	s_add_u32 s18, s18, s19
	s_add_u32 s12, s2, s18
	s_addc_u32 s13, s3, 0
	global_load_dwordx4 v[68:71], v126, s[12:13]
	s_add_u32 s12, s12, 0x8000
	s_addc_u32 s13, s13, 0
	global_load_dwordx4 v[72:75], v126, s[12:13]
	s_add_u32 s12, s12, 0x8000
	s_addc_u32 s13, s13, 0
	global_load_dwordx4 v[76:79], v126, s[12:13]
	s_add_u32 s12, s12, 0x8000
	s_addc_u32 s13, s13, 0
	global_load_dwordx4 v[80:83], v126, s[12:13]
	s_add_u32 s12, s12, 0x8000
	s_addc_u32 s13, s13, 0
	global_load_dwordx4 v[84:87], v126, s[12:13]
	s_add_u32 s12, s12, 0x8000
	s_addc_u32 s13, s13, 0
	global_load_dwordx4 v[88:91], v126, s[12:13]
	s_add_u32 s12, s12, 0x8000
	s_addc_u32 s13, s13, 0
	global_load_dwordx4 v[92:95], v126, s[12:13]
	s_add_u32 s12, s12, 0x8000
	s_addc_u32 s13, s13, 0
	global_load_dwordx4 v[96:99], v126, s[12:13]
	s_add_i32 s17, s16, 1056
	s_min_u32 s17, s17, 0x7ff
	s_lshr_b32 s18, s17, 5
	s_add_i32 s18, s18, 64
	s_and_b32 s19, s17, 31
	s_lshl_b32 s19, s19, 21
	s_lshl_b32 s18, s18, 7
	s_add_u32 s18, s18, s19
	s_add_u32 s14, s4, s18
	s_addc_u32 s15, s5, 0
	ds_read_b32 v100, v123
	ds_read_b32 v101, v123 offset:512
	ds_read_b32 v102, v123 offset:1024
	ds_read_b32 v103, v123 offset:1536
	ds_read_b32 v104, v123 offset:2048
	ds_read_b32 v105, v123 offset:2560
	ds_read_b32 v106, v123 offset:3072
	ds_read_b32 v107, v123 offset:3584
	ds_read_b32 v108, v123 offset:4096
	ds_read_b32 v109, v123 offset:4608
	ds_read_b32 v110, v123 offset:5120
	ds_read_b32 v111, v123 offset:5632
	ds_read_b32 v112, v123 offset:6144
	ds_read_b32 v113, v123 offset:6656
	ds_read_b32 v114, v123 offset:7168
	ds_read_b32 v115, v123 offset:7680
	s_waitcnt lgkmcnt(0)
	v_max_f32_e32 v100, v100, v100
	v_max_f32_e32 v101, v101, v101
	v_max_f32_e32 v102, v102, v102
	v_max_f32_e32 v103, v103, v103
	v_max_f32_e32 v104, v104, v104
	v_max_f32_e32 v105, v105, v105
	v_max_f32_e32 v106, v106, v106
	v_max_f32_e32 v107, v107, v107
	v_max_f32_e32 v108, v108, v108
	v_max_f32_e32 v109, v109, v109
	v_max_f32_e32 v110, v110, v110
	v_max_f32_e32 v111, v111, v111
	v_max_f32_e32 v112, v112, v112
	v_max_f32_e32 v113, v113, v113
	v_max_f32_e32 v114, v114, v114
	v_max_f32_e32 v115, v115, v115
	v_med3_f32 v100, v100, s20, v129
	v_med3_f32 v101, v101, s20, v129
	v_med3_f32 v102, v102, s20, v129
	v_med3_f32 v103, v103, s20, v129
	v_med3_f32 v104, v104, s20, v129
	v_med3_f32 v105, v105, s20, v129
	v_med3_f32 v106, v106, s20, v129
	v_med3_f32 v107, v107, s20, v129
	v_med3_f32 v108, v108, s20, v129
	v_med3_f32 v109, v109, s20, v129
	v_med3_f32 v110, v110, s20, v129
	v_med3_f32 v111, v111, s20, v129
	v_med3_f32 v112, v112, s20, v129
	v_med3_f32 v113, v113, s20, v129
	v_med3_f32 v114, v114, s20, v129
	v_med3_f32 v115, v115, s20, v129
	v_mov_b32_e32 v116, 0
	v_mov_b32_e32 v117, 0
	v_mov_b32_e32 v118, 0
	v_mov_b32_e32 v119, 0
	v_cvt_pk_fp8_f32 v116, v100, v101
	v_cvt_pk_fp8_f32 v117, v104, v105
	v_cvt_pk_fp8_f32 v118, v108, v109
	v_cvt_pk_fp8_f32 v119, v112, v113
	v_cvt_pk_fp8_f32 v116, v102, v103 op_sel:[0,0,1]
	v_cvt_pk_fp8_f32 v117, v106, v107 op_sel:[0,0,1]
	v_cvt_pk_fp8_f32 v118, v110, v111 op_sel:[0,0,1]
	v_cvt_pk_fp8_f32 v119, v114, v115 op_sel:[0,0,1]
	s_nop 0
	global_store_dwordx4 v127, v[116:119], s[14:15]
	ds_read_b32 v100, v125
	ds_read_b32 v101, v125 offset:512
	ds_read_b32 v102, v125 offset:1024
	ds_read_b32 v103, v125 offset:1536
	ds_read_b32 v104, v125 offset:2048
	ds_read_b32 v105, v125 offset:2560
	ds_read_b32 v106, v125 offset:3072
	ds_read_b32 v107, v125 offset:3584
	ds_read_b32 v108, v125 offset:4096
	ds_read_b32 v109, v125 offset:4608
	ds_read_b32 v110, v125 offset:5120
	ds_read_b32 v111, v125 offset:5632
	ds_read_b32 v112, v125 offset:6144
	ds_read_b32 v113, v125 offset:6656
	ds_read_b32 v114, v125 offset:7168
	ds_read_b32 v115, v125 offset:7680
	s_waitcnt lgkmcnt(0)
	v_max_f32_e32 v100, v100, v100
	v_max_f32_e32 v101, v101, v101
	v_max_f32_e32 v102, v102, v102
	v_max_f32_e32 v103, v103, v103
	v_max_f32_e32 v104, v104, v104
	v_max_f32_e32 v105, v105, v105
	v_max_f32_e32 v106, v106, v106
	v_max_f32_e32 v107, v107, v107
	v_max_f32_e32 v108, v108, v108
	v_max_f32_e32 v109, v109, v109
	v_max_f32_e32 v110, v110, v110
	v_max_f32_e32 v111, v111, v111
	v_max_f32_e32 v112, v112, v112
	v_max_f32_e32 v113, v113, v113
	v_max_f32_e32 v114, v114, v114
	v_max_f32_e32 v115, v115, v115
	v_med3_f32 v100, v100, s20, v129
	v_med3_f32 v101, v101, s20, v129
	v_med3_f32 v102, v102, s20, v129
	v_med3_f32 v103, v103, s20, v129
	v_med3_f32 v104, v104, s20, v129
	v_med3_f32 v105, v105, s20, v129
	v_med3_f32 v106, v106, s20, v129
	v_med3_f32 v107, v107, s20, v129
	v_med3_f32 v108, v108, s20, v129
	v_med3_f32 v109, v109, s20, v129
	v_med3_f32 v110, v110, s20, v129
	v_med3_f32 v111, v111, s20, v129
	v_med3_f32 v112, v112, s20, v129
	v_med3_f32 v113, v113, s20, v129
	v_med3_f32 v114, v114, s20, v129
	v_med3_f32 v115, v115, s20, v129
	v_mov_b32_e32 v116, 0
	v_mov_b32_e32 v117, 0
	v_mov_b32_e32 v118, 0
	v_mov_b32_e32 v119, 0
	v_cvt_pk_fp8_f32 v116, v100, v101
	v_cvt_pk_fp8_f32 v117, v104, v105
	v_cvt_pk_fp8_f32 v118, v108, v109
	v_cvt_pk_fp8_f32 v119, v112, v113
	v_cvt_pk_fp8_f32 v116, v102, v103 op_sel:[0,0,1]
	v_cvt_pk_fp8_f32 v117, v106, v107 op_sel:[0,0,1]
	v_cvt_pk_fp8_f32 v118, v110, v111 op_sel:[0,0,1]
	v_cvt_pk_fp8_f32 v119, v114, v115 op_sel:[0,0,1]
	s_nop 0
	global_store_dwordx4 v128, v[116:119], s[14:15]
	s_waitcnt vmcnt(12)
	v_mul_f32_e32 v36, 0x43000000, v36
	v_mul_f32_e32 v37, 0x43000000, v37
	v_mul_f32_e32 v38, 0x43000000, v38
	v_mul_f32_e32 v39, 0x43000000, v39
	ds_write_b128 v120, v[36:39]
	v_mul_f32_e32 v40, 0x43000000, v40
	v_mul_f32_e32 v41, 0x43000000, v41
	v_mul_f32_e32 v42, 0x43000000, v42
	v_mul_f32_e32 v43, 0x43000000, v43
	ds_write_b128 v120, v[40:43] offset:1024
	v_mul_f32_e32 v44, 0x43000000, v44
	v_mul_f32_e32 v45, 0x43000000, v45
	v_mul_f32_e32 v46, 0x43000000, v46
	v_mul_f32_e32 v47, 0x43000000, v47
	ds_write_b128 v120, v[44:47] offset:2048
	v_mul_f32_e32 v48, 0x43000000, v48
	v_mul_f32_e32 v49, 0x43000000, v49
	v_mul_f32_e32 v50, 0x43000000, v50
	v_mul_f32_e32 v51, 0x43000000, v51
	ds_write_b128 v120, v[48:51] offset:3072
	v_mul_f32_e32 v52, 0x43000000, v52
	v_mul_f32_e32 v53, 0x43000000, v53
	v_mul_f32_e32 v54, 0x43000000, v54
	v_mul_f32_e32 v55, 0x43000000, v55
	ds_write_b128 v120, v[52:55] offset:4096
	v_mul_f32_e32 v56, 0x43000000, v56
	v_mul_f32_e32 v57, 0x43000000, v57
	v_mul_f32_e32 v58, 0x43000000, v58
	v_mul_f32_e32 v59, 0x43000000, v59
	ds_write_b128 v120, v[56:59] offset:5120
	v_mul_f32_e32 v60, 0x43000000, v60
	v_mul_f32_e32 v61, 0x43000000, v61
	v_mul_f32_e32 v62, 0x43000000, v62
	v_mul_f32_e32 v63, 0x43000000, v63
	ds_write_b128 v120, v[60:63] offset:6144
	v_mul_f32_e32 v64, 0x43000000, v64
	v_mul_f32_e32 v65, 0x43000000, v65
	v_mul_f32_e32 v66, 0x43000000, v66
	v_mul_f32_e32 v67, 0x43000000, v67
	ds_write_b128 v120, v[64:67] offset:7168
	s_waitcnt lgkmcnt(0)
	s_barrier
; #define GAS __attribute__((address_space(1)))
; #define LAS __attribute__((address_space(3)))
; #define LDS_WAIT() asm volatile("s_waitcnt lgkmcnt(0)" ::: "memory")
; __device__ __forceinline__ unsigned pk4_fp8(float a, float b, float c, float d) {
;     a = fminf(fmaxf(a, -448.f), 448.f); b = fminf(fmaxf(b, -448.f), 448.f); c = fminf(fmaxf(c, -448.f), 448.f); d = fminf(fmaxf(d, -448.f), 448.f);
;     int w = __builtin_amdgcn_cvt_pk_fp8_f32(a, b, 0, false); w = __builtin_amdgcn_cvt_pk_fp8_f32(c, d, w, true); return (unsigned)w; }
;     ...
;     for (int i = 0; i < 32; ++i) v[i] = sc >= 0 ? W[(size_t)(k0 + 2 * i + (lane >> 5)) * Nsrc + sc] : 0.f;
; #pragma unroll
;     for (int i = 0; i < 32; ++i) { const int k = k0 + 2 * i + (lane >> 5); float x = v[i] * wscale; if (KS) x *= (k < ksplit ? ksA[k] : ksB[k - ksplit]); scr[(2 * i + (lane >> 5)) * 33 + (lane & 31)] = x; }
;     LDS_WAIT(); asm volatile("" ::: "memory");
;     const int c = lane & 7;
; #pragma unroll
;     for (int j = 0; j < 4; ++j) { const int n = (lane >> 3) + 8 * j; const LAS float* s = scr + (8 * c) * 33 + n;
;         const unsigned long long o = (unsigned long long)pg8::pk4_fp8(s[0 * 33], s[1 * 33], s[2 * 33], s[3 * 33]) | ((unsigned long long)pg8::pk4_fp8(s[4 * 33], s[5 * 33], s[6 * 33], s[7 * 33]) << 32);
;         *(GAS unsigned long long*)(WT + (size_t)(n0 + n) * K + k0 + 8 * c) = o; }
;     LDS_WAIT(); asm volatile("" ::: "memory");
	s_add_i32 s17, s16, 1344
	s_min_u32 s17, s17, 0x7ff
	s_lshr_b32 s18, s17, 5
	s_add_i32 s18, s18, 64
	s_and_b32 s19, s17, 31
	s_lshl_b32 s18, s18, 21
	s_lshl_b32 s19, s19, 9
	s_add_u32 s18, s18, s19
	s_add_u32 s12, s2, s18
	s_addc_u32 s13, s3, 0
	global_load_dwordx4 v[36:39], v126, s[12:13]
	s_add_u32 s12, s12, 0x8000
	s_addc_u32 s13, s13, 0
	global_load_dwordx4 v[40:43], v126, s[12:13]
	s_add_u32 s12, s12, 0x8000
	s_addc_u32 s13, s13, 0
	global_load_dwordx4 v[44:47], v126, s[12:13]
	s_add_u32 s12, s12, 0x8000
	s_addc_u32 s13, s13, 0
	global_load_dwordx4 v[48:51], v126, s[12:13]
	s_add_u32 s12, s12, 0x8000
	s_addc_u32 s13, s13, 0
	global_load_dwordx4 v[52:55], v126, s[12:13]
	s_add_u32 s12, s12, 0x8000
	s_addc_u32 s13, s13, 0
	global_load_dwordx4 v[56:59], v126, s[12:13]
	s_add_u32 s12, s12, 0x8000
	s_addc_u32 s13, s13, 0
	global_load_dwordx4 v[60:63], v126, s[12:13]
	s_add_u32 s12, s12, 0x8000
	s_addc_u32 s13, s13, 0
	global_load_dwordx4 v[64:67], v126, s[12:13]
	s_add_i32 s17, s16, 1152
	s_min_u32 s17, s17, 0x7ff
	s_lshr_b32 s18, s17, 5
	s_add_i32 s18, s18, 64
	s_and_b32 s19, s17, 31
	s_lshl_b32 s19, s19, 21
	s_lshl_b32 s18, s18, 7
	s_add_u32 s18, s18, s19
	s_add_u32 s14, s4, s18
	s_addc_u32 s15, s5, 0
	ds_read_b32 v100, v122
	ds_read_b32 v101, v122 offset:512
	ds_read_b32 v102, v122 offset:1024
	ds_read_b32 v103, v122 offset:1536
	ds_read_b32 v104, v122 offset:2048
	ds_read_b32 v105, v122 offset:2560
	ds_read_b32 v106, v122 offset:3072
	ds_read_b32 v107, v122 offset:3584
	ds_read_b32 v108, v122 offset:4096
	ds_read_b32 v109, v122 offset:4608
	ds_read_b32 v110, v122 offset:5120
	ds_read_b32 v111, v122 offset:5632
	ds_read_b32 v112, v122 offset:6144
	ds_read_b32 v113, v122 offset:6656
	ds_read_b32 v114, v122 offset:7168
	ds_read_b32 v115, v122 offset:7680
	s_waitcnt lgkmcnt(0)
	v_max_f32_e32 v100, v100, v100
	v_max_f32_e32 v101, v101, v101
	v_max_f32_e32 v102, v102, v102
	v_max_f32_e32 v103, v103, v103
	v_max_f32_e32 v104, v104, v104
	v_max_f32_e32 v105, v105, v105
	v_max_f32_e32 v106, v106, v106
	v_max_f32_e32 v107, v107, v107
	v_max_f32_e32 v108, v108, v108
	v_max_f32_e32 v109, v109, v109
	v_max_f32_e32 v110, v110, v110
	v_max_f32_e32 v111, v111, v111
	v_max_f32_e32 v112, v112, v112
	v_max_f32_e32 v113, v113, v113
	v_max_f32_e32 v114, v114, v114
	v_max_f32_e32 v115, v115, v115
	v_med3_f32 v100, v100, s20, v129
	v_med3_f32 v101, v101, s20, v129
	v_med3_f32 v102, v102, s20, v129
	v_med3_f32 v103, v103, s20, v129
	v_med3_f32 v104, v104, s20, v129
	v_med3_f32 v105, v105, s20, v129
	v_med3_f32 v106, v106, s20, v129
	v_med3_f32 v107, v107, s20, v129
	v_med3_f32 v108, v108, s20, v129
	v_med3_f32 v109, v109, s20, v129
	v_med3_f32 v110, v110, s20, v129
	v_med3_f32 v111, v111, s20, v129
	v_med3_f32 v112, v112, s20, v129
	v_med3_f32 v113, v113, s20, v129
	v_med3_f32 v114, v114, s20, v129
	v_med3_f32 v115, v115, s20, v129
	v_mov_b32_e32 v116, 0
	v_mov_b32_e32 v117, 0
	v_mov_b32_e32 v118, 0
	v_mov_b32_e32 v119, 0
	v_cvt_pk_fp8_f32 v116, v100, v101
	v_cvt_pk_fp8_f32 v117, v104, v105
	v_cvt_pk_fp8_f32 v118, v108, v109
	v_cvt_pk_fp8_f32 v119, v112, v113
	v_cvt_pk_fp8_f32 v116, v102, v103 op_sel:[0,0,1]
	v_cvt_pk_fp8_f32 v117, v106, v107 op_sel:[0,0,1]
	v_cvt_pk_fp8_f32 v118, v110, v111 op_sel:[0,0,1]
	v_cvt_pk_fp8_f32 v119, v114, v115 op_sel:[0,0,1]
	s_nop 0
	global_store_dwordx4 v127, v[116:119], s[14:15]
	ds_read_b32 v100, v124
	ds_read_b32 v101, v124 offset:512
	ds_read_b32 v102, v124 offset:1024
	ds_read_b32 v103, v124 offset:1536
	ds_read_b32 v104, v124 offset:2048
	ds_read_b32 v105, v124 offset:2560
	ds_read_b32 v106, v124 offset:3072
	ds_read_b32 v107, v124 offset:3584
	ds_read_b32 v108, v124 offset:4096
	ds_read_b32 v109, v124 offset:4608
	ds_read_b32 v110, v124 offset:5120
	ds_read_b32 v111, v124 offset:5632
	ds_read_b32 v112, v124 offset:6144
	ds_read_b32 v113, v124 offset:6656
	ds_read_b32 v114, v124 offset:7168
	ds_read_b32 v115, v124 offset:7680
	s_waitcnt lgkmcnt(0)
	v_max_f32_e32 v100, v100, v100
	v_max_f32_e32 v101, v101, v101
	v_max_f32_e32 v102, v102, v102
	v_max_f32_e32 v103, v103, v103
	v_max_f32_e32 v104, v104, v104
	v_max_f32_e32 v105, v105, v105
	v_max_f32_e32 v106, v106, v106
	v_max_f32_e32 v107, v107, v107
	v_max_f32_e32 v108, v108, v108
	v_max_f32_e32 v109, v109, v109
	v_max_f32_e32 v110, v110, v110
	v_max_f32_e32 v111, v111, v111
	v_max_f32_e32 v112, v112, v112
	v_max_f32_e32 v113, v113, v113
	v_max_f32_e32 v114, v114, v114
	v_max_f32_e32 v115, v115, v115
	v_med3_f32 v100, v100, s20, v129
	v_med3_f32 v101, v101, s20, v129
	v_med3_f32 v102, v102, s20, v129
	v_med3_f32 v103, v103, s20, v129
	v_med3_f32 v104, v104, s20, v129
	v_med3_f32 v105, v105, s20, v129
	v_med3_f32 v106, v106, s20, v129
	v_med3_f32 v107, v107, s20, v129
	v_med3_f32 v108, v108, s20, v129
	v_med3_f32 v109, v109, s20, v129
	v_med3_f32 v110, v110, s20, v129
	v_med3_f32 v111, v111, s20, v129
	v_med3_f32 v112, v112, s20, v129
	v_med3_f32 v113, v113, s20, v129
	v_med3_f32 v114, v114, s20, v129
	v_med3_f32 v115, v115, s20, v129
	v_mov_b32_e32 v116, 0
	v_mov_b32_e32 v117, 0
	v_mov_b32_e32 v118, 0
	v_mov_b32_e32 v119, 0
	v_cvt_pk_fp8_f32 v116, v100, v101
	v_cvt_pk_fp8_f32 v117, v104, v105
	v_cvt_pk_fp8_f32 v118, v108, v109
	v_cvt_pk_fp8_f32 v119, v112, v113
	v_cvt_pk_fp8_f32 v116, v102, v103 op_sel:[0,0,1]
	v_cvt_pk_fp8_f32 v117, v106, v107 op_sel:[0,0,1]
	v_cvt_pk_fp8_f32 v118, v110, v111 op_sel:[0,0,1]
	v_cvt_pk_fp8_f32 v119, v114, v115 op_sel:[0,0,1]
	s_nop 0
	global_store_dwordx4 v128, v[116:119], s[14:15]
	s_waitcnt vmcnt(12)
	v_mul_f32_e32 v68, 0x43000000, v68
	v_mul_f32_e32 v69, 0x43000000, v69
	v_mul_f32_e32 v70, 0x43000000, v70
	v_mul_f32_e32 v71, 0x43000000, v71
	ds_write_b128 v121, v[68:71]
	v_mul_f32_e32 v72, 0x43000000, v72
	v_mul_f32_e32 v73, 0x43000000, v73
	v_mul_f32_e32 v74, 0x43000000, v74
	v_mul_f32_e32 v75, 0x43000000, v75
	ds_write_b128 v121, v[72:75] offset:1024
	v_mul_f32_e32 v76, 0x43000000, v76
	v_mul_f32_e32 v77, 0x43000000, v77
	v_mul_f32_e32 v78, 0x43000000, v78
	v_mul_f32_e32 v79, 0x43000000, v79
	ds_write_b128 v121, v[76:79] offset:2048
	v_mul_f32_e32 v80, 0x43000000, v80
	v_mul_f32_e32 v81, 0x43000000, v81
	v_mul_f32_e32 v82, 0x43000000, v82
	v_mul_f32_e32 v83, 0x43000000, v83
	ds_write_b128 v121, v[80:83] offset:3072
	v_mul_f32_e32 v84, 0x43000000, v84
	v_mul_f32_e32 v85, 0x43000000, v85
	v_mul_f32_e32 v86, 0x43000000, v86
	v_mul_f32_e32 v87, 0x43000000, v87
	ds_write_b128 v121, v[84:87] offset:4096
	v_mul_f32_e32 v88, 0x43000000, v88
	v_mul_f32_e32 v89, 0x43000000, v89
	v_mul_f32_e32 v90, 0x43000000, v90
	v_mul_f32_e32 v91, 0x43000000, v91
	ds_write_b128 v121, v[88:91] offset:5120
	v_mul_f32_e32 v92, 0x43000000, v92
	v_mul_f32_e32 v93, 0x43000000, v93
	v_mul_f32_e32 v94, 0x43000000, v94
	v_mul_f32_e32 v95, 0x43000000, v95
	ds_write_b128 v121, v[92:95] offset:6144
	v_mul_f32_e32 v96, 0x43000000, v96
	v_mul_f32_e32 v97, 0x43000000, v97
	v_mul_f32_e32 v98, 0x43000000, v98
	v_mul_f32_e32 v99, 0x43000000, v99
	ds_write_b128 v121, v[96:99] offset:7168
	s_waitcnt lgkmcnt(0)
	s_barrier
; #define GAS __attribute__((address_space(1)))
; #define LAS __attribute__((address_space(3)))
; #define LDS_WAIT() asm volatile("s_waitcnt lgkmcnt(0)" ::: "memory")
; __device__ __forceinline__ unsigned pk4_fp8(float a, float b, float c, float d) {
;     a = fminf(fmaxf(a, -448.f), 448.f); b = fminf(fmaxf(b, -448.f), 448.f); c = fminf(fmaxf(c, -448.f), 448.f); d = fminf(fmaxf(d, -448.f), 448.f);
;     int w = __builtin_amdgcn_cvt_pk_fp8_f32(a, b, 0, false); w = __builtin_amdgcn_cvt_pk_fp8_f32(c, d, w, true); return (unsigned)w; }
;     ...
;     for (int i = 0; i < 32; ++i) v[i] = sc >= 0 ? W[(size_t)(k0 + 2 * i + (lane >> 5)) * Nsrc + sc] : 0.f;
; #pragma unroll
;     for (int i = 0; i < 32; ++i) { const int k = k0 + 2 * i + (lane >> 5); float x = v[i] * wscale; if (KS) x *= (k < ksplit ? ksA[k] : ksB[k - ksplit]); scr[(2 * i + (lane >> 5)) * 33 + (lane & 31)] = x; }
;     LDS_WAIT(); asm volatile("" ::: "memory");
;     const int c = lane & 7;
; #pragma unroll
;     for (int j = 0; j < 4; ++j) { const int n = (lane >> 3) + 8 * j; const LAS float* s = scr + (8 * c) * 33 + n;
;         const unsigned long long o = (unsigned long long)pg8::pk4_fp8(s[0 * 33], s[1 * 33], s[2 * 33], s[3 * 33]) | ((unsigned long long)pg8::pk4_fp8(s[4 * 33], s[5 * 33], s[6 * 33], s[7 * 33]) << 32);
;         *(GAS unsigned long long*)(WT + (size_t)(n0 + n) * K + k0 + 8 * c) = o; }
;     LDS_WAIT(); asm volatile("" ::: "memory");
	s_add_i32 s17, s16, 1440
	s_min_u32 s17, s17, 0x7ff
	s_lshr_b32 s18, s17, 5
	s_add_i32 s18, s18, 64
	s_and_b32 s19, s17, 31
	s_lshl_b32 s18, s18, 21
	s_lshl_b32 s19, s19, 9
	s_add_u32 s18, s18, s19
	s_add_u32 s12, s2, s18
	s_addc_u32 s13, s3, 0
	global_load_dwordx4 v[68:71], v126, s[12:13]
	s_add_u32 s12, s12, 0x8000
	s_addc_u32 s13, s13, 0
	global_load_dwordx4 v[72:75], v126, s[12:13]
	s_add_u32 s12, s12, 0x8000
	s_addc_u32 s13, s13, 0
	global_load_dwordx4 v[76:79], v126, s[12:13]
	s_add_u32 s12, s12, 0x8000
	s_addc_u32 s13, s13, 0
	global_load_dwordx4 v[80:83], v126, s[12:13]
	s_add_u32 s12, s12, 0x8000
	s_addc_u32 s13, s13, 0
	global_load_dwordx4 v[84:87], v126, s[12:13]
	s_add_u32 s12, s12, 0x8000
	s_addc_u32 s13, s13, 0
	global_load_dwordx4 v[88:91], v126, s[12:13]
	s_add_u32 s12, s12, 0x8000
	s_addc_u32 s13, s13, 0
	global_load_dwordx4 v[92:95], v126, s[12:13]
	s_add_u32 s12, s12, 0x8000
	s_addc_u32 s13, s13, 0
	global_load_dwordx4 v[96:99], v126, s[12:13]
	s_add_i32 s17, s16, 1248
	s_min_u32 s17, s17, 0x7ff
	s_lshr_b32 s18, s17, 5
	s_add_i32 s18, s18, 64
	s_and_b32 s19, s17, 31
	s_lshl_b32 s19, s19, 21
	s_lshl_b32 s18, s18, 7
	s_add_u32 s18, s18, s19
	s_add_u32 s14, s4, s18
	s_addc_u32 s15, s5, 0
	ds_read_b32 v100, v123
	ds_read_b32 v101, v123 offset:512
	ds_read_b32 v102, v123 offset:1024
	ds_read_b32 v103, v123 offset:1536
	ds_read_b32 v104, v123 offset:2048
	ds_read_b32 v105, v123 offset:2560
	ds_read_b32 v106, v123 offset:3072
	ds_read_b32 v107, v123 offset:3584
	ds_read_b32 v108, v123 offset:4096
	ds_read_b32 v109, v123 offset:4608
	ds_read_b32 v110, v123 offset:5120
	ds_read_b32 v111, v123 offset:5632
	ds_read_b32 v112, v123 offset:6144
	ds_read_b32 v113, v123 offset:6656
	ds_read_b32 v114, v123 offset:7168
	ds_read_b32 v115, v123 offset:7680
	s_waitcnt lgkmcnt(0)
	v_max_f32_e32 v100, v100, v100
	v_max_f32_e32 v101, v101, v101
	v_max_f32_e32 v102, v102, v102
	v_max_f32_e32 v103, v103, v103
	v_max_f32_e32 v104, v104, v104
	v_max_f32_e32 v105, v105, v105
	v_max_f32_e32 v106, v106, v106
	v_max_f32_e32 v107, v107, v107
	v_max_f32_e32 v108, v108, v108
	v_max_f32_e32 v109, v109, v109
	v_max_f32_e32 v110, v110, v110
	v_max_f32_e32 v111, v111, v111
	v_max_f32_e32 v112, v112, v112
	v_max_f32_e32 v113, v113, v113
	v_max_f32_e32 v114, v114, v114
	v_max_f32_e32 v115, v115, v115
	v_med3_f32 v100, v100, s20, v129
	v_med3_f32 v101, v101, s20, v129
	v_med3_f32 v102, v102, s20, v129
	v_med3_f32 v103, v103, s20, v129
	v_med3_f32 v104, v104, s20, v129
	v_med3_f32 v105, v105, s20, v129
	v_med3_f32 v106, v106, s20, v129
	v_med3_f32 v107, v107, s20, v129
	v_med3_f32 v108, v108, s20, v129
	v_med3_f32 v109, v109, s20, v129
	v_med3_f32 v110, v110, s20, v129
	v_med3_f32 v111, v111, s20, v129
	v_med3_f32 v112, v112, s20, v129
	v_med3_f32 v113, v113, s20, v129
	v_med3_f32 v114, v114, s20, v129
	v_med3_f32 v115, v115, s20, v129
	v_mov_b32_e32 v116, 0
	v_mov_b32_e32 v117, 0
	v_mov_b32_e32 v118, 0
	v_mov_b32_e32 v119, 0
	v_cvt_pk_fp8_f32 v116, v100, v101
	v_cvt_pk_fp8_f32 v117, v104, v105
	v_cvt_pk_fp8_f32 v118, v108, v109
	v_cvt_pk_fp8_f32 v119, v112, v113
	v_cvt_pk_fp8_f32 v116, v102, v103 op_sel:[0,0,1]
	v_cvt_pk_fp8_f32 v117, v106, v107 op_sel:[0,0,1]
	v_cvt_pk_fp8_f32 v118, v110, v111 op_sel:[0,0,1]
	v_cvt_pk_fp8_f32 v119, v114, v115 op_sel:[0,0,1]
	s_nop 0
	global_store_dwordx4 v127, v[116:119], s[14:15]
	ds_read_b32 v100, v125
	ds_read_b32 v101, v125 offset:512
	ds_read_b32 v102, v125 offset:1024
	ds_read_b32 v103, v125 offset:1536
	ds_read_b32 v104, v125 offset:2048
	ds_read_b32 v105, v125 offset:2560
	ds_read_b32 v106, v125 offset:3072
	ds_read_b32 v107, v125 offset:3584
	ds_read_b32 v108, v125 offset:4096
	ds_read_b32 v109, v125 offset:4608
	ds_read_b32 v110, v125 offset:5120
	ds_read_b32 v111, v125 offset:5632
	ds_read_b32 v112, v125 offset:6144
	ds_read_b32 v113, v125 offset:6656
	ds_read_b32 v114, v125 offset:7168
	ds_read_b32 v115, v125 offset:7680
	s_waitcnt lgkmcnt(0)
	v_max_f32_e32 v100, v100, v100
	v_max_f32_e32 v101, v101, v101
	v_max_f32_e32 v102, v102, v102
	v_max_f32_e32 v103, v103, v103
	v_max_f32_e32 v104, v104, v104
	v_max_f32_e32 v105, v105, v105
	v_max_f32_e32 v106, v106, v106
	v_max_f32_e32 v107, v107, v107
	v_max_f32_e32 v108, v108, v108
	v_max_f32_e32 v109, v109, v109
	v_max_f32_e32 v110, v110, v110
	v_max_f32_e32 v111, v111, v111
	v_max_f32_e32 v112, v112, v112
	v_max_f32_e32 v113, v113, v113
	v_max_f32_e32 v114, v114, v114
	v_max_f32_e32 v115, v115, v115
	v_med3_f32 v100, v100, s20, v129
	v_med3_f32 v101, v101, s20, v129
	v_med3_f32 v102, v102, s20, v129
	v_med3_f32 v103, v103, s20, v129
	v_med3_f32 v104, v104, s20, v129
	v_med3_f32 v105, v105, s20, v129
	v_med3_f32 v106, v106, s20, v129
	v_med3_f32 v107, v107, s20, v129
	v_med3_f32 v108, v108, s20, v129
	v_med3_f32 v109, v109, s20, v129
	v_med3_f32 v110, v110, s20, v129
	v_med3_f32 v111, v111, s20, v129
	v_med3_f32 v112, v112, s20, v129
	v_med3_f32 v113, v113, s20, v129
	v_med3_f32 v114, v114, s20, v129
	v_med3_f32 v115, v115, s20, v129
	v_mov_b32_e32 v116, 0
	v_mov_b32_e32 v117, 0
	v_mov_b32_e32 v118, 0
	v_mov_b32_e32 v119, 0
	v_cvt_pk_fp8_f32 v116, v100, v101
	v_cvt_pk_fp8_f32 v117, v104, v105
	v_cvt_pk_fp8_f32 v118, v108, v109
	v_cvt_pk_fp8_f32 v119, v112, v113
	v_cvt_pk_fp8_f32 v116, v102, v103 op_sel:[0,0,1]
	v_cvt_pk_fp8_f32 v117, v106, v107 op_sel:[0,0,1]
	v_cvt_pk_fp8_f32 v118, v110, v111 op_sel:[0,0,1]
	v_cvt_pk_fp8_f32 v119, v114, v115 op_sel:[0,0,1]
	s_nop 0
	global_store_dwordx4 v128, v[116:119], s[14:15]
	s_waitcnt vmcnt(12)
	v_mul_f32_e32 v36, 0x43000000, v36
	v_mul_f32_e32 v37, 0x43000000, v37
	v_mul_f32_e32 v38, 0x43000000, v38
	v_mul_f32_e32 v39, 0x43000000, v39
	ds_write_b128 v120, v[36:39]
	v_mul_f32_e32 v40, 0x43000000, v40
	v_mul_f32_e32 v41, 0x43000000, v41
	v_mul_f32_e32 v42, 0x43000000, v42
	v_mul_f32_e32 v43, 0x43000000, v43
	ds_write_b128 v120, v[40:43] offset:1024
	v_mul_f32_e32 v44, 0x43000000, v44
	v_mul_f32_e32 v45, 0x43000000, v45
	v_mul_f32_e32 v46, 0x43000000, v46
	v_mul_f32_e32 v47, 0x43000000, v47
	ds_write_b128 v120, v[44:47] offset:2048
	v_mul_f32_e32 v48, 0x43000000, v48
	v_mul_f32_e32 v49, 0x43000000, v49
	v_mul_f32_e32 v50, 0x43000000, v50
	v_mul_f32_e32 v51, 0x43000000, v51
	ds_write_b128 v120, v[48:51] offset:3072
	v_mul_f32_e32 v52, 0x43000000, v52
	v_mul_f32_e32 v53, 0x43000000, v53
	v_mul_f32_e32 v54, 0x43000000, v54
	v_mul_f32_e32 v55, 0x43000000, v55
	ds_write_b128 v120, v[52:55] offset:4096
	v_mul_f32_e32 v56, 0x43000000, v56
	v_mul_f32_e32 v57, 0x43000000, v57
	v_mul_f32_e32 v58, 0x43000000, v58
	v_mul_f32_e32 v59, 0x43000000, v59
	ds_write_b128 v120, v[56:59] offset:5120
	v_mul_f32_e32 v60, 0x43000000, v60
	v_mul_f32_e32 v61, 0x43000000, v61
	v_mul_f32_e32 v62, 0x43000000, v62
	v_mul_f32_e32 v63, 0x43000000, v63
	ds_write_b128 v120, v[60:63] offset:6144
	v_mul_f32_e32 v64, 0x43000000, v64
	v_mul_f32_e32 v65, 0x43000000, v65
	v_mul_f32_e32 v66, 0x43000000, v66
	v_mul_f32_e32 v67, 0x43000000, v67
	ds_write_b128 v120, v[64:67] offset:7168
	s_waitcnt lgkmcnt(0)
	s_barrier
; #define GAS __attribute__((address_space(1)))
; #define LAS __attribute__((address_space(3)))
; #define LDS_WAIT() asm volatile("s_waitcnt lgkmcnt(0)" ::: "memory")
; __device__ __forceinline__ unsigned pk4_fp8(float a, float b, float c, float d) {
;     a = fminf(fmaxf(a, -448.f), 448.f); b = fminf(fmaxf(b, -448.f), 448.f); c = fminf(fmaxf(c, -448.f), 448.f); d = fminf(fmaxf(d, -448.f), 448.f);
;     int w = __builtin_amdgcn_cvt_pk_fp8_f32(a, b, 0, false); w = __builtin_amdgcn_cvt_pk_fp8_f32(c, d, w, true); return (unsigned)w; }
;     ...
;     for (int i = 0; i < 32; ++i) v[i] = sc >= 0 ? W[(size_t)(k0 + 2 * i + (lane >> 5)) * Nsrc + sc] : 0.f;
; #pragma unroll
;     for (int i = 0; i < 32; ++i) { const int k = k0 + 2 * i + (lane >> 5); float x = v[i] * wscale; if (KS) x *= (k < ksplit ? ksA[k] : ksB[k - ksplit]); scr[(2 * i + (lane >> 5)) * 33 + (lane & 31)] = x; }
;     LDS_WAIT(); asm volatile("" ::: "memory");
;     const int c = lane & 7;
; #pragma unroll
;     for (int j = 0; j < 4; ++j) { const int n = (lane >> 3) + 8 * j; const LAS float* s = scr + (8 * c) * 33 + n;
;         const unsigned long long o = (unsigned long long)pg8::pk4_fp8(s[0 * 33], s[1 * 33], s[2 * 33], s[3 * 33]) | ((unsigned long long)pg8::pk4_fp8(s[4 * 33], s[5 * 33], s[6 * 33], s[7 * 33]) << 32);
;         *(GAS unsigned long long*)(WT + (size_t)(n0 + n) * K + k0 + 8 * c) = o; }
;     LDS_WAIT(); asm volatile("" ::: "memory");
	s_add_i32 s17, s16, 1536
	s_min_u32 s17, s17, 0x7ff
	s_lshr_b32 s18, s17, 5
	s_add_i32 s18, s18, 64
	s_and_b32 s19, s17, 31
	s_lshl_b32 s18, s18, 21
	s_lshl_b32 s19, s19, 9
	s_add_u32 s18, s18, s19
	s_add_u32 s12, s2, s18
	s_addc_u32 s13, s3, 0
	global_load_dwordx4 v[36:39], v126, s[12:13]
	s_add_u32 s12, s12, 0x8000
	s_addc_u32 s13, s13, 0
	global_load_dwordx4 v[40:43], v126, s[12:13]
	s_add_u32 s12, s12, 0x8000
	s_addc_u32 s13, s13, 0
	global_load_dwordx4 v[44:47], v126, s[12:13]
	s_add_u32 s12, s12, 0x8000
	s_addc_u32 s13, s13, 0
	global_load_dwordx4 v[48:51], v126, s[12:13]
	s_add_u32 s12, s12, 0x8000
	s_addc_u32 s13, s13, 0
	global_load_dwordx4 v[52:55], v126, s[12:13]
	s_add_u32 s12, s12, 0x8000
	s_addc_u32 s13, s13, 0
	global_load_dwordx4 v[56:59], v126, s[12:13]
	s_add_u32 s12, s12, 0x8000
	s_addc_u32 s13, s13, 0
	global_load_dwordx4 v[60:63], v126, s[12:13]
	s_add_u32 s12, s12, 0x8000
	s_addc_u32 s13, s13, 0
	global_load_dwordx4 v[64:67], v126, s[12:13]
	s_add_i32 s17, s16, 1344
	s_min_u32 s17, s17, 0x7ff
	s_lshr_b32 s18, s17, 5
	s_add_i32 s18, s18, 64
	s_and_b32 s19, s17, 31
	s_lshl_b32 s19, s19, 21
	s_lshl_b32 s18, s18, 7
	s_add_u32 s18, s18, s19
	s_add_u32 s14, s4, s18
	s_addc_u32 s15, s5, 0
	ds_read_b32 v100, v122
	ds_read_b32 v101, v122 offset:512
	ds_read_b32 v102, v122 offset:1024
	ds_read_b32 v103, v122 offset:1536
	ds_read_b32 v104, v122 offset:2048
	ds_read_b32 v105, v122 offset:2560
	ds_read_b32 v106, v122 offset:3072
	ds_read_b32 v107, v122 offset:3584
	ds_read_b32 v108, v122 offset:4096
	ds_read_b32 v109, v122 offset:4608
	ds_read_b32 v110, v122 offset:5120
	ds_read_b32 v111, v122 offset:5632
	ds_read_b32 v112, v122 offset:6144
	ds_read_b32 v113, v122 offset:6656
	ds_read_b32 v114, v122 offset:7168
	ds_read_b32 v115, v122 offset:7680
	s_waitcnt lgkmcnt(0)
	v_max_f32_e32 v100, v100, v100
	v_max_f32_e32 v101, v101, v101
	v_max_f32_e32 v102, v102, v102
	v_max_f32_e32 v103, v103, v103
	v_max_f32_e32 v104, v104, v104
	v_max_f32_e32 v105, v105, v105
	v_max_f32_e32 v106, v106, v106
	v_max_f32_e32 v107, v107, v107
	v_max_f32_e32 v108, v108, v108
	v_max_f32_e32 v109, v109, v109
	v_max_f32_e32 v110, v110, v110
	v_max_f32_e32 v111, v111, v111
	v_max_f32_e32 v112, v112, v112
	v_max_f32_e32 v113, v113, v113
	v_max_f32_e32 v114, v114, v114
	v_max_f32_e32 v115, v115, v115
	v_med3_f32 v100, v100, s20, v129
	v_med3_f32 v101, v101, s20, v129
	v_med3_f32 v102, v102, s20, v129
	v_med3_f32 v103, v103, s20, v129
	v_med3_f32 v104, v104, s20, v129
	v_med3_f32 v105, v105, s20, v129
	v_med3_f32 v106, v106, s20, v129
	v_med3_f32 v107, v107, s20, v129
	v_med3_f32 v108, v108, s20, v129
	v_med3_f32 v109, v109, s20, v129
	v_med3_f32 v110, v110, s20, v129
	v_med3_f32 v111, v111, s20, v129
	v_med3_f32 v112, v112, s20, v129
	v_med3_f32 v113, v113, s20, v129
	v_med3_f32 v114, v114, s20, v129
	v_med3_f32 v115, v115, s20, v129
	v_mov_b32_e32 v116, 0
	v_mov_b32_e32 v117, 0
	v_mov_b32_e32 v118, 0
	v_mov_b32_e32 v119, 0
	v_cvt_pk_fp8_f32 v116, v100, v101
	v_cvt_pk_fp8_f32 v117, v104, v105
	v_cvt_pk_fp8_f32 v118, v108, v109
	v_cvt_pk_fp8_f32 v119, v112, v113
	v_cvt_pk_fp8_f32 v116, v102, v103 op_sel:[0,0,1]
	v_cvt_pk_fp8_f32 v117, v106, v107 op_sel:[0,0,1]
	v_cvt_pk_fp8_f32 v118, v110, v111 op_sel:[0,0,1]
	v_cvt_pk_fp8_f32 v119, v114, v115 op_sel:[0,0,1]
	s_nop 0
	global_store_dwordx4 v127, v[116:119], s[14:15]
	ds_read_b32 v100, v124
	ds_read_b32 v101, v124 offset:512
	ds_read_b32 v102, v124 offset:1024
	ds_read_b32 v103, v124 offset:1536
	ds_read_b32 v104, v124 offset:2048
	ds_read_b32 v105, v124 offset:2560
	ds_read_b32 v106, v124 offset:3072
	ds_read_b32 v107, v124 offset:3584
	ds_read_b32 v108, v124 offset:4096
	ds_read_b32 v109, v124 offset:4608
	ds_read_b32 v110, v124 offset:5120
	ds_read_b32 v111, v124 offset:5632
	ds_read_b32 v112, v124 offset:6144
	ds_read_b32 v113, v124 offset:6656
	ds_read_b32 v114, v124 offset:7168
	ds_read_b32 v115, v124 offset:7680
	s_waitcnt lgkmcnt(0)
	v_max_f32_e32 v100, v100, v100
	v_max_f32_e32 v101, v101, v101
	v_max_f32_e32 v102, v102, v102
	v_max_f32_e32 v103, v103, v103
	v_max_f32_e32 v104, v104, v104
	v_max_f32_e32 v105, v105, v105
	v_max_f32_e32 v106, v106, v106
	v_max_f32_e32 v107, v107, v107
	v_max_f32_e32 v108, v108, v108
	v_max_f32_e32 v109, v109, v109
	v_max_f32_e32 v110, v110, v110
	v_max_f32_e32 v111, v111, v111
	v_max_f32_e32 v112, v112, v112
	v_max_f32_e32 v113, v113, v113
	v_max_f32_e32 v114, v114, v114
	v_max_f32_e32 v115, v115, v115
	v_med3_f32 v100, v100, s20, v129
	v_med3_f32 v101, v101, s20, v129
	v_med3_f32 v102, v102, s20, v129
	v_med3_f32 v103, v103, s20, v129
	v_med3_f32 v104, v104, s20, v129
	v_med3_f32 v105, v105, s20, v129
	v_med3_f32 v106, v106, s20, v129
	v_med3_f32 v107, v107, s20, v129
	v_med3_f32 v108, v108, s20, v129
	v_med3_f32 v109, v109, s20, v129
	v_med3_f32 v110, v110, s20, v129
	v_med3_f32 v111, v111, s20, v129
	v_med3_f32 v112, v112, s20, v129
	v_med3_f32 v113, v113, s20, v129
	v_med3_f32 v114, v114, s20, v129
	v_med3_f32 v115, v115, s20, v129
	v_mov_b32_e32 v116, 0
	v_mov_b32_e32 v117, 0
	v_mov_b32_e32 v118, 0
	v_mov_b32_e32 v119, 0
	v_cvt_pk_fp8_f32 v116, v100, v101
	v_cvt_pk_fp8_f32 v117, v104, v105
	v_cvt_pk_fp8_f32 v118, v108, v109
	v_cvt_pk_fp8_f32 v119, v112, v113
	v_cvt_pk_fp8_f32 v116, v102, v103 op_sel:[0,0,1]
	v_cvt_pk_fp8_f32 v117, v106, v107 op_sel:[0,0,1]
	v_cvt_pk_fp8_f32 v118, v110, v111 op_sel:[0,0,1]
	v_cvt_pk_fp8_f32 v119, v114, v115 op_sel:[0,0,1]
	s_nop 0
	global_store_dwordx4 v128, v[116:119], s[14:15]
	s_waitcnt vmcnt(12)
	v_mul_f32_e32 v68, 0x43000000, v68
	v_mul_f32_e32 v69, 0x43000000, v69
	v_mul_f32_e32 v70, 0x43000000, v70
	v_mul_f32_e32 v71, 0x43000000, v71
	ds_write_b128 v121, v[68:71]
	v_mul_f32_e32 v72, 0x43000000, v72
	v_mul_f32_e32 v73, 0x43000000, v73
	v_mul_f32_e32 v74, 0x43000000, v74
	v_mul_f32_e32 v75, 0x43000000, v75
	ds_write_b128 v121, v[72:75] offset:1024
	v_mul_f32_e32 v76, 0x43000000, v76
	v_mul_f32_e32 v77, 0x43000000, v77
	v_mul_f32_e32 v78, 0x43000000, v78
	v_mul_f32_e32 v79, 0x43000000, v79
	ds_write_b128 v121, v[76:79] offset:2048
	v_mul_f32_e32 v80, 0x43000000, v80
	v_mul_f32_e32 v81, 0x43000000, v81
	v_mul_f32_e32 v82, 0x43000000, v82
	v_mul_f32_e32 v83, 0x43000000, v83
	ds_write_b128 v121, v[80:83] offset:3072
	v_mul_f32_e32 v84, 0x43000000, v84
	v_mul_f32_e32 v85, 0x43000000, v85
	v_mul_f32_e32 v86, 0x43000000, v86
	v_mul_f32_e32 v87, 0x43000000, v87
	ds_write_b128 v121, v[84:87] offset:4096
	v_mul_f32_e32 v88, 0x43000000, v88
	v_mul_f32_e32 v89, 0x43000000, v89
	v_mul_f32_e32 v90, 0x43000000, v90
	v_mul_f32_e32 v91, 0x43000000, v91
	ds_write_b128 v121, v[88:91] offset:5120
	v_mul_f32_e32 v92, 0x43000000, v92
	v_mul_f32_e32 v93, 0x43000000, v93
	v_mul_f32_e32 v94, 0x43000000, v94
	v_mul_f32_e32 v95, 0x43000000, v95
	ds_write_b128 v121, v[92:95] offset:6144
	v_mul_f32_e32 v96, 0x43000000, v96
	v_mul_f32_e32 v97, 0x43000000, v97
	v_mul_f32_e32 v98, 0x43000000, v98
	v_mul_f32_e32 v99, 0x43000000, v99
	ds_write_b128 v121, v[96:99] offset:7168
	s_waitcnt lgkmcnt(0)
	s_barrier
; #define GAS __attribute__((address_space(1)))
; #define LAS __attribute__((address_space(3)))
; #define LDS_WAIT() asm volatile("s_waitcnt lgkmcnt(0)" ::: "memory")
; __device__ __forceinline__ unsigned pk4_fp8(float a, float b, float c, float d) {
;     a = fminf(fmaxf(a, -448.f), 448.f); b = fminf(fmaxf(b, -448.f), 448.f); c = fminf(fmaxf(c, -448.f), 448.f); d = fminf(fmaxf(d, -448.f), 448.f);
;     int w = __builtin_amdgcn_cvt_pk_fp8_f32(a, b, 0, false); w = __builtin_amdgcn_cvt_pk_fp8_f32(c, d, w, true); return (unsigned)w; }
;     ...
;     for (int i = 0; i < 32; ++i) v[i] = sc >= 0 ? W[(size_t)(k0 + 2 * i + (lane >> 5)) * Nsrc + sc] : 0.f;
; #pragma unroll
;     for (int i = 0; i < 32; ++i) { const int k = k0 + 2 * i + (lane >> 5); float x = v[i] * wscale; if (KS) x *= (k < ksplit ? ksA[k] : ksB[k - ksplit]); scr[(2 * i + (lane >> 5)) * 33 + (lane & 31)] = x; }
;     LDS_WAIT(); asm volatile("" ::: "memory");
;     const int c = lane & 7;
; #pragma unroll
;     for (int j = 0; j < 4; ++j) { const int n = (lane >> 3) + 8 * j; const LAS float* s = scr + (8 * c) * 33 + n;
;         const unsigned long long o = (unsigned long long)pg8::pk4_fp8(s[0 * 33], s[1 * 33], s[2 * 33], s[3 * 33]) | ((unsigned long long)pg8::pk4_fp8(s[4 * 33], s[5 * 33], s[6 * 33], s[7 * 33]) << 32);
;         *(GAS unsigned long long*)(WT + (size_t)(n0 + n) * K + k0 + 8 * c) = o; }
;     LDS_WAIT(); asm volatile("" ::: "memory");
	s_add_i32 s17, s16, 1632
	s_min_u32 s17, s17, 0x7ff
	s_lshr_b32 s18, s17, 5
	s_add_i32 s18, s18, 64
	s_and_b32 s19, s17, 31
	s_lshl_b32 s18, s18, 21
	s_lshl_b32 s19, s19, 9
	s_add_u32 s18, s18, s19
	s_add_u32 s12, s2, s18
	s_addc_u32 s13, s3, 0
	global_load_dwordx4 v[68:71], v126, s[12:13]
	s_add_u32 s12, s12, 0x8000
	s_addc_u32 s13, s13, 0
	global_load_dwordx4 v[72:75], v126, s[12:13]
	s_add_u32 s12, s12, 0x8000
	s_addc_u32 s13, s13, 0
	global_load_dwordx4 v[76:79], v126, s[12:13]
	s_add_u32 s12, s12, 0x8000
	s_addc_u32 s13, s13, 0
	global_load_dwordx4 v[80:83], v126, s[12:13]
	s_add_u32 s12, s12, 0x8000
	s_addc_u32 s13, s13, 0
	global_load_dwordx4 v[84:87], v126, s[12:13]
	s_add_u32 s12, s12, 0x8000
	s_addc_u32 s13, s13, 0
	global_load_dwordx4 v[88:91], v126, s[12:13]
	s_add_u32 s12, s12, 0x8000
	s_addc_u32 s13, s13, 0
	global_load_dwordx4 v[92:95], v126, s[12:13]
	s_add_u32 s12, s12, 0x8000
	s_addc_u32 s13, s13, 0
	global_load_dwordx4 v[96:99], v126, s[12:13]
	s_add_i32 s17, s16, 1440
	s_min_u32 s17, s17, 0x7ff
	s_lshr_b32 s18, s17, 5
	s_add_i32 s18, s18, 64
	s_and_b32 s19, s17, 31
	s_lshl_b32 s19, s19, 21
	s_lshl_b32 s18, s18, 7
	s_add_u32 s18, s18, s19
	s_add_u32 s14, s4, s18
	s_addc_u32 s15, s5, 0
	ds_read_b32 v100, v123
	ds_read_b32 v101, v123 offset:512
	ds_read_b32 v102, v123 offset:1024
	ds_read_b32 v103, v123 offset:1536
	ds_read_b32 v104, v123 offset:2048
	ds_read_b32 v105, v123 offset:2560
	ds_read_b32 v106, v123 offset:3072
	ds_read_b32 v107, v123 offset:3584
	ds_read_b32 v108, v123 offset:4096
	ds_read_b32 v109, v123 offset:4608
	ds_read_b32 v110, v123 offset:5120
	ds_read_b32 v111, v123 offset:5632
	ds_read_b32 v112, v123 offset:6144
	ds_read_b32 v113, v123 offset:6656
	ds_read_b32 v114, v123 offset:7168
	ds_read_b32 v115, v123 offset:7680
	s_waitcnt lgkmcnt(0)
	v_max_f32_e32 v100, v100, v100
	v_max_f32_e32 v101, v101, v101
	v_max_f32_e32 v102, v102, v102
	v_max_f32_e32 v103, v103, v103
	v_max_f32_e32 v104, v104, v104
	v_max_f32_e32 v105, v105, v105
	v_max_f32_e32 v106, v106, v106
	v_max_f32_e32 v107, v107, v107
	v_max_f32_e32 v108, v108, v108
	v_max_f32_e32 v109, v109, v109
	v_max_f32_e32 v110, v110, v110
	v_max_f32_e32 v111, v111, v111
	v_max_f32_e32 v112, v112, v112
	v_max_f32_e32 v113, v113, v113
	v_max_f32_e32 v114, v114, v114
	v_max_f32_e32 v115, v115, v115
	v_med3_f32 v100, v100, s20, v129
	v_med3_f32 v101, v101, s20, v129
	v_med3_f32 v102, v102, s20, v129
	v_med3_f32 v103, v103, s20, v129
	v_med3_f32 v104, v104, s20, v129
	v_med3_f32 v105, v105, s20, v129
	v_med3_f32 v106, v106, s20, v129
	v_med3_f32 v107, v107, s20, v129
	v_med3_f32 v108, v108, s20, v129
	v_med3_f32 v109, v109, s20, v129
	v_med3_f32 v110, v110, s20, v129
	v_med3_f32 v111, v111, s20, v129
	v_med3_f32 v112, v112, s20, v129
	v_med3_f32 v113, v113, s20, v129
	v_med3_f32 v114, v114, s20, v129
	v_med3_f32 v115, v115, s20, v129
	v_mov_b32_e32 v116, 0
	v_mov_b32_e32 v117, 0
	v_mov_b32_e32 v118, 0
	v_mov_b32_e32 v119, 0
	v_cvt_pk_fp8_f32 v116, v100, v101
	v_cvt_pk_fp8_f32 v117, v104, v105
	v_cvt_pk_fp8_f32 v118, v108, v109
	v_cvt_pk_fp8_f32 v119, v112, v113
	v_cvt_pk_fp8_f32 v116, v102, v103 op_sel:[0,0,1]
	v_cvt_pk_fp8_f32 v117, v106, v107 op_sel:[0,0,1]
	v_cvt_pk_fp8_f32 v118, v110, v111 op_sel:[0,0,1]
	v_cvt_pk_fp8_f32 v119, v114, v115 op_sel:[0,0,1]
	s_nop 0
	global_store_dwordx4 v127, v[116:119], s[14:15]
	ds_read_b32 v100, v125
	ds_read_b32 v101, v125 offset:512
	ds_read_b32 v102, v125 offset:1024
	ds_read_b32 v103, v125 offset:1536
	ds_read_b32 v104, v125 offset:2048
	ds_read_b32 v105, v125 offset:2560
	ds_read_b32 v106, v125 offset:3072
	ds_read_b32 v107, v125 offset:3584
	ds_read_b32 v108, v125 offset:4096
	ds_read_b32 v109, v125 offset:4608
	ds_read_b32 v110, v125 offset:5120
	ds_read_b32 v111, v125 offset:5632
	ds_read_b32 v112, v125 offset:6144
	ds_read_b32 v113, v125 offset:6656
	ds_read_b32 v114, v125 offset:7168
	ds_read_b32 v115, v125 offset:7680
	s_waitcnt lgkmcnt(0)
	v_max_f32_e32 v100, v100, v100
	v_max_f32_e32 v101, v101, v101
	v_max_f32_e32 v102, v102, v102
	v_max_f32_e32 v103, v103, v103
	v_max_f32_e32 v104, v104, v104
	v_max_f32_e32 v105, v105, v105
	v_max_f32_e32 v106, v106, v106
	v_max_f32_e32 v107, v107, v107
	v_max_f32_e32 v108, v108, v108
	v_max_f32_e32 v109, v109, v109
	v_max_f32_e32 v110, v110, v110
	v_max_f32_e32 v111, v111, v111
	v_max_f32_e32 v112, v112, v112
	v_max_f32_e32 v113, v113, v113
	v_max_f32_e32 v114, v114, v114
	v_max_f32_e32 v115, v115, v115
	v_med3_f32 v100, v100, s20, v129
	v_med3_f32 v101, v101, s20, v129
	v_med3_f32 v102, v102, s20, v129
	v_med3_f32 v103, v103, s20, v129
	v_med3_f32 v104, v104, s20, v129
	v_med3_f32 v105, v105, s20, v129
	v_med3_f32 v106, v106, s20, v129
	v_med3_f32 v107, v107, s20, v129
	v_med3_f32 v108, v108, s20, v129
	v_med3_f32 v109, v109, s20, v129
	v_med3_f32 v110, v110, s20, v129
	v_med3_f32 v111, v111, s20, v129
	v_med3_f32 v112, v112, s20, v129
	v_med3_f32 v113, v113, s20, v129
	v_med3_f32 v114, v114, s20, v129
	v_med3_f32 v115, v115, s20, v129
	v_mov_b32_e32 v116, 0
	v_mov_b32_e32 v117, 0
	v_mov_b32_e32 v118, 0
	v_mov_b32_e32 v119, 0
	v_cvt_pk_fp8_f32 v116, v100, v101
	v_cvt_pk_fp8_f32 v117, v104, v105
	v_cvt_pk_fp8_f32 v118, v108, v109
	v_cvt_pk_fp8_f32 v119, v112, v113
	v_cvt_pk_fp8_f32 v116, v102, v103 op_sel:[0,0,1]
	v_cvt_pk_fp8_f32 v117, v106, v107 op_sel:[0,0,1]
	v_cvt_pk_fp8_f32 v118, v110, v111 op_sel:[0,0,1]
	v_cvt_pk_fp8_f32 v119, v114, v115 op_sel:[0,0,1]
	s_nop 0
	global_store_dwordx4 v128, v[116:119], s[14:15]
	s_waitcnt vmcnt(12)
	v_mul_f32_e32 v36, 0x43000000, v36
	v_mul_f32_e32 v37, 0x43000000, v37
	v_mul_f32_e32 v38, 0x43000000, v38
	v_mul_f32_e32 v39, 0x43000000, v39
	ds_write_b128 v120, v[36:39]
	v_mul_f32_e32 v40, 0x43000000, v40
	v_mul_f32_e32 v41, 0x43000000, v41
	v_mul_f32_e32 v42, 0x43000000, v42
	v_mul_f32_e32 v43, 0x43000000, v43
	ds_write_b128 v120, v[40:43] offset:1024
	v_mul_f32_e32 v44, 0x43000000, v44
	v_mul_f32_e32 v45, 0x43000000, v45
	v_mul_f32_e32 v46, 0x43000000, v46
	v_mul_f32_e32 v47, 0x43000000, v47
	ds_write_b128 v120, v[44:47] offset:2048
	v_mul_f32_e32 v48, 0x43000000, v48
	v_mul_f32_e32 v49, 0x43000000, v49
	v_mul_f32_e32 v50, 0x43000000, v50
	v_mul_f32_e32 v51, 0x43000000, v51
	ds_write_b128 v120, v[48:51] offset:3072
	v_mul_f32_e32 v52, 0x43000000, v52
	v_mul_f32_e32 v53, 0x43000000, v53
	v_mul_f32_e32 v54, 0x43000000, v54
	v_mul_f32_e32 v55, 0x43000000, v55
	ds_write_b128 v120, v[52:55] offset:4096
	v_mul_f32_e32 v56, 0x43000000, v56
	v_mul_f32_e32 v57, 0x43000000, v57
	v_mul_f32_e32 v58, 0x43000000, v58
	v_mul_f32_e32 v59, 0x43000000, v59
	ds_write_b128 v120, v[56:59] offset:5120
	v_mul_f32_e32 v60, 0x43000000, v60
	v_mul_f32_e32 v61, 0x43000000, v61
	v_mul_f32_e32 v62, 0x43000000, v62
	v_mul_f32_e32 v63, 0x43000000, v63
	ds_write_b128 v120, v[60:63] offset:6144
	v_mul_f32_e32 v64, 0x43000000, v64
	v_mul_f32_e32 v65, 0x43000000, v65
	v_mul_f32_e32 v66, 0x43000000, v66
	v_mul_f32_e32 v67, 0x43000000, v67
	ds_write_b128 v120, v[64:67] offset:7168
	s_waitcnt lgkmcnt(0)
	s_barrier
; #define GAS __attribute__((address_space(1)))
; #define LAS __attribute__((address_space(3)))
; #define LDS_WAIT() asm volatile("s_waitcnt lgkmcnt(0)" ::: "memory")
; __device__ __forceinline__ unsigned pk4_fp8(float a, float b, float c, float d) {
;     a = fminf(fmaxf(a, -448.f), 448.f); b = fminf(fmaxf(b, -448.f), 448.f); c = fminf(fmaxf(c, -448.f), 448.f); d = fminf(fmaxf(d, -448.f), 448.f);
;     int w = __builtin_amdgcn_cvt_pk_fp8_f32(a, b, 0, false); w = __builtin_amdgcn_cvt_pk_fp8_f32(c, d, w, true); return (unsigned)w; }
;     ...
;     for (int i = 0; i < 32; ++i) v[i] = sc >= 0 ? W[(size_t)(k0 + 2 * i + (lane >> 5)) * Nsrc + sc] : 0.f;
; #pragma unroll
;     for (int i = 0; i < 32; ++i) { const int k = k0 + 2 * i + (lane >> 5); float x = v[i] * wscale; if (KS) x *= (k < ksplit ? ksA[k] : ksB[k - ksplit]); scr[(2 * i + (lane >> 5)) * 33 + (lane & 31)] = x; }
;     LDS_WAIT(); asm volatile("" ::: "memory");
;     const int c = lane & 7;
; #pragma unroll
;     for (int j = 0; j < 4; ++j) { const int n = (lane >> 3) + 8 * j; const LAS float* s = scr + (8 * c) * 33 + n;
;         const unsigned long long o = (unsigned long long)pg8::pk4_fp8(s[0 * 33], s[1 * 33], s[2 * 33], s[3 * 33]) | ((unsigned long long)pg8::pk4_fp8(s[4 * 33], s[5 * 33], s[6 * 33], s[7 * 33]) << 32);
;         *(GAS unsigned long long*)(WT + (size_t)(n0 + n) * K + k0 + 8 * c) = o; }
;     LDS_WAIT(); asm volatile("" ::: "memory");
	s_add_i32 s17, s16, 1728
	s_min_u32 s17, s17, 0x7ff
	s_lshr_b32 s18, s17, 5
	s_add_i32 s18, s18, 64
	s_and_b32 s19, s17, 31
	s_lshl_b32 s18, s18, 21
	s_lshl_b32 s19, s19, 9
	s_add_u32 s18, s18, s19
	s_add_u32 s12, s2, s18
	s_addc_u32 s13, s3, 0
	global_load_dwordx4 v[36:39], v126, s[12:13]
	s_add_u32 s12, s12, 0x8000
	s_addc_u32 s13, s13, 0
	global_load_dwordx4 v[40:43], v126, s[12:13]
	s_add_u32 s12, s12, 0x8000
	s_addc_u32 s13, s13, 0
	global_load_dwordx4 v[44:47], v126, s[12:13]
	s_add_u32 s12, s12, 0x8000
	s_addc_u32 s13, s13, 0
	global_load_dwordx4 v[48:51], v126, s[12:13]
	s_add_u32 s12, s12, 0x8000
	s_addc_u32 s13, s13, 0
	global_load_dwordx4 v[52:55], v126, s[12:13]
	s_add_u32 s12, s12, 0x8000
	s_addc_u32 s13, s13, 0
	global_load_dwordx4 v[56:59], v126, s[12:13]
	s_add_u32 s12, s12, 0x8000
	s_addc_u32 s13, s13, 0
	global_load_dwordx4 v[60:63], v126, s[12:13]
	s_add_u32 s12, s12, 0x8000
	s_addc_u32 s13, s13, 0
	global_load_dwordx4 v[64:67], v126, s[12:13]
	s_add_i32 s17, s16, 1536
	s_min_u32 s17, s17, 0x7ff
	s_lshr_b32 s18, s17, 5
	s_add_i32 s18, s18, 64
	s_and_b32 s19, s17, 31
	s_lshl_b32 s19, s19, 21
	s_lshl_b32 s18, s18, 7
	s_add_u32 s18, s18, s19
	s_add_u32 s14, s4, s18
	s_addc_u32 s15, s5, 0
	ds_read_b32 v100, v122
	ds_read_b32 v101, v122 offset:512
	ds_read_b32 v102, v122 offset:1024
	ds_read_b32 v103, v122 offset:1536
	ds_read_b32 v104, v122 offset:2048
	ds_read_b32 v105, v122 offset:2560
	ds_read_b32 v106, v122 offset:3072
	ds_read_b32 v107, v122 offset:3584
	ds_read_b32 v108, v122 offset:4096
	ds_read_b32 v109, v122 offset:4608
	ds_read_b32 v110, v122 offset:5120
	ds_read_b32 v111, v122 offset:5632
	ds_read_b32 v112, v122 offset:6144
	ds_read_b32 v113, v122 offset:6656
	ds_read_b32 v114, v122 offset:7168
	ds_read_b32 v115, v122 offset:7680
	s_waitcnt lgkmcnt(0)
	v_max_f32_e32 v100, v100, v100
	v_max_f32_e32 v101, v101, v101
	v_max_f32_e32 v102, v102, v102
	v_max_f32_e32 v103, v103, v103
	v_max_f32_e32 v104, v104, v104
	v_max_f32_e32 v105, v105, v105
	v_max_f32_e32 v106, v106, v106
	v_max_f32_e32 v107, v107, v107
	v_max_f32_e32 v108, v108, v108
	v_max_f32_e32 v109, v109, v109
	v_max_f32_e32 v110, v110, v110
	v_max_f32_e32 v111, v111, v111
	v_max_f32_e32 v112, v112, v112
	v_max_f32_e32 v113, v113, v113
	v_max_f32_e32 v114, v114, v114
	v_max_f32_e32 v115, v115, v115
	v_med3_f32 v100, v100, s20, v129
	v_med3_f32 v101, v101, s20, v129
	v_med3_f32 v102, v102, s20, v129
	v_med3_f32 v103, v103, s20, v129
	v_med3_f32 v104, v104, s20, v129
	v_med3_f32 v105, v105, s20, v129
	v_med3_f32 v106, v106, s20, v129
	v_med3_f32 v107, v107, s20, v129
	v_med3_f32 v108, v108, s20, v129
	v_med3_f32 v109, v109, s20, v129
	v_med3_f32 v110, v110, s20, v129
	v_med3_f32 v111, v111, s20, v129
	v_med3_f32 v112, v112, s20, v129
	v_med3_f32 v113, v113, s20, v129
	v_med3_f32 v114, v114, s20, v129
	v_med3_f32 v115, v115, s20, v129
	v_mov_b32_e32 v116, 0
	v_mov_b32_e32 v117, 0
	v_mov_b32_e32 v118, 0
	v_mov_b32_e32 v119, 0
	v_cvt_pk_fp8_f32 v116, v100, v101
	v_cvt_pk_fp8_f32 v117, v104, v105
	v_cvt_pk_fp8_f32 v118, v108, v109
	v_cvt_pk_fp8_f32 v119, v112, v113
	v_cvt_pk_fp8_f32 v116, v102, v103 op_sel:[0,0,1]
	v_cvt_pk_fp8_f32 v117, v106, v107 op_sel:[0,0,1]
	v_cvt_pk_fp8_f32 v118, v110, v111 op_sel:[0,0,1]
	v_cvt_pk_fp8_f32 v119, v114, v115 op_sel:[0,0,1]
	s_nop 0
	global_store_dwordx4 v127, v[116:119], s[14:15]
	ds_read_b32 v100, v124
	ds_read_b32 v101, v124 offset:512
	ds_read_b32 v102, v124 offset:1024
	ds_read_b32 v103, v124 offset:1536
	ds_read_b32 v104, v124 offset:2048
	ds_read_b32 v105, v124 offset:2560
	ds_read_b32 v106, v124 offset:3072
	ds_read_b32 v107, v124 offset:3584
	ds_read_b32 v108, v124 offset:4096
	ds_read_b32 v109, v124 offset:4608
	ds_read_b32 v110, v124 offset:5120
	ds_read_b32 v111, v124 offset:5632
	ds_read_b32 v112, v124 offset:6144
	ds_read_b32 v113, v124 offset:6656
	ds_read_b32 v114, v124 offset:7168
	ds_read_b32 v115, v124 offset:7680
	s_waitcnt lgkmcnt(0)
	v_max_f32_e32 v100, v100, v100
	v_max_f32_e32 v101, v101, v101
	v_max_f32_e32 v102, v102, v102
	v_max_f32_e32 v103, v103, v103
	v_max_f32_e32 v104, v104, v104
	v_max_f32_e32 v105, v105, v105
	v_max_f32_e32 v106, v106, v106
	v_max_f32_e32 v107, v107, v107
	v_max_f32_e32 v108, v108, v108
	v_max_f32_e32 v109, v109, v109
	v_max_f32_e32 v110, v110, v110
	v_max_f32_e32 v111, v111, v111
	v_max_f32_e32 v112, v112, v112
	v_max_f32_e32 v113, v113, v113
	v_max_f32_e32 v114, v114, v114
	v_max_f32_e32 v115, v115, v115
	v_med3_f32 v100, v100, s20, v129
	v_med3_f32 v101, v101, s20, v129
	v_med3_f32 v102, v102, s20, v129
	v_med3_f32 v103, v103, s20, v129
	v_med3_f32 v104, v104, s20, v129
	v_med3_f32 v105, v105, s20, v129
	v_med3_f32 v106, v106, s20, v129
	v_med3_f32 v107, v107, s20, v129
	v_med3_f32 v108, v108, s20, v129
	v_med3_f32 v109, v109, s20, v129
	v_med3_f32 v110, v110, s20, v129
	v_med3_f32 v111, v111, s20, v129
	v_med3_f32 v112, v112, s20, v129
	v_med3_f32 v113, v113, s20, v129
	v_med3_f32 v114, v114, s20, v129
	v_med3_f32 v115, v115, s20, v129
	v_mov_b32_e32 v116, 0
	v_mov_b32_e32 v117, 0
	v_mov_b32_e32 v118, 0
	v_mov_b32_e32 v119, 0
	v_cvt_pk_fp8_f32 v116, v100, v101
	v_cvt_pk_fp8_f32 v117, v104, v105
	v_cvt_pk_fp8_f32 v118, v108, v109
	v_cvt_pk_fp8_f32 v119, v112, v113
	v_cvt_pk_fp8_f32 v116, v102, v103 op_sel:[0,0,1]
	v_cvt_pk_fp8_f32 v117, v106, v107 op_sel:[0,0,1]
	v_cvt_pk_fp8_f32 v118, v110, v111 op_sel:[0,0,1]
	v_cvt_pk_fp8_f32 v119, v114, v115 op_sel:[0,0,1]
	s_nop 0
	global_store_dwordx4 v128, v[116:119], s[14:15]
	s_waitcnt vmcnt(12)
	v_mul_f32_e32 v68, 0x43000000, v68
	v_mul_f32_e32 v69, 0x43000000, v69
	v_mul_f32_e32 v70, 0x43000000, v70
	v_mul_f32_e32 v71, 0x43000000, v71
	ds_write_b128 v121, v[68:71]
	v_mul_f32_e32 v72, 0x43000000, v72
	v_mul_f32_e32 v73, 0x43000000, v73
	v_mul_f32_e32 v74, 0x43000000, v74
	v_mul_f32_e32 v75, 0x43000000, v75
	ds_write_b128 v121, v[72:75] offset:1024
	v_mul_f32_e32 v76, 0x43000000, v76
	v_mul_f32_e32 v77, 0x43000000, v77
	v_mul_f32_e32 v78, 0x43000000, v78
	v_mul_f32_e32 v79, 0x43000000, v79
	ds_write_b128 v121, v[76:79] offset:2048
	v_mul_f32_e32 v80, 0x43000000, v80
	v_mul_f32_e32 v81, 0x43000000, v81
	v_mul_f32_e32 v82, 0x43000000, v82
	v_mul_f32_e32 v83, 0x43000000, v83
	ds_write_b128 v121, v[80:83] offset:3072
	v_mul_f32_e32 v84, 0x43000000, v84
	v_mul_f32_e32 v85, 0x43000000, v85
	v_mul_f32_e32 v86, 0x43000000, v86
	v_mul_f32_e32 v87, 0x43000000, v87
	ds_write_b128 v121, v[84:87] offset:4096
	v_mul_f32_e32 v88, 0x43000000, v88
	v_mul_f32_e32 v89, 0x43000000, v89
	v_mul_f32_e32 v90, 0x43000000, v90
	v_mul_f32_e32 v91, 0x43000000, v91
	ds_write_b128 v121, v[88:91] offset:5120
	v_mul_f32_e32 v92, 0x43000000, v92
	v_mul_f32_e32 v93, 0x43000000, v93
	v_mul_f32_e32 v94, 0x43000000, v94
	v_mul_f32_e32 v95, 0x43000000, v95
	ds_write_b128 v121, v[92:95] offset:6144
	v_mul_f32_e32 v96, 0x43000000, v96
	v_mul_f32_e32 v97, 0x43000000, v97
	v_mul_f32_e32 v98, 0x43000000, v98
	v_mul_f32_e32 v99, 0x43000000, v99
	ds_write_b128 v121, v[96:99] offset:7168
	s_waitcnt lgkmcnt(0)
	s_barrier
; #define GAS __attribute__((address_space(1)))
; #define LAS __attribute__((address_space(3)))
; #define LDS_WAIT() asm volatile("s_waitcnt lgkmcnt(0)" ::: "memory")
; __device__ __forceinline__ unsigned pk4_fp8(float a, float b, float c, float d) {
;     a = fminf(fmaxf(a, -448.f), 448.f); b = fminf(fmaxf(b, -448.f), 448.f); c = fminf(fmaxf(c, -448.f), 448.f); d = fminf(fmaxf(d, -448.f), 448.f);
;     int w = __builtin_amdgcn_cvt_pk_fp8_f32(a, b, 0, false); w = __builtin_amdgcn_cvt_pk_fp8_f32(c, d, w, true); return (unsigned)w; }
;     ...
;     for (int i = 0; i < 32; ++i) v[i] = sc >= 0 ? W[(size_t)(k0 + 2 * i + (lane >> 5)) * Nsrc + sc] : 0.f;
; #pragma unroll
;     for (int i = 0; i < 32; ++i) { const int k = k0 + 2 * i + (lane >> 5); float x = v[i] * wscale; if (KS) x *= (k < ksplit ? ksA[k] : ksB[k - ksplit]); scr[(2 * i + (lane >> 5)) * 33 + (lane & 31)] = x; }
;     LDS_WAIT(); asm volatile("" ::: "memory");
;     const int c = lane & 7;
; #pragma unroll
;     for (int j = 0; j < 4; ++j) { const int n = (lane >> 3) + 8 * j; const LAS float* s = scr + (8 * c) * 33 + n;
;         const unsigned long long o = (unsigned long long)pg8::pk4_fp8(s[0 * 33], s[1 * 33], s[2 * 33], s[3 * 33]) | ((unsigned long long)pg8::pk4_fp8(s[4 * 33], s[5 * 33], s[6 * 33], s[7 * 33]) << 32);
;         *(GAS unsigned long long*)(WT + (size_t)(n0 + n) * K + k0 + 8 * c) = o; }
;     LDS_WAIT(); asm volatile("" ::: "memory");
	s_add_i32 s17, s16, 1824
	s_min_u32 s17, s17, 0x7ff
	s_lshr_b32 s18, s17, 5
	s_add_i32 s18, s18, 64
	s_and_b32 s19, s17, 31
	s_lshl_b32 s18, s18, 21
	s_lshl_b32 s19, s19, 9
	s_add_u32 s18, s18, s19
	s_add_u32 s12, s2, s18
	s_addc_u32 s13, s3, 0
	global_load_dwordx4 v[68:71], v126, s[12:13]
	s_add_u32 s12, s12, 0x8000
	s_addc_u32 s13, s13, 0
	global_load_dwordx4 v[72:75], v126, s[12:13]
	s_add_u32 s12, s12, 0x8000
	s_addc_u32 s13, s13, 0
	global_load_dwordx4 v[76:79], v126, s[12:13]
	s_add_u32 s12, s12, 0x8000
	s_addc_u32 s13, s13, 0
	global_load_dwordx4 v[80:83], v126, s[12:13]
	s_add_u32 s12, s12, 0x8000
	s_addc_u32 s13, s13, 0
	global_load_dwordx4 v[84:87], v126, s[12:13]
	s_add_u32 s12, s12, 0x8000
	s_addc_u32 s13, s13, 0
	global_load_dwordx4 v[88:91], v126, s[12:13]
	s_add_u32 s12, s12, 0x8000
	s_addc_u32 s13, s13, 0
	global_load_dwordx4 v[92:95], v126, s[12:13]
	s_add_u32 s12, s12, 0x8000
	s_addc_u32 s13, s13, 0
	global_load_dwordx4 v[96:99], v126, s[12:13]
	s_add_i32 s17, s16, 1632
	s_min_u32 s17, s17, 0x7ff
	s_lshr_b32 s18, s17, 5
	s_add_i32 s18, s18, 64
	s_and_b32 s19, s17, 31
	s_lshl_b32 s19, s19, 21
	s_lshl_b32 s18, s18, 7
	s_add_u32 s18, s18, s19
	s_add_u32 s14, s4, s18
	s_addc_u32 s15, s5, 0
	ds_read_b32 v100, v123
	ds_read_b32 v101, v123 offset:512
	ds_read_b32 v102, v123 offset:1024
	ds_read_b32 v103, v123 offset:1536
	ds_read_b32 v104, v123 offset:2048
	ds_read_b32 v105, v123 offset:2560
	ds_read_b32 v106, v123 offset:3072
	ds_read_b32 v107, v123 offset:3584
	ds_read_b32 v108, v123 offset:4096
	ds_read_b32 v109, v123 offset:4608
	ds_read_b32 v110, v123 offset:5120
	ds_read_b32 v111, v123 offset:5632
	ds_read_b32 v112, v123 offset:6144
	ds_read_b32 v113, v123 offset:6656
	ds_read_b32 v114, v123 offset:7168
	ds_read_b32 v115, v123 offset:7680
	s_waitcnt lgkmcnt(0)
	v_max_f32_e32 v100, v100, v100
	v_max_f32_e32 v101, v101, v101
	v_max_f32_e32 v102, v102, v102
	v_max_f32_e32 v103, v103, v103
	v_max_f32_e32 v104, v104, v104
	v_max_f32_e32 v105, v105, v105
	v_max_f32_e32 v106, v106, v106
	v_max_f32_e32 v107, v107, v107
	v_max_f32_e32 v108, v108, v108
	v_max_f32_e32 v109, v109, v109
	v_max_f32_e32 v110, v110, v110
	v_max_f32_e32 v111, v111, v111
	v_max_f32_e32 v112, v112, v112
	v_max_f32_e32 v113, v113, v113
	v_max_f32_e32 v114, v114, v114
	v_max_f32_e32 v115, v115, v115
	v_med3_f32 v100, v100, s20, v129
	v_med3_f32 v101, v101, s20, v129
	v_med3_f32 v102, v102, s20, v129
	v_med3_f32 v103, v103, s20, v129
	v_med3_f32 v104, v104, s20, v129
	v_med3_f32 v105, v105, s20, v129
	v_med3_f32 v106, v106, s20, v129
	v_med3_f32 v107, v107, s20, v129
	v_med3_f32 v108, v108, s20, v129
	v_med3_f32 v109, v109, s20, v129
	v_med3_f32 v110, v110, s20, v129
	v_med3_f32 v111, v111, s20, v129
	v_med3_f32 v112, v112, s20, v129
	v_med3_f32 v113, v113, s20, v129
	v_med3_f32 v114, v114, s20, v129
	v_med3_f32 v115, v115, s20, v129
	v_mov_b32_e32 v116, 0
	v_mov_b32_e32 v117, 0
	v_mov_b32_e32 v118, 0
	v_mov_b32_e32 v119, 0
	v_cvt_pk_fp8_f32 v116, v100, v101
	v_cvt_pk_fp8_f32 v117, v104, v105
	v_cvt_pk_fp8_f32 v118, v108, v109
	v_cvt_pk_fp8_f32 v119, v112, v113
	v_cvt_pk_fp8_f32 v116, v102, v103 op_sel:[0,0,1]
	v_cvt_pk_fp8_f32 v117, v106, v107 op_sel:[0,0,1]
	v_cvt_pk_fp8_f32 v118, v110, v111 op_sel:[0,0,1]
	v_cvt_pk_fp8_f32 v119, v114, v115 op_sel:[0,0,1]
	s_nop 0
	global_store_dwordx4 v127, v[116:119], s[14:15]
	ds_read_b32 v100, v125
	ds_read_b32 v101, v125 offset:512
	ds_read_b32 v102, v125 offset:1024
	ds_read_b32 v103, v125 offset:1536
	ds_read_b32 v104, v125 offset:2048
	ds_read_b32 v105, v125 offset:2560
	ds_read_b32 v106, v125 offset:3072
	ds_read_b32 v107, v125 offset:3584
	ds_read_b32 v108, v125 offset:4096
	ds_read_b32 v109, v125 offset:4608
	ds_read_b32 v110, v125 offset:5120
	ds_read_b32 v111, v125 offset:5632
	ds_read_b32 v112, v125 offset:6144
	ds_read_b32 v113, v125 offset:6656
	ds_read_b32 v114, v125 offset:7168
	ds_read_b32 v115, v125 offset:7680
	s_waitcnt lgkmcnt(0)
	v_max_f32_e32 v100, v100, v100
	v_max_f32_e32 v101, v101, v101
	v_max_f32_e32 v102, v102, v102
	v_max_f32_e32 v103, v103, v103
	v_max_f32_e32 v104, v104, v104
	v_max_f32_e32 v105, v105, v105
	v_max_f32_e32 v106, v106, v106
	v_max_f32_e32 v107, v107, v107
	v_max_f32_e32 v108, v108, v108
	v_max_f32_e32 v109, v109, v109
	v_max_f32_e32 v110, v110, v110
	v_max_f32_e32 v111, v111, v111
	v_max_f32_e32 v112, v112, v112
	v_max_f32_e32 v113, v113, v113
	v_max_f32_e32 v114, v114, v114
	v_max_f32_e32 v115, v115, v115
	v_med3_f32 v100, v100, s20, v129
	v_med3_f32 v101, v101, s20, v129
	v_med3_f32 v102, v102, s20, v129
	v_med3_f32 v103, v103, s20, v129
	v_med3_f32 v104, v104, s20, v129
	v_med3_f32 v105, v105, s20, v129
	v_med3_f32 v106, v106, s20, v129
	v_med3_f32 v107, v107, s20, v129
	v_med3_f32 v108, v108, s20, v129
	v_med3_f32 v109, v109, s20, v129
	v_med3_f32 v110, v110, s20, v129
	v_med3_f32 v111, v111, s20, v129
	v_med3_f32 v112, v112, s20, v129
	v_med3_f32 v113, v113, s20, v129
	v_med3_f32 v114, v114, s20, v129
	v_med3_f32 v115, v115, s20, v129
	v_mov_b32_e32 v116, 0
	v_mov_b32_e32 v117, 0
	v_mov_b32_e32 v118, 0
	v_mov_b32_e32 v119, 0
	v_cvt_pk_fp8_f32 v116, v100, v101
	v_cvt_pk_fp8_f32 v117, v104, v105
	v_cvt_pk_fp8_f32 v118, v108, v109
	v_cvt_pk_fp8_f32 v119, v112, v113
	v_cvt_pk_fp8_f32 v116, v102, v103 op_sel:[0,0,1]
	v_cvt_pk_fp8_f32 v117, v106, v107 op_sel:[0,0,1]
	v_cvt_pk_fp8_f32 v118, v110, v111 op_sel:[0,0,1]
	v_cvt_pk_fp8_f32 v119, v114, v115 op_sel:[0,0,1]
	s_nop 0
	global_store_dwordx4 v128, v[116:119], s[14:15]
	s_waitcnt vmcnt(12)
	v_mul_f32_e32 v36, 0x43000000, v36
	v_mul_f32_e32 v37, 0x43000000, v37
	v_mul_f32_e32 v38, 0x43000000, v38
	v_mul_f32_e32 v39, 0x43000000, v39
	ds_write_b128 v120, v[36:39]
	v_mul_f32_e32 v40, 0x43000000, v40
	v_mul_f32_e32 v41, 0x43000000, v41
	v_mul_f32_e32 v42, 0x43000000, v42
	v_mul_f32_e32 v43, 0x43000000, v43
	ds_write_b128 v120, v[40:43] offset:1024
	v_mul_f32_e32 v44, 0x43000000, v44
	v_mul_f32_e32 v45, 0x43000000, v45
	v_mul_f32_e32 v46, 0x43000000, v46
	v_mul_f32_e32 v47, 0x43000000, v47
	ds_write_b128 v120, v[44:47] offset:2048
	v_mul_f32_e32 v48, 0x43000000, v48
	v_mul_f32_e32 v49, 0x43000000, v49
	v_mul_f32_e32 v50, 0x43000000, v50
	v_mul_f32_e32 v51, 0x43000000, v51
	ds_write_b128 v120, v[48:51] offset:3072
	v_mul_f32_e32 v52, 0x43000000, v52
	v_mul_f32_e32 v53, 0x43000000, v53
	v_mul_f32_e32 v54, 0x43000000, v54
	v_mul_f32_e32 v55, 0x43000000, v55
	ds_write_b128 v120, v[52:55] offset:4096
	v_mul_f32_e32 v56, 0x43000000, v56
	v_mul_f32_e32 v57, 0x43000000, v57
	v_mul_f32_e32 v58, 0x43000000, v58
	v_mul_f32_e32 v59, 0x43000000, v59
	ds_write_b128 v120, v[56:59] offset:5120
	v_mul_f32_e32 v60, 0x43000000, v60
	v_mul_f32_e32 v61, 0x43000000, v61
	v_mul_f32_e32 v62, 0x43000000, v62
	v_mul_f32_e32 v63, 0x43000000, v63
	ds_write_b128 v120, v[60:63] offset:6144
	v_mul_f32_e32 v64, 0x43000000, v64
	v_mul_f32_e32 v65, 0x43000000, v65
	v_mul_f32_e32 v66, 0x43000000, v66
	v_mul_f32_e32 v67, 0x43000000, v67
	ds_write_b128 v120, v[64:67] offset:7168
	s_waitcnt lgkmcnt(0)
	s_barrier
; #define GAS __attribute__((address_space(1)))
; #define LAS __attribute__((address_space(3)))
; #define LDS_WAIT() asm volatile("s_waitcnt lgkmcnt(0)" ::: "memory")
; __device__ __forceinline__ unsigned pk4_fp8(float a, float b, float c, float d) {
;     a = fminf(fmaxf(a, -448.f), 448.f); b = fminf(fmaxf(b, -448.f), 448.f); c = fminf(fmaxf(c, -448.f), 448.f); d = fminf(fmaxf(d, -448.f), 448.f);
;     int w = __builtin_amdgcn_cvt_pk_fp8_f32(a, b, 0, false); w = __builtin_amdgcn_cvt_pk_fp8_f32(c, d, w, true); return (unsigned)w; }
;     ...
;     for (int i = 0; i < 32; ++i) v[i] = sc >= 0 ? W[(size_t)(k0 + 2 * i + (lane >> 5)) * Nsrc + sc] : 0.f;
; #pragma unroll
;     for (int i = 0; i < 32; ++i) { const int k = k0 + 2 * i + (lane >> 5); float x = v[i] * wscale; if (KS) x *= (k < ksplit ? ksA[k] : ksB[k - ksplit]); scr[(2 * i + (lane >> 5)) * 33 + (lane & 31)] = x; }
;     LDS_WAIT(); asm volatile("" ::: "memory");
;     const int c = lane & 7;
; #pragma unroll
;     for (int j = 0; j < 4; ++j) { const int n = (lane >> 3) + 8 * j; const LAS float* s = scr + (8 * c) * 33 + n;
;         const unsigned long long o = (unsigned long long)pg8::pk4_fp8(s[0 * 33], s[1 * 33], s[2 * 33], s[3 * 33]) | ((unsigned long long)pg8::pk4_fp8(s[4 * 33], s[5 * 33], s[6 * 33], s[7 * 33]) << 32);
;         *(GAS unsigned long long*)(WT + (size_t)(n0 + n) * K + k0 + 8 * c) = o; }
;     LDS_WAIT(); asm volatile("" ::: "memory");
	s_add_i32 s17, s16, 1920
	s_min_u32 s17, s17, 0x7ff
	s_lshr_b32 s18, s17, 5
	s_add_i32 s18, s18, 64
	s_and_b32 s19, s17, 31
	s_lshl_b32 s18, s18, 21
	s_lshl_b32 s19, s19, 9
	s_add_u32 s18, s18, s19
	s_add_u32 s12, s2, s18
	s_addc_u32 s13, s3, 0
	global_load_dwordx4 v[36:39], v126, s[12:13]
	s_add_u32 s12, s12, 0x8000
	s_addc_u32 s13, s13, 0
	global_load_dwordx4 v[40:43], v126, s[12:13]
	s_add_u32 s12, s12, 0x8000
	s_addc_u32 s13, s13, 0
	global_load_dwordx4 v[44:47], v126, s[12:13]
	s_add_u32 s12, s12, 0x8000
	s_addc_u32 s13, s13, 0
	global_load_dwordx4 v[48:51], v126, s[12:13]
	s_add_u32 s12, s12, 0x8000
	s_addc_u32 s13, s13, 0
	global_load_dwordx4 v[52:55], v126, s[12:13]
	s_add_u32 s12, s12, 0x8000
	s_addc_u32 s13, s13, 0
	global_load_dwordx4 v[56:59], v126, s[12:13]
	s_add_u32 s12, s12, 0x8000
	s_addc_u32 s13, s13, 0
	global_load_dwordx4 v[60:63], v126, s[12:13]
	s_add_u32 s12, s12, 0x8000
	s_addc_u32 s13, s13, 0
	global_load_dwordx4 v[64:67], v126, s[12:13]
	s_add_i32 s17, s16, 1728
	s_min_u32 s17, s17, 0x7ff
	s_lshr_b32 s18, s17, 5
	s_add_i32 s18, s18, 64
	s_and_b32 s19, s17, 31
	s_lshl_b32 s19, s19, 21
	s_lshl_b32 s18, s18, 7
	s_add_u32 s18, s18, s19
	s_add_u32 s14, s4, s18
	s_addc_u32 s15, s5, 0
	ds_read_b32 v100, v122
	ds_read_b32 v101, v122 offset:512
	ds_read_b32 v102, v122 offset:1024
	ds_read_b32 v103, v122 offset:1536
	ds_read_b32 v104, v122 offset:2048
	ds_read_b32 v105, v122 offset:2560
	ds_read_b32 v106, v122 offset:3072
	ds_read_b32 v107, v122 offset:3584
	ds_read_b32 v108, v122 offset:4096
	ds_read_b32 v109, v122 offset:4608
	ds_read_b32 v110, v122 offset:5120
	ds_read_b32 v111, v122 offset:5632
	ds_read_b32 v112, v122 offset:6144
	ds_read_b32 v113, v122 offset:6656
	ds_read_b32 v114, v122 offset:7168
	ds_read_b32 v115, v122 offset:7680
	s_waitcnt lgkmcnt(0)
	v_max_f32_e32 v100, v100, v100
	v_max_f32_e32 v101, v101, v101
	v_max_f32_e32 v102, v102, v102
	v_max_f32_e32 v103, v103, v103
	v_max_f32_e32 v104, v104, v104
	v_max_f32_e32 v105, v105, v105
	v_max_f32_e32 v106, v106, v106
	v_max_f32_e32 v107, v107, v107
	v_max_f32_e32 v108, v108, v108
	v_max_f32_e32 v109, v109, v109
	v_max_f32_e32 v110, v110, v110
	v_max_f32_e32 v111, v111, v111
	v_max_f32_e32 v112, v112, v112
	v_max_f32_e32 v113, v113, v113
	v_max_f32_e32 v114, v114, v114
	v_max_f32_e32 v115, v115, v115
	v_med3_f32 v100, v100, s20, v129
	v_med3_f32 v101, v101, s20, v129
	v_med3_f32 v102, v102, s20, v129
	v_med3_f32 v103, v103, s20, v129
	v_med3_f32 v104, v104, s20, v129
	v_med3_f32 v105, v105, s20, v129
	v_med3_f32 v106, v106, s20, v129
	v_med3_f32 v107, v107, s20, v129
	v_med3_f32 v108, v108, s20, v129
	v_med3_f32 v109, v109, s20, v129
	v_med3_f32 v110, v110, s20, v129
	v_med3_f32 v111, v111, s20, v129
	v_med3_f32 v112, v112, s20, v129
	v_med3_f32 v113, v113, s20, v129
	v_med3_f32 v114, v114, s20, v129
	v_med3_f32 v115, v115, s20, v129
	v_mov_b32_e32 v116, 0
	v_mov_b32_e32 v117, 0
	v_mov_b32_e32 v118, 0
	v_mov_b32_e32 v119, 0
	v_cvt_pk_fp8_f32 v116, v100, v101
	v_cvt_pk_fp8_f32 v117, v104, v105
	v_cvt_pk_fp8_f32 v118, v108, v109
	v_cvt_pk_fp8_f32 v119, v112, v113
	v_cvt_pk_fp8_f32 v116, v102, v103 op_sel:[0,0,1]
	v_cvt_pk_fp8_f32 v117, v106, v107 op_sel:[0,0,1]
	v_cvt_pk_fp8_f32 v118, v110, v111 op_sel:[0,0,1]
	v_cvt_pk_fp8_f32 v119, v114, v115 op_sel:[0,0,1]
	s_nop 0
	global_store_dwordx4 v127, v[116:119], s[14:15]
	ds_read_b32 v100, v124
	ds_read_b32 v101, v124 offset:512
	ds_read_b32 v102, v124 offset:1024
	ds_read_b32 v103, v124 offset:1536
	ds_read_b32 v104, v124 offset:2048
	ds_read_b32 v105, v124 offset:2560
	ds_read_b32 v106, v124 offset:3072
	ds_read_b32 v107, v124 offset:3584
	ds_read_b32 v108, v124 offset:4096
	ds_read_b32 v109, v124 offset:4608
	ds_read_b32 v110, v124 offset:5120
	ds_read_b32 v111, v124 offset:5632
	ds_read_b32 v112, v124 offset:6144
	ds_read_b32 v113, v124 offset:6656
	ds_read_b32 v114, v124 offset:7168
	ds_read_b32 v115, v124 offset:7680
	s_waitcnt lgkmcnt(0)
	v_max_f32_e32 v100, v100, v100
	v_max_f32_e32 v101, v101, v101
	v_max_f32_e32 v102, v102, v102
	v_max_f32_e32 v103, v103, v103
	v_max_f32_e32 v104, v104, v104
	v_max_f32_e32 v105, v105, v105
	v_max_f32_e32 v106, v106, v106
	v_max_f32_e32 v107, v107, v107
	v_max_f32_e32 v108, v108, v108
	v_max_f32_e32 v109, v109, v109
	v_max_f32_e32 v110, v110, v110
	v_max_f32_e32 v111, v111, v111
	v_max_f32_e32 v112, v112, v112
	v_max_f32_e32 v113, v113, v113
	v_max_f32_e32 v114, v114, v114
	v_max_f32_e32 v115, v115, v115
	v_med3_f32 v100, v100, s20, v129
	v_med3_f32 v101, v101, s20, v129
	v_med3_f32 v102, v102, s20, v129
	v_med3_f32 v103, v103, s20, v129
	v_med3_f32 v104, v104, s20, v129
	v_med3_f32 v105, v105, s20, v129
	v_med3_f32 v106, v106, s20, v129
	v_med3_f32 v107, v107, s20, v129
	v_med3_f32 v108, v108, s20, v129
	v_med3_f32 v109, v109, s20, v129
	v_med3_f32 v110, v110, s20, v129
	v_med3_f32 v111, v111, s20, v129
	v_med3_f32 v112, v112, s20, v129
	v_med3_f32 v113, v113, s20, v129
	v_med3_f32 v114, v114, s20, v129
	v_med3_f32 v115, v115, s20, v129
	v_mov_b32_e32 v116, 0
	v_mov_b32_e32 v117, 0
	v_mov_b32_e32 v118, 0
	v_mov_b32_e32 v119, 0
	v_cvt_pk_fp8_f32 v116, v100, v101
	v_cvt_pk_fp8_f32 v117, v104, v105
	v_cvt_pk_fp8_f32 v118, v108, v109
	v_cvt_pk_fp8_f32 v119, v112, v113
	v_cvt_pk_fp8_f32 v116, v102, v103 op_sel:[0,0,1]
	v_cvt_pk_fp8_f32 v117, v106, v107 op_sel:[0,0,1]
	v_cvt_pk_fp8_f32 v118, v110, v111 op_sel:[0,0,1]
	v_cvt_pk_fp8_f32 v119, v114, v115 op_sel:[0,0,1]
	s_nop 0
	global_store_dwordx4 v128, v[116:119], s[14:15]
	s_waitcnt vmcnt(12)
	v_mul_f32_e32 v68, 0x43000000, v68
	v_mul_f32_e32 v69, 0x43000000, v69
	v_mul_f32_e32 v70, 0x43000000, v70
	v_mul_f32_e32 v71, 0x43000000, v71
	ds_write_b128 v121, v[68:71]
	v_mul_f32_e32 v72, 0x43000000, v72
	v_mul_f32_e32 v73, 0x43000000, v73
	v_mul_f32_e32 v74, 0x43000000, v74
	v_mul_f32_e32 v75, 0x43000000, v75
	ds_write_b128 v121, v[72:75] offset:1024
	v_mul_f32_e32 v76, 0x43000000, v76
	v_mul_f32_e32 v77, 0x43000000, v77
	v_mul_f32_e32 v78, 0x43000000, v78
	v_mul_f32_e32 v79, 0x43000000, v79
	ds_write_b128 v121, v[76:79] offset:2048
	v_mul_f32_e32 v80, 0x43000000, v80
	v_mul_f32_e32 v81, 0x43000000, v81
	v_mul_f32_e32 v82, 0x43000000, v82
	v_mul_f32_e32 v83, 0x43000000, v83
	ds_write_b128 v121, v[80:83] offset:3072
	v_mul_f32_e32 v84, 0x43000000, v84
	v_mul_f32_e32 v85, 0x43000000, v85
	v_mul_f32_e32 v86, 0x43000000, v86
	v_mul_f32_e32 v87, 0x43000000, v87
	ds_write_b128 v121, v[84:87] offset:4096
	v_mul_f32_e32 v88, 0x43000000, v88
	v_mul_f32_e32 v89, 0x43000000, v89
	v_mul_f32_e32 v90, 0x43000000, v90
	v_mul_f32_e32 v91, 0x43000000, v91
	ds_write_b128 v121, v[88:91] offset:5120
	v_mul_f32_e32 v92, 0x43000000, v92
	v_mul_f32_e32 v93, 0x43000000, v93
	v_mul_f32_e32 v94, 0x43000000, v94
	v_mul_f32_e32 v95, 0x43000000, v95
	ds_write_b128 v121, v[92:95] offset:6144
	v_mul_f32_e32 v96, 0x43000000, v96
	v_mul_f32_e32 v97, 0x43000000, v97
	v_mul_f32_e32 v98, 0x43000000, v98
	v_mul_f32_e32 v99, 0x43000000, v99
	ds_write_b128 v121, v[96:99] offset:7168
	s_waitcnt lgkmcnt(0)
	s_barrier
; #define GAS __attribute__((address_space(1)))
; #define LAS __attribute__((address_space(3)))
; #define LDS_WAIT() asm volatile("s_waitcnt lgkmcnt(0)" ::: "memory")
; __device__ __forceinline__ unsigned pk4_fp8(float a, float b, float c, float d) {
;     a = fminf(fmaxf(a, -448.f), 448.f); b = fminf(fmaxf(b, -448.f), 448.f); c = fminf(fmaxf(c, -448.f), 448.f); d = fminf(fmaxf(d, -448.f), 448.f);
;     int w = __builtin_amdgcn_cvt_pk_fp8_f32(a, b, 0, false); w = __builtin_amdgcn_cvt_pk_fp8_f32(c, d, w, true); return (unsigned)w; }
;     ...
;     for (int i = 0; i < 32; ++i) v[i] = sc >= 0 ? W[(size_t)(k0 + 2 * i + (lane >> 5)) * Nsrc + sc] : 0.f;
; #pragma unroll
;     for (int i = 0; i < 32; ++i) { const int k = k0 + 2 * i + (lane >> 5); float x = v[i] * wscale; if (KS) x *= (k < ksplit ? ksA[k] : ksB[k - ksplit]); scr[(2 * i + (lane >> 5)) * 33 + (lane & 31)] = x; }
;     LDS_WAIT(); asm volatile("" ::: "memory");
;     const int c = lane & 7;
; #pragma unroll
;     for (int j = 0; j < 4; ++j) { const int n = (lane >> 3) + 8 * j; const LAS float* s = scr + (8 * c) * 33 + n;
;         const unsigned long long o = (unsigned long long)pg8::pk4_fp8(s[0 * 33], s[1 * 33], s[2 * 33], s[3 * 33]) | ((unsigned long long)pg8::pk4_fp8(s[4 * 33], s[5 * 33], s[6 * 33], s[7 * 33]) << 32);
;         *(GAS unsigned long long*)(WT + (size_t)(n0 + n) * K + k0 + 8 * c) = o; }
;     LDS_WAIT(); asm volatile("" ::: "memory");
	s_add_i32 s17, s16, 2016
	s_min_u32 s17, s17, 0x7ff
	s_lshr_b32 s18, s17, 5
	s_add_i32 s18, s18, 64
	s_and_b32 s19, s17, 31
	s_lshl_b32 s18, s18, 21
	s_lshl_b32 s19, s19, 9
	s_add_u32 s18, s18, s19
	s_add_u32 s12, s2, s18
	s_addc_u32 s13, s3, 0
	global_load_dwordx4 v[68:71], v126, s[12:13]
	s_add_u32 s12, s12, 0x8000
	s_addc_u32 s13, s13, 0
	global_load_dwordx4 v[72:75], v126, s[12:13]
	s_add_u32 s12, s12, 0x8000
	s_addc_u32 s13, s13, 0
	global_load_dwordx4 v[76:79], v126, s[12:13]
	s_add_u32 s12, s12, 0x8000
	s_addc_u32 s13, s13, 0
	global_load_dwordx4 v[80:83], v126, s[12:13]
	s_add_u32 s12, s12, 0x8000
	s_addc_u32 s13, s13, 0
	global_load_dwordx4 v[84:87], v126, s[12:13]
	s_add_u32 s12, s12, 0x8000
	s_addc_u32 s13, s13, 0
	global_load_dwordx4 v[88:91], v126, s[12:13]
	s_add_u32 s12, s12, 0x8000
	s_addc_u32 s13, s13, 0
	global_load_dwordx4 v[92:95], v126, s[12:13]
	s_add_u32 s12, s12, 0x8000
	s_addc_u32 s13, s13, 0
	global_load_dwordx4 v[96:99], v126, s[12:13]
	s_add_i32 s17, s16, 1824
	s_min_u32 s17, s17, 0x7ff
	s_lshr_b32 s18, s17, 5
	s_add_i32 s18, s18, 64
	s_and_b32 s19, s17, 31
	s_lshl_b32 s19, s19, 21
	s_lshl_b32 s18, s18, 7
	s_add_u32 s18, s18, s19
	s_add_u32 s14, s4, s18
	s_addc_u32 s15, s5, 0
	ds_read_b32 v100, v123
	ds_read_b32 v101, v123 offset:512
	ds_read_b32 v102, v123 offset:1024
	ds_read_b32 v103, v123 offset:1536
	ds_read_b32 v104, v123 offset:2048
	ds_read_b32 v105, v123 offset:2560
	ds_read_b32 v106, v123 offset:3072
	ds_read_b32 v107, v123 offset:3584
	ds_read_b32 v108, v123 offset:4096
	ds_read_b32 v109, v123 offset:4608
	ds_read_b32 v110, v123 offset:5120
	ds_read_b32 v111, v123 offset:5632
	ds_read_b32 v112, v123 offset:6144
	ds_read_b32 v113, v123 offset:6656
	ds_read_b32 v114, v123 offset:7168
	ds_read_b32 v115, v123 offset:7680
	s_waitcnt lgkmcnt(0)
	v_max_f32_e32 v100, v100, v100
	v_max_f32_e32 v101, v101, v101
	v_max_f32_e32 v102, v102, v102
	v_max_f32_e32 v103, v103, v103
	v_max_f32_e32 v104, v104, v104
	v_max_f32_e32 v105, v105, v105
	v_max_f32_e32 v106, v106, v106
	v_max_f32_e32 v107, v107, v107
	v_max_f32_e32 v108, v108, v108
	v_max_f32_e32 v109, v109, v109
	v_max_f32_e32 v110, v110, v110
	v_max_f32_e32 v111, v111, v111
	v_max_f32_e32 v112, v112, v112
	v_max_f32_e32 v113, v113, v113
	v_max_f32_e32 v114, v114, v114
	v_max_f32_e32 v115, v115, v115
	v_med3_f32 v100, v100, s20, v129
	v_med3_f32 v101, v101, s20, v129
	v_med3_f32 v102, v102, s20, v129
	v_med3_f32 v103, v103, s20, v129
	v_med3_f32 v104, v104, s20, v129
	v_med3_f32 v105, v105, s20, v129
	v_med3_f32 v106, v106, s20, v129
	v_med3_f32 v107, v107, s20, v129
	v_med3_f32 v108, v108, s20, v129
	v_med3_f32 v109, v109, s20, v129
	v_med3_f32 v110, v110, s20, v129
	v_med3_f32 v111, v111, s20, v129
	v_med3_f32 v112, v112, s20, v129
	v_med3_f32 v113, v113, s20, v129
	v_med3_f32 v114, v114, s20, v129
	v_med3_f32 v115, v115, s20, v129
	v_mov_b32_e32 v116, 0
	v_mov_b32_e32 v117, 0
	v_mov_b32_e32 v118, 0
	v_mov_b32_e32 v119, 0
	v_cvt_pk_fp8_f32 v116, v100, v101
	v_cvt_pk_fp8_f32 v117, v104, v105
	v_cvt_pk_fp8_f32 v118, v108, v109
	v_cvt_pk_fp8_f32 v119, v112, v113
	v_cvt_pk_fp8_f32 v116, v102, v103 op_sel:[0,0,1]
	v_cvt_pk_fp8_f32 v117, v106, v107 op_sel:[0,0,1]
	v_cvt_pk_fp8_f32 v118, v110, v111 op_sel:[0,0,1]
	v_cvt_pk_fp8_f32 v119, v114, v115 op_sel:[0,0,1]
	s_nop 0
	global_store_dwordx4 v127, v[116:119], s[14:15]
	ds_read_b32 v100, v125
	ds_read_b32 v101, v125 offset:512
	ds_read_b32 v102, v125 offset:1024
	ds_read_b32 v103, v125 offset:1536
	ds_read_b32 v104, v125 offset:2048
	ds_read_b32 v105, v125 offset:2560
	ds_read_b32 v106, v125 offset:3072
	ds_read_b32 v107, v125 offset:3584
	ds_read_b32 v108, v125 offset:4096
	ds_read_b32 v109, v125 offset:4608
	ds_read_b32 v110, v125 offset:5120
	ds_read_b32 v111, v125 offset:5632
	ds_read_b32 v112, v125 offset:6144
	ds_read_b32 v113, v125 offset:6656
	ds_read_b32 v114, v125 offset:7168
	ds_read_b32 v115, v125 offset:7680
	s_waitcnt lgkmcnt(0)
	v_max_f32_e32 v100, v100, v100
	v_max_f32_e32 v101, v101, v101
	v_max_f32_e32 v102, v102, v102
	v_max_f32_e32 v103, v103, v103
	v_max_f32_e32 v104, v104, v104
	v_max_f32_e32 v105, v105, v105
	v_max_f32_e32 v106, v106, v106
	v_max_f32_e32 v107, v107, v107
	v_max_f32_e32 v108, v108, v108
	v_max_f32_e32 v109, v109, v109
	v_max_f32_e32 v110, v110, v110
	v_max_f32_e32 v111, v111, v111
	v_max_f32_e32 v112, v112, v112
	v_max_f32_e32 v113, v113, v113
	v_max_f32_e32 v114, v114, v114
	v_max_f32_e32 v115, v115, v115
	v_med3_f32 v100, v100, s20, v129
	v_med3_f32 v101, v101, s20, v129
	v_med3_f32 v102, v102, s20, v129
	v_med3_f32 v103, v103, s20, v129
	v_med3_f32 v104, v104, s20, v129
	v_med3_f32 v105, v105, s20, v129
	v_med3_f32 v106, v106, s20, v129
	v_med3_f32 v107, v107, s20, v129
	v_med3_f32 v108, v108, s20, v129
	v_med3_f32 v109, v109, s20, v129
	v_med3_f32 v110, v110, s20, v129
	v_med3_f32 v111, v111, s20, v129
	v_med3_f32 v112, v112, s20, v129
	v_med3_f32 v113, v113, s20, v129
	v_med3_f32 v114, v114, s20, v129
	v_med3_f32 v115, v115, s20, v129
	v_mov_b32_e32 v116, 0
	v_mov_b32_e32 v117, 0
	v_mov_b32_e32 v118, 0
	v_mov_b32_e32 v119, 0
	v_cvt_pk_fp8_f32 v116, v100, v101
	v_cvt_pk_fp8_f32 v117, v104, v105
	v_cvt_pk_fp8_f32 v118, v108, v109
	v_cvt_pk_fp8_f32 v119, v112, v113
	v_cvt_pk_fp8_f32 v116, v102, v103 op_sel:[0,0,1]
	v_cvt_pk_fp8_f32 v117, v106, v107 op_sel:[0,0,1]
	v_cvt_pk_fp8_f32 v118, v110, v111 op_sel:[0,0,1]
	v_cvt_pk_fp8_f32 v119, v114, v115 op_sel:[0,0,1]
	s_nop 0
	global_store_dwordx4 v128, v[116:119], s[14:15]
	s_waitcnt vmcnt(12)
	v_mul_f32_e32 v36, 0x43000000, v36
	v_mul_f32_e32 v37, 0x43000000, v37
	v_mul_f32_e32 v38, 0x43000000, v38
	v_mul_f32_e32 v39, 0x43000000, v39
	ds_write_b128 v120, v[36:39]
	v_mul_f32_e32 v40, 0x43000000, v40
	v_mul_f32_e32 v41, 0x43000000, v41
	v_mul_f32_e32 v42, 0x43000000, v42
	v_mul_f32_e32 v43, 0x43000000, v43
	ds_write_b128 v120, v[40:43] offset:1024
	v_mul_f32_e32 v44, 0x43000000, v44
	v_mul_f32_e32 v45, 0x43000000, v45
	v_mul_f32_e32 v46, 0x43000000, v46
	v_mul_f32_e32 v47, 0x43000000, v47
	ds_write_b128 v120, v[44:47] offset:2048
	v_mul_f32_e32 v48, 0x43000000, v48
	v_mul_f32_e32 v49, 0x43000000, v49
	v_mul_f32_e32 v50, 0x43000000, v50
	v_mul_f32_e32 v51, 0x43000000, v51
	ds_write_b128 v120, v[48:51] offset:3072
	v_mul_f32_e32 v52, 0x43000000, v52
	v_mul_f32_e32 v53, 0x43000000, v53
	v_mul_f32_e32 v54, 0x43000000, v54
	v_mul_f32_e32 v55, 0x43000000, v55
	ds_write_b128 v120, v[52:55] offset:4096
	v_mul_f32_e32 v56, 0x43000000, v56
	v_mul_f32_e32 v57, 0x43000000, v57
	v_mul_f32_e32 v58, 0x43000000, v58
	v_mul_f32_e32 v59, 0x43000000, v59
	ds_write_b128 v120, v[56:59] offset:5120
	v_mul_f32_e32 v60, 0x43000000, v60
	v_mul_f32_e32 v61, 0x43000000, v61
	v_mul_f32_e32 v62, 0x43000000, v62
	v_mul_f32_e32 v63, 0x43000000, v63
	ds_write_b128 v120, v[60:63] offset:6144
	v_mul_f32_e32 v64, 0x43000000, v64
	v_mul_f32_e32 v65, 0x43000000, v65
	v_mul_f32_e32 v66, 0x43000000, v66
	v_mul_f32_e32 v67, 0x43000000, v67
	ds_write_b128 v120, v[64:67] offset:7168
	s_waitcnt lgkmcnt(0)
	s_barrier
; #define GAS __attribute__((address_space(1)))
; #define LAS __attribute__((address_space(3)))
; #define LDS_WAIT() asm volatile("s_waitcnt lgkmcnt(0)" ::: "memory")
; __device__ __forceinline__ unsigned pk4_fp8(float a, float b, float c, float d) {
;     a = fminf(fmaxf(a, -448.f), 448.f); b = fminf(fmaxf(b, -448.f), 448.f); c = fminf(fmaxf(c, -448.f), 448.f); d = fminf(fmaxf(d, -448.f), 448.f);
;     int w = __builtin_amdgcn_cvt_pk_fp8_f32(a, b, 0, false); w = __builtin_amdgcn_cvt_pk_fp8_f32(c, d, w, true); return (unsigned)w; }
;     ...
;     for (int i = 0; i < 32; ++i) v[i] = sc >= 0 ? W[(size_t)(k0 + 2 * i + (lane >> 5)) * Nsrc + sc] : 0.f;
; #pragma unroll
;     for (int i = 0; i < 32; ++i) { const int k = k0 + 2 * i + (lane >> 5); float x = v[i] * wscale; if (KS) x *= (k < ksplit ? ksA[k] : ksB[k - ksplit]); scr[(2 * i + (lane >> 5)) * 33 + (lane & 31)] = x; }
;     LDS_WAIT(); asm volatile("" ::: "memory");
;     const int c = lane & 7;
; #pragma unroll
;     for (int j = 0; j < 4; ++j) { const int n = (lane >> 3) + 8 * j; const LAS float* s = scr + (8 * c) * 33 + n;
;         const unsigned long long o = (unsigned long long)pg8::pk4_fp8(s[0 * 33], s[1 * 33], s[2 * 33], s[3 * 33]) | ((unsigned long long)pg8::pk4_fp8(s[4 * 33], s[5 * 33], s[6 * 33], s[7 * 33]) << 32);
;         *(GAS unsigned long long*)(WT + (size_t)(n0 + n) * K + k0 + 8 * c) = o; }
;     LDS_WAIT(); asm volatile("" ::: "memory");
	s_add_i32 s17, s16, 1920
	s_min_u32 s17, s17, 0x7ff
	s_lshr_b32 s18, s17, 5
	s_add_i32 s18, s18, 64
	s_and_b32 s19, s17, 31
	s_lshl_b32 s19, s19, 21
	s_lshl_b32 s18, s18, 7
	s_add_u32 s18, s18, s19
	s_add_u32 s14, s4, s18
	s_addc_u32 s15, s5, 0
	ds_read_b32 v100, v122
	ds_read_b32 v101, v122 offset:512
	ds_read_b32 v102, v122 offset:1024
	ds_read_b32 v103, v122 offset:1536
	ds_read_b32 v104, v122 offset:2048
	ds_read_b32 v105, v122 offset:2560
	ds_read_b32 v106, v122 offset:3072
	ds_read_b32 v107, v122 offset:3584
	ds_read_b32 v108, v122 offset:4096
	ds_read_b32 v109, v122 offset:4608
	ds_read_b32 v110, v122 offset:5120
	ds_read_b32 v111, v122 offset:5632
	ds_read_b32 v112, v122 offset:6144
	ds_read_b32 v113, v122 offset:6656
	ds_read_b32 v114, v122 offset:7168
	ds_read_b32 v115, v122 offset:7680
	s_waitcnt lgkmcnt(0)
	v_max_f32_e32 v100, v100, v100
	v_max_f32_e32 v101, v101, v101
	v_max_f32_e32 v102, v102, v102
	v_max_f32_e32 v103, v103, v103
	v_max_f32_e32 v104, v104, v104
	v_max_f32_e32 v105, v105, v105
	v_max_f32_e32 v106, v106, v106
	v_max_f32_e32 v107, v107, v107
	v_max_f32_e32 v108, v108, v108
	v_max_f32_e32 v109, v109, v109
	v_max_f32_e32 v110, v110, v110
	v_max_f32_e32 v111, v111, v111
	v_max_f32_e32 v112, v112, v112
	v_max_f32_e32 v113, v113, v113
	v_max_f32_e32 v114, v114, v114
	v_max_f32_e32 v115, v115, v115
	v_med3_f32 v100, v100, s20, v129
	v_med3_f32 v101, v101, s20, v129
	v_med3_f32 v102, v102, s20, v129
	v_med3_f32 v103, v103, s20, v129
	v_med3_f32 v104, v104, s20, v129
	v_med3_f32 v105, v105, s20, v129
	v_med3_f32 v106, v106, s20, v129
	v_med3_f32 v107, v107, s20, v129
	v_med3_f32 v108, v108, s20, v129
	v_med3_f32 v109, v109, s20, v129
	v_med3_f32 v110, v110, s20, v129
	v_med3_f32 v111, v111, s20, v129
	v_med3_f32 v112, v112, s20, v129
	v_med3_f32 v113, v113, s20, v129
	v_med3_f32 v114, v114, s20, v129
	v_med3_f32 v115, v115, s20, v129
	v_mov_b32_e32 v116, 0
	v_mov_b32_e32 v117, 0
	v_mov_b32_e32 v118, 0
	v_mov_b32_e32 v119, 0
	v_cvt_pk_fp8_f32 v116, v100, v101
	v_cvt_pk_fp8_f32 v117, v104, v105
	v_cvt_pk_fp8_f32 v118, v108, v109
	v_cvt_pk_fp8_f32 v119, v112, v113
	v_cvt_pk_fp8_f32 v116, v102, v103 op_sel:[0,0,1]
	v_cvt_pk_fp8_f32 v117, v106, v107 op_sel:[0,0,1]
	v_cvt_pk_fp8_f32 v118, v110, v111 op_sel:[0,0,1]
	v_cvt_pk_fp8_f32 v119, v114, v115 op_sel:[0,0,1]
	s_nop 0
	global_store_dwordx4 v127, v[116:119], s[14:15]
	ds_read_b32 v100, v124
	ds_read_b32 v101, v124 offset:512
	ds_read_b32 v102, v124 offset:1024
	ds_read_b32 v103, v124 offset:1536
	ds_read_b32 v104, v124 offset:2048
	ds_read_b32 v105, v124 offset:2560
	ds_read_b32 v106, v124 offset:3072
	ds_read_b32 v107, v124 offset:3584
	ds_read_b32 v108, v124 offset:4096
	ds_read_b32 v109, v124 offset:4608
	ds_read_b32 v110, v124 offset:5120
	ds_read_b32 v111, v124 offset:5632
	ds_read_b32 v112, v124 offset:6144
	ds_read_b32 v113, v124 offset:6656
	ds_read_b32 v114, v124 offset:7168
	ds_read_b32 v115, v124 offset:7680
	s_waitcnt lgkmcnt(0)
	v_max_f32_e32 v100, v100, v100
	v_max_f32_e32 v101, v101, v101
	v_max_f32_e32 v102, v102, v102
	v_max_f32_e32 v103, v103, v103
	v_max_f32_e32 v104, v104, v104
	v_max_f32_e32 v105, v105, v105
	v_max_f32_e32 v106, v106, v106
	v_max_f32_e32 v107, v107, v107
	v_max_f32_e32 v108, v108, v108
	v_max_f32_e32 v109, v109, v109
	v_max_f32_e32 v110, v110, v110
	v_max_f32_e32 v111, v111, v111
	v_max_f32_e32 v112, v112, v112
	v_max_f32_e32 v113, v113, v113
	v_max_f32_e32 v114, v114, v114
	v_max_f32_e32 v115, v115, v115
	v_med3_f32 v100, v100, s20, v129
	v_med3_f32 v101, v101, s20, v129
	v_med3_f32 v102, v102, s20, v129
	v_med3_f32 v103, v103, s20, v129
	v_med3_f32 v104, v104, s20, v129
	v_med3_f32 v105, v105, s20, v129
	v_med3_f32 v106, v106, s20, v129
	v_med3_f32 v107, v107, s20, v129
	v_med3_f32 v108, v108, s20, v129
	v_med3_f32 v109, v109, s20, v129
	v_med3_f32 v110, v110, s20, v129
	v_med3_f32 v111, v111, s20, v129
	v_med3_f32 v112, v112, s20, v129
	v_med3_f32 v113, v113, s20, v129
	v_med3_f32 v114, v114, s20, v129
	v_med3_f32 v115, v115, s20, v129
	v_mov_b32_e32 v116, 0
	v_mov_b32_e32 v117, 0
	v_mov_b32_e32 v118, 0
	v_mov_b32_e32 v119, 0
	v_cvt_pk_fp8_f32 v116, v100, v101
	v_cvt_pk_fp8_f32 v117, v104, v105
	v_cvt_pk_fp8_f32 v118, v108, v109
	v_cvt_pk_fp8_f32 v119, v112, v113
	v_cvt_pk_fp8_f32 v116, v102, v103 op_sel:[0,0,1]
	v_cvt_pk_fp8_f32 v117, v106, v107 op_sel:[0,0,1]
	v_cvt_pk_fp8_f32 v118, v110, v111 op_sel:[0,0,1]
	v_cvt_pk_fp8_f32 v119, v114, v115 op_sel:[0,0,1]
	s_nop 0
	global_store_dwordx4 v128, v[116:119], s[14:15]
	s_waitcnt vmcnt(4)
	v_mul_f32_e32 v68, 0x43000000, v68
	v_mul_f32_e32 v69, 0x43000000, v69
	v_mul_f32_e32 v70, 0x43000000, v70
	v_mul_f32_e32 v71, 0x43000000, v71
	ds_write_b128 v121, v[68:71]
	v_mul_f32_e32 v72, 0x43000000, v72
	v_mul_f32_e32 v73, 0x43000000, v73
	v_mul_f32_e32 v74, 0x43000000, v74
	v_mul_f32_e32 v75, 0x43000000, v75
	ds_write_b128 v121, v[72:75] offset:1024
	v_mul_f32_e32 v76, 0x43000000, v76
	v_mul_f32_e32 v77, 0x43000000, v77
	v_mul_f32_e32 v78, 0x43000000, v78
	v_mul_f32_e32 v79, 0x43000000, v79
	ds_write_b128 v121, v[76:79] offset:2048
	v_mul_f32_e32 v80, 0x43000000, v80
	v_mul_f32_e32 v81, 0x43000000, v81
	v_mul_f32_e32 v82, 0x43000000, v82
	v_mul_f32_e32 v83, 0x43000000, v83
	ds_write_b128 v121, v[80:83] offset:3072
	v_mul_f32_e32 v84, 0x43000000, v84
	v_mul_f32_e32 v85, 0x43000000, v85
	v_mul_f32_e32 v86, 0x43000000, v86
	v_mul_f32_e32 v87, 0x43000000, v87
	ds_write_b128 v121, v[84:87] offset:4096
	v_mul_f32_e32 v88, 0x43000000, v88
	v_mul_f32_e32 v89, 0x43000000, v89
	v_mul_f32_e32 v90, 0x43000000, v90
	v_mul_f32_e32 v91, 0x43000000, v91
	ds_write_b128 v121, v[88:91] offset:5120
	v_mul_f32_e32 v92, 0x43000000, v92
	v_mul_f32_e32 v93, 0x43000000, v93
	v_mul_f32_e32 v94, 0x43000000, v94
	v_mul_f32_e32 v95, 0x43000000, v95
	ds_write_b128 v121, v[92:95] offset:6144
	v_mul_f32_e32 v96, 0x43000000, v96
	v_mul_f32_e32 v97, 0x43000000, v97
	v_mul_f32_e32 v98, 0x43000000, v98
	v_mul_f32_e32 v99, 0x43000000, v99
	ds_write_b128 v121, v[96:99] offset:7168
	s_waitcnt lgkmcnt(0)
	s_barrier
; #define GAS __attribute__((address_space(1)))
; #define LAS __attribute__((address_space(3)))
; #define LDS_WAIT() asm volatile("s_waitcnt lgkmcnt(0)" ::: "memory")
; __device__ __forceinline__ unsigned pk4_fp8(float a, float b, float c, float d) {
;     a = fminf(fmaxf(a, -448.f), 448.f); b = fminf(fmaxf(b, -448.f), 448.f); c = fminf(fmaxf(c, -448.f), 448.f); d = fminf(fmaxf(d, -448.f), 448.f);
;     int w = __builtin_amdgcn_cvt_pk_fp8_f32(a, b, 0, false); w = __builtin_amdgcn_cvt_pk_fp8_f32(c, d, w, true); return (unsigned)w; }
;     ...
;     for (int i = 0; i < 32; ++i) v[i] = sc >= 0 ? W[(size_t)(k0 + 2 * i + (lane >> 5)) * Nsrc + sc] : 0.f;
; #pragma unroll
;     for (int i = 0; i < 32; ++i) { const int k = k0 + 2 * i + (lane >> 5); float x = v[i] * wscale; if (KS) x *= (k < ksplit ? ksA[k] : ksB[k - ksplit]); scr[(2 * i + (lane >> 5)) * 33 + (lane & 31)] = x; }
;     LDS_WAIT(); asm volatile("" ::: "memory");
;     const int c = lane & 7;
; #pragma unroll
;     for (int j = 0; j < 4; ++j) { const int n = (lane >> 3) + 8 * j; const LAS float* s = scr + (8 * c) * 33 + n;
;         const unsigned long long o = (unsigned long long)pg8::pk4_fp8(s[0 * 33], s[1 * 33], s[2 * 33], s[3 * 33]) | ((unsigned long long)pg8::pk4_fp8(s[4 * 33], s[5 * 33], s[6 * 33], s[7 * 33]) << 32);
;         *(GAS unsigned long long*)(WT + (size_t)(n0 + n) * K + k0 + 8 * c) = o; }
;     LDS_WAIT(); asm volatile("" ::: "memory");
	s_add_i32 s17, s16, 2016
	s_min_u32 s17, s17, 0x7ff
	s_lshr_b32 s18, s17, 5
	s_add_i32 s18, s18, 64
	s_and_b32 s19, s17, 31
	s_lshl_b32 s19, s19, 21
	s_lshl_b32 s18, s18, 7
	s_add_u32 s18, s18, s19
	s_add_u32 s14, s4, s18
	s_addc_u32 s15, s5, 0
	ds_read_b32 v100, v123
	ds_read_b32 v101, v123 offset:512
	ds_read_b32 v102, v123 offset:1024
	ds_read_b32 v103, v123 offset:1536
	ds_read_b32 v104, v123 offset:2048
	ds_read_b32 v105, v123 offset:2560
	ds_read_b32 v106, v123 offset:3072
	ds_read_b32 v107, v123 offset:3584
	ds_read_b32 v108, v123 offset:4096
	ds_read_b32 v109, v123 offset:4608
	ds_read_b32 v110, v123 offset:5120
	ds_read_b32 v111, v123 offset:5632
	ds_read_b32 v112, v123 offset:6144
	ds_read_b32 v113, v123 offset:6656
	ds_read_b32 v114, v123 offset:7168
	ds_read_b32 v115, v123 offset:7680
	s_waitcnt lgkmcnt(0)
	v_max_f32_e32 v100, v100, v100
	v_max_f32_e32 v101, v101, v101
	v_max_f32_e32 v102, v102, v102
	v_max_f32_e32 v103, v103, v103
	v_max_f32_e32 v104, v104, v104
	v_max_f32_e32 v105, v105, v105
	v_max_f32_e32 v106, v106, v106
	v_max_f32_e32 v107, v107, v107
	v_max_f32_e32 v108, v108, v108
	v_max_f32_e32 v109, v109, v109
	v_max_f32_e32 v110, v110, v110
	v_max_f32_e32 v111, v111, v111
	v_max_f32_e32 v112, v112, v112
	v_max_f32_e32 v113, v113, v113
	v_max_f32_e32 v114, v114, v114
	v_max_f32_e32 v115, v115, v115
	v_med3_f32 v100, v100, s20, v129
	v_med3_f32 v101, v101, s20, v129
	v_med3_f32 v102, v102, s20, v129
	v_med3_f32 v103, v103, s20, v129
	v_med3_f32 v104, v104, s20, v129
	v_med3_f32 v105, v105, s20, v129
	v_med3_f32 v106, v106, s20, v129
	v_med3_f32 v107, v107, s20, v129
	v_med3_f32 v108, v108, s20, v129
	v_med3_f32 v109, v109, s20, v129
	v_med3_f32 v110, v110, s20, v129
	v_med3_f32 v111, v111, s20, v129
	v_med3_f32 v112, v112, s20, v129
	v_med3_f32 v113, v113, s20, v129
	v_med3_f32 v114, v114, s20, v129
	v_med3_f32 v115, v115, s20, v129
	v_mov_b32_e32 v116, 0
	v_mov_b32_e32 v117, 0
	v_mov_b32_e32 v118, 0
	v_mov_b32_e32 v119, 0
	v_cvt_pk_fp8_f32 v116, v100, v101
	v_cvt_pk_fp8_f32 v117, v104, v105
	v_cvt_pk_fp8_f32 v118, v108, v109
	v_cvt_pk_fp8_f32 v119, v112, v113
	v_cvt_pk_fp8_f32 v116, v102, v103 op_sel:[0,0,1]
	v_cvt_pk_fp8_f32 v117, v106, v107 op_sel:[0,0,1]
	v_cvt_pk_fp8_f32 v118, v110, v111 op_sel:[0,0,1]
	v_cvt_pk_fp8_f32 v119, v114, v115 op_sel:[0,0,1]
	s_nop 0
	global_store_dwordx4 v127, v[116:119], s[14:15]
	ds_read_b32 v100, v125
	ds_read_b32 v101, v125 offset:512
	ds_read_b32 v102, v125 offset:1024
	ds_read_b32 v103, v125 offset:1536
	ds_read_b32 v104, v125 offset:2048
	ds_read_b32 v105, v125 offset:2560
	ds_read_b32 v106, v125 offset:3072
	ds_read_b32 v107, v125 offset:3584
	ds_read_b32 v108, v125 offset:4096
	ds_read_b32 v109, v125 offset:4608
	ds_read_b32 v110, v125 offset:5120
	ds_read_b32 v111, v125 offset:5632
	ds_read_b32 v112, v125 offset:6144
	ds_read_b32 v113, v125 offset:6656
	ds_read_b32 v114, v125 offset:7168
	ds_read_b32 v115, v125 offset:7680
	s_waitcnt lgkmcnt(0)
	v_max_f32_e32 v100, v100, v100
	v_max_f32_e32 v101, v101, v101
	v_max_f32_e32 v102, v102, v102
	v_max_f32_e32 v103, v103, v103
	v_max_f32_e32 v104, v104, v104
	v_max_f32_e32 v105, v105, v105
	v_max_f32_e32 v106, v106, v106
	v_max_f32_e32 v107, v107, v107
	v_max_f32_e32 v108, v108, v108
	v_max_f32_e32 v109, v109, v109
	v_max_f32_e32 v110, v110, v110
	v_max_f32_e32 v111, v111, v111
	v_max_f32_e32 v112, v112, v112
	v_max_f32_e32 v113, v113, v113
	v_max_f32_e32 v114, v114, v114
	v_max_f32_e32 v115, v115, v115
	v_med3_f32 v100, v100, s20, v129
	v_med3_f32 v101, v101, s20, v129
	v_med3_f32 v102, v102, s20, v129
	v_med3_f32 v103, v103, s20, v129
	v_med3_f32 v104, v104, s20, v129
	v_med3_f32 v105, v105, s20, v129
	v_med3_f32 v106, v106, s20, v129
	v_med3_f32 v107, v107, s20, v129
	v_med3_f32 v108, v108, s20, v129
	v_med3_f32 v109, v109, s20, v129
	v_med3_f32 v110, v110, s20, v129
	v_med3_f32 v111, v111, s20, v129
	v_med3_f32 v112, v112, s20, v129
	v_med3_f32 v113, v113, s20, v129
	v_med3_f32 v114, v114, s20, v129
	v_med3_f32 v115, v115, s20, v129
	v_mov_b32_e32 v116, 0
	v_mov_b32_e32 v117, 0
	v_mov_b32_e32 v118, 0
	v_mov_b32_e32 v119, 0
	v_cvt_pk_fp8_f32 v116, v100, v101
	v_cvt_pk_fp8_f32 v117, v104, v105
	v_cvt_pk_fp8_f32 v118, v108, v109
	v_cvt_pk_fp8_f32 v119, v112, v113
	v_cvt_pk_fp8_f32 v116, v102, v103 op_sel:[0,0,1]
	v_cvt_pk_fp8_f32 v117, v106, v107 op_sel:[0,0,1]
	v_cvt_pk_fp8_f32 v118, v110, v111 op_sel:[0,0,1]
	v_cvt_pk_fp8_f32 v119, v114, v115 op_sel:[0,0,1]
	s_nop 0
	global_store_dwordx4 v128, v[116:119], s[14:15]
	s_waitcnt vmcnt(0) lgkmcnt(0)
	s_barrier
